# GEMM K-loops: per-block s_setprio flips removed, one static s_setprio 1 for waves 0-3 (older half) per gemm call, reset at grid barriers
# speedup vs baseline: 1.0036x; 1.0036x over previous
.LBB0_56:
	s_andn2_b64 vcc, exec, s[16:17]
	s_cbranch_vccnz .LBB0_106
	s_waitcnt vmcnt(0)
	s_waitcnt lgkmcnt(0)
	s_barrier
	s_setprio 0
	s_mov_b64 s[2:3], exec
	v_readlane_b32 s4, v250, 5
	v_readlane_b32 s5, v250, 6
	s_and_b64 s[4:5], s[2:3], s[4:5]
	s_mov_b64 exec, s[4:5]
	s_cbranch_execz .LBB0_105
	s_add_i32 s4, 0, 0x27ff0
	v_mov_b32_e32 v1, s4
	s_waitcnt vmcnt(0) expcnt(0) lgkmcnt(0)
	ds_read_b32 v3, v1
	s_add_i32 s4, 0, 0x27ff4
	v_mov_b32_e32 v1, s4
	ds_read_b32 v1, v1
	s_waitcnt lgkmcnt(1)
	v_cmp_ne_u32_e32 vcc, 0, v3
	s_cbranch_vccnz .LBB0_73
	v_readlane_b32 s4, v250, 2
	v_readlane_b32 s5, v250, 3
	s_load_dwordx2 s[8:9], s[4:5], 0x4
	s_load_dword s10, s[0:1], 0x110
	s_add_u32 s4, s52, 0x1000
	s_addc_u32 s5, s53, 0
	s_add_u32 s6, s52, 0x1100
	s_addc_u32 s7, s53, 0
	s_waitcnt lgkmcnt(0)
	s_mul_i32 s20, s8, s10
	s_add_u32 s8, s52, 0x1200
	s_mul_i32 s20, s20, s9
	s_addc_u32 s9, s53, 0
	s_add_u32 s10, s52, 0x1300
	s_addc_u32 s11, s53, 0
	s_mov_b32 s21, 1
	v_mov_b32_e32 v17, 0
	s_branch .LBB0_61

.LBB0_112:
	s_load_dwordx16 s[16:31], s[0:1], 0x80
	s_cmp_gt_i32 s55, 1
	s_cselect_b64 s[0:1], -1, 0
	s_and_b64 s[2:3], s[14:15], s[0:1]
	s_andn2_b64 vcc, exec, s[2:3]
	s_waitcnt lgkmcnt(0)
	v_writelane_b32 v250, s16, 44
	s_nop 1
	v_writelane_b32 v250, s17, 45
	v_writelane_b32 v250, s18, 46
	v_writelane_b32 v250, s19, 47
	v_writelane_b32 v250, s20, 48
	v_writelane_b32 v250, s21, 49
	v_writelane_b32 v250, s22, 50
	v_writelane_b32 v250, s23, 51
	v_writelane_b32 v250, s24, 52
	v_writelane_b32 v250, s25, 53
	v_writelane_b32 v250, s26, 54
	v_writelane_b32 v250, s27, 55
	v_writelane_b32 v250, s28, 56
	v_writelane_b32 v250, s29, 57
	v_writelane_b32 v250, s30, 58
	v_writelane_b32 v250, s31, 59
	s_cbranch_vccnz .LBB0_162
	s_waitcnt vmcnt(0)
	s_barrier
	s_setprio 0
	s_mov_b64 s[2:3], exec
	v_readlane_b32 s4, v250, 5
	v_readlane_b32 s5, v250, 6
	s_and_b64 s[4:5], s[2:3], s[4:5]
	s_mov_b64 exec, s[4:5]
	s_cbranch_execz .LBB0_161
	s_add_i32 s4, 0, 0x27ff0
	v_mov_b32_e32 v1, s4
	s_waitcnt vmcnt(0) expcnt(0) lgkmcnt(0)
	ds_read_b32 v3, v1
	s_add_i32 s4, 0, 0x27ff4
	v_mov_b32_e32 v1, s4
	ds_read_b32 v1, v1
	s_waitcnt lgkmcnt(1)
	v_cmp_ne_u32_e32 vcc, 0, v3
	s_cbranch_vccnz .LBB0_129
	v_readlane_b32 s4, v250, 2
	v_readlane_b32 s5, v250, 3
	s_load_dwordx2 s[8:9], s[4:5], 0x4
	s_add_u32 s4, s52, 0x1000
	s_addc_u32 s5, s53, 0
	s_add_u32 s6, s52, 0x1100
	s_addc_u32 s7, s53, 0
	v_readlane_b32 s10, v250, 1
	s_waitcnt lgkmcnt(0)
	s_mul_i32 s18, s8, s10
	s_add_u32 s8, s52, 0x1200
	s_mul_i32 s18, s18, s9
	s_addc_u32 s9, s53, 0
	s_add_u32 s10, s52, 0x1300
	s_addc_u32 s11, s53, 0
	s_mov_b32 s19, 1
	v_mov_b32_e32 v17, 0
	s_branch .LBB0_117

.LBB0_181:
	s_cmpk_gt_i32 s33, 0x40f
	v_readfirstlane_b32 s39, v0
	s_barrier
	s_cbranch_scc1 .LBB0_193
	v_lshlrev_b32_e32 v1, 4, v0
	v_bfe_u32 v2, v0, 3, 25
	v_and_b32_e32 v5, 32, v0
	v_or_b32_e32 v2, 64, v2
	v_bfe_u32 v3, v0, 2, 4
	s_movk_i32 s0, 0x70
	v_bitop3_b32 v1, v1, v5, 48 bitop3:0x6c
	s_add_u32 s40, s6, 0x1170000
	v_and_or_b32 v4, v2, s0, v3
	v_and_or_b32 v1, v0, 64, v1
	s_addc_u32 s41, s7, 0
	v_lshl_or_b32 v132, v4, 9, v1
	v_lshrrev_b32_e32 v4, 5, v0
	v_lshrrev_b32_e32 v6, 1, v0
	s_add_u32 s42, s6, 0x130000
	v_and_b32_e32 v4, 4, v4
	v_bfe_u32 v5, v0, 2, 2
	v_and_b32_e32 v10, 24, v6
	s_addc_u32 s43, s7, 0
	v_or3_b32 v4, v4, v5, v10
	s_movk_i32 s0, 0x60
	s_ashr_i32 s45, s33, 31
	v_and_or_b32 v2, v2, s0, v4
	s_lshr_b32 s0, s45, 29
	s_add_i32 s0, s33, s0
	s_lshr_b32 s2, s39, 6
	s_ashr_i32 s3, s0, 3
	s_and_b32 s0, s0, -8
	s_lshr_b32 s1, s39, 8
	s_lshl_b32 s44, s2, 10
	s_sub_i32 s0, s33, s0
	s_cmp_lt_i32 s0, 0
	s_movk_i32 s46, 0x83
	s_cselect_b32 s8, s46, 0x82
	s_mul_i32 s0, s8, s0
	s_add_i32 s0, s0, s3
	s_mul_hi_i32 s3, s0, 0x7e07e07f
	s_lshr_b32 s8, s3, 31
	s_ashr_i32 s3, s3, 8
	s_add_i32 s3, s3, s8
	s_lshl_b32 s8, s3, 3
	s_mulk_i32 s3, 0x208
	s_sub_i32 s3, s0, s3
	s_bfe_u32 s0, s3, 0x3001c
	s_add_i32 s9, s3, s0
	s_sext_i32_i16 s0, s9
	s_and_b32 s9, s9, 0xfff8
	s_sub_i32 s3, s3, s9
	s_sext_i32_i16 s3, s3
	s_add_i32 s16, s8, s3
	s_ashr_i32 s17, s16, 31
	s_lshr_b32 s0, s0, 3
	s_lshl_b64 s[8:9], s[16:17], 17
	s_add_u32 s18, s40, s8
	s_addc_u32 s19, s41, s9
	s_bfe_i64 s[8:9], s[0:1], 0x100000
	s_lshl_b64 s[8:9], s[8:9], 17
	v_lshl_or_b32 v134, v2, 9, v1
	v_lshrrev_b32_e32 v2, 3, v0
	s_add_u32 s20, s42, s8
	v_and_or_b32 v3, v2, 48, v3
	v_and_or_b32 v2, v2, 32, v4
	s_addc_u32 s21, s43, s9
	s_add_i32 s17, s44, 0
	v_lshl_or_b32 v138, v2, 9, v1
	s_add_i32 m0, s17, 0x10000
	v_lshl_or_b32 v136, v3, 9, v1
	global_load_lds_dwordx4 v138, s[20:21]
	s_add_i32 m0, s17, 0x12000
	s_add_i32 s47, s17, 0x2000
	global_load_lds_dwordx4 v134, s[20:21]
	s_mov_b32 m0, s17
	s_add_u32 s8, s20, 0x10000
	global_load_lds_dwordx4 v136, s[18:19]
	s_mov_b32 m0, s47
	s_addc_u32 s9, s21, 0
	global_load_lds_dwordx4 v132, s[18:19]
	s_add_i32 m0, s17, 0x14000
	v_mov_b32_e32 v139, 0
	global_load_lds_dwordx4 v138, s[8:9]
	s_add_i32 m0, s17, 0x16000
	v_mov_b32_e32 v135, v139
	global_load_lds_dwordx4 v134, s[8:9]
	s_add_u32 s8, s18, 0x10000
	s_addc_u32 s9, s19, 0
	s_add_i32 s48, s17, 0x4000
	s_mov_b32 m0, s48
	s_add_i32 s49, s17, 0x6000
	global_load_lds_dwordx4 v136, s[8:9]
	s_mov_b32 m0, s49
	v_mov_b32_e32 v137, v139
	global_load_lds_dwordx4 v132, s[8:9]
	v_mov_b32_e32 v133, v139
	s_mov_b32 s50, 0
	v_lshl_add_u64 v[8:9], s[20:21], 0, v[138:139]
	v_lshl_add_u64 v[6:7], s[20:21], 0, v[134:135]
	v_lshl_add_u64 v[4:5], s[18:19], 0, v[136:137]
	s_setprio 1
	s_cmp_lg_u32 s1, 1
	v_lshl_add_u64 v[2:3], s[18:19], 0, v[132:133]
	s_cbranch_scc1 .LBB0_184
	s_barrier
	s_setprio 0

.LBB0_188:
	s_add_u32 s27, s18, s26
	s_addc_u32 s37, s19, 0
	s_add_u32 s30, s27, 0x100
	s_addc_u32 s31, s37, 0
	s_and_b64 s[28:29], s[24:25], exec
	s_cselect_b32 s31, s11, s31
	s_cselect_b32 s30, s57, s30
	s_add_u32 s26, s20, s26
	s_addc_u32 s28, s21, 0
	s_add_u32 s26, s26, 0x100
	s_addc_u32 s28, s28, 0
	s_and_b64 s[24:25], s[24:25], exec
	s_cselect_b32 s35, s9, s28
	s_cselect_b32 s34, s58, s26
	s_add_u32 s36, s27, 0x10080
	s_addc_u32 s37, s37, 0
	s_add_i32 s68, s54, s44
	s_add_i32 m0, s17, 0xc000
	s_add_i32 s69, s17, 0xe000
	s_add_i32 s67, s68, 0x2000
	s_add_u32 s28, s34, 0x10000
	s_addc_u32 s29, s35, 0
	s_add_i32 s66, s55, s44
	ds_read_b128 v[144:147], v151
	ds_read_b128 v[156:159], v151 offset:1024
	ds_read_b128 v[160:163], v151 offset:2048
	ds_read_b128 v[164:167], v151 offset:3072
	s_add_i32 s65, s66, 0x2000
	s_add_i32 s64, 0, 0x18000
	s_add_u32 s26, s30, 0x10000
	s_addc_u32 s27, s31, 0
	s_add_i32 s63, s64, s44
	s_add_i32 s62, 0, 0x1c000
	s_add_i32 s61, s63, 0x2000
	s_add_u32 s24, s34, 0x10080
	s_addc_u32 s25, s35, 0
	s_add_i32 s60, s62, s44
	s_add_i32 s59, s60, 0x2000
	v_lshl_add_u64 v[148:149], s[36:37], 0, v[136:137]
	ds_read_b128 v[168:171], v152
	ds_read_b128 v[172:175], v152 offset:1024
	ds_read_b128 v[176:179], v152 offset:2048
	ds_read_b128 v[180:183], v152 offset:3072
	ds_read_b128 v[184:187], v152 offset:4096
	ds_read_b128 v[192:195], v152 offset:5120
	ds_read_b128 v[196:199], v152 offset:6144
	ds_read_b128 v[200:203], v152 offset:7168
	global_load_lds_dwordx4 v[148:149], off
	v_lshl_add_u64 v[148:149], s[36:37], 0, v[132:133]
	s_mov_b32 m0, s69
	s_nop 0
	global_load_lds_dwordx4 v[148:149], off
	s_waitcnt lgkmcnt(8)
	s_barrier
	s_waitcnt lgkmcnt(0)
	s_waitcnt lgkmcnt(0)
	v_mfma_f32_16x16x32_bf16 v[126:129], v[144:147], v[168:171], v[126:129]
	v_mfma_f32_16x16x32_bf16 v[122:125], v[160:163], v[168:171], v[122:125]
	v_mfma_f32_16x16x32_bf16 v[110:113], v[144:147], v[176:179], v[110:113]
	v_mfma_f32_16x16x32_bf16 v[106:109], v[160:163], v[176:179], v[106:109]
	v_mfma_f32_16x16x32_bf16 v[94:97], v[144:147], v[184:187], v[94:97]
	v_mfma_f32_16x16x32_bf16 v[90:93], v[160:163], v[184:187], v[90:93]
	v_mfma_f32_16x16x32_bf16 v[78:81], v[144:147], v[196:199], v[78:81]
	v_mfma_f32_16x16x32_bf16 v[74:77], v[160:163], v[196:199], v[74:77]
	v_mfma_f32_16x16x32_bf16 v[126:129], v[156:159], v[172:175], v[126:129]
	v_mfma_f32_16x16x32_bf16 v[122:125], v[164:167], v[172:175], v[122:125]
	v_mfma_f32_16x16x32_bf16 v[110:113], v[156:159], v[180:183], v[110:113]
	v_mfma_f32_16x16x32_bf16 v[106:109], v[164:167], v[180:183], v[106:109]
	v_mfma_f32_16x16x32_bf16 v[94:97], v[156:159], v[192:195], v[94:97]
	v_mfma_f32_16x16x32_bf16 v[90:93], v[164:167], v[192:195], v[90:93]
	v_mfma_f32_16x16x32_bf16 v[78:81], v[156:159], v[200:203], v[78:81]
	v_mfma_f32_16x16x32_bf16 v[74:77], v[164:167], v[200:203], v[74:77]
	s_barrier
	s_mov_b32 m0, s68
	v_lshl_add_u64 v[148:149], s[34:35], 0, v[138:139]
	ds_read_b128 v[204:207], v153
	ds_read_b128 v[208:211], v153 offset:1024
	ds_read_b128 v[212:215], v153 offset:2048
	ds_read_b128 v[216:219], v153 offset:3072
	global_load_lds_dwordx4 v[148:149], off
	v_lshl_add_u64 v[188:189], s[34:35], 0, v[134:135]
	s_mov_b32 m0, s67
	s_nop 0
	global_load_lds_dwordx4 v[188:189], off
	s_barrier
	s_waitcnt lgkmcnt(0)
	s_waitcnt lgkmcnt(0)
	v_mfma_f32_16x16x32_bf16 v[118:121], v[204:207], v[168:171], v[118:121]
	v_mfma_f32_16x16x32_bf16 v[114:117], v[212:215], v[168:171], v[114:117]
	v_mfma_f32_16x16x32_bf16 v[102:105], v[204:207], v[176:179], v[102:105]
	v_mfma_f32_16x16x32_bf16 v[98:101], v[212:215], v[176:179], v[98:101]
	v_mfma_f32_16x16x32_bf16 v[86:89], v[204:207], v[184:187], v[86:89]
	v_mfma_f32_16x16x32_bf16 v[82:85], v[212:215], v[184:187], v[82:85]
	v_mfma_f32_16x16x32_bf16 v[70:73], v[204:207], v[196:199], v[70:73]
	v_mfma_f32_16x16x32_bf16 v[66:69], v[212:215], v[196:199], v[66:69]
	v_mfma_f32_16x16x32_bf16 v[118:121], v[208:211], v[172:175], v[118:121]
	v_mfma_f32_16x16x32_bf16 v[114:117], v[216:219], v[172:175], v[114:117]
	v_mfma_f32_16x16x32_bf16 v[102:105], v[208:211], v[180:183], v[102:105]
	v_mfma_f32_16x16x32_bf16 v[98:101], v[216:219], v[180:183], v[98:101]
	v_mfma_f32_16x16x32_bf16 v[86:89], v[208:211], v[192:195], v[86:89]
	v_mfma_f32_16x16x32_bf16 v[82:85], v[216:219], v[192:195], v[82:85]
	v_mfma_f32_16x16x32_bf16 v[70:73], v[208:211], v[200:203], v[70:73]
	v_mfma_f32_16x16x32_bf16 v[66:69], v[216:219], v[200:203], v[66:69]
	s_mov_b32 m0, s17
	v_lshl_add_u64 v[190:191], s[30:31], 0, v[136:137]
	s_barrier
	ds_read_b128 v[168:171], v152 offset:16384
	ds_read_b128 v[172:175], v152 offset:17408
	ds_read_b128 v[176:179], v152 offset:18432
	ds_read_b128 v[180:183], v152 offset:19456
	ds_read_b128 v[184:187], v152 offset:20480
	ds_read_b128 v[192:195], v152 offset:21504
	ds_read_b128 v[196:199], v152 offset:22528
	ds_read_b128 v[200:203], v152 offset:23552
	global_load_lds_dwordx4 v[190:191], off
	v_lshl_add_u64 v[220:221], s[30:31], 0, v[132:133]
	s_mov_b32 m0, s47
	s_nop 0
	global_load_lds_dwordx4 v[220:221], off
	s_barrier
	s_waitcnt lgkmcnt(0)
	s_waitcnt lgkmcnt(0)
	v_mfma_f32_16x16x32_bf16 v[62:65], v[144:147], v[168:171], v[62:65]
	v_mfma_f32_16x16x32_bf16 v[58:61], v[160:163], v[168:171], v[58:61]
	v_mfma_f32_16x16x32_bf16 v[46:49], v[144:147], v[176:179], v[46:49]
	v_mfma_f32_16x16x32_bf16 v[42:45], v[160:163], v[176:179], v[42:45]
	v_mfma_f32_16x16x32_bf16 v[30:33], v[144:147], v[184:187], v[30:33]
	v_mfma_f32_16x16x32_bf16 v[26:29], v[160:163], v[184:187], v[26:29]
	v_mfma_f32_16x16x32_bf16 v[14:17], v[144:147], v[196:199], v[14:17]
	v_mfma_f32_16x16x32_bf16 v[10:13], v[160:163], v[196:199], v[10:13]
	v_mfma_f32_16x16x32_bf16 v[62:65], v[156:159], v[172:175], v[62:65]
	v_mfma_f32_16x16x32_bf16 v[58:61], v[164:167], v[172:175], v[58:61]
	v_mfma_f32_16x16x32_bf16 v[46:49], v[156:159], v[180:183], v[46:49]
	v_mfma_f32_16x16x32_bf16 v[42:45], v[164:167], v[180:183], v[42:45]
	v_mfma_f32_16x16x32_bf16 v[30:33], v[156:159], v[192:195], v[30:33]
	v_mfma_f32_16x16x32_bf16 v[26:29], v[164:167], v[192:195], v[26:29]
	v_mfma_f32_16x16x32_bf16 v[14:17], v[156:159], v[200:203], v[14:17]
	v_mfma_f32_16x16x32_bf16 v[10:13], v[164:167], v[200:203], v[10:13]
	s_barrier
	s_mov_b32 m0, s66
	v_lshl_add_u64 v[144:145], s[28:29], 0, v[138:139]
	global_load_lds_dwordx4 v[144:145], off
	v_lshl_add_u64 v[144:145], s[28:29], 0, v[134:135]
	s_mov_b32 m0, s65
	s_nop 0
	global_load_lds_dwordx4 v[144:145], off
	s_waitcnt vmcnt(6)
	s_barrier
	v_mfma_f32_16x16x32_bf16 v[54:57], v[204:207], v[168:171], v[54:57]
	v_mfma_f32_16x16x32_bf16 v[50:53], v[212:215], v[168:171], v[50:53]
	v_mfma_f32_16x16x32_bf16 v[38:41], v[204:207], v[176:179], v[38:41]
	v_mfma_f32_16x16x32_bf16 v[34:37], v[212:215], v[176:179], v[34:37]
	v_mfma_f32_16x16x32_bf16 v[22:25], v[204:207], v[184:187], v[22:25]
	v_mfma_f32_16x16x32_bf16 v[18:21], v[212:215], v[184:187], v[18:21]
	v_mfma_f32_16x16x32_bf16 v[6:9], v[204:207], v[196:199], v[6:9]
	v_mfma_f32_16x16x32_bf16 v[2:5], v[212:215], v[196:199], v[2:5]
	v_mfma_f32_16x16x32_bf16 v[54:57], v[208:211], v[172:175], v[54:57]
	v_mfma_f32_16x16x32_bf16 v[50:53], v[216:219], v[172:175], v[50:53]
	v_mfma_f32_16x16x32_bf16 v[38:41], v[208:211], v[180:183], v[38:41]
	v_mfma_f32_16x16x32_bf16 v[34:37], v[216:219], v[180:183], v[34:37]
	v_mfma_f32_16x16x32_bf16 v[22:25], v[208:211], v[192:195], v[22:25]
	v_mfma_f32_16x16x32_bf16 v[18:21], v[216:219], v[192:195], v[18:21]
	v_mfma_f32_16x16x32_bf16 v[6:9], v[208:211], v[200:203], v[6:9]
	v_mfma_f32_16x16x32_bf16 v[2:5], v[216:219], v[200:203], v[2:5]
	v_add_u32_e32 v164, s64, v131
	s_barrier
	ds_read_b128 v[144:147], v164
	ds_read_b128 v[156:159], v164 offset:1024
	ds_read_b128 v[160:163], v164 offset:2048
	ds_read_b128 v[164:167], v164 offset:3072
	s_mov_b32 m0, s48
	v_lshl_add_u64 v[204:205], s[26:27], 0, v[136:137]
	ds_read_b128 v[168:171], v152 offset:32768
	ds_read_b128 v[172:175], v152 offset:33792
	ds_read_b128 v[176:179], v152 offset:34816
	ds_read_b128 v[180:183], v152 offset:35840
	ds_read_b128 v[184:187], v152 offset:36864
	ds_read_b128 v[192:195], v152 offset:37888
	ds_read_b128 v[196:199], v152 offset:38912
	ds_read_b128 v[200:203], v152 offset:39936
	global_load_lds_dwordx4 v[204:205], off
	v_lshl_add_u64 v[204:205], s[26:27], 0, v[132:133]
	s_mov_b32 m0, s49
	s_nop 0
	global_load_lds_dwordx4 v[204:205], off
	s_waitcnt lgkmcnt(8)
	s_barrier
	s_waitcnt lgkmcnt(0)
	s_waitcnt lgkmcnt(0)
	v_mfma_f32_16x16x32_bf16 v[126:129], v[144:147], v[168:171], v[126:129]
	v_mfma_f32_16x16x32_bf16 v[122:125], v[160:163], v[168:171], v[122:125]
	v_mfma_f32_16x16x32_bf16 v[110:113], v[144:147], v[176:179], v[110:113]
	v_mfma_f32_16x16x32_bf16 v[106:109], v[160:163], v[176:179], v[106:109]
	v_mfma_f32_16x16x32_bf16 v[94:97], v[144:147], v[184:187], v[94:97]
	v_mfma_f32_16x16x32_bf16 v[90:93], v[160:163], v[184:187], v[90:93]
	v_mfma_f32_16x16x32_bf16 v[78:81], v[144:147], v[196:199], v[78:81]
	v_mfma_f32_16x16x32_bf16 v[74:77], v[160:163], v[196:199], v[74:77]
	v_mfma_f32_16x16x32_bf16 v[126:129], v[156:159], v[172:175], v[126:129]
	v_mfma_f32_16x16x32_bf16 v[122:125], v[164:167], v[172:175], v[122:125]
	v_mfma_f32_16x16x32_bf16 v[110:113], v[156:159], v[180:183], v[110:113]
	v_mfma_f32_16x16x32_bf16 v[106:109], v[164:167], v[180:183], v[106:109]
	v_mfma_f32_16x16x32_bf16 v[94:97], v[156:159], v[192:195], v[94:97]
	v_mfma_f32_16x16x32_bf16 v[90:93], v[164:167], v[192:195], v[90:93]
	v_mfma_f32_16x16x32_bf16 v[78:81], v[156:159], v[200:203], v[78:81]
	v_mfma_f32_16x16x32_bf16 v[74:77], v[164:167], v[200:203], v[74:77]
	s_barrier
	s_mov_b32 m0, s63
	v_add_u32_e32 v216, s62, v131
	v_lshl_add_u64 v[148:149], v[148:149], 0, s[2:3]
	ds_read_b128 v[204:207], v216
	ds_read_b128 v[208:211], v216 offset:1024
	ds_read_b128 v[212:215], v216 offset:2048
	ds_read_b128 v[216:219], v216 offset:3072
	global_load_lds_dwordx4 v[148:149], off
	v_lshl_add_u64 v[148:149], v[188:189], 0, s[2:3]
	s_mov_b32 m0, s61
	s_nop 0
	global_load_lds_dwordx4 v[148:149], off
	s_barrier
	s_waitcnt lgkmcnt(0)
	s_waitcnt lgkmcnt(0)
	v_mfma_f32_16x16x32_bf16 v[118:121], v[204:207], v[168:171], v[118:121]
	v_mfma_f32_16x16x32_bf16 v[114:117], v[212:215], v[168:171], v[114:117]
	v_mfma_f32_16x16x32_bf16 v[102:105], v[204:207], v[176:179], v[102:105]
	v_mfma_f32_16x16x32_bf16 v[98:101], v[212:215], v[176:179], v[98:101]
	v_mfma_f32_16x16x32_bf16 v[86:89], v[204:207], v[184:187], v[86:89]
	v_mfma_f32_16x16x32_bf16 v[82:85], v[212:215], v[184:187], v[82:85]
	v_mfma_f32_16x16x32_bf16 v[70:73], v[204:207], v[196:199], v[70:73]
	v_mfma_f32_16x16x32_bf16 v[66:69], v[212:215], v[196:199], v[66:69]
	v_mfma_f32_16x16x32_bf16 v[118:121], v[208:211], v[172:175], v[118:121]
	v_mfma_f32_16x16x32_bf16 v[114:117], v[216:219], v[172:175], v[114:117]
	v_mfma_f32_16x16x32_bf16 v[102:105], v[208:211], v[180:183], v[102:105]
	v_mfma_f32_16x16x32_bf16 v[98:101], v[216:219], v[180:183], v[98:101]
	v_mfma_f32_16x16x32_bf16 v[86:89], v[208:211], v[192:195], v[86:89]
	v_mfma_f32_16x16x32_bf16 v[82:85], v[216:219], v[192:195], v[82:85]
	v_mfma_f32_16x16x32_bf16 v[70:73], v[208:211], v[200:203], v[70:73]
	v_mfma_f32_16x16x32_bf16 v[66:69], v[216:219], v[200:203], v[66:69]
	s_mov_b32 m0, s51
	v_lshl_add_u64 v[148:149], v[190:191], 0, s[2:3]
	s_barrier
	ds_read_b128 v[168:171], v152 offset:49152
	ds_read_b128 v[172:175], v152 offset:50176
	ds_read_b128 v[176:179], v152 offset:51200
	ds_read_b128 v[180:183], v152 offset:52224
	ds_read_b128 v[184:187], v152 offset:53248
	ds_read_b128 v[192:195], v152 offset:54272
	ds_read_b128 v[196:199], v152 offset:55296
	ds_read_b128 v[200:203], v152 offset:56320
	global_load_lds_dwordx4 v[148:149], off
	v_lshl_add_u64 v[148:149], v[220:221], 0, s[2:3]
	s_mov_b32 m0, s52
	s_nop 0
	global_load_lds_dwordx4 v[148:149], off
	s_barrier
	s_waitcnt lgkmcnt(0)
	s_waitcnt lgkmcnt(0)
	v_mfma_f32_16x16x32_bf16 v[62:65], v[144:147], v[168:171], v[62:65]
	v_mfma_f32_16x16x32_bf16 v[58:61], v[160:163], v[168:171], v[58:61]
	v_mfma_f32_16x16x32_bf16 v[46:49], v[144:147], v[176:179], v[46:49]
	v_mfma_f32_16x16x32_bf16 v[42:45], v[160:163], v[176:179], v[42:45]
	v_mfma_f32_16x16x32_bf16 v[30:33], v[144:147], v[184:187], v[30:33]
	v_mfma_f32_16x16x32_bf16 v[26:29], v[160:163], v[184:187], v[26:29]
	v_mfma_f32_16x16x32_bf16 v[14:17], v[144:147], v[196:199], v[14:17]
	v_mfma_f32_16x16x32_bf16 v[10:13], v[160:163], v[196:199], v[10:13]
	v_mfma_f32_16x16x32_bf16 v[62:65], v[156:159], v[172:175], v[62:65]
	v_mfma_f32_16x16x32_bf16 v[58:61], v[164:167], v[172:175], v[58:61]
	v_mfma_f32_16x16x32_bf16 v[46:49], v[156:159], v[180:183], v[46:49]
	v_mfma_f32_16x16x32_bf16 v[42:45], v[164:167], v[180:183], v[42:45]
	v_mfma_f32_16x16x32_bf16 v[30:33], v[156:159], v[192:195], v[30:33]
	v_mfma_f32_16x16x32_bf16 v[26:29], v[164:167], v[192:195], v[26:29]
	v_mfma_f32_16x16x32_bf16 v[14:17], v[156:159], v[200:203], v[14:17]
	v_mfma_f32_16x16x32_bf16 v[10:13], v[164:167], v[200:203], v[10:13]
	s_barrier
	s_mov_b32 m0, s60
	v_lshl_add_u64 v[144:145], s[24:25], 0, v[138:139]
	global_load_lds_dwordx4 v[144:145], off
	v_lshl_add_u64 v[144:145], s[24:25], 0, v[134:135]
	s_mov_b32 m0, s59
	s_nop 0
	global_load_lds_dwordx4 v[144:145], off
	s_waitcnt vmcnt(6)
	s_barrier
	v_mfma_f32_16x16x32_bf16 v[54:57], v[204:207], v[168:171], v[54:57]
	v_mfma_f32_16x16x32_bf16 v[50:53], v[212:215], v[168:171], v[50:53]
	v_mfma_f32_16x16x32_bf16 v[38:41], v[204:207], v[176:179], v[38:41]
	v_mfma_f32_16x16x32_bf16 v[34:37], v[212:215], v[176:179], v[34:37]
	v_mfma_f32_16x16x32_bf16 v[22:25], v[204:207], v[184:187], v[22:25]
	v_mfma_f32_16x16x32_bf16 v[18:21], v[212:215], v[184:187], v[18:21]
	v_mfma_f32_16x16x32_bf16 v[6:9], v[204:207], v[196:199], v[6:9]
	v_mfma_f32_16x16x32_bf16 v[2:5], v[212:215], v[196:199], v[2:5]
	v_mfma_f32_16x16x32_bf16 v[54:57], v[208:211], v[172:175], v[54:57]
	v_mfma_f32_16x16x32_bf16 v[50:53], v[216:219], v[172:175], v[50:53]
	v_mfma_f32_16x16x32_bf16 v[38:41], v[208:211], v[180:183], v[38:41]
	v_mfma_f32_16x16x32_bf16 v[34:37], v[216:219], v[180:183], v[34:37]
	v_mfma_f32_16x16x32_bf16 v[22:25], v[208:211], v[192:195], v[22:25]
	v_mfma_f32_16x16x32_bf16 v[18:21], v[216:219], v[192:195], v[18:21]
	v_mfma_f32_16x16x32_bf16 v[6:9], v[208:211], v[200:203], v[6:9]
	v_mfma_f32_16x16x32_bf16 v[2:5], v[216:219], v[200:203], v[2:5]
	s_movk_i32 s26, 0x100
	s_andn2_b64 vcc, exec, s[22:23]
	s_mov_b64 s[24:25], -1
	s_mov_b64 s[22:23], 0
	s_barrier
	s_cbranch_vccz .LBB0_188
	v_lshl_add_u32 v144, s16, 8, v1
	v_readlane_b32 s60, v250, 44
	v_ashrrev_i32_e32 v145, 31, v144
	v_readlane_b32 s61, v250, 45
	s_lshl_b32 s9, s56, 8
	s_cmp_eq_u32 s56, 64
	v_lshl_add_u64 v[146:147], v[144:145], 2, s[60:61]
	global_load_dword v168, v[146:147], off
	global_load_dword v178, v[146:147], off offset:64
	global_load_dword v179, v[146:147], off offset:128
	global_load_dword v180, v[146:147], off offset:192
	global_load_dword v181, v[146:147], off offset:512
	global_load_dword v182, v[146:147], off offset:576
	global_load_dword v183, v[146:147], off offset:640
	global_load_dword v184, v[146:147], off offset:704
	s_cselect_b64 vcc, -1, 0
	s_mov_b32 s11, 0x17c0000
	s_and_b64 s[18:19], vcc, exec
	s_cselect_b32 s16, 0, s9
	s_cselect_b32 s11, s11, 0x22940000
	s_cselect_b32 s9, 8, 14
	v_or_b32_e32 v164, s16, v150
	s_add_u32 s18, s6, s11
	v_lshlrev_b64 v[156:157], s9, v[144:145]
	s_addc_u32 s19, s7, 0
	v_ashrrev_i32_e32 v165, 31, v164
	v_cvt_f32_i32_e32 v145, v164
	v_or_b32_e32 v158, 1, v164
	v_or_b32_e32 v159, 2, v164
	v_or_b32_e32 v161, 4, v164
	v_or_b32_e32 v166, 7, v164
	v_or_b32_e32 v160, 3, v164
	v_or_b32_e32 v162, 5, v164
	v_or_b32_e32 v163, 6, v164
	v_or_b32_e32 v167, 0x80, v164
	v_lshl_add_u64 v[148:149], v[164:165], 1, s[18:19]
	v_cvt_f32_i32_e32 v158, v158
	v_cvt_f32_i32_e32 v159, v159
	v_cvt_f32_i32_e32 v165, v161
	v_cvt_f32_i32_e32 v172, v166
	v_cvt_f32_i32_e32 v160, v160
	v_cvt_f32_i32_e32 v170, v162
	v_cvt_f32_i32_e32 v171, v163
	v_cvt_f32_i32_e32 v173, v167
	v_cndmask_b32_e32 v169, v154, v155, vcc
	v_mul_f32_e64 v163, v169, -v145
	v_lshl_add_u64 v[166:167], v[156:157], 1, v[148:149]
	v_mul_f32_e64 v162, v169, -v158
	v_mul_f32_e64 v161, v169, -v159
	v_mul_f32_e64 v159, v169, -v165
	v_mul_f32_e64 v156, v169, -v172
	v_mul_f32_e64 v160, v169, -v160
	v_mul_f32_e64 v158, v169, -v170
	v_mul_f32_e64 v157, v169, -v171
	v_mul_f32_e64 v145, v169, -v173
	s_and_b64 vcc, exec, s[0:1]
	s_mov_b32 s56, s8
	s_mov_b32 s16, s10
	s_mov_b64 s[20:21], s[14:15]
	s_mov_b64 s[18:19], s[12:13]
	v_readlane_b32 s62, v250, 46
	v_readlane_b32 s63, v250, 47
	v_readlane_b32 s64, v250, 48
	v_readlane_b32 s65, v250, 49
	v_readlane_b32 s66, v250, 50
	v_readlane_b32 s67, v250, 51
	v_readlane_b32 s68, v250, 52
	v_readlane_b32 s69, v250, 53
	v_readlane_b32 s70, v250, 54
	v_readlane_b32 s71, v250, 55
	v_readlane_b32 s72, v250, 56
	v_readlane_b32 s73, v250, 57
	v_readlane_b32 s74, v250, 58
	v_readlane_b32 s75, v250, 59
	s_waitcnt vmcnt(0)
	v_mul_f32_e64 v165, v163, |v168|
	v_mul_f32_e64 v170, v162, |v168|
	v_mul_f32_e64 v173, v159, |v168|
	v_mul_f32_e64 v176, v156, |v168|
	v_mul_f32_e32 v165, 0x3fb8aa3b, v165
	v_mul_f32_e64 v171, v161, |v168|
	v_mul_f32_e64 v172, v160, |v168|
	v_mul_f32_e64 v174, v158, |v168|
	v_mul_f32_e64 v175, v157, |v168|
	v_mul_f32_e32 v170, 0x3fb8aa3b, v170
	v_mul_f32_e32 v173, 0x3fb8aa3b, v173
	v_mul_f32_e32 v176, 0x3fb8aa3b, v176
	v_exp_f32_e32 v165, v165
	v_mul_f32_e64 v177, v145, |v168|
	v_mul_f32_e32 v171, 0x3fb8aa3b, v171
	v_mul_f32_e32 v172, 0x3fb8aa3b, v172
	v_mul_f32_e32 v174, 0x3fb8aa3b, v174
	v_mul_f32_e32 v175, 0x3fb8aa3b, v175
	v_exp_f32_e32 v170, v170
	v_exp_f32_e32 v173, v173
	v_exp_f32_e32 v176, v176
	v_mul_f32_e32 v177, 0x3fb8aa3b, v177
	v_exp_f32_e32 v171, v171
	v_exp_f32_e32 v172, v172
	v_exp_f32_e32 v174, v174
	v_exp_f32_e32 v175, v175
	v_exp_f32_e32 v177, v177
	v_add_f32_e32 v165, 0x3d4ccccd, v165
	v_add_f32_e32 v170, 0x3d4ccccd, v170
	v_add_f32_e32 v173, 0x3d4ccccd, v173
	v_add_f32_e32 v176, 0x3d4ccccd, v176
	v_mul_f32_e32 v126, v126, v165
	v_add_f32_e32 v171, 0x3d4ccccd, v171
	v_add_f32_e32 v172, 0x3d4ccccd, v172
	v_add_f32_e32 v174, 0x3d4ccccd, v174
	v_add_f32_e32 v175, 0x3d4ccccd, v175
	v_mul_f32_e32 v127, v127, v170
	v_mul_f32_e32 v165, v122, v173
	v_mul_f32_e32 v125, v125, v176
	v_cvt_pk_bf16_f32 v122, v126, v127
	v_or_b32_e32 v126, 0x81, v164
	v_mul_f32_e32 v128, v128, v171
	v_mul_f32_e32 v129, v129, v172
	v_mul_f32_e32 v170, v123, v174
	v_mul_f32_e32 v171, v124, v175
	v_cvt_pk_bf16_f32 v123, v128, v129
	v_cvt_pk_bf16_f32 v124, v165, v170
	v_cvt_pk_bf16_f32 v125, v171, v125
	v_cvt_f32_i32_e32 v126, v126
	global_store_dwordx4 v[166:167], v[122:125], off
	v_or_b32_e32 v129, 0x86, v164
	v_cvt_f32_i32_e32 v129, v129
	v_add_f32_e32 v122, 0x3d4ccccd, v177
	v_mul_f32_e32 v124, v118, v122
	v_or_b32_e32 v122, 0x82, v164
	v_cvt_f32_i32_e32 v122, v122
	v_mul_f32_e64 v118, v169, -v126
	v_mul_f32_e64 v123, v118, |v168|
	v_mul_f32_e32 v123, 0x3fb8aa3b, v123
	v_mul_f32_e64 v122, v169, -v122
	v_exp_f32_e32 v123, v123
	v_mul_f32_e64 v125, v122, |v168|
	v_or_b32_e32 v126, 0x83, v164
	v_mul_f32_e32 v125, 0x3fb8aa3b, v125
	v_cvt_f32_i32_e32 v126, v126
	v_exp_f32_e32 v125, v125
	v_add_f32_e32 v123, 0x3d4ccccd, v123
	v_mul_f32_e32 v127, v119, v123
	v_mul_f32_e64 v119, v169, -v126
	v_add_f32_e32 v123, 0x3d4ccccd, v125
	v_mul_f32_e64 v125, v119, |v168|
	v_mul_f32_e32 v125, 0x3fb8aa3b, v125
	v_exp_f32_e32 v125, v125
	v_or_b32_e32 v126, 0x84, v164
	v_cvt_f32_i32_e32 v126, v126
	v_mul_f32_e32 v128, v120, v123
	v_add_f32_e32 v120, 0x3d4ccccd, v125
	v_mul_f32_e32 v125, v121, v120
	v_mul_f32_e64 v120, v169, -v126
	v_mul_f32_e64 v123, v120, |v168|
	v_mul_f32_e32 v123, 0x3fb8aa3b, v123
	v_exp_f32_e32 v123, v123
	v_or_b32_e32 v121, 0x85, v164
	v_cvt_f32_i32_e32 v121, v121
	v_cvt_pk_bf16_f32 v124, v124, v127
	v_add_f32_e32 v123, 0x3d4ccccd, v123
	v_mul_f32_e32 v165, v114, v123
	v_or_b32_e32 v114, 0x87, v164
	v_cvt_f32_i32_e32 v114, v114
	v_mul_f32_e64 v121, v169, -v121
	v_mul_f32_e64 v126, v121, |v168|
	v_mul_f32_e64 v123, v169, -v129
	v_mul_f32_e32 v126, 0x3fb8aa3b, v126
	v_mul_f32_e64 v129, v123, |v168|
	v_mul_f32_e64 v114, v169, -v114
	v_exp_f32_e32 v126, v126
	v_mul_f32_e32 v129, 0x3fb8aa3b, v129
	v_mul_f32_e64 v164, v114, |v168|
	v_exp_f32_e32 v129, v129
	v_mul_f32_e32 v164, 0x3fb8aa3b, v164
	v_exp_f32_e32 v164, v164
	v_add_f32_e32 v126, 0x3d4ccccd, v126
	v_mul_f32_e32 v115, v115, v126
	v_add_f32_e32 v126, 0x3d4ccccd, v129
	v_mul_f32_e32 v116, v116, v126
	v_add_f32_e32 v126, 0x3d4ccccd, v164
	v_mul_f32_e32 v117, v117, v126
	v_cvt_pk_bf16_f32 v125, v128, v125
	v_cvt_pk_bf16_f32 v126, v165, v115
	v_cvt_pk_bf16_f32 v127, v116, v117
	global_store_dwordx4 v[166:167], v[124:127], off offset:256
	s_nop 1
	v_mov_b32_e32 v115, v178
	v_or_b32_e32 v116, 16, v144
	v_ashrrev_i32_e32 v117, 31, v116
	v_lshlrev_b64 v[116:117], s9, v[116:117]
	v_lshl_add_u64 v[116:117], v[116:117], 1, v[148:149]
	s_nop 0
	v_mul_f32_e64 v125, v162, |v115|
	v_mul_f32_e64 v124, v163, |v115|
	v_mul_f32_e32 v125, 0x3fb8aa3b, v125
	v_mul_f32_e32 v124, 0x3fb8aa3b, v124
	v_exp_f32_e32 v125, v125
	v_exp_f32_e32 v124, v124
	v_mul_f32_e64 v128, v159, |v115|
	v_mul_f32_e64 v126, v161, |v115|
	v_add_f32_e32 v125, 0x3d4ccccd, v125
	v_mul_f32_e32 v128, 0x3fb8aa3b, v128
	v_add_f32_e32 v124, 0x3d4ccccd, v124
	v_mul_f32_e32 v111, v111, v125
	v_mul_f32_e64 v125, v158, |v115|
	v_mul_f32_e32 v126, 0x3fb8aa3b, v126
	v_mul_f32_e32 v110, v110, v124
	v_exp_f32_e32 v124, v128
	v_mul_f32_e32 v125, 0x3fb8aa3b, v125
	v_exp_f32_e32 v126, v126
	v_exp_f32_e32 v125, v125
	v_mul_f32_e64 v127, v160, |v115|
	v_add_f32_e32 v124, 0x3d4ccccd, v124
	v_mul_f32_e32 v127, 0x3fb8aa3b, v127
	v_add_f32_e32 v126, 0x3d4ccccd, v126
	v_mul_f32_e32 v124, v106, v124
	v_add_f32_e32 v106, 0x3d4ccccd, v125
	v_mul_f32_e64 v125, v157, |v115|
	v_exp_f32_e32 v127, v127
	v_mul_f32_e32 v112, v112, v126
	v_mul_f32_e32 v125, 0x3fb8aa3b, v125
	v_mul_f32_e64 v126, v156, |v115|
	v_exp_f32_e32 v125, v125
	v_mul_f32_e32 v126, 0x3fb8aa3b, v126
	v_exp_f32_e32 v126, v126
	v_add_f32_e32 v127, 0x3d4ccccd, v127
	v_mul_f32_e32 v113, v113, v127
	v_mul_f32_e32 v127, v107, v106
	v_add_f32_e32 v106, 0x3d4ccccd, v125
	v_mul_f32_e32 v125, v108, v106
	v_add_f32_e32 v106, 0x3d4ccccd, v126
	v_mul_f32_e32 v109, v109, v106
	v_cvt_pk_bf16_f32 v106, v110, v111
	v_mul_f32_e64 v110, v145, |v115|
	v_cvt_pk_bf16_f32 v107, v112, v113
	v_mul_f32_e32 v110, 0x3fb8aa3b, v110
	v_mul_f32_e64 v111, v118, |v115|
	v_cvt_pk_bf16_f32 v108, v124, v127
	v_cvt_pk_bf16_f32 v109, v125, v109
	v_exp_f32_e32 v110, v110
	v_mul_f32_e32 v111, 0x3fb8aa3b, v111
	global_store_dwordx4 v[116:117], v[106:109], off
	v_exp_f32_e32 v111, v111
	s_nop 0
	v_mul_f32_e64 v107, v122, |v115|
	v_mul_f32_e32 v107, 0x3fb8aa3b, v107
	v_mul_f32_e64 v108, v119, |v115|
	v_exp_f32_e32 v107, v107
	v_mul_f32_e32 v108, 0x3fb8aa3b, v108
	v_exp_f32_e32 v108, v108
	v_add_f32_e32 v106, 0x3d4ccccd, v110
	v_mul_f32_e32 v102, v102, v106
	v_add_f32_e32 v106, 0x3d4ccccd, v111
	v_mul_f32_e32 v103, v103, v106
	v_add_f32_e32 v106, 0x3d4ccccd, v107
	v_mul_f32_e64 v107, v120, |v115|
	v_mul_f32_e32 v104, v104, v106
	v_add_f32_e32 v106, 0x3d4ccccd, v108
	v_mul_f32_e32 v107, 0x3fb8aa3b, v107
	v_mul_f32_e64 v108, v121, |v115|
	v_exp_f32_e32 v107, v107
	v_mul_f32_e32 v108, 0x3fb8aa3b, v108
	v_exp_f32_e32 v108, v108
	v_mul_f32_e32 v105, v105, v106
	v_add_f32_e32 v106, 0x3d4ccccd, v107
	v_mul_f32_e64 v107, v123, |v115|
	v_mul_f32_e32 v106, v98, v106
	v_add_f32_e32 v98, 0x3d4ccccd, v108
	v_mul_f32_e32 v107, 0x3fb8aa3b, v107
	v_mul_f32_e64 v108, v114, |v115|
	v_exp_f32_e32 v107, v107
	v_mul_f32_e32 v108, 0x3fb8aa3b, v108
	v_exp_f32_e32 v108, v108
	v_mul_f32_e32 v109, v99, v98
	v_add_f32_e32 v98, 0x3d4ccccd, v107
	v_mul_f32_e32 v107, v100, v98
	v_add_f32_e32 v98, 0x3d4ccccd, v108
	v_mul_f32_e32 v101, v101, v98
	v_cvt_pk_bf16_f32 v98, v102, v103
	v_cvt_pk_bf16_f32 v99, v104, v105
	v_cvt_pk_bf16_f32 v100, v106, v109
	v_cvt_pk_bf16_f32 v101, v107, v101
	global_store_dwordx4 v[116:117], v[98:101], off offset:256
	s_nop 1
	v_mov_b32_e32 v100, v179
	s_nop 0
	v_mul_f32_e64 v102, v162, |v100|
	v_mul_f32_e64 v103, v161, |v100|
	v_mul_f32_e32 v102, 0x3fb8aa3b, v102
	v_mul_f32_e32 v103, 0x3fb8aa3b, v103
	v_exp_f32_e32 v102, v102
	v_exp_f32_e32 v103, v103
	v_mul_f32_e64 v101, v163, |v100|
	v_mul_f32_e64 v104, v160, |v100|
	v_mul_f32_e32 v101, 0x3fb8aa3b, v101
	v_add_f32_e32 v102, 0x3d4ccccd, v102
	v_mul_f32_e32 v104, 0x3fb8aa3b, v104
	v_exp_f32_e32 v101, v101
	v_add_f32_e32 v103, 0x3d4ccccd, v103
	v_mul_f32_e32 v95, v95, v102
	v_mul_f32_e64 v102, v159, |v100|
	v_exp_f32_e32 v104, v104
	v_mul_f32_e32 v96, v96, v103
	v_mul_f32_e32 v102, 0x3fb8aa3b, v102
	v_mul_f32_e64 v103, v158, |v100|
	v_exp_f32_e32 v102, v102
	v_mul_f32_e32 v103, 0x3fb8aa3b, v103
	v_exp_f32_e32 v103, v103
	v_add_f32_e32 v101, 0x3d4ccccd, v101
	v_mul_f32_e32 v94, v94, v101
	v_add_f32_e32 v101, 0x3d4ccccd, v104
	v_mul_f32_e32 v97, v97, v101
	v_add_f32_e32 v101, 0x3d4ccccd, v102
	v_mul_f32_e64 v102, v157, |v100|
	v_mul_f32_e32 v101, v90, v101
	v_add_f32_e32 v90, 0x3d4ccccd, v103
	v_mul_f32_e32 v102, 0x3fb8aa3b, v102
	v_mul_f32_e64 v103, v156, |v100|
	v_exp_f32_e32 v102, v102
	v_mul_f32_e32 v103, 0x3fb8aa3b, v103
	v_exp_f32_e32 v103, v103
	v_or_b32_e32 v98, 32, v144
	v_mul_f32_e32 v104, v91, v90
	v_add_f32_e32 v90, 0x3d4ccccd, v102
	v_ashrrev_i32_e32 v99, 31, v98
	v_mul_f32_e32 v102, v92, v90
	v_add_f32_e32 v90, 0x3d4ccccd, v103
	v_lshlrev_b64 v[98:99], s9, v[98:99]
	v_mul_f32_e32 v93, v93, v90
	v_cvt_pk_bf16_f32 v90, v94, v95
	v_mul_f32_e64 v94, v145, |v100|
	v_lshl_add_u64 v[98:99], v[98:99], 1, v[148:149]
	v_cvt_pk_bf16_f32 v91, v96, v97
	v_mul_f32_e32 v94, 0x3fb8aa3b, v94
	v_mul_f32_e64 v95, v118, |v100|
	v_cvt_pk_bf16_f32 v92, v101, v104
	v_cvt_pk_bf16_f32 v93, v102, v93
	v_exp_f32_e32 v94, v94
	v_mul_f32_e32 v95, 0x3fb8aa3b, v95
	global_store_dwordx4 v[98:99], v[90:93], off
	v_exp_f32_e32 v95, v95
	s_nop 0
	v_mul_f32_e64 v91, v122, |v100|
	v_mul_f32_e32 v91, 0x3fb8aa3b, v91
	v_mul_f32_e64 v92, v119, |v100|
	v_exp_f32_e32 v91, v91
	v_mul_f32_e32 v92, 0x3fb8aa3b, v92
	v_exp_f32_e32 v92, v92
	v_add_f32_e32 v90, 0x3d4ccccd, v94
	v_mul_f32_e32 v86, v86, v90
	v_add_f32_e32 v90, 0x3d4ccccd, v95
	v_mul_f32_e32 v87, v87, v90
	v_add_f32_e32 v90, 0x3d4ccccd, v91
	v_mul_f32_e64 v91, v120, |v100|
	v_mul_f32_e32 v88, v88, v90
	v_add_f32_e32 v90, 0x3d4ccccd, v92
	v_mul_f32_e32 v91, 0x3fb8aa3b, v91
	v_mul_f32_e64 v92, v121, |v100|
	v_exp_f32_e32 v91, v91
	v_mul_f32_e32 v92, 0x3fb8aa3b, v92
	v_exp_f32_e32 v92, v92
	v_mul_f32_e32 v89, v89, v90
	v_add_f32_e32 v90, 0x3d4ccccd, v91
	v_mul_f32_e64 v91, v123, |v100|
	v_mul_f32_e32 v90, v82, v90
	v_add_f32_e32 v82, 0x3d4ccccd, v92
	v_mul_f32_e32 v91, 0x3fb8aa3b, v91
	v_mul_f32_e64 v92, v114, |v100|
	v_exp_f32_e32 v91, v91
	v_mul_f32_e32 v92, 0x3fb8aa3b, v92
	v_exp_f32_e32 v92, v92
	v_mul_f32_e32 v93, v83, v82
	v_add_f32_e32 v82, 0x3d4ccccd, v91
	v_mul_f32_e32 v91, v84, v82
	v_add_f32_e32 v82, 0x3d4ccccd, v92
	v_mul_f32_e32 v85, v85, v82
	v_cvt_pk_bf16_f32 v82, v86, v87
	v_cvt_pk_bf16_f32 v83, v88, v89
	v_cvt_pk_bf16_f32 v84, v90, v93
	v_cvt_pk_bf16_f32 v85, v91, v85
	global_store_dwordx4 v[98:99], v[82:85], off offset:256
	s_nop 1
	v_mov_b32_e32 v84, v180
	s_nop 0
	v_mul_f32_e64 v86, v162, |v84|
	v_mul_f32_e64 v85, v163, |v84|
	v_mul_f32_e64 v87, v161, |v84|
	v_mul_f32_e32 v86, 0x3fb8aa3b, v86
	v_mul_f32_e32 v85, 0x3fb8aa3b, v85
	v_exp_f32_e32 v86, v86
	v_mul_f32_e32 v87, 0x3fb8aa3b, v87
	v_exp_f32_e32 v85, v85
	v_exp_f32_e32 v87, v87
	v_add_f32_e32 v86, 0x3d4ccccd, v86
	v_mul_f32_e64 v88, v160, |v84|
	v_add_f32_e32 v85, 0x3d4ccccd, v85
	v_mul_f32_e32 v79, v79, v86
	v_add_f32_e32 v86, 0x3d4ccccd, v87
	v_mul_f32_e32 v78, v78, v85
	v_mul_f32_e32 v85, 0x3fb8aa3b, v88
	v_mul_f32_e32 v80, v80, v86
	v_mul_f32_e64 v86, v159, |v84|
	v_exp_f32_e32 v85, v85
	v_mul_f32_e32 v86, 0x3fb8aa3b, v86
	v_mul_f32_e64 v87, v158, |v84|
	v_exp_f32_e32 v86, v86
	v_mul_f32_e32 v87, 0x3fb8aa3b, v87
	v_exp_f32_e32 v87, v87
	v_add_f32_e32 v85, 0x3d4ccccd, v85
	v_mul_f32_e32 v81, v81, v85
	v_add_f32_e32 v85, 0x3d4ccccd, v86
	v_mul_f32_e64 v86, v157, |v84|
	v_mul_f32_e32 v85, v74, v85
	v_add_f32_e32 v74, 0x3d4ccccd, v87
	v_mul_f32_e32 v86, 0x3fb8aa3b, v86
	v_mul_f32_e64 v87, v156, |v84|
	v_exp_f32_e32 v86, v86
	v_mul_f32_e32 v87, 0x3fb8aa3b, v87
	v_exp_f32_e32 v87, v87
	v_or_b32_e32 v82, 48, v144
	v_mul_f32_e32 v88, v75, v74
	v_add_f32_e32 v74, 0x3d4ccccd, v86
	v_ashrrev_i32_e32 v83, 31, v82
	v_mul_f32_e32 v86, v76, v74
	v_add_f32_e32 v74, 0x3d4ccccd, v87
	v_lshlrev_b64 v[82:83], s9, v[82:83]
	v_mul_f32_e32 v77, v77, v74
	v_cvt_pk_bf16_f32 v74, v78, v79
	v_mul_f32_e64 v78, v145, |v84|
	v_lshl_add_u64 v[82:83], v[82:83], 1, v[148:149]
	v_cvt_pk_bf16_f32 v75, v80, v81
	v_mul_f32_e32 v78, 0x3fb8aa3b, v78
	v_mul_f32_e64 v79, v118, |v84|
	v_cvt_pk_bf16_f32 v76, v85, v88
	v_cvt_pk_bf16_f32 v77, v86, v77
	v_exp_f32_e32 v78, v78
	v_mul_f32_e32 v79, 0x3fb8aa3b, v79
	global_store_dwordx4 v[82:83], v[74:77], off
	v_exp_f32_e32 v79, v79
	s_nop 0
	v_mul_f32_e64 v75, v122, |v84|
	v_mul_f32_e32 v75, 0x3fb8aa3b, v75
	v_mul_f32_e64 v76, v119, |v84|
	v_exp_f32_e32 v75, v75
	v_mul_f32_e32 v76, 0x3fb8aa3b, v76
	v_exp_f32_e32 v76, v76
	v_add_f32_e32 v74, 0x3d4ccccd, v78
	v_mul_f32_e32 v70, v70, v74
	v_add_f32_e32 v74, 0x3d4ccccd, v79
	v_mul_f32_e32 v71, v71, v74
	v_add_f32_e32 v74, 0x3d4ccccd, v75
	v_mul_f32_e64 v75, v120, |v84|
	v_mul_f32_e32 v72, v72, v74
	v_add_f32_e32 v74, 0x3d4ccccd, v76
	v_mul_f32_e32 v75, 0x3fb8aa3b, v75
	v_mul_f32_e64 v76, v121, |v84|
	v_exp_f32_e32 v75, v75
	v_mul_f32_e32 v76, 0x3fb8aa3b, v76
	v_exp_f32_e32 v76, v76
	v_mul_f32_e32 v73, v73, v74
	v_add_f32_e32 v74, 0x3d4ccccd, v75
	v_mul_f32_e64 v75, v123, |v84|
	v_mul_f32_e32 v74, v66, v74
	v_add_f32_e32 v66, 0x3d4ccccd, v76
	v_mul_f32_e32 v75, 0x3fb8aa3b, v75
	v_mul_f32_e64 v76, v114, |v84|
	v_exp_f32_e32 v75, v75
	v_mul_f32_e32 v76, 0x3fb8aa3b, v76
	v_exp_f32_e32 v76, v76
	v_mul_f32_e32 v77, v67, v66
	v_add_f32_e32 v66, 0x3d4ccccd, v75
	v_mul_f32_e32 v75, v68, v66
	v_add_f32_e32 v66, 0x3d4ccccd, v76
	v_mul_f32_e32 v69, v69, v66
	v_cvt_pk_bf16_f32 v66, v70, v71
	v_cvt_pk_bf16_f32 v67, v72, v73
	v_cvt_pk_bf16_f32 v68, v74, v77
	v_cvt_pk_bf16_f32 v69, v75, v69
	global_store_dwordx4 v[82:83], v[66:69], off offset:256
	s_nop 1
	v_mov_b32_e32 v68, v181
	s_nop 0
	v_mul_f32_e64 v70, v162, |v68|
	v_mul_f32_e64 v69, v163, |v68|
	v_mul_f32_e32 v69, 0x3fb8aa3b, v69
	v_exp_f32_e32 v69, v69
	v_mul_f32_e32 v70, 0x3fb8aa3b, v70
	v_exp_f32_e32 v70, v70
	v_mul_f32_e64 v71, v160, |v68|
	v_add_f32_e32 v69, 0x3d4ccccd, v69
	v_mul_f32_e32 v62, v62, v69
	v_mul_f32_e64 v69, v161, |v68|
	v_mul_f32_e32 v69, 0x3fb8aa3b, v69
	v_exp_f32_e32 v69, v69
	v_mul_f32_e32 v71, 0x3fb8aa3b, v71
	v_exp_f32_e32 v71, v71
	v_add_f32_e32 v70, 0x3d4ccccd, v70
	v_mul_f32_e32 v63, v63, v70
	v_add_f32_e32 v69, 0x3d4ccccd, v69
	v_mul_f32_e64 v70, v159, |v68|
	v_mul_f32_e32 v64, v64, v69
	v_add_f32_e32 v69, 0x3d4ccccd, v71
	v_mul_f32_e32 v70, 0x3fb8aa3b, v70
	v_mul_f32_e64 v71, v158, |v68|
	v_exp_f32_e32 v70, v70
	v_mul_f32_e32 v71, 0x3fb8aa3b, v71
	v_exp_f32_e32 v71, v71
	v_mul_f32_e32 v65, v65, v69
	v_add_f32_e32 v69, 0x3d4ccccd, v70
	v_mul_f32_e64 v70, v157, |v68|
	v_mul_f32_e32 v69, v58, v69
	v_add_f32_e32 v58, 0x3d4ccccd, v71
	v_mul_f32_e32 v70, 0x3fb8aa3b, v70
	v_mul_f32_e64 v71, v156, |v68|
	v_exp_f32_e32 v70, v70
	v_mul_f32_e32 v71, 0x3fb8aa3b, v71
	v_exp_f32_e32 v71, v71
	v_add_u32_e32 v66, 0x80, v144
	v_mul_f32_e32 v72, v59, v58
	v_add_f32_e32 v58, 0x3d4ccccd, v70
	v_ashrrev_i32_e32 v67, 31, v66
	v_mul_f32_e32 v70, v60, v58
	v_add_f32_e32 v58, 0x3d4ccccd, v71
	v_lshlrev_b64 v[66:67], s9, v[66:67]
	v_mul_f32_e32 v61, v61, v58
	v_cvt_pk_bf16_f32 v58, v62, v63
	v_mul_f32_e64 v62, v145, |v68|
	v_lshl_add_u64 v[66:67], v[66:67], 1, v[148:149]
	v_cvt_pk_bf16_f32 v59, v64, v65
	v_mul_f32_e32 v62, 0x3fb8aa3b, v62
	v_mul_f32_e64 v63, v118, |v68|
	v_cvt_pk_bf16_f32 v60, v69, v72
	v_cvt_pk_bf16_f32 v61, v70, v61
	v_exp_f32_e32 v62, v62
	v_mul_f32_e32 v63, 0x3fb8aa3b, v63
	global_store_dwordx4 v[66:67], v[58:61], off
	v_exp_f32_e32 v63, v63
	s_nop 0
	v_mul_f32_e64 v59, v122, |v68|
	v_mul_f32_e32 v59, 0x3fb8aa3b, v59
	v_mul_f32_e64 v60, v119, |v68|
	v_exp_f32_e32 v59, v59
	v_mul_f32_e32 v60, 0x3fb8aa3b, v60
	v_exp_f32_e32 v60, v60
	v_add_f32_e32 v58, 0x3d4ccccd, v62
	v_mul_f32_e32 v54, v54, v58
	v_add_f32_e32 v58, 0x3d4ccccd, v63
	v_mul_f32_e32 v55, v55, v58
	v_add_f32_e32 v58, 0x3d4ccccd, v59
	v_mul_f32_e64 v59, v120, |v68|
	v_mul_f32_e32 v56, v56, v58
	v_add_f32_e32 v58, 0x3d4ccccd, v60
	v_mul_f32_e32 v59, 0x3fb8aa3b, v59
	v_mul_f32_e64 v60, v121, |v68|
	v_exp_f32_e32 v59, v59
	v_mul_f32_e32 v60, 0x3fb8aa3b, v60
	v_exp_f32_e32 v60, v60
	v_mul_f32_e32 v57, v57, v58
	v_add_f32_e32 v58, 0x3d4ccccd, v59
	v_mul_f32_e64 v59, v123, |v68|
	v_mul_f32_e32 v58, v50, v58
	v_add_f32_e32 v50, 0x3d4ccccd, v60
	v_mul_f32_e32 v59, 0x3fb8aa3b, v59
	v_mul_f32_e64 v60, v114, |v68|
	v_exp_f32_e32 v59, v59
	v_mul_f32_e32 v60, 0x3fb8aa3b, v60
	v_exp_f32_e32 v60, v60
	v_mul_f32_e32 v61, v51, v50
	v_add_f32_e32 v50, 0x3d4ccccd, v59
	v_mul_f32_e32 v59, v52, v50
	v_add_f32_e32 v50, 0x3d4ccccd, v60
	v_mul_f32_e32 v53, v53, v50
	v_cvt_pk_bf16_f32 v50, v54, v55
	v_cvt_pk_bf16_f32 v51, v56, v57
	v_cvt_pk_bf16_f32 v52, v58, v61
	v_cvt_pk_bf16_f32 v53, v59, v53
	global_store_dwordx4 v[66:67], v[50:53], off offset:256
	s_nop 1
	v_mov_b32_e32 v52, v182
	s_nop 0
	v_mul_f32_e64 v54, v162, |v52|
	v_mul_f32_e64 v53, v163, |v52|
	v_mul_f32_e32 v53, 0x3fb8aa3b, v53
	v_exp_f32_e32 v53, v53
	v_mul_f32_e32 v54, 0x3fb8aa3b, v54
	v_exp_f32_e32 v54, v54
	v_mul_f32_e64 v55, v160, |v52|
	v_add_f32_e32 v53, 0x3d4ccccd, v53
	v_mul_f32_e32 v46, v46, v53
	v_add_f32_e32 v53, 0x3d4ccccd, v54
	v_mul_f32_e64 v54, v161, |v52|
	v_mul_f32_e32 v54, 0x3fb8aa3b, v54
	v_exp_f32_e32 v54, v54
	v_mul_f32_e32 v55, 0x3fb8aa3b, v55
	v_exp_f32_e32 v55, v55
	v_mul_f32_e32 v47, v47, v53
	v_add_f32_e32 v53, 0x3d4ccccd, v54
	v_mul_f32_e64 v54, v159, |v52|
	v_mul_f32_e32 v48, v48, v53
	v_add_f32_e32 v53, 0x3d4ccccd, v55
	v_mul_f32_e32 v54, 0x3fb8aa3b, v54
	v_mul_f32_e64 v55, v158, |v52|
	v_exp_f32_e32 v54, v54
	v_mul_f32_e32 v55, 0x3fb8aa3b, v55
	v_exp_f32_e32 v55, v55
	v_mul_f32_e32 v49, v49, v53
	v_add_f32_e32 v53, 0x3d4ccccd, v54
	v_mul_f32_e64 v54, v157, |v52|
	v_mul_f32_e32 v53, v42, v53
	v_add_f32_e32 v42, 0x3d4ccccd, v55
	v_mul_f32_e32 v54, 0x3fb8aa3b, v54
	v_mul_f32_e64 v55, v156, |v52|
	v_exp_f32_e32 v54, v54
	v_mul_f32_e32 v55, 0x3fb8aa3b, v55
	v_exp_f32_e32 v55, v55
	v_add_u32_e32 v50, 0x90, v144
	v_mul_f32_e32 v56, v43, v42
	v_add_f32_e32 v42, 0x3d4ccccd, v54
	v_ashrrev_i32_e32 v51, 31, v50
	v_mul_f32_e32 v54, v44, v42
	v_add_f32_e32 v42, 0x3d4ccccd, v55
	v_lshlrev_b64 v[50:51], s9, v[50:51]
	v_mul_f32_e32 v45, v45, v42
	v_cvt_pk_bf16_f32 v42, v46, v47
	v_mul_f32_e64 v46, v145, |v52|
	v_lshl_add_u64 v[50:51], v[50:51], 1, v[148:149]
	v_cvt_pk_bf16_f32 v43, v48, v49
	v_mul_f32_e32 v46, 0x3fb8aa3b, v46
	v_mul_f32_e64 v47, v118, |v52|
	v_cvt_pk_bf16_f32 v44, v53, v56
	v_cvt_pk_bf16_f32 v45, v54, v45
	v_exp_f32_e32 v46, v46
	v_mul_f32_e32 v47, 0x3fb8aa3b, v47
	global_store_dwordx4 v[50:51], v[42:45], off
	v_exp_f32_e32 v47, v47
	s_nop 0
	v_mul_f32_e64 v43, v122, |v52|
	v_mul_f32_e32 v43, 0x3fb8aa3b, v43
	v_mul_f32_e64 v44, v119, |v52|
	v_exp_f32_e32 v43, v43
	v_mul_f32_e32 v44, 0x3fb8aa3b, v44
	v_exp_f32_e32 v44, v44
	v_add_f32_e32 v42, 0x3d4ccccd, v46
	v_mul_f32_e32 v38, v38, v42
	v_add_f32_e32 v42, 0x3d4ccccd, v47
	v_mul_f32_e32 v39, v39, v42
	v_add_f32_e32 v42, 0x3d4ccccd, v43
	v_mul_f32_e64 v43, v120, |v52|
	v_mul_f32_e32 v40, v40, v42
	v_add_f32_e32 v42, 0x3d4ccccd, v44
	v_mul_f32_e32 v43, 0x3fb8aa3b, v43
	v_mul_f32_e64 v44, v121, |v52|
	v_exp_f32_e32 v43, v43
	v_mul_f32_e32 v44, 0x3fb8aa3b, v44
	v_exp_f32_e32 v44, v44
	v_mul_f32_e32 v41, v41, v42
	v_add_f32_e32 v42, 0x3d4ccccd, v43
	v_mul_f32_e64 v43, v123, |v52|
	v_mul_f32_e32 v42, v34, v42
	v_add_f32_e32 v34, 0x3d4ccccd, v44
	v_mul_f32_e32 v43, 0x3fb8aa3b, v43
	v_mul_f32_e64 v44, v114, |v52|
	v_exp_f32_e32 v43, v43
	v_mul_f32_e32 v44, 0x3fb8aa3b, v44
	v_exp_f32_e32 v44, v44
	v_mul_f32_e32 v45, v35, v34
	v_add_f32_e32 v34, 0x3d4ccccd, v43
	v_mul_f32_e32 v43, v36, v34
	v_add_f32_e32 v34, 0x3d4ccccd, v44
	v_mul_f32_e32 v37, v37, v34
	v_cvt_pk_bf16_f32 v34, v38, v39
	v_cvt_pk_bf16_f32 v35, v40, v41
	v_cvt_pk_bf16_f32 v36, v42, v45
	v_cvt_pk_bf16_f32 v37, v43, v37
	global_store_dwordx4 v[50:51], v[34:37], off offset:256
	s_nop 1
	v_mov_b32_e32 v36, v183
	s_nop 0
	v_mul_f32_e64 v38, v162, |v36|
	v_mul_f32_e64 v37, v163, |v36|
	v_mul_f32_e32 v37, 0x3fb8aa3b, v37
	v_exp_f32_e32 v37, v37
	v_mul_f32_e32 v38, 0x3fb8aa3b, v38
	v_exp_f32_e32 v38, v38
	v_mul_f32_e64 v39, v160, |v36|
	v_add_f32_e32 v37, 0x3d4ccccd, v37
	v_mul_f32_e32 v30, v30, v37
	v_add_f32_e32 v37, 0x3d4ccccd, v38
	v_mul_f32_e64 v38, v161, |v36|
	v_mul_f32_e32 v38, 0x3fb8aa3b, v38
	v_exp_f32_e32 v38, v38
	v_mul_f32_e32 v39, 0x3fb8aa3b, v39
	v_exp_f32_e32 v39, v39
	v_mul_f32_e32 v31, v31, v37
	v_add_f32_e32 v37, 0x3d4ccccd, v38
	v_mul_f32_e64 v38, v159, |v36|
	v_mul_f32_e32 v32, v32, v37
	v_add_f32_e32 v37, 0x3d4ccccd, v39
	v_mul_f32_e32 v38, 0x3fb8aa3b, v38
	v_mul_f32_e64 v39, v158, |v36|
	v_exp_f32_e32 v38, v38
	v_mul_f32_e32 v39, 0x3fb8aa3b, v39
	v_exp_f32_e32 v39, v39
	v_mul_f32_e32 v33, v33, v37
	v_add_f32_e32 v37, 0x3d4ccccd, v38
	v_mul_f32_e64 v38, v157, |v36|
	v_mul_f32_e32 v37, v26, v37
	v_add_f32_e32 v26, 0x3d4ccccd, v39
	v_mul_f32_e32 v38, 0x3fb8aa3b, v38
	v_mul_f32_e64 v39, v156, |v36|
	v_exp_f32_e32 v38, v38
	v_mul_f32_e32 v39, 0x3fb8aa3b, v39
	v_exp_f32_e32 v39, v39
	v_add_u32_e32 v34, 0xa0, v144
	v_mul_f32_e32 v40, v27, v26
	v_add_f32_e32 v26, 0x3d4ccccd, v38
	v_ashrrev_i32_e32 v35, 31, v34
	v_mul_f32_e32 v38, v28, v26
	v_add_f32_e32 v26, 0x3d4ccccd, v39
	v_lshlrev_b64 v[34:35], s9, v[34:35]
	v_mul_f32_e32 v29, v29, v26
	v_cvt_pk_bf16_f32 v26, v30, v31
	v_mul_f32_e64 v30, v145, |v36|
	v_lshl_add_u64 v[34:35], v[34:35], 1, v[148:149]
	v_cvt_pk_bf16_f32 v27, v32, v33
	v_mul_f32_e32 v30, 0x3fb8aa3b, v30
	v_mul_f32_e64 v31, v118, |v36|
	v_cvt_pk_bf16_f32 v28, v37, v40
	v_cvt_pk_bf16_f32 v29, v38, v29
	v_exp_f32_e32 v30, v30
	v_mul_f32_e32 v31, 0x3fb8aa3b, v31
	global_store_dwordx4 v[34:35], v[26:29], off
	v_exp_f32_e32 v31, v31
	s_nop 0
	v_mul_f32_e64 v27, v122, |v36|
	v_mul_f32_e32 v27, 0x3fb8aa3b, v27
	v_mul_f32_e64 v28, v119, |v36|
	v_exp_f32_e32 v27, v27
	v_mul_f32_e32 v28, 0x3fb8aa3b, v28
	v_exp_f32_e32 v28, v28
	v_add_f32_e32 v26, 0x3d4ccccd, v30
	v_mul_f32_e32 v22, v22, v26
	v_add_f32_e32 v26, 0x3d4ccccd, v31
	v_mul_f32_e32 v23, v23, v26
	v_add_f32_e32 v26, 0x3d4ccccd, v27
	v_mul_f32_e64 v27, v120, |v36|
	v_mul_f32_e32 v24, v24, v26
	v_add_f32_e32 v26, 0x3d4ccccd, v28
	v_mul_f32_e32 v27, 0x3fb8aa3b, v27
	v_mul_f32_e64 v28, v121, |v36|
	v_exp_f32_e32 v27, v27
	v_mul_f32_e32 v28, 0x3fb8aa3b, v28
	v_exp_f32_e32 v28, v28
	v_mul_f32_e32 v25, v25, v26
	v_add_f32_e32 v26, 0x3d4ccccd, v27
	v_mul_f32_e64 v27, v123, |v36|
	v_mul_f32_e32 v26, v18, v26
	v_add_f32_e32 v18, 0x3d4ccccd, v28
	v_mul_f32_e32 v27, 0x3fb8aa3b, v27
	v_mul_f32_e64 v28, v114, |v36|
	v_exp_f32_e32 v27, v27
	v_mul_f32_e32 v28, 0x3fb8aa3b, v28
	v_exp_f32_e32 v28, v28
	v_mul_f32_e32 v29, v19, v18
	v_add_f32_e32 v18, 0x3d4ccccd, v27
	v_mul_f32_e32 v27, v20, v18
	v_add_f32_e32 v18, 0x3d4ccccd, v28
	v_mul_f32_e32 v21, v21, v18
	v_cvt_pk_bf16_f32 v18, v22, v23
	v_cvt_pk_bf16_f32 v19, v24, v25
	v_cvt_pk_bf16_f32 v20, v26, v29
	v_cvt_pk_bf16_f32 v21, v27, v21
	global_store_dwordx4 v[34:35], v[18:21], off offset:256
	s_nop 1
	v_mov_b32_e32 v20, v184
	s_nop 0
	v_mul_f32_e64 v22, v162, |v20|
	v_mul_f32_e64 v21, v163, |v20|
	v_mul_f32_e32 v21, 0x3fb8aa3b, v21
	v_exp_f32_e32 v21, v21
	v_mul_f32_e32 v22, 0x3fb8aa3b, v22
	v_exp_f32_e32 v22, v22
	v_mul_f32_e64 v23, v160, |v20|
	v_add_f32_e32 v21, 0x3d4ccccd, v21
	v_mul_f32_e32 v14, v14, v21
	v_add_f32_e32 v21, 0x3d4ccccd, v22
	v_mul_f32_e64 v22, v161, |v20|
	v_mul_f32_e32 v22, 0x3fb8aa3b, v22
	v_exp_f32_e32 v22, v22
	v_mul_f32_e32 v23, 0x3fb8aa3b, v23
	v_exp_f32_e32 v23, v23
	v_mul_f32_e32 v15, v15, v21
	v_add_f32_e32 v21, 0x3d4ccccd, v22
	v_mul_f32_e64 v22, v159, |v20|
	v_mul_f32_e32 v16, v16, v21
	v_add_f32_e32 v21, 0x3d4ccccd, v23
	v_mul_f32_e32 v22, 0x3fb8aa3b, v22
	v_mul_f32_e64 v23, v158, |v20|
	v_exp_f32_e32 v22, v22
	v_mul_f32_e32 v23, 0x3fb8aa3b, v23
	v_exp_f32_e32 v23, v23
	v_mul_f32_e32 v17, v17, v21
	v_add_f32_e32 v21, 0x3d4ccccd, v22
	v_mul_f32_e64 v22, v157, |v20|
	v_mul_f32_e32 v21, v10, v21
	v_add_f32_e32 v10, 0x3d4ccccd, v23
	v_mul_f32_e32 v22, 0x3fb8aa3b, v22
	v_mul_f32_e64 v23, v156, |v20|
	v_exp_f32_e32 v22, v22
	v_mul_f32_e32 v23, 0x3fb8aa3b, v23
	v_exp_f32_e32 v23, v23
	v_add_u32_e32 v18, 0xb0, v144
	v_mul_f32_e32 v24, v11, v10
	v_add_f32_e32 v10, 0x3d4ccccd, v22
	v_ashrrev_i32_e32 v19, 31, v18
	v_mul_f32_e32 v22, v12, v10
	v_add_f32_e32 v10, 0x3d4ccccd, v23
	v_lshlrev_b64 v[18:19], s9, v[18:19]
	v_mul_f32_e32 v13, v13, v10
	v_cvt_pk_bf16_f32 v10, v14, v15
	v_mul_f32_e64 v14, v123, |v20|
	v_lshl_add_u64 v[18:19], v[18:19], 1, v[148:149]
	v_cvt_pk_bf16_f32 v11, v16, v17
	v_mul_f32_e32 v14, 0x3fb8aa3b, v14
	v_mul_f32_e64 v15, v121, |v20|
	v_cvt_pk_bf16_f32 v12, v21, v24
	v_cvt_pk_bf16_f32 v13, v22, v13
	v_exp_f32_e32 v14, v14
	v_mul_f32_e32 v15, 0x3fb8aa3b, v15
	global_store_dwordx4 v[18:19], v[10:13], off
	v_exp_f32_e32 v15, v15
	s_nop 0
	v_mul_f32_e64 v11, v120, |v20|
	v_mul_f32_e32 v11, 0x3fb8aa3b, v11
	v_exp_f32_e32 v11, v11
	v_mul_f32_e64 v12, v119, |v20|
	v_add_f32_e32 v10, 0x3d4ccccd, v14
	v_mul_f32_e32 v12, 0x3fb8aa3b, v12
	v_mul_f32_e32 v10, v4, v10
	v_add_f32_e32 v4, 0x3d4ccccd, v15
	v_exp_f32_e32 v12, v12
	v_mul_f32_e32 v4, v3, v4
	v_add_f32_e32 v3, 0x3d4ccccd, v11
	v_mul_f32_e32 v11, v2, v3
	v_mul_f32_e64 v3, v122, |v20|
	v_mul_f32_e32 v3, 0x3fb8aa3b, v3
	v_add_f32_e32 v2, 0x3d4ccccd, v12
	v_exp_f32_e32 v3, v3
	v_mul_f32_e64 v12, v118, |v20|
	v_mul_f32_e32 v12, 0x3fb8aa3b, v12
	v_exp_f32_e32 v12, v12
	v_mul_f32_e32 v9, v9, v2
	v_add_f32_e32 v2, 0x3d4ccccd, v3
	v_mul_f32_e32 v3, v8, v2
	v_mul_f32_e64 v8, v145, |v20|
	v_add_f32_e32 v2, 0x3d4ccccd, v12
	v_mul_f32_e32 v8, 0x3fb8aa3b, v8
	v_mul_f32_e64 v12, v114, |v20|
	v_exp_f32_e32 v8, v8
	v_mul_f32_e32 v12, 0x3fb8aa3b, v12
	v_exp_f32_e32 v12, v12
	v_mul_f32_e32 v2, v7, v2
	v_add_f32_e32 v7, 0x3d4ccccd, v8
	v_mul_f32_e32 v6, v6, v7
	v_add_f32_e32 v7, 0x3d4ccccd, v12
	v_mul_f32_e32 v5, v5, v7
	v_cvt_pk_bf16_f32 v2, v6, v2
	v_cvt_pk_bf16_f32 v3, v3, v9
	v_cvt_pk_bf16_f32 v4, v11, v4
	v_cvt_pk_bf16_f32 v5, v10, v5
	global_store_dwordx4 v[18:19], v[2:5], off offset:256
	s_cbranch_vccz .LBB0_185
	s_waitcnt vmcnt(0)
	v_readlane_b32 s52, v250, 40
	s_cmpk_gt_u32 s39, 0xff
	v_readlane_b32 s53, v250, 41
	v_readlane_b32 s54, v250, 42
	v_readlane_b32 s55, v250, 43
	s_cbranch_scc1 .LBB0_192
	s_barrier

.LBB0_241:
	s_cmp_gt_i32 s55, 2
	s_cselect_b64 s[0:1], -1, 0
	s_and_b64 s[2:3], s[4:5], s[0:1]
	s_andn2_b64 vcc, exec, s[2:3]
	s_cbranch_vccnz .LBB0_291
	s_waitcnt vmcnt(0)
	s_barrier
	s_setprio 0
	s_mov_b64 s[2:3], exec
	v_readlane_b32 s4, v250, 5
	v_readlane_b32 s5, v250, 6
	s_and_b64 s[4:5], s[2:3], s[4:5]
	s_mov_b64 exec, s[4:5]
	s_cbranch_execz .LBB0_290
	s_add_i32 s4, 0, 0x27ff0
	v_mov_b32_e32 v1, s4
	s_waitcnt vmcnt(0) expcnt(0) lgkmcnt(0)
	ds_read_b32 v3, v1
	s_add_i32 s4, 0, 0x27ff4
	v_mov_b32_e32 v1, s4
	ds_read_b32 v1, v1
	s_waitcnt lgkmcnt(1)
	v_cmp_ne_u32_e32 vcc, 0, v3
	s_cbranch_vccnz .LBB0_258
	v_readlane_b32 s4, v250, 2
	v_readlane_b32 s5, v250, 3
	s_load_dwordx2 s[8:9], s[4:5], 0x4
	s_add_u32 s4, s52, 0x1000
	s_addc_u32 s5, s53, 0
	s_add_u32 s6, s52, 0x1100
	s_addc_u32 s7, s53, 0
	v_readlane_b32 s10, v250, 1
	s_waitcnt lgkmcnt(0)
	s_mul_i32 s18, s8, s10
	s_add_u32 s8, s52, 0x1200
	s_mul_i32 s18, s18, s9
	s_addc_u32 s9, s53, 0
	s_add_u32 s10, s52, 0x1300
	s_addc_u32 s11, s53, 0
	s_mov_b32 s19, 1
	v_mov_b32_e32 v17, 0
	s_branch .LBB0_246

.LBB0_303:
	s_andn2_b64 vcc, exec, s[6:7]
	s_cbranch_vccnz .LBB0_376
	v_lshrrev_b32_e32 v3, 1, v0
	s_waitcnt vmcnt(8)
	v_and_b32_e32 v14, 24, v3
	v_lshrrev_b32_e32 v3, 5, v0
	v_lshlrev_b32_e32 v1, 4, v0
	v_and_b32_e32 v2, 32, v0
	v_and_b32_e32 v3, 4, v3
	v_bfe_u32 v4, v0, 2, 2
	s_add_u32 s38, s16, 0x11f40000
	v_bfe_u32 v12, v0, 2, 4
	v_bitop3_b32 v10, v1, v2, 48 bitop3:0x6c
	v_and_b32_e32 v11, 64, v0
	v_or3_b32 v3, v3, v4, v14
	v_lshrrev_b32_e32 v4, 3, v0
	v_or_b32_e32 v13, 0x2000, v1
	s_addc_u32 s39, s17, 0
	v_or_b32_e32 v2, v10, v11
	v_and_or_b32 v5, v4, 48, v12
	v_and_or_b32 v4, v4, 32, v3
	v_lshrrev_b32_e32 v1, 7, v13
	s_movk_i32 s1, 0x70
	s_add_u32 s40, s16, 0x3af40000
	v_lshl_or_b32 v134, v4, 12, v2
	v_and_or_b32 v4, v1, s1, v12
	s_movk_i32 s1, 0x60
	s_addc_u32 s41, s17, 0
	v_and_or_b32 v1, v1, s1, v3
	s_lshr_b32 s6, s37, 6
	s_ashr_i32 s1, s0, 31
	s_lshr_b32 s8, s37, 8
	s_lshl_b32 s42, s6, 10
	s_ashr_i32 s7, s34, 31
	s_add_i32 s9, s34, 0xfffffc18
	s_lshl_b64 s[4:5], s[0:1], 20
	s_add_u32 s1, s40, s4
	s_addc_u32 s10, s41, s5
	s_add_u32 s4, s38, s4
	s_addc_u32 s5, s39, s5
	s_add_u32 s11, s4, 0xc00000
	s_addc_u32 s12, s5, 0
	s_cmpk_gt_i32 s34, 0x3e7
	s_cselect_b32 s5, 0, s7
	s_cselect_b32 s4, s9, s34
	s_cselect_b32 s7, s39, s41
	s_cselect_b32 s9, s38, s40
	s_cselect_b32 s28, s1, s11
	s_cselect_b32 s29, s10, s12
	s_lshl_b64 s[4:5], s[4:5], 20
	s_add_u32 s26, s9, s4
	s_addc_u32 s27, s7, s5
	s_add_i32 s43, s42, 0
	s_add_i32 m0, s43, 0x10000
	v_lshl_or_b32 v138, v1, 12, v2
	global_load_lds_dwordx4 v134, s[28:29]
	s_add_i32 m0, s43, 0x12000
	v_lshl_or_b32 v136, v5, 12, v2
	global_load_lds_dwordx4 v138, s[28:29]
	s_mov_b32 m0, s43
	s_add_i32 s44, s43, 0x2000
	v_lshl_or_b32 v140, v4, 12, v2
	global_load_lds_dwordx4 v136, s[26:27]
	s_mov_b32 m0, s44
	s_add_u32 s4, s28, 0x80000
	global_load_lds_dwordx4 v140, s[26:27]
	s_addc_u32 s5, s29, 0
	s_add_i32 m0, s43, 0x14000
	v_mov_b32_e32 v135, 0
	global_load_lds_dwordx4 v134, s[4:5]
	s_add_i32 m0, s43, 0x16000
	v_mov_b32_e32 v139, v135
	global_load_lds_dwordx4 v138, s[4:5]
	s_add_u32 s4, s26, 0x80000
	s_addc_u32 s5, s27, 0
	s_add_i32 s45, s43, 0x4000
	s_mov_b32 m0, s45
	s_add_i32 s46, s43, 0x6000
	global_load_lds_dwordx4 v136, s[4:5]
	s_mov_b32 m0, s46
	v_mov_b32_e32 v137, v135
	global_load_lds_dwordx4 v140, s[4:5]
	v_mov_b32_e32 v141, v135
	s_mov_b32 s47, 0
	v_lshl_add_u64 v[8:9], s[28:29], 0, v[134:135]
	v_lshl_add_u64 v[6:7], s[28:29], 0, v[138:139]
	v_lshl_add_u64 v[4:5], s[26:27], 0, v[136:137]
	s_setprio 1
	s_cmp_lg_u32 s8, 1
	v_lshl_add_u64 v[2:3], s[26:27], 0, v[140:141]
	s_cbranch_scc1 .LBB0_306
	s_barrier
	s_setprio 0

.LBB0_322:
	ds_read_b128 v[130:133], v155
	ds_read_b128 v[158:161], v155 offset:1024
	ds_read_b128 v[162:165], v155 offset:2048
	ds_read_b128 v[166:169], v155 offset:3072
	s_add_u32 s28, s26, 0xfff80080
	s_addc_u32 s29, s27, -1
	s_cmp_eq_u32 s59, 28
	s_cselect_b32 s31, s1, s29
	s_cselect_b32 s30, s19, s28
	s_cselect_b32 s29, s35, s58
	s_cselect_b32 s28, s56, s57
	v_lshl_add_u64 v[150:151], s[26:27], 0, v[142:143]
	s_add_i32 m0, s43, 0xc000
	ds_read_b128 v[170:173], v156
	ds_read_b128 v[174:177], v156 offset:1024
	ds_read_b128 v[178:181], v156 offset:2048
	ds_read_b128 v[182:185], v156 offset:3072
	ds_read_b128 v[186:189], v156 offset:4096
	ds_read_b128 v[192:195], v156 offset:5120
	ds_read_b128 v[196:199], v156 offset:6144
	ds_read_b128 v[200:203], v156 offset:7168
	global_load_lds_dwordx4 v[150:151], off
	v_lshl_add_u64 v[150:151], s[26:27], 0, v[144:145]
	s_add_i32 m0, s43, 0xe000
	s_nop 0
	global_load_lds_dwordx4 v[150:151], off
	s_waitcnt lgkmcnt(8)
	s_barrier
	s_waitcnt lgkmcnt(0)
	s_waitcnt lgkmcnt(0)
	v_mfma_f32_16x16x32_bf16 v[126:129], v[130:133], v[170:173], v[126:129]
	v_mfma_f32_16x16x32_bf16 v[122:125], v[162:165], v[170:173], v[122:125]
	v_mfma_f32_16x16x32_bf16 v[118:121], v[130:133], v[178:181], v[118:121]
	v_mfma_f32_16x16x32_bf16 v[110:113], v[162:165], v[178:181], v[110:113]
	v_mfma_f32_16x16x32_bf16 v[102:105], v[130:133], v[186:189], v[102:105]
	v_mfma_f32_16x16x32_bf16 v[94:97], v[162:165], v[186:189], v[94:97]
	v_mfma_f32_16x16x32_bf16 v[86:89], v[130:133], v[196:199], v[86:89]
	v_mfma_f32_16x16x32_bf16 v[78:81], v[162:165], v[196:199], v[78:81]
	v_mfma_f32_16x16x32_bf16 v[126:129], v[158:161], v[174:177], v[126:129]
	v_mfma_f32_16x16x32_bf16 v[122:125], v[166:169], v[174:177], v[122:125]
	v_mfma_f32_16x16x32_bf16 v[118:121], v[158:161], v[182:185], v[118:121]
	v_mfma_f32_16x16x32_bf16 v[110:113], v[166:169], v[182:185], v[110:113]
	v_mfma_f32_16x16x32_bf16 v[102:105], v[158:161], v[192:195], v[102:105]
	v_mfma_f32_16x16x32_bf16 v[94:97], v[166:169], v[192:195], v[94:97]
	v_mfma_f32_16x16x32_bf16 v[86:89], v[158:161], v[200:203], v[86:89]
	v_mfma_f32_16x16x32_bf16 v[78:81], v[166:169], v[200:203], v[78:81]
	s_barrier
	s_add_i32 s60, s52, s42
	v_lshl_add_u64 v[150:151], s[28:29], 0, v[134:135]
	s_mov_b32 m0, s60
	ds_read_b128 v[204:207], v157
	ds_read_b128 v[208:211], v157 offset:1024
	ds_read_b128 v[212:215], v157 offset:2048
	ds_read_b128 v[216:219], v157 offset:3072
	global_load_lds_dwordx4 v[150:151], off
	v_lshl_add_u64 v[190:191], s[28:29], 0, v[138:139]
	s_add_i32 m0, s60, 0x2000
	s_nop 0
	global_load_lds_dwordx4 v[190:191], off
	s_barrier
	s_waitcnt lgkmcnt(0)
	s_waitcnt lgkmcnt(0)
	v_mfma_f32_16x16x32_bf16 v[114:117], v[204:207], v[170:173], v[114:117]
	v_mfma_f32_16x16x32_bf16 v[106:109], v[212:215], v[170:173], v[106:109]
	v_mfma_f32_16x16x32_bf16 v[98:101], v[204:207], v[178:181], v[98:101]
	v_mfma_f32_16x16x32_bf16 v[90:93], v[212:215], v[178:181], v[90:93]
	v_mfma_f32_16x16x32_bf16 v[82:85], v[204:207], v[186:189], v[82:85]
	v_mfma_f32_16x16x32_bf16 v[74:77], v[212:215], v[186:189], v[74:77]
	v_mfma_f32_16x16x32_bf16 v[70:73], v[204:207], v[196:199], v[70:73]
	v_mfma_f32_16x16x32_bf16 v[66:69], v[212:215], v[196:199], v[66:69]
	v_mfma_f32_16x16x32_bf16 v[114:117], v[208:211], v[174:177], v[114:117]
	v_mfma_f32_16x16x32_bf16 v[106:109], v[216:219], v[174:177], v[106:109]
	v_mfma_f32_16x16x32_bf16 v[98:101], v[208:211], v[182:185], v[98:101]
	v_mfma_f32_16x16x32_bf16 v[90:93], v[216:219], v[182:185], v[90:93]
	v_mfma_f32_16x16x32_bf16 v[82:85], v[208:211], v[192:195], v[82:85]
	v_mfma_f32_16x16x32_bf16 v[74:77], v[216:219], v[192:195], v[74:77]
	v_mfma_f32_16x16x32_bf16 v[70:73], v[208:211], v[200:203], v[70:73]
	v_mfma_f32_16x16x32_bf16 v[66:69], v[216:219], v[200:203], v[66:69]
	s_mov_b32 m0, s43
	v_lshl_add_u64 v[220:221], s[30:31], 0, v[136:137]
	s_barrier
	ds_read_b128 v[170:173], v156 offset:16384
	ds_read_b128 v[174:177], v156 offset:17408
	ds_read_b128 v[178:181], v156 offset:18432
	ds_read_b128 v[182:185], v156 offset:19456
	ds_read_b128 v[186:189], v156 offset:20480
	ds_read_b128 v[192:195], v156 offset:21504
	ds_read_b128 v[196:199], v156 offset:22528
	ds_read_b128 v[200:203], v156 offset:23552
	global_load_lds_dwordx4 v[220:221], off
	v_lshl_add_u64 v[222:223], s[30:31], 0, v[140:141]
	s_mov_b32 m0, s44
	s_nop 0
	global_load_lds_dwordx4 v[222:223], off
	s_barrier
	s_waitcnt lgkmcnt(0)
	s_waitcnt lgkmcnt(0)
	v_mfma_f32_16x16x32_bf16 v[62:65], v[130:133], v[170:173], v[62:65]
	v_mfma_f32_16x16x32_bf16 v[58:61], v[162:165], v[170:173], v[58:61]
	v_mfma_f32_16x16x32_bf16 v[54:57], v[130:133], v[178:181], v[54:57]
	v_mfma_f32_16x16x32_bf16 v[46:49], v[162:165], v[178:181], v[46:49]
	v_mfma_f32_16x16x32_bf16 v[38:41], v[130:133], v[186:189], v[38:41]
	v_mfma_f32_16x16x32_bf16 v[30:33], v[162:165], v[186:189], v[30:33]
	v_mfma_f32_16x16x32_bf16 v[22:25], v[130:133], v[196:199], v[22:25]
	v_mfma_f32_16x16x32_bf16 v[14:17], v[162:165], v[196:199], v[14:17]
	v_mfma_f32_16x16x32_bf16 v[62:65], v[158:161], v[174:177], v[62:65]
	v_mfma_f32_16x16x32_bf16 v[58:61], v[166:169], v[174:177], v[58:61]
	v_mfma_f32_16x16x32_bf16 v[54:57], v[158:161], v[182:185], v[54:57]
	v_mfma_f32_16x16x32_bf16 v[46:49], v[166:169], v[182:185], v[46:49]
	v_mfma_f32_16x16x32_bf16 v[38:41], v[158:161], v[192:195], v[38:41]
	v_mfma_f32_16x16x32_bf16 v[30:33], v[166:169], v[192:195], v[30:33]
	v_mfma_f32_16x16x32_bf16 v[22:25], v[158:161], v[200:203], v[22:25]
	v_mfma_f32_16x16x32_bf16 v[14:17], v[166:169], v[200:203], v[14:17]
	s_barrier
	s_add_u32 s60, s28, 0x80000
	s_addc_u32 s61, s29, 0
	s_add_i32 s62, s53, s42
	v_lshl_add_u64 v[130:131], s[60:61], 0, v[134:135]
	s_mov_b32 m0, s62
	s_nop 0
	global_load_lds_dwordx4 v[130:131], off
	v_lshl_add_u64 v[130:131], s[60:61], 0, v[138:139]
	s_add_i32 m0, s62, 0x2000
	s_nop 0
	global_load_lds_dwordx4 v[130:131], off
	s_waitcnt vmcnt(6)
	s_barrier
	v_mfma_f32_16x16x32_bf16 v[50:53], v[204:207], v[170:173], v[50:53]
	v_mfma_f32_16x16x32_bf16 v[42:45], v[212:215], v[170:173], v[42:45]
	v_mfma_f32_16x16x32_bf16 v[34:37], v[204:207], v[178:181], v[34:37]
	v_mfma_f32_16x16x32_bf16 v[26:29], v[212:215], v[178:181], v[26:29]
	v_mfma_f32_16x16x32_bf16 v[18:21], v[204:207], v[186:189], v[18:21]
	v_mfma_f32_16x16x32_bf16 v[10:13], v[212:215], v[186:189], v[10:13]
	v_mfma_f32_16x16x32_bf16 v[6:9], v[204:207], v[196:199], v[6:9]
	v_mfma_f32_16x16x32_bf16 v[2:5], v[212:215], v[196:199], v[2:5]
	v_mfma_f32_16x16x32_bf16 v[50:53], v[208:211], v[174:177], v[50:53]
	v_mfma_f32_16x16x32_bf16 v[42:45], v[216:219], v[174:177], v[42:45]
	v_mfma_f32_16x16x32_bf16 v[34:37], v[208:211], v[182:185], v[34:37]
	v_mfma_f32_16x16x32_bf16 v[26:29], v[216:219], v[182:185], v[26:29]
	v_mfma_f32_16x16x32_bf16 v[18:21], v[208:211], v[192:195], v[18:21]
	v_mfma_f32_16x16x32_bf16 v[10:13], v[216:219], v[192:195], v[10:13]
	v_mfma_f32_16x16x32_bf16 v[6:9], v[208:211], v[200:203], v[6:9]
	v_mfma_f32_16x16x32_bf16 v[2:5], v[216:219], v[200:203], v[2:5]
	s_add_i32 s60, 0, 0x18000
	v_add_u32_e32 v166, s60, v152
	s_barrier
	ds_read_b128 v[130:133], v166
	ds_read_b128 v[158:161], v166 offset:1024
	ds_read_b128 v[162:165], v166 offset:2048
	ds_read_b128 v[166:169], v166 offset:3072
	s_add_u32 s30, s30, 0x80000
	s_addc_u32 s31, s31, 0
	s_mov_b32 m0, s45
	v_lshl_add_u64 v[204:205], s[30:31], 0, v[136:137]
	ds_read_b128 v[170:173], v156 offset:32768
	ds_read_b128 v[174:177], v156 offset:33792
	ds_read_b128 v[178:181], v156 offset:34816
	ds_read_b128 v[182:185], v156 offset:35840
	ds_read_b128 v[186:189], v156 offset:36864
	ds_read_b128 v[192:195], v156 offset:37888
	ds_read_b128 v[196:199], v156 offset:38912
	ds_read_b128 v[200:203], v156 offset:39936
	global_load_lds_dwordx4 v[204:205], off
	v_lshl_add_u64 v[204:205], s[30:31], 0, v[140:141]
	s_mov_b32 m0, s46
	s_nop 0
	global_load_lds_dwordx4 v[204:205], off
	s_waitcnt lgkmcnt(8)
	s_barrier
	s_waitcnt lgkmcnt(0)
	s_waitcnt lgkmcnt(0)
	v_mfma_f32_16x16x32_bf16 v[126:129], v[130:133], v[170:173], v[126:129]
	v_mfma_f32_16x16x32_bf16 v[122:125], v[162:165], v[170:173], v[122:125]
	v_mfma_f32_16x16x32_bf16 v[118:121], v[130:133], v[178:181], v[118:121]
	v_mfma_f32_16x16x32_bf16 v[110:113], v[162:165], v[178:181], v[110:113]
	v_mfma_f32_16x16x32_bf16 v[102:105], v[130:133], v[186:189], v[102:105]
	v_mfma_f32_16x16x32_bf16 v[94:97], v[162:165], v[186:189], v[94:97]
	v_mfma_f32_16x16x32_bf16 v[86:89], v[130:133], v[196:199], v[86:89]
	v_mfma_f32_16x16x32_bf16 v[78:81], v[162:165], v[196:199], v[78:81]
	v_mfma_f32_16x16x32_bf16 v[126:129], v[158:161], v[174:177], v[126:129]
	v_mfma_f32_16x16x32_bf16 v[122:125], v[166:169], v[174:177], v[122:125]
	v_mfma_f32_16x16x32_bf16 v[118:121], v[158:161], v[182:185], v[118:121]
	v_mfma_f32_16x16x32_bf16 v[110:113], v[166:169], v[182:185], v[110:113]
	v_mfma_f32_16x16x32_bf16 v[102:105], v[158:161], v[192:195], v[102:105]
	v_mfma_f32_16x16x32_bf16 v[94:97], v[166:169], v[192:195], v[94:97]
	v_mfma_f32_16x16x32_bf16 v[86:89], v[158:161], v[200:203], v[86:89]
	v_mfma_f32_16x16x32_bf16 v[78:81], v[166:169], v[200:203], v[78:81]
	s_barrier
	s_add_i32 s30, 0, 0x1c000
	s_add_i32 s31, s60, s42
	v_add_u32_e32 v216, s30, v152
	v_lshl_add_u64 v[150:151], v[150:151], 0, s[6:7]
	s_mov_b32 m0, s31
	ds_read_b128 v[204:207], v216
	ds_read_b128 v[208:211], v216 offset:1024
	ds_read_b128 v[212:215], v216 offset:2048
	ds_read_b128 v[216:219], v216 offset:3072
	global_load_lds_dwordx4 v[150:151], off
	v_lshl_add_u64 v[150:151], v[190:191], 0, s[6:7]
	s_add_i32 m0, s31, 0x2000
	s_nop 0
	global_load_lds_dwordx4 v[150:151], off
	s_barrier
	s_waitcnt lgkmcnt(0)
	s_waitcnt lgkmcnt(0)
	v_mfma_f32_16x16x32_bf16 v[114:117], v[204:207], v[170:173], v[114:117]
	v_mfma_f32_16x16x32_bf16 v[106:109], v[212:215], v[170:173], v[106:109]
	v_mfma_f32_16x16x32_bf16 v[98:101], v[204:207], v[178:181], v[98:101]
	v_mfma_f32_16x16x32_bf16 v[90:93], v[212:215], v[178:181], v[90:93]
	v_mfma_f32_16x16x32_bf16 v[82:85], v[204:207], v[186:189], v[82:85]
	v_mfma_f32_16x16x32_bf16 v[74:77], v[212:215], v[186:189], v[74:77]
	v_mfma_f32_16x16x32_bf16 v[70:73], v[204:207], v[196:199], v[70:73]
	v_mfma_f32_16x16x32_bf16 v[66:69], v[212:215], v[196:199], v[66:69]
	v_mfma_f32_16x16x32_bf16 v[114:117], v[208:211], v[174:177], v[114:117]
	v_mfma_f32_16x16x32_bf16 v[106:109], v[216:219], v[174:177], v[106:109]
	v_mfma_f32_16x16x32_bf16 v[98:101], v[208:211], v[182:185], v[98:101]
	v_mfma_f32_16x16x32_bf16 v[90:93], v[216:219], v[182:185], v[90:93]
	v_mfma_f32_16x16x32_bf16 v[82:85], v[208:211], v[192:195], v[82:85]
	v_mfma_f32_16x16x32_bf16 v[74:77], v[216:219], v[192:195], v[74:77]
	v_mfma_f32_16x16x32_bf16 v[70:73], v[208:211], v[200:203], v[70:73]
	v_mfma_f32_16x16x32_bf16 v[66:69], v[216:219], v[200:203], v[66:69]
	s_mov_b32 m0, s48
	v_lshl_add_u64 v[150:151], v[220:221], 0, s[6:7]
	s_barrier
	ds_read_b128 v[170:173], v156 offset:49152
	ds_read_b128 v[174:177], v156 offset:50176
	ds_read_b128 v[178:181], v156 offset:51200
	ds_read_b128 v[182:185], v156 offset:52224
	ds_read_b128 v[186:189], v156 offset:53248
	ds_read_b128 v[192:195], v156 offset:54272
	ds_read_b128 v[196:199], v156 offset:55296
	ds_read_b128 v[200:203], v156 offset:56320
	global_load_lds_dwordx4 v[150:151], off
	v_lshl_add_u64 v[150:151], v[222:223], 0, s[6:7]
	s_mov_b32 m0, s49
	s_nop 0
	global_load_lds_dwordx4 v[150:151], off
	s_barrier
	s_waitcnt lgkmcnt(0)
	s_waitcnt lgkmcnt(0)
	v_mfma_f32_16x16x32_bf16 v[62:65], v[130:133], v[170:173], v[62:65]
	v_mfma_f32_16x16x32_bf16 v[58:61], v[162:165], v[170:173], v[58:61]
	v_mfma_f32_16x16x32_bf16 v[54:57], v[130:133], v[178:181], v[54:57]
	v_mfma_f32_16x16x32_bf16 v[46:49], v[162:165], v[178:181], v[46:49]
	v_mfma_f32_16x16x32_bf16 v[38:41], v[130:133], v[186:189], v[38:41]
	v_mfma_f32_16x16x32_bf16 v[30:33], v[162:165], v[186:189], v[30:33]
	v_mfma_f32_16x16x32_bf16 v[22:25], v[130:133], v[196:199], v[22:25]
	v_mfma_f32_16x16x32_bf16 v[14:17], v[162:165], v[196:199], v[14:17]
	v_mfma_f32_16x16x32_bf16 v[62:65], v[158:161], v[174:177], v[62:65]
	v_mfma_f32_16x16x32_bf16 v[58:61], v[166:169], v[174:177], v[58:61]
	v_mfma_f32_16x16x32_bf16 v[54:57], v[158:161], v[182:185], v[54:57]
	v_mfma_f32_16x16x32_bf16 v[46:49], v[166:169], v[182:185], v[46:49]
	v_mfma_f32_16x16x32_bf16 v[38:41], v[158:161], v[192:195], v[38:41]
	v_mfma_f32_16x16x32_bf16 v[30:33], v[166:169], v[192:195], v[30:33]
	v_mfma_f32_16x16x32_bf16 v[22:25], v[158:161], v[200:203], v[22:25]
	v_mfma_f32_16x16x32_bf16 v[14:17], v[166:169], v[200:203], v[14:17]
	s_barrier
	s_add_u32 s28, s28, 0x80080
	s_addc_u32 s29, s29, 0
	s_add_i32 s30, s30, s42
	v_lshl_add_u64 v[130:131], s[28:29], 0, v[134:135]
	s_mov_b32 m0, s30
	s_nop 0
	global_load_lds_dwordx4 v[130:131], off
	v_lshl_add_u64 v[130:131], s[28:29], 0, v[138:139]
	s_add_i32 m0, s30, 0x2000
	s_nop 0
	global_load_lds_dwordx4 v[130:131], off
	s_waitcnt vmcnt(6)
	s_barrier
	v_mfma_f32_16x16x32_bf16 v[50:53], v[204:207], v[170:173], v[50:53]
	v_mfma_f32_16x16x32_bf16 v[42:45], v[212:215], v[170:173], v[42:45]
	v_mfma_f32_16x16x32_bf16 v[34:37], v[204:207], v[178:181], v[34:37]
	v_mfma_f32_16x16x32_bf16 v[26:29], v[212:215], v[178:181], v[26:29]
	v_mfma_f32_16x16x32_bf16 v[18:21], v[204:207], v[186:189], v[18:21]
	v_mfma_f32_16x16x32_bf16 v[10:13], v[212:215], v[186:189], v[10:13]
	v_mfma_f32_16x16x32_bf16 v[6:9], v[204:207], v[196:199], v[6:9]
	v_mfma_f32_16x16x32_bf16 v[2:5], v[212:215], v[196:199], v[2:5]
	v_mfma_f32_16x16x32_bf16 v[50:53], v[208:211], v[174:177], v[50:53]
	v_mfma_f32_16x16x32_bf16 v[42:45], v[216:219], v[174:177], v[42:45]
	v_mfma_f32_16x16x32_bf16 v[34:37], v[208:211], v[182:185], v[34:37]
	v_mfma_f32_16x16x32_bf16 v[26:29], v[216:219], v[182:185], v[26:29]
	v_mfma_f32_16x16x32_bf16 v[18:21], v[208:211], v[192:195], v[18:21]
	v_mfma_f32_16x16x32_bf16 v[10:13], v[216:219], v[192:195], v[10:13]
	v_mfma_f32_16x16x32_bf16 v[6:9], v[208:211], v[200:203], v[6:9]
	v_mfma_f32_16x16x32_bf16 v[2:5], v[216:219], v[200:203], v[2:5]
	s_add_i32 s59, s59, 2
	s_add_u32 s26, s26, 0x100
	s_addc_u32 s27, s27, 0
	s_add_u32 s57, s57, 0x100
	s_addc_u32 s58, s58, 0
	s_cmp_gt_u32 s59, 29
	s_barrier
	s_cbranch_scc0 .LBB0_322
	s_lshl_b32 s19, s34, 8
	s_lshl_b32 s56, s0, 8
	s_cmpk_lt_i32 s34, 0x3e8
	s_mov_b64 s[26:27], -1
	s_cbranch_scc0 .LBB0_371
	s_cmp_lt_i32 s0, 4
	s_cbranch_scc1 .LBB0_337
	s_cmp_gt_u32 s0, 5
	s_mov_b64 s[34:35], -1
	s_cbranch_scc0 .LBB0_335
	s_cmp_gt_u32 s0, 9
	s_cbranch_scc0 .LBB0_332
	s_mov_b64 s[30:31], -1
	s_cmp_gt_u32 s0, 17
	s_mov_b64 s[0:1], -1
	s_cbranch_scc0 .LBB0_329
	s_add_i32 s57, s56, 0xffffee00
	s_mov_b64 s[0:1], 0

.LBB0_377:
	s_cmp_gt_i32 s55, 3
	s_cselect_b64 s[0:1], -1, 0
	s_and_b64 s[2:3], s[2:3], s[0:1]
	s_andn2_b64 vcc, exec, s[2:3]
	s_cbranch_vccnz .LBB0_430
	s_waitcnt vmcnt(0)
	s_barrier
	s_setprio 0
	s_mov_b64 s[2:3], exec
	v_readlane_b32 s4, v250, 5
	v_readlane_b32 s5, v250, 6
	s_and_b64 s[4:5], s[2:3], s[4:5]
	s_mov_b64 exec, s[4:5]
	s_cbranch_execz .LBB0_429
	s_add_i32 s4, 0, 0x27ff0
	v_mov_b32_e32 v1, s4
	s_waitcnt vmcnt(0) expcnt(0) lgkmcnt(0)
	ds_read_b32 v3, v1
	s_add_i32 s4, 0, 0x27ff4
	v_mov_b32_e32 v1, s4
	ds_read_b32 v1, v1
	s_waitcnt lgkmcnt(1)
	v_cmp_ne_u32_e32 vcc, 0, v3
	s_cbranch_vccnz .LBB0_394
	v_readlane_b32 s4, v250, 2
	v_readlane_b32 s5, v250, 3
	s_load_dwordx2 s[8:9], s[4:5], 0x4
	s_add_u32 s4, s52, 0x1000
	s_addc_u32 s5, s53, 0
	s_add_u32 s6, s52, 0x1100
	s_addc_u32 s7, s53, 0
	v_readlane_b32 s10, v250, 1
	s_waitcnt lgkmcnt(0)
	s_mul_i32 s18, s8, s10
	s_add_u32 s8, s52, 0x1200
	s_mul_i32 s18, s18, s9
	s_addc_u32 s9, s53, 0
	s_add_u32 s10, s52, 0x1300
	s_addc_u32 s11, s53, 0
	s_mov_b32 s19, 1
	v_mov_b32_e32 v17, 0
	s_branch .LBB0_382

.LBB0_558:
	s_cmp_gt_i32 s55, 4
	s_cselect_b64 s[0:1], -1, 0
	s_and_b64 s[2:3], s[14:15], s[0:1]
	s_andn2_b64 vcc, exec, s[2:3]
	s_cbranch_vccnz .LBB0_608
	s_waitcnt vmcnt(0)
	s_barrier
	s_setprio 0
	s_mov_b64 s[2:3], exec
	v_readlane_b32 s4, v250, 5
	v_readlane_b32 s5, v250, 6
	s_and_b64 s[4:5], s[2:3], s[4:5]
	s_mov_b64 exec, s[4:5]
	s_cbranch_execz .LBB0_607
	s_add_i32 s4, 0, 0x27ff0
	v_mov_b32_e32 v1, s4
	s_waitcnt vmcnt(0) expcnt(0) lgkmcnt(0)
	ds_read_b32 v3, v1
	s_add_i32 s4, 0, 0x27ff4
	v_mov_b32_e32 v1, s4
	ds_read_b32 v1, v1
	s_waitcnt lgkmcnt(1)
	v_cmp_ne_u32_e32 vcc, 0, v3
	s_cbranch_vccnz .LBB0_575
	v_readlane_b32 s4, v250, 2
	v_readlane_b32 s5, v250, 3
	s_load_dwordx2 s[8:9], s[4:5], 0x4
	s_add_u32 s4, s52, 0x1000
	s_addc_u32 s5, s53, 0
	s_add_u32 s6, s52, 0x1100
	s_addc_u32 s7, s53, 0
	v_readlane_b32 s10, v250, 1
	s_waitcnt lgkmcnt(0)
	s_mul_i32 s18, s8, s10
	s_add_u32 s8, s52, 0x1200
	s_mul_i32 s18, s18, s9
	s_addc_u32 s9, s53, 0
	s_add_u32 s10, s52, 0x1300
	s_addc_u32 s11, s53, 0
	s_mov_b32 s19, 1
	v_mov_b32_e32 v17, 0
	s_branch .LBB0_563

.LBB0_1086:
	s_cmp_gt_i32 s55, 5
	v_readlane_b32 s2, v250, 60
	s_cselect_b64 s[0:1], -1, 0
	v_readlane_b32 s3, v250, 61
	s_and_b64 s[2:3], s[2:3], s[0:1]
	s_andn2_b64 vcc, exec, s[2:3]
	s_cbranch_vccnz .LBB0_1136
	s_waitcnt vmcnt(0)
	s_barrier
	s_setprio 0
	s_mov_b64 s[2:3], exec
	v_readlane_b32 s4, v250, 5
	v_readlane_b32 s5, v250, 6
	s_and_b64 s[4:5], s[2:3], s[4:5]
	s_mov_b64 exec, s[4:5]
	s_cbranch_execz .LBB0_1135
	s_add_i32 s4, 0, 0x27ff0
	v_mov_b32_e32 v1, s4
	s_waitcnt vmcnt(0) expcnt(0) lgkmcnt(0)
	ds_read_b32 v3, v1
	s_add_i32 s4, 0, 0x27ff4
	v_mov_b32_e32 v1, s4
	ds_read_b32 v1, v1
	s_waitcnt lgkmcnt(1)
	v_cmp_ne_u32_e32 vcc, 0, v3
	s_cbranch_vccnz .LBB0_1103
	v_readlane_b32 s4, v250, 2
	v_readlane_b32 s5, v250, 3
	s_load_dwordx2 s[8:9], s[4:5], 0x4
	s_add_u32 s4, s52, 0x1000
	s_addc_u32 s5, s53, 0
	s_add_u32 s6, s52, 0x1100
	s_addc_u32 s7, s53, 0
	v_readlane_b32 s10, v250, 1
	s_waitcnt lgkmcnt(0)
	s_mul_i32 s18, s8, s10
	s_add_u32 s8, s52, 0x1200
	s_mul_i32 s18, s18, s9
	s_addc_u32 s9, s53, 0
	s_add_u32 s10, s52, 0x1300
	s_addc_u32 s11, s53, 0
	s_mov_b32 s19, 1
	v_mov_b32_e32 v17, 0
	s_branch .LBB0_1091

.LBB0_1141:
	s_cmp_gt_i32 s55, 6
	s_cselect_b64 s[0:1], -1, 0
	s_and_b64 s[2:3], s[2:3], s[0:1]
	s_andn2_b64 vcc, exec, s[2:3]
	s_cbranch_vccnz .LBB0_1191
	s_waitcnt vmcnt(0)
	s_barrier
	s_setprio 0
	s_mov_b64 s[2:3], exec
	v_readlane_b32 s4, v250, 5
	v_readlane_b32 s5, v250, 6
	s_and_b64 s[4:5], s[2:3], s[4:5]
	s_mov_b64 exec, s[4:5]
	s_cbranch_execz .LBB0_1190
	s_add_i32 s4, 0, 0x27ff0
	v_mov_b32_e32 v1, s4
	s_waitcnt vmcnt(0) expcnt(0) lgkmcnt(0)
	ds_read_b32 v3, v1
	s_add_i32 s4, 0, 0x27ff4
	v_mov_b32_e32 v1, s4
	ds_read_b32 v1, v1
	s_waitcnt lgkmcnt(1)
	v_cmp_ne_u32_e32 vcc, 0, v3
	s_cbranch_vccnz .LBB0_1158
	v_readlane_b32 s4, v250, 2
	v_readlane_b32 s5, v250, 3
	s_load_dwordx2 s[8:9], s[4:5], 0x4
	s_add_u32 s4, s52, 0x1000
	s_addc_u32 s5, s53, 0
	s_add_u32 s6, s52, 0x1100
	s_addc_u32 s7, s53, 0
	v_readlane_b32 s10, v250, 1
	s_waitcnt lgkmcnt(0)
	s_mul_i32 s18, s8, s10
	s_add_u32 s8, s52, 0x1200
	s_mul_i32 s18, s18, s9
	s_addc_u32 s9, s53, 0
	s_add_u32 s10, s52, 0x1300
	s_addc_u32 s11, s53, 0
	s_mov_b32 s19, 1
	v_mov_b32_e32 v17, 0
	s_branch .LBB0_1146

.LBB0_1191:
	s_cmp_lt_i32 s54, 7
	s_cselect_b64 s[4:5], -1, 0
	s_and_b64 s[0:1], s[4:5], s[0:1]
	s_andn2_b64 vcc, exec, s[0:1]
	s_cbranch_vccnz .LBB0_1229
	v_mov_b32_e32 v1, v248
	s_waitcnt vmcnt(11)
	v_mov_b32_e32 v2, v0
	v_readlane_b32 s30, v250, 1
	v_readlane_b32 s31, v250, 0
	v_readlane_b32 s0, v250, 39
	s_mov_b64 s[0:1], s[90:91]
	s_mov_b64 s[6:7], s[52:53]
	v_lshlrev_b32_e32 v2, 4, v0
	v_and_b32_e32 v1, 32, v0
	v_or_b32_e32 v150, 0x2000, v2
	v_bfe_u32 v149, v0, 2, 4
	v_bitop3_b32 v1, v2, v1, 48 bitop3:0x6c
	v_and_b32_e32 v148, 64, v0
	v_lshrrev_b32_e32 v4, 3, v0
	v_lshrrev_b32_e32 v2, 7, v150
	s_movk_i32 s0, 0x70
	v_or_b32_e32 v3, v1, v148
	v_and_or_b32 v4, v4, 48, v149
	v_and_or_b32 v2, v2, s0, v149
	v_lshl_or_b32 v130, v4, 11, v3
	v_lshl_or_b32 v132, v2, 11, v3
	v_bfe_u32 v151, v0, 4, 2
	v_lshlrev_b32_e32 v2, 6, v0
	v_lshlrev_b32_e32 v3, 2, v0
	v_lshlrev_b32_e32 v153, 4, v151
	v_and_b32_e32 v2, 0x3c0, v2
	v_and_b32_e32 v3, 32, v3
	s_cmpk_lt_i32 s31, 0x208
	v_readfirstlane_b32 s33, v0
	v_and_b32_e32 v152, 15, v0
	s_cselect_b64 s[2:3], -1, 0
	s_cmpk_gt_i32 s31, 0x207
	v_bitop3_b32 v154, v153, v3, v2 bitop3:0x36
	s_barrier
	s_cbranch_scc1 .LBB0_1204
	s_add_u32 s34, s6, 0x3cf40000
	s_addc_u32 s35, s7, 0
	s_add_u32 s36, s6, 0x15540000
	s_addc_u32 s37, s7, 0
	s_ashr_i32 s39, s31, 31
	s_lshr_b32 s0, s39, 29
	s_add_i32 s0, s31, s0
	s_lshr_b32 s8, s33, 6
	s_ashr_i32 s9, s0, 3
	s_and_b32 s0, s0, -8
	s_lshr_b32 s1, s33, 8
	s_lshl_b32 s38, s8, 10
	s_sub_i32 s0, s31, s0
	s_cmp_lt_i32 s0, 0
	s_movk_i32 s40, 0x42
	s_cselect_b32 s10, s40, 0x41
	s_mul_i32 s0, s10, s0
	s_add_i32 s0, s0, s9
	s_ashr_i32 s9, s0, 31
	s_lshr_b32 s9, s9, 26
	s_add_i32 s9, s0, s9
	s_ashr_i32 s10, s9, 6
	s_lshl_b32 s12, s10, 3
	s_sub_i32 s10, 0x41, s12
	s_min_u32 s13, s10, 8
	s_andn2_b32 s9, s9, 63
	s_sub_i32 s9, s0, s9
	v_cvt_f32_ubyte0_e32 v3, s13
	v_cvt_f32_i32_e32 v2, s9
	v_rcp_iflag_f32_e32 v4, v3
	s_ashr_i32 s0, s9, 30
	s_or_b32 s0, s0, 1
	v_mov_b32_e32 v131, 0
	v_mul_f32_e32 v4, v2, v4
	v_trunc_f32_e32 v4, v4
	v_fma_f32 v2, -v4, v3, v2
	v_cvt_i32_f32_e32 v4, v4
	v_cmp_ge_f32_e64 s[10:11], |v2|, v3
	s_and_b64 s[10:11], s[10:11], exec
	s_cselect_b32 s0, s0, 0
	v_readfirstlane_b32 s10, v4
	s_add_i32 s0, s10, s0
	s_mul_i32 s10, s0, s13
	s_sub_i32 s9, s9, s10
	s_sext_i32_i8 s9, s9
	s_add_i32 s22, s12, s9
	s_ashr_i32 s23, s22, 31
	s_lshl_b64 s[10:11], s[22:23], 19
	s_add_u32 s24, s34, s10
	s_addc_u32 s25, s35, s11
	s_bfe_i64 s[10:11], s[0:1], 0x80000
	s_lshl_b64 s[10:11], s[10:11], 19
	s_add_u32 s26, s36, s10
	s_addc_u32 s27, s37, s11
	s_add_i32 s23, s38, 0
	s_add_i32 m0, s23, 0x10000
	s_add_i32 s41, s23, 0x2000
	global_load_lds_dwordx4 v130, s[26:27]
	s_add_i32 m0, s23, 0x12000
	s_add_u32 s10, s26, 0x40000
	global_load_lds_dwordx4 v132, s[26:27]
	s_mov_b32 m0, s23
	s_addc_u32 s11, s27, 0
	global_load_lds_dwordx4 v130, s[24:25]
	s_mov_b32 m0, s41
	v_mov_b32_e32 v133, v131
	global_load_lds_dwordx4 v132, s[24:25]
	s_add_i32 m0, s23, 0x14000
	s_mov_b32 s44, 0
	global_load_lds_dwordx4 v130, s[10:11]
	s_add_i32 m0, s23, 0x16000
	s_waitcnt vmcnt(0)
	v_lshl_add_u64 v[8:9], s[26:27], 0, v[130:131]
	global_load_lds_dwordx4 v132, s[10:11]
	s_add_u32 s10, s24, 0x40000
	s_addc_u32 s11, s25, 0
	s_add_i32 s42, s23, 0x4000
	s_mov_b32 m0, s42
	s_add_i32 s43, s23, 0x6000
	global_load_lds_dwordx4 v130, s[10:11]
	s_mov_b32 m0, s43
	v_lshl_add_u64 v[6:7], s[26:27], 0, v[132:133]
	global_load_lds_dwordx4 v132, s[10:11]
	v_lshl_add_u64 v[4:5], s[24:25], 0, v[130:131]
	s_setprio 1
	s_cmp_lg_u32 s1, 1
	v_lshl_add_u64 v[2:3], s[24:25], 0, v[132:133]
	s_cbranch_scc1 .LBB0_1195
	s_barrier
	s_setprio 0

.LBB0_1199:
	ds_read_b128 v[142:145], v158
	ds_read_b128 v[162:165], v158 offset:1024
	ds_read_b128 v[166:169], v158 offset:2048
	ds_read_b128 v[170:173], v158 offset:3072
	s_add_u32 s26, s24, 0xfffc0080
	s_addc_u32 s27, s25, -1
	s_cmp_eq_u32 s56, 12
	s_cselect_b32 s29, s17, s27
	s_cselect_b32 s28, s52, s26
	s_cselect_b32 s27, s15, s55
	s_cselect_b32 s26, s53, s54
	v_lshl_add_u64 v[146:147], s[24:25], 0, v[134:135]
	s_add_i32 m0, s23, 0xc000
	ds_read_b128 v[174:177], v159
	ds_read_b128 v[178:181], v159 offset:1024
	ds_read_b128 v[182:185], v159 offset:2048
	ds_read_b128 v[186:189], v159 offset:3072
	ds_read_b128 v[192:195], v159 offset:4096
	ds_read_b128 v[196:199], v159 offset:5120
	ds_read_b128 v[200:203], v159 offset:6144
	ds_read_b128 v[204:207], v159 offset:7168
	global_load_lds_dwordx4 v[146:147], off
	v_lshl_add_u64 v[146:147], s[24:25], 0, v[136:137]
	s_add_i32 m0, s23, 0xe000
	s_nop 0
	global_load_lds_dwordx4 v[146:147], off
	s_waitcnt lgkmcnt(8)
	s_barrier
	s_waitcnt lgkmcnt(0)
	s_waitcnt lgkmcnt(0)
	v_mfma_f32_16x16x32_bf16 v[126:129], v[142:145], v[174:177], v[126:129]
	v_mfma_f32_16x16x32_bf16 v[122:125], v[166:169], v[174:177], v[122:125]
	v_mfma_f32_16x16x32_bf16 v[114:117], v[142:145], v[182:185], v[114:117]
	v_mfma_f32_16x16x32_bf16 v[106:109], v[166:169], v[182:185], v[106:109]
	v_mfma_f32_16x16x32_bf16 v[98:101], v[142:145], v[192:195], v[98:101]
	v_mfma_f32_16x16x32_bf16 v[90:93], v[166:169], v[192:195], v[90:93]
	v_mfma_f32_16x16x32_bf16 v[82:85], v[142:145], v[200:203], v[82:85]
	v_mfma_f32_16x16x32_bf16 v[74:77], v[166:169], v[200:203], v[74:77]
	v_mfma_f32_16x16x32_bf16 v[126:129], v[162:165], v[178:181], v[126:129]
	v_mfma_f32_16x16x32_bf16 v[122:125], v[170:173], v[178:181], v[122:125]
	v_mfma_f32_16x16x32_bf16 v[114:117], v[162:165], v[186:189], v[114:117]
	v_mfma_f32_16x16x32_bf16 v[106:109], v[170:173], v[186:189], v[106:109]
	v_mfma_f32_16x16x32_bf16 v[98:101], v[162:165], v[196:199], v[98:101]
	v_mfma_f32_16x16x32_bf16 v[90:93], v[170:173], v[196:199], v[90:93]
	v_mfma_f32_16x16x32_bf16 v[82:85], v[162:165], v[204:207], v[82:85]
	v_mfma_f32_16x16x32_bf16 v[74:77], v[170:173], v[204:207], v[74:77]
	s_barrier
	s_add_i32 s57, s48, s38
	v_lshl_add_u64 v[146:147], s[26:27], 0, v[130:131]
	s_mov_b32 m0, s57
	ds_read_b128 v[208:211], v160
	ds_read_b128 v[212:215], v160 offset:1024
	ds_read_b128 v[216:219], v160 offset:2048
	ds_read_b128 v[220:223], v160 offset:3072
	global_load_lds_dwordx4 v[146:147], off
	v_lshl_add_u64 v[190:191], s[26:27], 0, v[132:133]
	s_add_i32 m0, s57, 0x2000
	s_nop 0
	global_load_lds_dwordx4 v[190:191], off
	s_barrier
	s_waitcnt lgkmcnt(0)
	s_waitcnt lgkmcnt(0)
	v_mfma_f32_16x16x32_bf16 v[118:121], v[208:211], v[174:177], v[118:121]
	v_mfma_f32_16x16x32_bf16 v[110:113], v[216:219], v[174:177], v[110:113]
	v_mfma_f32_16x16x32_bf16 v[102:105], v[208:211], v[182:185], v[102:105]
	v_mfma_f32_16x16x32_bf16 v[94:97], v[216:219], v[182:185], v[94:97]
	v_mfma_f32_16x16x32_bf16 v[86:89], v[208:211], v[192:195], v[86:89]
	v_mfma_f32_16x16x32_bf16 v[78:81], v[216:219], v[192:195], v[78:81]
	v_mfma_f32_16x16x32_bf16 v[70:73], v[208:211], v[200:203], v[70:73]
	v_mfma_f32_16x16x32_bf16 v[66:69], v[216:219], v[200:203], v[66:69]
	v_mfma_f32_16x16x32_bf16 v[118:121], v[212:215], v[178:181], v[118:121]
	v_mfma_f32_16x16x32_bf16 v[110:113], v[220:223], v[178:181], v[110:113]
	v_mfma_f32_16x16x32_bf16 v[102:105], v[212:215], v[186:189], v[102:105]
	v_mfma_f32_16x16x32_bf16 v[94:97], v[220:223], v[186:189], v[94:97]
	v_mfma_f32_16x16x32_bf16 v[86:89], v[212:215], v[196:199], v[86:89]
	v_mfma_f32_16x16x32_bf16 v[78:81], v[220:223], v[196:199], v[78:81]
	v_mfma_f32_16x16x32_bf16 v[70:73], v[212:215], v[204:207], v[70:73]
	v_mfma_f32_16x16x32_bf16 v[66:69], v[220:223], v[204:207], v[66:69]
	s_mov_b32 m0, s23
	v_lshl_add_u64 v[224:225], s[28:29], 0, v[130:131]
	s_barrier
	ds_read_b128 v[174:177], v159 offset:16384
	ds_read_b128 v[178:181], v159 offset:17408
	ds_read_b128 v[182:185], v159 offset:18432
	ds_read_b128 v[186:189], v159 offset:19456
	ds_read_b128 v[192:195], v159 offset:20480
	ds_read_b128 v[196:199], v159 offset:21504
	ds_read_b128 v[200:203], v159 offset:22528
	ds_read_b128 v[204:207], v159 offset:23552
	global_load_lds_dwordx4 v[224:225], off
	v_lshl_add_u64 v[226:227], s[28:29], 0, v[132:133]
	s_mov_b32 m0, s41
	s_nop 0
	global_load_lds_dwordx4 v[226:227], off
	s_barrier
	s_waitcnt lgkmcnt(0)
	s_waitcnt lgkmcnt(0)
	v_mfma_f32_16x16x32_bf16 v[62:65], v[142:145], v[174:177], v[62:65]
	v_mfma_f32_16x16x32_bf16 v[58:61], v[166:169], v[174:177], v[58:61]
	v_mfma_f32_16x16x32_bf16 v[50:53], v[142:145], v[182:185], v[50:53]
	v_mfma_f32_16x16x32_bf16 v[42:45], v[166:169], v[182:185], v[42:45]
	v_mfma_f32_16x16x32_bf16 v[34:37], v[142:145], v[192:195], v[34:37]
	v_mfma_f32_16x16x32_bf16 v[26:29], v[166:169], v[192:195], v[26:29]
	v_mfma_f32_16x16x32_bf16 v[18:21], v[142:145], v[200:203], v[18:21]
	v_mfma_f32_16x16x32_bf16 v[10:13], v[166:169], v[200:203], v[10:13]
	v_mfma_f32_16x16x32_bf16 v[62:65], v[162:165], v[178:181], v[62:65]
	v_mfma_f32_16x16x32_bf16 v[58:61], v[170:173], v[178:181], v[58:61]
	v_mfma_f32_16x16x32_bf16 v[50:53], v[162:165], v[186:189], v[50:53]
	v_mfma_f32_16x16x32_bf16 v[42:45], v[170:173], v[186:189], v[42:45]
	v_mfma_f32_16x16x32_bf16 v[34:37], v[162:165], v[196:199], v[34:37]
	v_mfma_f32_16x16x32_bf16 v[26:29], v[170:173], v[196:199], v[26:29]
	v_mfma_f32_16x16x32_bf16 v[18:21], v[162:165], v[204:207], v[18:21]
	v_mfma_f32_16x16x32_bf16 v[10:13], v[170:173], v[204:207], v[10:13]
	s_barrier
	s_add_u32 s58, s26, 0x40000
	s_addc_u32 s59, s27, 0
	s_add_i32 s57, s49, s38
	v_lshl_add_u64 v[142:143], s[58:59], 0, v[130:131]
	s_mov_b32 m0, s57
	s_nop 0
	global_load_lds_dwordx4 v[142:143], off
	v_lshl_add_u64 v[142:143], s[58:59], 0, v[132:133]
	s_add_i32 m0, s57, 0x2000
	s_nop 0
	global_load_lds_dwordx4 v[142:143], off
	s_waitcnt vmcnt(6)
	s_barrier
	v_mfma_f32_16x16x32_bf16 v[54:57], v[208:211], v[174:177], v[54:57]
	v_mfma_f32_16x16x32_bf16 v[46:49], v[216:219], v[174:177], v[46:49]
	v_mfma_f32_16x16x32_bf16 v[38:41], v[208:211], v[182:185], v[38:41]
	v_mfma_f32_16x16x32_bf16 v[30:33], v[216:219], v[182:185], v[30:33]
	v_mfma_f32_16x16x32_bf16 v[22:25], v[208:211], v[192:195], v[22:25]
	v_mfma_f32_16x16x32_bf16 v[14:17], v[216:219], v[192:195], v[14:17]
	v_mfma_f32_16x16x32_bf16 v[6:9], v[208:211], v[200:203], v[6:9]
	v_mfma_f32_16x16x32_bf16 v[2:5], v[216:219], v[200:203], v[2:5]
	v_mfma_f32_16x16x32_bf16 v[54:57], v[212:215], v[178:181], v[54:57]
	v_mfma_f32_16x16x32_bf16 v[46:49], v[220:223], v[178:181], v[46:49]
	v_mfma_f32_16x16x32_bf16 v[38:41], v[212:215], v[186:189], v[38:41]
	v_mfma_f32_16x16x32_bf16 v[30:33], v[220:223], v[186:189], v[30:33]
	v_mfma_f32_16x16x32_bf16 v[22:25], v[212:215], v[196:199], v[22:25]
	v_mfma_f32_16x16x32_bf16 v[14:17], v[220:223], v[196:199], v[14:17]
	v_mfma_f32_16x16x32_bf16 v[6:9], v[212:215], v[204:207], v[6:9]
	v_mfma_f32_16x16x32_bf16 v[2:5], v[220:223], v[204:207], v[2:5]
	s_add_i32 s57, 0, 0x18000
	v_add_u32_e32 v161, s57, v156
	s_barrier
	ds_read_b128 v[142:145], v161
	ds_read_b128 v[162:165], v161 offset:1024
	ds_read_b128 v[166:169], v161 offset:2048
	ds_read_b128 v[170:173], v161 offset:3072
	s_add_u32 s28, s28, 0x40000
	s_addc_u32 s29, s29, 0
	s_mov_b32 m0, s42
	v_lshl_add_u64 v[208:209], s[28:29], 0, v[130:131]
	ds_read_b128 v[174:177], v159 offset:32768
	ds_read_b128 v[178:181], v159 offset:33792
	ds_read_b128 v[182:185], v159 offset:34816
	ds_read_b128 v[186:189], v159 offset:35840
	ds_read_b128 v[192:195], v159 offset:36864
	ds_read_b128 v[196:199], v159 offset:37888
	ds_read_b128 v[200:203], v159 offset:38912
	ds_read_b128 v[204:207], v159 offset:39936
	global_load_lds_dwordx4 v[208:209], off
	v_lshl_add_u64 v[208:209], s[28:29], 0, v[132:133]
	s_mov_b32 m0, s43
	s_nop 0
	global_load_lds_dwordx4 v[208:209], off
	s_waitcnt lgkmcnt(8)
	s_barrier
	s_waitcnt lgkmcnt(0)
	s_waitcnt lgkmcnt(0)
	v_mfma_f32_16x16x32_bf16 v[126:129], v[142:145], v[174:177], v[126:129]
	v_mfma_f32_16x16x32_bf16 v[122:125], v[166:169], v[174:177], v[122:125]
	v_mfma_f32_16x16x32_bf16 v[114:117], v[142:145], v[182:185], v[114:117]
	v_mfma_f32_16x16x32_bf16 v[106:109], v[166:169], v[182:185], v[106:109]
	v_mfma_f32_16x16x32_bf16 v[98:101], v[142:145], v[192:195], v[98:101]
	v_mfma_f32_16x16x32_bf16 v[90:93], v[166:169], v[192:195], v[90:93]
	v_mfma_f32_16x16x32_bf16 v[82:85], v[142:145], v[200:203], v[82:85]
	v_mfma_f32_16x16x32_bf16 v[74:77], v[166:169], v[200:203], v[74:77]
	v_mfma_f32_16x16x32_bf16 v[126:129], v[162:165], v[178:181], v[126:129]
	v_mfma_f32_16x16x32_bf16 v[122:125], v[170:173], v[178:181], v[122:125]
	v_mfma_f32_16x16x32_bf16 v[114:117], v[162:165], v[186:189], v[114:117]
	v_mfma_f32_16x16x32_bf16 v[106:109], v[170:173], v[186:189], v[106:109]
	v_mfma_f32_16x16x32_bf16 v[98:101], v[162:165], v[196:199], v[98:101]
	v_mfma_f32_16x16x32_bf16 v[90:93], v[170:173], v[196:199], v[90:93]
	v_mfma_f32_16x16x32_bf16 v[82:85], v[162:165], v[204:207], v[82:85]
	v_mfma_f32_16x16x32_bf16 v[74:77], v[170:173], v[204:207], v[74:77]
	s_barrier
	s_add_i32 s28, 0, 0x1c000
	s_add_i32 s29, s57, s38
	v_add_u32_e32 v161, s28, v156
	v_lshl_add_u64 v[146:147], v[146:147], 0, s[8:9]
	s_mov_b32 m0, s29
	ds_read_b128 v[208:211], v161
	ds_read_b128 v[212:215], v161 offset:1024
	ds_read_b128 v[216:219], v161 offset:2048
	ds_read_b128 v[220:223], v161 offset:3072
	global_load_lds_dwordx4 v[146:147], off
	v_lshl_add_u64 v[146:147], v[190:191], 0, s[8:9]
	s_add_i32 m0, s29, 0x2000
	s_nop 0
	global_load_lds_dwordx4 v[146:147], off
	s_barrier
	s_waitcnt lgkmcnt(0)
	s_waitcnt lgkmcnt(0)
	v_mfma_f32_16x16x32_bf16 v[118:121], v[208:211], v[174:177], v[118:121]
	v_mfma_f32_16x16x32_bf16 v[110:113], v[216:219], v[174:177], v[110:113]
	v_mfma_f32_16x16x32_bf16 v[102:105], v[208:211], v[182:185], v[102:105]
	v_mfma_f32_16x16x32_bf16 v[94:97], v[216:219], v[182:185], v[94:97]
	v_mfma_f32_16x16x32_bf16 v[86:89], v[208:211], v[192:195], v[86:89]
	v_mfma_f32_16x16x32_bf16 v[78:81], v[216:219], v[192:195], v[78:81]
	v_mfma_f32_16x16x32_bf16 v[70:73], v[208:211], v[200:203], v[70:73]
	v_mfma_f32_16x16x32_bf16 v[66:69], v[216:219], v[200:203], v[66:69]
	v_mfma_f32_16x16x32_bf16 v[118:121], v[212:215], v[178:181], v[118:121]
	v_mfma_f32_16x16x32_bf16 v[110:113], v[220:223], v[178:181], v[110:113]
	v_mfma_f32_16x16x32_bf16 v[102:105], v[212:215], v[186:189], v[102:105]
	v_mfma_f32_16x16x32_bf16 v[94:97], v[220:223], v[186:189], v[94:97]
	v_mfma_f32_16x16x32_bf16 v[86:89], v[212:215], v[196:199], v[86:89]
	v_mfma_f32_16x16x32_bf16 v[78:81], v[220:223], v[196:199], v[78:81]
	v_mfma_f32_16x16x32_bf16 v[70:73], v[212:215], v[204:207], v[70:73]
	v_mfma_f32_16x16x32_bf16 v[66:69], v[220:223], v[204:207], v[66:69]
	s_mov_b32 m0, s45
	v_lshl_add_u64 v[146:147], v[224:225], 0, s[8:9]
	s_barrier
	ds_read_b128 v[174:177], v159 offset:49152
	ds_read_b128 v[178:181], v159 offset:50176
	ds_read_b128 v[182:185], v159 offset:51200
	ds_read_b128 v[186:189], v159 offset:52224
	ds_read_b128 v[192:195], v159 offset:53248
	ds_read_b128 v[196:199], v159 offset:54272
	ds_read_b128 v[200:203], v159 offset:55296
	ds_read_b128 v[204:207], v159 offset:56320
	global_load_lds_dwordx4 v[146:147], off
	v_lshl_add_u64 v[146:147], v[226:227], 0, s[8:9]
	s_mov_b32 m0, s46
	s_nop 0
	global_load_lds_dwordx4 v[146:147], off
	s_barrier
	s_waitcnt lgkmcnt(0)
	s_waitcnt lgkmcnt(0)
	v_mfma_f32_16x16x32_bf16 v[62:65], v[142:145], v[174:177], v[62:65]
	v_mfma_f32_16x16x32_bf16 v[58:61], v[166:169], v[174:177], v[58:61]
	v_mfma_f32_16x16x32_bf16 v[50:53], v[142:145], v[182:185], v[50:53]
	v_mfma_f32_16x16x32_bf16 v[42:45], v[166:169], v[182:185], v[42:45]
	v_mfma_f32_16x16x32_bf16 v[34:37], v[142:145], v[192:195], v[34:37]
	v_mfma_f32_16x16x32_bf16 v[26:29], v[166:169], v[192:195], v[26:29]
	v_mfma_f32_16x16x32_bf16 v[18:21], v[142:145], v[200:203], v[18:21]
	v_mfma_f32_16x16x32_bf16 v[10:13], v[166:169], v[200:203], v[10:13]
	v_mfma_f32_16x16x32_bf16 v[62:65], v[162:165], v[178:181], v[62:65]
	v_mfma_f32_16x16x32_bf16 v[58:61], v[170:173], v[178:181], v[58:61]
	v_mfma_f32_16x16x32_bf16 v[50:53], v[162:165], v[186:189], v[50:53]
	v_mfma_f32_16x16x32_bf16 v[42:45], v[170:173], v[186:189], v[42:45]
	v_mfma_f32_16x16x32_bf16 v[34:37], v[162:165], v[196:199], v[34:37]
	v_mfma_f32_16x16x32_bf16 v[26:29], v[170:173], v[196:199], v[26:29]
	v_mfma_f32_16x16x32_bf16 v[18:21], v[162:165], v[204:207], v[18:21]
	v_mfma_f32_16x16x32_bf16 v[10:13], v[170:173], v[204:207], v[10:13]
	s_barrier
	s_add_u32 s26, s26, 0x40080
	s_addc_u32 s27, s27, 0
	s_add_i32 s28, s28, s38
	v_lshl_add_u64 v[142:143], s[26:27], 0, v[130:131]
	s_mov_b32 m0, s28
	s_nop 0
	global_load_lds_dwordx4 v[142:143], off
	v_lshl_add_u64 v[142:143], s[26:27], 0, v[132:133]
	s_add_i32 m0, s28, 0x2000
	s_nop 0
	global_load_lds_dwordx4 v[142:143], off
	s_waitcnt vmcnt(6)
	s_barrier
	v_mfma_f32_16x16x32_bf16 v[54:57], v[208:211], v[174:177], v[54:57]
	v_mfma_f32_16x16x32_bf16 v[46:49], v[216:219], v[174:177], v[46:49]
	v_mfma_f32_16x16x32_bf16 v[38:41], v[208:211], v[182:185], v[38:41]
	v_mfma_f32_16x16x32_bf16 v[30:33], v[216:219], v[182:185], v[30:33]
	v_mfma_f32_16x16x32_bf16 v[22:25], v[208:211], v[192:195], v[22:25]
	v_mfma_f32_16x16x32_bf16 v[14:17], v[216:219], v[192:195], v[14:17]
	v_mfma_f32_16x16x32_bf16 v[6:9], v[208:211], v[200:203], v[6:9]
	v_mfma_f32_16x16x32_bf16 v[2:5], v[216:219], v[200:203], v[2:5]
	v_mfma_f32_16x16x32_bf16 v[54:57], v[212:215], v[178:181], v[54:57]
	v_mfma_f32_16x16x32_bf16 v[46:49], v[220:223], v[178:181], v[46:49]
	v_mfma_f32_16x16x32_bf16 v[38:41], v[212:215], v[186:189], v[38:41]
	v_mfma_f32_16x16x32_bf16 v[30:33], v[220:223], v[186:189], v[30:33]
	v_mfma_f32_16x16x32_bf16 v[22:25], v[212:215], v[196:199], v[22:25]
	v_mfma_f32_16x16x32_bf16 v[14:17], v[220:223], v[196:199], v[14:17]
	v_mfma_f32_16x16x32_bf16 v[6:9], v[212:215], v[204:207], v[6:9]
	v_mfma_f32_16x16x32_bf16 v[2:5], v[220:223], v[204:207], v[2:5]
	s_add_i32 s56, s56, 2
	s_add_u32 s24, s24, 0x100
	s_addc_u32 s25, s25, 0
	s_add_u32 s54, s54, 0x100
	s_addc_u32 s55, s55, 0
	s_cmp_gt_u32 s56, 13
	s_barrier
	s_cbranch_scc0 .LBB0_1199
	v_lshl_or_b32 v142, s51, 8, v157
	v_lshl_add_u32 v144, s22, 8, v155
	v_ashrrev_i32_e32 v143, 31, v142
	v_mov_b64_e32 v[146:147], s[10:11]
	v_mad_i64_i32 v[162:163], s[24:25], v144, s50, v[146:147]
	v_lshlrev_b64 v[142:143], 1, v[142:143]
	v_lshl_add_u64 v[162:163], v[162:163], 0, v[142:143]
	v_mov_b32_e32 v238, v162
	v_mov_b32_e32 v239, v163
	global_load_dwordx2 v[168:169], v[238:239], off
	global_load_dwordx2 v[170:171], v[238:239], off offset:32
	global_load_dwordx2 v[172:173], v[238:239], off offset:256
	global_load_dwordx2 v[174:175], v[238:239], off offset:288
	v_mov_b32_e32 v242, 16
	v_mad_i64_i32 v[240:241], s[24:25], v242, s50, v[238:239]
	global_load_dwordx2 v[176:177], v[240:241], off
	global_load_dwordx2 v[178:179], v[240:241], off offset:32
	global_load_dwordx2 v[180:181], v[240:241], off offset:256
	global_load_dwordx2 v[182:183], v[240:241], off offset:288
	v_mov_b32_e32 v242, 32
	v_mad_i64_i32 v[240:241], s[24:25], v242, s50, v[238:239]
	global_load_dwordx2 v[184:185], v[240:241], off
	global_load_dwordx2 v[186:187], v[240:241], off offset:32
	global_load_dwordx2 v[188:189], v[240:241], off offset:256
	global_load_dwordx2 v[192:193], v[240:241], off offset:288
	v_mov_b32_e32 v242, 48
	v_mad_i64_i32 v[240:241], s[24:25], v242, s50, v[238:239]
	global_load_dwordx2 v[194:195], v[240:241], off
	global_load_dwordx2 v[196:197], v[240:241], off offset:32
	global_load_dwordx2 v[198:199], v[240:241], off offset:256
	global_load_dwordx2 v[200:201], v[240:241], off offset:288
	v_mov_b32_e32 v242, 128
	v_mad_i64_i32 v[240:241], s[24:25], v242, s50, v[238:239]
	global_load_dwordx2 v[202:203], v[240:241], off
	global_load_dwordx2 v[204:205], v[240:241], off offset:32
	global_load_dwordx2 v[206:207], v[240:241], off offset:256
	global_load_dwordx2 v[208:209], v[240:241], off offset:288
	v_mov_b32_e32 v242, 144
	v_mad_i64_i32 v[240:241], s[24:25], v242, s50, v[238:239]
	global_load_dwordx2 v[210:211], v[240:241], off
	global_load_dwordx2 v[212:213], v[240:241], off offset:32
	global_load_dwordx2 v[214:215], v[240:241], off offset:256
	global_load_dwordx2 v[216:217], v[240:241], off offset:288
	v_mov_b32_e32 v242, 160
	v_mad_i64_i32 v[240:241], s[24:25], v242, s50, v[238:239]
	global_load_dwordx2 v[218:219], v[240:241], off
	global_load_dwordx2 v[220:221], v[240:241], off offset:32
	global_load_dwordx2 v[222:223], v[240:241], off offset:256
	global_load_dwordx2 v[228:229], v[240:241], off offset:288
	v_mov_b32_e32 v242, 176
	v_mad_i64_i32 v[240:241], s[24:25], v242, s50, v[238:239]
	global_load_dwordx2 v[230:231], v[240:241], off
	global_load_dwordx2 v[232:233], v[240:241], off offset:32
	global_load_dwordx2 v[234:235], v[240:241], off offset:256
	global_load_dwordx2 v[236:237], v[240:241], off offset:288
	s_waitcnt vmcnt(0)
	v_mov_b32_e32 v164, v168
	v_mov_b32_e32 v165, v169
	v_ashrrev_i32_e32 v145, 31, v144
	s_and_b64 vcc, exec, s[0:1]
	s_mov_b32 s51, s14
	s_mov_b32 s22, s16
	s_mov_b64 s[26:27], s[20:21]
	s_nop 0
	v_lshlrev_b32_e32 v166, 16, v164
	v_and_b32_e32 v167, 0xffff0000, v164
	v_lshlrev_b32_e32 v164, 16, v165
	v_and_b32_e32 v165, 0xffff0000, v165
	v_pk_mul_f32 v[128:129], v[128:129], v[164:165]
	v_pk_mul_f32 v[126:127], v[126:127], v[166:167]
	v_lshlrev_b64 v[164:165], 12, v[144:145]
	v_cvt_pk_bf16_f32 v126, v126, v127
	v_cvt_pk_bf16_f32 v127, v128, v129
	v_mov_b32_e32 v128, v170
	v_mov_b32_e32 v129, v171
	v_lshl_add_u64 v[164:165], s[12:13], 0, v[164:165]
	v_lshl_add_u64 v[164:165], v[164:165], 0, v[142:143]
	global_store_dwordx2 v[164:165], v[126:127], off
	s_nop 0
	v_lshlrev_b32_e32 v126, 16, v128
	v_and_b32_e32 v127, 0xffff0000, v128
	v_lshlrev_b32_e32 v128, 16, v129
	v_and_b32_e32 v129, 0xffff0000, v129
	v_pk_mul_f32 v[124:125], v[124:125], v[128:129]
	v_pk_mul_f32 v[122:123], v[122:123], v[126:127]
	s_nop 0
	v_cvt_pk_bf16_f32 v122, v122, v123
	v_cvt_pk_bf16_f32 v123, v124, v125
	v_mov_b32_e32 v124, v172
	v_mov_b32_e32 v125, v173
	s_nop 0
	global_store_dwordx2 v[164:165], v[122:123], off offset:32
	s_nop 0
	v_lshlrev_b32_e32 v122, 16, v124
	v_and_b32_e32 v123, 0xffff0000, v124
	v_lshlrev_b32_e32 v124, 16, v125
	v_and_b32_e32 v125, 0xffff0000, v125
	v_pk_mul_f32 v[120:121], v[120:121], v[124:125]
	v_pk_mul_f32 v[118:119], v[118:119], v[122:123]
	v_or_b32_e32 v122, 16, v144
	v_cvt_pk_bf16_f32 v118, v118, v119
	v_cvt_pk_bf16_f32 v119, v120, v121
	v_mov_b32_e32 v120, v174
	v_mov_b32_e32 v121, v175
	v_mad_i64_i32 v[124:125], s[24:25], v122, s50, v[146:147]
	global_store_dwordx2 v[164:165], v[118:119], off offset:256
	v_lshl_add_u64 v[124:125], v[124:125], 0, v[142:143]
	v_ashrrev_i32_e32 v123, 31, v122
	s_nop 0
	v_lshlrev_b32_e32 v118, 16, v120
	v_and_b32_e32 v119, 0xffff0000, v120
	v_lshlrev_b32_e32 v120, 16, v121
	v_and_b32_e32 v121, 0xffff0000, v121
	v_pk_mul_f32 v[112:113], v[112:113], v[120:121]
	v_pk_mul_f32 v[110:111], v[110:111], v[118:119]
	s_nop 0
	v_cvt_pk_bf16_f32 v110, v110, v111
	v_cvt_pk_bf16_f32 v111, v112, v113
	v_mov_b32_e32 v112, v176
	v_mov_b32_e32 v113, v177
	s_nop 0
	global_store_dwordx2 v[164:165], v[110:111], off offset:288
	s_nop 0
	v_lshlrev_b32_e32 v110, 16, v112
	v_and_b32_e32 v111, 0xffff0000, v112
	v_lshlrev_b32_e32 v112, 16, v113
	v_and_b32_e32 v113, 0xffff0000, v113
	v_pk_mul_f32 v[112:113], v[116:117], v[112:113]
	v_pk_mul_f32 v[110:111], v[114:115], v[110:111]
	v_lshlrev_b64 v[114:115], 12, v[122:123]
	v_cvt_pk_bf16_f32 v110, v110, v111
	v_cvt_pk_bf16_f32 v111, v112, v113
	v_mov_b32_e32 v112, v178
	v_mov_b32_e32 v113, v179
	v_lshl_add_u64 v[114:115], s[12:13], 0, v[114:115]
	v_lshl_add_u64 v[114:115], v[114:115], 0, v[142:143]
	global_store_dwordx2 v[114:115], v[110:111], off
	s_nop 0
	v_lshlrev_b32_e32 v110, 16, v112
	v_and_b32_e32 v111, 0xffff0000, v112
	v_lshlrev_b32_e32 v112, 16, v113
	v_and_b32_e32 v113, 0xffff0000, v113
	v_pk_mul_f32 v[108:109], v[108:109], v[112:113]
	v_pk_mul_f32 v[106:107], v[106:107], v[110:111]
	s_nop 0
	v_cvt_pk_bf16_f32 v106, v106, v107
	v_cvt_pk_bf16_f32 v107, v108, v109
	v_mov_b32_e32 v108, v180
	v_mov_b32_e32 v109, v181
	s_nop 0
	global_store_dwordx2 v[114:115], v[106:107], off offset:32
	s_nop 0
	v_lshlrev_b32_e32 v106, 16, v108
	v_and_b32_e32 v107, 0xffff0000, v108
	v_lshlrev_b32_e32 v108, 16, v109
	v_and_b32_e32 v109, 0xffff0000, v109
	v_pk_mul_f32 v[104:105], v[104:105], v[108:109]
	v_pk_mul_f32 v[102:103], v[102:103], v[106:107]
	v_or_b32_e32 v106, 32, v144
	v_cvt_pk_bf16_f32 v102, v102, v103
	v_cvt_pk_bf16_f32 v103, v104, v105
	v_mov_b32_e32 v104, v182
	v_mov_b32_e32 v105, v183
	v_mad_i64_i32 v[108:109], s[24:25], v106, s50, v[146:147]
	global_store_dwordx2 v[114:115], v[102:103], off offset:256
	v_lshl_add_u64 v[108:109], v[108:109], 0, v[142:143]
	v_ashrrev_i32_e32 v107, 31, v106
	s_nop 0
	v_lshlrev_b32_e32 v102, 16, v104
	v_and_b32_e32 v103, 0xffff0000, v104
	v_lshlrev_b32_e32 v104, 16, v105
	v_and_b32_e32 v105, 0xffff0000, v105
	v_pk_mul_f32 v[96:97], v[96:97], v[104:105]
	v_pk_mul_f32 v[94:95], v[94:95], v[102:103]
	s_nop 0
	v_cvt_pk_bf16_f32 v94, v94, v95
	v_cvt_pk_bf16_f32 v95, v96, v97
	v_mov_b32_e32 v96, v184
	v_mov_b32_e32 v97, v185
	s_nop 0
	global_store_dwordx2 v[114:115], v[94:95], off offset:288
	s_nop 0
	v_lshlrev_b32_e32 v94, 16, v96
	v_and_b32_e32 v95, 0xffff0000, v96
	v_lshlrev_b32_e32 v96, 16, v97
	v_and_b32_e32 v97, 0xffff0000, v97
	v_pk_mul_f32 v[96:97], v[100:101], v[96:97]
	v_pk_mul_f32 v[94:95], v[98:99], v[94:95]
	v_lshlrev_b64 v[98:99], 12, v[106:107]
	v_cvt_pk_bf16_f32 v94, v94, v95
	v_cvt_pk_bf16_f32 v95, v96, v97
	v_mov_b32_e32 v96, v186
	v_mov_b32_e32 v97, v187
	v_lshl_add_u64 v[98:99], s[12:13], 0, v[98:99]
	v_lshl_add_u64 v[98:99], v[98:99], 0, v[142:143]
	global_store_dwordx2 v[98:99], v[94:95], off
	s_nop 0
	v_lshlrev_b32_e32 v94, 16, v96
	v_and_b32_e32 v95, 0xffff0000, v96
	v_lshlrev_b32_e32 v96, 16, v97
	v_and_b32_e32 v97, 0xffff0000, v97
	v_pk_mul_f32 v[92:93], v[92:93], v[96:97]
	v_pk_mul_f32 v[90:91], v[90:91], v[94:95]
	s_nop 0
	v_cvt_pk_bf16_f32 v90, v90, v91
	v_cvt_pk_bf16_f32 v91, v92, v93
	v_mov_b32_e32 v92, v188
	v_mov_b32_e32 v93, v189
	s_nop 0
	global_store_dwordx2 v[98:99], v[90:91], off offset:32
	s_nop 0
	v_lshlrev_b32_e32 v90, 16, v92
	v_and_b32_e32 v91, 0xffff0000, v92
	v_lshlrev_b32_e32 v92, 16, v93
	v_and_b32_e32 v93, 0xffff0000, v93
	v_pk_mul_f32 v[88:89], v[88:89], v[92:93]
	v_pk_mul_f32 v[86:87], v[86:87], v[90:91]
	v_or_b32_e32 v90, 48, v144
	v_cvt_pk_bf16_f32 v86, v86, v87
	v_cvt_pk_bf16_f32 v87, v88, v89
	v_mov_b32_e32 v88, v192
	v_mov_b32_e32 v89, v193
	v_mad_i64_i32 v[92:93], s[24:25], v90, s50, v[146:147]
	global_store_dwordx2 v[98:99], v[86:87], off offset:256
	v_lshl_add_u64 v[92:93], v[92:93], 0, v[142:143]
	v_ashrrev_i32_e32 v91, 31, v90
	s_nop 0
	v_lshlrev_b32_e32 v86, 16, v88
	v_and_b32_e32 v87, 0xffff0000, v88
	v_lshlrev_b32_e32 v88, 16, v89
	v_and_b32_e32 v89, 0xffff0000, v89
	v_pk_mul_f32 v[80:81], v[80:81], v[88:89]
	v_pk_mul_f32 v[78:79], v[78:79], v[86:87]
	s_nop 0
	v_cvt_pk_bf16_f32 v78, v78, v79
	v_cvt_pk_bf16_f32 v79, v80, v81
	v_mov_b32_e32 v80, v194
	v_mov_b32_e32 v81, v195
	s_nop 0
	global_store_dwordx2 v[98:99], v[78:79], off offset:288
	s_nop 0
	v_lshlrev_b32_e32 v78, 16, v80
	v_and_b32_e32 v79, 0xffff0000, v80
	v_lshlrev_b32_e32 v80, 16, v81
	v_and_b32_e32 v81, 0xffff0000, v81
	v_pk_mul_f32 v[80:81], v[84:85], v[80:81]
	v_pk_mul_f32 v[78:79], v[82:83], v[78:79]
	v_lshlrev_b64 v[82:83], 12, v[90:91]
	v_cvt_pk_bf16_f32 v78, v78, v79
	v_cvt_pk_bf16_f32 v79, v80, v81
	v_mov_b32_e32 v80, v196
	v_mov_b32_e32 v81, v197
	v_lshl_add_u64 v[82:83], s[12:13], 0, v[82:83]
	v_lshl_add_u64 v[82:83], v[82:83], 0, v[142:143]
	global_store_dwordx2 v[82:83], v[78:79], off
	s_nop 0
	v_lshlrev_b32_e32 v78, 16, v80
	v_and_b32_e32 v79, 0xffff0000, v80
	v_lshlrev_b32_e32 v80, 16, v81
	v_and_b32_e32 v81, 0xffff0000, v81
	v_pk_mul_f32 v[76:77], v[76:77], v[80:81]
	v_pk_mul_f32 v[74:75], v[74:75], v[78:79]
	s_nop 0
	v_cvt_pk_bf16_f32 v74, v74, v75
	v_cvt_pk_bf16_f32 v75, v76, v77
	v_mov_b32_e32 v76, v198
	v_mov_b32_e32 v77, v199
	s_nop 0
	global_store_dwordx2 v[82:83], v[74:75], off offset:32
	s_nop 0
	v_lshlrev_b32_e32 v74, 16, v76
	v_and_b32_e32 v75, 0xffff0000, v76
	v_lshlrev_b32_e32 v76, 16, v77
	v_and_b32_e32 v77, 0xffff0000, v77
	v_pk_mul_f32 v[72:73], v[72:73], v[76:77]
	v_pk_mul_f32 v[70:71], v[70:71], v[74:75]
	v_add_u32_e32 v74, 0x80, v144
	v_cvt_pk_bf16_f32 v70, v70, v71
	v_cvt_pk_bf16_f32 v71, v72, v73
	v_mov_b32_e32 v72, v200
	v_mov_b32_e32 v73, v201
	v_mad_i64_i32 v[76:77], s[24:25], v74, s50, v[146:147]
	global_store_dwordx2 v[82:83], v[70:71], off offset:256
	v_lshl_add_u64 v[76:77], v[76:77], 0, v[142:143]
	v_ashrrev_i32_e32 v75, 31, v74
	s_nop 0
	v_lshlrev_b32_e32 v70, 16, v72
	v_and_b32_e32 v71, 0xffff0000, v72
	v_lshlrev_b32_e32 v72, 16, v73
	v_and_b32_e32 v73, 0xffff0000, v73
	v_pk_mul_f32 v[68:69], v[68:69], v[72:73]
	v_pk_mul_f32 v[66:67], v[66:67], v[70:71]
	s_nop 0
	v_cvt_pk_bf16_f32 v66, v66, v67
	v_cvt_pk_bf16_f32 v67, v68, v69
	v_mov_b32_e32 v68, v202
	v_mov_b32_e32 v69, v203
	s_nop 0
	global_store_dwordx2 v[82:83], v[66:67], off offset:288
	s_nop 0
	v_lshlrev_b32_e32 v66, 16, v68
	v_and_b32_e32 v67, 0xffff0000, v68
	v_lshlrev_b32_e32 v68, 16, v69
	v_and_b32_e32 v69, 0xffff0000, v69
	v_pk_mul_f32 v[64:65], v[64:65], v[68:69]
	v_pk_mul_f32 v[62:63], v[62:63], v[66:67]
	v_lshlrev_b64 v[66:67], 12, v[74:75]
	v_cvt_pk_bf16_f32 v62, v62, v63
	v_cvt_pk_bf16_f32 v63, v64, v65
	v_mov_b32_e32 v64, v204
	v_mov_b32_e32 v65, v205
	v_lshl_add_u64 v[66:67], s[12:13], 0, v[66:67]
	v_lshl_add_u64 v[66:67], v[66:67], 0, v[142:143]
	global_store_dwordx2 v[66:67], v[62:63], off
	s_nop 0
	v_lshlrev_b32_e32 v62, 16, v64
	v_and_b32_e32 v63, 0xffff0000, v64
	v_lshlrev_b32_e32 v64, 16, v65
	v_and_b32_e32 v65, 0xffff0000, v65
	v_pk_mul_f32 v[60:61], v[60:61], v[64:65]
	v_pk_mul_f32 v[58:59], v[58:59], v[62:63]
	s_nop 0
	v_cvt_pk_bf16_f32 v58, v58, v59
	v_cvt_pk_bf16_f32 v59, v60, v61
	v_mov_b32_e32 v60, v206
	v_mov_b32_e32 v61, v207
	s_nop 0
	global_store_dwordx2 v[66:67], v[58:59], off offset:32
	s_nop 0
	v_lshlrev_b32_e32 v58, 16, v60
	v_and_b32_e32 v59, 0xffff0000, v60
	v_lshlrev_b32_e32 v60, 16, v61
	v_and_b32_e32 v61, 0xffff0000, v61
	v_pk_mul_f32 v[56:57], v[56:57], v[60:61]
	v_pk_mul_f32 v[54:55], v[54:55], v[58:59]
	v_add_u32_e32 v58, 0x90, v144
	v_cvt_pk_bf16_f32 v54, v54, v55
	v_cvt_pk_bf16_f32 v55, v56, v57
	v_mov_b32_e32 v56, v208
	v_mov_b32_e32 v57, v209
	v_mad_i64_i32 v[60:61], s[24:25], v58, s50, v[146:147]
	global_store_dwordx2 v[66:67], v[54:55], off offset:256
	v_lshl_add_u64 v[60:61], v[60:61], 0, v[142:143]
	v_ashrrev_i32_e32 v59, 31, v58
	s_nop 0
	v_lshlrev_b32_e32 v54, 16, v56
	v_and_b32_e32 v55, 0xffff0000, v56
	v_lshlrev_b32_e32 v56, 16, v57
	v_and_b32_e32 v57, 0xffff0000, v57
	v_pk_mul_f32 v[48:49], v[48:49], v[56:57]
	v_pk_mul_f32 v[46:47], v[46:47], v[54:55]
	s_nop 0
	v_cvt_pk_bf16_f32 v46, v46, v47
	v_cvt_pk_bf16_f32 v47, v48, v49
	v_mov_b32_e32 v48, v210
	v_mov_b32_e32 v49, v211
	s_nop 0
	global_store_dwordx2 v[66:67], v[46:47], off offset:288
	s_nop 0
	v_lshlrev_b32_e32 v46, 16, v48
	v_and_b32_e32 v47, 0xffff0000, v48
	v_lshlrev_b32_e32 v48, 16, v49
	v_and_b32_e32 v49, 0xffff0000, v49
	v_pk_mul_f32 v[48:49], v[52:53], v[48:49]
	v_pk_mul_f32 v[46:47], v[50:51], v[46:47]
	v_lshlrev_b64 v[50:51], 12, v[58:59]
	v_cvt_pk_bf16_f32 v46, v46, v47
	v_cvt_pk_bf16_f32 v47, v48, v49
	v_mov_b32_e32 v48, v212
	v_mov_b32_e32 v49, v213
	v_lshl_add_u64 v[50:51], s[12:13], 0, v[50:51]
	v_lshl_add_u64 v[50:51], v[50:51], 0, v[142:143]
	global_store_dwordx2 v[50:51], v[46:47], off
	s_nop 0
	v_lshlrev_b32_e32 v46, 16, v48
	v_and_b32_e32 v47, 0xffff0000, v48
	v_lshlrev_b32_e32 v48, 16, v49
	v_and_b32_e32 v49, 0xffff0000, v49
	v_pk_mul_f32 v[44:45], v[44:45], v[48:49]
	v_pk_mul_f32 v[42:43], v[42:43], v[46:47]
	s_nop 0
	v_cvt_pk_bf16_f32 v42, v42, v43
	v_cvt_pk_bf16_f32 v43, v44, v45
	v_mov_b32_e32 v44, v214
	v_mov_b32_e32 v45, v215
	s_nop 0
	global_store_dwordx2 v[50:51], v[42:43], off offset:32
	s_nop 0
	v_lshlrev_b32_e32 v42, 16, v44
	v_and_b32_e32 v43, 0xffff0000, v44
	v_lshlrev_b32_e32 v44, 16, v45
	v_and_b32_e32 v45, 0xffff0000, v45
	v_pk_mul_f32 v[40:41], v[40:41], v[44:45]
	v_pk_mul_f32 v[38:39], v[38:39], v[42:43]
	v_add_u32_e32 v42, 0xa0, v144
	v_cvt_pk_bf16_f32 v38, v38, v39
	v_cvt_pk_bf16_f32 v39, v40, v41
	v_mov_b32_e32 v40, v216
	v_mov_b32_e32 v41, v217
	v_mad_i64_i32 v[44:45], s[24:25], v42, s50, v[146:147]
	global_store_dwordx2 v[50:51], v[38:39], off offset:256
	v_lshl_add_u64 v[44:45], v[44:45], 0, v[142:143]
	v_ashrrev_i32_e32 v43, 31, v42
	s_nop 0
	v_lshlrev_b32_e32 v38, 16, v40
	v_and_b32_e32 v39, 0xffff0000, v40
	v_lshlrev_b32_e32 v40, 16, v41
	v_and_b32_e32 v41, 0xffff0000, v41
	v_pk_mul_f32 v[32:33], v[32:33], v[40:41]
	v_pk_mul_f32 v[30:31], v[30:31], v[38:39]
	s_nop 0
	v_cvt_pk_bf16_f32 v30, v30, v31
	v_cvt_pk_bf16_f32 v31, v32, v33
	v_mov_b32_e32 v32, v218
	v_mov_b32_e32 v33, v219
	s_nop 0
	global_store_dwordx2 v[50:51], v[30:31], off offset:288
	s_nop 0
	v_lshlrev_b32_e32 v30, 16, v32
	v_and_b32_e32 v31, 0xffff0000, v32
	v_lshlrev_b32_e32 v32, 16, v33
	v_and_b32_e32 v33, 0xffff0000, v33
	v_pk_mul_f32 v[32:33], v[36:37], v[32:33]
	v_pk_mul_f32 v[30:31], v[34:35], v[30:31]
	v_lshlrev_b64 v[34:35], 12, v[42:43]
	v_cvt_pk_bf16_f32 v30, v30, v31
	v_cvt_pk_bf16_f32 v31, v32, v33
	v_mov_b32_e32 v32, v220
	v_mov_b32_e32 v33, v221
	v_lshl_add_u64 v[34:35], s[12:13], 0, v[34:35]
	v_lshl_add_u64 v[34:35], v[34:35], 0, v[142:143]
	global_store_dwordx2 v[34:35], v[30:31], off
	s_nop 0
	v_lshlrev_b32_e32 v30, 16, v32
	v_and_b32_e32 v31, 0xffff0000, v32
	v_lshlrev_b32_e32 v32, 16, v33
	v_and_b32_e32 v33, 0xffff0000, v33
	v_pk_mul_f32 v[28:29], v[28:29], v[32:33]
	v_pk_mul_f32 v[26:27], v[26:27], v[30:31]
	s_nop 0
	v_cvt_pk_bf16_f32 v26, v26, v27
	v_cvt_pk_bf16_f32 v27, v28, v29
	v_mov_b32_e32 v28, v222
	v_mov_b32_e32 v29, v223
	s_nop 0
	global_store_dwordx2 v[34:35], v[26:27], off offset:32
	s_nop 0
	v_lshlrev_b32_e32 v26, 16, v28
	v_and_b32_e32 v27, 0xffff0000, v28
	v_lshlrev_b32_e32 v28, 16, v29
	v_and_b32_e32 v29, 0xffff0000, v29
	v_pk_mul_f32 v[24:25], v[24:25], v[28:29]
	v_pk_mul_f32 v[22:23], v[22:23], v[26:27]
	v_add_u32_e32 v26, 0xb0, v144
	v_cvt_pk_bf16_f32 v22, v22, v23
	v_cvt_pk_bf16_f32 v23, v24, v25
	v_mov_b32_e32 v24, v228
	v_mov_b32_e32 v25, v229
	v_mad_i64_i32 v[28:29], s[24:25], v26, s50, v[146:147]
	global_store_dwordx2 v[34:35], v[22:23], off offset:256
	v_lshl_add_u64 v[28:29], v[28:29], 0, v[142:143]
	v_ashrrev_i32_e32 v27, 31, v26
	s_mov_b64 s[24:25], s[18:19]
	s_nop 0
	v_lshlrev_b32_e32 v22, 16, v24
	v_and_b32_e32 v23, 0xffff0000, v24
	v_lshlrev_b32_e32 v24, 16, v25
	v_and_b32_e32 v25, 0xffff0000, v25
	v_pk_mul_f32 v[16:17], v[16:17], v[24:25]
	v_pk_mul_f32 v[14:15], v[14:15], v[22:23]
	s_nop 0
	v_cvt_pk_bf16_f32 v14, v14, v15
	v_cvt_pk_bf16_f32 v15, v16, v17
	v_mov_b32_e32 v16, v230
	v_mov_b32_e32 v17, v231
	s_nop 0
	global_store_dwordx2 v[34:35], v[14:15], off offset:288
	s_nop 0
	v_lshlrev_b32_e32 v14, 16, v16
	v_and_b32_e32 v15, 0xffff0000, v16
	v_lshlrev_b32_e32 v16, 16, v17
	v_and_b32_e32 v17, 0xffff0000, v17
	v_pk_mul_f32 v[16:17], v[20:21], v[16:17]
	v_pk_mul_f32 v[14:15], v[18:19], v[14:15]
	v_lshlrev_b64 v[18:19], 12, v[26:27]
	v_cvt_pk_bf16_f32 v14, v14, v15
	v_cvt_pk_bf16_f32 v15, v16, v17
	v_mov_b32_e32 v16, v232
	v_mov_b32_e32 v17, v233
	v_lshl_add_u64 v[18:19], s[12:13], 0, v[18:19]
	v_lshl_add_u64 v[18:19], v[18:19], 0, v[142:143]
	global_store_dwordx2 v[18:19], v[14:15], off
	s_nop 0
	v_lshlrev_b32_e32 v14, 16, v16
	v_and_b32_e32 v15, 0xffff0000, v16
	v_lshlrev_b32_e32 v16, 16, v17
	v_and_b32_e32 v17, 0xffff0000, v17
	v_pk_mul_f32 v[12:13], v[12:13], v[16:17]
	v_pk_mul_f32 v[10:11], v[10:11], v[14:15]
	s_nop 0
	v_cvt_pk_bf16_f32 v10, v10, v11
	v_cvt_pk_bf16_f32 v11, v12, v13
	v_mov_b32_e32 v12, v234
	v_mov_b32_e32 v13, v235
	s_nop 0
	global_store_dwordx2 v[18:19], v[10:11], off offset:32
	s_nop 0
	v_lshlrev_b32_e32 v10, 16, v12
	v_and_b32_e32 v11, 0xffff0000, v12
	v_lshlrev_b32_e32 v12, 16, v13
	v_and_b32_e32 v13, 0xffff0000, v13
	v_pk_mul_f32 v[8:9], v[8:9], v[12:13]
	v_pk_mul_f32 v[6:7], v[6:7], v[10:11]
	s_nop 0
	v_cvt_pk_bf16_f32 v6, v6, v7
	v_cvt_pk_bf16_f32 v7, v8, v9
	v_mov_b32_e32 v8, v236
	v_mov_b32_e32 v9, v237
	s_nop 0
	global_store_dwordx2 v[18:19], v[6:7], off offset:256
	s_nop 0
	v_lshlrev_b32_e32 v6, 16, v8
	v_and_b32_e32 v7, 0xffff0000, v8
	v_lshlrev_b32_e32 v8, 16, v9
	v_and_b32_e32 v9, 0xffff0000, v9
	v_pk_mul_f32 v[2:3], v[2:3], v[6:7]
	v_pk_mul_f32 v[4:5], v[4:5], v[8:9]
	v_cvt_pk_bf16_f32 v2, v2, v3
	s_nop 0
	v_cvt_pk_bf16_f32 v3, v4, v5
	global_store_dwordx2 v[18:19], v[2:3], off offset:288
	s_cbranch_vccz .LBB0_1196
	s_waitcnt vmcnt(0)
	s_cmpk_gt_u32 s33, 0xff
	s_cbranch_scc1 .LBB0_1203
	s_barrier

.LBB0_1204:
	v_cndmask_b32_e64 v2, 0, 1, s[2:3]
	v_cmp_ne_u32_e64 s[0:1], 1, v2
	s_andn2_b64 vcc, exec, s[2:3]
	v_readfirstlane_b32 s33, v0
	s_cbranch_vccnz .LBB0_1216
	s_add_u32 s34, s6, 0x4e400000
	s_addc_u32 s35, s7, 0
	s_add_u32 s36, s6, 0x15940000
	s_addc_u32 s37, s7, 0
	s_ashr_i32 s39, s31, 31
	s_lshr_b32 s2, s39, 29
	s_add_i32 s2, s31, s2
	s_lshr_b32 s8, s33, 6
	s_ashr_i32 s9, s2, 3
	s_and_b32 s2, s2, -8
	s_lshr_b32 s3, s33, 8
	s_lshl_b32 s38, s8, 10
	s_sub_i32 s2, s31, s2
	s_cmp_lt_i32 s2, 0
	s_movk_i32 s40, 0x42
	s_cselect_b32 s10, s40, 0x41
	s_mul_i32 s2, s10, s2
	s_add_i32 s2, s2, s9
	s_ashr_i32 s9, s2, 31
	s_lshr_b32 s9, s9, 26
	s_add_i32 s9, s2, s9
	s_ashr_i32 s10, s9, 6
	s_lshl_b32 s12, s10, 3
	s_sub_i32 s10, 0x41, s12
	s_min_u32 s13, s10, 8
	s_andn2_b32 s9, s9, 63
	s_sub_i32 s9, s2, s9
	v_cvt_f32_ubyte0_e32 v3, s13
	v_cvt_f32_i32_e32 v2, s9
	v_rcp_iflag_f32_e32 v4, v3
	s_ashr_i32 s2, s9, 30
	s_or_b32 s2, s2, 1
	v_mov_b32_e32 v131, 0
	v_mul_f32_e32 v4, v2, v4
	v_trunc_f32_e32 v4, v4
	v_fma_f32 v2, -v4, v3, v2
	v_cvt_i32_f32_e32 v4, v4
	v_cmp_ge_f32_e64 s[10:11], |v2|, v3
	s_and_b64 s[10:11], s[10:11], exec
	s_cselect_b32 s2, s2, 0
	v_readfirstlane_b32 s10, v4
	s_add_i32 s2, s10, s2
	s_mul_i32 s10, s2, s13
	s_sub_i32 s9, s9, s10
	s_sext_i32_i8 s9, s9
	s_add_i32 s22, s12, s9
	s_ashr_i32 s23, s22, 31
	s_lshl_b64 s[10:11], s[22:23], 19
	s_add_u32 s24, s34, s10
	s_addc_u32 s25, s35, s11
	s_bfe_i64 s[10:11], s[2:3], 0x80000
	s_lshl_b64 s[10:11], s[10:11], 19
	s_add_u32 s26, s36, s10
	s_addc_u32 s27, s37, s11
	s_add_i32 s23, s38, 0
	s_add_i32 m0, s23, 0x10000
	s_add_i32 s41, s23, 0x2000
	global_load_lds_dwordx4 v130, s[26:27]
	s_add_i32 m0, s23, 0x12000
	s_add_u32 s10, s26, 0x40000
	global_load_lds_dwordx4 v132, s[26:27]
	s_mov_b32 m0, s23
	s_addc_u32 s11, s27, 0
	global_load_lds_dwordx4 v130, s[24:25]
	s_mov_b32 m0, s41
	v_mov_b32_e32 v133, v131
	global_load_lds_dwordx4 v132, s[24:25]
	s_add_i32 m0, s23, 0x14000
	s_mov_b32 s44, 0
	global_load_lds_dwordx4 v130, s[10:11]
	s_add_i32 m0, s23, 0x16000
	s_waitcnt vmcnt(0)
	v_lshl_add_u64 v[8:9], s[26:27], 0, v[130:131]
	global_load_lds_dwordx4 v132, s[10:11]
	s_add_u32 s10, s24, 0x40000
	s_addc_u32 s11, s25, 0
	s_add_i32 s42, s23, 0x4000
	s_mov_b32 m0, s42
	s_add_i32 s43, s23, 0x6000
	global_load_lds_dwordx4 v130, s[10:11]
	s_mov_b32 m0, s43
	v_lshl_add_u64 v[6:7], s[26:27], 0, v[132:133]
	global_load_lds_dwordx4 v132, s[10:11]
	v_lshl_add_u64 v[4:5], s[24:25], 0, v[130:131]
	s_setprio 1
	s_cmp_lg_u32 s3, 1
	v_lshl_add_u64 v[2:3], s[24:25], 0, v[132:133]
	s_cbranch_scc1 .LBB0_1207
	s_barrier
	s_setprio 0

.LBB0_1211:
	ds_read_b128 v[142:145], v158
	ds_read_b128 v[162:165], v158 offset:1024
	ds_read_b128 v[166:169], v158 offset:2048
	ds_read_b128 v[170:173], v158 offset:3072
	s_add_u32 s26, s24, 0xfffc0080
	s_addc_u32 s27, s25, -1
	s_cmp_eq_u32 s57, 12
	s_cselect_b32 s29, s17, s27
	s_cselect_b32 s28, s53, s26
	s_cselect_b32 s27, s15, s56
	s_cselect_b32 s26, s54, s55
	v_lshl_add_u64 v[146:147], s[24:25], 0, v[134:135]
	s_add_i32 m0, s23, 0xc000
	ds_read_b128 v[174:177], v159
	ds_read_b128 v[178:181], v159 offset:1024
	ds_read_b128 v[182:185], v159 offset:2048
	ds_read_b128 v[186:189], v159 offset:3072
	ds_read_b128 v[192:195], v159 offset:4096
	ds_read_b128 v[196:199], v159 offset:5120
	ds_read_b128 v[200:203], v159 offset:6144
	ds_read_b128 v[204:207], v159 offset:7168
	global_load_lds_dwordx4 v[146:147], off
	v_lshl_add_u64 v[146:147], s[24:25], 0, v[136:137]
	s_add_i32 m0, s23, 0xe000
	s_nop 0
	global_load_lds_dwordx4 v[146:147], off
	s_waitcnt lgkmcnt(8)
	s_barrier
	s_waitcnt lgkmcnt(0)
	s_waitcnt lgkmcnt(0)
	v_mfma_f32_16x16x32_bf16 v[126:129], v[142:145], v[174:177], v[126:129]
	v_mfma_f32_16x16x32_bf16 v[122:125], v[166:169], v[174:177], v[122:125]
	v_mfma_f32_16x16x32_bf16 v[110:113], v[142:145], v[182:185], v[110:113]
	v_mfma_f32_16x16x32_bf16 v[106:109], v[166:169], v[182:185], v[106:109]
	v_mfma_f32_16x16x32_bf16 v[94:97], v[142:145], v[192:195], v[94:97]
	v_mfma_f32_16x16x32_bf16 v[90:93], v[166:169], v[192:195], v[90:93]
	v_mfma_f32_16x16x32_bf16 v[78:81], v[142:145], v[200:203], v[78:81]
	v_mfma_f32_16x16x32_bf16 v[74:77], v[166:169], v[200:203], v[74:77]
	v_mfma_f32_16x16x32_bf16 v[126:129], v[162:165], v[178:181], v[126:129]
	v_mfma_f32_16x16x32_bf16 v[122:125], v[170:173], v[178:181], v[122:125]
	v_mfma_f32_16x16x32_bf16 v[110:113], v[162:165], v[186:189], v[110:113]
	v_mfma_f32_16x16x32_bf16 v[106:109], v[170:173], v[186:189], v[106:109]
	v_mfma_f32_16x16x32_bf16 v[94:97], v[162:165], v[196:199], v[94:97]
	v_mfma_f32_16x16x32_bf16 v[90:93], v[170:173], v[196:199], v[90:93]
	v_mfma_f32_16x16x32_bf16 v[78:81], v[162:165], v[204:207], v[78:81]
	v_mfma_f32_16x16x32_bf16 v[74:77], v[170:173], v[204:207], v[74:77]
	s_barrier
	s_add_i32 s58, s48, s38
	v_lshl_add_u64 v[146:147], s[26:27], 0, v[130:131]
	s_mov_b32 m0, s58
	ds_read_b128 v[208:211], v160
	ds_read_b128 v[212:215], v160 offset:1024
	ds_read_b128 v[216:219], v160 offset:2048
	ds_read_b128 v[220:223], v160 offset:3072
	global_load_lds_dwordx4 v[146:147], off
	v_lshl_add_u64 v[190:191], s[26:27], 0, v[132:133]
	s_add_i32 m0, s58, 0x2000
	s_nop 0
	global_load_lds_dwordx4 v[190:191], off
	s_barrier
	s_waitcnt lgkmcnt(0)
	s_waitcnt lgkmcnt(0)
	v_mfma_f32_16x16x32_bf16 v[118:121], v[208:211], v[174:177], v[118:121]
	v_mfma_f32_16x16x32_bf16 v[114:117], v[216:219], v[174:177], v[114:117]
	v_mfma_f32_16x16x32_bf16 v[102:105], v[208:211], v[182:185], v[102:105]
	v_mfma_f32_16x16x32_bf16 v[98:101], v[216:219], v[182:185], v[98:101]
	v_mfma_f32_16x16x32_bf16 v[86:89], v[208:211], v[192:195], v[86:89]
	v_mfma_f32_16x16x32_bf16 v[82:85], v[216:219], v[192:195], v[82:85]
	v_mfma_f32_16x16x32_bf16 v[70:73], v[208:211], v[200:203], v[70:73]
	v_mfma_f32_16x16x32_bf16 v[66:69], v[216:219], v[200:203], v[66:69]
	v_mfma_f32_16x16x32_bf16 v[118:121], v[212:215], v[178:181], v[118:121]
	v_mfma_f32_16x16x32_bf16 v[114:117], v[220:223], v[178:181], v[114:117]
	v_mfma_f32_16x16x32_bf16 v[102:105], v[212:215], v[186:189], v[102:105]
	v_mfma_f32_16x16x32_bf16 v[98:101], v[220:223], v[186:189], v[98:101]
	v_mfma_f32_16x16x32_bf16 v[86:89], v[212:215], v[196:199], v[86:89]
	v_mfma_f32_16x16x32_bf16 v[82:85], v[220:223], v[196:199], v[82:85]
	v_mfma_f32_16x16x32_bf16 v[70:73], v[212:215], v[204:207], v[70:73]
	v_mfma_f32_16x16x32_bf16 v[66:69], v[220:223], v[204:207], v[66:69]
	s_mov_b32 m0, s23
	v_lshl_add_u64 v[224:225], s[28:29], 0, v[130:131]
	s_barrier
	ds_read_b128 v[174:177], v159 offset:16384
	ds_read_b128 v[178:181], v159 offset:17408
	ds_read_b128 v[182:185], v159 offset:18432
	ds_read_b128 v[186:189], v159 offset:19456
	ds_read_b128 v[192:195], v159 offset:20480
	ds_read_b128 v[196:199], v159 offset:21504
	ds_read_b128 v[200:203], v159 offset:22528
	ds_read_b128 v[204:207], v159 offset:23552
	global_load_lds_dwordx4 v[224:225], off
	v_lshl_add_u64 v[226:227], s[28:29], 0, v[132:133]
	s_mov_b32 m0, s41
	s_nop 0
	global_load_lds_dwordx4 v[226:227], off
	s_barrier
	s_waitcnt lgkmcnt(0)
	s_waitcnt lgkmcnt(0)
	v_mfma_f32_16x16x32_bf16 v[62:65], v[142:145], v[174:177], v[62:65]
	v_mfma_f32_16x16x32_bf16 v[58:61], v[166:169], v[174:177], v[58:61]
	v_mfma_f32_16x16x32_bf16 v[46:49], v[142:145], v[182:185], v[46:49]
	v_mfma_f32_16x16x32_bf16 v[42:45], v[166:169], v[182:185], v[42:45]
	v_mfma_f32_16x16x32_bf16 v[30:33], v[142:145], v[192:195], v[30:33]
	v_mfma_f32_16x16x32_bf16 v[26:29], v[166:169], v[192:195], v[26:29]
	v_mfma_f32_16x16x32_bf16 v[14:17], v[142:145], v[200:203], v[14:17]
	v_mfma_f32_16x16x32_bf16 v[10:13], v[166:169], v[200:203], v[10:13]
	v_mfma_f32_16x16x32_bf16 v[62:65], v[162:165], v[178:181], v[62:65]
	v_mfma_f32_16x16x32_bf16 v[58:61], v[170:173], v[178:181], v[58:61]
	v_mfma_f32_16x16x32_bf16 v[46:49], v[162:165], v[186:189], v[46:49]
	v_mfma_f32_16x16x32_bf16 v[42:45], v[170:173], v[186:189], v[42:45]
	v_mfma_f32_16x16x32_bf16 v[30:33], v[162:165], v[196:199], v[30:33]
	v_mfma_f32_16x16x32_bf16 v[26:29], v[170:173], v[196:199], v[26:29]
	v_mfma_f32_16x16x32_bf16 v[14:17], v[162:165], v[204:207], v[14:17]
	v_mfma_f32_16x16x32_bf16 v[10:13], v[170:173], v[204:207], v[10:13]
	s_barrier
	s_add_u32 s58, s26, 0x40000
	s_addc_u32 s59, s27, 0
	s_add_i32 s60, s49, s38
	v_lshl_add_u64 v[142:143], s[58:59], 0, v[130:131]
	s_mov_b32 m0, s60
	s_nop 0
	global_load_lds_dwordx4 v[142:143], off
	v_lshl_add_u64 v[142:143], s[58:59], 0, v[132:133]
	s_add_i32 m0, s60, 0x2000
	s_nop 0
	global_load_lds_dwordx4 v[142:143], off
	s_waitcnt vmcnt(6)
	s_barrier
	v_mfma_f32_16x16x32_bf16 v[54:57], v[208:211], v[174:177], v[54:57]
	v_mfma_f32_16x16x32_bf16 v[50:53], v[216:219], v[174:177], v[50:53]
	v_mfma_f32_16x16x32_bf16 v[38:41], v[208:211], v[182:185], v[38:41]
	v_mfma_f32_16x16x32_bf16 v[34:37], v[216:219], v[182:185], v[34:37]
	v_mfma_f32_16x16x32_bf16 v[22:25], v[208:211], v[192:195], v[22:25]
	v_mfma_f32_16x16x32_bf16 v[18:21], v[216:219], v[192:195], v[18:21]
	v_mfma_f32_16x16x32_bf16 v[6:9], v[208:211], v[200:203], v[6:9]
	v_mfma_f32_16x16x32_bf16 v[2:5], v[216:219], v[200:203], v[2:5]
	v_mfma_f32_16x16x32_bf16 v[54:57], v[212:215], v[178:181], v[54:57]
	v_mfma_f32_16x16x32_bf16 v[50:53], v[220:223], v[178:181], v[50:53]
	v_mfma_f32_16x16x32_bf16 v[38:41], v[212:215], v[186:189], v[38:41]
	v_mfma_f32_16x16x32_bf16 v[34:37], v[220:223], v[186:189], v[34:37]
	v_mfma_f32_16x16x32_bf16 v[22:25], v[212:215], v[196:199], v[22:25]
	v_mfma_f32_16x16x32_bf16 v[18:21], v[220:223], v[196:199], v[18:21]
	v_mfma_f32_16x16x32_bf16 v[6:9], v[212:215], v[204:207], v[6:9]
	v_mfma_f32_16x16x32_bf16 v[2:5], v[220:223], v[204:207], v[2:5]
	s_add_i32 s58, 0, 0x18000
	v_add_u32_e32 v161, s58, v156
	s_barrier
	ds_read_b128 v[142:145], v161
	ds_read_b128 v[162:165], v161 offset:1024
	ds_read_b128 v[166:169], v161 offset:2048
	ds_read_b128 v[170:173], v161 offset:3072
	s_add_u32 s28, s28, 0x40000
	s_addc_u32 s29, s29, 0
	s_mov_b32 m0, s42
	v_lshl_add_u64 v[208:209], s[28:29], 0, v[130:131]
	ds_read_b128 v[174:177], v159 offset:32768
	ds_read_b128 v[178:181], v159 offset:33792
	ds_read_b128 v[182:185], v159 offset:34816
	ds_read_b128 v[186:189], v159 offset:35840
	ds_read_b128 v[192:195], v159 offset:36864
	ds_read_b128 v[196:199], v159 offset:37888
	ds_read_b128 v[200:203], v159 offset:38912
	ds_read_b128 v[204:207], v159 offset:39936
	global_load_lds_dwordx4 v[208:209], off
	v_lshl_add_u64 v[208:209], s[28:29], 0, v[132:133]
	s_mov_b32 m0, s43
	s_nop 0
	global_load_lds_dwordx4 v[208:209], off
	s_waitcnt lgkmcnt(8)
	s_barrier
	s_waitcnt lgkmcnt(0)
	s_waitcnt lgkmcnt(0)
	v_mfma_f32_16x16x32_bf16 v[126:129], v[142:145], v[174:177], v[126:129]
	v_mfma_f32_16x16x32_bf16 v[122:125], v[166:169], v[174:177], v[122:125]
	v_mfma_f32_16x16x32_bf16 v[110:113], v[142:145], v[182:185], v[110:113]
	v_mfma_f32_16x16x32_bf16 v[106:109], v[166:169], v[182:185], v[106:109]
	v_mfma_f32_16x16x32_bf16 v[94:97], v[142:145], v[192:195], v[94:97]
	v_mfma_f32_16x16x32_bf16 v[90:93], v[166:169], v[192:195], v[90:93]
	v_mfma_f32_16x16x32_bf16 v[78:81], v[142:145], v[200:203], v[78:81]
	v_mfma_f32_16x16x32_bf16 v[74:77], v[166:169], v[200:203], v[74:77]
	v_mfma_f32_16x16x32_bf16 v[126:129], v[162:165], v[178:181], v[126:129]
	v_mfma_f32_16x16x32_bf16 v[122:125], v[170:173], v[178:181], v[122:125]
	v_mfma_f32_16x16x32_bf16 v[110:113], v[162:165], v[186:189], v[110:113]
	v_mfma_f32_16x16x32_bf16 v[106:109], v[170:173], v[186:189], v[106:109]
	v_mfma_f32_16x16x32_bf16 v[94:97], v[162:165], v[196:199], v[94:97]
	v_mfma_f32_16x16x32_bf16 v[90:93], v[170:173], v[196:199], v[90:93]
	v_mfma_f32_16x16x32_bf16 v[78:81], v[162:165], v[204:207], v[78:81]
	v_mfma_f32_16x16x32_bf16 v[74:77], v[170:173], v[204:207], v[74:77]
	s_barrier
	s_add_i32 s28, 0, 0x1c000
	s_add_i32 s29, s58, s38
	v_add_u32_e32 v161, s28, v156
	v_lshl_add_u64 v[146:147], v[146:147], 0, s[8:9]
	s_mov_b32 m0, s29
	ds_read_b128 v[208:211], v161
	ds_read_b128 v[212:215], v161 offset:1024
	ds_read_b128 v[216:219], v161 offset:2048
	ds_read_b128 v[220:223], v161 offset:3072
	global_load_lds_dwordx4 v[146:147], off
	v_lshl_add_u64 v[146:147], v[190:191], 0, s[8:9]
	s_add_i32 m0, s29, 0x2000
	s_nop 0
	global_load_lds_dwordx4 v[146:147], off
	s_barrier
	s_waitcnt lgkmcnt(0)
	s_waitcnt lgkmcnt(0)
	v_mfma_f32_16x16x32_bf16 v[118:121], v[208:211], v[174:177], v[118:121]
	v_mfma_f32_16x16x32_bf16 v[114:117], v[216:219], v[174:177], v[114:117]
	v_mfma_f32_16x16x32_bf16 v[102:105], v[208:211], v[182:185], v[102:105]
	v_mfma_f32_16x16x32_bf16 v[98:101], v[216:219], v[182:185], v[98:101]
	v_mfma_f32_16x16x32_bf16 v[86:89], v[208:211], v[192:195], v[86:89]
	v_mfma_f32_16x16x32_bf16 v[82:85], v[216:219], v[192:195], v[82:85]
	v_mfma_f32_16x16x32_bf16 v[70:73], v[208:211], v[200:203], v[70:73]
	v_mfma_f32_16x16x32_bf16 v[66:69], v[216:219], v[200:203], v[66:69]
	v_mfma_f32_16x16x32_bf16 v[118:121], v[212:215], v[178:181], v[118:121]
	v_mfma_f32_16x16x32_bf16 v[114:117], v[220:223], v[178:181], v[114:117]
	v_mfma_f32_16x16x32_bf16 v[102:105], v[212:215], v[186:189], v[102:105]
	v_mfma_f32_16x16x32_bf16 v[98:101], v[220:223], v[186:189], v[98:101]
	v_mfma_f32_16x16x32_bf16 v[86:89], v[212:215], v[196:199], v[86:89]
	v_mfma_f32_16x16x32_bf16 v[82:85], v[220:223], v[196:199], v[82:85]
	v_mfma_f32_16x16x32_bf16 v[70:73], v[212:215], v[204:207], v[70:73]
	v_mfma_f32_16x16x32_bf16 v[66:69], v[220:223], v[204:207], v[66:69]
	s_mov_b32 m0, s45
	v_lshl_add_u64 v[146:147], v[224:225], 0, s[8:9]
	s_barrier
	ds_read_b128 v[174:177], v159 offset:49152
	ds_read_b128 v[178:181], v159 offset:50176
	ds_read_b128 v[182:185], v159 offset:51200
	ds_read_b128 v[186:189], v159 offset:52224
	ds_read_b128 v[192:195], v159 offset:53248
	ds_read_b128 v[196:199], v159 offset:54272
	ds_read_b128 v[200:203], v159 offset:55296
	ds_read_b128 v[204:207], v159 offset:56320
	global_load_lds_dwordx4 v[146:147], off
	v_lshl_add_u64 v[146:147], v[226:227], 0, s[8:9]
	s_mov_b32 m0, s46
	s_nop 0
	global_load_lds_dwordx4 v[146:147], off
	s_barrier
	s_waitcnt lgkmcnt(0)
	s_waitcnt lgkmcnt(0)
	v_mfma_f32_16x16x32_bf16 v[62:65], v[142:145], v[174:177], v[62:65]
	v_mfma_f32_16x16x32_bf16 v[58:61], v[166:169], v[174:177], v[58:61]
	v_mfma_f32_16x16x32_bf16 v[46:49], v[142:145], v[182:185], v[46:49]
	v_mfma_f32_16x16x32_bf16 v[42:45], v[166:169], v[182:185], v[42:45]
	v_mfma_f32_16x16x32_bf16 v[30:33], v[142:145], v[192:195], v[30:33]
	v_mfma_f32_16x16x32_bf16 v[26:29], v[166:169], v[192:195], v[26:29]
	v_mfma_f32_16x16x32_bf16 v[14:17], v[142:145], v[200:203], v[14:17]
	v_mfma_f32_16x16x32_bf16 v[10:13], v[166:169], v[200:203], v[10:13]
	v_mfma_f32_16x16x32_bf16 v[62:65], v[162:165], v[178:181], v[62:65]
	v_mfma_f32_16x16x32_bf16 v[58:61], v[170:173], v[178:181], v[58:61]
	v_mfma_f32_16x16x32_bf16 v[46:49], v[162:165], v[186:189], v[46:49]
	v_mfma_f32_16x16x32_bf16 v[42:45], v[170:173], v[186:189], v[42:45]
	v_mfma_f32_16x16x32_bf16 v[30:33], v[162:165], v[196:199], v[30:33]
	v_mfma_f32_16x16x32_bf16 v[26:29], v[170:173], v[196:199], v[26:29]
	v_mfma_f32_16x16x32_bf16 v[14:17], v[162:165], v[204:207], v[14:17]
	v_mfma_f32_16x16x32_bf16 v[10:13], v[170:173], v[204:207], v[10:13]
	s_barrier
	s_add_u32 s26, s26, 0x40080
	s_addc_u32 s27, s27, 0
	s_add_i32 s28, s28, s38
	v_lshl_add_u64 v[142:143], s[26:27], 0, v[130:131]
	s_mov_b32 m0, s28
	s_nop 0
	global_load_lds_dwordx4 v[142:143], off
	v_lshl_add_u64 v[142:143], s[26:27], 0, v[132:133]
	s_add_i32 m0, s28, 0x2000
	s_nop 0
	global_load_lds_dwordx4 v[142:143], off
	s_waitcnt vmcnt(6)
	s_barrier
	v_mfma_f32_16x16x32_bf16 v[54:57], v[208:211], v[174:177], v[54:57]
	v_mfma_f32_16x16x32_bf16 v[50:53], v[216:219], v[174:177], v[50:53]
	v_mfma_f32_16x16x32_bf16 v[38:41], v[208:211], v[182:185], v[38:41]
	v_mfma_f32_16x16x32_bf16 v[34:37], v[216:219], v[182:185], v[34:37]
	v_mfma_f32_16x16x32_bf16 v[22:25], v[208:211], v[192:195], v[22:25]
	v_mfma_f32_16x16x32_bf16 v[18:21], v[216:219], v[192:195], v[18:21]
	v_mfma_f32_16x16x32_bf16 v[6:9], v[208:211], v[200:203], v[6:9]
	v_mfma_f32_16x16x32_bf16 v[2:5], v[216:219], v[200:203], v[2:5]
	v_mfma_f32_16x16x32_bf16 v[54:57], v[212:215], v[178:181], v[54:57]
	v_mfma_f32_16x16x32_bf16 v[50:53], v[220:223], v[178:181], v[50:53]
	v_mfma_f32_16x16x32_bf16 v[38:41], v[212:215], v[186:189], v[38:41]
	v_mfma_f32_16x16x32_bf16 v[34:37], v[220:223], v[186:189], v[34:37]
	v_mfma_f32_16x16x32_bf16 v[22:25], v[212:215], v[196:199], v[22:25]
	v_mfma_f32_16x16x32_bf16 v[18:21], v[220:223], v[196:199], v[18:21]
	v_mfma_f32_16x16x32_bf16 v[6:9], v[212:215], v[204:207], v[6:9]
	v_mfma_f32_16x16x32_bf16 v[2:5], v[220:223], v[204:207], v[2:5]
	s_add_i32 s57, s57, 2
	s_add_u32 s24, s24, 0x100
	s_addc_u32 s25, s25, 0
	s_add_u32 s55, s55, 0x100
	s_addc_u32 s56, s56, 0
	s_cmp_gt_u32 s57, 13
	s_barrier
	s_cbranch_scc0 .LBB0_1211
	v_lshl_or_b32 v142, s52, 8, v157
	v_lshl_add_u32 v144, s22, 8, v155
	v_ashrrev_i32_e32 v143, 31, v142
	v_mov_b64_e32 v[146:147], s[6:7]
	v_ashrrev_i32_e32 v145, 31, v144
	v_mad_i64_i32 v[162:163], s[24:25], v144, s50, v[146:147]
	v_lshlrev_b64 v[142:143], 1, v[142:143]
	v_lshl_add_u64 v[162:163], v[162:163], 0, v[142:143]
	v_lshlrev_b64 v[166:167], 12, v[144:145]
	v_add_co_u32_e32 v164, vcc, 0x2ec41000, v162
	v_lshl_add_u64 v[166:167], s[10:11], 0, v[166:167]
	s_nop 0
	v_addc_co_u32_e32 v165, vcc, 0, v163, vcc
	v_lshl_add_u64 v[166:167], v[166:167], 0, v[142:143]
	v_mov_b32_e32 v228, v164
	v_mov_b32_e32 v229, v165
	v_mov_b32_e32 v232, v166
	v_mov_b32_e32 v233, v167
	v_mov_b32_e32 v237, 0x1000
	global_load_dwordx2 v[174:175], v[228:229], off
	global_load_dwordx2 v[176:177], v[232:233], off
	global_load_dwordx2 v[178:179], v[228:229], off offset:32
	global_load_dwordx2 v[180:181], v[232:233], off offset:32
	global_load_dwordx2 v[182:183], v[228:229], off offset:256
	global_load_dwordx2 v[184:185], v[232:233], off offset:256
	global_load_dwordx2 v[186:187], v[228:229], off offset:288
	global_load_dwordx2 v[188:189], v[232:233], off offset:288
	v_mov_b32_e32 v236, 16
	v_mad_i64_i32 v[230:231], s[24:25], v236, s50, v[228:229]
	v_mad_i64_i32 v[234:235], s[24:25], v236, v237, v[232:233]
	global_load_dwordx2 v[192:193], v[230:231], off
	global_load_dwordx2 v[194:195], v[234:235], off
	global_load_dwordx2 v[196:197], v[230:231], off offset:32
	global_load_dwordx2 v[198:199], v[234:235], off offset:32
	global_load_dwordx2 v[200:201], v[230:231], off offset:256
	global_load_dwordx2 v[202:203], v[234:235], off offset:256
	global_load_dwordx2 v[204:205], v[230:231], off offset:288
	global_load_dwordx2 v[206:207], v[234:235], off offset:288
	v_mov_b32_e32 v236, 32
	v_mad_i64_i32 v[230:231], s[24:25], v236, s50, v[228:229]
	v_mad_i64_i32 v[234:235], s[24:25], v236, v237, v[232:233]
	global_load_dwordx2 v[208:209], v[230:231], off
	global_load_dwordx2 v[210:211], v[234:235], off
	global_load_dwordx2 v[212:213], v[230:231], off offset:32
	global_load_dwordx2 v[214:215], v[234:235], off offset:32
	global_load_dwordx2 v[216:217], v[230:231], off offset:256
	global_load_dwordx2 v[218:219], v[234:235], off offset:256
	global_load_dwordx2 v[220:221], v[230:231], off offset:288
	global_load_dwordx2 v[222:223], v[234:235], off offset:288
	s_waitcnt vmcnt(0)
	v_mov_b32_e32 v164, v174
	v_mov_b32_e32 v165, v175
	v_lshl_add_u64 v[162:163], v[162:163], 0, s[12:13]
	v_mov_b32_e32 v168, v176
	v_mov_b32_e32 v169, v177
	s_mov_b32 s52, s14
	s_mov_b32 s22, s16
	s_mov_b64 s[26:27], s[20:21]
	s_nop 0
	v_lshlrev_b32_e32 v170, 16, v164
	v_and_b32_e32 v171, 0xffff0000, v164
	v_lshlrev_b32_e32 v164, 16, v165
	v_and_b32_e32 v165, 0xffff0000, v165
	v_lshlrev_b32_e32 v172, 16, v168
	v_and_b32_e32 v173, 0xffff0000, v168
	v_lshlrev_b32_e32 v168, 16, v169
	v_and_b32_e32 v169, 0xffff0000, v169
	v_pk_fma_f32 v[128:129], v[128:129], v[164:165], v[168:169]
	v_pk_fma_f32 v[126:127], v[126:127], v[170:171], v[172:173]
	s_nop 0
	v_cvt_pk_bf16_f32 v126, v126, v127
	v_cvt_pk_bf16_f32 v127, v128, v129
	v_mov_b32_e32 v128, v178
	v_mov_b32_e32 v129, v179
	v_mov_b32_e32 v164, v180
	v_mov_b32_e32 v165, v181
	s_nop 0
	v_lshlrev_b32_e32 v168, 16, v164
	global_store_dwordx2 v[166:167], v[126:127], off
	v_lshlrev_b32_e32 v126, 16, v128
	v_and_b32_e32 v127, 0xffff0000, v128
	v_lshlrev_b32_e32 v128, 16, v129
	v_and_b32_e32 v129, 0xffff0000, v129
	v_and_b32_e32 v169, 0xffff0000, v164
	v_lshlrev_b32_e32 v164, 16, v165
	v_and_b32_e32 v165, 0xffff0000, v165
	v_pk_fma_f32 v[124:125], v[124:125], v[128:129], v[164:165]
	v_pk_fma_f32 v[122:123], v[122:123], v[126:127], v[168:169]
	s_nop 0
	v_cvt_pk_bf16_f32 v122, v122, v123
	v_cvt_pk_bf16_f32 v123, v124, v125
	v_mov_b32_e32 v124, v182
	v_mov_b32_e32 v125, v183
	v_mov_b32_e32 v126, v184
	v_mov_b32_e32 v127, v185
	s_nop 0
	v_lshlrev_b32_e32 v128, 16, v126
	global_store_dwordx2 v[166:167], v[122:123], off offset:32
	v_lshlrev_b32_e32 v122, 16, v124
	v_and_b32_e32 v123, 0xffff0000, v124
	v_lshlrev_b32_e32 v124, 16, v125
	v_and_b32_e32 v125, 0xffff0000, v125
	v_and_b32_e32 v129, 0xffff0000, v126
	v_lshlrev_b32_e32 v126, 16, v127
	v_and_b32_e32 v127, 0xffff0000, v127
	v_pk_fma_f32 v[120:121], v[120:121], v[124:125], v[126:127]
	v_pk_fma_f32 v[118:119], v[118:119], v[122:123], v[128:129]
	v_or_b32_e32 v124, 16, v144
	v_cvt_pk_bf16_f32 v118, v118, v119
	v_cvt_pk_bf16_f32 v119, v120, v121
	v_mov_b32_e32 v120, v186
	v_mov_b32_e32 v121, v187
	v_mov_b32_e32 v122, v188
	v_mov_b32_e32 v123, v189
	v_ashrrev_i32_e32 v125, 31, v124
	v_mad_i64_i32 v[126:127], s[24:25], v124, s50, v[146:147]
	global_store_dwordx2 v[166:167], v[118:119], off offset:256
	v_lshl_add_u64 v[126:127], v[126:127], 0, v[142:143]
	v_add_co_u32_e32 v128, vcc, s51, v126
	s_nop 0
	v_lshlrev_b32_e32 v118, 16, v120
	v_and_b32_e32 v119, 0xffff0000, v120
	v_lshlrev_b32_e32 v162, 16, v122
	v_and_b32_e32 v163, 0xffff0000, v122
	v_pk_fma_f32 v[114:115], v[114:115], v[118:119], v[162:163]
	v_lshlrev_b64 v[118:119], 12, v[124:125]
	v_lshlrev_b32_e32 v120, 16, v121
	v_and_b32_e32 v121, 0xffff0000, v121
	v_lshlrev_b32_e32 v122, 16, v123
	v_and_b32_e32 v123, 0xffff0000, v123
	v_lshl_add_u64 v[118:119], s[10:11], 0, v[118:119]
	v_addc_co_u32_e32 v129, vcc, 0, v127, vcc
	v_pk_fma_f32 v[116:117], v[116:117], v[120:121], v[122:123]
	v_lshl_add_u64 v[118:119], v[118:119], 0, v[142:143]
	v_cvt_pk_bf16_f32 v114, v114, v115
	v_cvt_pk_bf16_f32 v115, v116, v117
	v_mov_b32_e32 v116, v192
	v_mov_b32_e32 v117, v193
	v_mov_b32_e32 v120, v194
	v_mov_b32_e32 v121, v195
	v_lshl_add_u64 v[122:123], v[126:127], 0, s[12:13]
	global_store_dwordx2 v[166:167], v[114:115], off offset:288
	s_nop 0
	v_lshlrev_b32_e32 v114, 16, v116
	v_and_b32_e32 v115, 0xffff0000, v116
	v_lshlrev_b32_e32 v116, 16, v117
	v_and_b32_e32 v117, 0xffff0000, v117
	v_lshlrev_b32_e32 v124, 16, v120
	v_and_b32_e32 v125, 0xffff0000, v120
	v_lshlrev_b32_e32 v120, 16, v121
	v_and_b32_e32 v121, 0xffff0000, v121
	v_pk_fma_f32 v[112:113], v[112:113], v[116:117], v[120:121]
	v_pk_fma_f32 v[110:111], v[110:111], v[114:115], v[124:125]
	s_nop 0
	v_cvt_pk_bf16_f32 v110, v110, v111
	v_cvt_pk_bf16_f32 v111, v112, v113
	v_mov_b32_e32 v112, v196
	v_mov_b32_e32 v113, v197
	v_mov_b32_e32 v114, v198
	v_mov_b32_e32 v115, v199
	s_nop 0
	v_lshlrev_b32_e32 v116, 16, v114
	global_store_dwordx2 v[118:119], v[110:111], off
	v_lshlrev_b32_e32 v110, 16, v112
	v_and_b32_e32 v111, 0xffff0000, v112
	v_lshlrev_b32_e32 v112, 16, v113
	v_and_b32_e32 v113, 0xffff0000, v113
	v_and_b32_e32 v117, 0xffff0000, v114
	v_lshlrev_b32_e32 v114, 16, v115
	v_and_b32_e32 v115, 0xffff0000, v115
	v_pk_fma_f32 v[108:109], v[108:109], v[112:113], v[114:115]
	v_pk_fma_f32 v[106:107], v[106:107], v[110:111], v[116:117]
	s_nop 0
	v_cvt_pk_bf16_f32 v106, v106, v107
	v_cvt_pk_bf16_f32 v107, v108, v109
	v_mov_b32_e32 v108, v200
	v_mov_b32_e32 v109, v201
	v_mov_b32_e32 v110, v202
	v_mov_b32_e32 v111, v203
	s_nop 0
	v_lshlrev_b32_e32 v112, 16, v110
	global_store_dwordx2 v[118:119], v[106:107], off offset:32
	v_lshlrev_b32_e32 v106, 16, v108
	v_and_b32_e32 v107, 0xffff0000, v108
	v_lshlrev_b32_e32 v108, 16, v109
	v_and_b32_e32 v109, 0xffff0000, v109
	v_and_b32_e32 v113, 0xffff0000, v110
	v_lshlrev_b32_e32 v110, 16, v111
	v_and_b32_e32 v111, 0xffff0000, v111
	v_pk_fma_f32 v[104:105], v[104:105], v[108:109], v[110:111]
	v_pk_fma_f32 v[102:103], v[102:103], v[106:107], v[112:113]
	v_or_b32_e32 v108, 32, v144
	v_cvt_pk_bf16_f32 v102, v102, v103
	v_cvt_pk_bf16_f32 v103, v104, v105
	v_mov_b32_e32 v104, v204
	v_mov_b32_e32 v105, v205
	v_mov_b32_e32 v106, v206
	v_mov_b32_e32 v107, v207
	v_ashrrev_i32_e32 v109, 31, v108
	v_mad_i64_i32 v[110:111], s[24:25], v108, s50, v[146:147]
	global_store_dwordx2 v[118:119], v[102:103], off offset:256
	v_lshl_add_u64 v[110:111], v[110:111], 0, v[142:143]
	v_add_co_u32_e32 v112, vcc, s51, v110
	s_nop 0
	v_lshlrev_b32_e32 v102, 16, v104
	v_and_b32_e32 v103, 0xffff0000, v104
	v_lshlrev_b32_e32 v114, 16, v106
	v_and_b32_e32 v115, 0xffff0000, v106
	v_pk_fma_f32 v[98:99], v[98:99], v[102:103], v[114:115]
	v_lshlrev_b64 v[102:103], 12, v[108:109]
	v_lshlrev_b32_e32 v104, 16, v105
	v_and_b32_e32 v105, 0xffff0000, v105
	v_lshlrev_b32_e32 v106, 16, v107
	v_and_b32_e32 v107, 0xffff0000, v107
	v_lshl_add_u64 v[102:103], s[10:11], 0, v[102:103]
	v_addc_co_u32_e32 v113, vcc, 0, v111, vcc
	v_pk_fma_f32 v[100:101], v[100:101], v[104:105], v[106:107]
	v_lshl_add_u64 v[102:103], v[102:103], 0, v[142:143]
	v_cvt_pk_bf16_f32 v98, v98, v99
	v_cvt_pk_bf16_f32 v99, v100, v101
	v_mov_b32_e32 v100, v208
	v_mov_b32_e32 v101, v209
	v_mov_b32_e32 v104, v210
	v_mov_b32_e32 v105, v211
	v_lshl_add_u64 v[106:107], v[110:111], 0, s[12:13]
	global_store_dwordx2 v[118:119], v[98:99], off offset:288
	s_nop 0
	v_lshlrev_b32_e32 v98, 16, v100
	v_and_b32_e32 v99, 0xffff0000, v100
	v_lshlrev_b32_e32 v100, 16, v101
	v_and_b32_e32 v101, 0xffff0000, v101
	v_lshlrev_b32_e32 v108, 16, v104
	v_and_b32_e32 v109, 0xffff0000, v104
	v_lshlrev_b32_e32 v104, 16, v105
	v_and_b32_e32 v105, 0xffff0000, v105
	v_pk_fma_f32 v[96:97], v[96:97], v[100:101], v[104:105]
	v_pk_fma_f32 v[94:95], v[94:95], v[98:99], v[108:109]
	s_nop 0
	v_cvt_pk_bf16_f32 v94, v94, v95
	v_cvt_pk_bf16_f32 v95, v96, v97
	v_mov_b32_e32 v96, v212
	v_mov_b32_e32 v97, v213
	v_mov_b32_e32 v98, v214
	v_mov_b32_e32 v99, v215
	s_nop 0
	v_lshlrev_b32_e32 v100, 16, v98
	global_store_dwordx2 v[102:103], v[94:95], off
	v_lshlrev_b32_e32 v94, 16, v96
	v_and_b32_e32 v95, 0xffff0000, v96
	v_lshlrev_b32_e32 v96, 16, v97
	v_and_b32_e32 v97, 0xffff0000, v97
	v_and_b32_e32 v101, 0xffff0000, v98
	v_lshlrev_b32_e32 v98, 16, v99
	v_and_b32_e32 v99, 0xffff0000, v99
	v_pk_fma_f32 v[92:93], v[92:93], v[96:97], v[98:99]
	v_pk_fma_f32 v[90:91], v[90:91], v[94:95], v[100:101]
	s_nop 0
	v_cvt_pk_bf16_f32 v90, v90, v91
	v_cvt_pk_bf16_f32 v91, v92, v93
	v_mov_b32_e32 v92, v216
	v_mov_b32_e32 v93, v217
	v_mov_b32_e32 v94, v218
	v_mov_b32_e32 v95, v219
	s_nop 0
	v_lshlrev_b32_e32 v96, 16, v94
	global_store_dwordx2 v[102:103], v[90:91], off offset:32
	v_lshlrev_b32_e32 v90, 16, v92
	v_and_b32_e32 v91, 0xffff0000, v92
	v_lshlrev_b32_e32 v92, 16, v93
	v_and_b32_e32 v93, 0xffff0000, v93
	v_and_b32_e32 v97, 0xffff0000, v94
	v_lshlrev_b32_e32 v94, 16, v95
	v_and_b32_e32 v95, 0xffff0000, v95
	v_pk_fma_f32 v[88:89], v[88:89], v[92:93], v[94:95]
	v_pk_fma_f32 v[86:87], v[86:87], v[90:91], v[96:97]
	v_or_b32_e32 v92, 48, v144
	v_cvt_pk_bf16_f32 v86, v86, v87
	v_cvt_pk_bf16_f32 v87, v88, v89
	v_mov_b32_e32 v88, v220
	v_mov_b32_e32 v89, v221
	v_mov_b32_e32 v90, v222
	v_mov_b32_e32 v91, v223
	v_ashrrev_i32_e32 v93, 31, v92
	v_mad_i64_i32 v[94:95], s[24:25], v92, s50, v[146:147]
	global_store_dwordx2 v[102:103], v[86:87], off offset:256
	v_lshl_add_u64 v[94:95], v[94:95], 0, v[142:143]
	v_add_co_u32_e32 v96, vcc, s51, v94
	s_nop 0
	v_lshlrev_b32_e32 v86, 16, v88
	v_and_b32_e32 v87, 0xffff0000, v88
	v_lshlrev_b32_e32 v98, 16, v90
	v_and_b32_e32 v99, 0xffff0000, v90
	v_pk_fma_f32 v[82:83], v[82:83], v[86:87], v[98:99]
	v_lshlrev_b64 v[86:87], 12, v[92:93]
	v_lshlrev_b32_e32 v88, 16, v89
	v_and_b32_e32 v89, 0xffff0000, v89
	v_lshlrev_b32_e32 v90, 16, v91
	v_and_b32_e32 v91, 0xffff0000, v91
	v_lshl_add_u64 v[86:87], s[10:11], 0, v[86:87]
	v_addc_co_u32_e32 v97, vcc, 0, v95, vcc
	v_pk_fma_f32 v[84:85], v[84:85], v[88:89], v[90:91]
	v_lshl_add_u64 v[86:87], v[86:87], 0, v[142:143]
	v_cvt_pk_bf16_f32 v82, v82, v83
	v_cvt_pk_bf16_f32 v83, v84, v85
	v_mov_b32_e32 v237, 0x1000
	v_mov_b32_e32 v236, 48
	v_mad_i64_i32 v[230:231], s[24:25], v236, s50, v[228:229]
	v_mad_i64_i32 v[234:235], s[24:25], v236, v237, v[232:233]
	global_load_dwordx2 v[174:175], v[230:231], off
	global_load_dwordx2 v[176:177], v[234:235], off
	global_load_dwordx2 v[178:179], v[230:231], off offset:32
	global_load_dwordx2 v[180:181], v[234:235], off offset:32
	global_load_dwordx2 v[182:183], v[230:231], off offset:256
	global_load_dwordx2 v[184:185], v[234:235], off offset:256
	global_load_dwordx2 v[186:187], v[230:231], off offset:288
	global_load_dwordx2 v[188:189], v[234:235], off offset:288
	v_mov_b32_e32 v236, 128
	v_mad_i64_i32 v[230:231], s[24:25], v236, s50, v[228:229]
	v_mad_i64_i32 v[234:235], s[24:25], v236, v237, v[232:233]
	global_load_dwordx2 v[192:193], v[230:231], off
	global_load_dwordx2 v[194:195], v[234:235], off
	global_load_dwordx2 v[196:197], v[230:231], off offset:32
	global_load_dwordx2 v[198:199], v[234:235], off offset:32
	global_load_dwordx2 v[200:201], v[230:231], off offset:256
	global_load_dwordx2 v[202:203], v[234:235], off offset:256
	global_load_dwordx2 v[204:205], v[230:231], off offset:288
	global_load_dwordx2 v[206:207], v[234:235], off offset:288
	v_mov_b32_e32 v236, 144
	v_mad_i64_i32 v[230:231], s[24:25], v236, s50, v[228:229]
	v_mad_i64_i32 v[234:235], s[24:25], v236, v237, v[232:233]
	global_load_dwordx2 v[208:209], v[230:231], off
	global_load_dwordx2 v[210:211], v[234:235], off
	global_load_dwordx2 v[212:213], v[230:231], off offset:32
	global_load_dwordx2 v[214:215], v[234:235], off offset:32
	global_load_dwordx2 v[216:217], v[230:231], off offset:256
	global_load_dwordx2 v[218:219], v[234:235], off offset:256
	global_load_dwordx2 v[220:221], v[230:231], off offset:288
	global_load_dwordx2 v[222:223], v[234:235], off offset:288
	s_waitcnt vmcnt(0)
	v_mov_b32_e32 v84, v174
	v_mov_b32_e32 v85, v175
	v_mov_b32_e32 v88, v176
	v_mov_b32_e32 v89, v177
	v_lshl_add_u64 v[90:91], v[94:95], 0, s[12:13]
	global_store_dwordx2 v[102:103], v[82:83], off offset:288
	s_nop 0
	v_lshlrev_b32_e32 v82, 16, v84
	v_and_b32_e32 v83, 0xffff0000, v84
	v_lshlrev_b32_e32 v84, 16, v85
	v_and_b32_e32 v85, 0xffff0000, v85
	v_lshlrev_b32_e32 v92, 16, v88
	v_and_b32_e32 v93, 0xffff0000, v88
	v_lshlrev_b32_e32 v88, 16, v89
	v_and_b32_e32 v89, 0xffff0000, v89
	v_pk_fma_f32 v[80:81], v[80:81], v[84:85], v[88:89]
	v_pk_fma_f32 v[78:79], v[78:79], v[82:83], v[92:93]
	s_nop 0
	v_cvt_pk_bf16_f32 v78, v78, v79
	v_cvt_pk_bf16_f32 v79, v80, v81
	v_mov_b32_e32 v80, v178
	v_mov_b32_e32 v81, v179
	v_mov_b32_e32 v82, v180
	v_mov_b32_e32 v83, v181
	s_nop 0
	v_lshlrev_b32_e32 v84, 16, v82
	global_store_dwordx2 v[86:87], v[78:79], off
	v_lshlrev_b32_e32 v78, 16, v80
	v_and_b32_e32 v79, 0xffff0000, v80
	v_lshlrev_b32_e32 v80, 16, v81
	v_and_b32_e32 v81, 0xffff0000, v81
	v_and_b32_e32 v85, 0xffff0000, v82
	v_lshlrev_b32_e32 v82, 16, v83
	v_and_b32_e32 v83, 0xffff0000, v83
	v_pk_fma_f32 v[76:77], v[76:77], v[80:81], v[82:83]
	v_pk_fma_f32 v[74:75], v[74:75], v[78:79], v[84:85]
	s_nop 0
	v_cvt_pk_bf16_f32 v74, v74, v75
	v_cvt_pk_bf16_f32 v75, v76, v77
	v_mov_b32_e32 v76, v182
	v_mov_b32_e32 v77, v183
	v_mov_b32_e32 v78, v184
	v_mov_b32_e32 v79, v185
	s_nop 0
	v_lshlrev_b32_e32 v80, 16, v78
	global_store_dwordx2 v[86:87], v[74:75], off offset:32
	v_lshlrev_b32_e32 v74, 16, v76
	v_and_b32_e32 v75, 0xffff0000, v76
	v_lshlrev_b32_e32 v76, 16, v77
	v_and_b32_e32 v77, 0xffff0000, v77
	v_and_b32_e32 v81, 0xffff0000, v78
	v_lshlrev_b32_e32 v78, 16, v79
	v_and_b32_e32 v79, 0xffff0000, v79
	v_pk_fma_f32 v[72:73], v[72:73], v[76:77], v[78:79]
	v_pk_fma_f32 v[70:71], v[70:71], v[74:75], v[80:81]
	v_add_u32_e32 v76, 0x80, v144
	v_cvt_pk_bf16_f32 v70, v70, v71
	v_cvt_pk_bf16_f32 v71, v72, v73
	v_mov_b32_e32 v72, v186
	v_mov_b32_e32 v73, v187
	v_mov_b32_e32 v74, v188
	v_mov_b32_e32 v75, v189
	v_ashrrev_i32_e32 v77, 31, v76
	v_mad_i64_i32 v[78:79], s[24:25], v76, s50, v[146:147]
	global_store_dwordx2 v[86:87], v[70:71], off offset:256
	v_lshl_add_u64 v[78:79], v[78:79], 0, v[142:143]
	v_add_co_u32_e32 v80, vcc, s51, v78
	s_nop 0
	v_lshlrev_b32_e32 v70, 16, v72
	v_and_b32_e32 v71, 0xffff0000, v72
	v_lshlrev_b32_e32 v82, 16, v74
	v_and_b32_e32 v83, 0xffff0000, v74
	v_pk_fma_f32 v[66:67], v[66:67], v[70:71], v[82:83]
	v_lshlrev_b64 v[70:71], 12, v[76:77]
	v_lshlrev_b32_e32 v72, 16, v73
	v_and_b32_e32 v73, 0xffff0000, v73
	v_lshlrev_b32_e32 v74, 16, v75
	v_and_b32_e32 v75, 0xffff0000, v75
	v_lshl_add_u64 v[70:71], s[10:11], 0, v[70:71]
	v_addc_co_u32_e32 v81, vcc, 0, v79, vcc
	v_pk_fma_f32 v[68:69], v[68:69], v[72:73], v[74:75]
	v_lshl_add_u64 v[70:71], v[70:71], 0, v[142:143]
	v_cvt_pk_bf16_f32 v66, v66, v67
	v_cvt_pk_bf16_f32 v67, v68, v69
	v_mov_b32_e32 v68, v192
	v_mov_b32_e32 v69, v193
	v_mov_b32_e32 v72, v194
	v_mov_b32_e32 v73, v195
	v_lshl_add_u64 v[74:75], v[78:79], 0, s[12:13]
	global_store_dwordx2 v[86:87], v[66:67], off offset:288
	s_nop 0
	v_lshlrev_b32_e32 v66, 16, v68
	v_and_b32_e32 v67, 0xffff0000, v68
	v_lshlrev_b32_e32 v68, 16, v69
	v_and_b32_e32 v69, 0xffff0000, v69
	v_lshlrev_b32_e32 v76, 16, v72
	v_and_b32_e32 v77, 0xffff0000, v72
	v_lshlrev_b32_e32 v72, 16, v73
	v_and_b32_e32 v73, 0xffff0000, v73
	v_pk_fma_f32 v[64:65], v[64:65], v[68:69], v[72:73]
	v_pk_fma_f32 v[62:63], v[62:63], v[66:67], v[76:77]
	s_nop 0
	v_cvt_pk_bf16_f32 v62, v62, v63
	v_cvt_pk_bf16_f32 v63, v64, v65
	v_mov_b32_e32 v64, v196
	v_mov_b32_e32 v65, v197
	v_mov_b32_e32 v66, v198
	v_mov_b32_e32 v67, v199
	s_nop 0
	v_lshlrev_b32_e32 v68, 16, v66
	global_store_dwordx2 v[70:71], v[62:63], off
	v_lshlrev_b32_e32 v62, 16, v64
	v_and_b32_e32 v63, 0xffff0000, v64
	v_lshlrev_b32_e32 v64, 16, v65
	v_and_b32_e32 v65, 0xffff0000, v65
	v_and_b32_e32 v69, 0xffff0000, v66
	v_lshlrev_b32_e32 v66, 16, v67
	v_and_b32_e32 v67, 0xffff0000, v67
	v_pk_fma_f32 v[60:61], v[60:61], v[64:65], v[66:67]
	v_pk_fma_f32 v[58:59], v[58:59], v[62:63], v[68:69]
	s_nop 0
	v_cvt_pk_bf16_f32 v58, v58, v59
	v_cvt_pk_bf16_f32 v59, v60, v61
	v_mov_b32_e32 v60, v200
	v_mov_b32_e32 v61, v201
	v_mov_b32_e32 v62, v202
	v_mov_b32_e32 v63, v203
	s_nop 0
	v_lshlrev_b32_e32 v64, 16, v62
	global_store_dwordx2 v[70:71], v[58:59], off offset:32
	v_lshlrev_b32_e32 v58, 16, v60
	v_and_b32_e32 v59, 0xffff0000, v60
	v_lshlrev_b32_e32 v60, 16, v61
	v_and_b32_e32 v61, 0xffff0000, v61
	v_and_b32_e32 v65, 0xffff0000, v62
	v_lshlrev_b32_e32 v62, 16, v63
	v_and_b32_e32 v63, 0xffff0000, v63
	v_pk_fma_f32 v[56:57], v[56:57], v[60:61], v[62:63]
	v_pk_fma_f32 v[54:55], v[54:55], v[58:59], v[64:65]
	v_add_u32_e32 v60, 0x90, v144
	v_cvt_pk_bf16_f32 v54, v54, v55
	v_cvt_pk_bf16_f32 v55, v56, v57
	v_mov_b32_e32 v56, v204
	v_mov_b32_e32 v57, v205
	v_mov_b32_e32 v58, v206
	v_mov_b32_e32 v59, v207
	v_ashrrev_i32_e32 v61, 31, v60
	v_mad_i64_i32 v[62:63], s[24:25], v60, s50, v[146:147]
	global_store_dwordx2 v[70:71], v[54:55], off offset:256
	v_lshl_add_u64 v[62:63], v[62:63], 0, v[142:143]
	v_add_co_u32_e32 v64, vcc, s51, v62
	s_nop 0
	v_lshlrev_b32_e32 v54, 16, v56
	v_and_b32_e32 v55, 0xffff0000, v56
	v_lshlrev_b32_e32 v66, 16, v58
	v_and_b32_e32 v67, 0xffff0000, v58
	v_pk_fma_f32 v[50:51], v[50:51], v[54:55], v[66:67]
	v_lshlrev_b64 v[54:55], 12, v[60:61]
	v_lshlrev_b32_e32 v56, 16, v57
	v_and_b32_e32 v57, 0xffff0000, v57
	v_lshlrev_b32_e32 v58, 16, v59
	v_and_b32_e32 v59, 0xffff0000, v59
	v_lshl_add_u64 v[54:55], s[10:11], 0, v[54:55]
	v_addc_co_u32_e32 v65, vcc, 0, v63, vcc
	v_pk_fma_f32 v[52:53], v[52:53], v[56:57], v[58:59]
	v_lshl_add_u64 v[54:55], v[54:55], 0, v[142:143]
	v_cvt_pk_bf16_f32 v50, v50, v51
	v_cvt_pk_bf16_f32 v51, v52, v53
	v_mov_b32_e32 v52, v208
	v_mov_b32_e32 v53, v209
	v_mov_b32_e32 v56, v210
	v_mov_b32_e32 v57, v211
	v_lshl_add_u64 v[58:59], v[62:63], 0, s[12:13]
	global_store_dwordx2 v[70:71], v[50:51], off offset:288
	s_nop 0
	v_lshlrev_b32_e32 v50, 16, v52
	v_and_b32_e32 v51, 0xffff0000, v52
	v_lshlrev_b32_e32 v52, 16, v53
	v_and_b32_e32 v53, 0xffff0000, v53
	v_lshlrev_b32_e32 v60, 16, v56
	v_and_b32_e32 v61, 0xffff0000, v56
	v_lshlrev_b32_e32 v56, 16, v57
	v_and_b32_e32 v57, 0xffff0000, v57
	v_pk_fma_f32 v[48:49], v[48:49], v[52:53], v[56:57]
	v_pk_fma_f32 v[46:47], v[46:47], v[50:51], v[60:61]
	s_nop 0
	v_cvt_pk_bf16_f32 v46, v46, v47
	v_cvt_pk_bf16_f32 v47, v48, v49
	v_mov_b32_e32 v48, v212
	v_mov_b32_e32 v49, v213
	v_mov_b32_e32 v50, v214
	v_mov_b32_e32 v51, v215
	s_nop 0
	v_lshlrev_b32_e32 v52, 16, v50
	global_store_dwordx2 v[54:55], v[46:47], off
	v_lshlrev_b32_e32 v46, 16, v48
	v_and_b32_e32 v47, 0xffff0000, v48
	v_lshlrev_b32_e32 v48, 16, v49
	v_and_b32_e32 v49, 0xffff0000, v49
	v_and_b32_e32 v53, 0xffff0000, v50
	v_lshlrev_b32_e32 v50, 16, v51
	v_and_b32_e32 v51, 0xffff0000, v51
	v_pk_fma_f32 v[44:45], v[44:45], v[48:49], v[50:51]
	v_pk_fma_f32 v[42:43], v[42:43], v[46:47], v[52:53]
	s_nop 0
	v_cvt_pk_bf16_f32 v42, v42, v43
	v_cvt_pk_bf16_f32 v43, v44, v45
	v_mov_b32_e32 v44, v216
	v_mov_b32_e32 v45, v217
	v_mov_b32_e32 v46, v218
	v_mov_b32_e32 v47, v219
	s_nop 0
	v_lshlrev_b32_e32 v48, 16, v46
	global_store_dwordx2 v[54:55], v[42:43], off offset:32
	v_lshlrev_b32_e32 v42, 16, v44
	v_and_b32_e32 v43, 0xffff0000, v44
	v_lshlrev_b32_e32 v44, 16, v45
	v_and_b32_e32 v45, 0xffff0000, v45
	v_and_b32_e32 v49, 0xffff0000, v46
	v_lshlrev_b32_e32 v46, 16, v47
	v_and_b32_e32 v47, 0xffff0000, v47
	v_pk_fma_f32 v[40:41], v[40:41], v[44:45], v[46:47]
	v_pk_fma_f32 v[38:39], v[38:39], v[42:43], v[48:49]
	v_add_u32_e32 v44, 0xa0, v144
	v_cvt_pk_bf16_f32 v38, v38, v39
	v_cvt_pk_bf16_f32 v39, v40, v41
	v_mov_b32_e32 v40, v220
	v_mov_b32_e32 v41, v221
	v_mov_b32_e32 v42, v222
	v_mov_b32_e32 v43, v223
	v_ashrrev_i32_e32 v45, 31, v44
	v_mad_i64_i32 v[46:47], s[24:25], v44, s50, v[146:147]
	global_store_dwordx2 v[54:55], v[38:39], off offset:256
	v_lshl_add_u64 v[46:47], v[46:47], 0, v[142:143]
	v_add_co_u32_e32 v48, vcc, s51, v46
	s_nop 0
	v_lshlrev_b32_e32 v38, 16, v40
	v_and_b32_e32 v39, 0xffff0000, v40
	v_lshlrev_b32_e32 v50, 16, v42
	v_and_b32_e32 v51, 0xffff0000, v42
	v_pk_fma_f32 v[34:35], v[34:35], v[38:39], v[50:51]
	v_lshlrev_b64 v[38:39], 12, v[44:45]
	v_lshlrev_b32_e32 v40, 16, v41
	v_and_b32_e32 v41, 0xffff0000, v41
	v_lshlrev_b32_e32 v42, 16, v43
	v_and_b32_e32 v43, 0xffff0000, v43
	v_lshl_add_u64 v[38:39], s[10:11], 0, v[38:39]
	v_addc_co_u32_e32 v49, vcc, 0, v47, vcc
	v_pk_fma_f32 v[36:37], v[36:37], v[40:41], v[42:43]
	v_lshl_add_u64 v[38:39], v[38:39], 0, v[142:143]
	v_cvt_pk_bf16_f32 v34, v34, v35
	v_cvt_pk_bf16_f32 v35, v36, v37
	v_mov_b32_e32 v237, 0x1000
	v_mov_b32_e32 v236, 160
	v_mad_i64_i32 v[230:231], s[24:25], v236, s50, v[228:229]
	v_mad_i64_i32 v[234:235], s[24:25], v236, v237, v[232:233]
	global_load_dwordx2 v[174:175], v[230:231], off
	global_load_dwordx2 v[176:177], v[234:235], off
	global_load_dwordx2 v[178:179], v[230:231], off offset:32
	global_load_dwordx2 v[180:181], v[234:235], off offset:32
	global_load_dwordx2 v[182:183], v[230:231], off offset:256
	global_load_dwordx2 v[184:185], v[234:235], off offset:256
	global_load_dwordx2 v[186:187], v[230:231], off offset:288
	global_load_dwordx2 v[188:189], v[234:235], off offset:288
	v_mov_b32_e32 v236, 176
	v_mad_i64_i32 v[230:231], s[24:25], v236, s50, v[228:229]
	v_mad_i64_i32 v[234:235], s[24:25], v236, v237, v[232:233]
	global_load_dwordx2 v[192:193], v[230:231], off
	global_load_dwordx2 v[194:195], v[234:235], off
	global_load_dwordx2 v[196:197], v[230:231], off offset:32
	global_load_dwordx2 v[198:199], v[234:235], off offset:32
	global_load_dwordx2 v[200:201], v[230:231], off offset:256
	global_load_dwordx2 v[202:203], v[234:235], off offset:256
	global_load_dwordx2 v[204:205], v[230:231], off offset:288
	global_load_dwordx2 v[206:207], v[234:235], off offset:288
	s_waitcnt vmcnt(0)
	v_mov_b32_e32 v36, v174
	v_mov_b32_e32 v37, v175
	v_mov_b32_e32 v40, v176
	v_mov_b32_e32 v41, v177
	v_lshl_add_u64 v[42:43], v[46:47], 0, s[12:13]
	global_store_dwordx2 v[54:55], v[34:35], off offset:288
	s_nop 0
	v_lshlrev_b32_e32 v34, 16, v36
	v_and_b32_e32 v35, 0xffff0000, v36
	v_lshlrev_b32_e32 v36, 16, v37
	v_and_b32_e32 v37, 0xffff0000, v37
	v_lshlrev_b32_e32 v44, 16, v40
	v_and_b32_e32 v45, 0xffff0000, v40
	v_lshlrev_b32_e32 v40, 16, v41
	v_and_b32_e32 v41, 0xffff0000, v41
	v_pk_fma_f32 v[32:33], v[32:33], v[36:37], v[40:41]
	v_pk_fma_f32 v[30:31], v[30:31], v[34:35], v[44:45]
	s_nop 0
	v_cvt_pk_bf16_f32 v30, v30, v31
	v_cvt_pk_bf16_f32 v31, v32, v33
	v_mov_b32_e32 v32, v178
	v_mov_b32_e32 v33, v179
	v_mov_b32_e32 v34, v180
	v_mov_b32_e32 v35, v181
	s_nop 0
	v_lshlrev_b32_e32 v36, 16, v34
	global_store_dwordx2 v[38:39], v[30:31], off
	v_lshlrev_b32_e32 v30, 16, v32
	v_and_b32_e32 v31, 0xffff0000, v32
	v_lshlrev_b32_e32 v32, 16, v33
	v_and_b32_e32 v33, 0xffff0000, v33
	v_and_b32_e32 v37, 0xffff0000, v34
	v_lshlrev_b32_e32 v34, 16, v35
	v_and_b32_e32 v35, 0xffff0000, v35
	v_pk_fma_f32 v[28:29], v[28:29], v[32:33], v[34:35]
	v_pk_fma_f32 v[26:27], v[26:27], v[30:31], v[36:37]
	s_nop 0
	v_cvt_pk_bf16_f32 v26, v26, v27
	v_cvt_pk_bf16_f32 v27, v28, v29
	v_mov_b32_e32 v28, v182
	v_mov_b32_e32 v29, v183
	v_mov_b32_e32 v30, v184
	v_mov_b32_e32 v31, v185
	s_nop 0
	v_lshlrev_b32_e32 v32, 16, v30
	global_store_dwordx2 v[38:39], v[26:27], off offset:32
	v_lshlrev_b32_e32 v26, 16, v28
	v_and_b32_e32 v27, 0xffff0000, v28
	v_lshlrev_b32_e32 v28, 16, v29
	v_and_b32_e32 v29, 0xffff0000, v29
	v_and_b32_e32 v33, 0xffff0000, v30
	v_lshlrev_b32_e32 v30, 16, v31
	v_and_b32_e32 v31, 0xffff0000, v31
	v_pk_fma_f32 v[24:25], v[24:25], v[28:29], v[30:31]
	v_pk_fma_f32 v[22:23], v[22:23], v[26:27], v[32:33]
	v_add_u32_e32 v28, 0xb0, v144
	v_cvt_pk_bf16_f32 v22, v22, v23
	v_cvt_pk_bf16_f32 v23, v24, v25
	v_mov_b32_e32 v24, v186
	v_mov_b32_e32 v25, v187
	v_mov_b32_e32 v26, v188
	v_mov_b32_e32 v27, v189
	v_ashrrev_i32_e32 v29, 31, v28
	v_mad_i64_i32 v[30:31], s[24:25], v28, s50, v[146:147]
	global_store_dwordx2 v[38:39], v[22:23], off offset:256
	v_lshl_add_u64 v[30:31], v[30:31], 0, v[142:143]
	v_add_co_u32_e32 v32, vcc, s51, v30
	s_mov_b64 s[24:25], s[18:19]
	s_nop 0
	v_addc_co_u32_e32 v33, vcc, 0, v31, vcc
	s_and_b64 vcc, exec, s[2:3]
	s_nop 0
	v_lshlrev_b32_e32 v22, 16, v24
	v_and_b32_e32 v23, 0xffff0000, v24
	v_lshlrev_b32_e32 v34, 16, v26
	v_and_b32_e32 v35, 0xffff0000, v26
	v_pk_fma_f32 v[18:19], v[18:19], v[22:23], v[34:35]
	v_lshlrev_b64 v[22:23], 12, v[28:29]
	v_lshlrev_b32_e32 v24, 16, v25
	v_and_b32_e32 v25, 0xffff0000, v25
	v_lshlrev_b32_e32 v26, 16, v27
	v_and_b32_e32 v27, 0xffff0000, v27
	v_lshl_add_u64 v[22:23], s[10:11], 0, v[22:23]
	v_pk_fma_f32 v[20:21], v[20:21], v[24:25], v[26:27]
	v_lshl_add_u64 v[22:23], v[22:23], 0, v[142:143]
	v_cvt_pk_bf16_f32 v18, v18, v19
	v_cvt_pk_bf16_f32 v19, v20, v21
	v_mov_b32_e32 v20, v192
	v_mov_b32_e32 v21, v193
	v_mov_b32_e32 v24, v194
	v_mov_b32_e32 v25, v195
	v_lshl_add_u64 v[26:27], v[30:31], 0, s[12:13]
	global_store_dwordx2 v[38:39], v[18:19], off offset:288
	s_nop 0
	v_lshlrev_b32_e32 v18, 16, v20
	v_and_b32_e32 v19, 0xffff0000, v20
	v_lshlrev_b32_e32 v20, 16, v21
	v_and_b32_e32 v21, 0xffff0000, v21
	v_lshlrev_b32_e32 v28, 16, v24
	v_and_b32_e32 v29, 0xffff0000, v24
	v_lshlrev_b32_e32 v24, 16, v25
	v_and_b32_e32 v25, 0xffff0000, v25
	v_pk_fma_f32 v[16:17], v[16:17], v[20:21], v[24:25]
	v_pk_fma_f32 v[14:15], v[14:15], v[18:19], v[28:29]
	s_nop 0
	v_cvt_pk_bf16_f32 v14, v14, v15
	v_cvt_pk_bf16_f32 v15, v16, v17
	v_mov_b32_e32 v16, v196
	v_mov_b32_e32 v17, v197
	v_mov_b32_e32 v18, v198
	v_mov_b32_e32 v19, v199
	s_nop 0
	v_lshlrev_b32_e32 v20, 16, v18
	global_store_dwordx2 v[22:23], v[14:15], off
	v_lshlrev_b32_e32 v14, 16, v16
	v_and_b32_e32 v15, 0xffff0000, v16
	v_lshlrev_b32_e32 v16, 16, v17
	v_and_b32_e32 v17, 0xffff0000, v17
	v_and_b32_e32 v21, 0xffff0000, v18
	v_lshlrev_b32_e32 v18, 16, v19
	v_and_b32_e32 v19, 0xffff0000, v19
	v_pk_fma_f32 v[12:13], v[12:13], v[16:17], v[18:19]
	v_pk_fma_f32 v[10:11], v[10:11], v[14:15], v[20:21]
	s_nop 0
	v_cvt_pk_bf16_f32 v10, v10, v11
	v_cvt_pk_bf16_f32 v11, v12, v13
	v_mov_b32_e32 v12, v200
	v_mov_b32_e32 v13, v201
	v_mov_b32_e32 v14, v202
	v_mov_b32_e32 v15, v203
	s_nop 0
	v_lshlrev_b32_e32 v16, 16, v14
	global_store_dwordx2 v[22:23], v[10:11], off offset:32
	v_lshlrev_b32_e32 v10, 16, v12
	v_and_b32_e32 v11, 0xffff0000, v12
	v_lshlrev_b32_e32 v12, 16, v13
	v_and_b32_e32 v13, 0xffff0000, v13
	v_and_b32_e32 v17, 0xffff0000, v14
	v_lshlrev_b32_e32 v14, 16, v15
	v_and_b32_e32 v15, 0xffff0000, v15
	v_pk_fma_f32 v[8:9], v[8:9], v[12:13], v[14:15]
	v_pk_fma_f32 v[6:7], v[6:7], v[10:11], v[16:17]
	s_nop 0
	v_cvt_pk_bf16_f32 v6, v6, v7
	v_cvt_pk_bf16_f32 v7, v8, v9
	v_mov_b32_e32 v8, v204
	v_mov_b32_e32 v9, v205
	v_mov_b32_e32 v10, v206
	v_mov_b32_e32 v11, v207
	s_nop 0
	v_lshlrev_b32_e32 v12, 16, v10
	global_store_dwordx2 v[22:23], v[6:7], off offset:256
	v_lshlrev_b32_e32 v6, 16, v8
	v_and_b32_e32 v7, 0xffff0000, v8
	v_and_b32_e32 v13, 0xffff0000, v10
	v_lshlrev_b32_e32 v8, 16, v9
	v_and_b32_e32 v9, 0xffff0000, v9
	v_lshlrev_b32_e32 v10, 16, v11
	v_and_b32_e32 v11, 0xffff0000, v11
	v_pk_fma_f32 v[2:3], v[2:3], v[6:7], v[12:13]
	v_pk_fma_f32 v[4:5], v[4:5], v[8:9], v[10:11]
	v_cvt_pk_bf16_f32 v2, v2, v3
	s_nop 0
	v_cvt_pk_bf16_f32 v3, v4, v5
	global_store_dwordx2 v[22:23], v[2:3], off offset:288
	s_cbranch_vccz .LBB0_1208
	s_waitcnt vmcnt(0)
	v_readlane_b32 s52, v250, 40
	s_cmpk_gt_u32 s33, 0xff
	v_readlane_b32 s53, v250, 41
	v_readlane_b32 s54, v250, 42
	v_readlane_b32 s55, v250, 43
	s_cbranch_scc1 .LBB0_1215
	s_barrier

.LBB0_1216:
	s_and_b64 vcc, exec, s[0:1]
	v_readfirstlane_b32 s28, v0
	s_cbranch_vccnz .LBB0_1228
	s_add_u32 s29, s6, 0x50480000
	s_addc_u32 s33, s7, 0
	s_add_u32 s34, s6, 0x15d40000
	s_addc_u32 s35, s7, 0
	s_ashr_i32 s37, s31, 31
	s_lshr_b32 s0, s37, 29
	s_add_i32 s0, s31, s0
	s_lshr_b32 s2, s28, 6
	s_ashr_i32 s3, s0, 3
	s_and_b32 s0, s0, -8
	s_lshr_b32 s1, s28, 8
	s_lshl_b32 s36, s2, 10
	s_sub_i32 s0, s31, s0
	s_cmp_lt_i32 s0, 0
	s_movk_i32 s38, 0x42
	s_cselect_b32 s8, s38, 0x41
	s_mul_i32 s0, s8, s0
	s_add_i32 s0, s0, s3
	s_ashr_i32 s3, s0, 31
	s_lshr_b32 s3, s3, 26
	s_add_i32 s3, s0, s3
	s_ashr_i32 s8, s3, 6
	s_lshl_b32 s10, s8, 3
	s_sub_i32 s8, 0x41, s10
	s_min_u32 s11, s8, 8
	s_andn2_b32 s3, s3, 63
	s_sub_i32 s3, s0, s3
	v_cvt_f32_ubyte0_e32 v3, s11
	v_cvt_f32_i32_e32 v2, s3
	v_rcp_iflag_f32_e32 v4, v3
	s_ashr_i32 s0, s3, 30
	s_or_b32 s0, s0, 1
	v_mov_b32_e32 v131, 0
	v_mul_f32_e32 v4, v2, v4
	v_trunc_f32_e32 v4, v4
	v_fma_f32 v2, -v4, v3, v2
	v_cvt_i32_f32_e32 v4, v4
	v_cmp_ge_f32_e64 s[8:9], |v2|, v3
	s_and_b64 s[8:9], s[8:9], exec
	s_cselect_b32 s0, s0, 0
	v_readfirstlane_b32 s8, v4
	s_add_i32 s0, s8, s0
	s_mul_i32 s8, s0, s11
	s_sub_i32 s3, s3, s8
	s_sext_i32_i8 s3, s3
	s_add_i32 s20, s10, s3
	s_ashr_i32 s21, s20, 31
	s_lshl_b64 s[8:9], s[20:21], 19
	s_add_u32 s22, s29, s8
	s_addc_u32 s23, s33, s9
	s_bfe_i64 s[8:9], s[0:1], 0x80000
	s_lshl_b64 s[8:9], s[8:9], 19
	s_add_u32 s24, s34, s8
	s_addc_u32 s25, s35, s9
	s_add_i32 s21, s36, 0
	s_add_i32 m0, s21, 0x10000
	s_add_i32 s39, s21, 0x2000
	global_load_lds_dwordx4 v130, s[24:25]
	s_add_i32 m0, s21, 0x12000
	s_add_u32 s8, s24, 0x40000
	global_load_lds_dwordx4 v132, s[24:25]
	s_mov_b32 m0, s21
	s_addc_u32 s9, s25, 0
	global_load_lds_dwordx4 v130, s[22:23]
	s_mov_b32 m0, s39
	v_mov_b32_e32 v133, v131
	global_load_lds_dwordx4 v132, s[22:23]
	s_add_i32 m0, s21, 0x14000
	s_mov_b32 s42, 0
	global_load_lds_dwordx4 v130, s[8:9]
	s_add_i32 m0, s21, 0x16000
	s_waitcnt vmcnt(0)
	v_lshl_add_u64 v[8:9], s[24:25], 0, v[130:131]
	global_load_lds_dwordx4 v132, s[8:9]
	s_add_u32 s8, s22, 0x40000
	s_addc_u32 s9, s23, 0
	s_add_i32 s40, s21, 0x4000
	s_mov_b32 m0, s40
	s_add_i32 s41, s21, 0x6000
	global_load_lds_dwordx4 v130, s[8:9]
	s_mov_b32 m0, s41
	v_lshl_add_u64 v[6:7], s[24:25], 0, v[132:133]
	global_load_lds_dwordx4 v132, s[8:9]
	v_lshl_add_u64 v[4:5], s[22:23], 0, v[130:131]
	s_setprio 1
	s_cmp_lg_u32 s1, 1
	v_lshl_add_u64 v[2:3], s[22:23], 0, v[132:133]
	s_cbranch_scc1 .LBB0_1219
	s_barrier
	s_setprio 0

.LBB0_1223:
	ds_read_b128 v[142:145], v1
	ds_read_b128 v[156:159], v1 offset:1024
	ds_read_b128 v[160:163], v1 offset:2048
	ds_read_b128 v[164:167], v1 offset:3072
	s_add_u32 s24, s22, 0xfffc0080
	s_addc_u32 s25, s23, -1
	s_cmp_eq_u32 s55, 12
	s_cselect_b32 s27, s15, s25
	s_cselect_b32 s26, s51, s24
	s_cselect_b32 s25, s13, s54
	s_cselect_b32 s24, s52, s53
	v_lshl_add_u64 v[146:147], s[22:23], 0, v[134:135]
	s_add_i32 m0, s21, 0xc000
	ds_read_b128 v[168:171], v148
	ds_read_b128 v[172:175], v148 offset:1024
	ds_read_b128 v[176:179], v148 offset:2048
	ds_read_b128 v[180:183], v148 offset:3072
	ds_read_b128 v[184:187], v148 offset:4096
	ds_read_b128 v[192:195], v148 offset:5120
	ds_read_b128 v[196:199], v148 offset:6144
	ds_read_b128 v[200:203], v148 offset:7168
	global_load_lds_dwordx4 v[146:147], off
	v_lshl_add_u64 v[146:147], s[22:23], 0, v[136:137]
	s_add_i32 m0, s21, 0xe000
	s_nop 0
	global_load_lds_dwordx4 v[146:147], off
	s_waitcnt lgkmcnt(8)
	s_barrier
	s_waitcnt lgkmcnt(0)
	s_waitcnt lgkmcnt(0)
	v_mfma_f32_16x16x32_bf16 v[126:129], v[142:145], v[168:171], v[126:129]
	v_mfma_f32_16x16x32_bf16 v[122:125], v[160:163], v[168:171], v[122:125]
	v_mfma_f32_16x16x32_bf16 v[110:113], v[142:145], v[176:179], v[110:113]
	v_mfma_f32_16x16x32_bf16 v[106:109], v[160:163], v[176:179], v[106:109]
	v_mfma_f32_16x16x32_bf16 v[94:97], v[142:145], v[184:187], v[94:97]
	v_mfma_f32_16x16x32_bf16 v[90:93], v[160:163], v[184:187], v[90:93]
	v_mfma_f32_16x16x32_bf16 v[78:81], v[142:145], v[196:199], v[78:81]
	v_mfma_f32_16x16x32_bf16 v[74:77], v[160:163], v[196:199], v[74:77]
	v_mfma_f32_16x16x32_bf16 v[126:129], v[156:159], v[172:175], v[126:129]
	v_mfma_f32_16x16x32_bf16 v[122:125], v[164:167], v[172:175], v[122:125]
	v_mfma_f32_16x16x32_bf16 v[110:113], v[156:159], v[180:183], v[110:113]
	v_mfma_f32_16x16x32_bf16 v[106:109], v[164:167], v[180:183], v[106:109]
	v_mfma_f32_16x16x32_bf16 v[94:97], v[156:159], v[192:195], v[94:97]
	v_mfma_f32_16x16x32_bf16 v[90:93], v[164:167], v[192:195], v[90:93]
	v_mfma_f32_16x16x32_bf16 v[78:81], v[156:159], v[200:203], v[78:81]
	v_mfma_f32_16x16x32_bf16 v[74:77], v[164:167], v[200:203], v[74:77]
	s_barrier
	s_add_i32 s56, s46, s36
	v_lshl_add_u64 v[146:147], s[24:25], 0, v[130:131]
	s_mov_b32 m0, s56
	ds_read_b128 v[204:207], v149
	ds_read_b128 v[208:211], v149 offset:1024
	ds_read_b128 v[212:215], v149 offset:2048
	ds_read_b128 v[216:219], v149 offset:3072
	global_load_lds_dwordx4 v[146:147], off
	v_lshl_add_u64 v[188:189], s[24:25], 0, v[132:133]
	s_add_i32 m0, s56, 0x2000
	s_nop 0
	global_load_lds_dwordx4 v[188:189], off
	s_barrier
	s_waitcnt lgkmcnt(0)
	s_waitcnt lgkmcnt(0)
	v_mfma_f32_16x16x32_bf16 v[118:121], v[204:207], v[168:171], v[118:121]
	v_mfma_f32_16x16x32_bf16 v[114:117], v[212:215], v[168:171], v[114:117]
	v_mfma_f32_16x16x32_bf16 v[102:105], v[204:207], v[176:179], v[102:105]
	v_mfma_f32_16x16x32_bf16 v[98:101], v[212:215], v[176:179], v[98:101]
	v_mfma_f32_16x16x32_bf16 v[86:89], v[204:207], v[184:187], v[86:89]
	v_mfma_f32_16x16x32_bf16 v[82:85], v[212:215], v[184:187], v[82:85]
	v_mfma_f32_16x16x32_bf16 v[70:73], v[204:207], v[196:199], v[70:73]
	v_mfma_f32_16x16x32_bf16 v[66:69], v[212:215], v[196:199], v[66:69]
	v_mfma_f32_16x16x32_bf16 v[118:121], v[208:211], v[172:175], v[118:121]
	v_mfma_f32_16x16x32_bf16 v[114:117], v[216:219], v[172:175], v[114:117]
	v_mfma_f32_16x16x32_bf16 v[102:105], v[208:211], v[180:183], v[102:105]
	v_mfma_f32_16x16x32_bf16 v[98:101], v[216:219], v[180:183], v[98:101]
	v_mfma_f32_16x16x32_bf16 v[86:89], v[208:211], v[192:195], v[86:89]
	v_mfma_f32_16x16x32_bf16 v[82:85], v[216:219], v[192:195], v[82:85]
	v_mfma_f32_16x16x32_bf16 v[70:73], v[208:211], v[200:203], v[70:73]
	v_mfma_f32_16x16x32_bf16 v[66:69], v[216:219], v[200:203], v[66:69]
	s_mov_b32 m0, s21
	v_lshl_add_u64 v[190:191], s[26:27], 0, v[130:131]
	s_barrier
	ds_read_b128 v[168:171], v148 offset:16384
	ds_read_b128 v[172:175], v148 offset:17408
	ds_read_b128 v[176:179], v148 offset:18432
	ds_read_b128 v[180:183], v148 offset:19456
	ds_read_b128 v[184:187], v148 offset:20480
	ds_read_b128 v[192:195], v148 offset:21504
	ds_read_b128 v[196:199], v148 offset:22528
	ds_read_b128 v[200:203], v148 offset:23552
	global_load_lds_dwordx4 v[190:191], off
	v_lshl_add_u64 v[220:221], s[26:27], 0, v[132:133]
	s_mov_b32 m0, s39
	s_nop 0
	global_load_lds_dwordx4 v[220:221], off
	s_barrier
	s_waitcnt lgkmcnt(0)
	s_waitcnt lgkmcnt(0)
	v_mfma_f32_16x16x32_bf16 v[62:65], v[142:145], v[168:171], v[62:65]
	v_mfma_f32_16x16x32_bf16 v[58:61], v[160:163], v[168:171], v[58:61]
	v_mfma_f32_16x16x32_bf16 v[46:49], v[142:145], v[176:179], v[46:49]
	v_mfma_f32_16x16x32_bf16 v[42:45], v[160:163], v[176:179], v[42:45]
	v_mfma_f32_16x16x32_bf16 v[30:33], v[142:145], v[184:187], v[30:33]
	v_mfma_f32_16x16x32_bf16 v[26:29], v[160:163], v[184:187], v[26:29]
	v_mfma_f32_16x16x32_bf16 v[14:17], v[142:145], v[196:199], v[14:17]
	v_mfma_f32_16x16x32_bf16 v[10:13], v[160:163], v[196:199], v[10:13]
	v_mfma_f32_16x16x32_bf16 v[62:65], v[156:159], v[172:175], v[62:65]
	v_mfma_f32_16x16x32_bf16 v[58:61], v[164:167], v[172:175], v[58:61]
	v_mfma_f32_16x16x32_bf16 v[46:49], v[156:159], v[180:183], v[46:49]
	v_mfma_f32_16x16x32_bf16 v[42:45], v[164:167], v[180:183], v[42:45]
	v_mfma_f32_16x16x32_bf16 v[30:33], v[156:159], v[192:195], v[30:33]
	v_mfma_f32_16x16x32_bf16 v[26:29], v[164:167], v[192:195], v[26:29]
	v_mfma_f32_16x16x32_bf16 v[14:17], v[156:159], v[200:203], v[14:17]
	v_mfma_f32_16x16x32_bf16 v[10:13], v[164:167], v[200:203], v[10:13]
	s_barrier
	s_add_u32 s56, s24, 0x40000
	s_addc_u32 s57, s25, 0
	s_add_i32 s58, s47, s36
	v_lshl_add_u64 v[142:143], s[56:57], 0, v[130:131]
	s_mov_b32 m0, s58
	s_nop 0
	global_load_lds_dwordx4 v[142:143], off
	v_lshl_add_u64 v[142:143], s[56:57], 0, v[132:133]
	s_add_i32 m0, s58, 0x2000
	s_nop 0
	global_load_lds_dwordx4 v[142:143], off
	s_waitcnt vmcnt(6)
	s_barrier
	v_mfma_f32_16x16x32_bf16 v[54:57], v[204:207], v[168:171], v[54:57]
	v_mfma_f32_16x16x32_bf16 v[50:53], v[212:215], v[168:171], v[50:53]
	v_mfma_f32_16x16x32_bf16 v[38:41], v[204:207], v[176:179], v[38:41]
	v_mfma_f32_16x16x32_bf16 v[34:37], v[212:215], v[176:179], v[34:37]
	v_mfma_f32_16x16x32_bf16 v[22:25], v[204:207], v[184:187], v[22:25]
	v_mfma_f32_16x16x32_bf16 v[18:21], v[212:215], v[184:187], v[18:21]
	v_mfma_f32_16x16x32_bf16 v[6:9], v[204:207], v[196:199], v[6:9]
	v_mfma_f32_16x16x32_bf16 v[2:5], v[212:215], v[196:199], v[2:5]
	v_mfma_f32_16x16x32_bf16 v[54:57], v[208:211], v[172:175], v[54:57]
	v_mfma_f32_16x16x32_bf16 v[50:53], v[216:219], v[172:175], v[50:53]
	v_mfma_f32_16x16x32_bf16 v[38:41], v[208:211], v[180:183], v[38:41]
	v_mfma_f32_16x16x32_bf16 v[34:37], v[216:219], v[180:183], v[34:37]
	v_mfma_f32_16x16x32_bf16 v[22:25], v[208:211], v[192:195], v[22:25]
	v_mfma_f32_16x16x32_bf16 v[18:21], v[216:219], v[192:195], v[18:21]
	v_mfma_f32_16x16x32_bf16 v[6:9], v[208:211], v[200:203], v[6:9]
	v_mfma_f32_16x16x32_bf16 v[2:5], v[216:219], v[200:203], v[2:5]
	s_add_i32 s56, 0, 0x18000
	v_add_u32_e32 v150, s56, v152
	s_barrier
	ds_read_b128 v[142:145], v150
	ds_read_b128 v[156:159], v150 offset:1024
	ds_read_b128 v[160:163], v150 offset:2048
	ds_read_b128 v[164:167], v150 offset:3072
	s_add_u32 s26, s26, 0x40000
	s_addc_u32 s27, s27, 0
	s_mov_b32 m0, s40
	v_lshl_add_u64 v[204:205], s[26:27], 0, v[130:131]
	ds_read_b128 v[168:171], v148 offset:32768
	ds_read_b128 v[172:175], v148 offset:33792
	ds_read_b128 v[176:179], v148 offset:34816
	ds_read_b128 v[180:183], v148 offset:35840
	ds_read_b128 v[184:187], v148 offset:36864
	ds_read_b128 v[192:195], v148 offset:37888
	ds_read_b128 v[196:199], v148 offset:38912
	ds_read_b128 v[200:203], v148 offset:39936
	global_load_lds_dwordx4 v[204:205], off
	v_lshl_add_u64 v[204:205], s[26:27], 0, v[132:133]
	s_mov_b32 m0, s41
	s_nop 0
	global_load_lds_dwordx4 v[204:205], off
	s_waitcnt lgkmcnt(8)
	s_barrier
	s_waitcnt lgkmcnt(0)
	s_waitcnt lgkmcnt(0)
	v_mfma_f32_16x16x32_bf16 v[126:129], v[142:145], v[168:171], v[126:129]
	v_mfma_f32_16x16x32_bf16 v[122:125], v[160:163], v[168:171], v[122:125]
	v_mfma_f32_16x16x32_bf16 v[110:113], v[142:145], v[176:179], v[110:113]
	v_mfma_f32_16x16x32_bf16 v[106:109], v[160:163], v[176:179], v[106:109]
	v_mfma_f32_16x16x32_bf16 v[94:97], v[142:145], v[184:187], v[94:97]
	v_mfma_f32_16x16x32_bf16 v[90:93], v[160:163], v[184:187], v[90:93]
	v_mfma_f32_16x16x32_bf16 v[78:81], v[142:145], v[196:199], v[78:81]
	v_mfma_f32_16x16x32_bf16 v[74:77], v[160:163], v[196:199], v[74:77]
	v_mfma_f32_16x16x32_bf16 v[126:129], v[156:159], v[172:175], v[126:129]
	v_mfma_f32_16x16x32_bf16 v[122:125], v[164:167], v[172:175], v[122:125]
	v_mfma_f32_16x16x32_bf16 v[110:113], v[156:159], v[180:183], v[110:113]
	v_mfma_f32_16x16x32_bf16 v[106:109], v[164:167], v[180:183], v[106:109]
	v_mfma_f32_16x16x32_bf16 v[94:97], v[156:159], v[192:195], v[94:97]
	v_mfma_f32_16x16x32_bf16 v[90:93], v[164:167], v[192:195], v[90:93]
	v_mfma_f32_16x16x32_bf16 v[78:81], v[156:159], v[200:203], v[78:81]
	v_mfma_f32_16x16x32_bf16 v[74:77], v[164:167], v[200:203], v[74:77]
	s_barrier
	s_add_i32 s26, 0, 0x1c000
	s_add_i32 s27, s56, s36
	v_add_u32_e32 v150, s26, v152
	v_lshl_add_u64 v[146:147], v[146:147], 0, s[2:3]
	s_mov_b32 m0, s27
	ds_read_b128 v[204:207], v150
	ds_read_b128 v[208:211], v150 offset:1024
	ds_read_b128 v[212:215], v150 offset:2048
	ds_read_b128 v[216:219], v150 offset:3072
	global_load_lds_dwordx4 v[146:147], off
	v_lshl_add_u64 v[146:147], v[188:189], 0, s[2:3]
	s_add_i32 m0, s27, 0x2000
	s_nop 0
	global_load_lds_dwordx4 v[146:147], off
	s_barrier
	s_waitcnt lgkmcnt(0)
	s_waitcnt lgkmcnt(0)
	v_mfma_f32_16x16x32_bf16 v[118:121], v[204:207], v[168:171], v[118:121]
	v_mfma_f32_16x16x32_bf16 v[114:117], v[212:215], v[168:171], v[114:117]
	v_mfma_f32_16x16x32_bf16 v[102:105], v[204:207], v[176:179], v[102:105]
	v_mfma_f32_16x16x32_bf16 v[98:101], v[212:215], v[176:179], v[98:101]
	v_mfma_f32_16x16x32_bf16 v[86:89], v[204:207], v[184:187], v[86:89]
	v_mfma_f32_16x16x32_bf16 v[82:85], v[212:215], v[184:187], v[82:85]
	v_mfma_f32_16x16x32_bf16 v[70:73], v[204:207], v[196:199], v[70:73]
	v_mfma_f32_16x16x32_bf16 v[66:69], v[212:215], v[196:199], v[66:69]
	v_mfma_f32_16x16x32_bf16 v[118:121], v[208:211], v[172:175], v[118:121]
	v_mfma_f32_16x16x32_bf16 v[114:117], v[216:219], v[172:175], v[114:117]
	v_mfma_f32_16x16x32_bf16 v[102:105], v[208:211], v[180:183], v[102:105]
	v_mfma_f32_16x16x32_bf16 v[98:101], v[216:219], v[180:183], v[98:101]
	v_mfma_f32_16x16x32_bf16 v[86:89], v[208:211], v[192:195], v[86:89]
	v_mfma_f32_16x16x32_bf16 v[82:85], v[216:219], v[192:195], v[82:85]
	v_mfma_f32_16x16x32_bf16 v[70:73], v[208:211], v[200:203], v[70:73]
	v_mfma_f32_16x16x32_bf16 v[66:69], v[216:219], v[200:203], v[66:69]
	s_mov_b32 m0, s43
	v_lshl_add_u64 v[146:147], v[190:191], 0, s[2:3]
	s_barrier
	ds_read_b128 v[168:171], v148 offset:49152
	ds_read_b128 v[172:175], v148 offset:50176
	ds_read_b128 v[176:179], v148 offset:51200
	ds_read_b128 v[180:183], v148 offset:52224
	ds_read_b128 v[184:187], v148 offset:53248
	ds_read_b128 v[192:195], v148 offset:54272
	ds_read_b128 v[196:199], v148 offset:55296
	ds_read_b128 v[200:203], v148 offset:56320
	global_load_lds_dwordx4 v[146:147], off
	v_lshl_add_u64 v[146:147], v[220:221], 0, s[2:3]
	s_mov_b32 m0, s44
	s_nop 0
	global_load_lds_dwordx4 v[146:147], off
	s_barrier
	s_waitcnt lgkmcnt(0)
	s_waitcnt lgkmcnt(0)
	v_mfma_f32_16x16x32_bf16 v[62:65], v[142:145], v[168:171], v[62:65]
	v_mfma_f32_16x16x32_bf16 v[58:61], v[160:163], v[168:171], v[58:61]
	v_mfma_f32_16x16x32_bf16 v[46:49], v[142:145], v[176:179], v[46:49]
	v_mfma_f32_16x16x32_bf16 v[42:45], v[160:163], v[176:179], v[42:45]
	v_mfma_f32_16x16x32_bf16 v[30:33], v[142:145], v[184:187], v[30:33]
	v_mfma_f32_16x16x32_bf16 v[26:29], v[160:163], v[184:187], v[26:29]
	v_mfma_f32_16x16x32_bf16 v[14:17], v[142:145], v[196:199], v[14:17]
	v_mfma_f32_16x16x32_bf16 v[10:13], v[160:163], v[196:199], v[10:13]
	v_mfma_f32_16x16x32_bf16 v[62:65], v[156:159], v[172:175], v[62:65]
	v_mfma_f32_16x16x32_bf16 v[58:61], v[164:167], v[172:175], v[58:61]
	v_mfma_f32_16x16x32_bf16 v[46:49], v[156:159], v[180:183], v[46:49]
	v_mfma_f32_16x16x32_bf16 v[42:45], v[164:167], v[180:183], v[42:45]
	v_mfma_f32_16x16x32_bf16 v[30:33], v[156:159], v[192:195], v[30:33]
	v_mfma_f32_16x16x32_bf16 v[26:29], v[164:167], v[192:195], v[26:29]
	v_mfma_f32_16x16x32_bf16 v[14:17], v[156:159], v[200:203], v[14:17]
	v_mfma_f32_16x16x32_bf16 v[10:13], v[164:167], v[200:203], v[10:13]
	s_barrier
	s_add_u32 s24, s24, 0x40080
	s_addc_u32 s25, s25, 0
	s_add_i32 s26, s26, s36
	v_lshl_add_u64 v[142:143], s[24:25], 0, v[130:131]
	s_mov_b32 m0, s26
	s_nop 0
	global_load_lds_dwordx4 v[142:143], off
	v_lshl_add_u64 v[142:143], s[24:25], 0, v[132:133]
	s_add_i32 m0, s26, 0x2000
	s_nop 0
	global_load_lds_dwordx4 v[142:143], off
	s_waitcnt vmcnt(6)
	s_barrier
	v_mfma_f32_16x16x32_bf16 v[54:57], v[204:207], v[168:171], v[54:57]
	v_mfma_f32_16x16x32_bf16 v[50:53], v[212:215], v[168:171], v[50:53]
	v_mfma_f32_16x16x32_bf16 v[38:41], v[204:207], v[176:179], v[38:41]
	v_mfma_f32_16x16x32_bf16 v[34:37], v[212:215], v[176:179], v[34:37]
	v_mfma_f32_16x16x32_bf16 v[22:25], v[204:207], v[184:187], v[22:25]
	v_mfma_f32_16x16x32_bf16 v[18:21], v[212:215], v[184:187], v[18:21]
	v_mfma_f32_16x16x32_bf16 v[6:9], v[204:207], v[196:199], v[6:9]
	v_mfma_f32_16x16x32_bf16 v[2:5], v[212:215], v[196:199], v[2:5]
	v_mfma_f32_16x16x32_bf16 v[54:57], v[208:211], v[172:175], v[54:57]
	v_mfma_f32_16x16x32_bf16 v[50:53], v[216:219], v[172:175], v[50:53]
	v_mfma_f32_16x16x32_bf16 v[38:41], v[208:211], v[180:183], v[38:41]
	v_mfma_f32_16x16x32_bf16 v[34:37], v[216:219], v[180:183], v[34:37]
	v_mfma_f32_16x16x32_bf16 v[22:25], v[208:211], v[192:195], v[22:25]
	v_mfma_f32_16x16x32_bf16 v[18:21], v[216:219], v[192:195], v[18:21]
	v_mfma_f32_16x16x32_bf16 v[6:9], v[208:211], v[200:203], v[6:9]
	v_mfma_f32_16x16x32_bf16 v[2:5], v[216:219], v[200:203], v[2:5]
	s_add_i32 s55, s55, 2
	s_add_u32 s22, s22, 0x100
	s_addc_u32 s23, s23, 0
	s_add_u32 s53, s53, 0x100
	s_addc_u32 s54, s54, 0
	s_cmp_gt_u32 s55, 13
	s_barrier
	s_cbranch_scc0 .LBB0_1223
	v_lshl_or_b32 v142, s50, 8, v151
	v_lshl_add_u32 v144, s20, 8, v155
	v_ashrrev_i32_e32 v143, 31, v142
	v_mov_b64_e32 v[146:147], s[6:7]
	v_ashrrev_i32_e32 v145, 31, v144
	v_mad_i64_i32 v[156:157], s[22:23], v144, s48, v[146:147]
	v_lshlrev_b64 v[142:143], 1, v[142:143]
	v_lshl_add_u64 v[156:157], v[156:157], 0, v[142:143]
	v_lshlrev_b64 v[160:161], 12, v[144:145]
	v_add_co_u32_e32 v158, vcc, 0x2ec42000, v156
	v_lshl_add_u64 v[160:161], s[8:9], 0, v[160:161]
	s_nop 0
	v_addc_co_u32_e32 v159, vcc, 0, v157, vcc
	v_lshl_add_u64 v[160:161], v[160:161], 0, v[142:143]
	v_mov_b32_e32 v228, v158
	v_mov_b32_e32 v229, v159
	v_mov_b32_e32 v232, v160
	v_mov_b32_e32 v233, v161
	v_mov_b32_e32 v237, 0x1000
	global_load_dwordx2 v[168:169], v[228:229], off
	global_load_dwordx2 v[170:171], v[232:233], off
	global_load_dwordx2 v[172:173], v[228:229], off offset:32
	global_load_dwordx2 v[174:175], v[232:233], off offset:32
	global_load_dwordx2 v[176:177], v[228:229], off offset:256
	global_load_dwordx2 v[178:179], v[232:233], off offset:256
	global_load_dwordx2 v[180:181], v[228:229], off offset:288
	global_load_dwordx2 v[182:183], v[232:233], off offset:288
	v_mov_b32_e32 v236, 16
	v_mad_i64_i32 v[230:231], s[22:23], v236, s48, v[228:229]
	v_mad_i64_i32 v[234:235], s[22:23], v236, v237, v[232:233]
	global_load_dwordx2 v[184:185], v[230:231], off
	global_load_dwordx2 v[186:187], v[234:235], off
	global_load_dwordx2 v[192:193], v[230:231], off offset:32
	global_load_dwordx2 v[194:195], v[234:235], off offset:32
	global_load_dwordx2 v[196:197], v[230:231], off offset:256
	global_load_dwordx2 v[198:199], v[234:235], off offset:256
	global_load_dwordx2 v[200:201], v[230:231], off offset:288
	global_load_dwordx2 v[202:203], v[234:235], off offset:288
	v_mov_b32_e32 v236, 32
	v_mad_i64_i32 v[230:231], s[22:23], v236, s48, v[228:229]
	v_mad_i64_i32 v[234:235], s[22:23], v236, v237, v[232:233]
	global_load_dwordx2 v[204:205], v[230:231], off
	global_load_dwordx2 v[206:207], v[234:235], off
	global_load_dwordx2 v[208:209], v[230:231], off offset:32
	global_load_dwordx2 v[210:211], v[234:235], off offset:32
	global_load_dwordx2 v[212:213], v[230:231], off offset:256
	global_load_dwordx2 v[214:215], v[234:235], off offset:256
	global_load_dwordx2 v[216:217], v[230:231], off offset:288
	global_load_dwordx2 v[218:219], v[234:235], off offset:288
	s_waitcnt vmcnt(0)
	v_mov_b32_e32 v158, v168
	v_mov_b32_e32 v159, v169
	v_lshl_add_u64 v[156:157], v[156:157], 0, s[10:11]
	v_mov_b32_e32 v162, v170
	v_mov_b32_e32 v163, v171
	s_mov_b32 s50, s12
	s_mov_b32 s20, s14
	s_mov_b64 s[24:25], s[18:19]
	s_nop 0
	v_lshlrev_b32_e32 v164, 16, v158
	v_and_b32_e32 v165, 0xffff0000, v158
	v_lshlrev_b32_e32 v158, 16, v159
	v_and_b32_e32 v159, 0xffff0000, v159
	v_lshlrev_b32_e32 v166, 16, v162
	v_and_b32_e32 v167, 0xffff0000, v162
	v_lshlrev_b32_e32 v162, 16, v163
	v_and_b32_e32 v163, 0xffff0000, v163
	v_pk_fma_f32 v[128:129], v[128:129], v[158:159], v[162:163]
	v_pk_fma_f32 v[126:127], v[126:127], v[164:165], v[166:167]
	s_nop 0
	v_cvt_pk_bf16_f32 v126, v126, v127
	v_cvt_pk_bf16_f32 v127, v128, v129
	v_mov_b32_e32 v128, v172
	v_mov_b32_e32 v129, v173
	v_mov_b32_e32 v158, v174
	v_mov_b32_e32 v159, v175
	s_nop 0
	v_lshlrev_b32_e32 v162, 16, v158
	global_store_dwordx2 v[160:161], v[126:127], off
	v_lshlrev_b32_e32 v126, 16, v128
	v_and_b32_e32 v127, 0xffff0000, v128
	v_lshlrev_b32_e32 v128, 16, v129
	v_and_b32_e32 v129, 0xffff0000, v129
	v_and_b32_e32 v163, 0xffff0000, v158
	v_lshlrev_b32_e32 v158, 16, v159
	v_and_b32_e32 v159, 0xffff0000, v159
	v_pk_fma_f32 v[124:125], v[124:125], v[128:129], v[158:159]
	v_pk_fma_f32 v[122:123], v[122:123], v[126:127], v[162:163]
	s_nop 0
	v_cvt_pk_bf16_f32 v122, v122, v123
	v_cvt_pk_bf16_f32 v123, v124, v125
	v_mov_b32_e32 v124, v176
	v_mov_b32_e32 v125, v177
	v_mov_b32_e32 v126, v178
	v_mov_b32_e32 v127, v179
	s_nop 0
	v_lshlrev_b32_e32 v128, 16, v126
	global_store_dwordx2 v[160:161], v[122:123], off offset:32
	v_lshlrev_b32_e32 v122, 16, v124
	v_and_b32_e32 v123, 0xffff0000, v124
	v_lshlrev_b32_e32 v124, 16, v125
	v_and_b32_e32 v125, 0xffff0000, v125
	v_and_b32_e32 v129, 0xffff0000, v126
	v_lshlrev_b32_e32 v126, 16, v127
	v_and_b32_e32 v127, 0xffff0000, v127
	v_pk_fma_f32 v[120:121], v[120:121], v[124:125], v[126:127]
	v_pk_fma_f32 v[118:119], v[118:119], v[122:123], v[128:129]
	v_or_b32_e32 v124, 16, v144
	v_cvt_pk_bf16_f32 v118, v118, v119
	v_cvt_pk_bf16_f32 v119, v120, v121
	v_mov_b32_e32 v120, v180
	v_mov_b32_e32 v121, v181
	v_mov_b32_e32 v122, v182
	v_mov_b32_e32 v123, v183
	v_ashrrev_i32_e32 v125, 31, v124
	v_mad_i64_i32 v[126:127], s[22:23], v124, s48, v[146:147]
	global_store_dwordx2 v[160:161], v[118:119], off offset:256
	v_lshl_add_u64 v[126:127], v[126:127], 0, v[142:143]
	v_add_co_u32_e32 v128, vcc, s49, v126
	s_nop 0
	v_lshlrev_b32_e32 v118, 16, v120
	v_and_b32_e32 v119, 0xffff0000, v120
	v_lshlrev_b32_e32 v156, 16, v122
	v_and_b32_e32 v157, 0xffff0000, v122
	v_pk_fma_f32 v[114:115], v[114:115], v[118:119], v[156:157]
	v_lshlrev_b64 v[118:119], 12, v[124:125]
	v_lshlrev_b32_e32 v120, 16, v121
	v_and_b32_e32 v121, 0xffff0000, v121
	v_lshlrev_b32_e32 v122, 16, v123
	v_and_b32_e32 v123, 0xffff0000, v123
	v_lshl_add_u64 v[118:119], s[8:9], 0, v[118:119]
	v_addc_co_u32_e32 v129, vcc, 0, v127, vcc
	v_pk_fma_f32 v[116:117], v[116:117], v[120:121], v[122:123]
	v_lshl_add_u64 v[118:119], v[118:119], 0, v[142:143]
	v_cvt_pk_bf16_f32 v114, v114, v115
	v_cvt_pk_bf16_f32 v115, v116, v117
	v_mov_b32_e32 v116, v184
	v_mov_b32_e32 v117, v185
	v_mov_b32_e32 v120, v186
	v_mov_b32_e32 v121, v187
	v_lshl_add_u64 v[122:123], v[126:127], 0, s[10:11]
	global_store_dwordx2 v[160:161], v[114:115], off offset:288
	s_nop 0
	v_lshlrev_b32_e32 v114, 16, v116
	v_and_b32_e32 v115, 0xffff0000, v116
	v_lshlrev_b32_e32 v116, 16, v117
	v_and_b32_e32 v117, 0xffff0000, v117
	v_lshlrev_b32_e32 v124, 16, v120
	v_and_b32_e32 v125, 0xffff0000, v120
	v_lshlrev_b32_e32 v120, 16, v121
	v_and_b32_e32 v121, 0xffff0000, v121
	v_pk_fma_f32 v[112:113], v[112:113], v[116:117], v[120:121]
	v_pk_fma_f32 v[110:111], v[110:111], v[114:115], v[124:125]
	s_nop 0
	v_cvt_pk_bf16_f32 v110, v110, v111
	v_cvt_pk_bf16_f32 v111, v112, v113
	v_mov_b32_e32 v112, v192
	v_mov_b32_e32 v113, v193
	v_mov_b32_e32 v114, v194
	v_mov_b32_e32 v115, v195
	s_nop 0
	v_lshlrev_b32_e32 v116, 16, v114
	global_store_dwordx2 v[118:119], v[110:111], off
	v_lshlrev_b32_e32 v110, 16, v112
	v_and_b32_e32 v111, 0xffff0000, v112
	v_lshlrev_b32_e32 v112, 16, v113
	v_and_b32_e32 v113, 0xffff0000, v113
	v_and_b32_e32 v117, 0xffff0000, v114
	v_lshlrev_b32_e32 v114, 16, v115
	v_and_b32_e32 v115, 0xffff0000, v115
	v_pk_fma_f32 v[108:109], v[108:109], v[112:113], v[114:115]
	v_pk_fma_f32 v[106:107], v[106:107], v[110:111], v[116:117]
	s_nop 0
	v_cvt_pk_bf16_f32 v106, v106, v107
	v_cvt_pk_bf16_f32 v107, v108, v109
	v_mov_b32_e32 v108, v196
	v_mov_b32_e32 v109, v197
	v_mov_b32_e32 v110, v198
	v_mov_b32_e32 v111, v199
	s_nop 0
	v_lshlrev_b32_e32 v112, 16, v110
	global_store_dwordx2 v[118:119], v[106:107], off offset:32
	v_lshlrev_b32_e32 v106, 16, v108
	v_and_b32_e32 v107, 0xffff0000, v108
	v_lshlrev_b32_e32 v108, 16, v109
	v_and_b32_e32 v109, 0xffff0000, v109
	v_and_b32_e32 v113, 0xffff0000, v110
	v_lshlrev_b32_e32 v110, 16, v111
	v_and_b32_e32 v111, 0xffff0000, v111
	v_pk_fma_f32 v[104:105], v[104:105], v[108:109], v[110:111]
	v_pk_fma_f32 v[102:103], v[102:103], v[106:107], v[112:113]
	v_or_b32_e32 v108, 32, v144
	v_cvt_pk_bf16_f32 v102, v102, v103
	v_cvt_pk_bf16_f32 v103, v104, v105
	v_mov_b32_e32 v104, v200
	v_mov_b32_e32 v105, v201
	v_mov_b32_e32 v106, v202
	v_mov_b32_e32 v107, v203
	v_ashrrev_i32_e32 v109, 31, v108
	v_mad_i64_i32 v[110:111], s[22:23], v108, s48, v[146:147]
	global_store_dwordx2 v[118:119], v[102:103], off offset:256
	v_lshl_add_u64 v[110:111], v[110:111], 0, v[142:143]
	v_add_co_u32_e32 v112, vcc, s49, v110
	s_nop 0
	v_lshlrev_b32_e32 v102, 16, v104
	v_and_b32_e32 v103, 0xffff0000, v104
	v_lshlrev_b32_e32 v114, 16, v106
	v_and_b32_e32 v115, 0xffff0000, v106
	v_pk_fma_f32 v[98:99], v[98:99], v[102:103], v[114:115]
	v_lshlrev_b64 v[102:103], 12, v[108:109]
	v_lshlrev_b32_e32 v104, 16, v105
	v_and_b32_e32 v105, 0xffff0000, v105
	v_lshlrev_b32_e32 v106, 16, v107
	v_and_b32_e32 v107, 0xffff0000, v107
	v_lshl_add_u64 v[102:103], s[8:9], 0, v[102:103]
	v_addc_co_u32_e32 v113, vcc, 0, v111, vcc
	v_pk_fma_f32 v[100:101], v[100:101], v[104:105], v[106:107]
	v_lshl_add_u64 v[102:103], v[102:103], 0, v[142:143]
	v_cvt_pk_bf16_f32 v98, v98, v99
	v_cvt_pk_bf16_f32 v99, v100, v101
	v_mov_b32_e32 v100, v204
	v_mov_b32_e32 v101, v205
	v_mov_b32_e32 v104, v206
	v_mov_b32_e32 v105, v207
	v_lshl_add_u64 v[106:107], v[110:111], 0, s[10:11]
	global_store_dwordx2 v[118:119], v[98:99], off offset:288
	s_nop 0
	v_lshlrev_b32_e32 v98, 16, v100
	v_and_b32_e32 v99, 0xffff0000, v100
	v_lshlrev_b32_e32 v100, 16, v101
	v_and_b32_e32 v101, 0xffff0000, v101
	v_lshlrev_b32_e32 v108, 16, v104
	v_and_b32_e32 v109, 0xffff0000, v104
	v_lshlrev_b32_e32 v104, 16, v105
	v_and_b32_e32 v105, 0xffff0000, v105
	v_pk_fma_f32 v[96:97], v[96:97], v[100:101], v[104:105]
	v_pk_fma_f32 v[94:95], v[94:95], v[98:99], v[108:109]
	s_nop 0
	v_cvt_pk_bf16_f32 v94, v94, v95
	v_cvt_pk_bf16_f32 v95, v96, v97
	v_mov_b32_e32 v96, v208
	v_mov_b32_e32 v97, v209
	v_mov_b32_e32 v98, v210
	v_mov_b32_e32 v99, v211
	s_nop 0
	v_lshlrev_b32_e32 v100, 16, v98
	global_store_dwordx2 v[102:103], v[94:95], off
	v_lshlrev_b32_e32 v94, 16, v96
	v_and_b32_e32 v95, 0xffff0000, v96
	v_lshlrev_b32_e32 v96, 16, v97
	v_and_b32_e32 v97, 0xffff0000, v97
	v_and_b32_e32 v101, 0xffff0000, v98
	v_lshlrev_b32_e32 v98, 16, v99
	v_and_b32_e32 v99, 0xffff0000, v99
	v_pk_fma_f32 v[92:93], v[92:93], v[96:97], v[98:99]
	v_pk_fma_f32 v[90:91], v[90:91], v[94:95], v[100:101]
	s_nop 0
	v_cvt_pk_bf16_f32 v90, v90, v91
	v_cvt_pk_bf16_f32 v91, v92, v93
	v_mov_b32_e32 v92, v212
	v_mov_b32_e32 v93, v213
	v_mov_b32_e32 v94, v214
	v_mov_b32_e32 v95, v215
	s_nop 0
	v_lshlrev_b32_e32 v96, 16, v94
	global_store_dwordx2 v[102:103], v[90:91], off offset:32
	v_lshlrev_b32_e32 v90, 16, v92
	v_and_b32_e32 v91, 0xffff0000, v92
	v_lshlrev_b32_e32 v92, 16, v93
	v_and_b32_e32 v93, 0xffff0000, v93
	v_and_b32_e32 v97, 0xffff0000, v94
	v_lshlrev_b32_e32 v94, 16, v95
	v_and_b32_e32 v95, 0xffff0000, v95
	v_pk_fma_f32 v[88:89], v[88:89], v[92:93], v[94:95]
	v_pk_fma_f32 v[86:87], v[86:87], v[90:91], v[96:97]
	v_or_b32_e32 v92, 48, v144
	v_cvt_pk_bf16_f32 v86, v86, v87
	v_cvt_pk_bf16_f32 v87, v88, v89
	v_mov_b32_e32 v88, v216
	v_mov_b32_e32 v89, v217
	v_mov_b32_e32 v90, v218
	v_mov_b32_e32 v91, v219
	v_ashrrev_i32_e32 v93, 31, v92
	v_mad_i64_i32 v[94:95], s[22:23], v92, s48, v[146:147]
	global_store_dwordx2 v[102:103], v[86:87], off offset:256
	v_lshl_add_u64 v[94:95], v[94:95], 0, v[142:143]
	v_add_co_u32_e32 v96, vcc, s49, v94
	s_nop 0
	v_lshlrev_b32_e32 v86, 16, v88
	v_and_b32_e32 v87, 0xffff0000, v88
	v_lshlrev_b32_e32 v98, 16, v90
	v_and_b32_e32 v99, 0xffff0000, v90
	v_pk_fma_f32 v[82:83], v[82:83], v[86:87], v[98:99]
	v_lshlrev_b64 v[86:87], 12, v[92:93]
	v_lshlrev_b32_e32 v88, 16, v89
	v_and_b32_e32 v89, 0xffff0000, v89
	v_lshlrev_b32_e32 v90, 16, v91
	v_and_b32_e32 v91, 0xffff0000, v91
	v_lshl_add_u64 v[86:87], s[8:9], 0, v[86:87]
	v_addc_co_u32_e32 v97, vcc, 0, v95, vcc
	v_pk_fma_f32 v[84:85], v[84:85], v[88:89], v[90:91]
	v_lshl_add_u64 v[86:87], v[86:87], 0, v[142:143]
	v_cvt_pk_bf16_f32 v82, v82, v83
	v_cvt_pk_bf16_f32 v83, v84, v85
	v_mov_b32_e32 v237, 0x1000
	v_mov_b32_e32 v236, 48
	v_mad_i64_i32 v[230:231], s[22:23], v236, s48, v[228:229]
	v_mad_i64_i32 v[234:235], s[22:23], v236, v237, v[232:233]
	global_load_dwordx2 v[168:169], v[230:231], off
	global_load_dwordx2 v[170:171], v[234:235], off
	global_load_dwordx2 v[172:173], v[230:231], off offset:32
	global_load_dwordx2 v[174:175], v[234:235], off offset:32
	global_load_dwordx2 v[176:177], v[230:231], off offset:256
	global_load_dwordx2 v[178:179], v[234:235], off offset:256
	global_load_dwordx2 v[180:181], v[230:231], off offset:288
	global_load_dwordx2 v[182:183], v[234:235], off offset:288
	v_mov_b32_e32 v236, 128
	v_mad_i64_i32 v[230:231], s[22:23], v236, s48, v[228:229]
	v_mad_i64_i32 v[234:235], s[22:23], v236, v237, v[232:233]
	global_load_dwordx2 v[184:185], v[230:231], off
	global_load_dwordx2 v[186:187], v[234:235], off
	global_load_dwordx2 v[192:193], v[230:231], off offset:32
	global_load_dwordx2 v[194:195], v[234:235], off offset:32
	global_load_dwordx2 v[196:197], v[230:231], off offset:256
	global_load_dwordx2 v[198:199], v[234:235], off offset:256
	global_load_dwordx2 v[200:201], v[230:231], off offset:288
	global_load_dwordx2 v[202:203], v[234:235], off offset:288
	v_mov_b32_e32 v236, 144
	v_mad_i64_i32 v[230:231], s[22:23], v236, s48, v[228:229]
	v_mad_i64_i32 v[234:235], s[22:23], v236, v237, v[232:233]
	global_load_dwordx2 v[204:205], v[230:231], off
	global_load_dwordx2 v[206:207], v[234:235], off
	global_load_dwordx2 v[208:209], v[230:231], off offset:32
	global_load_dwordx2 v[210:211], v[234:235], off offset:32
	global_load_dwordx2 v[212:213], v[230:231], off offset:256
	global_load_dwordx2 v[214:215], v[234:235], off offset:256
	global_load_dwordx2 v[216:217], v[230:231], off offset:288
	global_load_dwordx2 v[218:219], v[234:235], off offset:288
	s_waitcnt vmcnt(0)
	v_mov_b32_e32 v84, v168
	v_mov_b32_e32 v85, v169
	v_mov_b32_e32 v88, v170
	v_mov_b32_e32 v89, v171
	v_lshl_add_u64 v[90:91], v[94:95], 0, s[10:11]
	global_store_dwordx2 v[102:103], v[82:83], off offset:288
	s_nop 0
	v_lshlrev_b32_e32 v82, 16, v84
	v_and_b32_e32 v83, 0xffff0000, v84
	v_lshlrev_b32_e32 v84, 16, v85
	v_and_b32_e32 v85, 0xffff0000, v85
	v_lshlrev_b32_e32 v92, 16, v88
	v_and_b32_e32 v93, 0xffff0000, v88
	v_lshlrev_b32_e32 v88, 16, v89
	v_and_b32_e32 v89, 0xffff0000, v89
	v_pk_fma_f32 v[80:81], v[80:81], v[84:85], v[88:89]
	v_pk_fma_f32 v[78:79], v[78:79], v[82:83], v[92:93]
	s_nop 0
	v_cvt_pk_bf16_f32 v78, v78, v79
	v_cvt_pk_bf16_f32 v79, v80, v81
	v_mov_b32_e32 v80, v172
	v_mov_b32_e32 v81, v173
	v_mov_b32_e32 v82, v174
	v_mov_b32_e32 v83, v175
	s_nop 0
	v_lshlrev_b32_e32 v84, 16, v82
	global_store_dwordx2 v[86:87], v[78:79], off
	v_lshlrev_b32_e32 v78, 16, v80
	v_and_b32_e32 v79, 0xffff0000, v80
	v_lshlrev_b32_e32 v80, 16, v81
	v_and_b32_e32 v81, 0xffff0000, v81
	v_and_b32_e32 v85, 0xffff0000, v82
	v_lshlrev_b32_e32 v82, 16, v83
	v_and_b32_e32 v83, 0xffff0000, v83
	v_pk_fma_f32 v[76:77], v[76:77], v[80:81], v[82:83]
	v_pk_fma_f32 v[74:75], v[74:75], v[78:79], v[84:85]
	s_nop 0
	v_cvt_pk_bf16_f32 v74, v74, v75
	v_cvt_pk_bf16_f32 v75, v76, v77
	v_mov_b32_e32 v76, v176
	v_mov_b32_e32 v77, v177
	v_mov_b32_e32 v78, v178
	v_mov_b32_e32 v79, v179
	s_nop 0
	v_lshlrev_b32_e32 v80, 16, v78
	global_store_dwordx2 v[86:87], v[74:75], off offset:32
	v_lshlrev_b32_e32 v74, 16, v76
	v_and_b32_e32 v75, 0xffff0000, v76
	v_lshlrev_b32_e32 v76, 16, v77
	v_and_b32_e32 v77, 0xffff0000, v77
	v_and_b32_e32 v81, 0xffff0000, v78
	v_lshlrev_b32_e32 v78, 16, v79
	v_and_b32_e32 v79, 0xffff0000, v79
	v_pk_fma_f32 v[72:73], v[72:73], v[76:77], v[78:79]
	v_pk_fma_f32 v[70:71], v[70:71], v[74:75], v[80:81]
	v_add_u32_e32 v76, 0x80, v144
	v_cvt_pk_bf16_f32 v70, v70, v71
	v_cvt_pk_bf16_f32 v71, v72, v73
	v_mov_b32_e32 v72, v180
	v_mov_b32_e32 v73, v181
	v_mov_b32_e32 v74, v182
	v_mov_b32_e32 v75, v183
	v_ashrrev_i32_e32 v77, 31, v76
	v_mad_i64_i32 v[78:79], s[22:23], v76, s48, v[146:147]
	global_store_dwordx2 v[86:87], v[70:71], off offset:256
	v_lshl_add_u64 v[78:79], v[78:79], 0, v[142:143]
	v_add_co_u32_e32 v80, vcc, s49, v78
	s_nop 0
	v_lshlrev_b32_e32 v70, 16, v72
	v_and_b32_e32 v71, 0xffff0000, v72
	v_lshlrev_b32_e32 v82, 16, v74
	v_and_b32_e32 v83, 0xffff0000, v74
	v_pk_fma_f32 v[66:67], v[66:67], v[70:71], v[82:83]
	v_lshlrev_b64 v[70:71], 12, v[76:77]
	v_lshlrev_b32_e32 v72, 16, v73
	v_and_b32_e32 v73, 0xffff0000, v73
	v_lshlrev_b32_e32 v74, 16, v75
	v_and_b32_e32 v75, 0xffff0000, v75
	v_lshl_add_u64 v[70:71], s[8:9], 0, v[70:71]
	v_addc_co_u32_e32 v81, vcc, 0, v79, vcc
	v_pk_fma_f32 v[68:69], v[68:69], v[72:73], v[74:75]
	v_lshl_add_u64 v[70:71], v[70:71], 0, v[142:143]
	v_cvt_pk_bf16_f32 v66, v66, v67
	v_cvt_pk_bf16_f32 v67, v68, v69
	v_mov_b32_e32 v68, v184
	v_mov_b32_e32 v69, v185
	v_mov_b32_e32 v72, v186
	v_mov_b32_e32 v73, v187
	v_lshl_add_u64 v[74:75], v[78:79], 0, s[10:11]
	global_store_dwordx2 v[86:87], v[66:67], off offset:288
	s_nop 0
	v_lshlrev_b32_e32 v66, 16, v68
	v_and_b32_e32 v67, 0xffff0000, v68
	v_lshlrev_b32_e32 v68, 16, v69
	v_and_b32_e32 v69, 0xffff0000, v69
	v_lshlrev_b32_e32 v76, 16, v72
	v_and_b32_e32 v77, 0xffff0000, v72
	v_lshlrev_b32_e32 v72, 16, v73
	v_and_b32_e32 v73, 0xffff0000, v73
	v_pk_fma_f32 v[64:65], v[64:65], v[68:69], v[72:73]
	v_pk_fma_f32 v[62:63], v[62:63], v[66:67], v[76:77]
	s_nop 0
	v_cvt_pk_bf16_f32 v62, v62, v63
	v_cvt_pk_bf16_f32 v63, v64, v65
	v_mov_b32_e32 v64, v192
	v_mov_b32_e32 v65, v193
	v_mov_b32_e32 v66, v194
	v_mov_b32_e32 v67, v195
	s_nop 0
	v_lshlrev_b32_e32 v68, 16, v66
	global_store_dwordx2 v[70:71], v[62:63], off
	v_lshlrev_b32_e32 v62, 16, v64
	v_and_b32_e32 v63, 0xffff0000, v64
	v_lshlrev_b32_e32 v64, 16, v65
	v_and_b32_e32 v65, 0xffff0000, v65
	v_and_b32_e32 v69, 0xffff0000, v66
	v_lshlrev_b32_e32 v66, 16, v67
	v_and_b32_e32 v67, 0xffff0000, v67
	v_pk_fma_f32 v[60:61], v[60:61], v[64:65], v[66:67]
	v_pk_fma_f32 v[58:59], v[58:59], v[62:63], v[68:69]
	s_nop 0
	v_cvt_pk_bf16_f32 v58, v58, v59
	v_cvt_pk_bf16_f32 v59, v60, v61
	v_mov_b32_e32 v60, v196
	v_mov_b32_e32 v61, v197
	v_mov_b32_e32 v62, v198
	v_mov_b32_e32 v63, v199
	s_nop 0
	v_lshlrev_b32_e32 v64, 16, v62
	global_store_dwordx2 v[70:71], v[58:59], off offset:32
	v_lshlrev_b32_e32 v58, 16, v60
	v_and_b32_e32 v59, 0xffff0000, v60
	v_lshlrev_b32_e32 v60, 16, v61
	v_and_b32_e32 v61, 0xffff0000, v61
	v_and_b32_e32 v65, 0xffff0000, v62
	v_lshlrev_b32_e32 v62, 16, v63
	v_and_b32_e32 v63, 0xffff0000, v63
	v_pk_fma_f32 v[56:57], v[56:57], v[60:61], v[62:63]
	v_pk_fma_f32 v[54:55], v[54:55], v[58:59], v[64:65]
	v_add_u32_e32 v60, 0x90, v144
	v_cvt_pk_bf16_f32 v54, v54, v55
	v_cvt_pk_bf16_f32 v55, v56, v57
	v_mov_b32_e32 v56, v200
	v_mov_b32_e32 v57, v201
	v_mov_b32_e32 v58, v202
	v_mov_b32_e32 v59, v203
	v_ashrrev_i32_e32 v61, 31, v60
	v_mad_i64_i32 v[62:63], s[22:23], v60, s48, v[146:147]
	global_store_dwordx2 v[70:71], v[54:55], off offset:256
	v_lshl_add_u64 v[62:63], v[62:63], 0, v[142:143]
	v_add_co_u32_e32 v64, vcc, s49, v62
	s_nop 0
	v_lshlrev_b32_e32 v54, 16, v56
	v_and_b32_e32 v55, 0xffff0000, v56
	v_lshlrev_b32_e32 v66, 16, v58
	v_and_b32_e32 v67, 0xffff0000, v58
	v_pk_fma_f32 v[50:51], v[50:51], v[54:55], v[66:67]
	v_lshlrev_b64 v[54:55], 12, v[60:61]
	v_lshlrev_b32_e32 v56, 16, v57
	v_and_b32_e32 v57, 0xffff0000, v57
	v_lshlrev_b32_e32 v58, 16, v59
	v_and_b32_e32 v59, 0xffff0000, v59
	v_lshl_add_u64 v[54:55], s[8:9], 0, v[54:55]
	v_addc_co_u32_e32 v65, vcc, 0, v63, vcc
	v_pk_fma_f32 v[52:53], v[52:53], v[56:57], v[58:59]
	v_lshl_add_u64 v[54:55], v[54:55], 0, v[142:143]
	v_cvt_pk_bf16_f32 v50, v50, v51
	v_cvt_pk_bf16_f32 v51, v52, v53
	v_mov_b32_e32 v52, v204
	v_mov_b32_e32 v53, v205
	v_mov_b32_e32 v56, v206
	v_mov_b32_e32 v57, v207
	v_lshl_add_u64 v[58:59], v[62:63], 0, s[10:11]
	global_store_dwordx2 v[70:71], v[50:51], off offset:288
	s_nop 0
	v_lshlrev_b32_e32 v50, 16, v52
	v_and_b32_e32 v51, 0xffff0000, v52
	v_lshlrev_b32_e32 v52, 16, v53
	v_and_b32_e32 v53, 0xffff0000, v53
	v_lshlrev_b32_e32 v60, 16, v56
	v_and_b32_e32 v61, 0xffff0000, v56
	v_lshlrev_b32_e32 v56, 16, v57
	v_and_b32_e32 v57, 0xffff0000, v57
	v_pk_fma_f32 v[48:49], v[48:49], v[52:53], v[56:57]
	v_pk_fma_f32 v[46:47], v[46:47], v[50:51], v[60:61]
	s_nop 0
	v_cvt_pk_bf16_f32 v46, v46, v47
	v_cvt_pk_bf16_f32 v47, v48, v49
	v_mov_b32_e32 v48, v208
	v_mov_b32_e32 v49, v209
	v_mov_b32_e32 v50, v210
	v_mov_b32_e32 v51, v211
	s_nop 0
	v_lshlrev_b32_e32 v52, 16, v50
	global_store_dwordx2 v[54:55], v[46:47], off
	v_lshlrev_b32_e32 v46, 16, v48
	v_and_b32_e32 v47, 0xffff0000, v48
	v_lshlrev_b32_e32 v48, 16, v49
	v_and_b32_e32 v49, 0xffff0000, v49
	v_and_b32_e32 v53, 0xffff0000, v50
	v_lshlrev_b32_e32 v50, 16, v51
	v_and_b32_e32 v51, 0xffff0000, v51
	v_pk_fma_f32 v[44:45], v[44:45], v[48:49], v[50:51]
	v_pk_fma_f32 v[42:43], v[42:43], v[46:47], v[52:53]
	s_nop 0
	v_cvt_pk_bf16_f32 v42, v42, v43
	v_cvt_pk_bf16_f32 v43, v44, v45
	v_mov_b32_e32 v44, v212
	v_mov_b32_e32 v45, v213
	v_mov_b32_e32 v46, v214
	v_mov_b32_e32 v47, v215
	s_nop 0
	v_lshlrev_b32_e32 v48, 16, v46
	global_store_dwordx2 v[54:55], v[42:43], off offset:32
	v_lshlrev_b32_e32 v42, 16, v44
	v_and_b32_e32 v43, 0xffff0000, v44
	v_lshlrev_b32_e32 v44, 16, v45
	v_and_b32_e32 v45, 0xffff0000, v45
	v_and_b32_e32 v49, 0xffff0000, v46
	v_lshlrev_b32_e32 v46, 16, v47
	v_and_b32_e32 v47, 0xffff0000, v47
	v_pk_fma_f32 v[40:41], v[40:41], v[44:45], v[46:47]
	v_pk_fma_f32 v[38:39], v[38:39], v[42:43], v[48:49]
	v_add_u32_e32 v44, 0xa0, v144
	v_cvt_pk_bf16_f32 v38, v38, v39
	v_cvt_pk_bf16_f32 v39, v40, v41
	v_mov_b32_e32 v40, v216
	v_mov_b32_e32 v41, v217
	v_mov_b32_e32 v42, v218
	v_mov_b32_e32 v43, v219
	v_ashrrev_i32_e32 v45, 31, v44
	v_mad_i64_i32 v[46:47], s[22:23], v44, s48, v[146:147]
	global_store_dwordx2 v[54:55], v[38:39], off offset:256
	v_lshl_add_u64 v[46:47], v[46:47], 0, v[142:143]
	v_add_co_u32_e32 v48, vcc, s49, v46
	s_nop 0
	v_lshlrev_b32_e32 v38, 16, v40
	v_and_b32_e32 v39, 0xffff0000, v40
	v_lshlrev_b32_e32 v50, 16, v42
	v_and_b32_e32 v51, 0xffff0000, v42
	v_pk_fma_f32 v[34:35], v[34:35], v[38:39], v[50:51]
	v_lshlrev_b64 v[38:39], 12, v[44:45]
	v_lshlrev_b32_e32 v40, 16, v41
	v_and_b32_e32 v41, 0xffff0000, v41
	v_lshlrev_b32_e32 v42, 16, v43
	v_and_b32_e32 v43, 0xffff0000, v43
	v_lshl_add_u64 v[38:39], s[8:9], 0, v[38:39]
	v_addc_co_u32_e32 v49, vcc, 0, v47, vcc
	v_pk_fma_f32 v[36:37], v[36:37], v[40:41], v[42:43]
	v_lshl_add_u64 v[38:39], v[38:39], 0, v[142:143]
	v_cvt_pk_bf16_f32 v34, v34, v35
	v_cvt_pk_bf16_f32 v35, v36, v37
	v_mov_b32_e32 v237, 0x1000
	v_mov_b32_e32 v236, 160
	v_mad_i64_i32 v[230:231], s[22:23], v236, s48, v[228:229]
	v_mad_i64_i32 v[234:235], s[22:23], v236, v237, v[232:233]
	global_load_dwordx2 v[168:169], v[230:231], off
	global_load_dwordx2 v[170:171], v[234:235], off
	global_load_dwordx2 v[172:173], v[230:231], off offset:32
	global_load_dwordx2 v[174:175], v[234:235], off offset:32
	global_load_dwordx2 v[176:177], v[230:231], off offset:256
	global_load_dwordx2 v[178:179], v[234:235], off offset:256
	global_load_dwordx2 v[180:181], v[230:231], off offset:288
	global_load_dwordx2 v[182:183], v[234:235], off offset:288
	v_mov_b32_e32 v236, 176
	v_mad_i64_i32 v[230:231], s[22:23], v236, s48, v[228:229]
	v_mad_i64_i32 v[234:235], s[22:23], v236, v237, v[232:233]
	global_load_dwordx2 v[184:185], v[230:231], off
	global_load_dwordx2 v[186:187], v[234:235], off
	global_load_dwordx2 v[192:193], v[230:231], off offset:32
	global_load_dwordx2 v[194:195], v[234:235], off offset:32
	global_load_dwordx2 v[196:197], v[230:231], off offset:256
	global_load_dwordx2 v[198:199], v[234:235], off offset:256
	global_load_dwordx2 v[200:201], v[230:231], off offset:288
	global_load_dwordx2 v[202:203], v[234:235], off offset:288
	s_waitcnt vmcnt(0)
	v_mov_b32_e32 v36, v168
	v_mov_b32_e32 v37, v169
	v_mov_b32_e32 v40, v170
	v_mov_b32_e32 v41, v171
	v_lshl_add_u64 v[42:43], v[46:47], 0, s[10:11]
	global_store_dwordx2 v[54:55], v[34:35], off offset:288
	s_nop 0
	v_lshlrev_b32_e32 v34, 16, v36
	v_and_b32_e32 v35, 0xffff0000, v36
	v_lshlrev_b32_e32 v36, 16, v37
	v_and_b32_e32 v37, 0xffff0000, v37
	v_lshlrev_b32_e32 v44, 16, v40
	v_and_b32_e32 v45, 0xffff0000, v40
	v_lshlrev_b32_e32 v40, 16, v41
	v_and_b32_e32 v41, 0xffff0000, v41
	v_pk_fma_f32 v[32:33], v[32:33], v[36:37], v[40:41]
	v_pk_fma_f32 v[30:31], v[30:31], v[34:35], v[44:45]
	s_nop 0
	v_cvt_pk_bf16_f32 v30, v30, v31
	v_cvt_pk_bf16_f32 v31, v32, v33
	v_mov_b32_e32 v32, v172
	v_mov_b32_e32 v33, v173
	v_mov_b32_e32 v34, v174
	v_mov_b32_e32 v35, v175
	s_nop 0
	v_lshlrev_b32_e32 v36, 16, v34
	global_store_dwordx2 v[38:39], v[30:31], off
	v_lshlrev_b32_e32 v30, 16, v32
	v_and_b32_e32 v31, 0xffff0000, v32
	v_lshlrev_b32_e32 v32, 16, v33
	v_and_b32_e32 v33, 0xffff0000, v33
	v_and_b32_e32 v37, 0xffff0000, v34
	v_lshlrev_b32_e32 v34, 16, v35
	v_and_b32_e32 v35, 0xffff0000, v35
	v_pk_fma_f32 v[28:29], v[28:29], v[32:33], v[34:35]
	v_pk_fma_f32 v[26:27], v[26:27], v[30:31], v[36:37]
	s_nop 0
	v_cvt_pk_bf16_f32 v26, v26, v27
	v_cvt_pk_bf16_f32 v27, v28, v29
	v_mov_b32_e32 v28, v176
	v_mov_b32_e32 v29, v177
	v_mov_b32_e32 v30, v178
	v_mov_b32_e32 v31, v179
	s_nop 0
	v_lshlrev_b32_e32 v32, 16, v30
	global_store_dwordx2 v[38:39], v[26:27], off offset:32
	v_lshlrev_b32_e32 v26, 16, v28
	v_and_b32_e32 v27, 0xffff0000, v28
	v_lshlrev_b32_e32 v28, 16, v29
	v_and_b32_e32 v29, 0xffff0000, v29
	v_and_b32_e32 v33, 0xffff0000, v30
	v_lshlrev_b32_e32 v30, 16, v31
	v_and_b32_e32 v31, 0xffff0000, v31
	v_pk_fma_f32 v[24:25], v[24:25], v[28:29], v[30:31]
	v_pk_fma_f32 v[22:23], v[22:23], v[26:27], v[32:33]
	v_add_u32_e32 v28, 0xb0, v144
	v_cvt_pk_bf16_f32 v22, v22, v23
	v_cvt_pk_bf16_f32 v23, v24, v25
	v_mov_b32_e32 v24, v180
	v_mov_b32_e32 v25, v181
	v_mov_b32_e32 v26, v182
	v_mov_b32_e32 v27, v183
	v_ashrrev_i32_e32 v29, 31, v28
	v_mad_i64_i32 v[30:31], s[22:23], v28, s48, v[146:147]
	global_store_dwordx2 v[38:39], v[22:23], off offset:256
	v_lshl_add_u64 v[30:31], v[30:31], 0, v[142:143]
	v_add_co_u32_e32 v32, vcc, s49, v30
	s_mov_b64 s[22:23], s[16:17]
	s_nop 0
	v_addc_co_u32_e32 v33, vcc, 0, v31, vcc
	s_and_b64 vcc, exec, s[0:1]
	s_nop 0
	v_lshlrev_b32_e32 v22, 16, v24
	v_and_b32_e32 v23, 0xffff0000, v24
	v_lshlrev_b32_e32 v34, 16, v26
	v_and_b32_e32 v35, 0xffff0000, v26
	v_pk_fma_f32 v[18:19], v[18:19], v[22:23], v[34:35]
	v_lshlrev_b64 v[22:23], 12, v[28:29]
	v_lshlrev_b32_e32 v24, 16, v25
	v_and_b32_e32 v25, 0xffff0000, v25
	v_lshlrev_b32_e32 v26, 16, v27
	v_and_b32_e32 v27, 0xffff0000, v27
	v_lshl_add_u64 v[22:23], s[8:9], 0, v[22:23]
	v_pk_fma_f32 v[20:21], v[20:21], v[24:25], v[26:27]
	v_lshl_add_u64 v[22:23], v[22:23], 0, v[142:143]
	v_cvt_pk_bf16_f32 v18, v18, v19
	v_cvt_pk_bf16_f32 v19, v20, v21
	v_mov_b32_e32 v20, v184
	v_mov_b32_e32 v21, v185
	v_mov_b32_e32 v24, v186
	v_mov_b32_e32 v25, v187
	v_lshl_add_u64 v[26:27], v[30:31], 0, s[10:11]
	global_store_dwordx2 v[38:39], v[18:19], off offset:288
	s_nop 0
	v_lshlrev_b32_e32 v18, 16, v20
	v_and_b32_e32 v19, 0xffff0000, v20
	v_lshlrev_b32_e32 v20, 16, v21
	v_and_b32_e32 v21, 0xffff0000, v21
	v_lshlrev_b32_e32 v28, 16, v24
	v_and_b32_e32 v29, 0xffff0000, v24
	v_lshlrev_b32_e32 v24, 16, v25
	v_and_b32_e32 v25, 0xffff0000, v25
	v_pk_fma_f32 v[16:17], v[16:17], v[20:21], v[24:25]
	v_pk_fma_f32 v[14:15], v[14:15], v[18:19], v[28:29]
	s_nop 0
	v_cvt_pk_bf16_f32 v14, v14, v15
	v_cvt_pk_bf16_f32 v15, v16, v17
	v_mov_b32_e32 v16, v192
	v_mov_b32_e32 v17, v193
	v_mov_b32_e32 v18, v194
	v_mov_b32_e32 v19, v195
	s_nop 0
	v_lshlrev_b32_e32 v20, 16, v18
	global_store_dwordx2 v[22:23], v[14:15], off
	v_lshlrev_b32_e32 v14, 16, v16
	v_and_b32_e32 v15, 0xffff0000, v16
	v_lshlrev_b32_e32 v16, 16, v17
	v_and_b32_e32 v17, 0xffff0000, v17
	v_and_b32_e32 v21, 0xffff0000, v18
	v_lshlrev_b32_e32 v18, 16, v19
	v_and_b32_e32 v19, 0xffff0000, v19
	v_pk_fma_f32 v[12:13], v[12:13], v[16:17], v[18:19]
	v_pk_fma_f32 v[10:11], v[10:11], v[14:15], v[20:21]
	s_nop 0
	v_cvt_pk_bf16_f32 v10, v10, v11
	v_cvt_pk_bf16_f32 v11, v12, v13
	v_mov_b32_e32 v12, v196
	v_mov_b32_e32 v13, v197
	v_mov_b32_e32 v14, v198
	v_mov_b32_e32 v15, v199
	s_nop 0
	v_lshlrev_b32_e32 v16, 16, v14
	global_store_dwordx2 v[22:23], v[10:11], off offset:32
	v_lshlrev_b32_e32 v10, 16, v12
	v_and_b32_e32 v11, 0xffff0000, v12
	v_lshlrev_b32_e32 v12, 16, v13
	v_and_b32_e32 v13, 0xffff0000, v13
	v_and_b32_e32 v17, 0xffff0000, v14
	v_lshlrev_b32_e32 v14, 16, v15
	v_and_b32_e32 v15, 0xffff0000, v15
	v_pk_fma_f32 v[8:9], v[8:9], v[12:13], v[14:15]
	v_pk_fma_f32 v[6:7], v[6:7], v[10:11], v[16:17]
	s_nop 0
	v_cvt_pk_bf16_f32 v6, v6, v7
	v_cvt_pk_bf16_f32 v7, v8, v9
	v_mov_b32_e32 v8, v200
	v_mov_b32_e32 v9, v201
	v_mov_b32_e32 v10, v202
	v_mov_b32_e32 v11, v203
	s_nop 0
	v_lshlrev_b32_e32 v12, 16, v10
	global_store_dwordx2 v[22:23], v[6:7], off offset:256
	v_lshlrev_b32_e32 v6, 16, v8
	v_and_b32_e32 v7, 0xffff0000, v8
	v_and_b32_e32 v13, 0xffff0000, v10
	v_lshlrev_b32_e32 v8, 16, v9
	v_and_b32_e32 v9, 0xffff0000, v9
	v_lshlrev_b32_e32 v10, 16, v11
	v_and_b32_e32 v11, 0xffff0000, v11
	v_pk_fma_f32 v[2:3], v[2:3], v[6:7], v[12:13]
	v_pk_fma_f32 v[4:5], v[4:5], v[8:9], v[10:11]
	v_cvt_pk_bf16_f32 v2, v2, v3
	s_nop 0
	v_cvt_pk_bf16_f32 v3, v4, v5
	global_store_dwordx2 v[22:23], v[2:3], off offset:288
	s_cbranch_vccz .LBB0_1220
	s_waitcnt vmcnt(0)
	s_cmpk_gt_u32 s28, 0xff
	s_cbranch_scc1 .LBB0_1227
	s_barrier

.LBB0_1229:
	s_cmp_gt_i32 s55, 7
	s_cselect_b64 s[0:1], -1, 0
	s_and_b64 s[2:3], s[4:5], s[0:1]
	s_andn2_b64 vcc, exec, s[2:3]
	s_cbranch_vccnz .LBB0_1279
	s_waitcnt vmcnt(0)
	s_barrier
	s_setprio 0
	s_mov_b64 s[2:3], exec
	v_readlane_b32 s4, v250, 5
	v_readlane_b32 s5, v250, 6
	s_and_b64 s[4:5], s[2:3], s[4:5]
	s_mov_b64 exec, s[4:5]
	s_cbranch_execz .LBB0_1278
	s_add_i32 s4, 0, 0x27ff0
	v_mov_b32_e32 v1, s4
	s_waitcnt vmcnt(0) expcnt(0) lgkmcnt(0)
	ds_read_b32 v3, v1
	s_add_i32 s4, 0, 0x27ff4
	v_mov_b32_e32 v1, s4
	ds_read_b32 v1, v1
	s_waitcnt lgkmcnt(1)
	v_cmp_ne_u32_e32 vcc, 0, v3
	s_cbranch_vccnz .LBB0_1246
	v_readlane_b32 s4, v250, 2
	v_readlane_b32 s5, v250, 3
	s_load_dwordx2 s[8:9], s[4:5], 0x4
	s_add_u32 s4, s52, 0x1000
	s_addc_u32 s5, s53, 0
	s_add_u32 s6, s52, 0x1100
	s_addc_u32 s7, s53, 0
	v_readlane_b32 s10, v250, 1
	s_waitcnt lgkmcnt(0)
	s_mul_i32 s18, s8, s10
	s_add_u32 s8, s52, 0x1200
	s_mul_i32 s18, s18, s9
	s_addc_u32 s9, s53, 0
	s_add_u32 s10, s52, 0x1300
	s_addc_u32 s11, s53, 0
	s_mov_b32 s19, 1
	v_mov_b32_e32 v17, 0
	s_branch .LBB0_1234

.LBB0_1279:
	s_cmp_lt_i32 s54, 8
	s_cselect_b64 s[2:3], -1, 0
	s_and_b64 s[0:1], s[2:3], s[0:1]
	s_andn2_b64 vcc, exec, s[0:1]
	s_cbranch_vccnz .LBB0_1293
	v_mov_b32_e32 v1, v248
	s_waitcnt vmcnt(11)
	v_mov_b32_e32 v2, v0
	v_readlane_b32 s28, v250, 1
	v_readlane_b32 s29, v250, 0
	v_readlane_b32 s0, v250, 39
	s_mov_b64 s[0:1], s[90:91]
	s_mov_b64 s[4:5], s[52:53]
	s_cmpk_gt_i32 s29, 0x207
	v_readfirstlane_b32 s30, v0
	s_barrier
	s_cbranch_scc1 .LBB0_1292
	s_add_u32 s31, s4, 0x2ab40000
	s_addc_u32 s33, s5, 0
	v_lshlrev_b32_e32 v1, 4, v0
	s_add_u32 s34, s4, 0x16140000
	s_waitcnt vmcnt(9)
	v_or_b32_e32 v10, 0x2000, v1
	s_addc_u32 s35, s5, 0
	v_lshrrev_b32_e32 v2, 7, v10
	v_bfe_u32 v13, v0, 2, 4
	s_movk_i32 s0, 0x70
	s_ashr_i32 s37, s29, 31
	v_and_or_b32 v2, v2, s0, v13
	s_lshr_b32 s0, s37, 29
	s_add_i32 s0, s29, s0
	s_ashr_i32 s7, s0, 3
	s_and_b32 s0, s0, -8
	s_sub_i32 s0, s29, s0
	s_lshr_b32 s8, s0, 31
	s_addk_i32 s8, 0x41
	s_mul_i32 s0, s8, s0
	s_add_i32 s0, s0, s7
	s_ashr_i32 s7, s0, 31
	s_lshr_b32 s7, s7, 26
	s_add_i32 s7, s0, s7
	s_ashr_i32 s8, s7, 6
	s_lshl_b32 s10, s8, 3
	s_sub_i32 s8, 0x41, s10
	s_min_u32 s11, s8, 8
	s_andn2_b32 s7, s7, 63
	v_and_b32_e32 v3, 32, v0
	s_sub_i32 s7, s0, s7
	v_cvt_f32_ubyte0_e32 v4, s11
	v_bitop3_b32 v11, v1, v3, 48 bitop3:0x6c
	v_and_b32_e32 v12, 64, v0
	v_cvt_f32_i32_e32 v3, s7
	v_rcp_iflag_f32_e32 v5, v4
	v_or_b32_e32 v1, v11, v12
	v_lshl_or_b32 v130, v2, 12, v1
	v_lshrrev_b32_e32 v2, 3, v0
	v_and_or_b32 v2, v2, 48, v13
	v_lshl_or_b32 v132, v2, 12, v1
	v_mul_f32_e32 v1, v3, v5
	v_trunc_f32_e32 v1, v1
	v_fma_f32 v2, -v1, v4, v3
	v_cvt_i32_f32_e32 v1, v1
	s_lshr_b32 s6, s30, 6
	s_ashr_i32 s0, s7, 30
	s_lshr_b32 s1, s30, 8
	s_lshl_b32 s36, s6, 10
	s_or_b32 s0, s0, 1
	v_cmp_ge_f32_e64 s[8:9], |v2|, v4
	s_and_b64 s[8:9], s[8:9], exec
	s_cselect_b32 s0, s0, 0
	v_readfirstlane_b32 s8, v1
	s_add_i32 s0, s8, s0
	s_mul_i32 s8, s0, s11
	s_sub_i32 s7, s7, s8
	s_sext_i32_i8 s7, s7
	s_add_i32 s20, s10, s7
	s_ashr_i32 s21, s20, 31
	s_lshl_b64 s[8:9], s[20:21], 20
	s_add_u32 s22, s31, s8
	s_addc_u32 s23, s33, s9
	s_bfe_i64 s[8:9], s[0:1], 0x80000
	s_lshl_b64 s[8:9], s[8:9], 20
	s_add_u32 s24, s34, s8
	s_addc_u32 s25, s35, s9
	s_add_i32 s21, s36, 0
	s_add_i32 m0, s21, 0x10000
	s_add_i32 s38, s21, 0x2000
	global_load_lds_dwordx4 v132, s[24:25]
	s_add_i32 m0, s21, 0x12000
	s_add_u32 s8, s24, 0x80000
	global_load_lds_dwordx4 v130, s[24:25]
	s_mov_b32 m0, s21
	s_addc_u32 s9, s25, 0
	global_load_lds_dwordx4 v132, s[22:23]
	s_mov_b32 m0, s38
	v_mov_b32_e32 v135, 0
	global_load_lds_dwordx4 v130, s[22:23]
	s_add_i32 m0, s21, 0x14000
	v_mov_b32_e32 v133, v135
	global_load_lds_dwordx4 v132, s[8:9]
	s_add_i32 m0, s21, 0x16000
	v_mov_b32_e32 v131, v135
	global_load_lds_dwordx4 v130, s[8:9]
	s_add_u32 s8, s22, 0x80000
	s_addc_u32 s9, s23, 0
	s_add_i32 s39, s21, 0x4000
	s_mov_b32 m0, s39
	s_add_i32 s40, s21, 0x6000
	global_load_lds_dwordx4 v132, s[8:9]
	s_mov_b32 m0, s40
	s_mov_b32 s41, 0
	global_load_lds_dwordx4 v130, s[8:9]
	v_lshl_add_u64 v[8:9], s[24:25], 0, v[132:133]
	v_lshl_add_u64 v[6:7], s[24:25], 0, v[130:131]
	v_lshl_add_u64 v[4:5], s[22:23], 0, v[132:133]
	s_setprio 1
	s_cmp_lg_u32 s1, 1
	v_lshl_add_u64 v[2:3], s[22:23], 0, v[130:131]
	v_readlane_b32 s44, v250, 7
	v_readlane_b32 s45, v250, 8
	v_readlane_b32 s46, v250, 9
	v_readlane_b32 s47, v250, 10
	v_readlane_b32 s48, v250, 11
	v_readlane_b32 s49, v250, 12
	v_readlane_b32 s50, v250, 13
	v_readlane_b32 s51, v250, 14
	v_readlane_b32 s52, v250, 15
	v_readlane_b32 s53, v250, 16
	v_readlane_b32 s54, v250, 17
	v_readlane_b32 s55, v250, 18
	v_readlane_b32 s56, v250, 19
	v_readlane_b32 s57, v250, 20
	v_readlane_b32 s58, v250, 21
	v_readlane_b32 s59, v250, 22
	s_cbranch_scc1 .LBB0_1283
	s_barrier
	s_setprio 0

.LBB0_1287:
	ds_read_b128 v[144:147], v150
	ds_read_b128 v[154:157], v150 offset:1024
	ds_read_b128 v[158:161], v150 offset:2048
	ds_read_b128 v[162:165], v150 offset:3072
	s_add_u32 s24, s22, 0xfff80080
	s_addc_u32 s25, s23, -1
	s_cmp_eq_u32 s53, 28
	s_cselect_b32 s27, s15, s25
	s_cselect_b32 s26, s49, s24
	s_cselect_b32 s25, s13, s52
	s_cselect_b32 s24, s50, s51
	v_lshl_add_u64 v[190:191], s[22:23], 0, v[136:137]
	s_add_i32 m0, s21, 0xc000
	ds_read_b128 v[166:169], v151
	ds_read_b128 v[170:173], v151 offset:1024
	ds_read_b128 v[174:177], v151 offset:2048
	ds_read_b128 v[178:181], v151 offset:3072
	ds_read_b128 v[182:185], v151 offset:4096
	ds_read_b128 v[186:189], v151 offset:5120
	ds_read_b128 v[192:195], v151 offset:6144
	ds_read_b128 v[196:199], v151 offset:7168
	global_load_lds_dwordx4 v[190:191], off
	v_lshl_add_u64 v[190:191], s[22:23], 0, v[138:139]
	s_add_i32 m0, s21, 0xe000
	s_nop 0
	global_load_lds_dwordx4 v[190:191], off
	s_waitcnt lgkmcnt(8)
	s_barrier
	s_waitcnt lgkmcnt(0)
	s_waitcnt lgkmcnt(0)
	v_mfma_f32_16x16x32_bf16 v[126:129], v[144:147], v[166:169], v[126:129]
	v_mfma_f32_16x16x32_bf16 v[122:125], v[158:161], v[166:169], v[122:125]
	v_mfma_f32_16x16x32_bf16 v[114:117], v[144:147], v[174:177], v[114:117]
	v_mfma_f32_16x16x32_bf16 v[106:109], v[158:161], v[174:177], v[106:109]
	v_mfma_f32_16x16x32_bf16 v[98:101], v[144:147], v[182:185], v[98:101]
	v_mfma_f32_16x16x32_bf16 v[90:93], v[158:161], v[182:185], v[90:93]
	v_mfma_f32_16x16x32_bf16 v[82:85], v[144:147], v[192:195], v[82:85]
	v_mfma_f32_16x16x32_bf16 v[74:77], v[158:161], v[192:195], v[74:77]
	v_mfma_f32_16x16x32_bf16 v[126:129], v[154:157], v[170:173], v[126:129]
	v_mfma_f32_16x16x32_bf16 v[122:125], v[162:165], v[170:173], v[122:125]
	v_mfma_f32_16x16x32_bf16 v[114:117], v[154:157], v[178:181], v[114:117]
	v_mfma_f32_16x16x32_bf16 v[106:109], v[162:165], v[178:181], v[106:109]
	v_mfma_f32_16x16x32_bf16 v[98:101], v[154:157], v[186:189], v[98:101]
	v_mfma_f32_16x16x32_bf16 v[90:93], v[162:165], v[186:189], v[90:93]
	v_mfma_f32_16x16x32_bf16 v[82:85], v[154:157], v[196:199], v[82:85]
	v_mfma_f32_16x16x32_bf16 v[74:77], v[162:165], v[196:199], v[74:77]
	s_barrier
	s_add_i32 s54, s45, s36
	v_lshl_add_u64 v[190:191], s[24:25], 0, v[132:133]
	s_mov_b32 m0, s54
	ds_read_b128 v[200:203], v152
	ds_read_b128 v[204:207], v152 offset:1024
	ds_read_b128 v[208:211], v152 offset:2048
	ds_read_b128 v[212:215], v152 offset:3072
	global_load_lds_dwordx4 v[190:191], off
	v_lshl_add_u64 v[216:217], s[24:25], 0, v[130:131]
	s_add_i32 m0, s54, 0x2000
	s_nop 0
	global_load_lds_dwordx4 v[216:217], off
	s_barrier
	s_waitcnt lgkmcnt(0)
	s_waitcnt lgkmcnt(0)
	v_mfma_f32_16x16x32_bf16 v[118:121], v[200:203], v[166:169], v[118:121]
	v_mfma_f32_16x16x32_bf16 v[110:113], v[208:211], v[166:169], v[110:113]
	v_mfma_f32_16x16x32_bf16 v[102:105], v[200:203], v[174:177], v[102:105]
	v_mfma_f32_16x16x32_bf16 v[94:97], v[208:211], v[174:177], v[94:97]
	v_mfma_f32_16x16x32_bf16 v[86:89], v[200:203], v[182:185], v[86:89]
	v_mfma_f32_16x16x32_bf16 v[78:81], v[208:211], v[182:185], v[78:81]
	v_mfma_f32_16x16x32_bf16 v[70:73], v[200:203], v[192:195], v[70:73]
	v_mfma_f32_16x16x32_bf16 v[66:69], v[208:211], v[192:195], v[66:69]
	v_mfma_f32_16x16x32_bf16 v[118:121], v[204:207], v[170:173], v[118:121]
	v_mfma_f32_16x16x32_bf16 v[110:113], v[212:215], v[170:173], v[110:113]
	v_mfma_f32_16x16x32_bf16 v[102:105], v[204:207], v[178:181], v[102:105]
	v_mfma_f32_16x16x32_bf16 v[94:97], v[212:215], v[178:181], v[94:97]
	v_mfma_f32_16x16x32_bf16 v[86:89], v[204:207], v[186:189], v[86:89]
	v_mfma_f32_16x16x32_bf16 v[78:81], v[212:215], v[186:189], v[78:81]
	v_mfma_f32_16x16x32_bf16 v[70:73], v[204:207], v[196:199], v[70:73]
	v_mfma_f32_16x16x32_bf16 v[66:69], v[212:215], v[196:199], v[66:69]
	s_mov_b32 m0, s21
	v_lshl_add_u64 v[218:219], s[26:27], 0, v[132:133]
	s_barrier
	ds_read_b128 v[166:169], v151 offset:16384
	ds_read_b128 v[170:173], v151 offset:17408
	ds_read_b128 v[174:177], v151 offset:18432
	ds_read_b128 v[178:181], v151 offset:19456
	ds_read_b128 v[182:185], v151 offset:20480
	ds_read_b128 v[186:189], v151 offset:21504
	ds_read_b128 v[192:195], v151 offset:22528
	ds_read_b128 v[196:199], v151 offset:23552
	global_load_lds_dwordx4 v[218:219], off
	v_lshl_add_u64 v[220:221], s[26:27], 0, v[130:131]
	s_mov_b32 m0, s38
	s_nop 0
	global_load_lds_dwordx4 v[220:221], off
	s_barrier
	s_waitcnt lgkmcnt(0)
	s_waitcnt lgkmcnt(0)
	v_mfma_f32_16x16x32_bf16 v[62:65], v[144:147], v[166:169], v[62:65]
	v_mfma_f32_16x16x32_bf16 v[58:61], v[158:161], v[166:169], v[58:61]
	v_mfma_f32_16x16x32_bf16 v[50:53], v[144:147], v[174:177], v[50:53]
	v_mfma_f32_16x16x32_bf16 v[42:45], v[158:161], v[174:177], v[42:45]
	v_mfma_f32_16x16x32_bf16 v[34:37], v[144:147], v[182:185], v[34:37]
	v_mfma_f32_16x16x32_bf16 v[26:29], v[158:161], v[182:185], v[26:29]
	v_mfma_f32_16x16x32_bf16 v[18:21], v[144:147], v[192:195], v[18:21]
	v_mfma_f32_16x16x32_bf16 v[10:13], v[158:161], v[192:195], v[10:13]
	v_mfma_f32_16x16x32_bf16 v[62:65], v[154:157], v[170:173], v[62:65]
	v_mfma_f32_16x16x32_bf16 v[58:61], v[162:165], v[170:173], v[58:61]
	v_mfma_f32_16x16x32_bf16 v[50:53], v[154:157], v[178:181], v[50:53]
	v_mfma_f32_16x16x32_bf16 v[42:45], v[162:165], v[178:181], v[42:45]
	v_mfma_f32_16x16x32_bf16 v[34:37], v[154:157], v[186:189], v[34:37]
	v_mfma_f32_16x16x32_bf16 v[26:29], v[162:165], v[186:189], v[26:29]
	v_mfma_f32_16x16x32_bf16 v[18:21], v[154:157], v[196:199], v[18:21]
	v_mfma_f32_16x16x32_bf16 v[10:13], v[162:165], v[196:199], v[10:13]
	s_barrier
	s_add_u32 s54, s24, 0x80000
	s_addc_u32 s55, s25, 0
	s_add_i32 s56, s46, s36
	v_lshl_add_u64 v[144:145], s[54:55], 0, v[132:133]
	s_mov_b32 m0, s56
	s_nop 0
	global_load_lds_dwordx4 v[144:145], off
	v_lshl_add_u64 v[144:145], s[54:55], 0, v[130:131]
	s_add_i32 m0, s56, 0x2000
	s_nop 0
	global_load_lds_dwordx4 v[144:145], off
	s_waitcnt vmcnt(6)
	s_barrier
	v_mfma_f32_16x16x32_bf16 v[54:57], v[200:203], v[166:169], v[54:57]
	v_mfma_f32_16x16x32_bf16 v[46:49], v[208:211], v[166:169], v[46:49]
	v_mfma_f32_16x16x32_bf16 v[38:41], v[200:203], v[174:177], v[38:41]
	v_mfma_f32_16x16x32_bf16 v[30:33], v[208:211], v[174:177], v[30:33]
	v_mfma_f32_16x16x32_bf16 v[22:25], v[200:203], v[182:185], v[22:25]
	v_mfma_f32_16x16x32_bf16 v[14:17], v[208:211], v[182:185], v[14:17]
	v_mfma_f32_16x16x32_bf16 v[6:9], v[200:203], v[192:195], v[6:9]
	v_mfma_f32_16x16x32_bf16 v[2:5], v[208:211], v[192:195], v[2:5]
	v_mfma_f32_16x16x32_bf16 v[54:57], v[204:207], v[170:173], v[54:57]
	v_mfma_f32_16x16x32_bf16 v[46:49], v[212:215], v[170:173], v[46:49]
	v_mfma_f32_16x16x32_bf16 v[38:41], v[204:207], v[178:181], v[38:41]
	v_mfma_f32_16x16x32_bf16 v[30:33], v[212:215], v[178:181], v[30:33]
	v_mfma_f32_16x16x32_bf16 v[22:25], v[204:207], v[186:189], v[22:25]
	v_mfma_f32_16x16x32_bf16 v[14:17], v[212:215], v[186:189], v[14:17]
	v_mfma_f32_16x16x32_bf16 v[6:9], v[204:207], v[196:199], v[6:9]
	v_mfma_f32_16x16x32_bf16 v[2:5], v[212:215], v[196:199], v[2:5]
	s_add_i32 s54, 0, 0x18000
	v_add_u32_e32 v134, s54, v148
	s_barrier
	ds_read_b128 v[144:147], v134
	ds_read_b128 v[154:157], v134 offset:1024
	ds_read_b128 v[158:161], v134 offset:2048
	ds_read_b128 v[162:165], v134 offset:3072
	s_add_u32 s26, s26, 0x80000
	s_addc_u32 s27, s27, 0
	s_mov_b32 m0, s39
	v_lshl_add_u64 v[200:201], s[26:27], 0, v[132:133]
	ds_read_b128 v[166:169], v151 offset:32768
	ds_read_b128 v[170:173], v151 offset:33792
	ds_read_b128 v[174:177], v151 offset:34816
	ds_read_b128 v[178:181], v151 offset:35840
	ds_read_b128 v[182:185], v151 offset:36864
	ds_read_b128 v[186:189], v151 offset:37888
	ds_read_b128 v[192:195], v151 offset:38912
	ds_read_b128 v[196:199], v151 offset:39936
	global_load_lds_dwordx4 v[200:201], off
	v_lshl_add_u64 v[200:201], s[26:27], 0, v[130:131]
	s_mov_b32 m0, s40
	s_nop 0
	global_load_lds_dwordx4 v[200:201], off
	s_waitcnt lgkmcnt(8)
	s_barrier
	s_waitcnt lgkmcnt(0)
	s_waitcnt lgkmcnt(0)
	v_mfma_f32_16x16x32_bf16 v[126:129], v[144:147], v[166:169], v[126:129]
	v_mfma_f32_16x16x32_bf16 v[122:125], v[158:161], v[166:169], v[122:125]
	v_mfma_f32_16x16x32_bf16 v[114:117], v[144:147], v[174:177], v[114:117]
	v_mfma_f32_16x16x32_bf16 v[106:109], v[158:161], v[174:177], v[106:109]
	v_mfma_f32_16x16x32_bf16 v[98:101], v[144:147], v[182:185], v[98:101]
	v_mfma_f32_16x16x32_bf16 v[90:93], v[158:161], v[182:185], v[90:93]
	v_mfma_f32_16x16x32_bf16 v[82:85], v[144:147], v[192:195], v[82:85]
	v_mfma_f32_16x16x32_bf16 v[74:77], v[158:161], v[192:195], v[74:77]
	v_mfma_f32_16x16x32_bf16 v[126:129], v[154:157], v[170:173], v[126:129]
	v_mfma_f32_16x16x32_bf16 v[122:125], v[162:165], v[170:173], v[122:125]
	v_mfma_f32_16x16x32_bf16 v[114:117], v[154:157], v[178:181], v[114:117]
	v_mfma_f32_16x16x32_bf16 v[106:109], v[162:165], v[178:181], v[106:109]
	v_mfma_f32_16x16x32_bf16 v[98:101], v[154:157], v[186:189], v[98:101]
	v_mfma_f32_16x16x32_bf16 v[90:93], v[162:165], v[186:189], v[90:93]
	v_mfma_f32_16x16x32_bf16 v[82:85], v[154:157], v[196:199], v[82:85]
	v_mfma_f32_16x16x32_bf16 v[74:77], v[162:165], v[196:199], v[74:77]
	s_barrier
	s_add_i32 s26, 0, 0x1c000
	s_add_i32 s27, s54, s36
	v_add_u32_e32 v134, s26, v148
	v_lshl_add_u64 v[190:191], v[190:191], 0, s[6:7]
	s_mov_b32 m0, s27
	ds_read_b128 v[200:203], v134
	ds_read_b128 v[204:207], v134 offset:1024
	ds_read_b128 v[208:211], v134 offset:2048
	ds_read_b128 v[212:215], v134 offset:3072
	global_load_lds_dwordx4 v[190:191], off
	v_lshl_add_u64 v[190:191], v[216:217], 0, s[6:7]
	s_add_i32 m0, s27, 0x2000
	s_nop 0
	global_load_lds_dwordx4 v[190:191], off
	s_barrier
	s_waitcnt lgkmcnt(0)
	s_waitcnt lgkmcnt(0)
	v_mfma_f32_16x16x32_bf16 v[118:121], v[200:203], v[166:169], v[118:121]
	v_mfma_f32_16x16x32_bf16 v[110:113], v[208:211], v[166:169], v[110:113]
	v_mfma_f32_16x16x32_bf16 v[102:105], v[200:203], v[174:177], v[102:105]
	v_mfma_f32_16x16x32_bf16 v[94:97], v[208:211], v[174:177], v[94:97]
	v_mfma_f32_16x16x32_bf16 v[86:89], v[200:203], v[182:185], v[86:89]
	v_mfma_f32_16x16x32_bf16 v[78:81], v[208:211], v[182:185], v[78:81]
	v_mfma_f32_16x16x32_bf16 v[70:73], v[200:203], v[192:195], v[70:73]
	v_mfma_f32_16x16x32_bf16 v[66:69], v[208:211], v[192:195], v[66:69]
	v_mfma_f32_16x16x32_bf16 v[118:121], v[204:207], v[170:173], v[118:121]
	v_mfma_f32_16x16x32_bf16 v[110:113], v[212:215], v[170:173], v[110:113]
	v_mfma_f32_16x16x32_bf16 v[102:105], v[204:207], v[178:181], v[102:105]
	v_mfma_f32_16x16x32_bf16 v[94:97], v[212:215], v[178:181], v[94:97]
	v_mfma_f32_16x16x32_bf16 v[86:89], v[204:207], v[186:189], v[86:89]
	v_mfma_f32_16x16x32_bf16 v[78:81], v[212:215], v[186:189], v[78:81]
	v_mfma_f32_16x16x32_bf16 v[70:73], v[204:207], v[196:199], v[70:73]
	v_mfma_f32_16x16x32_bf16 v[66:69], v[212:215], v[196:199], v[66:69]
	s_mov_b32 m0, s42
	v_lshl_add_u64 v[190:191], v[218:219], 0, s[6:7]
	s_barrier
	ds_read_b128 v[166:169], v151 offset:49152
	ds_read_b128 v[170:173], v151 offset:50176
	ds_read_b128 v[174:177], v151 offset:51200
	ds_read_b128 v[178:181], v151 offset:52224
	ds_read_b128 v[182:185], v151 offset:53248
	ds_read_b128 v[186:189], v151 offset:54272
	ds_read_b128 v[192:195], v151 offset:55296
	ds_read_b128 v[196:199], v151 offset:56320
	global_load_lds_dwordx4 v[190:191], off
	v_lshl_add_u64 v[190:191], v[220:221], 0, s[6:7]
	s_mov_b32 m0, s43
	s_nop 0
	global_load_lds_dwordx4 v[190:191], off
	s_barrier
	s_waitcnt lgkmcnt(0)
	s_waitcnt lgkmcnt(0)
	v_mfma_f32_16x16x32_bf16 v[62:65], v[144:147], v[166:169], v[62:65]
	v_mfma_f32_16x16x32_bf16 v[58:61], v[158:161], v[166:169], v[58:61]
	v_mfma_f32_16x16x32_bf16 v[50:53], v[144:147], v[174:177], v[50:53]
	v_mfma_f32_16x16x32_bf16 v[42:45], v[158:161], v[174:177], v[42:45]
	v_mfma_f32_16x16x32_bf16 v[34:37], v[144:147], v[182:185], v[34:37]
	v_mfma_f32_16x16x32_bf16 v[26:29], v[158:161], v[182:185], v[26:29]
	v_mfma_f32_16x16x32_bf16 v[18:21], v[144:147], v[192:195], v[18:21]
	v_mfma_f32_16x16x32_bf16 v[10:13], v[158:161], v[192:195], v[10:13]
	v_mfma_f32_16x16x32_bf16 v[62:65], v[154:157], v[170:173], v[62:65]
	v_mfma_f32_16x16x32_bf16 v[58:61], v[162:165], v[170:173], v[58:61]
	v_mfma_f32_16x16x32_bf16 v[50:53], v[154:157], v[178:181], v[50:53]
	v_mfma_f32_16x16x32_bf16 v[42:45], v[162:165], v[178:181], v[42:45]
	v_mfma_f32_16x16x32_bf16 v[34:37], v[154:157], v[186:189], v[34:37]
	v_mfma_f32_16x16x32_bf16 v[26:29], v[162:165], v[186:189], v[26:29]
	v_mfma_f32_16x16x32_bf16 v[18:21], v[154:157], v[196:199], v[18:21]
	v_mfma_f32_16x16x32_bf16 v[10:13], v[162:165], v[196:199], v[10:13]
	s_barrier
	s_add_u32 s24, s24, 0x80080
	s_addc_u32 s25, s25, 0
	s_add_i32 s26, s26, s36
	v_lshl_add_u64 v[144:145], s[24:25], 0, v[132:133]
	s_mov_b32 m0, s26
	s_nop 0
	global_load_lds_dwordx4 v[144:145], off
	v_lshl_add_u64 v[144:145], s[24:25], 0, v[130:131]
	s_add_i32 m0, s26, 0x2000
	s_nop 0
	global_load_lds_dwordx4 v[144:145], off
	s_waitcnt vmcnt(6)
	s_barrier
	v_mfma_f32_16x16x32_bf16 v[54:57], v[200:203], v[166:169], v[54:57]
	v_mfma_f32_16x16x32_bf16 v[46:49], v[208:211], v[166:169], v[46:49]
	v_mfma_f32_16x16x32_bf16 v[38:41], v[200:203], v[174:177], v[38:41]
	v_mfma_f32_16x16x32_bf16 v[30:33], v[208:211], v[174:177], v[30:33]
	v_mfma_f32_16x16x32_bf16 v[22:25], v[200:203], v[182:185], v[22:25]
	v_mfma_f32_16x16x32_bf16 v[14:17], v[208:211], v[182:185], v[14:17]
	v_mfma_f32_16x16x32_bf16 v[6:9], v[200:203], v[192:195], v[6:9]
	v_mfma_f32_16x16x32_bf16 v[2:5], v[208:211], v[192:195], v[2:5]
	v_mfma_f32_16x16x32_bf16 v[54:57], v[204:207], v[170:173], v[54:57]
	v_mfma_f32_16x16x32_bf16 v[46:49], v[212:215], v[170:173], v[46:49]
	v_mfma_f32_16x16x32_bf16 v[38:41], v[204:207], v[178:181], v[38:41]
	v_mfma_f32_16x16x32_bf16 v[30:33], v[212:215], v[178:181], v[30:33]
	v_mfma_f32_16x16x32_bf16 v[22:25], v[204:207], v[186:189], v[22:25]
	v_mfma_f32_16x16x32_bf16 v[14:17], v[212:215], v[186:189], v[14:17]
	v_mfma_f32_16x16x32_bf16 v[6:9], v[204:207], v[196:199], v[6:9]
	v_mfma_f32_16x16x32_bf16 v[2:5], v[212:215], v[196:199], v[2:5]
	s_add_i32 s53, s53, 2
	s_add_u32 s22, s22, 0x100
	s_addc_u32 s23, s23, 0
	s_add_u32 s51, s51, 0x100
	s_addc_u32 s52, s52, 0
	s_cmp_gt_u32 s53, 29
	s_barrier
	s_cbranch_scc0 .LBB0_1287
	v_lshl_add_u32 v144, s20, 8, v1
	s_movk_i32 s13, 0x4000
	v_lshl_or_b32 v146, s48, 8, v149
	v_ashrrev_i32_e32 v134, 31, v144
	v_cmp_gt_i32_e32 vcc, s13, v144
	v_readlane_b32 s48, v250, 7
	v_add_u32_e32 v154, 0xffffc000, v144
	v_cndmask_b32_e32 v145, 0, v134, vcc
	v_readlane_b32 s49, v250, 8
	v_readlane_b32 s52, v250, 11
	v_readlane_b32 s53, v250, 12
	v_cndmask_b32_e32 v158, v154, v144, vcc
	v_mov_b32_e32 v159, v145
	v_mov_b32_e32 v154, s53
	v_mov_b32_e32 v155, s49
	v_mov_b32_e32 v156, s52
	v_mov_b32_e32 v157, s48
	s_movk_i32 s13, 0x3fff
	v_ashrrev_i32_e32 v147, 31, v146
	v_cndmask_b32_e32 v161, v154, v155, vcc
	v_cndmask_b32_e32 v160, v156, v157, vcc
	v_lshlrev_b64 v[158:159], 13, v[158:159]
	v_cmp_lt_i32_e32 vcc, s13, v144
	v_lshl_add_u64 v[158:159], v[160:161], 0, v[158:159]
	v_lshlrev_b64 v[146:147], 2, v[146:147]
	v_cndmask_b32_e32 v134, 0, v153, vcc
	v_lshl_add_u64 v[166:167], v[158:159], 0, v[146:147]
	v_lshl_add_u64 v[158:159], s[4:5], 0, v[134:135]
	v_lshl_add_u64 v[168:169], v[158:159], 0, v[146:147]
	v_add_co_u32_e32 v158, vcc, s47, v168
	v_lshlrev_b64 v[170:171], 13, v[144:145]
	s_nop 0
	v_addc_co_u32_e32 v159, vcc, 0, v169, vcc
	v_lshl_add_u64 v[170:171], s[8:9], 0, v[170:171]
	v_lshl_add_u64 v[170:171], v[170:171], 0, v[146:147]
	v_lshl_add_u64 v[168:169], v[168:169], 0, s[10:11]
	global_load_dwordx4 v[144:147], v[158:159], off
	global_load_dwordx4 v[154:157], v[168:169], off offset:64
	global_load_dwordx4 v[160:163], v[168:169], off offset:512
	global_load_dwordx4 v[172:175], v[168:169], off offset:576
	global_load_dwordx4 v[176:179], v[166:167], off
	global_load_dwordx4 v[180:183], v[166:167], off offset:64
	global_load_dwordx4 v[184:187], v[166:167], off offset:512
	global_load_dwordx4 v[192:195], v[166:167], off offset:576
	v_add_co_u32_e32 v188, vcc, 0x20000, v166
	s_nop 1
	v_addc_co_u32_e32 v189, vcc, 0, v167, vcc
	global_load_dwordx4 v[196:199], v[188:189], off
	global_load_dwordx4 v[200:203], v[188:189], off offset:64
	global_load_dwordx4 v[204:207], v[188:189], off offset:512
	global_load_dwordx4 v[208:211], v[188:189], off offset:576
	v_add_co_u32_e32 v214, vcc, 0x20000, v170
	s_nop 1
	v_addc_co_u32_e32 v215, vcc, 0, v171, vcc
	s_waitcnt vmcnt(0)
	v_pk_fma_f32 v[128:129], v[128:129], v[146:147], v[178:179]
	v_pk_fma_f32 v[126:127], v[126:127], v[144:145], v[176:177]
	global_store_dwordx4 v[170:171], v[126:129], off
	v_pk_fma_f32 v[124:125], v[124:125], v[156:157], v[182:183]
	v_pk_fma_f32 v[122:123], v[122:123], v[154:155], v[180:181]
	global_store_dwordx4 v[170:171], v[122:125], off offset:64
	v_pk_fma_f32 v[120:121], v[120:121], v[162:163], v[186:187]
	v_pk_fma_f32 v[118:119], v[118:119], v[160:161], v[184:185]
	global_store_dwordx4 v[170:171], v[118:121], off offset:512
	v_pk_fma_f32 v[112:113], v[112:113], v[174:175], v[194:195]
	v_pk_fma_f32 v[110:111], v[110:111], v[172:173], v[192:193]
	global_store_dwordx4 v[170:171], v[110:113], off offset:576
	v_pk_fma_f32 v[116:117], v[116:117], v[146:147], v[198:199]
	v_pk_fma_f32 v[114:115], v[114:115], v[144:145], v[196:197]
	global_store_dwordx4 v[214:215], v[114:117], off
	v_pk_fma_f32 v[108:109], v[108:109], v[156:157], v[202:203]
	v_pk_fma_f32 v[106:107], v[106:107], v[154:155], v[200:201]
	global_store_dwordx4 v[214:215], v[106:109], off offset:64
	v_pk_fma_f32 v[104:105], v[104:105], v[162:163], v[206:207]
	v_pk_fma_f32 v[102:103], v[102:103], v[160:161], v[204:205]
	global_store_dwordx4 v[214:215], v[102:105], off offset:512
	v_pk_fma_f32 v[96:97], v[96:97], v[174:175], v[210:211]
	v_pk_fma_f32 v[94:95], v[94:95], v[172:173], v[208:209]
	global_store_dwordx4 v[214:215], v[94:97], off offset:576
	v_add_co_u32_e32 v164, vcc, 0x40000, v166
	s_nop 1
	v_addc_co_u32_e32 v165, vcc, 0, v167, vcc
	global_load_dwordx4 v[176:179], v[164:165], off
	global_load_dwordx4 v[180:183], v[164:165], off offset:64
	global_load_dwordx4 v[184:187], v[164:165], off offset:512
	global_load_dwordx4 v[192:195], v[164:165], off offset:576
	v_add_co_u32_e32 v188, vcc, 0x60000, v166
	s_nop 1
	v_addc_co_u32_e32 v189, vcc, 0, v167, vcc
	global_load_dwordx4 v[196:199], v[188:189], off
	global_load_dwordx4 v[200:203], v[188:189], off offset:64
	global_load_dwordx4 v[204:207], v[188:189], off offset:512
	global_load_dwordx4 v[208:211], v[188:189], off offset:576
	v_add_co_u32_e32 v212, vcc, 0x40000, v170
	s_nop 1
	v_addc_co_u32_e32 v213, vcc, 0, v171, vcc
	v_add_co_u32_e32 v214, vcc, 0x60000, v170
	s_nop 1
	v_addc_co_u32_e32 v215, vcc, 0, v171, vcc
	s_waitcnt vmcnt(0)
	v_pk_fma_f32 v[100:101], v[100:101], v[146:147], v[178:179]
	v_pk_fma_f32 v[98:99], v[98:99], v[144:145], v[176:177]
	global_store_dwordx4 v[212:213], v[98:101], off
	v_pk_fma_f32 v[92:93], v[92:93], v[156:157], v[182:183]
	v_pk_fma_f32 v[90:91], v[90:91], v[154:155], v[180:181]
	global_store_dwordx4 v[212:213], v[90:93], off offset:64
	v_pk_fma_f32 v[88:89], v[88:89], v[162:163], v[186:187]
	v_pk_fma_f32 v[86:87], v[86:87], v[160:161], v[184:185]
	global_store_dwordx4 v[212:213], v[86:89], off offset:512
	v_pk_fma_f32 v[80:81], v[80:81], v[174:175], v[194:195]
	v_pk_fma_f32 v[78:79], v[78:79], v[172:173], v[192:193]
	global_store_dwordx4 v[212:213], v[78:81], off offset:576
	v_pk_fma_f32 v[84:85], v[84:85], v[146:147], v[198:199]
	v_pk_fma_f32 v[82:83], v[82:83], v[144:145], v[196:197]
	global_store_dwordx4 v[214:215], v[82:85], off
	v_pk_fma_f32 v[76:77], v[76:77], v[156:157], v[202:203]
	v_pk_fma_f32 v[74:75], v[74:75], v[154:155], v[200:201]
	global_store_dwordx4 v[214:215], v[74:77], off offset:64
	v_pk_fma_f32 v[72:73], v[72:73], v[162:163], v[206:207]
	v_pk_fma_f32 v[70:71], v[70:71], v[160:161], v[204:205]
	global_store_dwordx4 v[214:215], v[70:73], off offset:512
	v_pk_fma_f32 v[68:69], v[68:69], v[174:175], v[210:211]
	v_pk_fma_f32 v[66:67], v[66:67], v[172:173], v[208:209]
	global_store_dwordx4 v[214:215], v[66:69], off offset:576
	v_add_co_u32_e32 v164, vcc, 0x100000, v166
	s_nop 1
	v_addc_co_u32_e32 v165, vcc, 0, v167, vcc
	global_load_dwordx4 v[176:179], v[164:165], off
	global_load_dwordx4 v[180:183], v[164:165], off offset:64
	global_load_dwordx4 v[184:187], v[164:165], off offset:512
	global_load_dwordx4 v[192:195], v[164:165], off offset:576
	v_add_co_u32_e32 v188, vcc, 0x120000, v166
	s_nop 1
	v_addc_co_u32_e32 v189, vcc, 0, v167, vcc
	global_load_dwordx4 v[196:199], v[188:189], off
	global_load_dwordx4 v[200:203], v[188:189], off offset:64
	global_load_dwordx4 v[204:207], v[188:189], off offset:512
	global_load_dwordx4 v[208:211], v[188:189], off offset:576
	v_add_co_u32_e32 v212, vcc, 0x100000, v170
	s_nop 1
	v_addc_co_u32_e32 v213, vcc, 0, v171, vcc
	v_add_co_u32_e32 v214, vcc, 0x120000, v170
	s_nop 1
	v_addc_co_u32_e32 v215, vcc, 0, v171, vcc
	s_waitcnt vmcnt(0)
	v_pk_fma_f32 v[64:65], v[64:65], v[146:147], v[178:179]
	v_pk_fma_f32 v[62:63], v[62:63], v[144:145], v[176:177]
	global_store_dwordx4 v[212:213], v[62:65], off
	v_pk_fma_f32 v[60:61], v[60:61], v[156:157], v[182:183]
	v_pk_fma_f32 v[58:59], v[58:59], v[154:155], v[180:181]
	global_store_dwordx4 v[212:213], v[58:61], off offset:64
	v_pk_fma_f32 v[56:57], v[56:57], v[162:163], v[186:187]
	v_pk_fma_f32 v[54:55], v[54:55], v[160:161], v[184:185]
	global_store_dwordx4 v[212:213], v[54:57], off offset:512
	v_pk_fma_f32 v[48:49], v[48:49], v[174:175], v[194:195]
	v_pk_fma_f32 v[46:47], v[46:47], v[172:173], v[192:193]
	global_store_dwordx4 v[212:213], v[46:49], off offset:576
	v_pk_fma_f32 v[52:53], v[52:53], v[146:147], v[198:199]
	v_pk_fma_f32 v[50:51], v[50:51], v[144:145], v[196:197]
	global_store_dwordx4 v[214:215], v[50:53], off
	v_pk_fma_f32 v[44:45], v[44:45], v[156:157], v[202:203]
	v_pk_fma_f32 v[42:43], v[42:43], v[154:155], v[200:201]
	global_store_dwordx4 v[214:215], v[42:45], off offset:64
	v_pk_fma_f32 v[40:41], v[40:41], v[162:163], v[206:207]
	v_pk_fma_f32 v[38:39], v[38:39], v[160:161], v[204:205]
	global_store_dwordx4 v[214:215], v[38:41], off offset:512
	v_pk_fma_f32 v[32:33], v[32:33], v[174:175], v[210:211]
	v_pk_fma_f32 v[30:31], v[30:31], v[172:173], v[208:209]
	global_store_dwordx4 v[214:215], v[30:33], off offset:576
	v_add_co_u32_e32 v164, vcc, 0x140000, v166
	s_nop 1
	v_addc_co_u32_e32 v165, vcc, 0, v167, vcc
	global_load_dwordx4 v[176:179], v[164:165], off
	global_load_dwordx4 v[180:183], v[164:165], off offset:64
	global_load_dwordx4 v[184:187], v[164:165], off offset:512
	global_load_dwordx4 v[192:195], v[164:165], off offset:576
	v_add_co_u32_e32 v188, vcc, 0x160000, v166
	s_nop 1
	v_addc_co_u32_e32 v189, vcc, 0, v167, vcc
	global_load_dwordx4 v[196:199], v[188:189], off
	global_load_dwordx4 v[200:203], v[188:189], off offset:64
	global_load_dwordx4 v[204:207], v[188:189], off offset:512
	global_load_dwordx4 v[208:211], v[188:189], off offset:576
	v_add_co_u32_e32 v212, vcc, 0x140000, v170
	s_nop 1
	v_addc_co_u32_e32 v213, vcc, 0, v171, vcc
	v_add_co_u32_e32 v214, vcc, 0x160000, v170
	s_nop 1
	v_addc_co_u32_e32 v215, vcc, 0, v171, vcc
	s_waitcnt vmcnt(0)
	v_pk_fma_f32 v[36:37], v[36:37], v[146:147], v[178:179]
	v_pk_fma_f32 v[34:35], v[34:35], v[144:145], v[176:177]
	global_store_dwordx4 v[212:213], v[34:37], off
	v_pk_fma_f32 v[28:29], v[28:29], v[156:157], v[182:183]
	v_pk_fma_f32 v[26:27], v[26:27], v[154:155], v[180:181]
	global_store_dwordx4 v[212:213], v[26:29], off offset:64
	v_pk_fma_f32 v[24:25], v[24:25], v[162:163], v[186:187]
	v_pk_fma_f32 v[22:23], v[22:23], v[160:161], v[184:185]
	global_store_dwordx4 v[212:213], v[22:25], off offset:512
	v_pk_fma_f32 v[16:17], v[16:17], v[174:175], v[194:195]
	v_pk_fma_f32 v[14:15], v[14:15], v[172:173], v[192:193]
	global_store_dwordx4 v[212:213], v[14:17], off offset:576
	v_pk_fma_f32 v[20:21], v[20:21], v[146:147], v[198:199]
	v_pk_fma_f32 v[18:19], v[18:19], v[144:145], v[196:197]
	global_store_dwordx4 v[214:215], v[18:21], off
	v_pk_fma_f32 v[12:13], v[12:13], v[156:157], v[202:203]
	v_pk_fma_f32 v[10:11], v[10:11], v[154:155], v[200:201]
	global_store_dwordx4 v[214:215], v[10:13], off offset:64
	v_pk_fma_f32 v[8:9], v[8:9], v[162:163], v[206:207]
	v_pk_fma_f32 v[6:7], v[6:7], v[160:161], v[204:205]
	global_store_dwordx4 v[214:215], v[6:9], off offset:512
	v_pk_fma_f32 v[4:5], v[4:5], v[174:175], v[210:211]
	v_pk_fma_f32 v[2:3], v[2:3], v[172:173], v[208:209]
	global_store_dwordx4 v[214:215], v[2:5], off offset:576
	s_mov_b32 s48, s12
	s_mov_b32 s20, s14
	s_mov_b64 s[24:25], s[18:19]
	s_mov_b64 s[22:23], s[16:17]
	v_readlane_b32 s50, v250, 9
	v_readlane_b32 s51, v250, 10
	v_readlane_b32 s54, v250, 13
	v_readlane_b32 s55, v250, 14
	v_readlane_b32 s56, v250, 15
	v_readlane_b32 s57, v250, 16
	v_readlane_b32 s58, v250, 17
	v_readlane_b32 s59, v250, 18
	v_readlane_b32 s60, v250, 19
	v_readlane_b32 s61, v250, 20
	v_readlane_b32 s62, v250, 21
	v_readlane_b32 s63, v250, 22
	s_and_b64 vcc, exec, s[0:1]
	s_cbranch_vccz .LBB0_1284
	s_waitcnt vmcnt(0)
	s_cmpk_gt_u32 s30, 0xff
	s_cbranch_scc1 .LBB0_1291
	s_barrier

.LBB0_1293:
	s_cmp_gt_i32 s55, 8
	s_cselect_b64 s[0:1], -1, 0
	s_and_b64 s[2:3], s[2:3], s[0:1]
	s_andn2_b64 vcc, exec, s[2:3]
	s_cbranch_vccnz .LBB0_1343
	s_waitcnt vmcnt(0)
	s_barrier
	s_setprio 0
	s_mov_b64 s[2:3], exec
	v_readlane_b32 s4, v250, 5
	v_readlane_b32 s5, v250, 6
	s_and_b64 s[4:5], s[2:3], s[4:5]
	s_mov_b64 exec, s[4:5]
	s_cbranch_execz .LBB0_1342
	s_add_i32 s4, 0, 0x27ff0
	v_mov_b32_e32 v1, s4
	s_waitcnt vmcnt(0) expcnt(0) lgkmcnt(0)
	ds_read_b32 v3, v1
	s_add_i32 s4, 0, 0x27ff4
	v_mov_b32_e32 v1, s4
	ds_read_b32 v1, v1
	s_waitcnt lgkmcnt(1)
	v_cmp_ne_u32_e32 vcc, 0, v3
	s_cbranch_vccnz .LBB0_1310
	v_readlane_b32 s4, v250, 2
	v_readlane_b32 s5, v250, 3
	s_load_dwordx2 s[8:9], s[4:5], 0x4
	s_add_u32 s4, s52, 0x1000
	s_addc_u32 s5, s53, 0
	s_add_u32 s6, s52, 0x1100
	s_addc_u32 s7, s53, 0
	v_readlane_b32 s10, v250, 1
	s_waitcnt lgkmcnt(0)
	s_mul_i32 s18, s8, s10
	s_add_u32 s8, s52, 0x1200
	s_mul_i32 s18, s18, s9
	s_addc_u32 s9, s53, 0
	s_add_u32 s10, s52, 0x1300
	s_addc_u32 s11, s53, 0
	s_mov_b32 s19, 1
	v_mov_b32_e32 v17, 0
	s_branch .LBB0_1298

.LBB0_1369:
	s_cmp_gt_i32 s55, 9
	s_cselect_b64 s[0:1], -1, 0
	s_and_b64 s[2:3], s[38:39], s[0:1]
	s_andn2_b64 vcc, exec, s[2:3]
	s_cbranch_vccnz .LBB0_1419
	s_waitcnt vmcnt(0)
	s_barrier
	s_setprio 0
	s_mov_b64 s[2:3], exec
	v_readlane_b32 s4, v250, 5
	v_readlane_b32 s5, v250, 6
	s_and_b64 s[4:5], s[2:3], s[4:5]
	s_mov_b64 exec, s[4:5]
	s_cbranch_execz .LBB0_1418
	s_add_i32 s4, 0, 0x27ff0
	v_mov_b32_e32 v1, s4
	s_waitcnt vmcnt(0) expcnt(0) lgkmcnt(0)
	ds_read_b32 v3, v1
	s_add_i32 s4, 0, 0x27ff4
	v_mov_b32_e32 v1, s4
	ds_read_b32 v1, v1
	s_waitcnt lgkmcnt(1)
	v_cmp_ne_u32_e32 vcc, 0, v3
	s_cbranch_vccnz .LBB0_1386
	v_readlane_b32 s4, v250, 2
	v_readlane_b32 s5, v250, 3
	s_load_dwordx2 s[8:9], s[4:5], 0x4
	s_add_u32 s4, s52, 0x1000
	s_addc_u32 s5, s53, 0
	s_add_u32 s6, s52, 0x1100
	s_addc_u32 s7, s53, 0
	v_readlane_b32 s10, v250, 1
	s_waitcnt lgkmcnt(0)
	s_mul_i32 s18, s8, s10
	s_add_u32 s8, s52, 0x1200
	s_mul_i32 s18, s18, s9
	s_addc_u32 s9, s53, 0
	s_add_u32 s10, s52, 0x1300
	s_addc_u32 s11, s53, 0
	s_mov_b32 s19, 1
	v_mov_b32_e32 v17, 0
	s_branch .LBB0_1374

.LBB0_2015:
	s_cmp_gt_i32 s55, 10
	s_cselect_b64 s[0:1], -1, 0
	s_and_b64 s[2:3], s[2:3], s[0:1]
	s_andn2_b64 vcc, exec, s[2:3]
	s_cbranch_vccnz .LBB0_2065
	s_waitcnt vmcnt(0)
	s_barrier
	s_setprio 0
	s_mov_b64 s[2:3], exec
	v_readlane_b32 s4, v250, 5
	v_readlane_b32 s5, v250, 6
	s_and_b64 s[4:5], s[2:3], s[4:5]
	s_mov_b64 exec, s[4:5]
	s_cbranch_execz .LBB0_2064
	s_add_i32 s4, 0, 0x27ff0
	v_mov_b32_e32 v1, s4
	s_waitcnt vmcnt(0) expcnt(0) lgkmcnt(0)
	ds_read_b32 v3, v1
	s_add_i32 s4, 0, 0x27ff4
	v_mov_b32_e32 v1, s4
	ds_read_b32 v1, v1
	s_waitcnt lgkmcnt(1)
	v_cmp_ne_u32_e32 vcc, 0, v3
	s_cbranch_vccnz .LBB0_2032
	v_readlane_b32 s4, v250, 2
	v_readlane_b32 s5, v250, 3
	s_load_dwordx2 s[8:9], s[4:5], 0x4
	s_add_u32 s4, s52, 0x1000
	s_addc_u32 s5, s53, 0
	s_add_u32 s6, s52, 0x1100
	s_addc_u32 s7, s53, 0
	v_readlane_b32 s10, v250, 1
	s_waitcnt lgkmcnt(0)
	s_mul_i32 s18, s8, s10
	s_add_u32 s8, s52, 0x1200
	s_mul_i32 s18, s18, s9
	s_addc_u32 s9, s53, 0
	s_add_u32 s10, s52, 0x1300
	s_addc_u32 s11, s53, 0
	s_mov_b32 s19, 1
	v_mov_b32_e32 v17, 0
	s_branch .LBB0_2020

.LBB0_2065:
	s_cmp_lt_i32 s54, 11
	s_cselect_b64 s[6:7], -1, 0
	s_and_b64 s[0:1], s[6:7], s[0:1]
	s_andn2_b64 vcc, exec, s[0:1]
	s_cbranch_vccnz .LBB0_2083
	v_mov_b32_e32 v1, v248
	s_waitcnt vmcnt(11)
	v_mov_b32_e32 v2, v0
	v_readlane_b32 s26, v250, 1
	v_readlane_b32 s27, v250, 0
	v_readlane_b32 s0, v250, 39
	s_mov_b64 s[0:1], s[52:53]
	s_mov_b64 s[2:3], s[90:91]
	s_cmpk_gt_i32 s27, 0x47f
	v_readfirstlane_b32 s28, v0
	s_barrier
	s_cbranch_scc1 .LBB0_2082
	s_add_u32 s8, s0, 0x2ec40000
	s_addc_u32 s9, s1, 0
	s_add_u32 s29, s0, 0x16940000
	s_addc_u32 s30, s1, 0
	s_add_u32 s10, s0, 0x1674000
	s_addc_u32 s11, s1, 0
	s_ashr_i32 s33, s27, 31
	s_lshr_b32 s5, s33, 29
	s_add_i32 s5, s27, s5
	s_lshr_b32 s4, s28, 6
	s_ashr_i32 s12, s5, 3
	s_and_b32 s5, s5, -8
	s_lshr_b32 s3, s28, 8
	s_lshl_b32 s31, s4, 10
	s_sub_i32 s5, s27, s5
	s_cmp_lt_i32 s5, 0
	s_movk_i32 s34, 0x91
	s_cselect_b32 s13, s34, 0x90
	s_mul_i32 s5, s13, s5
	s_add_i32 s5, s5, s12
	s_ashr_i32 s12, s5, 31
	s_lshr_b32 s12, s12, 26
	s_add_i32 s12, s5, s12
	s_ashr_i32 s13, s12, 6
	s_lshl_b32 s14, s13, 3
	s_sub_i32 s13, 0x90, s14
	s_min_u32 s15, s13, 8
	s_andn2_b32 s12, s12, 63
	s_sub_i32 s5, s5, s12
	v_cvt_f32_ubyte0_e32 v5, s15
	v_cvt_f32_i32_e32 v4, s5
	s_waitcnt vmcnt(10)
	v_rcp_iflag_f32_e32 v6, v5
	v_bfe_u32 v2, v0, 2, 4
	v_lshrrev_b32_e32 v3, 3, v0
	v_and_or_b32 v1, v3, 48, v2
	v_or_b32_e32 v3, 64, v3
	s_movk_i32 s2, 0x70
	v_and_or_b32 v150, v3, s2, v2
	v_mul_f32_e32 v2, v4, v6
	v_trunc_f32_e32 v2, v2
	v_fma_f32 v3, -v2, v5, v4
	v_cvt_i32_f32_e32 v2, v2
	s_ashr_i32 s2, s5, 30
	s_or_b32 s2, s2, 1
	v_cmp_ge_f32_e64 s[12:13], |v3|, v5
	s_and_b64 s[12:13], s[12:13], exec
	s_cselect_b32 s2, s2, 0
	v_readfirstlane_b32 s12, v2
	s_add_i32 s2, s12, s2
	s_mul_i32 s12, s2, s15
	s_sub_i32 s5, s5, s12
	s_sext_i32_i8 s5, s5
	s_add_i32 s46, s14, s5
	s_mul_hi_i32 s5, s46, 0x38e38e39
	s_lshr_b32 s12, s5, 31
	s_ashr_i32 s5, s5, 1
	s_add_i32 s12, s5, s12
	s_mul_i32 s5, s12, -9
	s_add_i32 s5, s5, s46
	s_mul_i32 s13, s12, 0x900
	s_lshl_b32 s5, s5, 8
	s_add_i32 s5, s5, s13
	v_or_b32_e32 v2, s5, v1
	v_or_b32_e32 v4, s5, v150
	s_bitset1_b32 s5, 7
	v_ashrrev_i32_e32 v3, 31, v2
	v_ashrrev_i32_e32 v5, 31, v4
	v_or_b32_e32 v6, s5, v1
	v_or_b32_e32 v8, s5, v150
	v_lshl_add_u64 v[2:3], v[2:3], 2, s[10:11]
	v_lshl_add_u64 v[4:5], v[4:5], 2, s[10:11]
	v_ashrrev_i32_e32 v7, 31, v6
	v_ashrrev_i32_e32 v9, 31, v8
	v_lshl_add_u64 v[6:7], v[6:7], 2, s[10:11]
	v_lshl_add_u64 v[8:9], v[8:9], 2, s[10:11]
	global_load_dword v2, v[2:3], off
	s_nop 0
	global_load_dword v3, v[4:5], off
	s_nop 0
	global_load_dword v4, v[6:7], off
	global_load_dword v5, v[8:9], off
	s_bfe_i64 s[14:15], s[2:3], 0x80000
	s_ashr_i32 s13, s12, 31
	s_lshl_b64 s[14:15], s[14:15], 20
	s_lshl_b64 s[12:13], s[12:13], 23
	s_add_u32 s5, s29, s12
	v_lshlrev_b32_e32 v6, 4, v0
	v_and_b32_e32 v7, 32, v0
	s_addc_u32 s12, s30, s13
	v_bitop3_b32 v6, v6, v7, 48 bitop3:0x6c
	s_add_u32 s20, s5, s14
	v_and_or_b32 v151, v0, 64, v6
	s_addc_u32 s21, s12, s15
	s_add_i32 s35, s31, 0
	v_lshl_or_b32 v132, v1, 12, v151
	s_add_i32 m0, s35, 0x10000
	v_lshl_or_b32 v130, v150, 12, v151
	global_load_lds_dwordx4 v132, s[20:21]
	s_add_i32 m0, s35, 0x12000
	s_add_i32 s36, s35, 0x2000
	global_load_lds_dwordx4 v130, s[20:21]
	s_mov_b32 m0, s35
	s_add_u32 s12, s20, 0x80000
	s_addc_u32 s13, s21, 0
	s_add_i32 s37, s35, 0x4000
	s_add_i32 s38, s35, 0x6000
	v_mov_b32_e32 v135, 0
	v_mov_b32_e32 v133, v135
	v_mov_b32_e32 v131, v135
	s_mov_b32 s39, 0
	v_mov_b32_e32 v141, v135
	s_waitcnt vmcnt(0)
	v_lshl_or_b32 v134, v2, 12, v151
	v_lshl_or_b32 v140, v3, 12, v151
	global_load_lds_dwordx4 v134, s[8:9]
	s_mov_b32 m0, s36
	v_lshl_or_b32 v142, v4, 12, v151
	global_load_lds_dwordx4 v140, s[8:9]
	s_add_i32 m0, s35, 0x14000
	v_lshl_or_b32 v144, v5, 12, v151
	global_load_lds_dwordx4 v132, s[12:13]
	s_add_i32 m0, s35, 0x16000
	v_lshl_add_u64 v[4:5], s[20:21], 0, v[132:133]
	global_load_lds_dwordx4 v130, s[12:13]
	s_mov_b32 m0, s37
	v_lshl_add_u64 v[2:3], s[20:21], 0, v[130:131]
	global_load_lds_dwordx4 v142, s[8:9]
	s_mov_b32 m0, s38
	s_setprio 1
	s_cmp_lg_u32 s3, 1
	global_load_lds_dwordx4 v144, s[8:9]
	s_cbranch_scc1 .LBB0_2069
	s_barrier
	s_setprio 0

.LBB0_2077:
	s_add_u32 s20, s4, 0x100
	s_addc_u32 s21, s5, 0
	s_add_u32 s24, s19, s4
	ds_read_b128 v[162:165], v155
	ds_read_b128 v[166:169], v155 offset:1024
	ds_read_b128 v[170:173], v155 offset:2048
	ds_read_b128 v[174:177], v155 offset:3072
	s_addc_u32 s25, s48, s5
	s_cmpk_eq_i32 s4, 0xf00
	s_cselect_b64 vcc, -1, 0
	s_and_b64 s[22:23], vcc, exec
	s_cselect_b32 s51, 0, s20
	s_cselect_b32 s50, 0, s21
	s_cselect_b32 s22, s2, s24
	s_cselect_b32 s23, s3, s25
	s_add_u32 s24, s8, s51
	v_cndmask_b32_e32 v134, v141, v158, vcc
	v_cndmask_b32_e32 v226, v140, v159, vcc
	v_cndmask_b32_e32 v143, v142, v160, vcc
	v_cndmask_b32_e32 v145, v144, v161, vcc
	s_addc_u32 s25, s9, s50
	v_lshl_add_u64 v[210:211], v[146:147], 0, s[4:5]
	s_add_i32 m0, s35, 0xc000
	ds_read_b128 v[178:181], v156
	ds_read_b128 v[182:185], v156 offset:1024
	ds_read_b128 v[186:189], v156 offset:2048
	ds_read_b128 v[190:193], v156 offset:3072
	ds_read_b128 v[194:197], v156 offset:4096
	ds_read_b128 v[198:201], v156 offset:5120
	ds_read_b128 v[202:205], v156 offset:6144
	ds_read_b128 v[206:209], v156 offset:7168
	global_load_lds_dwordx4 v[210:211], off
	v_lshl_add_u64 v[210:211], v[148:149], 0, s[4:5]
	s_add_i32 m0, s35, 0xe000
	s_nop 0
	global_load_lds_dwordx4 v[210:211], off
	s_waitcnt lgkmcnt(8)
	s_barrier
	s_waitcnt lgkmcnt(0)
	s_waitcnt lgkmcnt(0)
	v_mfma_f32_16x16x32_bf16 v[126:129], v[162:165], v[178:181], v[126:129]
	v_mfma_f32_16x16x32_bf16 v[122:125], v[170:173], v[178:181], v[122:125]
	v_mfma_f32_16x16x32_bf16 v[110:113], v[162:165], v[186:189], v[110:113]
	v_mfma_f32_16x16x32_bf16 v[106:109], v[170:173], v[186:189], v[106:109]
	v_mfma_f32_16x16x32_bf16 v[94:97], v[162:165], v[194:197], v[94:97]
	v_mfma_f32_16x16x32_bf16 v[90:93], v[170:173], v[194:197], v[90:93]
	v_mfma_f32_16x16x32_bf16 v[78:81], v[162:165], v[202:205], v[78:81]
	v_mfma_f32_16x16x32_bf16 v[74:77], v[170:173], v[202:205], v[74:77]
	v_mfma_f32_16x16x32_bf16 v[126:129], v[166:169], v[182:185], v[126:129]
	v_mfma_f32_16x16x32_bf16 v[122:125], v[174:177], v[182:185], v[122:125]
	v_mfma_f32_16x16x32_bf16 v[110:113], v[166:169], v[190:193], v[110:113]
	v_mfma_f32_16x16x32_bf16 v[106:109], v[174:177], v[190:193], v[106:109]
	v_mfma_f32_16x16x32_bf16 v[94:97], v[166:169], v[198:201], v[94:97]
	v_mfma_f32_16x16x32_bf16 v[90:93], v[174:177], v[198:201], v[90:93]
	v_mfma_f32_16x16x32_bf16 v[78:81], v[166:169], v[206:209], v[78:81]
	v_mfma_f32_16x16x32_bf16 v[74:77], v[174:177], v[206:209], v[74:77]
	s_barrier
	s_add_i32 s4, s43, s31
	v_lshl_add_u64 v[228:229], s[22:23], 0, v[132:133]
	s_mov_b32 m0, s4
	ds_read_b128 v[210:213], v157
	ds_read_b128 v[214:217], v157 offset:1024
	ds_read_b128 v[218:221], v157 offset:2048
	ds_read_b128 v[222:225], v157 offset:3072
	global_load_lds_dwordx4 v[228:229], off
	v_lshl_add_u64 v[230:231], s[22:23], 0, v[130:131]
	s_add_i32 m0, s4, 0x2000
	s_nop 0
	global_load_lds_dwordx4 v[230:231], off
	s_barrier
	s_waitcnt lgkmcnt(0)
	s_waitcnt lgkmcnt(0)
	v_mfma_f32_16x16x32_bf16 v[118:121], v[210:213], v[178:181], v[118:121]
	v_mfma_f32_16x16x32_bf16 v[114:117], v[218:221], v[178:181], v[114:117]
	v_mfma_f32_16x16x32_bf16 v[102:105], v[210:213], v[186:189], v[102:105]
	v_mfma_f32_16x16x32_bf16 v[98:101], v[218:221], v[186:189], v[98:101]
	v_mfma_f32_16x16x32_bf16 v[86:89], v[210:213], v[194:197], v[86:89]
	v_mfma_f32_16x16x32_bf16 v[82:85], v[218:221], v[194:197], v[82:85]
	v_mfma_f32_16x16x32_bf16 v[70:73], v[210:213], v[202:205], v[70:73]
	v_mfma_f32_16x16x32_bf16 v[66:69], v[218:221], v[202:205], v[66:69]
	v_mfma_f32_16x16x32_bf16 v[118:121], v[214:217], v[182:185], v[118:121]
	v_mfma_f32_16x16x32_bf16 v[114:117], v[222:225], v[182:185], v[114:117]
	v_mfma_f32_16x16x32_bf16 v[102:105], v[214:217], v[190:193], v[102:105]
	v_mfma_f32_16x16x32_bf16 v[98:101], v[222:225], v[190:193], v[98:101]
	v_mfma_f32_16x16x32_bf16 v[86:89], v[214:217], v[198:201], v[86:89]
	v_mfma_f32_16x16x32_bf16 v[82:85], v[222:225], v[198:201], v[82:85]
	v_mfma_f32_16x16x32_bf16 v[70:73], v[214:217], v[206:209], v[70:73]
	v_mfma_f32_16x16x32_bf16 v[66:69], v[222:225], v[206:209], v[66:69]
	s_mov_b32 m0, s35
	s_barrier
	ds_read_b128 v[178:181], v156 offset:16384
	ds_read_b128 v[182:185], v156 offset:17408
	ds_read_b128 v[186:189], v156 offset:18432
	ds_read_b128 v[190:193], v156 offset:19456
	ds_read_b128 v[194:197], v156 offset:20480
	ds_read_b128 v[198:201], v156 offset:21504
	ds_read_b128 v[202:205], v156 offset:22528
	ds_read_b128 v[206:209], v156 offset:23552
	global_load_lds_dwordx4 v134, s[24:25]
	s_mov_b32 m0, s36
	v_mov_b32_e32 v227, v135
	global_load_lds_dwordx4 v226, s[24:25]
	s_barrier
	s_waitcnt lgkmcnt(0)
	v_lshl_add_u64 v[232:233], s[24:25], 0, v[134:135]
	v_lshl_add_u64 v[226:227], s[24:25], 0, v[226:227]
	s_waitcnt lgkmcnt(0)
	v_mfma_f32_16x16x32_bf16 v[62:65], v[162:165], v[178:181], v[62:65]
	v_mfma_f32_16x16x32_bf16 v[58:61], v[170:173], v[178:181], v[58:61]
	v_mfma_f32_16x16x32_bf16 v[46:49], v[162:165], v[186:189], v[46:49]
	v_mfma_f32_16x16x32_bf16 v[42:45], v[170:173], v[186:189], v[42:45]
	v_mfma_f32_16x16x32_bf16 v[30:33], v[162:165], v[194:197], v[30:33]
	v_mfma_f32_16x16x32_bf16 v[26:29], v[170:173], v[194:197], v[26:29]
	v_mfma_f32_16x16x32_bf16 v[14:17], v[162:165], v[202:205], v[14:17]
	v_mfma_f32_16x16x32_bf16 v[10:13], v[170:173], v[202:205], v[10:13]
	v_mfma_f32_16x16x32_bf16 v[62:65], v[166:169], v[182:185], v[62:65]
	v_mfma_f32_16x16x32_bf16 v[58:61], v[174:177], v[182:185], v[58:61]
	v_mfma_f32_16x16x32_bf16 v[46:49], v[166:169], v[190:193], v[46:49]
	v_mfma_f32_16x16x32_bf16 v[42:45], v[174:177], v[190:193], v[42:45]
	v_mfma_f32_16x16x32_bf16 v[30:33], v[166:169], v[198:201], v[30:33]
	v_mfma_f32_16x16x32_bf16 v[26:29], v[174:177], v[198:201], v[26:29]
	v_mfma_f32_16x16x32_bf16 v[14:17], v[166:169], v[206:209], v[14:17]
	v_mfma_f32_16x16x32_bf16 v[10:13], v[174:177], v[206:209], v[10:13]
	s_barrier
	s_add_u32 s4, s22, 0x80000
	s_addc_u32 s5, s23, 0
	s_add_i32 s50, s44, s31
	v_lshl_add_u64 v[162:163], s[4:5], 0, v[132:133]
	s_mov_b32 m0, s50
	s_nop 0
	global_load_lds_dwordx4 v[162:163], off
	v_lshl_add_u64 v[162:163], s[4:5], 0, v[130:131]
	s_add_i32 m0, s50, 0x2000
	s_nop 0
	global_load_lds_dwordx4 v[162:163], off
	s_waitcnt vmcnt(6)
	s_barrier
	v_mfma_f32_16x16x32_bf16 v[54:57], v[210:213], v[178:181], v[54:57]
	v_mfma_f32_16x16x32_bf16 v[50:53], v[218:221], v[178:181], v[50:53]
	v_mfma_f32_16x16x32_bf16 v[38:41], v[210:213], v[186:189], v[38:41]
	v_mfma_f32_16x16x32_bf16 v[34:37], v[218:221], v[186:189], v[34:37]
	v_mfma_f32_16x16x32_bf16 v[22:25], v[210:213], v[194:197], v[22:25]
	v_mfma_f32_16x16x32_bf16 v[18:21], v[218:221], v[194:197], v[18:21]
	v_mfma_f32_16x16x32_bf16 v[6:9], v[210:213], v[202:205], v[6:9]
	v_mfma_f32_16x16x32_bf16 v[2:5], v[218:221], v[202:205], v[2:5]
	v_mfma_f32_16x16x32_bf16 v[54:57], v[214:217], v[182:185], v[54:57]
	v_mfma_f32_16x16x32_bf16 v[50:53], v[222:225], v[182:185], v[50:53]
	v_mfma_f32_16x16x32_bf16 v[38:41], v[214:217], v[190:193], v[38:41]
	v_mfma_f32_16x16x32_bf16 v[34:37], v[222:225], v[190:193], v[34:37]
	v_mfma_f32_16x16x32_bf16 v[22:25], v[214:217], v[198:201], v[22:25]
	v_mfma_f32_16x16x32_bf16 v[18:21], v[222:225], v[198:201], v[18:21]
	v_mfma_f32_16x16x32_bf16 v[6:9], v[214:217], v[206:209], v[6:9]
	v_mfma_f32_16x16x32_bf16 v[2:5], v[222:225], v[206:209], v[2:5]
	s_add_i32 s4, 0, 0x18000
	v_add_u32_e32 v134, s4, v153
	s_barrier
	ds_read_b128 v[162:165], v134
	ds_read_b128 v[166:169], v134 offset:1024
	ds_read_b128 v[170:173], v134 offset:2048
	ds_read_b128 v[174:177], v134 offset:3072
	s_mov_b32 m0, s37
	ds_read_b128 v[178:181], v156 offset:32768
	ds_read_b128 v[182:185], v156 offset:33792
	ds_read_b128 v[186:189], v156 offset:34816
	ds_read_b128 v[190:193], v156 offset:35840
	ds_read_b128 v[194:197], v156 offset:36864
	ds_read_b128 v[198:201], v156 offset:37888
	ds_read_b128 v[202:205], v156 offset:38912
	ds_read_b128 v[206:209], v156 offset:39936
	global_load_lds_dwordx4 v143, s[24:25]
	s_mov_b32 m0, s38
	s_nop 0
	global_load_lds_dwordx4 v145, s[24:25]
	s_waitcnt lgkmcnt(8)
	s_barrier
	s_waitcnt lgkmcnt(0)
	s_waitcnt lgkmcnt(0)
	v_mfma_f32_16x16x32_bf16 v[126:129], v[162:165], v[178:181], v[126:129]
	v_mfma_f32_16x16x32_bf16 v[122:125], v[170:173], v[178:181], v[122:125]
	v_mfma_f32_16x16x32_bf16 v[110:113], v[162:165], v[186:189], v[110:113]
	v_mfma_f32_16x16x32_bf16 v[106:109], v[170:173], v[186:189], v[106:109]
	v_mfma_f32_16x16x32_bf16 v[94:97], v[162:165], v[194:197], v[94:97]
	v_mfma_f32_16x16x32_bf16 v[90:93], v[170:173], v[194:197], v[90:93]
	v_mfma_f32_16x16x32_bf16 v[78:81], v[162:165], v[202:205], v[78:81]
	v_mfma_f32_16x16x32_bf16 v[74:77], v[170:173], v[202:205], v[74:77]
	v_mfma_f32_16x16x32_bf16 v[126:129], v[166:169], v[182:185], v[126:129]
	v_mfma_f32_16x16x32_bf16 v[122:125], v[174:177], v[182:185], v[122:125]
	v_mfma_f32_16x16x32_bf16 v[110:113], v[166:169], v[190:193], v[110:113]
	v_mfma_f32_16x16x32_bf16 v[106:109], v[174:177], v[190:193], v[106:109]
	v_mfma_f32_16x16x32_bf16 v[94:97], v[166:169], v[198:201], v[94:97]
	v_mfma_f32_16x16x32_bf16 v[90:93], v[174:177], v[198:201], v[90:93]
	v_mfma_f32_16x16x32_bf16 v[78:81], v[166:169], v[206:209], v[78:81]
	v_mfma_f32_16x16x32_bf16 v[74:77], v[174:177], v[206:209], v[74:77]
	s_barrier
	s_add_i32 s24, 0, 0x1c000
	s_add_i32 s4, s4, s31
	v_add_u32_e32 v134, s24, v153
	v_lshl_add_u64 v[228:229], v[228:229], 0, s[14:15]
	s_mov_b32 m0, s4
	ds_read_b128 v[210:213], v134
	ds_read_b128 v[214:217], v134 offset:1024
	ds_read_b128 v[218:221], v134 offset:2048
	ds_read_b128 v[222:225], v134 offset:3072
	global_load_lds_dwordx4 v[228:229], off
	v_lshl_add_u64 v[228:229], v[230:231], 0, s[14:15]
	s_add_i32 m0, s4, 0x2000
	s_nop 0
	global_load_lds_dwordx4 v[228:229], off
	s_barrier
	s_waitcnt lgkmcnt(0)
	s_waitcnt lgkmcnt(0)
	v_mfma_f32_16x16x32_bf16 v[118:121], v[210:213], v[178:181], v[118:121]
	v_mfma_f32_16x16x32_bf16 v[114:117], v[218:221], v[178:181], v[114:117]
	v_mfma_f32_16x16x32_bf16 v[102:105], v[210:213], v[186:189], v[102:105]
	v_mfma_f32_16x16x32_bf16 v[98:101], v[218:221], v[186:189], v[98:101]
	v_mfma_f32_16x16x32_bf16 v[86:89], v[210:213], v[194:197], v[86:89]
	v_mfma_f32_16x16x32_bf16 v[82:85], v[218:221], v[194:197], v[82:85]
	v_mfma_f32_16x16x32_bf16 v[70:73], v[210:213], v[202:205], v[70:73]
	v_mfma_f32_16x16x32_bf16 v[66:69], v[218:221], v[202:205], v[66:69]
	v_mfma_f32_16x16x32_bf16 v[118:121], v[214:217], v[182:185], v[118:121]
	v_mfma_f32_16x16x32_bf16 v[114:117], v[222:225], v[182:185], v[114:117]
	v_mfma_f32_16x16x32_bf16 v[102:105], v[214:217], v[190:193], v[102:105]
	v_mfma_f32_16x16x32_bf16 v[98:101], v[222:225], v[190:193], v[98:101]
	v_mfma_f32_16x16x32_bf16 v[86:89], v[214:217], v[198:201], v[86:89]
	v_mfma_f32_16x16x32_bf16 v[82:85], v[222:225], v[198:201], v[82:85]
	v_mfma_f32_16x16x32_bf16 v[70:73], v[214:217], v[206:209], v[70:73]
	v_mfma_f32_16x16x32_bf16 v[66:69], v[222:225], v[206:209], v[66:69]
	s_mov_b32 m0, s40
	v_lshl_add_u64 v[228:229], v[232:233], 0, s[14:15]
	s_barrier
	ds_read_b128 v[178:181], v156 offset:49152
	ds_read_b128 v[182:185], v156 offset:50176
	ds_read_b128 v[186:189], v156 offset:51200
	ds_read_b128 v[190:193], v156 offset:52224
	ds_read_b128 v[194:197], v156 offset:53248
	ds_read_b128 v[198:201], v156 offset:54272
	ds_read_b128 v[202:205], v156 offset:55296
	ds_read_b128 v[206:209], v156 offset:56320
	global_load_lds_dwordx4 v[228:229], off
	v_lshl_add_u64 v[226:227], v[226:227], 0, s[14:15]
	s_mov_b32 m0, s41
	s_nop 0
	global_load_lds_dwordx4 v[226:227], off
	s_barrier
	s_waitcnt lgkmcnt(0)
	s_waitcnt lgkmcnt(0)
	v_mfma_f32_16x16x32_bf16 v[62:65], v[162:165], v[178:181], v[62:65]
	v_mfma_f32_16x16x32_bf16 v[58:61], v[170:173], v[178:181], v[58:61]
	v_mfma_f32_16x16x32_bf16 v[46:49], v[162:165], v[186:189], v[46:49]
	v_mfma_f32_16x16x32_bf16 v[42:45], v[170:173], v[186:189], v[42:45]
	v_mfma_f32_16x16x32_bf16 v[30:33], v[162:165], v[194:197], v[30:33]
	v_mfma_f32_16x16x32_bf16 v[26:29], v[170:173], v[194:197], v[26:29]
	v_mfma_f32_16x16x32_bf16 v[14:17], v[162:165], v[202:205], v[14:17]
	v_mfma_f32_16x16x32_bf16 v[10:13], v[170:173], v[202:205], v[10:13]
	v_mfma_f32_16x16x32_bf16 v[62:65], v[166:169], v[182:185], v[62:65]
	v_mfma_f32_16x16x32_bf16 v[58:61], v[174:177], v[182:185], v[58:61]
	v_mfma_f32_16x16x32_bf16 v[46:49], v[166:169], v[190:193], v[46:49]
	v_mfma_f32_16x16x32_bf16 v[42:45], v[174:177], v[190:193], v[42:45]
	v_mfma_f32_16x16x32_bf16 v[30:33], v[166:169], v[198:201], v[30:33]
	v_mfma_f32_16x16x32_bf16 v[26:29], v[174:177], v[198:201], v[26:29]
	v_mfma_f32_16x16x32_bf16 v[14:17], v[166:169], v[206:209], v[14:17]
	v_mfma_f32_16x16x32_bf16 v[10:13], v[174:177], v[206:209], v[10:13]
	s_barrier
	s_add_u32 s4, s22, 0x80080
	s_addc_u32 s5, s23, 0
	s_add_i32 s22, s24, s31
	v_lshl_add_u64 v[162:163], s[4:5], 0, v[132:133]
	s_mov_b32 m0, s22
	s_nop 0
	global_load_lds_dwordx4 v[162:163], off
	v_lshl_add_u64 v[162:163], s[4:5], 0, v[130:131]
	s_add_i32 m0, s22, 0x2000
	s_nop 0
	global_load_lds_dwordx4 v[162:163], off
	s_waitcnt vmcnt(6)
	s_barrier
	v_mfma_f32_16x16x32_bf16 v[54:57], v[210:213], v[178:181], v[54:57]
	v_mfma_f32_16x16x32_bf16 v[50:53], v[218:221], v[178:181], v[50:53]
	v_mfma_f32_16x16x32_bf16 v[38:41], v[210:213], v[186:189], v[38:41]
	v_mfma_f32_16x16x32_bf16 v[34:37], v[218:221], v[186:189], v[34:37]
	v_mfma_f32_16x16x32_bf16 v[22:25], v[210:213], v[194:197], v[22:25]
	v_mfma_f32_16x16x32_bf16 v[18:21], v[218:221], v[194:197], v[18:21]
	v_mfma_f32_16x16x32_bf16 v[6:9], v[210:213], v[202:205], v[6:9]
	v_mfma_f32_16x16x32_bf16 v[2:5], v[218:221], v[202:205], v[2:5]
	v_mfma_f32_16x16x32_bf16 v[54:57], v[214:217], v[182:185], v[54:57]
	v_mfma_f32_16x16x32_bf16 v[50:53], v[222:225], v[182:185], v[50:53]
	v_mfma_f32_16x16x32_bf16 v[38:41], v[214:217], v[190:193], v[38:41]
	v_mfma_f32_16x16x32_bf16 v[34:37], v[222:225], v[190:193], v[34:37]
	v_mfma_f32_16x16x32_bf16 v[22:25], v[214:217], v[198:201], v[22:25]
	v_mfma_f32_16x16x32_bf16 v[18:21], v[222:225], v[198:201], v[18:21]
	v_mfma_f32_16x16x32_bf16 v[6:9], v[214:217], v[206:209], v[6:9]
	v_mfma_f32_16x16x32_bf16 v[2:5], v[222:225], v[206:209], v[2:5]
	s_add_i32 s49, s49, 2
	s_cmp_gt_u32 s49, 29
	s_mov_b64 s[4:5], s[20:21]
	s_barrier
	s_cbranch_scc0 .LBB0_2077
	s_mul_hi_i32 s4, s46, 0x38e38e39
	s_lshr_b32 s5, s4, 31
	s_ashr_i32 s4, s4, 1
	s_add_i32 s4, s4, s5
	s_mul_i32 s5, s4, -9
	s_add_i32 s5, s5, s46
	v_mul_f32_e32 v134, 0xbfb8aa3b, v126
	s_mulk_i32 s4, 0x900
	s_lshl_b32 s5, s5, 8
	v_exp_f32_e32 v134, v134
	s_add_i32 s5, s5, s4
	v_add_u32_e32 v144, s5, v152
	v_lshl_or_b32 v140, s47, 7, v154
	v_ashrrev_i32_e32 v145, 31, v144
	v_ashrrev_i32_e32 v141, 31, v140
	v_lshlrev_b64 v[142:143], 11, v[144:145]
	v_add_f32_e32 v134, 1.0, v134
	v_lshl_add_u64 v[146:147], s[12:13], 0, v[142:143]
	v_lshlrev_b64 v[142:143], 1, v[140:141]
	v_rcp_f32_e32 v134, v134
	v_mul_f32_e32 v140, 0xbfb8aa3b, v127
	v_exp_f32_e32 v145, v140
	v_lshl_add_u64 v[140:141], v[146:147], 0, v[142:143]
	v_mul_f32_e32 v126, v126, v134
	v_mul_f32_e32 v122, v122, v126
	v_add_f32_e32 v126, 1.0, v145
	v_mul_f32_e32 v134, 0xbfb8aa3b, v128
	v_rcp_f32_e32 v126, v126
	v_exp_f32_e32 v134, v134
	v_mul_f32_e32 v145, 0xbfb8aa3b, v129
	v_exp_f32_e32 v145, v145
	v_mul_f32_e32 v126, v127, v126
	v_add_f32_e32 v127, 1.0, v134
	v_rcp_f32_e32 v127, v127
	v_add_f32_e32 v134, 1.0, v145
	v_rcp_f32_e32 v134, v134
	v_mul_f32_e32 v123, v123, v126
	v_mul_f32_e32 v126, v128, v127
	v_mul_f32_e32 v127, 0xbfb8aa3b, v118
	v_exp_f32_e32 v127, v127
	v_mul_f32_e32 v124, v124, v126
	v_mul_f32_e32 v126, v129, v134
	v_mul_f32_e32 v125, v125, v126
	v_cvt_pk_bf16_f32 v122, v122, v123
	v_cvt_pk_bf16_f32 v123, v124, v125
	v_add_f32_e32 v124, 1.0, v127
	v_rcp_f32_e32 v124, v124
	v_mul_f32_e32 v125, 0xbfb8aa3b, v119
	v_exp_f32_e32 v125, v125
	global_store_dwordx2 v[140:141], v[122:123], off
	v_mul_f32_e32 v118, v118, v124
	v_mul_f32_e32 v114, v114, v118
	v_add_f32_e32 v118, 1.0, v125
	v_mul_f32_e32 v122, 0xbfb8aa3b, v120
	v_rcp_f32_e32 v118, v118
	v_exp_f32_e32 v122, v122
	v_mul_f32_e32 v123, 0xbfb8aa3b, v121
	v_exp_f32_e32 v123, v123
	v_mul_f32_e32 v118, v119, v118
	v_add_f32_e32 v119, 1.0, v122
	v_rcp_f32_e32 v119, v119
	v_add_f32_e32 v122, 1.0, v123
	v_rcp_f32_e32 v122, v122
	v_mul_f32_e32 v115, v115, v118
	v_mul_f32_e32 v118, v120, v119
	v_mul_f32_e32 v116, v116, v118
	v_mul_f32_e32 v118, v121, v122
	v_mul_f32_e32 v117, v117, v118
	v_cvt_pk_bf16_f32 v114, v114, v115
	v_cvt_pk_bf16_f32 v115, v116, v117
	global_store_dwordx2 v[140:141], v[114:115], off offset:128
	v_mul_f32_e32 v115, 0xbfb8aa3b, v110
	v_exp_f32_e32 v116, v115
	v_mul_f32_e32 v117, 0xbfb8aa3b, v111
	v_exp_f32_e32 v117, v117
	v_or_b32_e32 v114, 16, v144
	v_add_f32_e32 v116, 1.0, v116
	v_rcp_f32_e32 v116, v116
	v_ashrrev_i32_e32 v115, 31, v114
	v_lshlrev_b64 v[114:115], 11, v[114:115]
	v_lshl_add_u64 v[114:115], s[12:13], 0, v[114:115]
	v_mul_f32_e32 v110, v110, v116
	v_mul_f32_e32 v106, v106, v110
	v_add_f32_e32 v110, 1.0, v117
	v_mul_f32_e32 v116, 0xbfb8aa3b, v112
	v_rcp_f32_e32 v110, v110
	v_exp_f32_e32 v116, v116
	v_mul_f32_e32 v117, 0xbfb8aa3b, v113
	v_exp_f32_e32 v117, v117
	v_mul_f32_e32 v110, v111, v110
	v_add_f32_e32 v111, 1.0, v116
	v_rcp_f32_e32 v111, v111
	v_add_f32_e32 v116, 1.0, v117
	v_rcp_f32_e32 v116, v116
	v_mul_f32_e32 v107, v107, v110
	v_mul_f32_e32 v110, v112, v111
	v_mul_f32_e32 v111, 0xbfb8aa3b, v102
	v_exp_f32_e32 v111, v111
	v_mul_f32_e32 v108, v108, v110
	v_mul_f32_e32 v110, v113, v116
	v_mul_f32_e32 v109, v109, v110
	v_cvt_pk_bf16_f32 v106, v106, v107
	v_cvt_pk_bf16_f32 v107, v108, v109
	v_add_f32_e32 v108, 1.0, v111
	v_rcp_f32_e32 v108, v108
	v_mul_f32_e32 v109, 0xbfb8aa3b, v103
	v_exp_f32_e32 v109, v109
	v_lshl_add_u64 v[114:115], v[114:115], 0, v[142:143]
	v_mul_f32_e32 v102, v102, v108
	global_store_dwordx2 v[114:115], v[106:107], off
	v_mul_f32_e32 v98, v98, v102
	v_add_f32_e32 v102, 1.0, v109
	v_mul_f32_e32 v106, 0xbfb8aa3b, v104
	v_rcp_f32_e32 v102, v102
	v_exp_f32_e32 v106, v106
	v_mul_f32_e32 v107, 0xbfb8aa3b, v105
	v_exp_f32_e32 v107, v107
	v_mul_f32_e32 v102, v103, v102
	v_add_f32_e32 v103, 1.0, v106
	v_rcp_f32_e32 v103, v103
	v_add_f32_e32 v106, 1.0, v107
	v_rcp_f32_e32 v106, v106
	v_mul_f32_e32 v99, v99, v102
	v_mul_f32_e32 v102, v104, v103
	v_mul_f32_e32 v100, v100, v102
	v_mul_f32_e32 v102, v105, v106
	v_mul_f32_e32 v101, v101, v102
	v_cvt_pk_bf16_f32 v98, v98, v99
	v_cvt_pk_bf16_f32 v99, v100, v101
	global_store_dwordx2 v[114:115], v[98:99], off offset:128
	v_mul_f32_e32 v99, 0xbfb8aa3b, v94
	v_exp_f32_e32 v100, v99
	v_mul_f32_e32 v101, 0xbfb8aa3b, v95
	v_exp_f32_e32 v101, v101
	v_or_b32_e32 v98, 32, v144
	v_add_f32_e32 v100, 1.0, v100
	v_rcp_f32_e32 v100, v100
	v_ashrrev_i32_e32 v99, 31, v98
	v_lshlrev_b64 v[98:99], 11, v[98:99]
	v_lshl_add_u64 v[98:99], s[12:13], 0, v[98:99]
	v_mul_f32_e32 v94, v94, v100
	v_mul_f32_e32 v90, v90, v94
	v_add_f32_e32 v94, 1.0, v101
	v_mul_f32_e32 v100, 0xbfb8aa3b, v96
	v_rcp_f32_e32 v94, v94
	v_exp_f32_e32 v100, v100
	v_mul_f32_e32 v101, 0xbfb8aa3b, v97
	v_exp_f32_e32 v101, v101
	v_mul_f32_e32 v94, v95, v94
	v_add_f32_e32 v95, 1.0, v100
	v_rcp_f32_e32 v95, v95
	v_add_f32_e32 v100, 1.0, v101
	v_rcp_f32_e32 v100, v100
	v_mul_f32_e32 v91, v91, v94
	v_mul_f32_e32 v94, v96, v95
	v_mul_f32_e32 v95, 0xbfb8aa3b, v86
	v_exp_f32_e32 v95, v95
	v_mul_f32_e32 v92, v92, v94
	v_mul_f32_e32 v94, v97, v100
	v_mul_f32_e32 v93, v93, v94
	v_cvt_pk_bf16_f32 v90, v90, v91
	v_cvt_pk_bf16_f32 v91, v92, v93
	v_add_f32_e32 v92, 1.0, v95
	v_rcp_f32_e32 v92, v92
	v_mul_f32_e32 v93, 0xbfb8aa3b, v87
	v_exp_f32_e32 v93, v93
	v_lshl_add_u64 v[98:99], v[98:99], 0, v[142:143]
	v_mul_f32_e32 v86, v86, v92
	global_store_dwordx2 v[98:99], v[90:91], off
	v_mul_f32_e32 v82, v82, v86
	v_add_f32_e32 v86, 1.0, v93
	v_mul_f32_e32 v90, 0xbfb8aa3b, v88
	v_rcp_f32_e32 v86, v86
	v_exp_f32_e32 v90, v90
	v_mul_f32_e32 v91, 0xbfb8aa3b, v89
	v_exp_f32_e32 v91, v91
	v_mul_f32_e32 v86, v87, v86
	v_add_f32_e32 v87, 1.0, v90
	v_rcp_f32_e32 v87, v87
	v_add_f32_e32 v90, 1.0, v91
	v_rcp_f32_e32 v90, v90
	v_mul_f32_e32 v83, v83, v86
	v_mul_f32_e32 v86, v88, v87
	v_mul_f32_e32 v84, v84, v86
	v_mul_f32_e32 v86, v89, v90
	v_mul_f32_e32 v85, v85, v86
	v_cvt_pk_bf16_f32 v82, v82, v83
	v_cvt_pk_bf16_f32 v83, v84, v85
	global_store_dwordx2 v[98:99], v[82:83], off offset:128
	v_mul_f32_e32 v83, 0xbfb8aa3b, v78
	v_exp_f32_e32 v84, v83
	v_mul_f32_e32 v85, 0xbfb8aa3b, v79
	v_exp_f32_e32 v85, v85
	v_or_b32_e32 v82, 48, v144
	v_add_f32_e32 v84, 1.0, v84
	v_rcp_f32_e32 v84, v84
	v_ashrrev_i32_e32 v83, 31, v82
	v_lshlrev_b64 v[82:83], 11, v[82:83]
	v_lshl_add_u64 v[82:83], s[12:13], 0, v[82:83]
	v_mul_f32_e32 v78, v78, v84
	v_mul_f32_e32 v74, v74, v78
	v_add_f32_e32 v78, 1.0, v85
	v_mul_f32_e32 v84, 0xbfb8aa3b, v80
	v_rcp_f32_e32 v78, v78
	v_exp_f32_e32 v84, v84
	v_mul_f32_e32 v85, 0xbfb8aa3b, v81
	v_exp_f32_e32 v85, v85
	v_mul_f32_e32 v78, v79, v78
	v_add_f32_e32 v79, 1.0, v84
	v_rcp_f32_e32 v79, v79
	v_add_f32_e32 v84, 1.0, v85
	v_rcp_f32_e32 v84, v84
	v_mul_f32_e32 v75, v75, v78
	v_mul_f32_e32 v78, v80, v79
	v_mul_f32_e32 v79, 0xbfb8aa3b, v70
	v_exp_f32_e32 v79, v79
	v_mul_f32_e32 v76, v76, v78
	v_mul_f32_e32 v78, v81, v84
	v_mul_f32_e32 v77, v77, v78
	v_cvt_pk_bf16_f32 v74, v74, v75
	v_cvt_pk_bf16_f32 v75, v76, v77
	v_add_f32_e32 v76, 1.0, v79
	v_rcp_f32_e32 v76, v76
	v_mul_f32_e32 v77, 0xbfb8aa3b, v71
	v_exp_f32_e32 v77, v77
	v_lshl_add_u64 v[82:83], v[82:83], 0, v[142:143]
	v_mul_f32_e32 v70, v70, v76
	global_store_dwordx2 v[82:83], v[74:75], off
	v_mul_f32_e32 v66, v66, v70
	v_add_f32_e32 v70, 1.0, v77
	v_mul_f32_e32 v74, 0xbfb8aa3b, v72
	v_rcp_f32_e32 v70, v70
	v_exp_f32_e32 v74, v74
	v_mul_f32_e32 v75, 0xbfb8aa3b, v73
	v_exp_f32_e32 v75, v75
	v_mul_f32_e32 v70, v71, v70
	v_add_f32_e32 v71, 1.0, v74
	v_rcp_f32_e32 v71, v71
	v_add_f32_e32 v74, 1.0, v75
	v_rcp_f32_e32 v74, v74
	v_mul_f32_e32 v67, v67, v70
	v_mul_f32_e32 v70, v72, v71
	v_mul_f32_e32 v68, v68, v70
	v_mul_f32_e32 v70, v73, v74
	v_mul_f32_e32 v69, v69, v70
	v_cvt_pk_bf16_f32 v66, v66, v67
	v_cvt_pk_bf16_f32 v67, v68, v69
	v_mul_f32_e32 v68, 0xbfb8aa3b, v62
	v_exp_f32_e32 v68, v68
	global_store_dwordx2 v[82:83], v[66:67], off offset:128
	s_mov_b64 s[4:5], 0x40000
	v_mov_b32_e32 v142, v160
	v_add_f32_e32 v66, 1.0, v68
	v_rcp_f32_e32 v68, v66
	v_mul_f32_e32 v66, 0xbfb8aa3b, v63
	v_exp_f32_e32 v69, v66
	v_lshl_add_u64 v[66:67], v[140:141], 0, s[4:5]
	v_mul_f32_e32 v62, v62, v68
	v_mul_f32_e32 v58, v58, v62
	v_add_f32_e32 v62, 1.0, v69
	v_mul_f32_e32 v68, 0xbfb8aa3b, v64
	v_rcp_f32_e32 v62, v62
	v_exp_f32_e32 v68, v68
	v_mul_f32_e32 v69, 0xbfb8aa3b, v65
	v_exp_f32_e32 v69, v69
	v_mul_f32_e32 v62, v63, v62
	v_add_f32_e32 v63, 1.0, v68
	v_rcp_f32_e32 v63, v63
	v_add_f32_e32 v68, 1.0, v69
	v_rcp_f32_e32 v68, v68
	v_mul_f32_e32 v59, v59, v62
	v_mul_f32_e32 v62, v64, v63
	v_mul_f32_e32 v60, v60, v62
	v_mul_f32_e32 v62, v65, v68
	v_mul_f32_e32 v61, v61, v62
	v_cvt_pk_bf16_f32 v58, v58, v59
	v_cvt_pk_bf16_f32 v59, v60, v61
	v_mul_f32_e32 v60, 0xbfb8aa3b, v54
	v_exp_f32_e32 v62, v60
	v_mul_f32_e32 v63, 0xbfb8aa3b, v55
	v_exp_f32_e32 v63, v63
	s_mov_b32 s4, 0x40000
	v_add_f32_e32 v62, 1.0, v62
	v_rcp_f32_e32 v62, v62
	v_add_co_u32_e32 v60, vcc, s4, v140
	s_mov_b64 s[4:5], 0x48000
	s_nop 0
	v_addc_co_u32_e32 v61, vcc, 0, v141, vcc
	v_mul_f32_e32 v54, v54, v62
	global_store_dwordx2 v[60:61], v[58:59], off
	v_mul_f32_e32 v50, v50, v54
	v_add_f32_e32 v54, 1.0, v63
	v_mul_f32_e32 v58, 0xbfb8aa3b, v56
	v_rcp_f32_e32 v54, v54
	v_exp_f32_e32 v58, v58
	v_mul_f32_e32 v59, 0xbfb8aa3b, v57
	v_exp_f32_e32 v59, v59
	v_mul_f32_e32 v54, v55, v54
	v_add_f32_e32 v55, 1.0, v58
	v_rcp_f32_e32 v55, v55
	v_add_f32_e32 v58, 1.0, v59
	v_rcp_f32_e32 v58, v58
	v_mul_f32_e32 v51, v51, v54
	v_mul_f32_e32 v54, v56, v55
	v_mul_f32_e32 v52, v52, v54
	v_mul_f32_e32 v54, v57, v58
	v_mul_f32_e32 v53, v53, v54
	v_cvt_pk_bf16_f32 v50, v50, v51
	v_cvt_pk_bf16_f32 v51, v52, v53
	v_mul_f32_e32 v52, 0xbfb8aa3b, v46
	v_exp_f32_e32 v52, v52
	global_store_dwordx2 v[66:67], v[50:51], off offset:128
	v_mov_b32_e32 v144, v161
	s_mov_b32 s47, s18
	v_add_f32_e32 v50, 1.0, v52
	v_rcp_f32_e32 v52, v50
	v_mul_f32_e32 v50, 0xbfb8aa3b, v47
	v_exp_f32_e32 v53, v50
	v_lshl_add_u64 v[50:51], v[140:141], 0, s[4:5]
	v_mul_f32_e32 v46, v46, v52
	v_mul_f32_e32 v42, v42, v46
	v_add_f32_e32 v46, 1.0, v53
	v_mul_f32_e32 v52, 0xbfb8aa3b, v48
	v_rcp_f32_e32 v46, v46
	v_exp_f32_e32 v52, v52
	v_mul_f32_e32 v53, 0xbfb8aa3b, v49
	v_exp_f32_e32 v53, v53
	v_mul_f32_e32 v46, v47, v46
	v_add_f32_e32 v47, 1.0, v52
	v_rcp_f32_e32 v47, v47
	v_add_f32_e32 v52, 1.0, v53
	v_rcp_f32_e32 v52, v52
	v_mul_f32_e32 v43, v43, v46
	v_mul_f32_e32 v46, v48, v47
	v_mul_f32_e32 v44, v44, v46
	v_mul_f32_e32 v46, v49, v52
	v_mul_f32_e32 v45, v45, v46
	v_cvt_pk_bf16_f32 v42, v42, v43
	v_cvt_pk_bf16_f32 v43, v44, v45
	v_mul_f32_e32 v44, 0xbfb8aa3b, v38
	v_exp_f32_e32 v46, v44
	v_mul_f32_e32 v47, 0xbfb8aa3b, v39
	v_exp_f32_e32 v47, v47
	s_mov_b32 s4, 0x48000
	v_add_f32_e32 v46, 1.0, v46
	v_rcp_f32_e32 v46, v46
	v_add_co_u32_e32 v44, vcc, s4, v140
	s_mov_b64 s[4:5], 0x50000
	s_nop 0
	v_addc_co_u32_e32 v45, vcc, 0, v141, vcc
	v_mul_f32_e32 v38, v38, v46
	global_store_dwordx2 v[44:45], v[42:43], off
	v_mul_f32_e32 v34, v34, v38
	v_add_f32_e32 v38, 1.0, v47
	v_mul_f32_e32 v42, 0xbfb8aa3b, v40
	v_rcp_f32_e32 v38, v38
	v_exp_f32_e32 v42, v42
	v_mul_f32_e32 v43, 0xbfb8aa3b, v41
	v_exp_f32_e32 v43, v43
	v_mul_f32_e32 v38, v39, v38
	v_add_f32_e32 v39, 1.0, v42
	v_rcp_f32_e32 v39, v39
	v_add_f32_e32 v42, 1.0, v43
	v_rcp_f32_e32 v42, v42
	v_mul_f32_e32 v35, v35, v38
	v_mul_f32_e32 v38, v40, v39
	v_mul_f32_e32 v36, v36, v38
	v_mul_f32_e32 v38, v41, v42
	v_mul_f32_e32 v37, v37, v38
	v_cvt_pk_bf16_f32 v34, v34, v35
	v_cvt_pk_bf16_f32 v35, v36, v37
	v_mul_f32_e32 v36, 0xbfb8aa3b, v30
	v_exp_f32_e32 v36, v36
	global_store_dwordx2 v[50:51], v[34:35], off offset:128
	s_mov_b32 s46, s45
	s_mov_b64 s[20:21], s[2:3]
	v_add_f32_e32 v34, 1.0, v36
	v_rcp_f32_e32 v36, v34
	v_mul_f32_e32 v34, 0xbfb8aa3b, v31
	v_exp_f32_e32 v37, v34
	v_lshl_add_u64 v[34:35], v[140:141], 0, s[4:5]
	v_mul_f32_e32 v30, v30, v36
	v_mul_f32_e32 v26, v26, v30
	v_add_f32_e32 v30, 1.0, v37
	v_mul_f32_e32 v36, 0xbfb8aa3b, v32
	v_rcp_f32_e32 v30, v30
	v_exp_f32_e32 v36, v36
	v_mul_f32_e32 v37, 0xbfb8aa3b, v33
	v_exp_f32_e32 v37, v37
	v_mul_f32_e32 v30, v31, v30
	v_add_f32_e32 v31, 1.0, v36
	v_rcp_f32_e32 v31, v31
	v_add_f32_e32 v36, 1.0, v37
	v_rcp_f32_e32 v36, v36
	v_mul_f32_e32 v27, v27, v30
	v_mul_f32_e32 v30, v32, v31
	v_mul_f32_e32 v28, v28, v30
	v_mul_f32_e32 v30, v33, v36
	v_mul_f32_e32 v29, v29, v30
	v_cvt_pk_bf16_f32 v26, v26, v27
	v_cvt_pk_bf16_f32 v27, v28, v29
	v_mul_f32_e32 v28, 0xbfb8aa3b, v22
	v_exp_f32_e32 v30, v28
	v_mul_f32_e32 v31, 0xbfb8aa3b, v23
	v_exp_f32_e32 v31, v31
	s_mov_b32 s4, 0x50000
	v_add_f32_e32 v30, 1.0, v30
	v_rcp_f32_e32 v30, v30
	v_add_co_u32_e32 v28, vcc, s4, v140
	s_mov_b64 s[4:5], 0x58000
	s_nop 0
	v_addc_co_u32_e32 v29, vcc, 0, v141, vcc
	v_mul_f32_e32 v22, v22, v30
	global_store_dwordx2 v[28:29], v[26:27], off
	v_mul_f32_e32 v18, v18, v22
	v_add_f32_e32 v22, 1.0, v31
	v_mul_f32_e32 v26, 0xbfb8aa3b, v24
	v_rcp_f32_e32 v22, v22
	v_exp_f32_e32 v26, v26
	v_mul_f32_e32 v27, 0xbfb8aa3b, v25
	v_exp_f32_e32 v27, v27
	v_mul_f32_e32 v22, v23, v22
	v_add_f32_e32 v23, 1.0, v26
	v_rcp_f32_e32 v23, v23
	v_add_f32_e32 v26, 1.0, v27
	v_rcp_f32_e32 v26, v26
	v_mul_f32_e32 v19, v19, v22
	v_mul_f32_e32 v22, v24, v23
	v_mul_f32_e32 v20, v20, v22
	v_mul_f32_e32 v22, v25, v26
	v_mul_f32_e32 v21, v21, v22
	v_cvt_pk_bf16_f32 v18, v18, v19
	v_cvt_pk_bf16_f32 v19, v20, v21
	v_mul_f32_e32 v20, 0xbfb8aa3b, v14
	v_exp_f32_e32 v20, v20
	global_store_dwordx2 v[34:35], v[18:19], off offset:128
	v_add_f32_e32 v18, 1.0, v20
	v_rcp_f32_e32 v20, v18
	v_mul_f32_e32 v18, 0xbfb8aa3b, v15
	v_exp_f32_e32 v21, v18
	v_lshl_add_u64 v[18:19], v[140:141], 0, s[4:5]
	v_mul_f32_e32 v14, v14, v20
	v_mul_f32_e32 v10, v10, v14
	v_add_f32_e32 v14, 1.0, v21
	v_mul_f32_e32 v20, 0xbfb8aa3b, v16
	v_rcp_f32_e32 v14, v14
	v_exp_f32_e32 v20, v20
	v_mul_f32_e32 v21, 0xbfb8aa3b, v17
	v_exp_f32_e32 v21, v21
	v_mul_f32_e32 v14, v15, v14
	v_add_f32_e32 v15, 1.0, v20
	v_rcp_f32_e32 v15, v15
	v_add_f32_e32 v20, 1.0, v21
	v_rcp_f32_e32 v20, v20
	v_mul_f32_e32 v11, v11, v14
	v_mul_f32_e32 v14, v16, v15
	v_mul_f32_e32 v12, v12, v14
	v_mul_f32_e32 v14, v17, v20
	v_mul_f32_e32 v13, v13, v14
	v_cvt_pk_bf16_f32 v10, v10, v11
	v_cvt_pk_bf16_f32 v11, v12, v13
	v_mul_f32_e32 v12, 0xbfb8aa3b, v6
	v_exp_f32_e32 v14, v12
	v_mul_f32_e32 v15, 0xbfb8aa3b, v7
	v_exp_f32_e32 v15, v15
	s_mov_b32 s4, 0x58000
	v_add_f32_e32 v14, 1.0, v14
	v_rcp_f32_e32 v14, v14
	v_add_co_u32_e32 v12, vcc, s4, v140
	v_mov_b32_e32 v140, v159
	s_nop 0
	v_addc_co_u32_e32 v13, vcc, 0, v141, vcc
	v_mul_f32_e32 v6, v6, v14
	global_store_dwordx2 v[12:13], v[10:11], off
	v_mul_f32_e32 v2, v2, v6
	v_add_f32_e32 v6, 1.0, v15
	v_mul_f32_e32 v10, 0xbfb8aa3b, v8
	v_rcp_f32_e32 v6, v6
	v_exp_f32_e32 v10, v10
	v_mul_f32_e32 v11, 0xbfb8aa3b, v9
	v_exp_f32_e32 v11, v11
	v_mul_f32_e32 v6, v7, v6
	v_add_f32_e32 v7, 1.0, v10
	v_rcp_f32_e32 v7, v7
	v_add_f32_e32 v10, 1.0, v11
	v_rcp_f32_e32 v10, v10
	v_mul_f32_e32 v3, v3, v6
	v_mul_f32_e32 v6, v8, v7
	v_mul_f32_e32 v4, v4, v6
	v_mul_f32_e32 v6, v9, v10
	s_and_b64 vcc, exec, s[0:1]
	v_mov_b32_e32 v141, v158
	v_mul_f32_e32 v5, v5, v6
	v_cvt_pk_bf16_f32 v2, v2, v3
	v_cvt_pk_bf16_f32 v3, v4, v5
	global_store_dwordx2 v[18:19], v[2:3], off offset:128
	s_cbranch_vccz .LBB0_2070
	s_waitcnt vmcnt(0)
	s_cmpk_gt_u32 s28, 0xff
	s_cbranch_scc1 .LBB0_2081
	s_barrier

.LBB0_2083:
	s_cmp_gt_i32 s55, 11
	s_cselect_b64 s[0:1], -1, 0
	s_and_b64 s[2:3], s[6:7], s[0:1]
	s_andn2_b64 vcc, exec, s[2:3]
	s_cbranch_vccnz .LBB0_2133
	s_waitcnt vmcnt(0)
	s_barrier
	s_setprio 0
	s_mov_b64 s[2:3], exec
	v_readlane_b32 s4, v250, 5
	v_readlane_b32 s5, v250, 6
	s_and_b64 s[4:5], s[2:3], s[4:5]
	s_mov_b64 exec, s[4:5]
	s_cbranch_execz .LBB0_2132
	s_add_i32 s4, 0, 0x27ff0
	v_mov_b32_e32 v1, s4
	s_waitcnt vmcnt(0) expcnt(0) lgkmcnt(0)
	ds_read_b32 v3, v1
	s_add_i32 s4, 0, 0x27ff4
	v_mov_b32_e32 v1, s4
	ds_read_b32 v1, v1
	s_waitcnt lgkmcnt(1)
	v_cmp_ne_u32_e32 vcc, 0, v3
	s_cbranch_vccnz .LBB0_2100
	v_readlane_b32 s4, v250, 2
	v_readlane_b32 s5, v250, 3
	s_load_dwordx2 s[8:9], s[4:5], 0x4
	s_add_u32 s4, s52, 0x1000
	s_addc_u32 s5, s53, 0
	s_add_u32 s6, s52, 0x1100
	s_addc_u32 s7, s53, 0
	v_readlane_b32 s10, v250, 1
	s_waitcnt lgkmcnt(0)
	s_mul_i32 s18, s8, s10
	s_add_u32 s8, s52, 0x1200
	s_mul_i32 s18, s18, s9
	s_addc_u32 s9, s53, 0
	s_add_u32 s10, s52, 0x1300
	s_addc_u32 s11, s53, 0
	s_mov_b32 s19, 1
	v_mov_b32_e32 v17, 0
	s_branch .LBB0_2088

.LBB0_2133:
	s_cmp_lt_i32 s54, 12
	s_cselect_b64 s[6:7], -1, 0
	s_and_b64 s[0:1], s[6:7], s[0:1]
	s_andn2_b64 vcc, exec, s[0:1]
	s_cbranch_vccnz .LBB0_2151
	v_mov_b32_e32 v1, v248
	s_waitcnt vmcnt(11)
	v_mov_b32_e32 v2, v0
	v_readlane_b32 s20, v250, 1
	v_readlane_b32 s21, v250, 0
	v_readlane_b32 s0, v250, 39
	s_mov_b64 s[0:1], s[52:53]
	s_mov_b64 s[2:3], s[90:91]
	s_cmpk_gt_i32 s21, 0x47f
	v_readfirstlane_b32 s22, v0
	s_barrier
	s_cbranch_scc1 .LBB0_2150
	v_lshlrev_b32_e32 v1, 4, v0
	s_waitcnt vmcnt(9)
	v_or_b32_e32 v10, 0x2000, v1
	v_and_b32_e32 v4, 32, v0
	v_lshrrev_b32_e32 v2, 7, v10
	v_bfe_u32 v13, v0, 2, 4
	s_movk_i32 s2, 0x70
	v_bitop3_b32 v11, v1, v4, 48 bitop3:0x6c
	v_and_b32_e32 v12, 64, v0
	s_add_u32 s23, s0, 0x32d40000
	v_and_or_b32 v3, v2, s2, v13
	v_or_b32_e32 v1, v11, v12
	s_addc_u32 s24, s1, 0
	v_lshl_or_b32 v130, v3, 11, v1
	v_lshrrev_b32_e32 v3, 5, v0
	v_lshrrev_b32_e32 v5, 1, v0
	s_add_u32 s25, s0, 0x1e940000
	v_and_b32_e32 v3, 4, v3
	v_bfe_u32 v4, v0, 2, 2
	s_waitcnt vmcnt(8)
	v_and_b32_e32 v14, 24, v5
	s_addc_u32 s26, s1, 0
	v_or3_b32 v3, v3, v4, v14
	s_movk_i32 s2, 0x60
	s_ashr_i32 s28, s21, 31
	v_and_or_b32 v2, v2, s2, v3
	s_lshr_b32 s2, s28, 29
	s_add_i32 s2, s21, s2
	s_lshr_b32 s4, s22, 6
	s_ashr_i32 s5, s2, 3
	s_and_b32 s2, s2, -8
	s_lshr_b32 s3, s22, 8
	s_lshl_b32 s27, s4, 10
	s_sub_i32 s2, s21, s2
	s_cmp_lt_i32 s2, 0
	s_movk_i32 s29, 0x91
	s_cselect_b32 s8, s29, 0x90
	s_mul_i32 s2, s8, s2
	s_add_i32 s2, s2, s5
	s_ashr_i32 s5, s2, 31
	s_lshr_b32 s5, s5, 26
	s_add_i32 s5, s2, s5
	s_ashr_i32 s8, s5, 6
	s_lshl_b32 s10, s8, 3
	v_lshl_or_b32 v132, v2, 11, v1
	v_lshrrev_b32_e32 v2, 3, v0
	s_sub_i32 s8, 0x90, s10
	v_and_or_b32 v4, v2, 48, v13
	s_min_u32 s11, s8, 8
	s_andn2_b32 s5, s5, 63
	v_lshl_or_b32 v134, v4, 11, v1
	s_sub_i32 s5, s2, s5
	v_cvt_f32_ubyte0_e32 v4, s11
	v_and_or_b32 v2, v2, 32, v3
	v_cvt_f32_i32_e32 v3, s5
	v_rcp_iflag_f32_e32 v5, v4
	v_lshl_or_b32 v136, v2, 11, v1
	s_ashr_i32 s2, s5, 30
	s_or_b32 s2, s2, 1
	v_mul_f32_e32 v1, v3, v5
	v_trunc_f32_e32 v1, v1
	v_fma_f32 v2, -v1, v4, v3
	v_cvt_i32_f32_e32 v1, v1
	v_cmp_ge_f32_e64 s[8:9], |v2|, v4
	s_and_b64 s[8:9], s[8:9], exec
	s_cselect_b32 s2, s2, 0
	v_readfirstlane_b32 s8, v1
	s_add_i32 s2, s8, s2
	s_mul_i32 s8, s2, s11
	s_sub_i32 s5, s5, s8
	s_sext_i32_i8 s5, s5
	s_add_i32 s43, s10, s5
	s_mul_hi_i32 s5, s43, 0x38e38e39
	s_lshr_b32 s8, s5, 31
	s_ashr_i32 s5, s5, 1
	s_add_i32 s8, s5, s8
	s_mul_i32 s5, s8, -9
	s_add_i32 s5, s5, s43
	s_mul_i32 s9, s8, 0x900
	s_lshl_b32 s5, s5, 8
	s_add_i32 s10, s5, s9
	s_ashr_i32 s11, s10, 31
	s_lshl_b64 s[10:11], s[10:11], 11
	s_add_u32 s14, s23, s10
	s_addc_u32 s15, s24, s11
	s_ashr_i32 s9, s8, 31
	s_bfe_i64 s[10:11], s[2:3], 0x80000
	s_lshl_b64 s[10:11], s[10:11], 19
	s_lshl_b64 s[8:9], s[8:9], 22
	s_add_u32 s5, s25, s8
	s_addc_u32 s8, s26, s9
	s_add_u32 s16, s5, s10
	s_addc_u32 s17, s8, s11
	s_add_i32 s30, s27, 0
	s_add_i32 m0, s30, 0x10000
	s_add_i32 s31, s30, 0x2000
	global_load_lds_dwordx4 v136, s[16:17]
	s_add_i32 m0, s30, 0x12000
	s_add_u32 s8, s16, 0x40000
	global_load_lds_dwordx4 v132, s[16:17]
	s_mov_b32 m0, s30
	s_addc_u32 s9, s17, 0
	global_load_lds_dwordx4 v134, s[14:15]
	s_mov_b32 m0, s31
	v_mov_b32_e32 v137, 0
	global_load_lds_dwordx4 v130, s[14:15]
	s_add_i32 m0, s30, 0x14000
	v_mov_b32_e32 v133, v137
	global_load_lds_dwordx4 v136, s[8:9]
	s_add_i32 m0, s30, 0x16000
	v_mov_b32_e32 v135, v137
	global_load_lds_dwordx4 v132, s[8:9]
	s_add_u32 s8, s14, 0x40000
	s_addc_u32 s9, s15, 0
	s_add_i32 s33, s30, 0x4000
	s_mov_b32 m0, s33
	s_add_i32 s34, s30, 0x6000
	global_load_lds_dwordx4 v134, s[8:9]
	s_mov_b32 m0, s34
	v_mov_b32_e32 v131, v137
	global_load_lds_dwordx4 v130, s[8:9]
	s_mov_b32 s35, 0
	v_lshl_add_u64 v[8:9], s[16:17], 0, v[136:137]
	v_lshl_add_u64 v[6:7], s[16:17], 0, v[132:133]
	v_lshl_add_u64 v[4:5], s[14:15], 0, v[134:135]
	s_setprio 1
	s_cmp_lg_u32 s3, 1
	v_lshl_add_u64 v[2:3], s[14:15], 0, v[130:131]
	s_cbranch_scc1 .LBB0_2137
	s_barrier
	s_setprio 0

.LBB0_2145:
	ds_read_b128 v[154:157], v150
	ds_read_b128 v[158:161], v150 offset:1024
	ds_read_b128 v[162:165], v150 offset:2048
	ds_read_b128 v[166:169], v150 offset:3072
	s_add_u32 s16, s14, 0xfffc0080
	s_addc_u32 s17, s15, -1
	s_cmp_eq_u32 s46, 12
	s_cselect_b32 s19, s3, s17
	s_cselect_b32 s18, s2, s16
	s_cselect_b32 s17, s5, s45
	s_cselect_b32 s16, s4, s13
	v_lshl_add_u64 v[146:147], s[14:15], 0, v[138:139]
	s_add_i32 m0, s30, 0xc000
	ds_read_b128 v[170:173], v151
	ds_read_b128 v[174:177], v151 offset:1024
	ds_read_b128 v[178:181], v151 offset:2048
	ds_read_b128 v[182:185], v151 offset:3072
	ds_read_b128 v[186:189], v151 offset:4096
	ds_read_b128 v[190:193], v151 offset:5120
	ds_read_b128 v[194:197], v151 offset:6144
	ds_read_b128 v[198:201], v151 offset:7168
	global_load_lds_dwordx4 v[146:147], off
	v_lshl_add_u64 v[146:147], s[14:15], 0, v[140:141]
	s_add_i32 m0, s30, 0xe000
	s_nop 0
	global_load_lds_dwordx4 v[146:147], off
	s_waitcnt lgkmcnt(8)
	s_barrier
	s_waitcnt lgkmcnt(0)
	s_waitcnt lgkmcnt(0)
	v_mfma_f32_16x16x32_bf16 v[126:129], v[154:157], v[170:173], v[126:129]
	v_mfma_f32_16x16x32_bf16 v[122:125], v[162:165], v[170:173], v[122:125]
	v_mfma_f32_16x16x32_bf16 v[114:117], v[154:157], v[178:181], v[114:117]
	v_mfma_f32_16x16x32_bf16 v[106:109], v[162:165], v[178:181], v[106:109]
	v_mfma_f32_16x16x32_bf16 v[98:101], v[154:157], v[186:189], v[98:101]
	v_mfma_f32_16x16x32_bf16 v[90:93], v[162:165], v[186:189], v[90:93]
	v_mfma_f32_16x16x32_bf16 v[82:85], v[154:157], v[194:197], v[82:85]
	v_mfma_f32_16x16x32_bf16 v[74:77], v[162:165], v[194:197], v[74:77]
	v_mfma_f32_16x16x32_bf16 v[126:129], v[158:161], v[174:177], v[126:129]
	v_mfma_f32_16x16x32_bf16 v[122:125], v[166:169], v[174:177], v[122:125]
	v_mfma_f32_16x16x32_bf16 v[114:117], v[158:161], v[182:185], v[114:117]
	v_mfma_f32_16x16x32_bf16 v[106:109], v[166:169], v[182:185], v[106:109]
	v_mfma_f32_16x16x32_bf16 v[98:101], v[158:161], v[190:193], v[98:101]
	v_mfma_f32_16x16x32_bf16 v[90:93], v[166:169], v[190:193], v[90:93]
	v_mfma_f32_16x16x32_bf16 v[82:85], v[158:161], v[198:201], v[82:85]
	v_mfma_f32_16x16x32_bf16 v[74:77], v[166:169], v[198:201], v[74:77]
	s_barrier
	s_add_i32 s47, s39, s27
	v_lshl_add_u64 v[146:147], s[16:17], 0, v[136:137]
	s_mov_b32 m0, s47
	ds_read_b128 v[202:205], v152
	ds_read_b128 v[206:209], v152 offset:1024
	ds_read_b128 v[210:213], v152 offset:2048
	ds_read_b128 v[214:217], v152 offset:3072
	global_load_lds_dwordx4 v[146:147], off
	v_lshl_add_u64 v[218:219], s[16:17], 0, v[132:133]
	s_add_i32 m0, s47, 0x2000
	s_nop 0
	global_load_lds_dwordx4 v[218:219], off
	s_barrier
	s_waitcnt lgkmcnt(0)
	s_waitcnt lgkmcnt(0)
	v_mfma_f32_16x16x32_bf16 v[118:121], v[202:205], v[170:173], v[118:121]
	v_mfma_f32_16x16x32_bf16 v[110:113], v[210:213], v[170:173], v[110:113]
	v_mfma_f32_16x16x32_bf16 v[102:105], v[202:205], v[178:181], v[102:105]
	v_mfma_f32_16x16x32_bf16 v[94:97], v[210:213], v[178:181], v[94:97]
	v_mfma_f32_16x16x32_bf16 v[86:89], v[202:205], v[186:189], v[86:89]
	v_mfma_f32_16x16x32_bf16 v[78:81], v[210:213], v[186:189], v[78:81]
	v_mfma_f32_16x16x32_bf16 v[70:73], v[202:205], v[194:197], v[70:73]
	v_mfma_f32_16x16x32_bf16 v[66:69], v[210:213], v[194:197], v[66:69]
	v_mfma_f32_16x16x32_bf16 v[118:121], v[206:209], v[174:177], v[118:121]
	v_mfma_f32_16x16x32_bf16 v[110:113], v[214:217], v[174:177], v[110:113]
	v_mfma_f32_16x16x32_bf16 v[102:105], v[206:209], v[182:185], v[102:105]
	v_mfma_f32_16x16x32_bf16 v[94:97], v[214:217], v[182:185], v[94:97]
	v_mfma_f32_16x16x32_bf16 v[86:89], v[206:209], v[190:193], v[86:89]
	v_mfma_f32_16x16x32_bf16 v[78:81], v[214:217], v[190:193], v[78:81]
	v_mfma_f32_16x16x32_bf16 v[70:73], v[206:209], v[198:201], v[70:73]
	v_mfma_f32_16x16x32_bf16 v[66:69], v[214:217], v[198:201], v[66:69]
	s_mov_b32 m0, s30
	v_lshl_add_u64 v[220:221], s[18:19], 0, v[134:135]
	s_barrier
	ds_read_b128 v[170:173], v151 offset:16384
	ds_read_b128 v[174:177], v151 offset:17408
	ds_read_b128 v[178:181], v151 offset:18432
	ds_read_b128 v[182:185], v151 offset:19456
	ds_read_b128 v[186:189], v151 offset:20480
	ds_read_b128 v[190:193], v151 offset:21504
	ds_read_b128 v[194:197], v151 offset:22528
	ds_read_b128 v[198:201], v151 offset:23552
	global_load_lds_dwordx4 v[220:221], off
	v_lshl_add_u64 v[222:223], s[18:19], 0, v[130:131]
	s_mov_b32 m0, s31
	s_nop 0
	global_load_lds_dwordx4 v[222:223], off
	s_barrier
	s_waitcnt lgkmcnt(0)
	s_waitcnt lgkmcnt(0)
	v_mfma_f32_16x16x32_bf16 v[62:65], v[154:157], v[170:173], v[62:65]
	v_mfma_f32_16x16x32_bf16 v[58:61], v[162:165], v[170:173], v[58:61]
	v_mfma_f32_16x16x32_bf16 v[54:57], v[154:157], v[178:181], v[54:57]
	v_mfma_f32_16x16x32_bf16 v[46:49], v[162:165], v[178:181], v[46:49]
	v_mfma_f32_16x16x32_bf16 v[38:41], v[154:157], v[186:189], v[38:41]
	v_mfma_f32_16x16x32_bf16 v[30:33], v[162:165], v[186:189], v[30:33]
	v_mfma_f32_16x16x32_bf16 v[22:25], v[154:157], v[194:197], v[22:25]
	v_mfma_f32_16x16x32_bf16 v[14:17], v[162:165], v[194:197], v[14:17]
	v_mfma_f32_16x16x32_bf16 v[62:65], v[158:161], v[174:177], v[62:65]
	v_mfma_f32_16x16x32_bf16 v[58:61], v[166:169], v[174:177], v[58:61]
	v_mfma_f32_16x16x32_bf16 v[54:57], v[158:161], v[182:185], v[54:57]
	v_mfma_f32_16x16x32_bf16 v[46:49], v[166:169], v[182:185], v[46:49]
	v_mfma_f32_16x16x32_bf16 v[38:41], v[158:161], v[190:193], v[38:41]
	v_mfma_f32_16x16x32_bf16 v[30:33], v[166:169], v[190:193], v[30:33]
	v_mfma_f32_16x16x32_bf16 v[22:25], v[158:161], v[198:201], v[22:25]
	v_mfma_f32_16x16x32_bf16 v[14:17], v[166:169], v[198:201], v[14:17]
	s_barrier
	s_add_u32 s48, s16, 0x40000
	s_addc_u32 s49, s17, 0
	s_add_i32 s47, s40, s27
	v_lshl_add_u64 v[154:155], s[48:49], 0, v[136:137]
	s_mov_b32 m0, s47
	s_nop 0
	global_load_lds_dwordx4 v[154:155], off
	v_lshl_add_u64 v[154:155], s[48:49], 0, v[132:133]
	s_add_i32 m0, s47, 0x2000
	s_nop 0
	global_load_lds_dwordx4 v[154:155], off
	s_waitcnt vmcnt(6)
	s_barrier
	v_mfma_f32_16x16x32_bf16 v[50:53], v[202:205], v[170:173], v[50:53]
	v_mfma_f32_16x16x32_bf16 v[42:45], v[210:213], v[170:173], v[42:45]
	v_mfma_f32_16x16x32_bf16 v[34:37], v[202:205], v[178:181], v[34:37]
	v_mfma_f32_16x16x32_bf16 v[26:29], v[210:213], v[178:181], v[26:29]
	v_mfma_f32_16x16x32_bf16 v[18:21], v[202:205], v[186:189], v[18:21]
	v_mfma_f32_16x16x32_bf16 v[10:13], v[210:213], v[186:189], v[10:13]
	v_mfma_f32_16x16x32_bf16 v[6:9], v[202:205], v[194:197], v[6:9]
	v_mfma_f32_16x16x32_bf16 v[2:5], v[210:213], v[194:197], v[2:5]
	v_mfma_f32_16x16x32_bf16 v[50:53], v[206:209], v[174:177], v[50:53]
	v_mfma_f32_16x16x32_bf16 v[42:45], v[214:217], v[174:177], v[42:45]
	v_mfma_f32_16x16x32_bf16 v[34:37], v[206:209], v[182:185], v[34:37]
	v_mfma_f32_16x16x32_bf16 v[26:29], v[214:217], v[182:185], v[26:29]
	v_mfma_f32_16x16x32_bf16 v[18:21], v[206:209], v[190:193], v[18:21]
	v_mfma_f32_16x16x32_bf16 v[10:13], v[214:217], v[190:193], v[10:13]
	v_mfma_f32_16x16x32_bf16 v[6:9], v[206:209], v[198:201], v[6:9]
	v_mfma_f32_16x16x32_bf16 v[2:5], v[214:217], v[198:201], v[2:5]
	s_add_i32 s47, 0, 0x18000
	v_add_u32_e32 v153, s47, v148
	s_barrier
	ds_read_b128 v[154:157], v153
	ds_read_b128 v[158:161], v153 offset:1024
	ds_read_b128 v[162:165], v153 offset:2048
	ds_read_b128 v[166:169], v153 offset:3072
	s_add_u32 s18, s18, 0x40000
	s_addc_u32 s19, s19, 0
	s_mov_b32 m0, s33
	v_lshl_add_u64 v[202:203], s[18:19], 0, v[134:135]
	ds_read_b128 v[170:173], v151 offset:32768
	ds_read_b128 v[174:177], v151 offset:33792
	ds_read_b128 v[178:181], v151 offset:34816
	ds_read_b128 v[182:185], v151 offset:35840
	ds_read_b128 v[186:189], v151 offset:36864
	ds_read_b128 v[190:193], v151 offset:37888
	ds_read_b128 v[194:197], v151 offset:38912
	ds_read_b128 v[198:201], v151 offset:39936
	global_load_lds_dwordx4 v[202:203], off
	v_lshl_add_u64 v[202:203], s[18:19], 0, v[130:131]
	s_mov_b32 m0, s34
	s_nop 0
	global_load_lds_dwordx4 v[202:203], off
	s_waitcnt lgkmcnt(8)
	s_barrier
	s_waitcnt lgkmcnt(0)
	s_waitcnt lgkmcnt(0)
	v_mfma_f32_16x16x32_bf16 v[126:129], v[154:157], v[170:173], v[126:129]
	v_mfma_f32_16x16x32_bf16 v[122:125], v[162:165], v[170:173], v[122:125]
	v_mfma_f32_16x16x32_bf16 v[114:117], v[154:157], v[178:181], v[114:117]
	v_mfma_f32_16x16x32_bf16 v[106:109], v[162:165], v[178:181], v[106:109]
	v_mfma_f32_16x16x32_bf16 v[98:101], v[154:157], v[186:189], v[98:101]
	v_mfma_f32_16x16x32_bf16 v[90:93], v[162:165], v[186:189], v[90:93]
	v_mfma_f32_16x16x32_bf16 v[82:85], v[154:157], v[194:197], v[82:85]
	v_mfma_f32_16x16x32_bf16 v[74:77], v[162:165], v[194:197], v[74:77]
	v_mfma_f32_16x16x32_bf16 v[126:129], v[158:161], v[174:177], v[126:129]
	v_mfma_f32_16x16x32_bf16 v[122:125], v[166:169], v[174:177], v[122:125]
	v_mfma_f32_16x16x32_bf16 v[114:117], v[158:161], v[182:185], v[114:117]
	v_mfma_f32_16x16x32_bf16 v[106:109], v[166:169], v[182:185], v[106:109]
	v_mfma_f32_16x16x32_bf16 v[98:101], v[158:161], v[190:193], v[98:101]
	v_mfma_f32_16x16x32_bf16 v[90:93], v[166:169], v[190:193], v[90:93]
	v_mfma_f32_16x16x32_bf16 v[82:85], v[158:161], v[198:201], v[82:85]
	v_mfma_f32_16x16x32_bf16 v[74:77], v[166:169], v[198:201], v[74:77]
	s_barrier
	s_add_i32 s18, 0, 0x1c000
	s_add_i32 s19, s47, s27
	v_add_u32_e32 v153, s18, v148
	v_lshl_add_u64 v[146:147], v[146:147], 0, s[10:11]
	s_mov_b32 m0, s19
	ds_read_b128 v[202:205], v153
	ds_read_b128 v[206:209], v153 offset:1024
	ds_read_b128 v[210:213], v153 offset:2048
	ds_read_b128 v[214:217], v153 offset:3072
	global_load_lds_dwordx4 v[146:147], off
	v_lshl_add_u64 v[146:147], v[218:219], 0, s[10:11]
	s_add_i32 m0, s19, 0x2000
	s_nop 0
	global_load_lds_dwordx4 v[146:147], off
	s_barrier
	s_waitcnt lgkmcnt(0)
	s_waitcnt lgkmcnt(0)
	v_mfma_f32_16x16x32_bf16 v[118:121], v[202:205], v[170:173], v[118:121]
	v_mfma_f32_16x16x32_bf16 v[110:113], v[210:213], v[170:173], v[110:113]
	v_mfma_f32_16x16x32_bf16 v[102:105], v[202:205], v[178:181], v[102:105]
	v_mfma_f32_16x16x32_bf16 v[94:97], v[210:213], v[178:181], v[94:97]
	v_mfma_f32_16x16x32_bf16 v[86:89], v[202:205], v[186:189], v[86:89]
	v_mfma_f32_16x16x32_bf16 v[78:81], v[210:213], v[186:189], v[78:81]
	v_mfma_f32_16x16x32_bf16 v[70:73], v[202:205], v[194:197], v[70:73]
	v_mfma_f32_16x16x32_bf16 v[66:69], v[210:213], v[194:197], v[66:69]
	v_mfma_f32_16x16x32_bf16 v[118:121], v[206:209], v[174:177], v[118:121]
	v_mfma_f32_16x16x32_bf16 v[110:113], v[214:217], v[174:177], v[110:113]
	v_mfma_f32_16x16x32_bf16 v[102:105], v[206:209], v[182:185], v[102:105]
	v_mfma_f32_16x16x32_bf16 v[94:97], v[214:217], v[182:185], v[94:97]
	v_mfma_f32_16x16x32_bf16 v[86:89], v[206:209], v[190:193], v[86:89]
	v_mfma_f32_16x16x32_bf16 v[78:81], v[214:217], v[190:193], v[78:81]
	v_mfma_f32_16x16x32_bf16 v[70:73], v[206:209], v[198:201], v[70:73]
	v_mfma_f32_16x16x32_bf16 v[66:69], v[214:217], v[198:201], v[66:69]
	s_mov_b32 m0, s36
	v_lshl_add_u64 v[146:147], v[220:221], 0, s[10:11]
	s_barrier
	ds_read_b128 v[170:173], v151 offset:49152
	ds_read_b128 v[174:177], v151 offset:50176
	ds_read_b128 v[178:181], v151 offset:51200
	ds_read_b128 v[182:185], v151 offset:52224
	ds_read_b128 v[186:189], v151 offset:53248
	ds_read_b128 v[190:193], v151 offset:54272
	ds_read_b128 v[194:197], v151 offset:55296
	ds_read_b128 v[198:201], v151 offset:56320
	global_load_lds_dwordx4 v[146:147], off
	v_lshl_add_u64 v[146:147], v[222:223], 0, s[10:11]
	s_mov_b32 m0, s37
	s_nop 0
	global_load_lds_dwordx4 v[146:147], off
	s_barrier
	s_waitcnt lgkmcnt(0)
	s_waitcnt lgkmcnt(0)
	v_mfma_f32_16x16x32_bf16 v[62:65], v[154:157], v[170:173], v[62:65]
	v_mfma_f32_16x16x32_bf16 v[58:61], v[162:165], v[170:173], v[58:61]
	v_mfma_f32_16x16x32_bf16 v[54:57], v[154:157], v[178:181], v[54:57]
	v_mfma_f32_16x16x32_bf16 v[46:49], v[162:165], v[178:181], v[46:49]
	v_mfma_f32_16x16x32_bf16 v[38:41], v[154:157], v[186:189], v[38:41]
	v_mfma_f32_16x16x32_bf16 v[30:33], v[162:165], v[186:189], v[30:33]
	v_mfma_f32_16x16x32_bf16 v[22:25], v[154:157], v[194:197], v[22:25]
	v_mfma_f32_16x16x32_bf16 v[14:17], v[162:165], v[194:197], v[14:17]
	v_mfma_f32_16x16x32_bf16 v[62:65], v[158:161], v[174:177], v[62:65]
	v_mfma_f32_16x16x32_bf16 v[58:61], v[166:169], v[174:177], v[58:61]
	v_mfma_f32_16x16x32_bf16 v[54:57], v[158:161], v[182:185], v[54:57]
	v_mfma_f32_16x16x32_bf16 v[46:49], v[166:169], v[182:185], v[46:49]
	v_mfma_f32_16x16x32_bf16 v[38:41], v[158:161], v[190:193], v[38:41]
	v_mfma_f32_16x16x32_bf16 v[30:33], v[166:169], v[190:193], v[30:33]
	v_mfma_f32_16x16x32_bf16 v[22:25], v[158:161], v[198:201], v[22:25]
	v_mfma_f32_16x16x32_bf16 v[14:17], v[166:169], v[198:201], v[14:17]
	s_barrier
	s_add_u32 s16, s16, 0x40080
	s_addc_u32 s17, s17, 0
	s_add_i32 s18, s18, s27
	v_lshl_add_u64 v[146:147], s[16:17], 0, v[136:137]
	s_mov_b32 m0, s18
	s_nop 0
	global_load_lds_dwordx4 v[146:147], off
	v_lshl_add_u64 v[146:147], s[16:17], 0, v[132:133]
	s_add_i32 m0, s18, 0x2000
	s_nop 0
	global_load_lds_dwordx4 v[146:147], off
	s_waitcnt vmcnt(6)
	s_barrier
	v_mfma_f32_16x16x32_bf16 v[50:53], v[202:205], v[170:173], v[50:53]
	v_mfma_f32_16x16x32_bf16 v[42:45], v[210:213], v[170:173], v[42:45]
	v_mfma_f32_16x16x32_bf16 v[34:37], v[202:205], v[178:181], v[34:37]
	v_mfma_f32_16x16x32_bf16 v[26:29], v[210:213], v[178:181], v[26:29]
	v_mfma_f32_16x16x32_bf16 v[18:21], v[202:205], v[186:189], v[18:21]
	v_mfma_f32_16x16x32_bf16 v[10:13], v[210:213], v[186:189], v[10:13]
	v_mfma_f32_16x16x32_bf16 v[6:9], v[202:205], v[194:197], v[6:9]
	v_mfma_f32_16x16x32_bf16 v[2:5], v[210:213], v[194:197], v[2:5]
	v_mfma_f32_16x16x32_bf16 v[50:53], v[206:209], v[174:177], v[50:53]
	v_mfma_f32_16x16x32_bf16 v[42:45], v[214:217], v[174:177], v[42:45]
	v_mfma_f32_16x16x32_bf16 v[34:37], v[206:209], v[182:185], v[34:37]
	v_mfma_f32_16x16x32_bf16 v[26:29], v[214:217], v[182:185], v[26:29]
	v_mfma_f32_16x16x32_bf16 v[18:21], v[206:209], v[190:193], v[18:21]
	v_mfma_f32_16x16x32_bf16 v[10:13], v[214:217], v[190:193], v[10:13]
	v_mfma_f32_16x16x32_bf16 v[6:9], v[206:209], v[198:201], v[6:9]
	v_mfma_f32_16x16x32_bf16 v[2:5], v[214:217], v[198:201], v[2:5]
	s_add_i32 s46, s46, 2
	s_add_u32 s14, s14, 0x100
	s_addc_u32 s15, s15, 0
	s_add_u32 s13, s13, 0x100
	s_addc_u32 s45, s45, 0
	s_cmp_gt_u32 s46, 13
	s_barrier
	s_cbranch_scc0 .LBB0_2145
	s_mul_hi_i32 s13, s43, 0x38e38e39
	s_lshr_b32 s14, s13, 31
	s_ashr_i32 s13, s13, 1
	s_add_i32 s13, s13, s14
	s_mul_i32 s14, s13, -9
	s_add_i32 s14, s14, s43
	s_mulk_i32 s13, 0x900
	s_lshl_b32 s14, s14, 8
	s_add_i32 s14, s14, s13
	v_add_u32_e32 v154, s14, v1
	v_lshl_or_b32 v146, s44, 8, v149
	v_ashrrev_i32_e32 v155, 31, v154
	v_ashrrev_i32_e32 v147, 31, v146
	v_lshlrev_b64 v[156:157], 12, v[154:155]
	v_lshl_add_u64 v[156:157], s[8:9], 0, v[156:157]
	v_lshlrev_b64 v[158:159], 1, v[146:147]
	v_lshl_add_u64 v[146:147], v[156:157], 0, v[158:159]
	v_cvt_pk_bf16_f32 v126, v126, v127
	v_cvt_pk_bf16_f32 v127, v128, v129
	v_cvt_pk_bf16_f32 v128, v122, v123
	v_cvt_pk_bf16_f32 v129, v124, v125
	global_store_dwordx4 v[146:147], v[126:129], off
	v_cvt_pk_bf16_f32 v118, v118, v119
	v_cvt_pk_bf16_f32 v119, v120, v121
	v_cvt_pk_bf16_f32 v120, v110, v111
	v_or_b32_e32 v110, 16, v154
	v_ashrrev_i32_e32 v111, 31, v110
	v_lshlrev_b64 v[110:111], 12, v[110:111]
	v_lshl_add_u64 v[110:111], s[8:9], 0, v[110:111]
	v_cvt_pk_bf16_f32 v121, v112, v113
	global_store_dwordx4 v[146:147], v[118:121], off offset:256
	s_mov_b32 s13, 0x80000
	s_mov_b64 s[14:15], 0x80000
	v_lshl_add_u64 v[118:119], v[110:111], 0, v[158:159]
	v_cvt_pk_bf16_f32 v110, v114, v115
	v_cvt_pk_bf16_f32 v111, v116, v117
	v_cvt_pk_bf16_f32 v112, v106, v107
	v_cvt_pk_bf16_f32 v113, v108, v109
	global_store_dwordx4 v[118:119], v[110:113], off
	v_cvt_pk_bf16_f32 v102, v102, v103
	v_cvt_pk_bf16_f32 v103, v104, v105
	v_cvt_pk_bf16_f32 v104, v94, v95
	v_or_b32_e32 v94, 32, v154
	v_ashrrev_i32_e32 v95, 31, v94
	v_lshlrev_b64 v[94:95], 12, v[94:95]
	v_lshl_add_u64 v[94:95], s[8:9], 0, v[94:95]
	v_cvt_pk_bf16_f32 v105, v96, v97
	global_store_dwordx4 v[118:119], v[102:105], off offset:256
	s_mov_b32 s44, s12
	s_mov_b32 s43, s42
	v_lshl_add_u64 v[102:103], v[94:95], 0, v[158:159]
	v_cvt_pk_bf16_f32 v94, v98, v99
	v_cvt_pk_bf16_f32 v95, v100, v101
	v_cvt_pk_bf16_f32 v96, v90, v91
	v_cvt_pk_bf16_f32 v97, v92, v93
	global_store_dwordx4 v[102:103], v[94:97], off
	v_cvt_pk_bf16_f32 v86, v86, v87
	v_cvt_pk_bf16_f32 v87, v88, v89
	v_cvt_pk_bf16_f32 v88, v78, v79
	v_or_b32_e32 v78, 48, v154
	v_ashrrev_i32_e32 v79, 31, v78
	v_lshlrev_b64 v[78:79], 12, v[78:79]
	v_lshl_add_u64 v[78:79], s[8:9], 0, v[78:79]
	v_cvt_pk_bf16_f32 v89, v80, v81
	global_store_dwordx4 v[102:103], v[86:89], off offset:256
	s_mov_b64 s[16:17], s[4:5]
	s_nop 0
	v_lshl_add_u64 v[86:87], v[78:79], 0, v[158:159]
	v_cvt_pk_bf16_f32 v78, v82, v83
	v_cvt_pk_bf16_f32 v79, v84, v85
	v_cvt_pk_bf16_f32 v80, v74, v75
	v_cvt_pk_bf16_f32 v81, v76, v77
	global_store_dwordx4 v[86:87], v[78:81], off
	v_cvt_pk_bf16_f32 v70, v70, v71
	v_cvt_pk_bf16_f32 v71, v72, v73
	v_cvt_pk_bf16_f32 v72, v66, v67
	v_cvt_pk_bf16_f32 v73, v68, v69
	global_store_dwordx4 v[86:87], v[70:73], off offset:256
	v_cvt_pk_bf16_f32 v62, v62, v63
	v_cvt_pk_bf16_f32 v63, v64, v65
	v_cvt_pk_bf16_f32 v64, v58, v59
	v_add_co_u32_e32 v58, vcc, s13, v146
	v_lshl_add_u64 v[66:67], v[146:147], 0, s[14:15]
	s_nop 0
	v_addc_co_u32_e32 v59, vcc, 0, v147, vcc
	s_mov_b32 s13, 0x90000
	v_cvt_pk_bf16_f32 v65, v60, v61
	global_store_dwordx4 v[58:59], v[62:65], off
	v_cvt_pk_bf16_f32 v50, v50, v51
	v_cvt_pk_bf16_f32 v51, v52, v53
	v_cvt_pk_bf16_f32 v52, v42, v43
	v_cvt_pk_bf16_f32 v53, v44, v45
	global_store_dwordx4 v[66:67], v[50:53], off offset:256
	s_mov_b64 s[14:15], 0x90000
	v_cvt_pk_bf16_f32 v42, v54, v55
	v_cvt_pk_bf16_f32 v43, v56, v57
	v_cvt_pk_bf16_f32 v44, v46, v47
	v_add_co_u32_e32 v46, vcc, s13, v146
	v_lshl_add_u64 v[50:51], v[146:147], 0, s[14:15]
	s_nop 0
	v_addc_co_u32_e32 v47, vcc, 0, v147, vcc
	s_mov_b32 s13, 0xa0000
	v_cvt_pk_bf16_f32 v45, v48, v49
	global_store_dwordx4 v[46:47], v[42:45], off
	v_cvt_pk_bf16_f32 v34, v34, v35
	v_cvt_pk_bf16_f32 v35, v36, v37
	v_cvt_pk_bf16_f32 v36, v26, v27
	v_cvt_pk_bf16_f32 v37, v28, v29
	global_store_dwordx4 v[50:51], v[34:37], off offset:256
	s_mov_b64 s[14:15], 0xa0000
	v_cvt_pk_bf16_f32 v26, v38, v39
	v_cvt_pk_bf16_f32 v27, v40, v41
	v_cvt_pk_bf16_f32 v28, v30, v31
	v_add_co_u32_e32 v30, vcc, s13, v146
	v_lshl_add_u64 v[34:35], v[146:147], 0, s[14:15]
	s_nop 0
	v_addc_co_u32_e32 v31, vcc, 0, v147, vcc
	v_cvt_pk_bf16_f32 v29, v32, v33
	global_store_dwordx4 v[30:31], v[26:29], off
	v_cvt_pk_bf16_f32 v18, v18, v19
	v_cvt_pk_bf16_f32 v19, v20, v21
	v_cvt_pk_bf16_f32 v20, v10, v11
	v_cvt_pk_bf16_f32 v21, v12, v13
	global_store_dwordx4 v[34:35], v[18:21], off offset:256
	v_cvt_pk_bf16_f32 v10, v22, v23
	v_cvt_pk_bf16_f32 v11, v24, v25
	v_cvt_pk_bf16_f32 v12, v14, v15
	v_add_co_u32_e32 v14, vcc, s41, v146
	s_mov_b64 s[14:15], 0xb0000
	s_nop 0
	v_addc_co_u32_e32 v15, vcc, 0, v147, vcc
	v_lshl_add_u64 v[18:19], v[146:147], 0, s[14:15]
	s_and_b64 vcc, exec, s[0:1]
	s_mov_b64 s[14:15], s[2:3]
	v_cvt_pk_bf16_f32 v13, v16, v17
	global_store_dwordx4 v[14:15], v[10:13], off
	v_cvt_pk_bf16_f32 v6, v6, v7
	v_cvt_pk_bf16_f32 v7, v8, v9
	v_cvt_pk_bf16_f32 v8, v2, v3
	v_cvt_pk_bf16_f32 v9, v4, v5
	global_store_dwordx4 v[18:19], v[6:9], off offset:256
	s_cbranch_vccz .LBB0_2138
	s_waitcnt vmcnt(0)
	s_cmpk_gt_u32 s22, 0xff
	s_cbranch_scc1 .LBB0_2149
	s_barrier

.LBB0_2151:
	s_cmp_gt_i32 s55, 12
	s_cselect_b64 s[2:3], -1, 0
	s_and_b64 s[0:1], s[6:7], s[2:3]
	s_andn2_b64 vcc, exec, s[0:1]
	s_cbranch_vccnz .LBB0_2201
	s_waitcnt vmcnt(0)
	s_barrier
	s_setprio 0
	s_mov_b64 s[0:1], exec
	v_readlane_b32 s4, v250, 5
	v_readlane_b32 s5, v250, 6
	s_and_b64 s[4:5], s[0:1], s[4:5]
	s_mov_b64 exec, s[4:5]
	s_cbranch_execz .LBB0_2200
	s_add_i32 s4, 0, 0x27ff0
	v_mov_b32_e32 v1, s4
	s_waitcnt vmcnt(0) expcnt(0) lgkmcnt(0)
	ds_read_b32 v3, v1
	s_add_i32 s4, 0, 0x27ff4
	v_mov_b32_e32 v1, s4
	ds_read_b32 v1, v1
	s_waitcnt lgkmcnt(1)
	v_cmp_ne_u32_e32 vcc, 0, v3
	s_cbranch_vccnz .LBB0_2168
	v_readlane_b32 s4, v250, 2
	v_readlane_b32 s5, v250, 3
	s_load_dwordx2 s[8:9], s[4:5], 0x4
	s_add_u32 s4, s52, 0x1000
	s_addc_u32 s5, s53, 0
	s_add_u32 s6, s52, 0x1100
	s_addc_u32 s7, s53, 0
	v_readlane_b32 s10, v250, 1
	s_waitcnt lgkmcnt(0)
	s_mul_i32 s18, s8, s10
	s_add_u32 s8, s52, 0x1200
	s_mul_i32 s18, s18, s9
	s_addc_u32 s9, s53, 0
	s_add_u32 s10, s52, 0x1300
	s_addc_u32 s11, s53, 0
	s_mov_b32 s19, 1
	v_mov_b32_e32 v17, 0
	s_branch .LBB0_2156

.LBB0_2210:
	s_cmp_gt_i32 s55, 13
	s_cselect_b64 s[2:3], -1, 0
	s_and_b64 s[0:1], s[0:1], s[2:3]
	s_andn2_b64 vcc, exec, s[0:1]
	s_cbranch_vccnz .LBB0_2260
	s_waitcnt vmcnt(0)
	s_barrier
	s_setprio 0
	s_mov_b64 s[0:1], exec
	v_readlane_b32 s4, v250, 5
	v_readlane_b32 s5, v250, 6
	s_and_b64 s[4:5], s[0:1], s[4:5]
	s_mov_b64 exec, s[4:5]
	s_cbranch_execz .LBB0_2259
	s_add_i32 s4, 0, 0x27ff0
	v_mov_b32_e32 v1, s4
	s_waitcnt vmcnt(0) expcnt(0) lgkmcnt(0)
	ds_read_b32 v3, v1
	s_add_i32 s4, 0, 0x27ff4
	v_mov_b32_e32 v1, s4
	ds_read_b32 v1, v1
	s_waitcnt lgkmcnt(1)
	v_cmp_ne_u32_e32 vcc, 0, v3
	s_cbranch_vccnz .LBB0_2227
	v_readlane_b32 s4, v250, 2
	v_readlane_b32 s5, v250, 3
	s_load_dwordx2 s[8:9], s[4:5], 0x4
	s_add_u32 s4, s52, 0x1000
	s_addc_u32 s5, s53, 0
	s_add_u32 s6, s52, 0x1100
	s_addc_u32 s7, s53, 0
	v_readlane_b32 s10, v250, 1
	s_waitcnt lgkmcnt(0)
	s_mul_i32 s18, s8, s10
	s_add_u32 s8, s52, 0x1200
	s_mul_i32 s18, s18, s9
	s_addc_u32 s9, s53, 0
	s_add_u32 s10, s52, 0x1300
	s_addc_u32 s11, s53, 0
	s_mov_b32 s19, 1
	v_mov_b32_e32 v17, 0
	s_branch .LBB0_2215

.LBB0_2276:
	s_or_b64 exec, exec, s[8:9]
	s_cmpk_gt_i32 s33, 0x40f
	v_readfirstlane_b32 s41, v0
	s_waitcnt lgkmcnt(0)
	s_barrier
	s_barrier
	s_cbranch_scc1 .LBB0_2288
	v_lshlrev_b32_e32 v1, 4, v0
	s_waitcnt vmcnt(11)
	v_bfe_u32 v2, v0, 3, 25
	v_and_b32_e32 v5, 32, v0
	v_or_b32_e32 v2, 64, v2
	v_bfe_u32 v3, v0, 2, 4
	s_movk_i32 s0, 0x70
	v_bitop3_b32 v1, v1, v5, 48 bitop3:0x6c
	s_add_u32 s42, s6, 0x1370000
	v_and_or_b32 v4, v2, s0, v3
	v_and_or_b32 v1, v0, 64, v1
	s_addc_u32 s43, s7, 0
	v_lshl_or_b32 v132, v4, 9, v1
	v_lshrrev_b32_e32 v4, 5, v0
	s_waitcnt vmcnt(10)
	v_lshrrev_b32_e32 v6, 1, v0
	s_add_u32 s44, s6, 0x950000
	v_and_b32_e32 v4, 4, v4
	v_bfe_u32 v5, v0, 2, 2
	s_waitcnt vmcnt(9)
	v_and_b32_e32 v10, 24, v6
	s_addc_u32 s45, s7, 0
	v_or3_b32 v4, v4, v5, v10
	s_movk_i32 s0, 0x60
	s_ashr_i32 s47, s33, 31
	v_and_or_b32 v2, v2, s0, v4
	s_lshr_b32 s0, s47, 29
	s_add_i32 s0, s33, s0
	s_lshr_b32 s8, s41, 6
	s_ashr_i32 s2, s0, 3
	s_and_b32 s0, s0, -8
	s_lshr_b32 s1, s41, 8
	s_lshl_b32 s46, s8, 10
	s_sub_i32 s0, s33, s0
	s_cmp_lt_i32 s0, 0
	s_movk_i32 s48, 0x83
	s_cselect_b32 s3, s48, 0x82
	s_mul_i32 s0, s3, s0
	s_add_i32 s0, s0, s2
	s_mul_hi_i32 s2, s0, 0x7e07e07f
	s_lshr_b32 s3, s2, 31
	s_ashr_i32 s2, s2, 8
	s_add_i32 s2, s2, s3
	s_lshl_b32 s3, s2, 3
	s_mulk_i32 s2, 0x208
	s_sub_i32 s2, s0, s2
	s_bfe_u32 s0, s2, 0x3001c
	s_add_i32 s9, s2, s0
	s_sext_i32_i16 s0, s9
	s_and_b32 s9, s9, 0xfff8
	s_sub_i32 s2, s2, s9
	s_sext_i32_i16 s2, s2
	s_add_i32 s18, s3, s2
	s_ashr_i32 s19, s18, 31
	s_lshr_b32 s0, s0, 3
	s_lshl_b64 s[2:3], s[18:19], 17
	s_add_u32 s20, s42, s2
	s_addc_u32 s21, s43, s3
	s_bfe_i64 s[2:3], s[0:1], 0x100000
	s_lshl_b64 s[2:3], s[2:3], 17
	v_lshl_or_b32 v134, v2, 9, v1
	v_lshrrev_b32_e32 v2, 3, v0
	s_add_u32 s22, s44, s2
	v_and_or_b32 v3, v2, 48, v3
	v_and_or_b32 v2, v2, 32, v4
	s_addc_u32 s23, s45, s3
	s_add_i32 s19, s46, 0
	v_lshl_or_b32 v138, v2, 9, v1
	s_add_i32 m0, s19, 0x10000
	v_lshl_or_b32 v136, v3, 9, v1
	global_load_lds_dwordx4 v138, s[22:23]
	s_add_i32 m0, s19, 0x12000
	s_add_i32 s49, s19, 0x2000
	global_load_lds_dwordx4 v134, s[22:23]
	s_mov_b32 m0, s19
	s_add_u32 s2, s22, 0x10000
	global_load_lds_dwordx4 v136, s[20:21]
	s_mov_b32 m0, s49
	s_addc_u32 s3, s23, 0
	global_load_lds_dwordx4 v132, s[20:21]
	s_add_i32 m0, s19, 0x14000
	v_mov_b32_e32 v139, 0
	global_load_lds_dwordx4 v138, s[2:3]
	s_add_i32 m0, s19, 0x16000
	v_mov_b32_e32 v135, v139
	global_load_lds_dwordx4 v134, s[2:3]
	s_add_u32 s2, s20, 0x10000
	s_addc_u32 s3, s21, 0
	s_add_i32 s50, s19, 0x4000
	s_mov_b32 m0, s50
	s_add_i32 s51, s19, 0x6000
	global_load_lds_dwordx4 v136, s[2:3]
	s_mov_b32 m0, s51
	v_mov_b32_e32 v137, v139
	global_load_lds_dwordx4 v132, s[2:3]
	v_mov_b32_e32 v133, v139
	s_mov_b32 s52, 0
	v_lshl_add_u64 v[8:9], s[22:23], 0, v[138:139]
	v_lshl_add_u64 v[6:7], s[22:23], 0, v[134:135]
	v_lshl_add_u64 v[4:5], s[20:21], 0, v[136:137]
	s_setprio 1
	s_cmp_lg_u32 s1, 1
	v_lshl_add_u64 v[2:3], s[20:21], 0, v[132:133]
	s_cbranch_scc1 .LBB0_2279
	s_barrier
	s_setprio 0

.LBB0_2283:
	s_add_u32 s29, s20, s28
	s_addc_u32 s39, s21, 0
	s_add_u32 s34, s29, 0x100
	s_addc_u32 s35, s39, 0
	s_and_b64 s[30:31], s[26:27], exec
	s_cselect_b32 s35, s13, s35
	s_cselect_b32 s34, s59, s34
	s_add_u32 s28, s22, s28
	s_addc_u32 s30, s23, 0
	s_add_u32 s28, s28, 0x100
	s_addc_u32 s30, s30, 0
	s_and_b64 s[26:27], s[26:27], exec
	s_cselect_b32 s37, s11, s30
	s_cselect_b32 s36, s60, s28
	s_add_u32 s38, s29, 0x10080
	s_addc_u32 s39, s39, 0
	s_add_i32 s70, s56, s46
	s_add_i32 m0, s19, 0xc000
	s_add_i32 s71, s19, 0xe000
	s_add_i32 s69, s70, 0x2000
	s_add_u32 s30, s36, 0x10000
	s_addc_u32 s31, s37, 0
	s_add_i32 s68, s57, s46
	ds_read_b128 v[144:147], v151
	ds_read_b128 v[156:159], v151 offset:1024
	ds_read_b128 v[160:163], v151 offset:2048
	ds_read_b128 v[164:167], v151 offset:3072
	s_add_i32 s67, s68, 0x2000
	s_add_i32 s66, 0, 0x18000
	s_add_u32 s28, s34, 0x10000
	s_addc_u32 s29, s35, 0
	s_add_i32 s65, s66, s46
	s_add_i32 s64, 0, 0x1c000
	s_add_i32 s63, s65, 0x2000
	s_add_u32 s26, s36, 0x10080
	s_addc_u32 s27, s37, 0
	s_add_i32 s62, s64, s46
	s_add_i32 s61, s62, 0x2000
	v_lshl_add_u64 v[148:149], s[38:39], 0, v[136:137]
	ds_read_b128 v[168:171], v152
	ds_read_b128 v[172:175], v152 offset:1024
	ds_read_b128 v[176:179], v152 offset:2048
	ds_read_b128 v[180:183], v152 offset:3072
	ds_read_b128 v[184:187], v152 offset:4096
	ds_read_b128 v[188:191], v152 offset:5120
	ds_read_b128 v[192:195], v152 offset:6144
	ds_read_b128 v[196:199], v152 offset:7168
	global_load_lds_dwordx4 v[148:149], off
	v_lshl_add_u64 v[148:149], s[38:39], 0, v[132:133]
	s_mov_b32 m0, s71
	s_nop 0
	global_load_lds_dwordx4 v[148:149], off
	s_waitcnt lgkmcnt(8)
	s_barrier
	s_waitcnt lgkmcnt(0)
	s_waitcnt lgkmcnt(0)
	v_mfma_f32_16x16x32_bf16 v[126:129], v[144:147], v[168:171], v[126:129]
	v_mfma_f32_16x16x32_bf16 v[122:125], v[160:163], v[168:171], v[122:125]
	v_mfma_f32_16x16x32_bf16 v[110:113], v[144:147], v[176:179], v[110:113]
	v_mfma_f32_16x16x32_bf16 v[106:109], v[160:163], v[176:179], v[106:109]
	v_mfma_f32_16x16x32_bf16 v[94:97], v[144:147], v[184:187], v[94:97]
	v_mfma_f32_16x16x32_bf16 v[90:93], v[160:163], v[184:187], v[90:93]
	v_mfma_f32_16x16x32_bf16 v[78:81], v[144:147], v[192:195], v[78:81]
	v_mfma_f32_16x16x32_bf16 v[74:77], v[160:163], v[192:195], v[74:77]
	v_mfma_f32_16x16x32_bf16 v[126:129], v[156:159], v[172:175], v[126:129]
	v_mfma_f32_16x16x32_bf16 v[122:125], v[164:167], v[172:175], v[122:125]
	v_mfma_f32_16x16x32_bf16 v[110:113], v[156:159], v[180:183], v[110:113]
	v_mfma_f32_16x16x32_bf16 v[106:109], v[164:167], v[180:183], v[106:109]
	v_mfma_f32_16x16x32_bf16 v[94:97], v[156:159], v[188:191], v[94:97]
	v_mfma_f32_16x16x32_bf16 v[90:93], v[164:167], v[188:191], v[90:93]
	v_mfma_f32_16x16x32_bf16 v[78:81], v[156:159], v[196:199], v[78:81]
	v_mfma_f32_16x16x32_bf16 v[74:77], v[164:167], v[196:199], v[74:77]
	s_barrier
	s_mov_b32 m0, s70
	v_lshl_add_u64 v[148:149], s[36:37], 0, v[138:139]
	ds_read_b128 v[200:203], v153
	ds_read_b128 v[204:207], v153 offset:1024
	ds_read_b128 v[208:211], v153 offset:2048
	ds_read_b128 v[212:215], v153 offset:3072
	global_load_lds_dwordx4 v[148:149], off
	v_lshl_add_u64 v[216:217], s[36:37], 0, v[134:135]
	s_mov_b32 m0, s69
	s_nop 0
	global_load_lds_dwordx4 v[216:217], off
	s_barrier
	s_waitcnt lgkmcnt(0)
	s_waitcnt lgkmcnt(0)
	v_mfma_f32_16x16x32_bf16 v[118:121], v[200:203], v[168:171], v[118:121]
	v_mfma_f32_16x16x32_bf16 v[114:117], v[208:211], v[168:171], v[114:117]
	v_mfma_f32_16x16x32_bf16 v[102:105], v[200:203], v[176:179], v[102:105]
	v_mfma_f32_16x16x32_bf16 v[98:101], v[208:211], v[176:179], v[98:101]
	v_mfma_f32_16x16x32_bf16 v[86:89], v[200:203], v[184:187], v[86:89]
	v_mfma_f32_16x16x32_bf16 v[82:85], v[208:211], v[184:187], v[82:85]
	v_mfma_f32_16x16x32_bf16 v[70:73], v[200:203], v[192:195], v[70:73]
	v_mfma_f32_16x16x32_bf16 v[66:69], v[208:211], v[192:195], v[66:69]
	v_mfma_f32_16x16x32_bf16 v[118:121], v[204:207], v[172:175], v[118:121]
	v_mfma_f32_16x16x32_bf16 v[114:117], v[212:215], v[172:175], v[114:117]
	v_mfma_f32_16x16x32_bf16 v[102:105], v[204:207], v[180:183], v[102:105]
	v_mfma_f32_16x16x32_bf16 v[98:101], v[212:215], v[180:183], v[98:101]
	v_mfma_f32_16x16x32_bf16 v[86:89], v[204:207], v[188:191], v[86:89]
	v_mfma_f32_16x16x32_bf16 v[82:85], v[212:215], v[188:191], v[82:85]
	v_mfma_f32_16x16x32_bf16 v[70:73], v[204:207], v[196:199], v[70:73]
	v_mfma_f32_16x16x32_bf16 v[66:69], v[212:215], v[196:199], v[66:69]
	s_mov_b32 m0, s19
	v_lshl_add_u64 v[218:219], s[34:35], 0, v[136:137]
	s_barrier
	ds_read_b128 v[168:171], v152 offset:16384
	ds_read_b128 v[172:175], v152 offset:17408
	ds_read_b128 v[176:179], v152 offset:18432
	ds_read_b128 v[180:183], v152 offset:19456
	ds_read_b128 v[184:187], v152 offset:20480
	ds_read_b128 v[188:191], v152 offset:21504
	ds_read_b128 v[192:195], v152 offset:22528
	ds_read_b128 v[196:199], v152 offset:23552
	global_load_lds_dwordx4 v[218:219], off
	v_lshl_add_u64 v[220:221], s[34:35], 0, v[132:133]
	s_mov_b32 m0, s49
	s_nop 0
	global_load_lds_dwordx4 v[220:221], off
	s_barrier
	s_waitcnt lgkmcnt(0)
	s_waitcnt lgkmcnt(0)
	v_mfma_f32_16x16x32_bf16 v[62:65], v[144:147], v[168:171], v[62:65]
	v_mfma_f32_16x16x32_bf16 v[58:61], v[160:163], v[168:171], v[58:61]
	v_mfma_f32_16x16x32_bf16 v[46:49], v[144:147], v[176:179], v[46:49]
	v_mfma_f32_16x16x32_bf16 v[42:45], v[160:163], v[176:179], v[42:45]
	v_mfma_f32_16x16x32_bf16 v[30:33], v[144:147], v[184:187], v[30:33]
	v_mfma_f32_16x16x32_bf16 v[26:29], v[160:163], v[184:187], v[26:29]
	v_mfma_f32_16x16x32_bf16 v[14:17], v[144:147], v[192:195], v[14:17]
	v_mfma_f32_16x16x32_bf16 v[10:13], v[160:163], v[192:195], v[10:13]
	v_mfma_f32_16x16x32_bf16 v[62:65], v[156:159], v[172:175], v[62:65]
	v_mfma_f32_16x16x32_bf16 v[58:61], v[164:167], v[172:175], v[58:61]
	v_mfma_f32_16x16x32_bf16 v[46:49], v[156:159], v[180:183], v[46:49]
	v_mfma_f32_16x16x32_bf16 v[42:45], v[164:167], v[180:183], v[42:45]
	v_mfma_f32_16x16x32_bf16 v[30:33], v[156:159], v[188:191], v[30:33]
	v_mfma_f32_16x16x32_bf16 v[26:29], v[164:167], v[188:191], v[26:29]
	v_mfma_f32_16x16x32_bf16 v[14:17], v[156:159], v[196:199], v[14:17]
	v_mfma_f32_16x16x32_bf16 v[10:13], v[164:167], v[196:199], v[10:13]
	s_barrier
	s_mov_b32 m0, s68
	v_lshl_add_u64 v[144:145], s[30:31], 0, v[138:139]
	global_load_lds_dwordx4 v[144:145], off
	v_lshl_add_u64 v[144:145], s[30:31], 0, v[134:135]
	s_mov_b32 m0, s67
	s_nop 0
	global_load_lds_dwordx4 v[144:145], off
	s_waitcnt vmcnt(6)
	s_barrier
	v_mfma_f32_16x16x32_bf16 v[54:57], v[200:203], v[168:171], v[54:57]
	v_mfma_f32_16x16x32_bf16 v[50:53], v[208:211], v[168:171], v[50:53]
	v_mfma_f32_16x16x32_bf16 v[38:41], v[200:203], v[176:179], v[38:41]
	v_mfma_f32_16x16x32_bf16 v[34:37], v[208:211], v[176:179], v[34:37]
	v_mfma_f32_16x16x32_bf16 v[22:25], v[200:203], v[184:187], v[22:25]
	v_mfma_f32_16x16x32_bf16 v[18:21], v[208:211], v[184:187], v[18:21]
	v_mfma_f32_16x16x32_bf16 v[6:9], v[200:203], v[192:195], v[6:9]
	v_mfma_f32_16x16x32_bf16 v[2:5], v[208:211], v[192:195], v[2:5]
	v_mfma_f32_16x16x32_bf16 v[54:57], v[204:207], v[172:175], v[54:57]
	v_mfma_f32_16x16x32_bf16 v[50:53], v[212:215], v[172:175], v[50:53]
	v_mfma_f32_16x16x32_bf16 v[38:41], v[204:207], v[180:183], v[38:41]
	v_mfma_f32_16x16x32_bf16 v[34:37], v[212:215], v[180:183], v[34:37]
	v_mfma_f32_16x16x32_bf16 v[22:25], v[204:207], v[188:191], v[22:25]
	v_mfma_f32_16x16x32_bf16 v[18:21], v[212:215], v[188:191], v[18:21]
	v_mfma_f32_16x16x32_bf16 v[6:9], v[204:207], v[196:199], v[6:9]
	v_mfma_f32_16x16x32_bf16 v[2:5], v[212:215], v[196:199], v[2:5]
	v_add_u32_e32 v164, s66, v131
	s_barrier
	ds_read_b128 v[144:147], v164
	ds_read_b128 v[156:159], v164 offset:1024
	ds_read_b128 v[160:163], v164 offset:2048
	ds_read_b128 v[164:167], v164 offset:3072
	s_mov_b32 m0, s50
	v_lshl_add_u64 v[200:201], s[28:29], 0, v[136:137]
	ds_read_b128 v[168:171], v152 offset:32768
	ds_read_b128 v[172:175], v152 offset:33792
	ds_read_b128 v[176:179], v152 offset:34816
	ds_read_b128 v[180:183], v152 offset:35840
	ds_read_b128 v[184:187], v152 offset:36864
	ds_read_b128 v[188:191], v152 offset:37888
	ds_read_b128 v[192:195], v152 offset:38912
	ds_read_b128 v[196:199], v152 offset:39936
	global_load_lds_dwordx4 v[200:201], off
	v_lshl_add_u64 v[200:201], s[28:29], 0, v[132:133]
	s_mov_b32 m0, s51
	s_nop 0
	global_load_lds_dwordx4 v[200:201], off
	s_waitcnt lgkmcnt(8)
	s_barrier
	s_waitcnt lgkmcnt(0)
	s_waitcnt lgkmcnt(0)
	v_mfma_f32_16x16x32_bf16 v[126:129], v[144:147], v[168:171], v[126:129]
	v_mfma_f32_16x16x32_bf16 v[122:125], v[160:163], v[168:171], v[122:125]
	v_mfma_f32_16x16x32_bf16 v[110:113], v[144:147], v[176:179], v[110:113]
	v_mfma_f32_16x16x32_bf16 v[106:109], v[160:163], v[176:179], v[106:109]
	v_mfma_f32_16x16x32_bf16 v[94:97], v[144:147], v[184:187], v[94:97]
	v_mfma_f32_16x16x32_bf16 v[90:93], v[160:163], v[184:187], v[90:93]
	v_mfma_f32_16x16x32_bf16 v[78:81], v[144:147], v[192:195], v[78:81]
	v_mfma_f32_16x16x32_bf16 v[74:77], v[160:163], v[192:195], v[74:77]
	v_mfma_f32_16x16x32_bf16 v[126:129], v[156:159], v[172:175], v[126:129]
	v_mfma_f32_16x16x32_bf16 v[122:125], v[164:167], v[172:175], v[122:125]
	v_mfma_f32_16x16x32_bf16 v[110:113], v[156:159], v[180:183], v[110:113]
	v_mfma_f32_16x16x32_bf16 v[106:109], v[164:167], v[180:183], v[106:109]
	v_mfma_f32_16x16x32_bf16 v[94:97], v[156:159], v[188:191], v[94:97]
	v_mfma_f32_16x16x32_bf16 v[90:93], v[164:167], v[188:191], v[90:93]
	v_mfma_f32_16x16x32_bf16 v[78:81], v[156:159], v[196:199], v[78:81]
	v_mfma_f32_16x16x32_bf16 v[74:77], v[164:167], v[196:199], v[74:77]
	s_barrier
	s_mov_b32 m0, s65
	v_add_u32_e32 v212, s64, v131
	v_lshl_add_u64 v[148:149], v[148:149], 0, s[8:9]
	ds_read_b128 v[200:203], v212
	ds_read_b128 v[204:207], v212 offset:1024
	ds_read_b128 v[208:211], v212 offset:2048
	ds_read_b128 v[212:215], v212 offset:3072
	global_load_lds_dwordx4 v[148:149], off
	v_lshl_add_u64 v[148:149], v[216:217], 0, s[8:9]
	s_mov_b32 m0, s63
	s_nop 0
	global_load_lds_dwordx4 v[148:149], off
	s_barrier
	s_waitcnt lgkmcnt(0)
	s_waitcnt lgkmcnt(0)
	v_mfma_f32_16x16x32_bf16 v[118:121], v[200:203], v[168:171], v[118:121]
	v_mfma_f32_16x16x32_bf16 v[114:117], v[208:211], v[168:171], v[114:117]
	v_mfma_f32_16x16x32_bf16 v[102:105], v[200:203], v[176:179], v[102:105]
	v_mfma_f32_16x16x32_bf16 v[98:101], v[208:211], v[176:179], v[98:101]
	v_mfma_f32_16x16x32_bf16 v[86:89], v[200:203], v[184:187], v[86:89]
	v_mfma_f32_16x16x32_bf16 v[82:85], v[208:211], v[184:187], v[82:85]
	v_mfma_f32_16x16x32_bf16 v[70:73], v[200:203], v[192:195], v[70:73]
	v_mfma_f32_16x16x32_bf16 v[66:69], v[208:211], v[192:195], v[66:69]
	v_mfma_f32_16x16x32_bf16 v[118:121], v[204:207], v[172:175], v[118:121]
	v_mfma_f32_16x16x32_bf16 v[114:117], v[212:215], v[172:175], v[114:117]
	v_mfma_f32_16x16x32_bf16 v[102:105], v[204:207], v[180:183], v[102:105]
	v_mfma_f32_16x16x32_bf16 v[98:101], v[212:215], v[180:183], v[98:101]
	v_mfma_f32_16x16x32_bf16 v[86:89], v[204:207], v[188:191], v[86:89]
	v_mfma_f32_16x16x32_bf16 v[82:85], v[212:215], v[188:191], v[82:85]
	v_mfma_f32_16x16x32_bf16 v[70:73], v[204:207], v[196:199], v[70:73]
	v_mfma_f32_16x16x32_bf16 v[66:69], v[212:215], v[196:199], v[66:69]
	s_mov_b32 m0, s53
	v_lshl_add_u64 v[148:149], v[218:219], 0, s[8:9]
	s_barrier
	ds_read_b128 v[168:171], v152 offset:49152
	ds_read_b128 v[172:175], v152 offset:50176
	ds_read_b128 v[176:179], v152 offset:51200
	ds_read_b128 v[180:183], v152 offset:52224
	ds_read_b128 v[184:187], v152 offset:53248
	ds_read_b128 v[188:191], v152 offset:54272
	ds_read_b128 v[192:195], v152 offset:55296
	ds_read_b128 v[196:199], v152 offset:56320
	global_load_lds_dwordx4 v[148:149], off
	v_lshl_add_u64 v[148:149], v[220:221], 0, s[8:9]
	s_mov_b32 m0, s54
	s_nop 0
	global_load_lds_dwordx4 v[148:149], off
	s_barrier
	s_waitcnt lgkmcnt(0)
	s_waitcnt lgkmcnt(0)
	v_mfma_f32_16x16x32_bf16 v[62:65], v[144:147], v[168:171], v[62:65]
	v_mfma_f32_16x16x32_bf16 v[58:61], v[160:163], v[168:171], v[58:61]
	v_mfma_f32_16x16x32_bf16 v[46:49], v[144:147], v[176:179], v[46:49]
	v_mfma_f32_16x16x32_bf16 v[42:45], v[160:163], v[176:179], v[42:45]
	v_mfma_f32_16x16x32_bf16 v[30:33], v[144:147], v[184:187], v[30:33]
	v_mfma_f32_16x16x32_bf16 v[26:29], v[160:163], v[184:187], v[26:29]
	v_mfma_f32_16x16x32_bf16 v[14:17], v[144:147], v[192:195], v[14:17]
	v_mfma_f32_16x16x32_bf16 v[10:13], v[160:163], v[192:195], v[10:13]
	v_mfma_f32_16x16x32_bf16 v[62:65], v[156:159], v[172:175], v[62:65]
	v_mfma_f32_16x16x32_bf16 v[58:61], v[164:167], v[172:175], v[58:61]
	v_mfma_f32_16x16x32_bf16 v[46:49], v[156:159], v[180:183], v[46:49]
	v_mfma_f32_16x16x32_bf16 v[42:45], v[164:167], v[180:183], v[42:45]
	v_mfma_f32_16x16x32_bf16 v[30:33], v[156:159], v[188:191], v[30:33]
	v_mfma_f32_16x16x32_bf16 v[26:29], v[164:167], v[188:191], v[26:29]
	v_mfma_f32_16x16x32_bf16 v[14:17], v[156:159], v[196:199], v[14:17]
	v_mfma_f32_16x16x32_bf16 v[10:13], v[164:167], v[196:199], v[10:13]
	s_barrier
	s_mov_b32 m0, s62
	v_lshl_add_u64 v[144:145], s[26:27], 0, v[138:139]
	global_load_lds_dwordx4 v[144:145], off
	v_lshl_add_u64 v[144:145], s[26:27], 0, v[134:135]
	s_mov_b32 m0, s61
	s_nop 0
	global_load_lds_dwordx4 v[144:145], off
	s_waitcnt vmcnt(6)
	s_barrier
	v_mfma_f32_16x16x32_bf16 v[54:57], v[200:203], v[168:171], v[54:57]
	v_mfma_f32_16x16x32_bf16 v[50:53], v[208:211], v[168:171], v[50:53]
	v_mfma_f32_16x16x32_bf16 v[38:41], v[200:203], v[176:179], v[38:41]
	v_mfma_f32_16x16x32_bf16 v[34:37], v[208:211], v[176:179], v[34:37]
	v_mfma_f32_16x16x32_bf16 v[22:25], v[200:203], v[184:187], v[22:25]
	v_mfma_f32_16x16x32_bf16 v[18:21], v[208:211], v[184:187], v[18:21]
	v_mfma_f32_16x16x32_bf16 v[6:9], v[200:203], v[192:195], v[6:9]
	v_mfma_f32_16x16x32_bf16 v[2:5], v[208:211], v[192:195], v[2:5]
	v_mfma_f32_16x16x32_bf16 v[54:57], v[204:207], v[172:175], v[54:57]
	v_mfma_f32_16x16x32_bf16 v[50:53], v[212:215], v[172:175], v[50:53]
	v_mfma_f32_16x16x32_bf16 v[38:41], v[204:207], v[180:183], v[38:41]
	v_mfma_f32_16x16x32_bf16 v[34:37], v[212:215], v[180:183], v[34:37]
	v_mfma_f32_16x16x32_bf16 v[22:25], v[204:207], v[188:191], v[22:25]
	v_mfma_f32_16x16x32_bf16 v[18:21], v[212:215], v[188:191], v[18:21]
	v_mfma_f32_16x16x32_bf16 v[6:9], v[204:207], v[196:199], v[6:9]
	v_mfma_f32_16x16x32_bf16 v[2:5], v[212:215], v[196:199], v[2:5]
	s_movk_i32 s28, 0x100
	s_andn2_b64 vcc, exec, s[24:25]
	s_mov_b64 s[26:27], -1
	s_mov_b64 s[24:25], 0
	s_barrier
	s_cbranch_vccz .LBB0_2283
	v_lshl_add_u32 v144, s18, 8, v1
	v_ashrrev_i32_e32 v145, 31, v144
	v_lshl_add_u64 v[146:147], v[144:145], 2, s[2:3]
	global_load_dword v168, v[146:147], off
	global_load_dword v178, v[146:147], off offset:64
	global_load_dword v179, v[146:147], off offset:128
	global_load_dword v180, v[146:147], off offset:192
	global_load_dword v181, v[146:147], off offset:512
	global_load_dword v182, v[146:147], off offset:576
	global_load_dword v183, v[146:147], off offset:640
	global_load_dword v184, v[146:147], off offset:704
	s_lshl_b32 s11, s58, 8
	s_cmp_eq_u32 s58, 64
	s_cselect_b64 vcc, -1, 0
	s_mov_b32 s13, 0x17c0000
	s_and_b64 s[20:21], vcc, exec
	s_cselect_b32 s18, 0, s11
	s_cselect_b32 s13, s13, 0x22940000
	s_cselect_b32 s11, 8, 14
	v_or_b32_e32 v164, s18, v150
	s_add_u32 s20, s6, s13
	v_lshlrev_b64 v[156:157], s11, v[144:145]
	s_addc_u32 s21, s7, 0
	v_ashrrev_i32_e32 v165, 31, v164
	v_cvt_f32_i32_e32 v145, v164
	v_or_b32_e32 v158, 1, v164
	v_or_b32_e32 v159, 2, v164
	v_or_b32_e32 v161, 4, v164
	v_or_b32_e32 v166, 7, v164
	v_or_b32_e32 v160, 3, v164
	v_or_b32_e32 v162, 5, v164
	v_or_b32_e32 v163, 6, v164
	v_or_b32_e32 v167, 0x80, v164
	v_lshl_add_u64 v[148:149], v[164:165], 1, s[20:21]
	v_cvt_f32_i32_e32 v158, v158
	v_cvt_f32_i32_e32 v159, v159
	v_cvt_f32_i32_e32 v165, v161
	v_cvt_f32_i32_e32 v172, v166
	v_cvt_f32_i32_e32 v160, v160
	v_cvt_f32_i32_e32 v170, v162
	v_cvt_f32_i32_e32 v171, v163
	v_cvt_f32_i32_e32 v173, v167
	v_cndmask_b32_e32 v169, v154, v155, vcc
	v_mul_f32_e64 v163, v169, -v145
	v_lshl_add_u64 v[166:167], v[156:157], 1, v[148:149]
	v_mul_f32_e64 v162, v169, -v158
	v_mul_f32_e64 v161, v169, -v159
	v_mul_f32_e64 v159, v169, -v165
	v_mul_f32_e64 v156, v169, -v172
	v_mul_f32_e64 v160, v169, -v160
	v_mul_f32_e64 v158, v169, -v170
	v_mul_f32_e64 v157, v169, -v171
	v_mul_f32_e64 v145, v169, -v173
	s_and_b64 vcc, exec, s[0:1]
	s_mov_b32 s58, s10
	s_mov_b32 s18, s12
	s_mov_b64 s[22:23], s[16:17]
	s_mov_b64 s[20:21], s[14:15]
	s_waitcnt vmcnt(0)
	v_mul_f32_e64 v165, v163, |v168|
	v_mul_f32_e64 v170, v162, |v168|
	v_mul_f32_e64 v173, v159, |v168|
	v_mul_f32_e64 v176, v156, |v168|
	v_mul_f32_e32 v165, 0x3fb8aa3b, v165
	v_mul_f32_e64 v171, v161, |v168|
	v_mul_f32_e64 v172, v160, |v168|
	v_mul_f32_e64 v174, v158, |v168|
	v_mul_f32_e64 v175, v157, |v168|
	v_mul_f32_e32 v170, 0x3fb8aa3b, v170
	v_mul_f32_e32 v173, 0x3fb8aa3b, v173
	v_mul_f32_e32 v176, 0x3fb8aa3b, v176
	v_exp_f32_e32 v165, v165
	v_mul_f32_e64 v177, v145, |v168|
	v_mul_f32_e32 v171, 0x3fb8aa3b, v171
	v_mul_f32_e32 v172, 0x3fb8aa3b, v172
	v_mul_f32_e32 v174, 0x3fb8aa3b, v174
	v_mul_f32_e32 v175, 0x3fb8aa3b, v175
	v_exp_f32_e32 v170, v170
	v_exp_f32_e32 v173, v173
	v_exp_f32_e32 v176, v176
	v_mul_f32_e32 v177, 0x3fb8aa3b, v177
	v_exp_f32_e32 v171, v171
	v_exp_f32_e32 v172, v172
	v_exp_f32_e32 v174, v174
	v_exp_f32_e32 v175, v175
	v_exp_f32_e32 v177, v177
	v_add_f32_e32 v165, 0x3d4ccccd, v165
	v_add_f32_e32 v170, 0x3d4ccccd, v170
	v_add_f32_e32 v173, 0x3d4ccccd, v173
	v_add_f32_e32 v176, 0x3d4ccccd, v176
	v_mul_f32_e32 v126, v126, v165
	v_add_f32_e32 v171, 0x3d4ccccd, v171
	v_add_f32_e32 v172, 0x3d4ccccd, v172
	v_add_f32_e32 v174, 0x3d4ccccd, v174
	v_add_f32_e32 v175, 0x3d4ccccd, v175
	v_mul_f32_e32 v127, v127, v170
	v_mul_f32_e32 v165, v122, v173
	v_mul_f32_e32 v125, v125, v176
	v_cvt_pk_bf16_f32 v122, v126, v127
	v_or_b32_e32 v126, 0x81, v164
	v_mul_f32_e32 v128, v128, v171
	v_mul_f32_e32 v129, v129, v172
	v_mul_f32_e32 v170, v123, v174
	v_mul_f32_e32 v171, v124, v175
	v_cvt_pk_bf16_f32 v123, v128, v129
	v_cvt_pk_bf16_f32 v124, v165, v170
	v_cvt_pk_bf16_f32 v125, v171, v125
	v_cvt_f32_i32_e32 v126, v126
	global_store_dwordx4 v[166:167], v[122:125], off
	v_or_b32_e32 v129, 0x86, v164
	v_cvt_f32_i32_e32 v129, v129
	v_add_f32_e32 v122, 0x3d4ccccd, v177
	v_mul_f32_e32 v124, v118, v122
	v_or_b32_e32 v122, 0x82, v164
	v_cvt_f32_i32_e32 v122, v122
	v_mul_f32_e64 v118, v169, -v126
	v_mul_f32_e64 v123, v118, |v168|
	v_mul_f32_e32 v123, 0x3fb8aa3b, v123
	v_mul_f32_e64 v122, v169, -v122
	v_exp_f32_e32 v123, v123
	v_mul_f32_e64 v125, v122, |v168|
	v_or_b32_e32 v126, 0x83, v164
	v_mul_f32_e32 v125, 0x3fb8aa3b, v125
	v_cvt_f32_i32_e32 v126, v126
	v_exp_f32_e32 v125, v125
	v_add_f32_e32 v123, 0x3d4ccccd, v123
	v_mul_f32_e32 v127, v119, v123
	v_mul_f32_e64 v119, v169, -v126
	v_add_f32_e32 v123, 0x3d4ccccd, v125
	v_mul_f32_e64 v125, v119, |v168|
	v_mul_f32_e32 v125, 0x3fb8aa3b, v125
	v_exp_f32_e32 v125, v125
	v_or_b32_e32 v126, 0x84, v164
	v_cvt_f32_i32_e32 v126, v126
	v_mul_f32_e32 v128, v120, v123
	v_add_f32_e32 v120, 0x3d4ccccd, v125
	v_mul_f32_e32 v125, v121, v120
	v_mul_f32_e64 v120, v169, -v126
	v_mul_f32_e64 v123, v120, |v168|
	v_mul_f32_e32 v123, 0x3fb8aa3b, v123
	v_exp_f32_e32 v123, v123
	v_or_b32_e32 v121, 0x85, v164
	v_cvt_f32_i32_e32 v121, v121
	v_cvt_pk_bf16_f32 v124, v124, v127
	v_add_f32_e32 v123, 0x3d4ccccd, v123
	v_mul_f32_e32 v165, v114, v123
	v_or_b32_e32 v114, 0x87, v164
	v_cvt_f32_i32_e32 v114, v114
	v_mul_f32_e64 v121, v169, -v121
	v_mul_f32_e64 v126, v121, |v168|
	v_mul_f32_e64 v123, v169, -v129
	v_mul_f32_e32 v126, 0x3fb8aa3b, v126
	v_mul_f32_e64 v129, v123, |v168|
	v_mul_f32_e64 v114, v169, -v114
	v_exp_f32_e32 v126, v126
	v_mul_f32_e32 v129, 0x3fb8aa3b, v129
	v_mul_f32_e64 v164, v114, |v168|
	v_exp_f32_e32 v129, v129
	v_mul_f32_e32 v164, 0x3fb8aa3b, v164
	v_exp_f32_e32 v164, v164
	v_add_f32_e32 v126, 0x3d4ccccd, v126
	v_mul_f32_e32 v115, v115, v126
	v_add_f32_e32 v126, 0x3d4ccccd, v129
	v_mul_f32_e32 v116, v116, v126
	v_add_f32_e32 v126, 0x3d4ccccd, v164
	v_mul_f32_e32 v117, v117, v126
	v_cvt_pk_bf16_f32 v125, v128, v125
	v_cvt_pk_bf16_f32 v126, v165, v115
	v_cvt_pk_bf16_f32 v127, v116, v117
	v_or_b32_e32 v116, 16, v144
	v_ashrrev_i32_e32 v117, 31, v116
	global_store_dwordx4 v[166:167], v[124:127], off offset:256
	s_nop 1
	v_lshl_add_u64 v[124:125], v[116:117], 2, s[2:3]
	s_nop 1
	v_mov_b32_e32 v115, v178
	v_lshlrev_b64 v[116:117], s11, v[116:117]
	v_lshl_add_u64 v[116:117], v[116:117], 1, v[148:149]
	s_nop 0
	v_mul_f32_e64 v124, v163, |v115|
	v_mul_f32_e64 v125, v162, |v115|
	v_mul_f32_e32 v124, 0x3fb8aa3b, v124
	v_mul_f32_e32 v125, 0x3fb8aa3b, v125
	v_exp_f32_e32 v124, v124
	v_exp_f32_e32 v125, v125
	v_mul_f32_e64 v128, v159, |v115|
	v_mul_f32_e64 v126, v161, |v115|
	v_add_f32_e32 v124, 0x3d4ccccd, v124
	v_add_f32_e32 v125, 0x3d4ccccd, v125
	v_mul_f32_e32 v110, v110, v124
	v_mul_f32_e32 v111, v111, v125
	v_mul_f32_e32 v124, 0x3fb8aa3b, v128
	v_mul_f32_e64 v125, v158, |v115|
	v_mul_f32_e32 v126, 0x3fb8aa3b, v126
	v_exp_f32_e32 v124, v124
	v_mul_f32_e32 v125, 0x3fb8aa3b, v125
	v_exp_f32_e32 v126, v126
	v_exp_f32_e32 v125, v125
	v_mul_f32_e64 v127, v160, |v115|
	v_add_f32_e32 v124, 0x3d4ccccd, v124
	v_mul_f32_e32 v127, 0x3fb8aa3b, v127
	v_add_f32_e32 v126, 0x3d4ccccd, v126
	v_mul_f32_e32 v124, v106, v124
	v_add_f32_e32 v106, 0x3d4ccccd, v125
	v_mul_f32_e64 v125, v157, |v115|
	v_exp_f32_e32 v127, v127
	v_mul_f32_e32 v112, v112, v126
	v_mul_f32_e32 v125, 0x3fb8aa3b, v125
	v_mul_f32_e64 v126, v156, |v115|
	v_exp_f32_e32 v125, v125
	v_mul_f32_e32 v126, 0x3fb8aa3b, v126
	v_exp_f32_e32 v126, v126
	v_add_f32_e32 v127, 0x3d4ccccd, v127
	v_mul_f32_e32 v113, v113, v127
	v_mul_f32_e32 v127, v107, v106
	v_add_f32_e32 v106, 0x3d4ccccd, v125
	v_mul_f32_e32 v125, v108, v106
	v_add_f32_e32 v106, 0x3d4ccccd, v126
	v_mul_f32_e32 v109, v109, v106
	v_cvt_pk_bf16_f32 v106, v110, v111
	v_mul_f32_e64 v110, v145, |v115|
	v_cvt_pk_bf16_f32 v107, v112, v113
	v_mul_f32_e32 v110, 0x3fb8aa3b, v110
	v_mul_f32_e64 v111, v118, |v115|
	v_cvt_pk_bf16_f32 v108, v124, v127
	v_cvt_pk_bf16_f32 v109, v125, v109
	v_exp_f32_e32 v110, v110
	v_mul_f32_e32 v111, 0x3fb8aa3b, v111
	global_store_dwordx4 v[116:117], v[106:109], off
	v_exp_f32_e32 v111, v111
	s_nop 0
	v_mul_f32_e64 v107, v122, |v115|
	v_mul_f32_e32 v107, 0x3fb8aa3b, v107
	v_mul_f32_e64 v108, v119, |v115|
	v_exp_f32_e32 v107, v107
	v_mul_f32_e32 v108, 0x3fb8aa3b, v108
	v_exp_f32_e32 v108, v108
	v_add_f32_e32 v106, 0x3d4ccccd, v110
	v_mul_f32_e32 v102, v102, v106
	v_add_f32_e32 v106, 0x3d4ccccd, v111
	v_mul_f32_e32 v103, v103, v106
	v_add_f32_e32 v106, 0x3d4ccccd, v107
	v_mul_f32_e64 v107, v120, |v115|
	v_mul_f32_e32 v104, v104, v106
	v_add_f32_e32 v106, 0x3d4ccccd, v108
	v_mul_f32_e32 v107, 0x3fb8aa3b, v107
	v_mul_f32_e64 v108, v121, |v115|
	v_exp_f32_e32 v107, v107
	v_mul_f32_e32 v108, 0x3fb8aa3b, v108
	v_exp_f32_e32 v108, v108
	v_mul_f32_e32 v105, v105, v106
	v_add_f32_e32 v106, 0x3d4ccccd, v107
	v_mul_f32_e64 v107, v123, |v115|
	v_mul_f32_e32 v106, v98, v106
	v_add_f32_e32 v98, 0x3d4ccccd, v108
	v_mul_f32_e32 v107, 0x3fb8aa3b, v107
	v_mul_f32_e64 v108, v114, |v115|
	v_exp_f32_e32 v107, v107
	v_mul_f32_e32 v108, 0x3fb8aa3b, v108
	v_exp_f32_e32 v108, v108
	v_mul_f32_e32 v109, v99, v98
	v_add_f32_e32 v98, 0x3d4ccccd, v107
	v_mul_f32_e32 v107, v100, v98
	v_add_f32_e32 v98, 0x3d4ccccd, v108
	v_mul_f32_e32 v101, v101, v98
	v_cvt_pk_bf16_f32 v98, v102, v103
	v_cvt_pk_bf16_f32 v99, v104, v105
	v_cvt_pk_bf16_f32 v100, v106, v109
	v_cvt_pk_bf16_f32 v101, v107, v101
	global_store_dwordx4 v[116:117], v[98:101], off offset:256
	s_nop 1
	v_or_b32_e32 v98, 32, v144
	v_ashrrev_i32_e32 v99, 31, v98
	v_lshl_add_u64 v[100:101], v[98:99], 2, s[2:3]
	s_nop 1
	v_mov_b32_e32 v100, v179
	v_lshlrev_b64 v[98:99], s11, v[98:99]
	v_lshl_add_u64 v[98:99], v[98:99], 1, v[148:149]
	s_nop 0
	v_mul_f32_e64 v102, v162, |v100|
	v_mul_f32_e64 v101, v163, |v100|
	v_mul_f32_e32 v102, 0x3fb8aa3b, v102
	v_mul_f32_e64 v103, v161, |v100|
	v_mul_f32_e32 v101, 0x3fb8aa3b, v101
	v_exp_f32_e32 v102, v102
	v_mul_f32_e32 v103, 0x3fb8aa3b, v103
	v_exp_f32_e32 v101, v101
	v_exp_f32_e32 v103, v103
	v_mul_f32_e64 v104, v160, |v100|
	v_add_f32_e32 v102, 0x3d4ccccd, v102
	v_mul_f32_e32 v104, 0x3fb8aa3b, v104
	v_add_f32_e32 v101, 0x3d4ccccd, v101
	v_mul_f32_e32 v95, v95, v102
	v_mul_f32_e64 v102, v159, |v100|
	v_exp_f32_e32 v104, v104
	v_mul_f32_e32 v94, v94, v101
	v_add_f32_e32 v101, 0x3d4ccccd, v103
	v_mul_f32_e32 v102, 0x3fb8aa3b, v102
	v_mul_f32_e64 v103, v158, |v100|
	v_exp_f32_e32 v102, v102
	v_mul_f32_e32 v103, 0x3fb8aa3b, v103
	v_exp_f32_e32 v103, v103
	v_mul_f32_e32 v96, v96, v101
	v_add_f32_e32 v101, 0x3d4ccccd, v104
	v_mul_f32_e32 v97, v97, v101
	v_add_f32_e32 v101, 0x3d4ccccd, v102
	v_mul_f32_e64 v102, v157, |v100|
	v_mul_f32_e32 v101, v90, v101
	v_add_f32_e32 v90, 0x3d4ccccd, v103
	v_mul_f32_e32 v102, 0x3fb8aa3b, v102
	v_mul_f32_e64 v103, v156, |v100|
	v_exp_f32_e32 v102, v102
	v_mul_f32_e32 v103, 0x3fb8aa3b, v103
	v_exp_f32_e32 v103, v103
	v_mul_f32_e32 v104, v91, v90
	v_add_f32_e32 v90, 0x3d4ccccd, v102
	v_mul_f32_e32 v102, v92, v90
	v_add_f32_e32 v90, 0x3d4ccccd, v103
	v_mul_f32_e32 v93, v93, v90
	v_cvt_pk_bf16_f32 v90, v94, v95
	v_mul_f32_e64 v94, v145, |v100|
	v_cvt_pk_bf16_f32 v91, v96, v97
	v_mul_f32_e32 v94, 0x3fb8aa3b, v94
	v_mul_f32_e64 v95, v118, |v100|
	v_cvt_pk_bf16_f32 v92, v101, v104
	v_cvt_pk_bf16_f32 v93, v102, v93
	v_exp_f32_e32 v94, v94
	v_mul_f32_e32 v95, 0x3fb8aa3b, v95
	global_store_dwordx4 v[98:99], v[90:93], off
	v_exp_f32_e32 v95, v95
	s_nop 0
	v_mul_f32_e64 v91, v122, |v100|
	v_mul_f32_e32 v91, 0x3fb8aa3b, v91
	v_mul_f32_e64 v92, v119, |v100|
	v_exp_f32_e32 v91, v91
	v_mul_f32_e32 v92, 0x3fb8aa3b, v92
	v_exp_f32_e32 v92, v92
	v_add_f32_e32 v90, 0x3d4ccccd, v94
	v_mul_f32_e32 v86, v86, v90
	v_add_f32_e32 v90, 0x3d4ccccd, v95
	v_mul_f32_e32 v87, v87, v90
	v_add_f32_e32 v90, 0x3d4ccccd, v91
	v_mul_f32_e64 v91, v120, |v100|
	v_mul_f32_e32 v88, v88, v90
	v_add_f32_e32 v90, 0x3d4ccccd, v92
	v_mul_f32_e32 v91, 0x3fb8aa3b, v91
	v_mul_f32_e64 v92, v121, |v100|
	v_exp_f32_e32 v91, v91
	v_mul_f32_e32 v92, 0x3fb8aa3b, v92
	v_exp_f32_e32 v92, v92
	v_mul_f32_e32 v89, v89, v90
	v_add_f32_e32 v90, 0x3d4ccccd, v91
	v_mul_f32_e64 v91, v123, |v100|
	v_mul_f32_e32 v90, v82, v90
	v_add_f32_e32 v82, 0x3d4ccccd, v92
	v_mul_f32_e32 v91, 0x3fb8aa3b, v91
	v_mul_f32_e64 v92, v114, |v100|
	v_exp_f32_e32 v91, v91
	v_mul_f32_e32 v92, 0x3fb8aa3b, v92
	v_exp_f32_e32 v92, v92
	v_mul_f32_e32 v93, v83, v82
	v_add_f32_e32 v82, 0x3d4ccccd, v91
	v_mul_f32_e32 v91, v84, v82
	v_add_f32_e32 v82, 0x3d4ccccd, v92
	v_mul_f32_e32 v85, v85, v82
	v_cvt_pk_bf16_f32 v82, v86, v87
	v_cvt_pk_bf16_f32 v83, v88, v89
	v_cvt_pk_bf16_f32 v84, v90, v93
	v_cvt_pk_bf16_f32 v85, v91, v85
	global_store_dwordx4 v[98:99], v[82:85], off offset:256
	s_nop 1
	v_or_b32_e32 v82, 48, v144
	v_ashrrev_i32_e32 v83, 31, v82
	v_lshl_add_u64 v[84:85], v[82:83], 2, s[2:3]
	s_nop 1
	v_mov_b32_e32 v84, v180
	v_lshlrev_b64 v[82:83], s11, v[82:83]
	v_lshl_add_u64 v[82:83], v[82:83], 1, v[148:149]
	s_nop 0
	v_mul_f32_e64 v85, v163, |v84|
	v_mul_f32_e32 v85, 0x3fb8aa3b, v85
	v_exp_f32_e32 v85, v85
	v_mul_f32_e64 v86, v162, |v84|
	v_mul_f32_e32 v86, 0x3fb8aa3b, v86
	v_mul_f32_e64 v87, v161, |v84|
	v_add_f32_e32 v85, 0x3d4ccccd, v85
	v_exp_f32_e32 v86, v86
	v_mul_f32_e32 v78, v78, v85
	v_mul_f32_e32 v85, 0x3fb8aa3b, v87
	v_mul_f32_e64 v87, v160, |v84|
	v_exp_f32_e32 v85, v85
	v_mul_f32_e32 v87, 0x3fb8aa3b, v87
	v_exp_f32_e32 v87, v87
	v_add_f32_e32 v86, 0x3d4ccccd, v86
	v_mul_f32_e32 v79, v79, v86
	v_add_f32_e32 v85, 0x3d4ccccd, v85
	v_mul_f32_e64 v86, v159, |v84|
	v_mul_f32_e32 v80, v80, v85
	v_add_f32_e32 v85, 0x3d4ccccd, v87
	v_mul_f32_e32 v86, 0x3fb8aa3b, v86
	v_mul_f32_e64 v87, v158, |v84|
	v_exp_f32_e32 v86, v86
	v_mul_f32_e32 v87, 0x3fb8aa3b, v87
	v_exp_f32_e32 v87, v87
	v_mul_f32_e32 v81, v81, v85
	v_add_f32_e32 v85, 0x3d4ccccd, v86
	v_mul_f32_e64 v86, v157, |v84|
	v_mul_f32_e32 v85, v74, v85
	v_add_f32_e32 v74, 0x3d4ccccd, v87
	v_mul_f32_e32 v86, 0x3fb8aa3b, v86
	v_mul_f32_e64 v87, v156, |v84|
	v_exp_f32_e32 v86, v86
	v_mul_f32_e32 v87, 0x3fb8aa3b, v87
	v_exp_f32_e32 v87, v87
	v_mul_f32_e32 v88, v75, v74
	v_add_f32_e32 v74, 0x3d4ccccd, v86
	v_mul_f32_e32 v86, v76, v74
	v_add_f32_e32 v74, 0x3d4ccccd, v87
	v_mul_f32_e32 v77, v77, v74
	v_cvt_pk_bf16_f32 v74, v78, v79
	v_mul_f32_e64 v78, v145, |v84|
	v_cvt_pk_bf16_f32 v75, v80, v81
	v_mul_f32_e32 v78, 0x3fb8aa3b, v78
	v_mul_f32_e64 v79, v118, |v84|
	v_cvt_pk_bf16_f32 v76, v85, v88
	v_cvt_pk_bf16_f32 v77, v86, v77
	v_exp_f32_e32 v78, v78
	v_mul_f32_e32 v79, 0x3fb8aa3b, v79
	global_store_dwordx4 v[82:83], v[74:77], off
	v_exp_f32_e32 v79, v79
	s_nop 0
	v_mul_f32_e64 v75, v122, |v84|
	v_mul_f32_e32 v75, 0x3fb8aa3b, v75
	v_mul_f32_e64 v76, v119, |v84|
	v_exp_f32_e32 v75, v75
	v_mul_f32_e32 v76, 0x3fb8aa3b, v76
	v_exp_f32_e32 v76, v76
	v_add_f32_e32 v74, 0x3d4ccccd, v78
	v_mul_f32_e32 v70, v70, v74
	v_add_f32_e32 v74, 0x3d4ccccd, v79
	v_mul_f32_e32 v71, v71, v74
	v_add_f32_e32 v74, 0x3d4ccccd, v75
	v_mul_f32_e64 v75, v120, |v84|
	v_mul_f32_e32 v72, v72, v74
	v_add_f32_e32 v74, 0x3d4ccccd, v76
	v_mul_f32_e32 v75, 0x3fb8aa3b, v75
	v_mul_f32_e64 v76, v121, |v84|
	v_exp_f32_e32 v75, v75
	v_mul_f32_e32 v76, 0x3fb8aa3b, v76
	v_exp_f32_e32 v76, v76
	v_mul_f32_e32 v73, v73, v74
	v_add_f32_e32 v74, 0x3d4ccccd, v75
	v_mul_f32_e64 v75, v123, |v84|
	v_mul_f32_e32 v74, v66, v74
	v_add_f32_e32 v66, 0x3d4ccccd, v76
	v_mul_f32_e32 v75, 0x3fb8aa3b, v75
	v_mul_f32_e64 v76, v114, |v84|
	v_exp_f32_e32 v75, v75
	v_mul_f32_e32 v76, 0x3fb8aa3b, v76
	v_exp_f32_e32 v76, v76
	v_mul_f32_e32 v77, v67, v66
	v_add_f32_e32 v66, 0x3d4ccccd, v75
	v_mul_f32_e32 v75, v68, v66
	v_add_f32_e32 v66, 0x3d4ccccd, v76
	v_mul_f32_e32 v69, v69, v66
	v_cvt_pk_bf16_f32 v66, v70, v71
	v_cvt_pk_bf16_f32 v67, v72, v73
	v_cvt_pk_bf16_f32 v68, v74, v77
	v_cvt_pk_bf16_f32 v69, v75, v69
	global_store_dwordx4 v[82:83], v[66:69], off offset:256
	s_nop 1
	v_mov_b32_e32 v68, v181
	s_nop 0
	v_mul_f32_e64 v70, v162, |v68|
	v_mul_f32_e64 v69, v163, |v68|
	v_mul_f32_e32 v69, 0x3fb8aa3b, v69
	v_exp_f32_e32 v69, v69
	v_mul_f32_e32 v70, 0x3fb8aa3b, v70
	v_exp_f32_e32 v70, v70
	v_mul_f32_e64 v71, v160, |v68|
	v_add_f32_e32 v69, 0x3d4ccccd, v69
	v_mul_f32_e32 v62, v62, v69
	v_add_f32_e32 v69, 0x3d4ccccd, v70
	v_mul_f32_e64 v70, v161, |v68|
	v_mul_f32_e32 v70, 0x3fb8aa3b, v70
	v_exp_f32_e32 v70, v70
	v_mul_f32_e32 v71, 0x3fb8aa3b, v71
	v_exp_f32_e32 v71, v71
	v_mul_f32_e32 v63, v63, v69
	v_add_f32_e32 v69, 0x3d4ccccd, v70
	v_mul_f32_e64 v70, v159, |v68|
	v_mul_f32_e32 v64, v64, v69
	v_add_f32_e32 v69, 0x3d4ccccd, v71
	v_mul_f32_e32 v70, 0x3fb8aa3b, v70
	v_mul_f32_e64 v71, v158, |v68|
	v_exp_f32_e32 v70, v70
	v_mul_f32_e32 v71, 0x3fb8aa3b, v71
	v_exp_f32_e32 v71, v71
	v_mul_f32_e32 v65, v65, v69
	v_add_f32_e32 v69, 0x3d4ccccd, v70
	v_mul_f32_e64 v70, v157, |v68|
	v_mul_f32_e32 v69, v58, v69
	v_add_f32_e32 v58, 0x3d4ccccd, v71
	v_mul_f32_e32 v70, 0x3fb8aa3b, v70
	v_mul_f32_e64 v71, v156, |v68|
	v_exp_f32_e32 v70, v70
	v_mul_f32_e32 v71, 0x3fb8aa3b, v71
	v_exp_f32_e32 v71, v71
	v_add_u32_e32 v66, 0x80, v144
	v_mul_f32_e32 v72, v59, v58
	v_add_f32_e32 v58, 0x3d4ccccd, v70
	v_ashrrev_i32_e32 v67, 31, v66
	v_mul_f32_e32 v70, v60, v58
	v_add_f32_e32 v58, 0x3d4ccccd, v71
	v_lshlrev_b64 v[66:67], s11, v[66:67]
	v_mul_f32_e32 v61, v61, v58
	v_cvt_pk_bf16_f32 v58, v62, v63
	v_mul_f32_e64 v62, v145, |v68|
	v_lshl_add_u64 v[66:67], v[66:67], 1, v[148:149]
	v_cvt_pk_bf16_f32 v59, v64, v65
	v_mul_f32_e32 v62, 0x3fb8aa3b, v62
	v_mul_f32_e64 v63, v118, |v68|
	v_cvt_pk_bf16_f32 v60, v69, v72
	v_cvt_pk_bf16_f32 v61, v70, v61
	v_exp_f32_e32 v62, v62
	v_mul_f32_e32 v63, 0x3fb8aa3b, v63
	global_store_dwordx4 v[66:67], v[58:61], off
	v_exp_f32_e32 v63, v63
	s_nop 0
	v_mul_f32_e64 v59, v122, |v68|
	v_mul_f32_e32 v59, 0x3fb8aa3b, v59
	v_mul_f32_e64 v60, v119, |v68|
	v_exp_f32_e32 v59, v59
	v_mul_f32_e32 v60, 0x3fb8aa3b, v60
	v_exp_f32_e32 v60, v60
	v_add_f32_e32 v58, 0x3d4ccccd, v62
	v_mul_f32_e32 v54, v54, v58
	v_add_f32_e32 v58, 0x3d4ccccd, v63
	v_mul_f32_e32 v55, v55, v58
	v_add_f32_e32 v58, 0x3d4ccccd, v59
	v_mul_f32_e64 v59, v120, |v68|
	v_mul_f32_e32 v56, v56, v58
	v_add_f32_e32 v58, 0x3d4ccccd, v60
	v_mul_f32_e32 v59, 0x3fb8aa3b, v59
	v_mul_f32_e64 v60, v121, |v68|
	v_exp_f32_e32 v59, v59
	v_mul_f32_e32 v60, 0x3fb8aa3b, v60
	v_exp_f32_e32 v60, v60
	v_mul_f32_e32 v57, v57, v58
	v_add_f32_e32 v58, 0x3d4ccccd, v59
	v_mul_f32_e64 v59, v123, |v68|
	v_mul_f32_e32 v58, v50, v58
	v_add_f32_e32 v50, 0x3d4ccccd, v60
	v_mul_f32_e32 v59, 0x3fb8aa3b, v59
	v_mul_f32_e64 v60, v114, |v68|
	v_exp_f32_e32 v59, v59
	v_mul_f32_e32 v60, 0x3fb8aa3b, v60
	v_exp_f32_e32 v60, v60
	v_mul_f32_e32 v61, v51, v50
	v_add_f32_e32 v50, 0x3d4ccccd, v59
	v_mul_f32_e32 v59, v52, v50
	v_add_f32_e32 v50, 0x3d4ccccd, v60
	v_mul_f32_e32 v53, v53, v50
	v_cvt_pk_bf16_f32 v50, v54, v55
	v_cvt_pk_bf16_f32 v51, v56, v57
	v_cvt_pk_bf16_f32 v52, v58, v61
	v_cvt_pk_bf16_f32 v53, v59, v53
	global_store_dwordx4 v[66:67], v[50:53], off offset:256
	s_nop 1
	v_mov_b32_e32 v52, v182
	s_nop 0
	v_mul_f32_e64 v54, v162, |v52|
	v_mul_f32_e64 v53, v163, |v52|
	v_mul_f32_e32 v53, 0x3fb8aa3b, v53
	v_exp_f32_e32 v53, v53
	v_mul_f32_e32 v54, 0x3fb8aa3b, v54
	v_exp_f32_e32 v54, v54
	v_mul_f32_e64 v55, v160, |v52|
	v_add_f32_e32 v53, 0x3d4ccccd, v53
	v_mul_f32_e32 v46, v46, v53
	v_add_f32_e32 v53, 0x3d4ccccd, v54
	v_mul_f32_e64 v54, v161, |v52|
	v_mul_f32_e32 v54, 0x3fb8aa3b, v54
	v_exp_f32_e32 v54, v54
	v_mul_f32_e32 v55, 0x3fb8aa3b, v55
	v_exp_f32_e32 v55, v55
	v_mul_f32_e32 v47, v47, v53
	v_add_f32_e32 v53, 0x3d4ccccd, v54
	v_mul_f32_e64 v54, v159, |v52|
	v_mul_f32_e32 v48, v48, v53
	v_add_f32_e32 v53, 0x3d4ccccd, v55
	v_mul_f32_e32 v54, 0x3fb8aa3b, v54
	v_mul_f32_e64 v55, v158, |v52|
	v_exp_f32_e32 v54, v54
	v_mul_f32_e32 v55, 0x3fb8aa3b, v55
	v_exp_f32_e32 v55, v55
	v_mul_f32_e32 v49, v49, v53
	v_add_f32_e32 v53, 0x3d4ccccd, v54
	v_mul_f32_e64 v54, v157, |v52|
	v_mul_f32_e32 v53, v42, v53
	v_add_f32_e32 v42, 0x3d4ccccd, v55
	v_mul_f32_e32 v54, 0x3fb8aa3b, v54
	v_mul_f32_e64 v55, v156, |v52|
	v_exp_f32_e32 v54, v54
	v_mul_f32_e32 v55, 0x3fb8aa3b, v55
	v_exp_f32_e32 v55, v55
	v_add_u32_e32 v50, 0x90, v144
	v_mul_f32_e32 v56, v43, v42
	v_add_f32_e32 v42, 0x3d4ccccd, v54
	v_ashrrev_i32_e32 v51, 31, v50
	v_mul_f32_e32 v54, v44, v42
	v_add_f32_e32 v42, 0x3d4ccccd, v55
	v_lshlrev_b64 v[50:51], s11, v[50:51]
	v_mul_f32_e32 v45, v45, v42
	v_cvt_pk_bf16_f32 v42, v46, v47
	v_mul_f32_e64 v46, v145, |v52|
	v_lshl_add_u64 v[50:51], v[50:51], 1, v[148:149]
	v_cvt_pk_bf16_f32 v43, v48, v49
	v_mul_f32_e32 v46, 0x3fb8aa3b, v46
	v_mul_f32_e64 v47, v118, |v52|
	v_cvt_pk_bf16_f32 v44, v53, v56
	v_cvt_pk_bf16_f32 v45, v54, v45
	v_exp_f32_e32 v46, v46
	v_mul_f32_e32 v47, 0x3fb8aa3b, v47
	global_store_dwordx4 v[50:51], v[42:45], off
	v_exp_f32_e32 v47, v47
	s_nop 0
	v_mul_f32_e64 v43, v122, |v52|
	v_mul_f32_e32 v43, 0x3fb8aa3b, v43
	v_mul_f32_e64 v44, v119, |v52|
	v_exp_f32_e32 v43, v43
	v_mul_f32_e32 v44, 0x3fb8aa3b, v44
	v_exp_f32_e32 v44, v44
	v_add_f32_e32 v42, 0x3d4ccccd, v46
	v_mul_f32_e32 v38, v38, v42
	v_add_f32_e32 v42, 0x3d4ccccd, v47
	v_mul_f32_e32 v39, v39, v42
	v_add_f32_e32 v42, 0x3d4ccccd, v43
	v_mul_f32_e64 v43, v120, |v52|
	v_mul_f32_e32 v40, v40, v42
	v_add_f32_e32 v42, 0x3d4ccccd, v44
	v_mul_f32_e32 v43, 0x3fb8aa3b, v43
	v_mul_f32_e64 v44, v121, |v52|
	v_exp_f32_e32 v43, v43
	v_mul_f32_e32 v44, 0x3fb8aa3b, v44
	v_exp_f32_e32 v44, v44
	v_mul_f32_e32 v41, v41, v42
	v_add_f32_e32 v42, 0x3d4ccccd, v43
	v_mul_f32_e64 v43, v123, |v52|
	v_mul_f32_e32 v42, v34, v42
	v_add_f32_e32 v34, 0x3d4ccccd, v44
	v_mul_f32_e32 v43, 0x3fb8aa3b, v43
	v_mul_f32_e64 v44, v114, |v52|
	v_exp_f32_e32 v43, v43
	v_mul_f32_e32 v44, 0x3fb8aa3b, v44
	v_exp_f32_e32 v44, v44
	v_mul_f32_e32 v45, v35, v34
	v_add_f32_e32 v34, 0x3d4ccccd, v43
	v_mul_f32_e32 v43, v36, v34
	v_add_f32_e32 v34, 0x3d4ccccd, v44
	v_mul_f32_e32 v37, v37, v34
	v_cvt_pk_bf16_f32 v34, v38, v39
	v_cvt_pk_bf16_f32 v35, v40, v41
	v_cvt_pk_bf16_f32 v36, v42, v45
	v_cvt_pk_bf16_f32 v37, v43, v37
	global_store_dwordx4 v[50:51], v[34:37], off offset:256
	s_nop 1
	v_mov_b32_e32 v36, v183
	s_nop 0
	v_mul_f32_e64 v38, v162, |v36|
	v_mul_f32_e64 v37, v163, |v36|
	v_mul_f32_e32 v37, 0x3fb8aa3b, v37
	v_exp_f32_e32 v37, v37
	v_mul_f32_e32 v38, 0x3fb8aa3b, v38
	v_exp_f32_e32 v38, v38
	v_mul_f32_e64 v39, v160, |v36|
	v_add_f32_e32 v37, 0x3d4ccccd, v37
	v_mul_f32_e32 v30, v30, v37
	v_add_f32_e32 v37, 0x3d4ccccd, v38
	v_mul_f32_e64 v38, v161, |v36|
	v_mul_f32_e32 v38, 0x3fb8aa3b, v38
	v_exp_f32_e32 v38, v38
	v_mul_f32_e32 v39, 0x3fb8aa3b, v39
	v_exp_f32_e32 v39, v39
	v_mul_f32_e32 v31, v31, v37
	v_add_f32_e32 v37, 0x3d4ccccd, v38
	v_mul_f32_e64 v38, v159, |v36|
	v_mul_f32_e32 v32, v32, v37
	v_add_f32_e32 v37, 0x3d4ccccd, v39
	v_mul_f32_e32 v38, 0x3fb8aa3b, v38
	v_mul_f32_e64 v39, v158, |v36|
	v_exp_f32_e32 v38, v38
	v_mul_f32_e32 v39, 0x3fb8aa3b, v39
	v_exp_f32_e32 v39, v39
	v_mul_f32_e32 v33, v33, v37
	v_add_f32_e32 v37, 0x3d4ccccd, v38
	v_mul_f32_e64 v38, v157, |v36|
	v_mul_f32_e32 v37, v26, v37
	v_add_f32_e32 v26, 0x3d4ccccd, v39
	v_mul_f32_e32 v38, 0x3fb8aa3b, v38
	v_mul_f32_e64 v39, v156, |v36|
	v_exp_f32_e32 v38, v38
	v_mul_f32_e32 v39, 0x3fb8aa3b, v39
	v_exp_f32_e32 v39, v39
	v_add_u32_e32 v34, 0xa0, v144
	v_mul_f32_e32 v40, v27, v26
	v_add_f32_e32 v26, 0x3d4ccccd, v38
	v_ashrrev_i32_e32 v35, 31, v34
	v_mul_f32_e32 v38, v28, v26
	v_add_f32_e32 v26, 0x3d4ccccd, v39
	v_lshlrev_b64 v[34:35], s11, v[34:35]
	v_mul_f32_e32 v29, v29, v26
	v_cvt_pk_bf16_f32 v26, v30, v31
	v_mul_f32_e64 v30, v145, |v36|
	v_lshl_add_u64 v[34:35], v[34:35], 1, v[148:149]
	v_cvt_pk_bf16_f32 v27, v32, v33
	v_mul_f32_e32 v30, 0x3fb8aa3b, v30
	v_mul_f32_e64 v31, v118, |v36|
	v_cvt_pk_bf16_f32 v28, v37, v40
	v_cvt_pk_bf16_f32 v29, v38, v29
	v_exp_f32_e32 v30, v30
	v_mul_f32_e32 v31, 0x3fb8aa3b, v31
	global_store_dwordx4 v[34:35], v[26:29], off
	v_exp_f32_e32 v31, v31
	s_nop 0
	v_mul_f32_e64 v27, v122, |v36|
	v_mul_f32_e32 v27, 0x3fb8aa3b, v27
	v_mul_f32_e64 v28, v119, |v36|
	v_exp_f32_e32 v27, v27
	v_mul_f32_e32 v28, 0x3fb8aa3b, v28
	v_exp_f32_e32 v28, v28
	v_add_f32_e32 v26, 0x3d4ccccd, v30
	v_mul_f32_e32 v22, v22, v26
	v_add_f32_e32 v26, 0x3d4ccccd, v31
	v_mul_f32_e32 v23, v23, v26
	v_add_f32_e32 v26, 0x3d4ccccd, v27
	v_mul_f32_e64 v27, v120, |v36|
	v_mul_f32_e32 v24, v24, v26
	v_add_f32_e32 v26, 0x3d4ccccd, v28
	v_mul_f32_e32 v27, 0x3fb8aa3b, v27
	v_mul_f32_e64 v28, v121, |v36|
	v_exp_f32_e32 v27, v27
	v_mul_f32_e32 v28, 0x3fb8aa3b, v28
	v_exp_f32_e32 v28, v28
	v_mul_f32_e32 v25, v25, v26
	v_add_f32_e32 v26, 0x3d4ccccd, v27
	v_mul_f32_e64 v27, v123, |v36|
	v_mul_f32_e32 v26, v18, v26
	v_add_f32_e32 v18, 0x3d4ccccd, v28
	v_mul_f32_e32 v27, 0x3fb8aa3b, v27
	v_mul_f32_e64 v28, v114, |v36|
	v_exp_f32_e32 v27, v27
	v_mul_f32_e32 v28, 0x3fb8aa3b, v28
	v_exp_f32_e32 v28, v28
	v_mul_f32_e32 v29, v19, v18
	v_add_f32_e32 v18, 0x3d4ccccd, v27
	v_mul_f32_e32 v27, v20, v18
	v_add_f32_e32 v18, 0x3d4ccccd, v28
	v_mul_f32_e32 v21, v21, v18
	v_cvt_pk_bf16_f32 v18, v22, v23
	v_cvt_pk_bf16_f32 v19, v24, v25
	v_cvt_pk_bf16_f32 v20, v26, v29
	v_cvt_pk_bf16_f32 v21, v27, v21
	global_store_dwordx4 v[34:35], v[18:21], off offset:256
	s_nop 1
	v_mov_b32_e32 v20, v184
	s_nop 0
	v_mul_f32_e64 v22, v162, |v20|
	v_mul_f32_e64 v21, v163, |v20|
	v_mul_f32_e32 v21, 0x3fb8aa3b, v21
	v_exp_f32_e32 v21, v21
	v_mul_f32_e32 v22, 0x3fb8aa3b, v22
	v_exp_f32_e32 v22, v22
	v_mul_f32_e64 v23, v160, |v20|
	v_add_f32_e32 v21, 0x3d4ccccd, v21
	v_mul_f32_e32 v14, v14, v21
	v_add_f32_e32 v21, 0x3d4ccccd, v22
	v_mul_f32_e64 v22, v161, |v20|
	v_mul_f32_e32 v22, 0x3fb8aa3b, v22
	v_exp_f32_e32 v22, v22
	v_mul_f32_e32 v23, 0x3fb8aa3b, v23
	v_exp_f32_e32 v23, v23
	v_mul_f32_e32 v15, v15, v21
	v_add_f32_e32 v21, 0x3d4ccccd, v22
	v_mul_f32_e64 v22, v159, |v20|
	v_mul_f32_e32 v16, v16, v21
	v_add_f32_e32 v21, 0x3d4ccccd, v23
	v_mul_f32_e32 v22, 0x3fb8aa3b, v22
	v_mul_f32_e64 v23, v158, |v20|
	v_exp_f32_e32 v22, v22
	v_mul_f32_e32 v23, 0x3fb8aa3b, v23
	v_exp_f32_e32 v23, v23
	v_mul_f32_e32 v17, v17, v21
	v_add_f32_e32 v21, 0x3d4ccccd, v22
	v_mul_f32_e64 v22, v157, |v20|
	v_mul_f32_e32 v21, v10, v21
	v_add_f32_e32 v10, 0x3d4ccccd, v23
	v_mul_f32_e32 v22, 0x3fb8aa3b, v22
	v_mul_f32_e64 v23, v156, |v20|
	v_exp_f32_e32 v22, v22
	v_mul_f32_e32 v23, 0x3fb8aa3b, v23
	v_exp_f32_e32 v23, v23
	v_add_u32_e32 v18, 0xb0, v144
	v_mul_f32_e32 v24, v11, v10
	v_add_f32_e32 v10, 0x3d4ccccd, v22
	v_ashrrev_i32_e32 v19, 31, v18
	v_mul_f32_e32 v22, v12, v10
	v_add_f32_e32 v10, 0x3d4ccccd, v23
	v_lshlrev_b64 v[18:19], s11, v[18:19]
	v_mul_f32_e32 v13, v13, v10
	v_cvt_pk_bf16_f32 v10, v14, v15
	v_mul_f32_e64 v14, v123, |v20|
	v_lshl_add_u64 v[18:19], v[18:19], 1, v[148:149]
	v_cvt_pk_bf16_f32 v11, v16, v17
	v_mul_f32_e32 v14, 0x3fb8aa3b, v14
	v_mul_f32_e64 v15, v121, |v20|
	v_cvt_pk_bf16_f32 v12, v21, v24
	v_cvt_pk_bf16_f32 v13, v22, v13
	v_exp_f32_e32 v14, v14
	v_mul_f32_e32 v15, 0x3fb8aa3b, v15
	global_store_dwordx4 v[18:19], v[10:13], off
	v_exp_f32_e32 v15, v15
	s_nop 0
	v_mul_f32_e64 v11, v120, |v20|
	v_mul_f32_e32 v11, 0x3fb8aa3b, v11
	v_exp_f32_e32 v11, v11
	v_mul_f32_e64 v12, v119, |v20|
	v_add_f32_e32 v10, 0x3d4ccccd, v14
	v_mul_f32_e32 v12, 0x3fb8aa3b, v12
	v_mul_f32_e32 v10, v4, v10
	v_add_f32_e32 v4, 0x3d4ccccd, v15
	v_exp_f32_e32 v12, v12
	v_mul_f32_e32 v4, v3, v4
	v_add_f32_e32 v3, 0x3d4ccccd, v11
	v_mul_f32_e32 v11, v2, v3
	v_mul_f32_e64 v3, v122, |v20|
	v_mul_f32_e32 v3, 0x3fb8aa3b, v3
	v_add_f32_e32 v2, 0x3d4ccccd, v12
	v_exp_f32_e32 v3, v3
	v_mul_f32_e64 v12, v118, |v20|
	v_mul_f32_e32 v12, 0x3fb8aa3b, v12
	v_exp_f32_e32 v12, v12
	v_mul_f32_e32 v9, v9, v2
	v_add_f32_e32 v2, 0x3d4ccccd, v3
	v_mul_f32_e32 v3, v8, v2
	v_mul_f32_e64 v8, v145, |v20|
	v_add_f32_e32 v2, 0x3d4ccccd, v12
	v_mul_f32_e32 v8, 0x3fb8aa3b, v8
	v_mul_f32_e64 v12, v114, |v20|
	v_exp_f32_e32 v8, v8
	v_mul_f32_e32 v12, 0x3fb8aa3b, v12
	v_exp_f32_e32 v12, v12
	v_mul_f32_e32 v2, v7, v2
	v_add_f32_e32 v7, 0x3d4ccccd, v8
	v_mul_f32_e32 v6, v6, v7
	v_add_f32_e32 v7, 0x3d4ccccd, v12
	v_mul_f32_e32 v5, v5, v7
	v_cvt_pk_bf16_f32 v2, v6, v2
	v_cvt_pk_bf16_f32 v3, v3, v9
	v_cvt_pk_bf16_f32 v4, v11, v4
	v_cvt_pk_bf16_f32 v5, v10, v5
	global_store_dwordx4 v[18:19], v[2:5], off offset:256
	s_cbranch_vccz .LBB0_2280
	s_waitcnt vmcnt(0)
	s_cmpk_gt_u32 s41, 0xff
	s_cbranch_scc1 .LBB0_2287
	s_barrier

.LBB0_2336:
	s_cmp_gt_i32 s55, 14
	s_cselect_b64 s[0:1], -1, 0
	s_and_b64 s[2:3], s[4:5], s[0:1]
	s_andn2_b64 vcc, exec, s[2:3]
	s_cbranch_vccnz .LBB0_2386
	s_waitcnt vmcnt(0)
	s_barrier
	s_setprio 0
	s_mov_b64 s[2:3], exec
	v_readlane_b32 s4, v250, 5
	v_readlane_b32 s5, v250, 6
	s_and_b64 s[4:5], s[2:3], s[4:5]
	s_mov_b64 exec, s[4:5]
	s_cbranch_execz .LBB0_2385
	s_add_i32 s4, 0, 0x27ff0
	v_mov_b32_e32 v1, s4
	s_waitcnt vmcnt(0) expcnt(0) lgkmcnt(0)
	ds_read_b32 v3, v1
	s_add_i32 s4, 0, 0x27ff4
	v_mov_b32_e32 v1, s4
	ds_read_b32 v1, v1
	s_waitcnt lgkmcnt(1)
	v_cmp_ne_u32_e32 vcc, 0, v3
	s_cbranch_vccnz .LBB0_2353
	v_readlane_b32 s4, v250, 2
	v_readlane_b32 s5, v250, 3
	s_load_dwordx2 s[8:9], s[4:5], 0x4
	s_add_u32 s4, s52, 0x1000
	s_addc_u32 s5, s53, 0
	s_add_u32 s6, s52, 0x1100
	s_addc_u32 s7, s53, 0
	v_readlane_b32 s10, v250, 1
	s_waitcnt lgkmcnt(0)
	s_mul_i32 s18, s8, s10
	s_add_u32 s8, s52, 0x1200
	s_mul_i32 s18, s18, s9
	s_addc_u32 s9, s53, 0
	s_add_u32 s10, s52, 0x1300
	s_addc_u32 s11, s53, 0
	s_mov_b32 s19, 1
	v_mov_b32_e32 v17, 0
	s_branch .LBB0_2341

.LBB0_2417:
	ds_read_b128 v[130:133], v155
	ds_read_b128 v[158:161], v155 offset:1024
	ds_read_b128 v[162:165], v155 offset:2048
	ds_read_b128 v[166:169], v155 offset:3072
	s_add_u32 s28, s26, 0xfff80080
	s_addc_u32 s29, s27, -1
	s_cmp_eq_u32 s59, 28
	s_cselect_b32 s31, s1, s29
	s_cselect_b32 s30, s19, s28
	s_cselect_b32 s29, s35, s58
	s_cselect_b32 s28, s56, s57
	v_lshl_add_u64 v[150:151], s[26:27], 0, v[142:143]
	s_add_i32 m0, s43, 0xc000
	ds_read_b128 v[170:173], v156
	ds_read_b128 v[174:177], v156 offset:1024
	ds_read_b128 v[178:181], v156 offset:2048
	ds_read_b128 v[182:185], v156 offset:3072
	ds_read_b128 v[186:189], v156 offset:4096
	ds_read_b128 v[190:193], v156 offset:5120
	ds_read_b128 v[194:197], v156 offset:6144
	ds_read_b128 v[198:201], v156 offset:7168
	global_load_lds_dwordx4 v[150:151], off
	v_lshl_add_u64 v[150:151], s[26:27], 0, v[144:145]
	s_add_i32 m0, s43, 0xe000
	s_nop 0
	global_load_lds_dwordx4 v[150:151], off
	s_waitcnt lgkmcnt(8)
	s_barrier
	s_waitcnt lgkmcnt(0)
	s_waitcnt lgkmcnt(0)
	v_mfma_f32_16x16x32_bf16 v[126:129], v[130:133], v[170:173], v[126:129]
	v_mfma_f32_16x16x32_bf16 v[122:125], v[162:165], v[170:173], v[122:125]
	v_mfma_f32_16x16x32_bf16 v[118:121], v[130:133], v[178:181], v[118:121]
	v_mfma_f32_16x16x32_bf16 v[110:113], v[162:165], v[178:181], v[110:113]
	v_mfma_f32_16x16x32_bf16 v[102:105], v[130:133], v[186:189], v[102:105]
	v_mfma_f32_16x16x32_bf16 v[94:97], v[162:165], v[186:189], v[94:97]
	v_mfma_f32_16x16x32_bf16 v[86:89], v[130:133], v[194:197], v[86:89]
	v_mfma_f32_16x16x32_bf16 v[78:81], v[162:165], v[194:197], v[78:81]
	v_mfma_f32_16x16x32_bf16 v[126:129], v[158:161], v[174:177], v[126:129]
	v_mfma_f32_16x16x32_bf16 v[122:125], v[166:169], v[174:177], v[122:125]
	v_mfma_f32_16x16x32_bf16 v[118:121], v[158:161], v[182:185], v[118:121]
	v_mfma_f32_16x16x32_bf16 v[110:113], v[166:169], v[182:185], v[110:113]
	v_mfma_f32_16x16x32_bf16 v[102:105], v[158:161], v[190:193], v[102:105]
	v_mfma_f32_16x16x32_bf16 v[94:97], v[166:169], v[190:193], v[94:97]
	v_mfma_f32_16x16x32_bf16 v[86:89], v[158:161], v[198:201], v[86:89]
	v_mfma_f32_16x16x32_bf16 v[78:81], v[166:169], v[198:201], v[78:81]
	s_barrier
	s_add_i32 s60, s52, s42
	v_lshl_add_u64 v[150:151], s[28:29], 0, v[134:135]
	s_mov_b32 m0, s60
	ds_read_b128 v[202:205], v157
	ds_read_b128 v[206:209], v157 offset:1024
	ds_read_b128 v[210:213], v157 offset:2048
	ds_read_b128 v[214:217], v157 offset:3072
	global_load_lds_dwordx4 v[150:151], off
	v_lshl_add_u64 v[218:219], s[28:29], 0, v[138:139]
	s_add_i32 m0, s60, 0x2000
	s_nop 0
	global_load_lds_dwordx4 v[218:219], off
	s_barrier
	s_waitcnt lgkmcnt(0)
	s_waitcnt lgkmcnt(0)
	v_mfma_f32_16x16x32_bf16 v[114:117], v[202:205], v[170:173], v[114:117]
	v_mfma_f32_16x16x32_bf16 v[106:109], v[210:213], v[170:173], v[106:109]
	v_mfma_f32_16x16x32_bf16 v[98:101], v[202:205], v[178:181], v[98:101]
	v_mfma_f32_16x16x32_bf16 v[90:93], v[210:213], v[178:181], v[90:93]
	v_mfma_f32_16x16x32_bf16 v[82:85], v[202:205], v[186:189], v[82:85]
	v_mfma_f32_16x16x32_bf16 v[74:77], v[210:213], v[186:189], v[74:77]
	v_mfma_f32_16x16x32_bf16 v[70:73], v[202:205], v[194:197], v[70:73]
	v_mfma_f32_16x16x32_bf16 v[66:69], v[210:213], v[194:197], v[66:69]
	v_mfma_f32_16x16x32_bf16 v[114:117], v[206:209], v[174:177], v[114:117]
	v_mfma_f32_16x16x32_bf16 v[106:109], v[214:217], v[174:177], v[106:109]
	v_mfma_f32_16x16x32_bf16 v[98:101], v[206:209], v[182:185], v[98:101]
	v_mfma_f32_16x16x32_bf16 v[90:93], v[214:217], v[182:185], v[90:93]
	v_mfma_f32_16x16x32_bf16 v[82:85], v[206:209], v[190:193], v[82:85]
	v_mfma_f32_16x16x32_bf16 v[74:77], v[214:217], v[190:193], v[74:77]
	v_mfma_f32_16x16x32_bf16 v[70:73], v[206:209], v[198:201], v[70:73]
	v_mfma_f32_16x16x32_bf16 v[66:69], v[214:217], v[198:201], v[66:69]
	s_mov_b32 m0, s43
	v_lshl_add_u64 v[220:221], s[30:31], 0, v[136:137]
	s_barrier
	ds_read_b128 v[170:173], v156 offset:16384
	ds_read_b128 v[174:177], v156 offset:17408
	ds_read_b128 v[178:181], v156 offset:18432
	ds_read_b128 v[182:185], v156 offset:19456
	ds_read_b128 v[186:189], v156 offset:20480
	ds_read_b128 v[190:193], v156 offset:21504
	ds_read_b128 v[194:197], v156 offset:22528
	ds_read_b128 v[198:201], v156 offset:23552
	global_load_lds_dwordx4 v[220:221], off
	v_lshl_add_u64 v[222:223], s[30:31], 0, v[140:141]
	s_mov_b32 m0, s44
	s_nop 0
	global_load_lds_dwordx4 v[222:223], off
	s_barrier
	s_waitcnt lgkmcnt(0)
	s_waitcnt lgkmcnt(0)
	v_mfma_f32_16x16x32_bf16 v[62:65], v[130:133], v[170:173], v[62:65]
	v_mfma_f32_16x16x32_bf16 v[58:61], v[162:165], v[170:173], v[58:61]
	v_mfma_f32_16x16x32_bf16 v[54:57], v[130:133], v[178:181], v[54:57]
	v_mfma_f32_16x16x32_bf16 v[46:49], v[162:165], v[178:181], v[46:49]
	v_mfma_f32_16x16x32_bf16 v[38:41], v[130:133], v[186:189], v[38:41]
	v_mfma_f32_16x16x32_bf16 v[30:33], v[162:165], v[186:189], v[30:33]
	v_mfma_f32_16x16x32_bf16 v[22:25], v[130:133], v[194:197], v[22:25]
	v_mfma_f32_16x16x32_bf16 v[14:17], v[162:165], v[194:197], v[14:17]
	v_mfma_f32_16x16x32_bf16 v[62:65], v[158:161], v[174:177], v[62:65]
	v_mfma_f32_16x16x32_bf16 v[58:61], v[166:169], v[174:177], v[58:61]
	v_mfma_f32_16x16x32_bf16 v[54:57], v[158:161], v[182:185], v[54:57]
	v_mfma_f32_16x16x32_bf16 v[46:49], v[166:169], v[182:185], v[46:49]
	v_mfma_f32_16x16x32_bf16 v[38:41], v[158:161], v[190:193], v[38:41]
	v_mfma_f32_16x16x32_bf16 v[30:33], v[166:169], v[190:193], v[30:33]
	v_mfma_f32_16x16x32_bf16 v[22:25], v[158:161], v[198:201], v[22:25]
	v_mfma_f32_16x16x32_bf16 v[14:17], v[166:169], v[198:201], v[14:17]
	s_barrier
	s_add_u32 s60, s28, 0x80000
	s_addc_u32 s61, s29, 0
	s_add_i32 s62, s53, s42
	v_lshl_add_u64 v[130:131], s[60:61], 0, v[134:135]
	s_mov_b32 m0, s62
	s_nop 0
	global_load_lds_dwordx4 v[130:131], off
	v_lshl_add_u64 v[130:131], s[60:61], 0, v[138:139]
	s_add_i32 m0, s62, 0x2000
	s_nop 0
	global_load_lds_dwordx4 v[130:131], off
	s_waitcnt vmcnt(6)
	s_barrier
	v_mfma_f32_16x16x32_bf16 v[50:53], v[202:205], v[170:173], v[50:53]
	v_mfma_f32_16x16x32_bf16 v[42:45], v[210:213], v[170:173], v[42:45]
	v_mfma_f32_16x16x32_bf16 v[34:37], v[202:205], v[178:181], v[34:37]
	v_mfma_f32_16x16x32_bf16 v[26:29], v[210:213], v[178:181], v[26:29]
	v_mfma_f32_16x16x32_bf16 v[18:21], v[202:205], v[186:189], v[18:21]
	v_mfma_f32_16x16x32_bf16 v[10:13], v[210:213], v[186:189], v[10:13]
	v_mfma_f32_16x16x32_bf16 v[6:9], v[202:205], v[194:197], v[6:9]
	v_mfma_f32_16x16x32_bf16 v[2:5], v[210:213], v[194:197], v[2:5]
	v_mfma_f32_16x16x32_bf16 v[50:53], v[206:209], v[174:177], v[50:53]
	v_mfma_f32_16x16x32_bf16 v[42:45], v[214:217], v[174:177], v[42:45]
	v_mfma_f32_16x16x32_bf16 v[34:37], v[206:209], v[182:185], v[34:37]
	v_mfma_f32_16x16x32_bf16 v[26:29], v[214:217], v[182:185], v[26:29]
	v_mfma_f32_16x16x32_bf16 v[18:21], v[206:209], v[190:193], v[18:21]
	v_mfma_f32_16x16x32_bf16 v[10:13], v[214:217], v[190:193], v[10:13]
	v_mfma_f32_16x16x32_bf16 v[6:9], v[206:209], v[198:201], v[6:9]
	v_mfma_f32_16x16x32_bf16 v[2:5], v[214:217], v[198:201], v[2:5]
	s_add_i32 s60, 0, 0x18000
	v_add_u32_e32 v166, s60, v152
	s_barrier
	ds_read_b128 v[130:133], v166
	ds_read_b128 v[158:161], v166 offset:1024
	ds_read_b128 v[162:165], v166 offset:2048
	ds_read_b128 v[166:169], v166 offset:3072
	s_add_u32 s30, s30, 0x80000
	s_addc_u32 s31, s31, 0
	s_mov_b32 m0, s45
	v_lshl_add_u64 v[202:203], s[30:31], 0, v[136:137]
	ds_read_b128 v[170:173], v156 offset:32768
	ds_read_b128 v[174:177], v156 offset:33792
	ds_read_b128 v[178:181], v156 offset:34816
	ds_read_b128 v[182:185], v156 offset:35840
	ds_read_b128 v[186:189], v156 offset:36864
	ds_read_b128 v[190:193], v156 offset:37888
	ds_read_b128 v[194:197], v156 offset:38912
	ds_read_b128 v[198:201], v156 offset:39936
	global_load_lds_dwordx4 v[202:203], off
	v_lshl_add_u64 v[202:203], s[30:31], 0, v[140:141]
	s_mov_b32 m0, s46
	s_nop 0
	global_load_lds_dwordx4 v[202:203], off
	s_waitcnt lgkmcnt(8)
	s_barrier
	s_waitcnt lgkmcnt(0)
	s_waitcnt lgkmcnt(0)
	v_mfma_f32_16x16x32_bf16 v[126:129], v[130:133], v[170:173], v[126:129]
	v_mfma_f32_16x16x32_bf16 v[122:125], v[162:165], v[170:173], v[122:125]
	v_mfma_f32_16x16x32_bf16 v[118:121], v[130:133], v[178:181], v[118:121]
	v_mfma_f32_16x16x32_bf16 v[110:113], v[162:165], v[178:181], v[110:113]
	v_mfma_f32_16x16x32_bf16 v[102:105], v[130:133], v[186:189], v[102:105]
	v_mfma_f32_16x16x32_bf16 v[94:97], v[162:165], v[186:189], v[94:97]
	v_mfma_f32_16x16x32_bf16 v[86:89], v[130:133], v[194:197], v[86:89]
	v_mfma_f32_16x16x32_bf16 v[78:81], v[162:165], v[194:197], v[78:81]
	v_mfma_f32_16x16x32_bf16 v[126:129], v[158:161], v[174:177], v[126:129]
	v_mfma_f32_16x16x32_bf16 v[122:125], v[166:169], v[174:177], v[122:125]
	v_mfma_f32_16x16x32_bf16 v[118:121], v[158:161], v[182:185], v[118:121]
	v_mfma_f32_16x16x32_bf16 v[110:113], v[166:169], v[182:185], v[110:113]
	v_mfma_f32_16x16x32_bf16 v[102:105], v[158:161], v[190:193], v[102:105]
	v_mfma_f32_16x16x32_bf16 v[94:97], v[166:169], v[190:193], v[94:97]
	v_mfma_f32_16x16x32_bf16 v[86:89], v[158:161], v[198:201], v[86:89]
	v_mfma_f32_16x16x32_bf16 v[78:81], v[166:169], v[198:201], v[78:81]
	s_barrier
	s_add_i32 s30, 0, 0x1c000
	s_add_i32 s31, s60, s42
	v_add_u32_e32 v214, s30, v152
	v_lshl_add_u64 v[150:151], v[150:151], 0, s[6:7]
	s_mov_b32 m0, s31
	ds_read_b128 v[202:205], v214
	ds_read_b128 v[206:209], v214 offset:1024
	ds_read_b128 v[210:213], v214 offset:2048
	ds_read_b128 v[214:217], v214 offset:3072
	global_load_lds_dwordx4 v[150:151], off
	v_lshl_add_u64 v[150:151], v[218:219], 0, s[6:7]
	s_add_i32 m0, s31, 0x2000
	s_nop 0
	global_load_lds_dwordx4 v[150:151], off
	s_barrier
	s_waitcnt lgkmcnt(0)
	s_waitcnt lgkmcnt(0)
	v_mfma_f32_16x16x32_bf16 v[114:117], v[202:205], v[170:173], v[114:117]
	v_mfma_f32_16x16x32_bf16 v[106:109], v[210:213], v[170:173], v[106:109]
	v_mfma_f32_16x16x32_bf16 v[98:101], v[202:205], v[178:181], v[98:101]
	v_mfma_f32_16x16x32_bf16 v[90:93], v[210:213], v[178:181], v[90:93]
	v_mfma_f32_16x16x32_bf16 v[82:85], v[202:205], v[186:189], v[82:85]
	v_mfma_f32_16x16x32_bf16 v[74:77], v[210:213], v[186:189], v[74:77]
	v_mfma_f32_16x16x32_bf16 v[70:73], v[202:205], v[194:197], v[70:73]
	v_mfma_f32_16x16x32_bf16 v[66:69], v[210:213], v[194:197], v[66:69]
	v_mfma_f32_16x16x32_bf16 v[114:117], v[206:209], v[174:177], v[114:117]
	v_mfma_f32_16x16x32_bf16 v[106:109], v[214:217], v[174:177], v[106:109]
	v_mfma_f32_16x16x32_bf16 v[98:101], v[206:209], v[182:185], v[98:101]
	v_mfma_f32_16x16x32_bf16 v[90:93], v[214:217], v[182:185], v[90:93]
	v_mfma_f32_16x16x32_bf16 v[82:85], v[206:209], v[190:193], v[82:85]
	v_mfma_f32_16x16x32_bf16 v[74:77], v[214:217], v[190:193], v[74:77]
	v_mfma_f32_16x16x32_bf16 v[70:73], v[206:209], v[198:201], v[70:73]
	v_mfma_f32_16x16x32_bf16 v[66:69], v[214:217], v[198:201], v[66:69]
	s_mov_b32 m0, s48
	v_lshl_add_u64 v[150:151], v[220:221], 0, s[6:7]
	s_barrier
	ds_read_b128 v[170:173], v156 offset:49152
	ds_read_b128 v[174:177], v156 offset:50176
	ds_read_b128 v[178:181], v156 offset:51200
	ds_read_b128 v[182:185], v156 offset:52224
	ds_read_b128 v[186:189], v156 offset:53248
	ds_read_b128 v[190:193], v156 offset:54272
	ds_read_b128 v[194:197], v156 offset:55296
	ds_read_b128 v[198:201], v156 offset:56320
	global_load_lds_dwordx4 v[150:151], off
	v_lshl_add_u64 v[150:151], v[222:223], 0, s[6:7]
	s_mov_b32 m0, s49
	s_nop 0
	global_load_lds_dwordx4 v[150:151], off
	s_barrier
	s_waitcnt lgkmcnt(0)
	s_waitcnt lgkmcnt(0)
	v_mfma_f32_16x16x32_bf16 v[62:65], v[130:133], v[170:173], v[62:65]
	v_mfma_f32_16x16x32_bf16 v[58:61], v[162:165], v[170:173], v[58:61]
	v_mfma_f32_16x16x32_bf16 v[54:57], v[130:133], v[178:181], v[54:57]
	v_mfma_f32_16x16x32_bf16 v[46:49], v[162:165], v[178:181], v[46:49]
	v_mfma_f32_16x16x32_bf16 v[38:41], v[130:133], v[186:189], v[38:41]
	v_mfma_f32_16x16x32_bf16 v[30:33], v[162:165], v[186:189], v[30:33]
	v_mfma_f32_16x16x32_bf16 v[22:25], v[130:133], v[194:197], v[22:25]
	v_mfma_f32_16x16x32_bf16 v[14:17], v[162:165], v[194:197], v[14:17]
	v_mfma_f32_16x16x32_bf16 v[62:65], v[158:161], v[174:177], v[62:65]
	v_mfma_f32_16x16x32_bf16 v[58:61], v[166:169], v[174:177], v[58:61]
	v_mfma_f32_16x16x32_bf16 v[54:57], v[158:161], v[182:185], v[54:57]
	v_mfma_f32_16x16x32_bf16 v[46:49], v[166:169], v[182:185], v[46:49]
	v_mfma_f32_16x16x32_bf16 v[38:41], v[158:161], v[190:193], v[38:41]
	v_mfma_f32_16x16x32_bf16 v[30:33], v[166:169], v[190:193], v[30:33]
	v_mfma_f32_16x16x32_bf16 v[22:25], v[158:161], v[198:201], v[22:25]
	v_mfma_f32_16x16x32_bf16 v[14:17], v[166:169], v[198:201], v[14:17]
	s_barrier
	s_add_u32 s28, s28, 0x80080
	s_addc_u32 s29, s29, 0
	s_add_i32 s30, s30, s42
	v_lshl_add_u64 v[130:131], s[28:29], 0, v[134:135]
	s_mov_b32 m0, s30
	s_nop 0
	global_load_lds_dwordx4 v[130:131], off
	v_lshl_add_u64 v[130:131], s[28:29], 0, v[138:139]
	s_add_i32 m0, s30, 0x2000
	s_nop 0
	global_load_lds_dwordx4 v[130:131], off
	s_waitcnt vmcnt(6)
	s_barrier
	v_mfma_f32_16x16x32_bf16 v[50:53], v[202:205], v[170:173], v[50:53]
	v_mfma_f32_16x16x32_bf16 v[42:45], v[210:213], v[170:173], v[42:45]
	v_mfma_f32_16x16x32_bf16 v[34:37], v[202:205], v[178:181], v[34:37]
	v_mfma_f32_16x16x32_bf16 v[26:29], v[210:213], v[178:181], v[26:29]
	v_mfma_f32_16x16x32_bf16 v[18:21], v[202:205], v[186:189], v[18:21]
	v_mfma_f32_16x16x32_bf16 v[10:13], v[210:213], v[186:189], v[10:13]
	v_mfma_f32_16x16x32_bf16 v[6:9], v[202:205], v[194:197], v[6:9]
	v_mfma_f32_16x16x32_bf16 v[2:5], v[210:213], v[194:197], v[2:5]
	v_mfma_f32_16x16x32_bf16 v[50:53], v[206:209], v[174:177], v[50:53]
	v_mfma_f32_16x16x32_bf16 v[42:45], v[214:217], v[174:177], v[42:45]
	v_mfma_f32_16x16x32_bf16 v[34:37], v[206:209], v[182:185], v[34:37]
	v_mfma_f32_16x16x32_bf16 v[26:29], v[214:217], v[182:185], v[26:29]
	v_mfma_f32_16x16x32_bf16 v[18:21], v[206:209], v[190:193], v[18:21]
	v_mfma_f32_16x16x32_bf16 v[10:13], v[214:217], v[190:193], v[10:13]
	v_mfma_f32_16x16x32_bf16 v[6:9], v[206:209], v[198:201], v[6:9]
	v_mfma_f32_16x16x32_bf16 v[2:5], v[214:217], v[198:201], v[2:5]
	s_add_i32 s59, s59, 2
	s_add_u32 s26, s26, 0x100
	s_addc_u32 s27, s27, 0
	s_add_u32 s57, s57, 0x100
	s_addc_u32 s58, s58, 0
	s_cmp_gt_u32 s59, 29
	s_barrier
	s_cbranch_scc0 .LBB0_2417
	s_lshl_b32 s19, s34, 8
	s_lshl_b32 s56, s0, 8
	s_cmpk_lt_i32 s34, 0x3e8
	s_mov_b64 s[26:27], -1
	s_cbranch_scc0 .LBB0_2466
	s_cmp_lt_i32 s0, 4
	s_cbranch_scc1 .LBB0_2432
	s_cmp_gt_u32 s0, 5
	s_mov_b64 s[34:35], -1
	s_cbranch_scc0 .LBB0_2430
	s_cmp_gt_u32 s0, 9
	s_cbranch_scc0 .LBB0_2427
	s_mov_b64 s[30:31], -1
	s_cmp_gt_u32 s0, 17
	s_mov_b64 s[0:1], -1
	s_cbranch_scc0 .LBB0_2424
	s_add_i32 s57, s56, 0xffffee00
	s_mov_b64 s[0:1], 0

.LBB0_2472:
	s_cmp_gt_i32 s55, 15
	s_cselect_b64 s[0:1], -1, 0
	s_and_b64 s[2:3], s[2:3], s[0:1]
	s_andn2_b64 vcc, exec, s[2:3]
	s_cbranch_vccnz .LBB0_2525
	s_waitcnt vmcnt(0)
	s_barrier
	s_setprio 0
	s_mov_b64 s[2:3], exec
	v_readlane_b32 s4, v250, 5
	v_readlane_b32 s5, v250, 6
	s_and_b64 s[4:5], s[2:3], s[4:5]
	s_mov_b64 exec, s[4:5]
	s_cbranch_execz .LBB0_2524
	s_add_i32 s4, 0, 0x27ff0
	v_mov_b32_e32 v1, s4
	s_waitcnt vmcnt(0) expcnt(0) lgkmcnt(0)
	ds_read_b32 v3, v1
	s_add_i32 s4, 0, 0x27ff4
	v_mov_b32_e32 v1, s4
	ds_read_b32 v1, v1
	s_waitcnt lgkmcnt(1)
	v_cmp_ne_u32_e32 vcc, 0, v3
	s_cbranch_vccnz .LBB0_2489
	v_readlane_b32 s4, v250, 2
	v_readlane_b32 s5, v250, 3
	s_load_dwordx2 s[8:9], s[4:5], 0x4
	s_add_u32 s4, s52, 0x1000
	s_addc_u32 s5, s53, 0
	s_add_u32 s6, s52, 0x1100
	s_addc_u32 s7, s53, 0
	v_readlane_b32 s10, v250, 1
	s_waitcnt lgkmcnt(0)
	s_mul_i32 s18, s8, s10
	s_add_u32 s8, s52, 0x1200
	s_mul_i32 s18, s18, s9
	s_addc_u32 s9, s53, 0
	s_add_u32 s10, s52, 0x1300
	s_addc_u32 s11, s53, 0
	s_mov_b32 s19, 1
	v_mov_b32_e32 v17, 0
	s_branch .LBB0_2477

.LBB0_2654:
	s_cmp_gt_i32 s55, 16
	s_cselect_b64 s[0:1], -1, 0
	s_and_b64 s[2:3], s[14:15], s[0:1]
	s_andn2_b64 vcc, exec, s[2:3]
	s_cbranch_vccnz .LBB0_2704
	s_waitcnt vmcnt(0)
	s_barrier
	s_setprio 0
	s_mov_b64 s[2:3], exec
	v_readlane_b32 s4, v250, 5
	v_readlane_b32 s5, v250, 6
	s_and_b64 s[4:5], s[2:3], s[4:5]
	s_mov_b64 exec, s[4:5]
	s_cbranch_execz .LBB0_2703
	s_add_i32 s4, 0, 0x27ff0
	v_mov_b32_e32 v1, s4
	s_waitcnt vmcnt(0) expcnt(0) lgkmcnt(0)
	ds_read_b32 v3, v1
	s_add_i32 s4, 0, 0x27ff4
	v_mov_b32_e32 v1, s4
	ds_read_b32 v1, v1
	s_waitcnt lgkmcnt(1)
	v_cmp_ne_u32_e32 vcc, 0, v3
	s_cbranch_vccnz .LBB0_2671
	v_readlane_b32 s4, v250, 2
	v_readlane_b32 s5, v250, 3
	s_load_dwordx2 s[8:9], s[4:5], 0x4
	s_add_u32 s4, s52, 0x1000
	s_addc_u32 s5, s53, 0
	s_add_u32 s6, s52, 0x1100
	s_addc_u32 s7, s53, 0
	v_readlane_b32 s10, v250, 1
	s_waitcnt lgkmcnt(0)
	s_mul_i32 s18, s8, s10
	s_add_u32 s8, s52, 0x1200
	s_mul_i32 s18, s18, s9
	s_addc_u32 s9, s53, 0
	s_add_u32 s10, s52, 0x1300
	s_addc_u32 s11, s53, 0
	s_mov_b32 s19, 1
	v_mov_b32_e32 v17, 0
	s_branch .LBB0_2659

.LBB0_3118:
	s_cmp_gt_i32 s55, 17
	s_cselect_b64 s[0:1], -1, 0
	s_and_b64 s[2:3], s[2:3], s[0:1]
	s_andn2_b64 vcc, exec, s[2:3]
	s_cbranch_vccnz .LBB0_3168
	s_waitcnt vmcnt(0)
	s_barrier
	s_setprio 0
	s_mov_b64 s[2:3], exec
	v_readlane_b32 s4, v250, 5
	v_readlane_b32 s5, v250, 6
	s_and_b64 s[4:5], s[2:3], s[4:5]
	s_mov_b64 exec, s[4:5]
	s_cbranch_execz .LBB0_3167
	s_add_i32 s4, 0, 0x27ff0
	v_mov_b32_e32 v1, s4
	s_waitcnt vmcnt(0) expcnt(0) lgkmcnt(0)
	ds_read_b32 v3, v1
	s_add_i32 s4, 0, 0x27ff4
	v_mov_b32_e32 v1, s4
	ds_read_b32 v1, v1
	s_waitcnt lgkmcnt(1)
	v_cmp_ne_u32_e32 vcc, 0, v3
	s_cbranch_vccnz .LBB0_3135
	v_readlane_b32 s4, v250, 2
	v_readlane_b32 s5, v250, 3
	s_load_dwordx2 s[8:9], s[4:5], 0x4
	s_add_u32 s4, s52, 0x1000
	s_addc_u32 s5, s53, 0
	s_add_u32 s6, s52, 0x1100
	s_addc_u32 s7, s53, 0
	v_readlane_b32 s10, v250, 1
	s_waitcnt lgkmcnt(0)
	s_mul_i32 s18, s8, s10
	s_add_u32 s8, s52, 0x1200
	s_mul_i32 s18, s18, s9
	s_addc_u32 s9, s53, 0
	s_add_u32 s10, s52, 0x1300
	s_addc_u32 s11, s53, 0
	s_mov_b32 s19, 1
	v_mov_b32_e32 v17, 0
	s_branch .LBB0_3123

.LBB0_3173:
	s_cmp_gt_i32 s55, 18
	s_cselect_b64 s[0:1], -1, 0
	s_and_b64 s[2:3], s[2:3], s[0:1]
	s_andn2_b64 vcc, exec, s[2:3]
	s_cbranch_vccnz .LBB0_3223
	s_waitcnt vmcnt(0)
	s_barrier
	s_setprio 0
	s_mov_b64 s[2:3], exec
	v_readlane_b32 s4, v250, 5
	v_readlane_b32 s5, v250, 6
	s_and_b64 s[4:5], s[2:3], s[4:5]
	s_mov_b64 exec, s[4:5]
	s_cbranch_execz .LBB0_3222
	s_add_i32 s4, 0, 0x27ff0
	v_mov_b32_e32 v1, s4
	s_waitcnt vmcnt(0) expcnt(0) lgkmcnt(0)
	ds_read_b32 v3, v1
	s_add_i32 s4, 0, 0x27ff4
	v_mov_b32_e32 v1, s4
	ds_read_b32 v1, v1
	s_waitcnt lgkmcnt(1)
	v_cmp_ne_u32_e32 vcc, 0, v3
	s_cbranch_vccnz .LBB0_3190
	v_readlane_b32 s4, v250, 2
	v_readlane_b32 s5, v250, 3
	s_load_dwordx2 s[8:9], s[4:5], 0x4
	s_add_u32 s4, s52, 0x1000
	s_addc_u32 s5, s53, 0
	s_add_u32 s6, s52, 0x1100
	s_addc_u32 s7, s53, 0
	v_readlane_b32 s10, v250, 1
	s_waitcnt lgkmcnt(0)
	s_mul_i32 s18, s8, s10
	s_add_u32 s8, s52, 0x1200
	s_mul_i32 s18, s18, s9
	s_addc_u32 s9, s53, 0
	s_add_u32 s10, s52, 0x1300
	s_addc_u32 s11, s53, 0
	s_mov_b32 s19, 1
	v_mov_b32_e32 v17, 0
	s_branch .LBB0_3178

.LBB0_3223:
	s_cmp_lt_i32 s54, 19
	s_cselect_b64 s[4:5], -1, 0
	s_and_b64 s[0:1], s[4:5], s[0:1]
	s_andn2_b64 vcc, exec, s[0:1]
	s_cbranch_vccnz .LBB0_3261
	v_mov_b32_e32 v1, v0
	s_waitcnt vmcnt(11)
	v_mov_b32_e32 v2, v248
	v_readlane_b32 s30, v250, 0
	v_readlane_b32 s0, v250, 39
	v_readlane_b32 s31, v250, 1
	s_mov_b64 s[0:1], s[90:91]
	s_mov_b64 s[6:7], s[52:53]
	v_lshlrev_b32_e32 v2, 4, v0
	v_and_b32_e32 v1, 32, v0
	v_or_b32_e32 v150, 0x2000, v2
	v_bfe_u32 v149, v0, 2, 4
	v_bitop3_b32 v1, v2, v1, 48 bitop3:0x6c
	v_and_b32_e32 v148, 64, v0
	v_lshrrev_b32_e32 v4, 3, v0
	v_lshrrev_b32_e32 v2, 7, v150
	s_movk_i32 s0, 0x70
	v_or_b32_e32 v3, v1, v148
	v_and_or_b32 v4, v4, 48, v149
	v_and_or_b32 v2, v2, s0, v149
	v_lshl_or_b32 v130, v4, 11, v3
	v_lshl_or_b32 v132, v2, 11, v3
	v_bfe_u32 v151, v0, 4, 2
	v_lshlrev_b32_e32 v2, 6, v0
	v_lshlrev_b32_e32 v3, 2, v0
	v_lshlrev_b32_e32 v153, 4, v151
	v_and_b32_e32 v2, 0x3c0, v2
	v_and_b32_e32 v3, 32, v3
	s_cmpk_lt_i32 s30, 0x200
	v_readfirstlane_b32 s33, v0
	v_and_b32_e32 v152, 15, v0
	s_cselect_b64 s[2:3], -1, 0
	s_cmpk_gt_i32 s30, 0x1ff
	v_bitop3_b32 v154, v153, v3, v2 bitop3:0x36
	s_barrier
	s_cbranch_scc1 .LBB0_3236
	s_add_u32 s34, s6, 0x3cf40000
	s_addc_u32 s35, s7, 0
	s_add_u32 s36, s6, 0x15540000
	s_addc_u32 s37, s7, 0
	s_ashr_i32 s39, s30, 31
	s_lshr_b32 s0, s39, 29
	s_add_i32 s0, s30, s0
	s_lshr_b32 s8, s33, 6
	s_ashr_i32 s9, s0, 3
	s_and_b32 s0, s0, -8
	s_lshr_b32 s1, s33, 8
	s_lshl_b32 s38, s8, 10
	s_sub_i32 s0, s30, s0
	s_cmp_lt_i32 s0, 0
	s_cselect_b32 s10, 0x41, 64
	s_mul_i32 s0, s10, s0
	s_add_i32 s0, s0, s9
	s_ashr_i32 s9, s0, 31
	s_lshr_b32 s9, s9, 26
	s_add_i32 s9, s0, s9
	s_ashr_i32 s10, s9, 6
	s_lshl_b32 s12, s10, 3
	s_sub_i32 s10, 64, s12
	s_min_u32 s13, s10, 8
	s_andn2_b32 s9, s9, 63
	s_sub_i32 s9, s0, s9
	v_cvt_f32_ubyte0_e32 v3, s13
	v_cvt_f32_i32_e32 v2, s9
	v_rcp_iflag_f32_e32 v4, v3
	s_ashr_i32 s0, s9, 30
	s_or_b32 s0, s0, 1
	v_mov_b32_e32 v131, 0
	v_mul_f32_e32 v4, v2, v4
	v_trunc_f32_e32 v4, v4
	v_fma_f32 v2, -v4, v3, v2
	v_cvt_i32_f32_e32 v4, v4
	v_cmp_ge_f32_e64 s[10:11], |v2|, v3
	s_and_b64 s[10:11], s[10:11], exec
	s_cselect_b32 s0, s0, 0
	v_readfirstlane_b32 s10, v4
	s_add_i32 s0, s10, s0
	s_mul_i32 s10, s0, s13
	s_sub_i32 s9, s9, s10
	s_sext_i32_i8 s9, s9
	s_add_i32 s22, s12, s9
	s_ashr_i32 s23, s22, 31
	s_lshl_b64 s[10:11], s[22:23], 19
	s_add_u32 s24, s34, s10
	s_addc_u32 s25, s35, s11
	s_bfe_i64 s[10:11], s[0:1], 0x80000
	s_lshl_b64 s[10:11], s[10:11], 19
	s_add_u32 s26, s36, s10
	s_addc_u32 s27, s37, s11
	s_add_i32 s23, s38, 0
	s_add_i32 m0, s23, 0x10000
	s_add_i32 s40, s23, 0x2000
	global_load_lds_dwordx4 v130, s[26:27]
	s_add_i32 m0, s23, 0x12000
	s_add_u32 s10, s26, 0x40000
	global_load_lds_dwordx4 v132, s[26:27]
	s_mov_b32 m0, s23
	s_addc_u32 s11, s27, 0
	global_load_lds_dwordx4 v130, s[24:25]
	s_mov_b32 m0, s40
	v_mov_b32_e32 v133, v131
	global_load_lds_dwordx4 v132, s[24:25]
	s_add_i32 m0, s23, 0x14000
	s_mov_b32 s43, 0
	global_load_lds_dwordx4 v130, s[10:11]
	s_add_i32 m0, s23, 0x16000
	s_waitcnt vmcnt(0)
	v_lshl_add_u64 v[8:9], s[26:27], 0, v[130:131]
	global_load_lds_dwordx4 v132, s[10:11]
	s_add_u32 s10, s24, 0x40000
	s_addc_u32 s11, s25, 0
	s_add_i32 s41, s23, 0x4000
	s_mov_b32 m0, s41
	s_add_i32 s42, s23, 0x6000
	global_load_lds_dwordx4 v130, s[10:11]
	s_mov_b32 m0, s42
	v_lshl_add_u64 v[6:7], s[26:27], 0, v[132:133]
	global_load_lds_dwordx4 v132, s[10:11]
	v_lshl_add_u64 v[4:5], s[24:25], 0, v[130:131]
	s_setprio 1
	s_cmp_lg_u32 s1, 1
	v_lshl_add_u64 v[2:3], s[24:25], 0, v[132:133]
	s_cbranch_scc1 .LBB0_3227
	s_barrier
	s_setprio 0

.LBB0_3231:
	ds_read_b128 v[142:145], v158
	ds_read_b128 v[162:165], v158 offset:1024
	ds_read_b128 v[166:169], v158 offset:2048
	ds_read_b128 v[170:173], v158 offset:3072
	s_add_u32 s26, s24, 0xfffc0080
	s_addc_u32 s27, s25, -1
	s_cmp_eq_u32 s55, 12
	s_cselect_b32 s29, s17, s27
	s_cselect_b32 s28, s51, s26
	s_cselect_b32 s27, s15, s54
	s_cselect_b32 s26, s52, s53
	v_lshl_add_u64 v[146:147], s[24:25], 0, v[134:135]
	s_add_i32 m0, s23, 0xc000
	ds_read_b128 v[174:177], v159
	ds_read_b128 v[178:181], v159 offset:1024
	ds_read_b128 v[182:185], v159 offset:2048
	ds_read_b128 v[186:189], v159 offset:3072
	ds_read_b128 v[190:193], v159 offset:4096
	ds_read_b128 v[194:197], v159 offset:5120
	ds_read_b128 v[198:201], v159 offset:6144
	ds_read_b128 v[202:205], v159 offset:7168
	global_load_lds_dwordx4 v[146:147], off
	v_lshl_add_u64 v[146:147], s[24:25], 0, v[136:137]
	s_add_i32 m0, s23, 0xe000
	s_nop 0
	global_load_lds_dwordx4 v[146:147], off
	s_waitcnt lgkmcnt(8)
	s_barrier
	s_waitcnt lgkmcnt(0)
	s_waitcnt lgkmcnt(0)
	v_mfma_f32_16x16x32_bf16 v[126:129], v[142:145], v[174:177], v[126:129]
	v_mfma_f32_16x16x32_bf16 v[122:125], v[166:169], v[174:177], v[122:125]
	v_mfma_f32_16x16x32_bf16 v[114:117], v[142:145], v[182:185], v[114:117]
	v_mfma_f32_16x16x32_bf16 v[106:109], v[166:169], v[182:185], v[106:109]
	v_mfma_f32_16x16x32_bf16 v[98:101], v[142:145], v[190:193], v[98:101]
	v_mfma_f32_16x16x32_bf16 v[90:93], v[166:169], v[190:193], v[90:93]
	v_mfma_f32_16x16x32_bf16 v[82:85], v[142:145], v[198:201], v[82:85]
	v_mfma_f32_16x16x32_bf16 v[74:77], v[166:169], v[198:201], v[74:77]
	v_mfma_f32_16x16x32_bf16 v[126:129], v[162:165], v[178:181], v[126:129]
	v_mfma_f32_16x16x32_bf16 v[122:125], v[170:173], v[178:181], v[122:125]
	v_mfma_f32_16x16x32_bf16 v[114:117], v[162:165], v[186:189], v[114:117]
	v_mfma_f32_16x16x32_bf16 v[106:109], v[170:173], v[186:189], v[106:109]
	v_mfma_f32_16x16x32_bf16 v[98:101], v[162:165], v[194:197], v[98:101]
	v_mfma_f32_16x16x32_bf16 v[90:93], v[170:173], v[194:197], v[90:93]
	v_mfma_f32_16x16x32_bf16 v[82:85], v[162:165], v[202:205], v[82:85]
	v_mfma_f32_16x16x32_bf16 v[74:77], v[170:173], v[202:205], v[74:77]
	s_barrier
	s_add_i32 s56, s47, s38
	v_lshl_add_u64 v[146:147], s[26:27], 0, v[130:131]
	s_mov_b32 m0, s56
	ds_read_b128 v[206:209], v160
	ds_read_b128 v[210:213], v160 offset:1024
	ds_read_b128 v[214:217], v160 offset:2048
	ds_read_b128 v[218:221], v160 offset:3072
	global_load_lds_dwordx4 v[146:147], off
	v_lshl_add_u64 v[222:223], s[26:27], 0, v[132:133]
	s_add_i32 m0, s56, 0x2000
	s_nop 0
	global_load_lds_dwordx4 v[222:223], off
	s_barrier
	s_waitcnt lgkmcnt(0)
	s_waitcnt lgkmcnt(0)
	v_mfma_f32_16x16x32_bf16 v[118:121], v[206:209], v[174:177], v[118:121]
	v_mfma_f32_16x16x32_bf16 v[110:113], v[214:217], v[174:177], v[110:113]
	v_mfma_f32_16x16x32_bf16 v[102:105], v[206:209], v[182:185], v[102:105]
	v_mfma_f32_16x16x32_bf16 v[94:97], v[214:217], v[182:185], v[94:97]
	v_mfma_f32_16x16x32_bf16 v[86:89], v[206:209], v[190:193], v[86:89]
	v_mfma_f32_16x16x32_bf16 v[78:81], v[214:217], v[190:193], v[78:81]
	v_mfma_f32_16x16x32_bf16 v[70:73], v[206:209], v[198:201], v[70:73]
	v_mfma_f32_16x16x32_bf16 v[66:69], v[214:217], v[198:201], v[66:69]
	v_mfma_f32_16x16x32_bf16 v[118:121], v[210:213], v[178:181], v[118:121]
	v_mfma_f32_16x16x32_bf16 v[110:113], v[218:221], v[178:181], v[110:113]
	v_mfma_f32_16x16x32_bf16 v[102:105], v[210:213], v[186:189], v[102:105]
	v_mfma_f32_16x16x32_bf16 v[94:97], v[218:221], v[186:189], v[94:97]
	v_mfma_f32_16x16x32_bf16 v[86:89], v[210:213], v[194:197], v[86:89]
	v_mfma_f32_16x16x32_bf16 v[78:81], v[218:221], v[194:197], v[78:81]
	v_mfma_f32_16x16x32_bf16 v[70:73], v[210:213], v[202:205], v[70:73]
	v_mfma_f32_16x16x32_bf16 v[66:69], v[218:221], v[202:205], v[66:69]
	s_mov_b32 m0, s23
	v_lshl_add_u64 v[224:225], s[28:29], 0, v[130:131]
	s_barrier
	ds_read_b128 v[174:177], v159 offset:16384
	ds_read_b128 v[178:181], v159 offset:17408
	ds_read_b128 v[182:185], v159 offset:18432
	ds_read_b128 v[186:189], v159 offset:19456
	ds_read_b128 v[190:193], v159 offset:20480
	ds_read_b128 v[194:197], v159 offset:21504
	ds_read_b128 v[198:201], v159 offset:22528
	ds_read_b128 v[202:205], v159 offset:23552
	global_load_lds_dwordx4 v[224:225], off
	v_lshl_add_u64 v[226:227], s[28:29], 0, v[132:133]
	s_mov_b32 m0, s40
	s_nop 0
	global_load_lds_dwordx4 v[226:227], off
	s_barrier
	s_waitcnt lgkmcnt(0)
	s_waitcnt lgkmcnt(0)
	v_mfma_f32_16x16x32_bf16 v[62:65], v[142:145], v[174:177], v[62:65]
	v_mfma_f32_16x16x32_bf16 v[58:61], v[166:169], v[174:177], v[58:61]
	v_mfma_f32_16x16x32_bf16 v[50:53], v[142:145], v[182:185], v[50:53]
	v_mfma_f32_16x16x32_bf16 v[42:45], v[166:169], v[182:185], v[42:45]
	v_mfma_f32_16x16x32_bf16 v[34:37], v[142:145], v[190:193], v[34:37]
	v_mfma_f32_16x16x32_bf16 v[26:29], v[166:169], v[190:193], v[26:29]
	v_mfma_f32_16x16x32_bf16 v[18:21], v[142:145], v[198:201], v[18:21]
	v_mfma_f32_16x16x32_bf16 v[10:13], v[166:169], v[198:201], v[10:13]
	v_mfma_f32_16x16x32_bf16 v[62:65], v[162:165], v[178:181], v[62:65]
	v_mfma_f32_16x16x32_bf16 v[58:61], v[170:173], v[178:181], v[58:61]
	v_mfma_f32_16x16x32_bf16 v[50:53], v[162:165], v[186:189], v[50:53]
	v_mfma_f32_16x16x32_bf16 v[42:45], v[170:173], v[186:189], v[42:45]
	v_mfma_f32_16x16x32_bf16 v[34:37], v[162:165], v[194:197], v[34:37]
	v_mfma_f32_16x16x32_bf16 v[26:29], v[170:173], v[194:197], v[26:29]
	v_mfma_f32_16x16x32_bf16 v[18:21], v[162:165], v[202:205], v[18:21]
	v_mfma_f32_16x16x32_bf16 v[10:13], v[170:173], v[202:205], v[10:13]
	s_barrier
	s_add_u32 s56, s26, 0x40000
	s_addc_u32 s57, s27, 0
	s_add_i32 s58, s48, s38
	v_lshl_add_u64 v[142:143], s[56:57], 0, v[130:131]
	s_mov_b32 m0, s58
	s_nop 0
	global_load_lds_dwordx4 v[142:143], off
	v_lshl_add_u64 v[142:143], s[56:57], 0, v[132:133]
	s_add_i32 m0, s58, 0x2000
	s_nop 0
	global_load_lds_dwordx4 v[142:143], off
	s_waitcnt vmcnt(6)
	s_barrier
	v_mfma_f32_16x16x32_bf16 v[54:57], v[206:209], v[174:177], v[54:57]
	v_mfma_f32_16x16x32_bf16 v[46:49], v[214:217], v[174:177], v[46:49]
	v_mfma_f32_16x16x32_bf16 v[38:41], v[206:209], v[182:185], v[38:41]
	v_mfma_f32_16x16x32_bf16 v[30:33], v[214:217], v[182:185], v[30:33]
	v_mfma_f32_16x16x32_bf16 v[22:25], v[206:209], v[190:193], v[22:25]
	v_mfma_f32_16x16x32_bf16 v[14:17], v[214:217], v[190:193], v[14:17]
	v_mfma_f32_16x16x32_bf16 v[6:9], v[206:209], v[198:201], v[6:9]
	v_mfma_f32_16x16x32_bf16 v[2:5], v[214:217], v[198:201], v[2:5]
	v_mfma_f32_16x16x32_bf16 v[54:57], v[210:213], v[178:181], v[54:57]
	v_mfma_f32_16x16x32_bf16 v[46:49], v[218:221], v[178:181], v[46:49]
	v_mfma_f32_16x16x32_bf16 v[38:41], v[210:213], v[186:189], v[38:41]
	v_mfma_f32_16x16x32_bf16 v[30:33], v[218:221], v[186:189], v[30:33]
	v_mfma_f32_16x16x32_bf16 v[22:25], v[210:213], v[194:197], v[22:25]
	v_mfma_f32_16x16x32_bf16 v[14:17], v[218:221], v[194:197], v[14:17]
	v_mfma_f32_16x16x32_bf16 v[6:9], v[210:213], v[202:205], v[6:9]
	v_mfma_f32_16x16x32_bf16 v[2:5], v[218:221], v[202:205], v[2:5]
	s_add_i32 s56, 0, 0x18000
	v_add_u32_e32 v161, s56, v156
	s_barrier
	ds_read_b128 v[142:145], v161
	ds_read_b128 v[162:165], v161 offset:1024
	ds_read_b128 v[166:169], v161 offset:2048
	ds_read_b128 v[170:173], v161 offset:3072
	s_add_u32 s28, s28, 0x40000
	s_addc_u32 s29, s29, 0
	s_mov_b32 m0, s41
	v_lshl_add_u64 v[206:207], s[28:29], 0, v[130:131]
	ds_read_b128 v[174:177], v159 offset:32768
	ds_read_b128 v[178:181], v159 offset:33792
	ds_read_b128 v[182:185], v159 offset:34816
	ds_read_b128 v[186:189], v159 offset:35840
	ds_read_b128 v[190:193], v159 offset:36864
	ds_read_b128 v[194:197], v159 offset:37888
	ds_read_b128 v[198:201], v159 offset:38912
	ds_read_b128 v[202:205], v159 offset:39936
	global_load_lds_dwordx4 v[206:207], off
	v_lshl_add_u64 v[206:207], s[28:29], 0, v[132:133]
	s_mov_b32 m0, s42
	s_nop 0
	global_load_lds_dwordx4 v[206:207], off
	s_waitcnt lgkmcnt(8)
	s_barrier
	s_waitcnt lgkmcnt(0)
	s_waitcnt lgkmcnt(0)
	v_mfma_f32_16x16x32_bf16 v[126:129], v[142:145], v[174:177], v[126:129]
	v_mfma_f32_16x16x32_bf16 v[122:125], v[166:169], v[174:177], v[122:125]
	v_mfma_f32_16x16x32_bf16 v[114:117], v[142:145], v[182:185], v[114:117]
	v_mfma_f32_16x16x32_bf16 v[106:109], v[166:169], v[182:185], v[106:109]
	v_mfma_f32_16x16x32_bf16 v[98:101], v[142:145], v[190:193], v[98:101]
	v_mfma_f32_16x16x32_bf16 v[90:93], v[166:169], v[190:193], v[90:93]
	v_mfma_f32_16x16x32_bf16 v[82:85], v[142:145], v[198:201], v[82:85]
	v_mfma_f32_16x16x32_bf16 v[74:77], v[166:169], v[198:201], v[74:77]
	v_mfma_f32_16x16x32_bf16 v[126:129], v[162:165], v[178:181], v[126:129]
	v_mfma_f32_16x16x32_bf16 v[122:125], v[170:173], v[178:181], v[122:125]
	v_mfma_f32_16x16x32_bf16 v[114:117], v[162:165], v[186:189], v[114:117]
	v_mfma_f32_16x16x32_bf16 v[106:109], v[170:173], v[186:189], v[106:109]
	v_mfma_f32_16x16x32_bf16 v[98:101], v[162:165], v[194:197], v[98:101]
	v_mfma_f32_16x16x32_bf16 v[90:93], v[170:173], v[194:197], v[90:93]
	v_mfma_f32_16x16x32_bf16 v[82:85], v[162:165], v[202:205], v[82:85]
	v_mfma_f32_16x16x32_bf16 v[74:77], v[170:173], v[202:205], v[74:77]
	s_barrier
	s_add_i32 s28, 0, 0x1c000
	s_add_i32 s29, s56, s38
	v_add_u32_e32 v161, s28, v156
	v_lshl_add_u64 v[146:147], v[146:147], 0, s[8:9]
	s_mov_b32 m0, s29
	ds_read_b128 v[206:209], v161
	ds_read_b128 v[210:213], v161 offset:1024
	ds_read_b128 v[214:217], v161 offset:2048
	ds_read_b128 v[218:221], v161 offset:3072
	global_load_lds_dwordx4 v[146:147], off
	v_lshl_add_u64 v[146:147], v[222:223], 0, s[8:9]
	s_add_i32 m0, s29, 0x2000
	s_nop 0
	global_load_lds_dwordx4 v[146:147], off
	s_barrier
	s_waitcnt lgkmcnt(0)
	s_waitcnt lgkmcnt(0)
	v_mfma_f32_16x16x32_bf16 v[118:121], v[206:209], v[174:177], v[118:121]
	v_mfma_f32_16x16x32_bf16 v[110:113], v[214:217], v[174:177], v[110:113]
	v_mfma_f32_16x16x32_bf16 v[102:105], v[206:209], v[182:185], v[102:105]
	v_mfma_f32_16x16x32_bf16 v[94:97], v[214:217], v[182:185], v[94:97]
	v_mfma_f32_16x16x32_bf16 v[86:89], v[206:209], v[190:193], v[86:89]
	v_mfma_f32_16x16x32_bf16 v[78:81], v[214:217], v[190:193], v[78:81]
	v_mfma_f32_16x16x32_bf16 v[70:73], v[206:209], v[198:201], v[70:73]
	v_mfma_f32_16x16x32_bf16 v[66:69], v[214:217], v[198:201], v[66:69]
	v_mfma_f32_16x16x32_bf16 v[118:121], v[210:213], v[178:181], v[118:121]
	v_mfma_f32_16x16x32_bf16 v[110:113], v[218:221], v[178:181], v[110:113]
	v_mfma_f32_16x16x32_bf16 v[102:105], v[210:213], v[186:189], v[102:105]
	v_mfma_f32_16x16x32_bf16 v[94:97], v[218:221], v[186:189], v[94:97]
	v_mfma_f32_16x16x32_bf16 v[86:89], v[210:213], v[194:197], v[86:89]
	v_mfma_f32_16x16x32_bf16 v[78:81], v[218:221], v[194:197], v[78:81]
	v_mfma_f32_16x16x32_bf16 v[70:73], v[210:213], v[202:205], v[70:73]
	v_mfma_f32_16x16x32_bf16 v[66:69], v[218:221], v[202:205], v[66:69]
	s_mov_b32 m0, s44
	v_lshl_add_u64 v[146:147], v[224:225], 0, s[8:9]
	s_barrier
	ds_read_b128 v[174:177], v159 offset:49152
	ds_read_b128 v[178:181], v159 offset:50176
	ds_read_b128 v[182:185], v159 offset:51200
	ds_read_b128 v[186:189], v159 offset:52224
	ds_read_b128 v[190:193], v159 offset:53248
	ds_read_b128 v[194:197], v159 offset:54272
	ds_read_b128 v[198:201], v159 offset:55296
	ds_read_b128 v[202:205], v159 offset:56320
	global_load_lds_dwordx4 v[146:147], off
	v_lshl_add_u64 v[146:147], v[226:227], 0, s[8:9]
	s_mov_b32 m0, s45
	s_nop 0
	global_load_lds_dwordx4 v[146:147], off
	s_barrier
	s_waitcnt lgkmcnt(0)
	s_waitcnt lgkmcnt(0)
	v_mfma_f32_16x16x32_bf16 v[62:65], v[142:145], v[174:177], v[62:65]
	v_mfma_f32_16x16x32_bf16 v[58:61], v[166:169], v[174:177], v[58:61]
	v_mfma_f32_16x16x32_bf16 v[50:53], v[142:145], v[182:185], v[50:53]
	v_mfma_f32_16x16x32_bf16 v[42:45], v[166:169], v[182:185], v[42:45]
	v_mfma_f32_16x16x32_bf16 v[34:37], v[142:145], v[190:193], v[34:37]
	v_mfma_f32_16x16x32_bf16 v[26:29], v[166:169], v[190:193], v[26:29]
	v_mfma_f32_16x16x32_bf16 v[18:21], v[142:145], v[198:201], v[18:21]
	v_mfma_f32_16x16x32_bf16 v[10:13], v[166:169], v[198:201], v[10:13]
	v_mfma_f32_16x16x32_bf16 v[62:65], v[162:165], v[178:181], v[62:65]
	v_mfma_f32_16x16x32_bf16 v[58:61], v[170:173], v[178:181], v[58:61]
	v_mfma_f32_16x16x32_bf16 v[50:53], v[162:165], v[186:189], v[50:53]
	v_mfma_f32_16x16x32_bf16 v[42:45], v[170:173], v[186:189], v[42:45]
	v_mfma_f32_16x16x32_bf16 v[34:37], v[162:165], v[194:197], v[34:37]
	v_mfma_f32_16x16x32_bf16 v[26:29], v[170:173], v[194:197], v[26:29]
	v_mfma_f32_16x16x32_bf16 v[18:21], v[162:165], v[202:205], v[18:21]
	v_mfma_f32_16x16x32_bf16 v[10:13], v[170:173], v[202:205], v[10:13]
	s_barrier
	s_add_u32 s26, s26, 0x40080
	s_addc_u32 s27, s27, 0
	s_add_i32 s28, s28, s38
	v_lshl_add_u64 v[142:143], s[26:27], 0, v[130:131]
	s_mov_b32 m0, s28
	s_nop 0
	global_load_lds_dwordx4 v[142:143], off
	v_lshl_add_u64 v[142:143], s[26:27], 0, v[132:133]
	s_add_i32 m0, s28, 0x2000
	s_nop 0
	global_load_lds_dwordx4 v[142:143], off
	s_waitcnt vmcnt(6)
	s_barrier
	v_mfma_f32_16x16x32_bf16 v[54:57], v[206:209], v[174:177], v[54:57]
	v_mfma_f32_16x16x32_bf16 v[46:49], v[214:217], v[174:177], v[46:49]
	v_mfma_f32_16x16x32_bf16 v[38:41], v[206:209], v[182:185], v[38:41]
	v_mfma_f32_16x16x32_bf16 v[30:33], v[214:217], v[182:185], v[30:33]
	v_mfma_f32_16x16x32_bf16 v[22:25], v[206:209], v[190:193], v[22:25]
	v_mfma_f32_16x16x32_bf16 v[14:17], v[214:217], v[190:193], v[14:17]
	v_mfma_f32_16x16x32_bf16 v[6:9], v[206:209], v[198:201], v[6:9]
	v_mfma_f32_16x16x32_bf16 v[2:5], v[214:217], v[198:201], v[2:5]
	v_mfma_f32_16x16x32_bf16 v[54:57], v[210:213], v[178:181], v[54:57]
	v_mfma_f32_16x16x32_bf16 v[46:49], v[218:221], v[178:181], v[46:49]
	v_mfma_f32_16x16x32_bf16 v[38:41], v[210:213], v[186:189], v[38:41]
	v_mfma_f32_16x16x32_bf16 v[30:33], v[218:221], v[186:189], v[30:33]
	v_mfma_f32_16x16x32_bf16 v[22:25], v[210:213], v[194:197], v[22:25]
	v_mfma_f32_16x16x32_bf16 v[14:17], v[218:221], v[194:197], v[14:17]
	v_mfma_f32_16x16x32_bf16 v[6:9], v[210:213], v[202:205], v[6:9]
	v_mfma_f32_16x16x32_bf16 v[2:5], v[218:221], v[202:205], v[2:5]
	s_add_i32 s55, s55, 2
	s_add_u32 s24, s24, 0x100
	s_addc_u32 s25, s25, 0
	s_add_u32 s53, s53, 0x100
	s_addc_u32 s54, s54, 0
	s_cmp_gt_u32 s55, 13
	s_barrier
	s_cbranch_scc0 .LBB0_3231
	v_lshl_or_b32 v142, s50, 8, v157
	v_lshl_add_u32 v144, s22, 8, v155
	v_ashrrev_i32_e32 v143, 31, v142
	v_mov_b64_e32 v[146:147], s[10:11]
	v_mad_i64_i32 v[162:163], s[24:25], v144, s49, v[146:147]
	v_lshlrev_b64 v[142:143], 1, v[142:143]
	v_lshl_add_u64 v[162:163], v[162:163], 0, v[142:143]
	v_mov_b32_e32 v238, v162
	v_mov_b32_e32 v239, v163
	global_load_dwordx2 v[168:169], v[238:239], off
	global_load_dwordx2 v[170:171], v[238:239], off offset:32
	global_load_dwordx2 v[172:173], v[238:239], off offset:256
	global_load_dwordx2 v[174:175], v[238:239], off offset:288
	v_mov_b32_e32 v242, 16
	v_mad_i64_i32 v[240:241], s[24:25], v242, s49, v[238:239]
	global_load_dwordx2 v[176:177], v[240:241], off
	global_load_dwordx2 v[178:179], v[240:241], off offset:32
	global_load_dwordx2 v[180:181], v[240:241], off offset:256
	global_load_dwordx2 v[182:183], v[240:241], off offset:288
	v_mov_b32_e32 v242, 32
	v_mad_i64_i32 v[240:241], s[24:25], v242, s49, v[238:239]
	global_load_dwordx2 v[184:185], v[240:241], off
	global_load_dwordx2 v[186:187], v[240:241], off offset:32
	global_load_dwordx2 v[188:189], v[240:241], off offset:256
	global_load_dwordx2 v[190:191], v[240:241], off offset:288
	v_mov_b32_e32 v242, 48
	v_mad_i64_i32 v[240:241], s[24:25], v242, s49, v[238:239]
	global_load_dwordx2 v[192:193], v[240:241], off
	global_load_dwordx2 v[194:195], v[240:241], off offset:32
	global_load_dwordx2 v[196:197], v[240:241], off offset:256
	global_load_dwordx2 v[198:199], v[240:241], off offset:288
	v_mov_b32_e32 v242, 128
	v_mad_i64_i32 v[240:241], s[24:25], v242, s49, v[238:239]
	global_load_dwordx2 v[200:201], v[240:241], off
	global_load_dwordx2 v[202:203], v[240:241], off offset:32
	global_load_dwordx2 v[204:205], v[240:241], off offset:256
	global_load_dwordx2 v[206:207], v[240:241], off offset:288
	v_mov_b32_e32 v242, 144
	v_mad_i64_i32 v[240:241], s[24:25], v242, s49, v[238:239]
	global_load_dwordx2 v[208:209], v[240:241], off
	global_load_dwordx2 v[210:211], v[240:241], off offset:32
	global_load_dwordx2 v[212:213], v[240:241], off offset:256
	global_load_dwordx2 v[214:215], v[240:241], off offset:288
	v_mov_b32_e32 v242, 160
	v_mad_i64_i32 v[240:241], s[24:25], v242, s49, v[238:239]
	global_load_dwordx2 v[216:217], v[240:241], off
	global_load_dwordx2 v[218:219], v[240:241], off offset:32
	global_load_dwordx2 v[220:221], v[240:241], off offset:256
	global_load_dwordx2 v[228:229], v[240:241], off offset:288
	v_mov_b32_e32 v242, 176
	v_mad_i64_i32 v[240:241], s[24:25], v242, s49, v[238:239]
	global_load_dwordx2 v[230:231], v[240:241], off
	global_load_dwordx2 v[232:233], v[240:241], off offset:32
	global_load_dwordx2 v[234:235], v[240:241], off offset:256
	global_load_dwordx2 v[236:237], v[240:241], off offset:288
	s_waitcnt vmcnt(0)
	v_mov_b32_e32 v164, v168
	v_mov_b32_e32 v165, v169
	v_ashrrev_i32_e32 v145, 31, v144
	s_and_b64 vcc, exec, s[0:1]
	s_mov_b32 s50, s14
	s_mov_b32 s22, s16
	s_mov_b64 s[26:27], s[20:21]
	s_nop 0
	v_lshlrev_b32_e32 v166, 16, v164
	v_and_b32_e32 v167, 0xffff0000, v164
	v_lshlrev_b32_e32 v164, 16, v165
	v_and_b32_e32 v165, 0xffff0000, v165
	v_pk_mul_f32 v[128:129], v[128:129], v[164:165]
	v_pk_mul_f32 v[126:127], v[126:127], v[166:167]
	v_lshlrev_b64 v[164:165], 12, v[144:145]
	v_cvt_pk_bf16_f32 v126, v126, v127
	v_cvt_pk_bf16_f32 v127, v128, v129
	v_mov_b32_e32 v128, v170
	v_mov_b32_e32 v129, v171
	v_lshl_add_u64 v[164:165], s[12:13], 0, v[164:165]
	v_lshl_add_u64 v[164:165], v[164:165], 0, v[142:143]
	global_store_dwordx2 v[164:165], v[126:127], off
	s_nop 0
	v_lshlrev_b32_e32 v126, 16, v128
	v_and_b32_e32 v127, 0xffff0000, v128
	v_lshlrev_b32_e32 v128, 16, v129
	v_and_b32_e32 v129, 0xffff0000, v129
	v_pk_mul_f32 v[124:125], v[124:125], v[128:129]
	v_pk_mul_f32 v[122:123], v[122:123], v[126:127]
	s_nop 0
	v_cvt_pk_bf16_f32 v122, v122, v123
	v_cvt_pk_bf16_f32 v123, v124, v125
	v_mov_b32_e32 v124, v172
	v_mov_b32_e32 v125, v173
	s_nop 0
	global_store_dwordx2 v[164:165], v[122:123], off offset:32
	s_nop 0
	v_lshlrev_b32_e32 v122, 16, v124
	v_and_b32_e32 v123, 0xffff0000, v124
	v_lshlrev_b32_e32 v124, 16, v125
	v_and_b32_e32 v125, 0xffff0000, v125
	v_pk_mul_f32 v[120:121], v[120:121], v[124:125]
	v_pk_mul_f32 v[118:119], v[118:119], v[122:123]
	v_or_b32_e32 v122, 16, v144
	v_cvt_pk_bf16_f32 v118, v118, v119
	v_cvt_pk_bf16_f32 v119, v120, v121
	v_mov_b32_e32 v120, v174
	v_mov_b32_e32 v121, v175
	v_mad_i64_i32 v[124:125], s[24:25], v122, s49, v[146:147]
	global_store_dwordx2 v[164:165], v[118:119], off offset:256
	v_lshl_add_u64 v[124:125], v[124:125], 0, v[142:143]
	v_ashrrev_i32_e32 v123, 31, v122
	s_nop 0
	v_lshlrev_b32_e32 v118, 16, v120
	v_and_b32_e32 v119, 0xffff0000, v120
	v_lshlrev_b32_e32 v120, 16, v121
	v_and_b32_e32 v121, 0xffff0000, v121
	v_pk_mul_f32 v[112:113], v[112:113], v[120:121]
	v_pk_mul_f32 v[110:111], v[110:111], v[118:119]
	s_nop 0
	v_cvt_pk_bf16_f32 v110, v110, v111
	v_cvt_pk_bf16_f32 v111, v112, v113
	v_mov_b32_e32 v112, v176
	v_mov_b32_e32 v113, v177
	s_nop 0
	global_store_dwordx2 v[164:165], v[110:111], off offset:288
	s_nop 0
	v_lshlrev_b32_e32 v110, 16, v112
	v_and_b32_e32 v111, 0xffff0000, v112
	v_lshlrev_b32_e32 v112, 16, v113
	v_and_b32_e32 v113, 0xffff0000, v113
	v_pk_mul_f32 v[112:113], v[116:117], v[112:113]
	v_pk_mul_f32 v[110:111], v[114:115], v[110:111]
	v_lshlrev_b64 v[114:115], 12, v[122:123]
	v_cvt_pk_bf16_f32 v110, v110, v111
	v_cvt_pk_bf16_f32 v111, v112, v113
	v_mov_b32_e32 v112, v178
	v_mov_b32_e32 v113, v179
	v_lshl_add_u64 v[114:115], s[12:13], 0, v[114:115]
	v_lshl_add_u64 v[114:115], v[114:115], 0, v[142:143]
	global_store_dwordx2 v[114:115], v[110:111], off
	s_nop 0
	v_lshlrev_b32_e32 v110, 16, v112
	v_and_b32_e32 v111, 0xffff0000, v112
	v_lshlrev_b32_e32 v112, 16, v113
	v_and_b32_e32 v113, 0xffff0000, v113
	v_pk_mul_f32 v[108:109], v[108:109], v[112:113]
	v_pk_mul_f32 v[106:107], v[106:107], v[110:111]
	s_nop 0
	v_cvt_pk_bf16_f32 v106, v106, v107
	v_cvt_pk_bf16_f32 v107, v108, v109
	v_mov_b32_e32 v108, v180
	v_mov_b32_e32 v109, v181
	s_nop 0
	global_store_dwordx2 v[114:115], v[106:107], off offset:32
	s_nop 0
	v_lshlrev_b32_e32 v106, 16, v108
	v_and_b32_e32 v107, 0xffff0000, v108
	v_lshlrev_b32_e32 v108, 16, v109
	v_and_b32_e32 v109, 0xffff0000, v109
	v_pk_mul_f32 v[104:105], v[104:105], v[108:109]
	v_pk_mul_f32 v[102:103], v[102:103], v[106:107]
	v_or_b32_e32 v106, 32, v144
	v_cvt_pk_bf16_f32 v102, v102, v103
	v_cvt_pk_bf16_f32 v103, v104, v105
	v_mov_b32_e32 v104, v182
	v_mov_b32_e32 v105, v183
	v_mad_i64_i32 v[108:109], s[24:25], v106, s49, v[146:147]
	global_store_dwordx2 v[114:115], v[102:103], off offset:256
	v_lshl_add_u64 v[108:109], v[108:109], 0, v[142:143]
	v_ashrrev_i32_e32 v107, 31, v106
	s_nop 0
	v_lshlrev_b32_e32 v102, 16, v104
	v_and_b32_e32 v103, 0xffff0000, v104
	v_lshlrev_b32_e32 v104, 16, v105
	v_and_b32_e32 v105, 0xffff0000, v105
	v_pk_mul_f32 v[96:97], v[96:97], v[104:105]
	v_pk_mul_f32 v[94:95], v[94:95], v[102:103]
	s_nop 0
	v_cvt_pk_bf16_f32 v94, v94, v95
	v_cvt_pk_bf16_f32 v95, v96, v97
	v_mov_b32_e32 v96, v184
	v_mov_b32_e32 v97, v185
	s_nop 0
	global_store_dwordx2 v[114:115], v[94:95], off offset:288
	s_nop 0
	v_lshlrev_b32_e32 v94, 16, v96
	v_and_b32_e32 v95, 0xffff0000, v96
	v_lshlrev_b32_e32 v96, 16, v97
	v_and_b32_e32 v97, 0xffff0000, v97
	v_pk_mul_f32 v[96:97], v[100:101], v[96:97]
	v_pk_mul_f32 v[94:95], v[98:99], v[94:95]
	v_lshlrev_b64 v[98:99], 12, v[106:107]
	v_cvt_pk_bf16_f32 v94, v94, v95
	v_cvt_pk_bf16_f32 v95, v96, v97
	v_mov_b32_e32 v96, v186
	v_mov_b32_e32 v97, v187
	v_lshl_add_u64 v[98:99], s[12:13], 0, v[98:99]
	v_lshl_add_u64 v[98:99], v[98:99], 0, v[142:143]
	global_store_dwordx2 v[98:99], v[94:95], off
	s_nop 0
	v_lshlrev_b32_e32 v94, 16, v96
	v_and_b32_e32 v95, 0xffff0000, v96
	v_lshlrev_b32_e32 v96, 16, v97
	v_and_b32_e32 v97, 0xffff0000, v97
	v_pk_mul_f32 v[92:93], v[92:93], v[96:97]
	v_pk_mul_f32 v[90:91], v[90:91], v[94:95]
	s_nop 0
	v_cvt_pk_bf16_f32 v90, v90, v91
	v_cvt_pk_bf16_f32 v91, v92, v93
	v_mov_b32_e32 v92, v188
	v_mov_b32_e32 v93, v189
	s_nop 0
	global_store_dwordx2 v[98:99], v[90:91], off offset:32
	s_nop 0
	v_lshlrev_b32_e32 v90, 16, v92
	v_and_b32_e32 v91, 0xffff0000, v92
	v_lshlrev_b32_e32 v92, 16, v93
	v_and_b32_e32 v93, 0xffff0000, v93
	v_pk_mul_f32 v[88:89], v[88:89], v[92:93]
	v_pk_mul_f32 v[86:87], v[86:87], v[90:91]
	v_or_b32_e32 v90, 48, v144
	v_cvt_pk_bf16_f32 v86, v86, v87
	v_cvt_pk_bf16_f32 v87, v88, v89
	v_mov_b32_e32 v88, v190
	v_mov_b32_e32 v89, v191
	v_mad_i64_i32 v[92:93], s[24:25], v90, s49, v[146:147]
	global_store_dwordx2 v[98:99], v[86:87], off offset:256
	v_lshl_add_u64 v[92:93], v[92:93], 0, v[142:143]
	v_ashrrev_i32_e32 v91, 31, v90
	s_nop 0
	v_lshlrev_b32_e32 v86, 16, v88
	v_and_b32_e32 v87, 0xffff0000, v88
	v_lshlrev_b32_e32 v88, 16, v89
	v_and_b32_e32 v89, 0xffff0000, v89
	v_pk_mul_f32 v[80:81], v[80:81], v[88:89]
	v_pk_mul_f32 v[78:79], v[78:79], v[86:87]
	s_nop 0
	v_cvt_pk_bf16_f32 v78, v78, v79
	v_cvt_pk_bf16_f32 v79, v80, v81
	v_mov_b32_e32 v80, v192
	v_mov_b32_e32 v81, v193
	s_nop 0
	global_store_dwordx2 v[98:99], v[78:79], off offset:288
	s_nop 0
	v_lshlrev_b32_e32 v78, 16, v80
	v_and_b32_e32 v79, 0xffff0000, v80
	v_lshlrev_b32_e32 v80, 16, v81
	v_and_b32_e32 v81, 0xffff0000, v81
	v_pk_mul_f32 v[80:81], v[84:85], v[80:81]
	v_pk_mul_f32 v[78:79], v[82:83], v[78:79]
	v_lshlrev_b64 v[82:83], 12, v[90:91]
	v_cvt_pk_bf16_f32 v78, v78, v79
	v_cvt_pk_bf16_f32 v79, v80, v81
	v_mov_b32_e32 v80, v194
	v_mov_b32_e32 v81, v195
	v_lshl_add_u64 v[82:83], s[12:13], 0, v[82:83]
	v_lshl_add_u64 v[82:83], v[82:83], 0, v[142:143]
	global_store_dwordx2 v[82:83], v[78:79], off
	s_nop 0
	v_lshlrev_b32_e32 v78, 16, v80
	v_and_b32_e32 v79, 0xffff0000, v80
	v_lshlrev_b32_e32 v80, 16, v81
	v_and_b32_e32 v81, 0xffff0000, v81
	v_pk_mul_f32 v[76:77], v[76:77], v[80:81]
	v_pk_mul_f32 v[74:75], v[74:75], v[78:79]
	s_nop 0
	v_cvt_pk_bf16_f32 v74, v74, v75
	v_cvt_pk_bf16_f32 v75, v76, v77
	v_mov_b32_e32 v76, v196
	v_mov_b32_e32 v77, v197
	s_nop 0
	global_store_dwordx2 v[82:83], v[74:75], off offset:32
	s_nop 0
	v_lshlrev_b32_e32 v74, 16, v76
	v_and_b32_e32 v75, 0xffff0000, v76
	v_lshlrev_b32_e32 v76, 16, v77
	v_and_b32_e32 v77, 0xffff0000, v77
	v_pk_mul_f32 v[72:73], v[72:73], v[76:77]
	v_pk_mul_f32 v[70:71], v[70:71], v[74:75]
	v_add_u32_e32 v74, 0x80, v144
	v_cvt_pk_bf16_f32 v70, v70, v71
	v_cvt_pk_bf16_f32 v71, v72, v73
	v_mov_b32_e32 v72, v198
	v_mov_b32_e32 v73, v199
	v_mad_i64_i32 v[76:77], s[24:25], v74, s49, v[146:147]
	global_store_dwordx2 v[82:83], v[70:71], off offset:256
	v_lshl_add_u64 v[76:77], v[76:77], 0, v[142:143]
	v_ashrrev_i32_e32 v75, 31, v74
	s_nop 0
	v_lshlrev_b32_e32 v70, 16, v72
	v_and_b32_e32 v71, 0xffff0000, v72
	v_lshlrev_b32_e32 v72, 16, v73
	v_and_b32_e32 v73, 0xffff0000, v73
	v_pk_mul_f32 v[68:69], v[68:69], v[72:73]
	v_pk_mul_f32 v[66:67], v[66:67], v[70:71]
	s_nop 0
	v_cvt_pk_bf16_f32 v66, v66, v67
	v_cvt_pk_bf16_f32 v67, v68, v69
	v_mov_b32_e32 v68, v200
	v_mov_b32_e32 v69, v201
	s_nop 0
	global_store_dwordx2 v[82:83], v[66:67], off offset:288
	s_nop 0
	v_lshlrev_b32_e32 v66, 16, v68
	v_and_b32_e32 v67, 0xffff0000, v68
	v_lshlrev_b32_e32 v68, 16, v69
	v_and_b32_e32 v69, 0xffff0000, v69
	v_pk_mul_f32 v[64:65], v[64:65], v[68:69]
	v_pk_mul_f32 v[62:63], v[62:63], v[66:67]
	v_lshlrev_b64 v[66:67], 12, v[74:75]
	v_cvt_pk_bf16_f32 v62, v62, v63
	v_cvt_pk_bf16_f32 v63, v64, v65
	v_mov_b32_e32 v64, v202
	v_mov_b32_e32 v65, v203
	v_lshl_add_u64 v[66:67], s[12:13], 0, v[66:67]
	v_lshl_add_u64 v[66:67], v[66:67], 0, v[142:143]
	global_store_dwordx2 v[66:67], v[62:63], off
	s_nop 0
	v_lshlrev_b32_e32 v62, 16, v64
	v_and_b32_e32 v63, 0xffff0000, v64
	v_lshlrev_b32_e32 v64, 16, v65
	v_and_b32_e32 v65, 0xffff0000, v65
	v_pk_mul_f32 v[60:61], v[60:61], v[64:65]
	v_pk_mul_f32 v[58:59], v[58:59], v[62:63]
	s_nop 0
	v_cvt_pk_bf16_f32 v58, v58, v59
	v_cvt_pk_bf16_f32 v59, v60, v61
	v_mov_b32_e32 v60, v204
	v_mov_b32_e32 v61, v205
	s_nop 0
	global_store_dwordx2 v[66:67], v[58:59], off offset:32
	s_nop 0
	v_lshlrev_b32_e32 v58, 16, v60
	v_and_b32_e32 v59, 0xffff0000, v60
	v_lshlrev_b32_e32 v60, 16, v61
	v_and_b32_e32 v61, 0xffff0000, v61
	v_pk_mul_f32 v[56:57], v[56:57], v[60:61]
	v_pk_mul_f32 v[54:55], v[54:55], v[58:59]
	v_add_u32_e32 v58, 0x90, v144
	v_cvt_pk_bf16_f32 v54, v54, v55
	v_cvt_pk_bf16_f32 v55, v56, v57
	v_mov_b32_e32 v56, v206
	v_mov_b32_e32 v57, v207
	v_mad_i64_i32 v[60:61], s[24:25], v58, s49, v[146:147]
	global_store_dwordx2 v[66:67], v[54:55], off offset:256
	v_lshl_add_u64 v[60:61], v[60:61], 0, v[142:143]
	v_ashrrev_i32_e32 v59, 31, v58
	s_nop 0
	v_lshlrev_b32_e32 v54, 16, v56
	v_and_b32_e32 v55, 0xffff0000, v56
	v_lshlrev_b32_e32 v56, 16, v57
	v_and_b32_e32 v57, 0xffff0000, v57
	v_pk_mul_f32 v[48:49], v[48:49], v[56:57]
	v_pk_mul_f32 v[46:47], v[46:47], v[54:55]
	s_nop 0
	v_cvt_pk_bf16_f32 v46, v46, v47
	v_cvt_pk_bf16_f32 v47, v48, v49
	v_mov_b32_e32 v48, v208
	v_mov_b32_e32 v49, v209
	s_nop 0
	global_store_dwordx2 v[66:67], v[46:47], off offset:288
	s_nop 0
	v_lshlrev_b32_e32 v46, 16, v48
	v_and_b32_e32 v47, 0xffff0000, v48
	v_lshlrev_b32_e32 v48, 16, v49
	v_and_b32_e32 v49, 0xffff0000, v49
	v_pk_mul_f32 v[48:49], v[52:53], v[48:49]
	v_pk_mul_f32 v[46:47], v[50:51], v[46:47]
	v_lshlrev_b64 v[50:51], 12, v[58:59]
	v_cvt_pk_bf16_f32 v46, v46, v47
	v_cvt_pk_bf16_f32 v47, v48, v49
	v_mov_b32_e32 v48, v210
	v_mov_b32_e32 v49, v211
	v_lshl_add_u64 v[50:51], s[12:13], 0, v[50:51]
	v_lshl_add_u64 v[50:51], v[50:51], 0, v[142:143]
	global_store_dwordx2 v[50:51], v[46:47], off
	s_nop 0
	v_lshlrev_b32_e32 v46, 16, v48
	v_and_b32_e32 v47, 0xffff0000, v48
	v_lshlrev_b32_e32 v48, 16, v49
	v_and_b32_e32 v49, 0xffff0000, v49
	v_pk_mul_f32 v[44:45], v[44:45], v[48:49]
	v_pk_mul_f32 v[42:43], v[42:43], v[46:47]
	s_nop 0
	v_cvt_pk_bf16_f32 v42, v42, v43
	v_cvt_pk_bf16_f32 v43, v44, v45
	v_mov_b32_e32 v44, v212
	v_mov_b32_e32 v45, v213
	s_nop 0
	global_store_dwordx2 v[50:51], v[42:43], off offset:32
	s_nop 0
	v_lshlrev_b32_e32 v42, 16, v44
	v_and_b32_e32 v43, 0xffff0000, v44
	v_lshlrev_b32_e32 v44, 16, v45
	v_and_b32_e32 v45, 0xffff0000, v45
	v_pk_mul_f32 v[40:41], v[40:41], v[44:45]
	v_pk_mul_f32 v[38:39], v[38:39], v[42:43]
	v_add_u32_e32 v42, 0xa0, v144
	v_cvt_pk_bf16_f32 v38, v38, v39
	v_cvt_pk_bf16_f32 v39, v40, v41
	v_mov_b32_e32 v40, v214
	v_mov_b32_e32 v41, v215
	v_mad_i64_i32 v[44:45], s[24:25], v42, s49, v[146:147]
	global_store_dwordx2 v[50:51], v[38:39], off offset:256
	v_lshl_add_u64 v[44:45], v[44:45], 0, v[142:143]
	v_ashrrev_i32_e32 v43, 31, v42
	s_nop 0
	v_lshlrev_b32_e32 v38, 16, v40
	v_and_b32_e32 v39, 0xffff0000, v40
	v_lshlrev_b32_e32 v40, 16, v41
	v_and_b32_e32 v41, 0xffff0000, v41
	v_pk_mul_f32 v[32:33], v[32:33], v[40:41]
	v_pk_mul_f32 v[30:31], v[30:31], v[38:39]
	s_nop 0
	v_cvt_pk_bf16_f32 v30, v30, v31
	v_cvt_pk_bf16_f32 v31, v32, v33
	v_mov_b32_e32 v32, v216
	v_mov_b32_e32 v33, v217
	s_nop 0
	global_store_dwordx2 v[50:51], v[30:31], off offset:288
	s_nop 0
	v_lshlrev_b32_e32 v30, 16, v32
	v_and_b32_e32 v31, 0xffff0000, v32
	v_lshlrev_b32_e32 v32, 16, v33
	v_and_b32_e32 v33, 0xffff0000, v33
	v_pk_mul_f32 v[32:33], v[36:37], v[32:33]
	v_pk_mul_f32 v[30:31], v[34:35], v[30:31]
	v_lshlrev_b64 v[34:35], 12, v[42:43]
	v_cvt_pk_bf16_f32 v30, v30, v31
	v_cvt_pk_bf16_f32 v31, v32, v33
	v_mov_b32_e32 v32, v218
	v_mov_b32_e32 v33, v219
	v_lshl_add_u64 v[34:35], s[12:13], 0, v[34:35]
	v_lshl_add_u64 v[34:35], v[34:35], 0, v[142:143]
	global_store_dwordx2 v[34:35], v[30:31], off
	s_nop 0
	v_lshlrev_b32_e32 v30, 16, v32
	v_and_b32_e32 v31, 0xffff0000, v32
	v_lshlrev_b32_e32 v32, 16, v33
	v_and_b32_e32 v33, 0xffff0000, v33
	v_pk_mul_f32 v[28:29], v[28:29], v[32:33]
	v_pk_mul_f32 v[26:27], v[26:27], v[30:31]
	s_nop 0
	v_cvt_pk_bf16_f32 v26, v26, v27
	v_cvt_pk_bf16_f32 v27, v28, v29
	v_mov_b32_e32 v28, v220
	v_mov_b32_e32 v29, v221
	s_nop 0
	global_store_dwordx2 v[34:35], v[26:27], off offset:32
	s_nop 0
	v_lshlrev_b32_e32 v26, 16, v28
	v_and_b32_e32 v27, 0xffff0000, v28
	v_lshlrev_b32_e32 v28, 16, v29
	v_and_b32_e32 v29, 0xffff0000, v29
	v_pk_mul_f32 v[24:25], v[24:25], v[28:29]
	v_pk_mul_f32 v[22:23], v[22:23], v[26:27]
	v_add_u32_e32 v26, 0xb0, v144
	v_cvt_pk_bf16_f32 v22, v22, v23
	v_cvt_pk_bf16_f32 v23, v24, v25
	v_mov_b32_e32 v24, v228
	v_mov_b32_e32 v25, v229
	v_mad_i64_i32 v[28:29], s[24:25], v26, s49, v[146:147]
	global_store_dwordx2 v[34:35], v[22:23], off offset:256
	v_lshl_add_u64 v[28:29], v[28:29], 0, v[142:143]
	v_ashrrev_i32_e32 v27, 31, v26
	s_mov_b64 s[24:25], s[18:19]
	s_nop 0
	v_lshlrev_b32_e32 v22, 16, v24
	v_and_b32_e32 v23, 0xffff0000, v24
	v_lshlrev_b32_e32 v24, 16, v25
	v_and_b32_e32 v25, 0xffff0000, v25
	v_pk_mul_f32 v[16:17], v[16:17], v[24:25]
	v_pk_mul_f32 v[14:15], v[14:15], v[22:23]
	s_nop 0
	v_cvt_pk_bf16_f32 v14, v14, v15
	v_cvt_pk_bf16_f32 v15, v16, v17
	v_mov_b32_e32 v16, v230
	v_mov_b32_e32 v17, v231
	s_nop 0
	global_store_dwordx2 v[34:35], v[14:15], off offset:288
	s_nop 0
	v_lshlrev_b32_e32 v14, 16, v16
	v_and_b32_e32 v15, 0xffff0000, v16
	v_lshlrev_b32_e32 v16, 16, v17
	v_and_b32_e32 v17, 0xffff0000, v17
	v_pk_mul_f32 v[16:17], v[20:21], v[16:17]
	v_pk_mul_f32 v[14:15], v[18:19], v[14:15]
	v_lshlrev_b64 v[18:19], 12, v[26:27]
	v_cvt_pk_bf16_f32 v14, v14, v15
	v_cvt_pk_bf16_f32 v15, v16, v17
	v_mov_b32_e32 v16, v232
	v_mov_b32_e32 v17, v233
	v_lshl_add_u64 v[18:19], s[12:13], 0, v[18:19]
	v_lshl_add_u64 v[18:19], v[18:19], 0, v[142:143]
	global_store_dwordx2 v[18:19], v[14:15], off
	s_nop 0
	v_lshlrev_b32_e32 v14, 16, v16
	v_and_b32_e32 v15, 0xffff0000, v16
	v_lshlrev_b32_e32 v16, 16, v17
	v_and_b32_e32 v17, 0xffff0000, v17
	v_pk_mul_f32 v[12:13], v[12:13], v[16:17]
	v_pk_mul_f32 v[10:11], v[10:11], v[14:15]
	s_nop 0
	v_cvt_pk_bf16_f32 v10, v10, v11
	v_cvt_pk_bf16_f32 v11, v12, v13
	v_mov_b32_e32 v12, v234
	v_mov_b32_e32 v13, v235
	s_nop 0
	global_store_dwordx2 v[18:19], v[10:11], off offset:32
	s_nop 0
	v_lshlrev_b32_e32 v10, 16, v12
	v_and_b32_e32 v11, 0xffff0000, v12
	v_lshlrev_b32_e32 v12, 16, v13
	v_and_b32_e32 v13, 0xffff0000, v13
	v_pk_mul_f32 v[8:9], v[8:9], v[12:13]
	v_pk_mul_f32 v[6:7], v[6:7], v[10:11]
	s_nop 0
	v_cvt_pk_bf16_f32 v6, v6, v7
	v_cvt_pk_bf16_f32 v7, v8, v9
	v_mov_b32_e32 v8, v236
	v_mov_b32_e32 v9, v237
	s_nop 0
	global_store_dwordx2 v[18:19], v[6:7], off offset:256
	s_nop 0
	v_lshlrev_b32_e32 v6, 16, v8
	v_and_b32_e32 v7, 0xffff0000, v8
	v_lshlrev_b32_e32 v8, 16, v9
	v_and_b32_e32 v9, 0xffff0000, v9
	v_pk_mul_f32 v[2:3], v[2:3], v[6:7]
	v_pk_mul_f32 v[4:5], v[4:5], v[8:9]
	v_cvt_pk_bf16_f32 v2, v2, v3
	s_nop 0
	v_cvt_pk_bf16_f32 v3, v4, v5
	global_store_dwordx2 v[18:19], v[2:3], off offset:288
	s_cbranch_vccz .LBB0_3228
	s_waitcnt vmcnt(0)
	s_cmpk_gt_u32 s33, 0xff
	s_cbranch_scc1 .LBB0_3235
	s_barrier

.LBB0_3236:
	v_cndmask_b32_e64 v2, 0, 1, s[2:3]
	v_cmp_ne_u32_e64 s[0:1], 1, v2
	s_andn2_b64 vcc, exec, s[2:3]
	v_readfirstlane_b32 s33, v0
	s_cbranch_vccnz .LBB0_3248
	s_add_u32 s34, s6, 0x4e400000
	s_addc_u32 s35, s7, 0
	s_add_u32 s36, s6, 0x15940000
	s_addc_u32 s37, s7, 0
	s_ashr_i32 s39, s30, 31
	s_lshr_b32 s2, s39, 29
	s_add_i32 s2, s30, s2
	s_lshr_b32 s8, s33, 6
	s_ashr_i32 s9, s2, 3
	s_and_b32 s2, s2, -8
	s_lshr_b32 s3, s33, 8
	s_lshl_b32 s38, s8, 10
	s_sub_i32 s2, s30, s2
	s_cmp_lt_i32 s2, 0
	s_cselect_b32 s10, 0x41, 64
	s_mul_i32 s2, s10, s2
	s_add_i32 s2, s2, s9
	s_ashr_i32 s9, s2, 31
	s_lshr_b32 s9, s9, 26
	s_add_i32 s9, s2, s9
	s_ashr_i32 s10, s9, 6
	s_lshl_b32 s12, s10, 3
	s_sub_i32 s10, 64, s12
	s_min_u32 s13, s10, 8
	s_andn2_b32 s9, s9, 63
	s_sub_i32 s9, s2, s9
	v_cvt_f32_ubyte0_e32 v3, s13
	v_cvt_f32_i32_e32 v2, s9
	v_rcp_iflag_f32_e32 v4, v3
	s_ashr_i32 s2, s9, 30
	s_or_b32 s2, s2, 1
	v_mov_b32_e32 v131, 0
	v_mul_f32_e32 v4, v2, v4
	v_trunc_f32_e32 v4, v4
	v_fma_f32 v2, -v4, v3, v2
	v_cvt_i32_f32_e32 v4, v4
	v_cmp_ge_f32_e64 s[10:11], |v2|, v3
	s_and_b64 s[10:11], s[10:11], exec
	s_cselect_b32 s2, s2, 0
	v_readfirstlane_b32 s10, v4
	s_add_i32 s2, s10, s2
	s_mul_i32 s10, s2, s13
	s_sub_i32 s9, s9, s10
	s_sext_i32_i8 s9, s9
	s_add_i32 s22, s12, s9
	s_ashr_i32 s23, s22, 31
	s_lshl_b64 s[10:11], s[22:23], 19
	s_add_u32 s24, s34, s10
	s_addc_u32 s25, s35, s11
	s_bfe_i64 s[10:11], s[2:3], 0x80000
	s_lshl_b64 s[10:11], s[10:11], 19
	s_add_u32 s26, s36, s10
	s_addc_u32 s27, s37, s11
	s_add_i32 s23, s38, 0
	s_add_i32 m0, s23, 0x10000
	s_add_i32 s40, s23, 0x2000
	global_load_lds_dwordx4 v130, s[26:27]
	s_add_i32 m0, s23, 0x12000
	s_add_u32 s10, s26, 0x40000
	global_load_lds_dwordx4 v132, s[26:27]
	s_mov_b32 m0, s23
	s_addc_u32 s11, s27, 0
	global_load_lds_dwordx4 v130, s[24:25]
	s_mov_b32 m0, s40
	v_mov_b32_e32 v133, v131
	global_load_lds_dwordx4 v132, s[24:25]
	s_add_i32 m0, s23, 0x14000
	s_mov_b32 s43, 0
	global_load_lds_dwordx4 v130, s[10:11]
	s_add_i32 m0, s23, 0x16000
	s_waitcnt vmcnt(0)
	v_lshl_add_u64 v[8:9], s[26:27], 0, v[130:131]
	global_load_lds_dwordx4 v132, s[10:11]
	s_add_u32 s10, s24, 0x40000
	s_addc_u32 s11, s25, 0
	s_add_i32 s41, s23, 0x4000
	s_mov_b32 m0, s41
	s_add_i32 s42, s23, 0x6000
	global_load_lds_dwordx4 v130, s[10:11]
	s_mov_b32 m0, s42
	v_lshl_add_u64 v[6:7], s[26:27], 0, v[132:133]
	global_load_lds_dwordx4 v132, s[10:11]
	v_lshl_add_u64 v[4:5], s[24:25], 0, v[130:131]
	s_setprio 1
	s_cmp_lg_u32 s3, 1
	v_lshl_add_u64 v[2:3], s[24:25], 0, v[132:133]
	s_cbranch_scc1 .LBB0_3239
	s_barrier
	s_setprio 0

.LBB0_3243:
	ds_read_b128 v[142:145], v158
	ds_read_b128 v[162:165], v158 offset:1024
	ds_read_b128 v[166:169], v158 offset:2048
	ds_read_b128 v[170:173], v158 offset:3072
	s_add_u32 s26, s24, 0xfffc0080
	s_addc_u32 s27, s25, -1
	s_cmp_eq_u32 s56, 12
	s_cselect_b32 s29, s17, s27
	s_cselect_b32 s28, s52, s26
	s_cselect_b32 s27, s15, s55
	s_cselect_b32 s26, s53, s54
	v_lshl_add_u64 v[146:147], s[24:25], 0, v[134:135]
	s_add_i32 m0, s23, 0xc000
	ds_read_b128 v[174:177], v159
	ds_read_b128 v[178:181], v159 offset:1024
	ds_read_b128 v[182:185], v159 offset:2048
	ds_read_b128 v[186:189], v159 offset:3072
	ds_read_b128 v[190:193], v159 offset:4096
	ds_read_b128 v[194:197], v159 offset:5120
	ds_read_b128 v[198:201], v159 offset:6144
	ds_read_b128 v[202:205], v159 offset:7168
	global_load_lds_dwordx4 v[146:147], off
	v_lshl_add_u64 v[146:147], s[24:25], 0, v[136:137]
	s_add_i32 m0, s23, 0xe000
	s_nop 0
	global_load_lds_dwordx4 v[146:147], off
	s_waitcnt lgkmcnt(8)
	s_barrier
	s_waitcnt lgkmcnt(0)
	s_waitcnt lgkmcnt(0)
	v_mfma_f32_16x16x32_bf16 v[126:129], v[142:145], v[174:177], v[126:129]
	v_mfma_f32_16x16x32_bf16 v[122:125], v[166:169], v[174:177], v[122:125]
	v_mfma_f32_16x16x32_bf16 v[110:113], v[142:145], v[182:185], v[110:113]
	v_mfma_f32_16x16x32_bf16 v[106:109], v[166:169], v[182:185], v[106:109]
	v_mfma_f32_16x16x32_bf16 v[94:97], v[142:145], v[190:193], v[94:97]
	v_mfma_f32_16x16x32_bf16 v[90:93], v[166:169], v[190:193], v[90:93]
	v_mfma_f32_16x16x32_bf16 v[78:81], v[142:145], v[198:201], v[78:81]
	v_mfma_f32_16x16x32_bf16 v[74:77], v[166:169], v[198:201], v[74:77]
	v_mfma_f32_16x16x32_bf16 v[126:129], v[162:165], v[178:181], v[126:129]
	v_mfma_f32_16x16x32_bf16 v[122:125], v[170:173], v[178:181], v[122:125]
	v_mfma_f32_16x16x32_bf16 v[110:113], v[162:165], v[186:189], v[110:113]
	v_mfma_f32_16x16x32_bf16 v[106:109], v[170:173], v[186:189], v[106:109]
	v_mfma_f32_16x16x32_bf16 v[94:97], v[162:165], v[194:197], v[94:97]
	v_mfma_f32_16x16x32_bf16 v[90:93], v[170:173], v[194:197], v[90:93]
	v_mfma_f32_16x16x32_bf16 v[78:81], v[162:165], v[202:205], v[78:81]
	v_mfma_f32_16x16x32_bf16 v[74:77], v[170:173], v[202:205], v[74:77]
	s_barrier
	s_add_i32 s57, s47, s38
	v_lshl_add_u64 v[146:147], s[26:27], 0, v[130:131]
	s_mov_b32 m0, s57
	ds_read_b128 v[206:209], v160
	ds_read_b128 v[210:213], v160 offset:1024
	ds_read_b128 v[214:217], v160 offset:2048
	ds_read_b128 v[218:221], v160 offset:3072
	global_load_lds_dwordx4 v[146:147], off
	v_lshl_add_u64 v[222:223], s[26:27], 0, v[132:133]
	s_add_i32 m0, s57, 0x2000
	s_nop 0
	global_load_lds_dwordx4 v[222:223], off
	s_barrier
	s_waitcnt lgkmcnt(0)
	s_waitcnt lgkmcnt(0)
	v_mfma_f32_16x16x32_bf16 v[118:121], v[206:209], v[174:177], v[118:121]
	v_mfma_f32_16x16x32_bf16 v[114:117], v[214:217], v[174:177], v[114:117]
	v_mfma_f32_16x16x32_bf16 v[102:105], v[206:209], v[182:185], v[102:105]
	v_mfma_f32_16x16x32_bf16 v[98:101], v[214:217], v[182:185], v[98:101]
	v_mfma_f32_16x16x32_bf16 v[86:89], v[206:209], v[190:193], v[86:89]
	v_mfma_f32_16x16x32_bf16 v[82:85], v[214:217], v[190:193], v[82:85]
	v_mfma_f32_16x16x32_bf16 v[70:73], v[206:209], v[198:201], v[70:73]
	v_mfma_f32_16x16x32_bf16 v[66:69], v[214:217], v[198:201], v[66:69]
	v_mfma_f32_16x16x32_bf16 v[118:121], v[210:213], v[178:181], v[118:121]
	v_mfma_f32_16x16x32_bf16 v[114:117], v[218:221], v[178:181], v[114:117]
	v_mfma_f32_16x16x32_bf16 v[102:105], v[210:213], v[186:189], v[102:105]
	v_mfma_f32_16x16x32_bf16 v[98:101], v[218:221], v[186:189], v[98:101]
	v_mfma_f32_16x16x32_bf16 v[86:89], v[210:213], v[194:197], v[86:89]
	v_mfma_f32_16x16x32_bf16 v[82:85], v[218:221], v[194:197], v[82:85]
	v_mfma_f32_16x16x32_bf16 v[70:73], v[210:213], v[202:205], v[70:73]
	v_mfma_f32_16x16x32_bf16 v[66:69], v[218:221], v[202:205], v[66:69]
	s_mov_b32 m0, s23
	v_lshl_add_u64 v[224:225], s[28:29], 0, v[130:131]
	s_barrier
	ds_read_b128 v[174:177], v159 offset:16384
	ds_read_b128 v[178:181], v159 offset:17408
	ds_read_b128 v[182:185], v159 offset:18432
	ds_read_b128 v[186:189], v159 offset:19456
	ds_read_b128 v[190:193], v159 offset:20480
	ds_read_b128 v[194:197], v159 offset:21504
	ds_read_b128 v[198:201], v159 offset:22528
	ds_read_b128 v[202:205], v159 offset:23552
	global_load_lds_dwordx4 v[224:225], off
	v_lshl_add_u64 v[226:227], s[28:29], 0, v[132:133]
	s_mov_b32 m0, s40
	s_nop 0
	global_load_lds_dwordx4 v[226:227], off
	s_barrier
	s_waitcnt lgkmcnt(0)
	s_waitcnt lgkmcnt(0)
	v_mfma_f32_16x16x32_bf16 v[62:65], v[142:145], v[174:177], v[62:65]
	v_mfma_f32_16x16x32_bf16 v[58:61], v[166:169], v[174:177], v[58:61]
	v_mfma_f32_16x16x32_bf16 v[46:49], v[142:145], v[182:185], v[46:49]
	v_mfma_f32_16x16x32_bf16 v[42:45], v[166:169], v[182:185], v[42:45]
	v_mfma_f32_16x16x32_bf16 v[30:33], v[142:145], v[190:193], v[30:33]
	v_mfma_f32_16x16x32_bf16 v[26:29], v[166:169], v[190:193], v[26:29]
	v_mfma_f32_16x16x32_bf16 v[14:17], v[142:145], v[198:201], v[14:17]
	v_mfma_f32_16x16x32_bf16 v[10:13], v[166:169], v[198:201], v[10:13]
	v_mfma_f32_16x16x32_bf16 v[62:65], v[162:165], v[178:181], v[62:65]
	v_mfma_f32_16x16x32_bf16 v[58:61], v[170:173], v[178:181], v[58:61]
	v_mfma_f32_16x16x32_bf16 v[46:49], v[162:165], v[186:189], v[46:49]
	v_mfma_f32_16x16x32_bf16 v[42:45], v[170:173], v[186:189], v[42:45]
	v_mfma_f32_16x16x32_bf16 v[30:33], v[162:165], v[194:197], v[30:33]
	v_mfma_f32_16x16x32_bf16 v[26:29], v[170:173], v[194:197], v[26:29]
	v_mfma_f32_16x16x32_bf16 v[14:17], v[162:165], v[202:205], v[14:17]
	v_mfma_f32_16x16x32_bf16 v[10:13], v[170:173], v[202:205], v[10:13]
	s_barrier
	s_add_u32 s58, s26, 0x40000
	s_addc_u32 s59, s27, 0
	s_add_i32 s57, s48, s38
	v_lshl_add_u64 v[142:143], s[58:59], 0, v[130:131]
	s_mov_b32 m0, s57
	s_nop 0
	global_load_lds_dwordx4 v[142:143], off
	v_lshl_add_u64 v[142:143], s[58:59], 0, v[132:133]
	s_add_i32 m0, s57, 0x2000
	s_nop 0
	global_load_lds_dwordx4 v[142:143], off
	s_waitcnt vmcnt(6)
	s_barrier
	v_mfma_f32_16x16x32_bf16 v[54:57], v[206:209], v[174:177], v[54:57]
	v_mfma_f32_16x16x32_bf16 v[50:53], v[214:217], v[174:177], v[50:53]
	v_mfma_f32_16x16x32_bf16 v[38:41], v[206:209], v[182:185], v[38:41]
	v_mfma_f32_16x16x32_bf16 v[34:37], v[214:217], v[182:185], v[34:37]
	v_mfma_f32_16x16x32_bf16 v[22:25], v[206:209], v[190:193], v[22:25]
	v_mfma_f32_16x16x32_bf16 v[18:21], v[214:217], v[190:193], v[18:21]
	v_mfma_f32_16x16x32_bf16 v[6:9], v[206:209], v[198:201], v[6:9]
	v_mfma_f32_16x16x32_bf16 v[2:5], v[214:217], v[198:201], v[2:5]
	v_mfma_f32_16x16x32_bf16 v[54:57], v[210:213], v[178:181], v[54:57]
	v_mfma_f32_16x16x32_bf16 v[50:53], v[218:221], v[178:181], v[50:53]
	v_mfma_f32_16x16x32_bf16 v[38:41], v[210:213], v[186:189], v[38:41]
	v_mfma_f32_16x16x32_bf16 v[34:37], v[218:221], v[186:189], v[34:37]
	v_mfma_f32_16x16x32_bf16 v[22:25], v[210:213], v[194:197], v[22:25]
	v_mfma_f32_16x16x32_bf16 v[18:21], v[218:221], v[194:197], v[18:21]
	v_mfma_f32_16x16x32_bf16 v[6:9], v[210:213], v[202:205], v[6:9]
	v_mfma_f32_16x16x32_bf16 v[2:5], v[218:221], v[202:205], v[2:5]
	s_add_i32 s57, 0, 0x18000
	v_add_u32_e32 v161, s57, v156
	s_barrier
	ds_read_b128 v[142:145], v161
	ds_read_b128 v[162:165], v161 offset:1024
	ds_read_b128 v[166:169], v161 offset:2048
	ds_read_b128 v[170:173], v161 offset:3072
	s_add_u32 s28, s28, 0x40000
	s_addc_u32 s29, s29, 0
	s_mov_b32 m0, s41
	v_lshl_add_u64 v[206:207], s[28:29], 0, v[130:131]
	ds_read_b128 v[174:177], v159 offset:32768
	ds_read_b128 v[178:181], v159 offset:33792
	ds_read_b128 v[182:185], v159 offset:34816
	ds_read_b128 v[186:189], v159 offset:35840
	ds_read_b128 v[190:193], v159 offset:36864
	ds_read_b128 v[194:197], v159 offset:37888
	ds_read_b128 v[198:201], v159 offset:38912
	ds_read_b128 v[202:205], v159 offset:39936
	global_load_lds_dwordx4 v[206:207], off
	v_lshl_add_u64 v[206:207], s[28:29], 0, v[132:133]
	s_mov_b32 m0, s42
	s_nop 0
	global_load_lds_dwordx4 v[206:207], off
	s_waitcnt lgkmcnt(8)
	s_barrier
	s_waitcnt lgkmcnt(0)
	s_waitcnt lgkmcnt(0)
	v_mfma_f32_16x16x32_bf16 v[126:129], v[142:145], v[174:177], v[126:129]
	v_mfma_f32_16x16x32_bf16 v[122:125], v[166:169], v[174:177], v[122:125]
	v_mfma_f32_16x16x32_bf16 v[110:113], v[142:145], v[182:185], v[110:113]
	v_mfma_f32_16x16x32_bf16 v[106:109], v[166:169], v[182:185], v[106:109]
	v_mfma_f32_16x16x32_bf16 v[94:97], v[142:145], v[190:193], v[94:97]
	v_mfma_f32_16x16x32_bf16 v[90:93], v[166:169], v[190:193], v[90:93]
	v_mfma_f32_16x16x32_bf16 v[78:81], v[142:145], v[198:201], v[78:81]
	v_mfma_f32_16x16x32_bf16 v[74:77], v[166:169], v[198:201], v[74:77]
	v_mfma_f32_16x16x32_bf16 v[126:129], v[162:165], v[178:181], v[126:129]
	v_mfma_f32_16x16x32_bf16 v[122:125], v[170:173], v[178:181], v[122:125]
	v_mfma_f32_16x16x32_bf16 v[110:113], v[162:165], v[186:189], v[110:113]
	v_mfma_f32_16x16x32_bf16 v[106:109], v[170:173], v[186:189], v[106:109]
	v_mfma_f32_16x16x32_bf16 v[94:97], v[162:165], v[194:197], v[94:97]
	v_mfma_f32_16x16x32_bf16 v[90:93], v[170:173], v[194:197], v[90:93]
	v_mfma_f32_16x16x32_bf16 v[78:81], v[162:165], v[202:205], v[78:81]
	v_mfma_f32_16x16x32_bf16 v[74:77], v[170:173], v[202:205], v[74:77]
	s_barrier
	s_add_i32 s28, 0, 0x1c000
	s_add_i32 s29, s57, s38
	v_add_u32_e32 v161, s28, v156
	v_lshl_add_u64 v[146:147], v[146:147], 0, s[8:9]
	s_mov_b32 m0, s29
	ds_read_b128 v[206:209], v161
	ds_read_b128 v[210:213], v161 offset:1024
	ds_read_b128 v[214:217], v161 offset:2048
	ds_read_b128 v[218:221], v161 offset:3072
	global_load_lds_dwordx4 v[146:147], off
	v_lshl_add_u64 v[146:147], v[222:223], 0, s[8:9]
	s_add_i32 m0, s29, 0x2000
	s_nop 0
	global_load_lds_dwordx4 v[146:147], off
	s_barrier
	s_waitcnt lgkmcnt(0)
	s_waitcnt lgkmcnt(0)
	v_mfma_f32_16x16x32_bf16 v[118:121], v[206:209], v[174:177], v[118:121]
	v_mfma_f32_16x16x32_bf16 v[114:117], v[214:217], v[174:177], v[114:117]
	v_mfma_f32_16x16x32_bf16 v[102:105], v[206:209], v[182:185], v[102:105]
	v_mfma_f32_16x16x32_bf16 v[98:101], v[214:217], v[182:185], v[98:101]
	v_mfma_f32_16x16x32_bf16 v[86:89], v[206:209], v[190:193], v[86:89]
	v_mfma_f32_16x16x32_bf16 v[82:85], v[214:217], v[190:193], v[82:85]
	v_mfma_f32_16x16x32_bf16 v[70:73], v[206:209], v[198:201], v[70:73]
	v_mfma_f32_16x16x32_bf16 v[66:69], v[214:217], v[198:201], v[66:69]
	v_mfma_f32_16x16x32_bf16 v[118:121], v[210:213], v[178:181], v[118:121]
	v_mfma_f32_16x16x32_bf16 v[114:117], v[218:221], v[178:181], v[114:117]
	v_mfma_f32_16x16x32_bf16 v[102:105], v[210:213], v[186:189], v[102:105]
	v_mfma_f32_16x16x32_bf16 v[98:101], v[218:221], v[186:189], v[98:101]
	v_mfma_f32_16x16x32_bf16 v[86:89], v[210:213], v[194:197], v[86:89]
	v_mfma_f32_16x16x32_bf16 v[82:85], v[218:221], v[194:197], v[82:85]
	v_mfma_f32_16x16x32_bf16 v[70:73], v[210:213], v[202:205], v[70:73]
	v_mfma_f32_16x16x32_bf16 v[66:69], v[218:221], v[202:205], v[66:69]
	s_mov_b32 m0, s44
	v_lshl_add_u64 v[146:147], v[224:225], 0, s[8:9]
	s_barrier
	ds_read_b128 v[174:177], v159 offset:49152
	ds_read_b128 v[178:181], v159 offset:50176
	ds_read_b128 v[182:185], v159 offset:51200
	ds_read_b128 v[186:189], v159 offset:52224
	ds_read_b128 v[190:193], v159 offset:53248
	ds_read_b128 v[194:197], v159 offset:54272
	ds_read_b128 v[198:201], v159 offset:55296
	ds_read_b128 v[202:205], v159 offset:56320
	global_load_lds_dwordx4 v[146:147], off
	v_lshl_add_u64 v[146:147], v[226:227], 0, s[8:9]
	s_mov_b32 m0, s45
	s_nop 0
	global_load_lds_dwordx4 v[146:147], off
	s_barrier
	s_waitcnt lgkmcnt(0)
	s_waitcnt lgkmcnt(0)
	v_mfma_f32_16x16x32_bf16 v[62:65], v[142:145], v[174:177], v[62:65]
	v_mfma_f32_16x16x32_bf16 v[58:61], v[166:169], v[174:177], v[58:61]
	v_mfma_f32_16x16x32_bf16 v[46:49], v[142:145], v[182:185], v[46:49]
	v_mfma_f32_16x16x32_bf16 v[42:45], v[166:169], v[182:185], v[42:45]
	v_mfma_f32_16x16x32_bf16 v[30:33], v[142:145], v[190:193], v[30:33]
	v_mfma_f32_16x16x32_bf16 v[26:29], v[166:169], v[190:193], v[26:29]
	v_mfma_f32_16x16x32_bf16 v[14:17], v[142:145], v[198:201], v[14:17]
	v_mfma_f32_16x16x32_bf16 v[10:13], v[166:169], v[198:201], v[10:13]
	v_mfma_f32_16x16x32_bf16 v[62:65], v[162:165], v[178:181], v[62:65]
	v_mfma_f32_16x16x32_bf16 v[58:61], v[170:173], v[178:181], v[58:61]
	v_mfma_f32_16x16x32_bf16 v[46:49], v[162:165], v[186:189], v[46:49]
	v_mfma_f32_16x16x32_bf16 v[42:45], v[170:173], v[186:189], v[42:45]
	v_mfma_f32_16x16x32_bf16 v[30:33], v[162:165], v[194:197], v[30:33]
	v_mfma_f32_16x16x32_bf16 v[26:29], v[170:173], v[194:197], v[26:29]
	v_mfma_f32_16x16x32_bf16 v[14:17], v[162:165], v[202:205], v[14:17]
	v_mfma_f32_16x16x32_bf16 v[10:13], v[170:173], v[202:205], v[10:13]
	s_barrier
	s_add_u32 s26, s26, 0x40080
	s_addc_u32 s27, s27, 0
	s_add_i32 s28, s28, s38
	v_lshl_add_u64 v[142:143], s[26:27], 0, v[130:131]
	s_mov_b32 m0, s28
	s_nop 0
	global_load_lds_dwordx4 v[142:143], off
	v_lshl_add_u64 v[142:143], s[26:27], 0, v[132:133]
	s_add_i32 m0, s28, 0x2000
	s_nop 0
	global_load_lds_dwordx4 v[142:143], off
	s_waitcnt vmcnt(6)
	s_barrier
	v_mfma_f32_16x16x32_bf16 v[54:57], v[206:209], v[174:177], v[54:57]
	v_mfma_f32_16x16x32_bf16 v[50:53], v[214:217], v[174:177], v[50:53]
	v_mfma_f32_16x16x32_bf16 v[38:41], v[206:209], v[182:185], v[38:41]
	v_mfma_f32_16x16x32_bf16 v[34:37], v[214:217], v[182:185], v[34:37]
	v_mfma_f32_16x16x32_bf16 v[22:25], v[206:209], v[190:193], v[22:25]
	v_mfma_f32_16x16x32_bf16 v[18:21], v[214:217], v[190:193], v[18:21]
	v_mfma_f32_16x16x32_bf16 v[6:9], v[206:209], v[198:201], v[6:9]
	v_mfma_f32_16x16x32_bf16 v[2:5], v[214:217], v[198:201], v[2:5]
	v_mfma_f32_16x16x32_bf16 v[54:57], v[210:213], v[178:181], v[54:57]
	v_mfma_f32_16x16x32_bf16 v[50:53], v[218:221], v[178:181], v[50:53]
	v_mfma_f32_16x16x32_bf16 v[38:41], v[210:213], v[186:189], v[38:41]
	v_mfma_f32_16x16x32_bf16 v[34:37], v[218:221], v[186:189], v[34:37]
	v_mfma_f32_16x16x32_bf16 v[22:25], v[210:213], v[194:197], v[22:25]
	v_mfma_f32_16x16x32_bf16 v[18:21], v[218:221], v[194:197], v[18:21]
	v_mfma_f32_16x16x32_bf16 v[6:9], v[210:213], v[202:205], v[6:9]
	v_mfma_f32_16x16x32_bf16 v[2:5], v[218:221], v[202:205], v[2:5]
	s_add_i32 s56, s56, 2
	s_add_u32 s24, s24, 0x100
	s_addc_u32 s25, s25, 0
	s_add_u32 s54, s54, 0x100
	s_addc_u32 s55, s55, 0
	s_cmp_gt_u32 s56, 13
	s_barrier
	s_cbranch_scc0 .LBB0_3243
	v_lshl_or_b32 v142, s51, 8, v157
	v_lshl_add_u32 v144, s22, 8, v155
	v_ashrrev_i32_e32 v143, 31, v142
	v_mov_b64_e32 v[146:147], s[6:7]
	v_ashrrev_i32_e32 v145, 31, v144
	v_mad_i64_i32 v[162:163], s[24:25], v144, s49, v[146:147]
	v_lshlrev_b64 v[142:143], 1, v[142:143]
	v_lshl_add_u64 v[162:163], v[162:163], 0, v[142:143]
	v_lshlrev_b64 v[166:167], 12, v[144:145]
	v_add_co_u32_e32 v164, vcc, 0x2ec41000, v162
	v_lshl_add_u64 v[166:167], s[10:11], 0, v[166:167]
	s_nop 0
	v_addc_co_u32_e32 v165, vcc, 0, v163, vcc
	v_lshl_add_u64 v[166:167], v[166:167], 0, v[142:143]
	v_mov_b32_e32 v228, v164
	v_mov_b32_e32 v229, v165
	v_mov_b32_e32 v232, v166
	v_mov_b32_e32 v233, v167
	v_mov_b32_e32 v237, 0x1000
	global_load_dwordx2 v[174:175], v[228:229], off
	global_load_dwordx2 v[176:177], v[232:233], off
	global_load_dwordx2 v[178:179], v[228:229], off offset:32
	global_load_dwordx2 v[180:181], v[232:233], off offset:32
	global_load_dwordx2 v[182:183], v[228:229], off offset:256
	global_load_dwordx2 v[184:185], v[232:233], off offset:256
	global_load_dwordx2 v[186:187], v[228:229], off offset:288
	global_load_dwordx2 v[188:189], v[232:233], off offset:288
	v_mov_b32_e32 v236, 16
	v_mad_i64_i32 v[230:231], s[24:25], v236, s49, v[228:229]
	v_mad_i64_i32 v[234:235], s[24:25], v236, v237, v[232:233]
	global_load_dwordx2 v[190:191], v[230:231], off
	global_load_dwordx2 v[192:193], v[234:235], off
	global_load_dwordx2 v[194:195], v[230:231], off offset:32
	global_load_dwordx2 v[196:197], v[234:235], off offset:32
	global_load_dwordx2 v[198:199], v[230:231], off offset:256
	global_load_dwordx2 v[200:201], v[234:235], off offset:256
	global_load_dwordx2 v[202:203], v[230:231], off offset:288
	global_load_dwordx2 v[204:205], v[234:235], off offset:288
	v_mov_b32_e32 v236, 32
	v_mad_i64_i32 v[230:231], s[24:25], v236, s49, v[228:229]
	v_mad_i64_i32 v[234:235], s[24:25], v236, v237, v[232:233]
	global_load_dwordx2 v[206:207], v[230:231], off
	global_load_dwordx2 v[208:209], v[234:235], off
	global_load_dwordx2 v[210:211], v[230:231], off offset:32
	global_load_dwordx2 v[212:213], v[234:235], off offset:32
	global_load_dwordx2 v[214:215], v[230:231], off offset:256
	global_load_dwordx2 v[216:217], v[234:235], off offset:256
	global_load_dwordx2 v[218:219], v[230:231], off offset:288
	global_load_dwordx2 v[220:221], v[234:235], off offset:288
	s_waitcnt vmcnt(0)
	v_mov_b32_e32 v164, v174
	v_mov_b32_e32 v165, v175
	v_lshl_add_u64 v[162:163], v[162:163], 0, s[12:13]
	v_mov_b32_e32 v168, v176
	v_mov_b32_e32 v169, v177
	s_mov_b32 s51, s14
	s_mov_b32 s22, s16
	s_mov_b64 s[26:27], s[20:21]
	s_nop 0
	v_lshlrev_b32_e32 v170, 16, v164
	v_and_b32_e32 v171, 0xffff0000, v164
	v_lshlrev_b32_e32 v164, 16, v165
	v_and_b32_e32 v165, 0xffff0000, v165
	v_lshlrev_b32_e32 v172, 16, v168
	v_and_b32_e32 v173, 0xffff0000, v168
	v_lshlrev_b32_e32 v168, 16, v169
	v_and_b32_e32 v169, 0xffff0000, v169
	v_pk_fma_f32 v[128:129], v[128:129], v[164:165], v[168:169]
	v_pk_fma_f32 v[126:127], v[126:127], v[170:171], v[172:173]
	s_nop 0
	v_cvt_pk_bf16_f32 v126, v126, v127
	v_cvt_pk_bf16_f32 v127, v128, v129
	v_mov_b32_e32 v128, v178
	v_mov_b32_e32 v129, v179
	v_mov_b32_e32 v164, v180
	v_mov_b32_e32 v165, v181
	s_nop 0
	v_lshlrev_b32_e32 v168, 16, v164
	global_store_dwordx2 v[166:167], v[126:127], off
	v_lshlrev_b32_e32 v126, 16, v128
	v_and_b32_e32 v127, 0xffff0000, v128
	v_lshlrev_b32_e32 v128, 16, v129
	v_and_b32_e32 v129, 0xffff0000, v129
	v_and_b32_e32 v169, 0xffff0000, v164
	v_lshlrev_b32_e32 v164, 16, v165
	v_and_b32_e32 v165, 0xffff0000, v165
	v_pk_fma_f32 v[124:125], v[124:125], v[128:129], v[164:165]
	v_pk_fma_f32 v[122:123], v[122:123], v[126:127], v[168:169]
	s_nop 0
	v_cvt_pk_bf16_f32 v122, v122, v123
	v_cvt_pk_bf16_f32 v123, v124, v125
	v_mov_b32_e32 v124, v182
	v_mov_b32_e32 v125, v183
	v_mov_b32_e32 v126, v184
	v_mov_b32_e32 v127, v185
	s_nop 0
	v_lshlrev_b32_e32 v128, 16, v126
	global_store_dwordx2 v[166:167], v[122:123], off offset:32
	v_lshlrev_b32_e32 v122, 16, v124
	v_and_b32_e32 v123, 0xffff0000, v124
	v_lshlrev_b32_e32 v124, 16, v125
	v_and_b32_e32 v125, 0xffff0000, v125
	v_and_b32_e32 v129, 0xffff0000, v126
	v_lshlrev_b32_e32 v126, 16, v127
	v_and_b32_e32 v127, 0xffff0000, v127
	v_pk_fma_f32 v[120:121], v[120:121], v[124:125], v[126:127]
	v_pk_fma_f32 v[118:119], v[118:119], v[122:123], v[128:129]
	v_or_b32_e32 v124, 16, v144
	v_cvt_pk_bf16_f32 v118, v118, v119
	v_cvt_pk_bf16_f32 v119, v120, v121
	v_mov_b32_e32 v120, v186
	v_mov_b32_e32 v121, v187
	v_mov_b32_e32 v122, v188
	v_mov_b32_e32 v123, v189
	v_ashrrev_i32_e32 v125, 31, v124
	v_mad_i64_i32 v[126:127], s[24:25], v124, s49, v[146:147]
	global_store_dwordx2 v[166:167], v[118:119], off offset:256
	v_lshl_add_u64 v[126:127], v[126:127], 0, v[142:143]
	v_add_co_u32_e32 v128, vcc, s50, v126
	s_nop 0
	v_lshlrev_b32_e32 v118, 16, v120
	v_and_b32_e32 v119, 0xffff0000, v120
	v_lshlrev_b32_e32 v162, 16, v122
	v_and_b32_e32 v163, 0xffff0000, v122
	v_pk_fma_f32 v[114:115], v[114:115], v[118:119], v[162:163]
	v_lshlrev_b64 v[118:119], 12, v[124:125]
	v_lshlrev_b32_e32 v120, 16, v121
	v_and_b32_e32 v121, 0xffff0000, v121
	v_lshlrev_b32_e32 v122, 16, v123
	v_and_b32_e32 v123, 0xffff0000, v123
	v_lshl_add_u64 v[118:119], s[10:11], 0, v[118:119]
	v_addc_co_u32_e32 v129, vcc, 0, v127, vcc
	v_pk_fma_f32 v[116:117], v[116:117], v[120:121], v[122:123]
	v_lshl_add_u64 v[118:119], v[118:119], 0, v[142:143]
	v_cvt_pk_bf16_f32 v114, v114, v115
	v_cvt_pk_bf16_f32 v115, v116, v117
	v_mov_b32_e32 v116, v190
	v_mov_b32_e32 v117, v191
	v_mov_b32_e32 v120, v192
	v_mov_b32_e32 v121, v193
	v_lshl_add_u64 v[122:123], v[126:127], 0, s[12:13]
	global_store_dwordx2 v[166:167], v[114:115], off offset:288
	s_nop 0
	v_lshlrev_b32_e32 v114, 16, v116
	v_and_b32_e32 v115, 0xffff0000, v116
	v_lshlrev_b32_e32 v116, 16, v117
	v_and_b32_e32 v117, 0xffff0000, v117
	v_lshlrev_b32_e32 v124, 16, v120
	v_and_b32_e32 v125, 0xffff0000, v120
	v_lshlrev_b32_e32 v120, 16, v121
	v_and_b32_e32 v121, 0xffff0000, v121
	v_pk_fma_f32 v[112:113], v[112:113], v[116:117], v[120:121]
	v_pk_fma_f32 v[110:111], v[110:111], v[114:115], v[124:125]
	s_nop 0
	v_cvt_pk_bf16_f32 v110, v110, v111
	v_cvt_pk_bf16_f32 v111, v112, v113
	v_mov_b32_e32 v112, v194
	v_mov_b32_e32 v113, v195
	v_mov_b32_e32 v114, v196
	v_mov_b32_e32 v115, v197
	s_nop 0
	v_lshlrev_b32_e32 v116, 16, v114
	global_store_dwordx2 v[118:119], v[110:111], off
	v_lshlrev_b32_e32 v110, 16, v112
	v_and_b32_e32 v111, 0xffff0000, v112
	v_lshlrev_b32_e32 v112, 16, v113
	v_and_b32_e32 v113, 0xffff0000, v113
	v_and_b32_e32 v117, 0xffff0000, v114
	v_lshlrev_b32_e32 v114, 16, v115
	v_and_b32_e32 v115, 0xffff0000, v115
	v_pk_fma_f32 v[108:109], v[108:109], v[112:113], v[114:115]
	v_pk_fma_f32 v[106:107], v[106:107], v[110:111], v[116:117]
	s_nop 0
	v_cvt_pk_bf16_f32 v106, v106, v107
	v_cvt_pk_bf16_f32 v107, v108, v109
	v_mov_b32_e32 v108, v198
	v_mov_b32_e32 v109, v199
	v_mov_b32_e32 v110, v200
	v_mov_b32_e32 v111, v201
	s_nop 0
	v_lshlrev_b32_e32 v112, 16, v110
	global_store_dwordx2 v[118:119], v[106:107], off offset:32
	v_lshlrev_b32_e32 v106, 16, v108
	v_and_b32_e32 v107, 0xffff0000, v108
	v_lshlrev_b32_e32 v108, 16, v109
	v_and_b32_e32 v109, 0xffff0000, v109
	v_and_b32_e32 v113, 0xffff0000, v110
	v_lshlrev_b32_e32 v110, 16, v111
	v_and_b32_e32 v111, 0xffff0000, v111
	v_pk_fma_f32 v[104:105], v[104:105], v[108:109], v[110:111]
	v_pk_fma_f32 v[102:103], v[102:103], v[106:107], v[112:113]
	v_or_b32_e32 v108, 32, v144
	v_cvt_pk_bf16_f32 v102, v102, v103
	v_cvt_pk_bf16_f32 v103, v104, v105
	v_mov_b32_e32 v104, v202
	v_mov_b32_e32 v105, v203
	v_mov_b32_e32 v106, v204
	v_mov_b32_e32 v107, v205
	v_ashrrev_i32_e32 v109, 31, v108
	v_mad_i64_i32 v[110:111], s[24:25], v108, s49, v[146:147]
	global_store_dwordx2 v[118:119], v[102:103], off offset:256
	v_lshl_add_u64 v[110:111], v[110:111], 0, v[142:143]
	v_add_co_u32_e32 v112, vcc, s50, v110
	s_nop 0
	v_lshlrev_b32_e32 v102, 16, v104
	v_and_b32_e32 v103, 0xffff0000, v104
	v_lshlrev_b32_e32 v114, 16, v106
	v_and_b32_e32 v115, 0xffff0000, v106
	v_pk_fma_f32 v[98:99], v[98:99], v[102:103], v[114:115]
	v_lshlrev_b64 v[102:103], 12, v[108:109]
	v_lshlrev_b32_e32 v104, 16, v105
	v_and_b32_e32 v105, 0xffff0000, v105
	v_lshlrev_b32_e32 v106, 16, v107
	v_and_b32_e32 v107, 0xffff0000, v107
	v_lshl_add_u64 v[102:103], s[10:11], 0, v[102:103]
	v_addc_co_u32_e32 v113, vcc, 0, v111, vcc
	v_pk_fma_f32 v[100:101], v[100:101], v[104:105], v[106:107]
	v_lshl_add_u64 v[102:103], v[102:103], 0, v[142:143]
	v_cvt_pk_bf16_f32 v98, v98, v99
	v_cvt_pk_bf16_f32 v99, v100, v101
	v_mov_b32_e32 v100, v206
	v_mov_b32_e32 v101, v207
	v_mov_b32_e32 v104, v208
	v_mov_b32_e32 v105, v209
	v_lshl_add_u64 v[106:107], v[110:111], 0, s[12:13]
	global_store_dwordx2 v[118:119], v[98:99], off offset:288
	s_nop 0
	v_lshlrev_b32_e32 v98, 16, v100
	v_and_b32_e32 v99, 0xffff0000, v100
	v_lshlrev_b32_e32 v100, 16, v101
	v_and_b32_e32 v101, 0xffff0000, v101
	v_lshlrev_b32_e32 v108, 16, v104
	v_and_b32_e32 v109, 0xffff0000, v104
	v_lshlrev_b32_e32 v104, 16, v105
	v_and_b32_e32 v105, 0xffff0000, v105
	v_pk_fma_f32 v[96:97], v[96:97], v[100:101], v[104:105]
	v_pk_fma_f32 v[94:95], v[94:95], v[98:99], v[108:109]
	s_nop 0
	v_cvt_pk_bf16_f32 v94, v94, v95
	v_cvt_pk_bf16_f32 v95, v96, v97
	v_mov_b32_e32 v96, v210
	v_mov_b32_e32 v97, v211
	v_mov_b32_e32 v98, v212
	v_mov_b32_e32 v99, v213
	s_nop 0
	v_lshlrev_b32_e32 v100, 16, v98
	global_store_dwordx2 v[102:103], v[94:95], off
	v_lshlrev_b32_e32 v94, 16, v96
	v_and_b32_e32 v95, 0xffff0000, v96
	v_lshlrev_b32_e32 v96, 16, v97
	v_and_b32_e32 v97, 0xffff0000, v97
	v_and_b32_e32 v101, 0xffff0000, v98
	v_lshlrev_b32_e32 v98, 16, v99
	v_and_b32_e32 v99, 0xffff0000, v99
	v_pk_fma_f32 v[92:93], v[92:93], v[96:97], v[98:99]
	v_pk_fma_f32 v[90:91], v[90:91], v[94:95], v[100:101]
	s_nop 0
	v_cvt_pk_bf16_f32 v90, v90, v91
	v_cvt_pk_bf16_f32 v91, v92, v93
	v_mov_b32_e32 v92, v214
	v_mov_b32_e32 v93, v215
	v_mov_b32_e32 v94, v216
	v_mov_b32_e32 v95, v217
	s_nop 0
	v_lshlrev_b32_e32 v96, 16, v94
	global_store_dwordx2 v[102:103], v[90:91], off offset:32
	v_lshlrev_b32_e32 v90, 16, v92
	v_and_b32_e32 v91, 0xffff0000, v92
	v_lshlrev_b32_e32 v92, 16, v93
	v_and_b32_e32 v93, 0xffff0000, v93
	v_and_b32_e32 v97, 0xffff0000, v94
	v_lshlrev_b32_e32 v94, 16, v95
	v_and_b32_e32 v95, 0xffff0000, v95
	v_pk_fma_f32 v[88:89], v[88:89], v[92:93], v[94:95]
	v_pk_fma_f32 v[86:87], v[86:87], v[90:91], v[96:97]
	v_or_b32_e32 v92, 48, v144
	v_cvt_pk_bf16_f32 v86, v86, v87
	v_cvt_pk_bf16_f32 v87, v88, v89
	v_mov_b32_e32 v88, v218
	v_mov_b32_e32 v89, v219
	v_mov_b32_e32 v90, v220
	v_mov_b32_e32 v91, v221
	v_ashrrev_i32_e32 v93, 31, v92
	v_mad_i64_i32 v[94:95], s[24:25], v92, s49, v[146:147]
	global_store_dwordx2 v[102:103], v[86:87], off offset:256
	v_lshl_add_u64 v[94:95], v[94:95], 0, v[142:143]
	v_add_co_u32_e32 v96, vcc, s50, v94
	s_nop 0
	v_lshlrev_b32_e32 v86, 16, v88
	v_and_b32_e32 v87, 0xffff0000, v88
	v_lshlrev_b32_e32 v98, 16, v90
	v_and_b32_e32 v99, 0xffff0000, v90
	v_pk_fma_f32 v[82:83], v[82:83], v[86:87], v[98:99]
	v_lshlrev_b64 v[86:87], 12, v[92:93]
	v_lshlrev_b32_e32 v88, 16, v89
	v_and_b32_e32 v89, 0xffff0000, v89
	v_lshlrev_b32_e32 v90, 16, v91
	v_and_b32_e32 v91, 0xffff0000, v91
	v_lshl_add_u64 v[86:87], s[10:11], 0, v[86:87]
	v_addc_co_u32_e32 v97, vcc, 0, v95, vcc
	v_pk_fma_f32 v[84:85], v[84:85], v[88:89], v[90:91]
	v_lshl_add_u64 v[86:87], v[86:87], 0, v[142:143]
	v_cvt_pk_bf16_f32 v82, v82, v83
	v_cvt_pk_bf16_f32 v83, v84, v85
	v_mov_b32_e32 v237, 0x1000
	v_mov_b32_e32 v236, 48
	v_mad_i64_i32 v[230:231], s[24:25], v236, s49, v[228:229]
	v_mad_i64_i32 v[234:235], s[24:25], v236, v237, v[232:233]
	global_load_dwordx2 v[174:175], v[230:231], off
	global_load_dwordx2 v[176:177], v[234:235], off
	global_load_dwordx2 v[178:179], v[230:231], off offset:32
	global_load_dwordx2 v[180:181], v[234:235], off offset:32
	global_load_dwordx2 v[182:183], v[230:231], off offset:256
	global_load_dwordx2 v[184:185], v[234:235], off offset:256
	global_load_dwordx2 v[186:187], v[230:231], off offset:288
	global_load_dwordx2 v[188:189], v[234:235], off offset:288
	v_mov_b32_e32 v236, 128
	v_mad_i64_i32 v[230:231], s[24:25], v236, s49, v[228:229]
	v_mad_i64_i32 v[234:235], s[24:25], v236, v237, v[232:233]
	global_load_dwordx2 v[190:191], v[230:231], off
	global_load_dwordx2 v[192:193], v[234:235], off
	global_load_dwordx2 v[194:195], v[230:231], off offset:32
	global_load_dwordx2 v[196:197], v[234:235], off offset:32
	global_load_dwordx2 v[198:199], v[230:231], off offset:256
	global_load_dwordx2 v[200:201], v[234:235], off offset:256
	global_load_dwordx2 v[202:203], v[230:231], off offset:288
	global_load_dwordx2 v[204:205], v[234:235], off offset:288
	v_mov_b32_e32 v236, 144
	v_mad_i64_i32 v[230:231], s[24:25], v236, s49, v[228:229]
	v_mad_i64_i32 v[234:235], s[24:25], v236, v237, v[232:233]
	global_load_dwordx2 v[206:207], v[230:231], off
	global_load_dwordx2 v[208:209], v[234:235], off
	global_load_dwordx2 v[210:211], v[230:231], off offset:32
	global_load_dwordx2 v[212:213], v[234:235], off offset:32
	global_load_dwordx2 v[214:215], v[230:231], off offset:256
	global_load_dwordx2 v[216:217], v[234:235], off offset:256
	global_load_dwordx2 v[218:219], v[230:231], off offset:288
	global_load_dwordx2 v[220:221], v[234:235], off offset:288
	s_waitcnt vmcnt(0)
	v_mov_b32_e32 v84, v174
	v_mov_b32_e32 v85, v175
	v_mov_b32_e32 v88, v176
	v_mov_b32_e32 v89, v177
	v_lshl_add_u64 v[90:91], v[94:95], 0, s[12:13]
	global_store_dwordx2 v[102:103], v[82:83], off offset:288
	s_nop 0
	v_lshlrev_b32_e32 v82, 16, v84
	v_and_b32_e32 v83, 0xffff0000, v84
	v_lshlrev_b32_e32 v84, 16, v85
	v_and_b32_e32 v85, 0xffff0000, v85
	v_lshlrev_b32_e32 v92, 16, v88
	v_and_b32_e32 v93, 0xffff0000, v88
	v_lshlrev_b32_e32 v88, 16, v89
	v_and_b32_e32 v89, 0xffff0000, v89
	v_pk_fma_f32 v[80:81], v[80:81], v[84:85], v[88:89]
	v_pk_fma_f32 v[78:79], v[78:79], v[82:83], v[92:93]
	s_nop 0
	v_cvt_pk_bf16_f32 v78, v78, v79
	v_cvt_pk_bf16_f32 v79, v80, v81
	v_mov_b32_e32 v80, v178
	v_mov_b32_e32 v81, v179
	v_mov_b32_e32 v82, v180
	v_mov_b32_e32 v83, v181
	s_nop 0
	v_lshlrev_b32_e32 v84, 16, v82
	global_store_dwordx2 v[86:87], v[78:79], off
	v_lshlrev_b32_e32 v78, 16, v80
	v_and_b32_e32 v79, 0xffff0000, v80
	v_lshlrev_b32_e32 v80, 16, v81
	v_and_b32_e32 v81, 0xffff0000, v81
	v_and_b32_e32 v85, 0xffff0000, v82
	v_lshlrev_b32_e32 v82, 16, v83
	v_and_b32_e32 v83, 0xffff0000, v83
	v_pk_fma_f32 v[76:77], v[76:77], v[80:81], v[82:83]
	v_pk_fma_f32 v[74:75], v[74:75], v[78:79], v[84:85]
	s_nop 0
	v_cvt_pk_bf16_f32 v74, v74, v75
	v_cvt_pk_bf16_f32 v75, v76, v77
	v_mov_b32_e32 v76, v182
	v_mov_b32_e32 v77, v183
	v_mov_b32_e32 v78, v184
	v_mov_b32_e32 v79, v185
	s_nop 0
	v_lshlrev_b32_e32 v80, 16, v78
	global_store_dwordx2 v[86:87], v[74:75], off offset:32
	v_lshlrev_b32_e32 v74, 16, v76
	v_and_b32_e32 v75, 0xffff0000, v76
	v_lshlrev_b32_e32 v76, 16, v77
	v_and_b32_e32 v77, 0xffff0000, v77
	v_and_b32_e32 v81, 0xffff0000, v78
	v_lshlrev_b32_e32 v78, 16, v79
	v_and_b32_e32 v79, 0xffff0000, v79
	v_pk_fma_f32 v[72:73], v[72:73], v[76:77], v[78:79]
	v_pk_fma_f32 v[70:71], v[70:71], v[74:75], v[80:81]
	v_add_u32_e32 v76, 0x80, v144
	v_cvt_pk_bf16_f32 v70, v70, v71
	v_cvt_pk_bf16_f32 v71, v72, v73
	v_mov_b32_e32 v72, v186
	v_mov_b32_e32 v73, v187
	v_mov_b32_e32 v74, v188
	v_mov_b32_e32 v75, v189
	v_ashrrev_i32_e32 v77, 31, v76
	v_mad_i64_i32 v[78:79], s[24:25], v76, s49, v[146:147]
	global_store_dwordx2 v[86:87], v[70:71], off offset:256
	v_lshl_add_u64 v[78:79], v[78:79], 0, v[142:143]
	v_add_co_u32_e32 v80, vcc, s50, v78
	s_nop 0
	v_lshlrev_b32_e32 v70, 16, v72
	v_and_b32_e32 v71, 0xffff0000, v72
	v_lshlrev_b32_e32 v82, 16, v74
	v_and_b32_e32 v83, 0xffff0000, v74
	v_pk_fma_f32 v[66:67], v[66:67], v[70:71], v[82:83]
	v_lshlrev_b64 v[70:71], 12, v[76:77]
	v_lshlrev_b32_e32 v72, 16, v73
	v_and_b32_e32 v73, 0xffff0000, v73
	v_lshlrev_b32_e32 v74, 16, v75
	v_and_b32_e32 v75, 0xffff0000, v75
	v_lshl_add_u64 v[70:71], s[10:11], 0, v[70:71]
	v_addc_co_u32_e32 v81, vcc, 0, v79, vcc
	v_pk_fma_f32 v[68:69], v[68:69], v[72:73], v[74:75]
	v_lshl_add_u64 v[70:71], v[70:71], 0, v[142:143]
	v_cvt_pk_bf16_f32 v66, v66, v67
	v_cvt_pk_bf16_f32 v67, v68, v69
	v_mov_b32_e32 v68, v190
	v_mov_b32_e32 v69, v191
	v_mov_b32_e32 v72, v192
	v_mov_b32_e32 v73, v193
	v_lshl_add_u64 v[74:75], v[78:79], 0, s[12:13]
	global_store_dwordx2 v[86:87], v[66:67], off offset:288
	s_nop 0
	v_lshlrev_b32_e32 v66, 16, v68
	v_and_b32_e32 v67, 0xffff0000, v68
	v_lshlrev_b32_e32 v68, 16, v69
	v_and_b32_e32 v69, 0xffff0000, v69
	v_lshlrev_b32_e32 v76, 16, v72
	v_and_b32_e32 v77, 0xffff0000, v72
	v_lshlrev_b32_e32 v72, 16, v73
	v_and_b32_e32 v73, 0xffff0000, v73
	v_pk_fma_f32 v[64:65], v[64:65], v[68:69], v[72:73]
	v_pk_fma_f32 v[62:63], v[62:63], v[66:67], v[76:77]
	s_nop 0
	v_cvt_pk_bf16_f32 v62, v62, v63
	v_cvt_pk_bf16_f32 v63, v64, v65
	v_mov_b32_e32 v64, v194
	v_mov_b32_e32 v65, v195
	v_mov_b32_e32 v66, v196
	v_mov_b32_e32 v67, v197
	s_nop 0
	v_lshlrev_b32_e32 v68, 16, v66
	global_store_dwordx2 v[70:71], v[62:63], off
	v_lshlrev_b32_e32 v62, 16, v64
	v_and_b32_e32 v63, 0xffff0000, v64
	v_lshlrev_b32_e32 v64, 16, v65
	v_and_b32_e32 v65, 0xffff0000, v65
	v_and_b32_e32 v69, 0xffff0000, v66
	v_lshlrev_b32_e32 v66, 16, v67
	v_and_b32_e32 v67, 0xffff0000, v67
	v_pk_fma_f32 v[60:61], v[60:61], v[64:65], v[66:67]
	v_pk_fma_f32 v[58:59], v[58:59], v[62:63], v[68:69]
	s_nop 0
	v_cvt_pk_bf16_f32 v58, v58, v59
	v_cvt_pk_bf16_f32 v59, v60, v61
	v_mov_b32_e32 v60, v198
	v_mov_b32_e32 v61, v199
	v_mov_b32_e32 v62, v200
	v_mov_b32_e32 v63, v201
	s_nop 0
	v_lshlrev_b32_e32 v64, 16, v62
	global_store_dwordx2 v[70:71], v[58:59], off offset:32
	v_lshlrev_b32_e32 v58, 16, v60
	v_and_b32_e32 v59, 0xffff0000, v60
	v_lshlrev_b32_e32 v60, 16, v61
	v_and_b32_e32 v61, 0xffff0000, v61
	v_and_b32_e32 v65, 0xffff0000, v62
	v_lshlrev_b32_e32 v62, 16, v63
	v_and_b32_e32 v63, 0xffff0000, v63
	v_pk_fma_f32 v[56:57], v[56:57], v[60:61], v[62:63]
	v_pk_fma_f32 v[54:55], v[54:55], v[58:59], v[64:65]
	v_add_u32_e32 v60, 0x90, v144
	v_cvt_pk_bf16_f32 v54, v54, v55
	v_cvt_pk_bf16_f32 v55, v56, v57
	v_mov_b32_e32 v56, v202
	v_mov_b32_e32 v57, v203
	v_mov_b32_e32 v58, v204
	v_mov_b32_e32 v59, v205
	v_ashrrev_i32_e32 v61, 31, v60
	v_mad_i64_i32 v[62:63], s[24:25], v60, s49, v[146:147]
	global_store_dwordx2 v[70:71], v[54:55], off offset:256
	v_lshl_add_u64 v[62:63], v[62:63], 0, v[142:143]
	v_add_co_u32_e32 v64, vcc, s50, v62
	s_nop 0
	v_lshlrev_b32_e32 v54, 16, v56
	v_and_b32_e32 v55, 0xffff0000, v56
	v_lshlrev_b32_e32 v66, 16, v58
	v_and_b32_e32 v67, 0xffff0000, v58
	v_pk_fma_f32 v[50:51], v[50:51], v[54:55], v[66:67]
	v_lshlrev_b64 v[54:55], 12, v[60:61]
	v_lshlrev_b32_e32 v56, 16, v57
	v_and_b32_e32 v57, 0xffff0000, v57
	v_lshlrev_b32_e32 v58, 16, v59
	v_and_b32_e32 v59, 0xffff0000, v59
	v_lshl_add_u64 v[54:55], s[10:11], 0, v[54:55]
	v_addc_co_u32_e32 v65, vcc, 0, v63, vcc
	v_pk_fma_f32 v[52:53], v[52:53], v[56:57], v[58:59]
	v_lshl_add_u64 v[54:55], v[54:55], 0, v[142:143]
	v_cvt_pk_bf16_f32 v50, v50, v51
	v_cvt_pk_bf16_f32 v51, v52, v53
	v_mov_b32_e32 v52, v206
	v_mov_b32_e32 v53, v207
	v_mov_b32_e32 v56, v208
	v_mov_b32_e32 v57, v209
	v_lshl_add_u64 v[58:59], v[62:63], 0, s[12:13]
	global_store_dwordx2 v[70:71], v[50:51], off offset:288
	s_nop 0
	v_lshlrev_b32_e32 v50, 16, v52
	v_and_b32_e32 v51, 0xffff0000, v52
	v_lshlrev_b32_e32 v52, 16, v53
	v_and_b32_e32 v53, 0xffff0000, v53
	v_lshlrev_b32_e32 v60, 16, v56
	v_and_b32_e32 v61, 0xffff0000, v56
	v_lshlrev_b32_e32 v56, 16, v57
	v_and_b32_e32 v57, 0xffff0000, v57
	v_pk_fma_f32 v[48:49], v[48:49], v[52:53], v[56:57]
	v_pk_fma_f32 v[46:47], v[46:47], v[50:51], v[60:61]
	s_nop 0
	v_cvt_pk_bf16_f32 v46, v46, v47
	v_cvt_pk_bf16_f32 v47, v48, v49
	v_mov_b32_e32 v48, v210
	v_mov_b32_e32 v49, v211
	v_mov_b32_e32 v50, v212
	v_mov_b32_e32 v51, v213
	s_nop 0
	v_lshlrev_b32_e32 v52, 16, v50
	global_store_dwordx2 v[54:55], v[46:47], off
	v_lshlrev_b32_e32 v46, 16, v48
	v_and_b32_e32 v47, 0xffff0000, v48
	v_lshlrev_b32_e32 v48, 16, v49
	v_and_b32_e32 v49, 0xffff0000, v49
	v_and_b32_e32 v53, 0xffff0000, v50
	v_lshlrev_b32_e32 v50, 16, v51
	v_and_b32_e32 v51, 0xffff0000, v51
	v_pk_fma_f32 v[44:45], v[44:45], v[48:49], v[50:51]
	v_pk_fma_f32 v[42:43], v[42:43], v[46:47], v[52:53]
	s_nop 0
	v_cvt_pk_bf16_f32 v42, v42, v43
	v_cvt_pk_bf16_f32 v43, v44, v45
	v_mov_b32_e32 v44, v214
	v_mov_b32_e32 v45, v215
	v_mov_b32_e32 v46, v216
	v_mov_b32_e32 v47, v217
	s_nop 0
	v_lshlrev_b32_e32 v48, 16, v46
	global_store_dwordx2 v[54:55], v[42:43], off offset:32
	v_lshlrev_b32_e32 v42, 16, v44
	v_and_b32_e32 v43, 0xffff0000, v44
	v_lshlrev_b32_e32 v44, 16, v45
	v_and_b32_e32 v45, 0xffff0000, v45
	v_and_b32_e32 v49, 0xffff0000, v46
	v_lshlrev_b32_e32 v46, 16, v47
	v_and_b32_e32 v47, 0xffff0000, v47
	v_pk_fma_f32 v[40:41], v[40:41], v[44:45], v[46:47]
	v_pk_fma_f32 v[38:39], v[38:39], v[42:43], v[48:49]
	v_add_u32_e32 v44, 0xa0, v144
	v_cvt_pk_bf16_f32 v38, v38, v39
	v_cvt_pk_bf16_f32 v39, v40, v41
	v_mov_b32_e32 v40, v218
	v_mov_b32_e32 v41, v219
	v_mov_b32_e32 v42, v220
	v_mov_b32_e32 v43, v221
	v_ashrrev_i32_e32 v45, 31, v44
	v_mad_i64_i32 v[46:47], s[24:25], v44, s49, v[146:147]
	global_store_dwordx2 v[54:55], v[38:39], off offset:256
	v_lshl_add_u64 v[46:47], v[46:47], 0, v[142:143]
	v_add_co_u32_e32 v48, vcc, s50, v46
	s_nop 0
	v_lshlrev_b32_e32 v38, 16, v40
	v_and_b32_e32 v39, 0xffff0000, v40
	v_lshlrev_b32_e32 v50, 16, v42
	v_and_b32_e32 v51, 0xffff0000, v42
	v_pk_fma_f32 v[34:35], v[34:35], v[38:39], v[50:51]
	v_lshlrev_b64 v[38:39], 12, v[44:45]
	v_lshlrev_b32_e32 v40, 16, v41
	v_and_b32_e32 v41, 0xffff0000, v41
	v_lshlrev_b32_e32 v42, 16, v43
	v_and_b32_e32 v43, 0xffff0000, v43
	v_lshl_add_u64 v[38:39], s[10:11], 0, v[38:39]
	v_addc_co_u32_e32 v49, vcc, 0, v47, vcc
	v_pk_fma_f32 v[36:37], v[36:37], v[40:41], v[42:43]
	v_lshl_add_u64 v[38:39], v[38:39], 0, v[142:143]
	v_cvt_pk_bf16_f32 v34, v34, v35
	v_cvt_pk_bf16_f32 v35, v36, v37
	v_mov_b32_e32 v237, 0x1000
	v_mov_b32_e32 v236, 160
	v_mad_i64_i32 v[230:231], s[24:25], v236, s49, v[228:229]
	v_mad_i64_i32 v[234:235], s[24:25], v236, v237, v[232:233]
	global_load_dwordx2 v[174:175], v[230:231], off
	global_load_dwordx2 v[176:177], v[234:235], off
	global_load_dwordx2 v[178:179], v[230:231], off offset:32
	global_load_dwordx2 v[180:181], v[234:235], off offset:32
	global_load_dwordx2 v[182:183], v[230:231], off offset:256
	global_load_dwordx2 v[184:185], v[234:235], off offset:256
	global_load_dwordx2 v[186:187], v[230:231], off offset:288
	global_load_dwordx2 v[188:189], v[234:235], off offset:288
	v_mov_b32_e32 v236, 176
	v_mad_i64_i32 v[230:231], s[24:25], v236, s49, v[228:229]
	v_mad_i64_i32 v[234:235], s[24:25], v236, v237, v[232:233]
	global_load_dwordx2 v[190:191], v[230:231], off
	global_load_dwordx2 v[192:193], v[234:235], off
	global_load_dwordx2 v[194:195], v[230:231], off offset:32
	global_load_dwordx2 v[196:197], v[234:235], off offset:32
	global_load_dwordx2 v[198:199], v[230:231], off offset:256
	global_load_dwordx2 v[200:201], v[234:235], off offset:256
	global_load_dwordx2 v[202:203], v[230:231], off offset:288
	global_load_dwordx2 v[204:205], v[234:235], off offset:288
	s_waitcnt vmcnt(0)
	v_mov_b32_e32 v36, v174
	v_mov_b32_e32 v37, v175
	v_mov_b32_e32 v40, v176
	v_mov_b32_e32 v41, v177
	v_lshl_add_u64 v[42:43], v[46:47], 0, s[12:13]
	global_store_dwordx2 v[54:55], v[34:35], off offset:288
	s_nop 0
	v_lshlrev_b32_e32 v34, 16, v36
	v_and_b32_e32 v35, 0xffff0000, v36
	v_lshlrev_b32_e32 v36, 16, v37
	v_and_b32_e32 v37, 0xffff0000, v37
	v_lshlrev_b32_e32 v44, 16, v40
	v_and_b32_e32 v45, 0xffff0000, v40
	v_lshlrev_b32_e32 v40, 16, v41
	v_and_b32_e32 v41, 0xffff0000, v41
	v_pk_fma_f32 v[32:33], v[32:33], v[36:37], v[40:41]
	v_pk_fma_f32 v[30:31], v[30:31], v[34:35], v[44:45]
	s_nop 0
	v_cvt_pk_bf16_f32 v30, v30, v31
	v_cvt_pk_bf16_f32 v31, v32, v33
	v_mov_b32_e32 v32, v178
	v_mov_b32_e32 v33, v179
	v_mov_b32_e32 v34, v180
	v_mov_b32_e32 v35, v181
	s_nop 0
	v_lshlrev_b32_e32 v36, 16, v34
	global_store_dwordx2 v[38:39], v[30:31], off
	v_lshlrev_b32_e32 v30, 16, v32
	v_and_b32_e32 v31, 0xffff0000, v32
	v_lshlrev_b32_e32 v32, 16, v33
	v_and_b32_e32 v33, 0xffff0000, v33
	v_and_b32_e32 v37, 0xffff0000, v34
	v_lshlrev_b32_e32 v34, 16, v35
	v_and_b32_e32 v35, 0xffff0000, v35
	v_pk_fma_f32 v[28:29], v[28:29], v[32:33], v[34:35]
	v_pk_fma_f32 v[26:27], v[26:27], v[30:31], v[36:37]
	s_nop 0
	v_cvt_pk_bf16_f32 v26, v26, v27
	v_cvt_pk_bf16_f32 v27, v28, v29
	v_mov_b32_e32 v28, v182
	v_mov_b32_e32 v29, v183
	v_mov_b32_e32 v30, v184
	v_mov_b32_e32 v31, v185
	s_nop 0
	v_lshlrev_b32_e32 v32, 16, v30
	global_store_dwordx2 v[38:39], v[26:27], off offset:32
	v_lshlrev_b32_e32 v26, 16, v28
	v_and_b32_e32 v27, 0xffff0000, v28
	v_lshlrev_b32_e32 v28, 16, v29
	v_and_b32_e32 v29, 0xffff0000, v29
	v_and_b32_e32 v33, 0xffff0000, v30
	v_lshlrev_b32_e32 v30, 16, v31
	v_and_b32_e32 v31, 0xffff0000, v31
	v_pk_fma_f32 v[24:25], v[24:25], v[28:29], v[30:31]
	v_pk_fma_f32 v[22:23], v[22:23], v[26:27], v[32:33]
	v_add_u32_e32 v28, 0xb0, v144
	v_cvt_pk_bf16_f32 v22, v22, v23
	v_cvt_pk_bf16_f32 v23, v24, v25
	v_mov_b32_e32 v24, v186
	v_mov_b32_e32 v25, v187
	v_mov_b32_e32 v26, v188
	v_mov_b32_e32 v27, v189
	v_ashrrev_i32_e32 v29, 31, v28
	v_mad_i64_i32 v[30:31], s[24:25], v28, s49, v[146:147]
	global_store_dwordx2 v[38:39], v[22:23], off offset:256
	v_lshl_add_u64 v[30:31], v[30:31], 0, v[142:143]
	v_add_co_u32_e32 v32, vcc, s50, v30
	s_mov_b64 s[24:25], s[18:19]
	s_nop 0
	v_addc_co_u32_e32 v33, vcc, 0, v31, vcc
	s_and_b64 vcc, exec, s[2:3]
	s_nop 0
	v_lshlrev_b32_e32 v22, 16, v24
	v_and_b32_e32 v23, 0xffff0000, v24
	v_lshlrev_b32_e32 v34, 16, v26
	v_and_b32_e32 v35, 0xffff0000, v26
	v_pk_fma_f32 v[18:19], v[18:19], v[22:23], v[34:35]
	v_lshlrev_b64 v[22:23], 12, v[28:29]
	v_lshlrev_b32_e32 v24, 16, v25
	v_and_b32_e32 v25, 0xffff0000, v25
	v_lshlrev_b32_e32 v26, 16, v27
	v_and_b32_e32 v27, 0xffff0000, v27
	v_lshl_add_u64 v[22:23], s[10:11], 0, v[22:23]
	v_pk_fma_f32 v[20:21], v[20:21], v[24:25], v[26:27]
	v_lshl_add_u64 v[22:23], v[22:23], 0, v[142:143]
	v_cvt_pk_bf16_f32 v18, v18, v19
	v_cvt_pk_bf16_f32 v19, v20, v21
	v_mov_b32_e32 v20, v190
	v_mov_b32_e32 v21, v191
	v_mov_b32_e32 v24, v192
	v_mov_b32_e32 v25, v193
	v_lshl_add_u64 v[26:27], v[30:31], 0, s[12:13]
	global_store_dwordx2 v[38:39], v[18:19], off offset:288
	s_nop 0
	v_lshlrev_b32_e32 v18, 16, v20
	v_and_b32_e32 v19, 0xffff0000, v20
	v_lshlrev_b32_e32 v20, 16, v21
	v_and_b32_e32 v21, 0xffff0000, v21
	v_lshlrev_b32_e32 v28, 16, v24
	v_and_b32_e32 v29, 0xffff0000, v24
	v_lshlrev_b32_e32 v24, 16, v25
	v_and_b32_e32 v25, 0xffff0000, v25
	v_pk_fma_f32 v[16:17], v[16:17], v[20:21], v[24:25]
	v_pk_fma_f32 v[14:15], v[14:15], v[18:19], v[28:29]
	s_nop 0
	v_cvt_pk_bf16_f32 v14, v14, v15
	v_cvt_pk_bf16_f32 v15, v16, v17
	v_mov_b32_e32 v16, v194
	v_mov_b32_e32 v17, v195
	v_mov_b32_e32 v18, v196
	v_mov_b32_e32 v19, v197
	s_nop 0
	v_lshlrev_b32_e32 v20, 16, v18
	global_store_dwordx2 v[22:23], v[14:15], off
	v_lshlrev_b32_e32 v14, 16, v16
	v_and_b32_e32 v15, 0xffff0000, v16
	v_lshlrev_b32_e32 v16, 16, v17
	v_and_b32_e32 v17, 0xffff0000, v17
	v_and_b32_e32 v21, 0xffff0000, v18
	v_lshlrev_b32_e32 v18, 16, v19
	v_and_b32_e32 v19, 0xffff0000, v19
	v_pk_fma_f32 v[12:13], v[12:13], v[16:17], v[18:19]
	v_pk_fma_f32 v[10:11], v[10:11], v[14:15], v[20:21]
	s_nop 0
	v_cvt_pk_bf16_f32 v10, v10, v11
	v_cvt_pk_bf16_f32 v11, v12, v13
	v_mov_b32_e32 v12, v198
	v_mov_b32_e32 v13, v199
	v_mov_b32_e32 v14, v200
	v_mov_b32_e32 v15, v201
	s_nop 0
	v_lshlrev_b32_e32 v16, 16, v14
	global_store_dwordx2 v[22:23], v[10:11], off offset:32
	v_lshlrev_b32_e32 v10, 16, v12
	v_and_b32_e32 v11, 0xffff0000, v12
	v_lshlrev_b32_e32 v12, 16, v13
	v_and_b32_e32 v13, 0xffff0000, v13
	v_and_b32_e32 v17, 0xffff0000, v14
	v_lshlrev_b32_e32 v14, 16, v15
	v_and_b32_e32 v15, 0xffff0000, v15
	v_pk_fma_f32 v[8:9], v[8:9], v[12:13], v[14:15]
	v_pk_fma_f32 v[6:7], v[6:7], v[10:11], v[16:17]
	s_nop 0
	v_cvt_pk_bf16_f32 v6, v6, v7
	v_cvt_pk_bf16_f32 v7, v8, v9
	v_mov_b32_e32 v8, v202
	v_mov_b32_e32 v9, v203
	v_mov_b32_e32 v10, v204
	v_mov_b32_e32 v11, v205
	s_nop 0
	v_lshlrev_b32_e32 v12, 16, v10
	global_store_dwordx2 v[22:23], v[6:7], off offset:256
	v_lshlrev_b32_e32 v6, 16, v8
	v_and_b32_e32 v7, 0xffff0000, v8
	v_and_b32_e32 v13, 0xffff0000, v10
	v_lshlrev_b32_e32 v8, 16, v9
	v_and_b32_e32 v9, 0xffff0000, v9
	v_lshlrev_b32_e32 v10, 16, v11
	v_and_b32_e32 v11, 0xffff0000, v11
	v_pk_fma_f32 v[2:3], v[2:3], v[6:7], v[12:13]
	v_pk_fma_f32 v[4:5], v[4:5], v[8:9], v[10:11]
	v_cvt_pk_bf16_f32 v2, v2, v3
	s_nop 0
	v_cvt_pk_bf16_f32 v3, v4, v5
	global_store_dwordx2 v[22:23], v[2:3], off offset:288
	s_cbranch_vccz .LBB0_3240
	s_waitcnt vmcnt(0)
	s_cmpk_gt_u32 s33, 0xff
	s_cbranch_scc1 .LBB0_3247
	s_barrier

.LBB0_3248:
	s_and_b64 vcc, exec, s[0:1]
	v_readfirstlane_b32 s28, v0
	s_cbranch_vccnz .LBB0_3260
	s_add_u32 s29, s6, 0x50480000
	s_addc_u32 s33, s7, 0
	s_add_u32 s34, s6, 0x15d40000
	s_addc_u32 s35, s7, 0
	s_ashr_i32 s37, s30, 31
	s_lshr_b32 s0, s37, 29
	s_add_i32 s0, s30, s0
	s_lshr_b32 s2, s28, 6
	s_ashr_i32 s3, s0, 3
	s_and_b32 s0, s0, -8
	s_lshr_b32 s1, s28, 8
	s_lshl_b32 s36, s2, 10
	s_sub_i32 s0, s30, s0
	s_cmp_lt_i32 s0, 0
	s_cselect_b32 s8, 0x41, 64
	s_mul_i32 s0, s8, s0
	s_add_i32 s0, s0, s3
	s_ashr_i32 s3, s0, 31
	s_lshr_b32 s3, s3, 26
	s_add_i32 s3, s0, s3
	s_ashr_i32 s8, s3, 6
	s_lshl_b32 s10, s8, 3
	s_sub_i32 s8, 64, s10
	s_min_u32 s11, s8, 8
	s_andn2_b32 s3, s3, 63
	s_sub_i32 s3, s0, s3
	v_cvt_f32_ubyte0_e32 v3, s11
	v_cvt_f32_i32_e32 v2, s3
	v_rcp_iflag_f32_e32 v4, v3
	s_ashr_i32 s0, s3, 30
	s_or_b32 s0, s0, 1
	v_mov_b32_e32 v131, 0
	v_mul_f32_e32 v4, v2, v4
	v_trunc_f32_e32 v4, v4
	v_fma_f32 v2, -v4, v3, v2
	v_cvt_i32_f32_e32 v4, v4
	v_cmp_ge_f32_e64 s[8:9], |v2|, v3
	s_and_b64 s[8:9], s[8:9], exec
	s_cselect_b32 s0, s0, 0
	v_readfirstlane_b32 s8, v4
	s_add_i32 s0, s8, s0
	s_mul_i32 s8, s0, s11
	s_sub_i32 s3, s3, s8
	s_sext_i32_i8 s3, s3
	s_add_i32 s20, s10, s3
	s_ashr_i32 s21, s20, 31
	s_lshl_b64 s[8:9], s[20:21], 19
	s_add_u32 s22, s29, s8
	s_addc_u32 s23, s33, s9
	s_bfe_i64 s[8:9], s[0:1], 0x80000
	s_lshl_b64 s[8:9], s[8:9], 19
	s_add_u32 s24, s34, s8
	s_addc_u32 s25, s35, s9
	s_add_i32 s21, s36, 0
	s_add_i32 m0, s21, 0x10000
	s_add_i32 s38, s21, 0x2000
	global_load_lds_dwordx4 v130, s[24:25]
	s_add_i32 m0, s21, 0x12000
	s_add_u32 s8, s24, 0x40000
	global_load_lds_dwordx4 v132, s[24:25]
	s_mov_b32 m0, s21
	s_addc_u32 s9, s25, 0
	global_load_lds_dwordx4 v130, s[22:23]
	s_mov_b32 m0, s38
	v_mov_b32_e32 v133, v131
	global_load_lds_dwordx4 v132, s[22:23]
	s_add_i32 m0, s21, 0x14000
	s_mov_b32 s41, 0
	global_load_lds_dwordx4 v130, s[8:9]
	s_add_i32 m0, s21, 0x16000
	s_waitcnt vmcnt(0)
	v_lshl_add_u64 v[8:9], s[24:25], 0, v[130:131]
	global_load_lds_dwordx4 v132, s[8:9]
	s_add_u32 s8, s22, 0x40000
	s_addc_u32 s9, s23, 0
	s_add_i32 s39, s21, 0x4000
	s_mov_b32 m0, s39
	s_add_i32 s40, s21, 0x6000
	global_load_lds_dwordx4 v130, s[8:9]
	s_mov_b32 m0, s40
	v_lshl_add_u64 v[6:7], s[24:25], 0, v[132:133]
	global_load_lds_dwordx4 v132, s[8:9]
	v_lshl_add_u64 v[4:5], s[22:23], 0, v[130:131]
	s_setprio 1
	s_cmp_lg_u32 s1, 1
	v_lshl_add_u64 v[2:3], s[22:23], 0, v[132:133]
	s_cbranch_scc1 .LBB0_3251
	s_barrier
	s_setprio 0

.LBB0_3255:
	ds_read_b128 v[142:145], v1
	ds_read_b128 v[156:159], v1 offset:1024
	ds_read_b128 v[160:163], v1 offset:2048
	ds_read_b128 v[164:167], v1 offset:3072
	s_add_u32 s24, s22, 0xfffc0080
	s_addc_u32 s25, s23, -1
	s_cmp_eq_u32 s54, 12
	s_cselect_b32 s27, s15, s25
	s_cselect_b32 s26, s50, s24
	s_cselect_b32 s25, s13, s53
	s_cselect_b32 s24, s51, s52
	v_lshl_add_u64 v[146:147], s[22:23], 0, v[134:135]
	s_add_i32 m0, s21, 0xc000
	ds_read_b128 v[168:171], v148
	ds_read_b128 v[172:175], v148 offset:1024
	ds_read_b128 v[176:179], v148 offset:2048
	ds_read_b128 v[180:183], v148 offset:3072
	ds_read_b128 v[184:187], v148 offset:4096
	ds_read_b128 v[188:191], v148 offset:5120
	ds_read_b128 v[192:195], v148 offset:6144
	ds_read_b128 v[196:199], v148 offset:7168
	global_load_lds_dwordx4 v[146:147], off
	v_lshl_add_u64 v[146:147], s[22:23], 0, v[136:137]
	s_add_i32 m0, s21, 0xe000
	s_nop 0
	global_load_lds_dwordx4 v[146:147], off
	s_waitcnt lgkmcnt(8)
	s_barrier
	s_waitcnt lgkmcnt(0)
	s_waitcnt lgkmcnt(0)
	v_mfma_f32_16x16x32_bf16 v[126:129], v[142:145], v[168:171], v[126:129]
	v_mfma_f32_16x16x32_bf16 v[122:125], v[160:163], v[168:171], v[122:125]
	v_mfma_f32_16x16x32_bf16 v[110:113], v[142:145], v[176:179], v[110:113]
	v_mfma_f32_16x16x32_bf16 v[106:109], v[160:163], v[176:179], v[106:109]
	v_mfma_f32_16x16x32_bf16 v[94:97], v[142:145], v[184:187], v[94:97]
	v_mfma_f32_16x16x32_bf16 v[90:93], v[160:163], v[184:187], v[90:93]
	v_mfma_f32_16x16x32_bf16 v[78:81], v[142:145], v[192:195], v[78:81]
	v_mfma_f32_16x16x32_bf16 v[74:77], v[160:163], v[192:195], v[74:77]
	v_mfma_f32_16x16x32_bf16 v[126:129], v[156:159], v[172:175], v[126:129]
	v_mfma_f32_16x16x32_bf16 v[122:125], v[164:167], v[172:175], v[122:125]
	v_mfma_f32_16x16x32_bf16 v[110:113], v[156:159], v[180:183], v[110:113]
	v_mfma_f32_16x16x32_bf16 v[106:109], v[164:167], v[180:183], v[106:109]
	v_mfma_f32_16x16x32_bf16 v[94:97], v[156:159], v[188:191], v[94:97]
	v_mfma_f32_16x16x32_bf16 v[90:93], v[164:167], v[188:191], v[90:93]
	v_mfma_f32_16x16x32_bf16 v[78:81], v[156:159], v[196:199], v[78:81]
	v_mfma_f32_16x16x32_bf16 v[74:77], v[164:167], v[196:199], v[74:77]
	s_barrier
	s_add_i32 s55, s45, s36
	v_lshl_add_u64 v[146:147], s[24:25], 0, v[130:131]
	s_mov_b32 m0, s55
	ds_read_b128 v[200:203], v149
	ds_read_b128 v[204:207], v149 offset:1024
	ds_read_b128 v[208:211], v149 offset:2048
	ds_read_b128 v[212:215], v149 offset:3072
	global_load_lds_dwordx4 v[146:147], off
	v_lshl_add_u64 v[216:217], s[24:25], 0, v[132:133]
	s_add_i32 m0, s55, 0x2000
	s_nop 0
	global_load_lds_dwordx4 v[216:217], off
	s_barrier
	s_waitcnt lgkmcnt(0)
	s_waitcnt lgkmcnt(0)
	v_mfma_f32_16x16x32_bf16 v[118:121], v[200:203], v[168:171], v[118:121]
	v_mfma_f32_16x16x32_bf16 v[114:117], v[208:211], v[168:171], v[114:117]
	v_mfma_f32_16x16x32_bf16 v[102:105], v[200:203], v[176:179], v[102:105]
	v_mfma_f32_16x16x32_bf16 v[98:101], v[208:211], v[176:179], v[98:101]
	v_mfma_f32_16x16x32_bf16 v[86:89], v[200:203], v[184:187], v[86:89]
	v_mfma_f32_16x16x32_bf16 v[82:85], v[208:211], v[184:187], v[82:85]
	v_mfma_f32_16x16x32_bf16 v[70:73], v[200:203], v[192:195], v[70:73]
	v_mfma_f32_16x16x32_bf16 v[66:69], v[208:211], v[192:195], v[66:69]
	v_mfma_f32_16x16x32_bf16 v[118:121], v[204:207], v[172:175], v[118:121]
	v_mfma_f32_16x16x32_bf16 v[114:117], v[212:215], v[172:175], v[114:117]
	v_mfma_f32_16x16x32_bf16 v[102:105], v[204:207], v[180:183], v[102:105]
	v_mfma_f32_16x16x32_bf16 v[98:101], v[212:215], v[180:183], v[98:101]
	v_mfma_f32_16x16x32_bf16 v[86:89], v[204:207], v[188:191], v[86:89]
	v_mfma_f32_16x16x32_bf16 v[82:85], v[212:215], v[188:191], v[82:85]
	v_mfma_f32_16x16x32_bf16 v[70:73], v[204:207], v[196:199], v[70:73]
	v_mfma_f32_16x16x32_bf16 v[66:69], v[212:215], v[196:199], v[66:69]
	s_mov_b32 m0, s21
	v_lshl_add_u64 v[218:219], s[26:27], 0, v[130:131]
	s_barrier
	ds_read_b128 v[168:171], v148 offset:16384
	ds_read_b128 v[172:175], v148 offset:17408
	ds_read_b128 v[176:179], v148 offset:18432
	ds_read_b128 v[180:183], v148 offset:19456
	ds_read_b128 v[184:187], v148 offset:20480
	ds_read_b128 v[188:191], v148 offset:21504
	ds_read_b128 v[192:195], v148 offset:22528
	ds_read_b128 v[196:199], v148 offset:23552
	global_load_lds_dwordx4 v[218:219], off
	v_lshl_add_u64 v[220:221], s[26:27], 0, v[132:133]
	s_mov_b32 m0, s38
	s_nop 0
	global_load_lds_dwordx4 v[220:221], off
	s_barrier
	s_waitcnt lgkmcnt(0)
	s_waitcnt lgkmcnt(0)
	v_mfma_f32_16x16x32_bf16 v[62:65], v[142:145], v[168:171], v[62:65]
	v_mfma_f32_16x16x32_bf16 v[58:61], v[160:163], v[168:171], v[58:61]
	v_mfma_f32_16x16x32_bf16 v[46:49], v[142:145], v[176:179], v[46:49]
	v_mfma_f32_16x16x32_bf16 v[42:45], v[160:163], v[176:179], v[42:45]
	v_mfma_f32_16x16x32_bf16 v[30:33], v[142:145], v[184:187], v[30:33]
	v_mfma_f32_16x16x32_bf16 v[26:29], v[160:163], v[184:187], v[26:29]
	v_mfma_f32_16x16x32_bf16 v[14:17], v[142:145], v[192:195], v[14:17]
	v_mfma_f32_16x16x32_bf16 v[10:13], v[160:163], v[192:195], v[10:13]
	v_mfma_f32_16x16x32_bf16 v[62:65], v[156:159], v[172:175], v[62:65]
	v_mfma_f32_16x16x32_bf16 v[58:61], v[164:167], v[172:175], v[58:61]
	v_mfma_f32_16x16x32_bf16 v[46:49], v[156:159], v[180:183], v[46:49]
	v_mfma_f32_16x16x32_bf16 v[42:45], v[164:167], v[180:183], v[42:45]
	v_mfma_f32_16x16x32_bf16 v[30:33], v[156:159], v[188:191], v[30:33]
	v_mfma_f32_16x16x32_bf16 v[26:29], v[164:167], v[188:191], v[26:29]
	v_mfma_f32_16x16x32_bf16 v[14:17], v[156:159], v[196:199], v[14:17]
	v_mfma_f32_16x16x32_bf16 v[10:13], v[164:167], v[196:199], v[10:13]
	s_barrier
	s_add_u32 s56, s24, 0x40000
	s_addc_u32 s57, s25, 0
	s_add_i32 s55, s46, s36
	v_lshl_add_u64 v[142:143], s[56:57], 0, v[130:131]
	s_mov_b32 m0, s55
	s_nop 0
	global_load_lds_dwordx4 v[142:143], off
	v_lshl_add_u64 v[142:143], s[56:57], 0, v[132:133]
	s_add_i32 m0, s55, 0x2000
	s_nop 0
	global_load_lds_dwordx4 v[142:143], off
	s_waitcnt vmcnt(6)
	s_barrier
	v_mfma_f32_16x16x32_bf16 v[54:57], v[200:203], v[168:171], v[54:57]
	v_mfma_f32_16x16x32_bf16 v[50:53], v[208:211], v[168:171], v[50:53]
	v_mfma_f32_16x16x32_bf16 v[38:41], v[200:203], v[176:179], v[38:41]
	v_mfma_f32_16x16x32_bf16 v[34:37], v[208:211], v[176:179], v[34:37]
	v_mfma_f32_16x16x32_bf16 v[22:25], v[200:203], v[184:187], v[22:25]
	v_mfma_f32_16x16x32_bf16 v[18:21], v[208:211], v[184:187], v[18:21]
	v_mfma_f32_16x16x32_bf16 v[6:9], v[200:203], v[192:195], v[6:9]
	v_mfma_f32_16x16x32_bf16 v[2:5], v[208:211], v[192:195], v[2:5]
	v_mfma_f32_16x16x32_bf16 v[54:57], v[204:207], v[172:175], v[54:57]
	v_mfma_f32_16x16x32_bf16 v[50:53], v[212:215], v[172:175], v[50:53]
	v_mfma_f32_16x16x32_bf16 v[38:41], v[204:207], v[180:183], v[38:41]
	v_mfma_f32_16x16x32_bf16 v[34:37], v[212:215], v[180:183], v[34:37]
	v_mfma_f32_16x16x32_bf16 v[22:25], v[204:207], v[188:191], v[22:25]
	v_mfma_f32_16x16x32_bf16 v[18:21], v[212:215], v[188:191], v[18:21]
	v_mfma_f32_16x16x32_bf16 v[6:9], v[204:207], v[196:199], v[6:9]
	v_mfma_f32_16x16x32_bf16 v[2:5], v[212:215], v[196:199], v[2:5]
	s_add_i32 s55, 0, 0x18000
	v_add_u32_e32 v150, s55, v152
	s_barrier
	ds_read_b128 v[142:145], v150
	ds_read_b128 v[156:159], v150 offset:1024
	ds_read_b128 v[160:163], v150 offset:2048
	ds_read_b128 v[164:167], v150 offset:3072
	s_add_u32 s26, s26, 0x40000
	s_addc_u32 s27, s27, 0
	s_mov_b32 m0, s39
	v_lshl_add_u64 v[200:201], s[26:27], 0, v[130:131]
	ds_read_b128 v[168:171], v148 offset:32768
	ds_read_b128 v[172:175], v148 offset:33792
	ds_read_b128 v[176:179], v148 offset:34816
	ds_read_b128 v[180:183], v148 offset:35840
	ds_read_b128 v[184:187], v148 offset:36864
	ds_read_b128 v[188:191], v148 offset:37888
	ds_read_b128 v[192:195], v148 offset:38912
	ds_read_b128 v[196:199], v148 offset:39936
	global_load_lds_dwordx4 v[200:201], off
	v_lshl_add_u64 v[200:201], s[26:27], 0, v[132:133]
	s_mov_b32 m0, s40
	s_nop 0
	global_load_lds_dwordx4 v[200:201], off
	s_waitcnt lgkmcnt(8)
	s_barrier
	s_waitcnt lgkmcnt(0)
	s_waitcnt lgkmcnt(0)
	v_mfma_f32_16x16x32_bf16 v[126:129], v[142:145], v[168:171], v[126:129]
	v_mfma_f32_16x16x32_bf16 v[122:125], v[160:163], v[168:171], v[122:125]
	v_mfma_f32_16x16x32_bf16 v[110:113], v[142:145], v[176:179], v[110:113]
	v_mfma_f32_16x16x32_bf16 v[106:109], v[160:163], v[176:179], v[106:109]
	v_mfma_f32_16x16x32_bf16 v[94:97], v[142:145], v[184:187], v[94:97]
	v_mfma_f32_16x16x32_bf16 v[90:93], v[160:163], v[184:187], v[90:93]
	v_mfma_f32_16x16x32_bf16 v[78:81], v[142:145], v[192:195], v[78:81]
	v_mfma_f32_16x16x32_bf16 v[74:77], v[160:163], v[192:195], v[74:77]
	v_mfma_f32_16x16x32_bf16 v[126:129], v[156:159], v[172:175], v[126:129]
	v_mfma_f32_16x16x32_bf16 v[122:125], v[164:167], v[172:175], v[122:125]
	v_mfma_f32_16x16x32_bf16 v[110:113], v[156:159], v[180:183], v[110:113]
	v_mfma_f32_16x16x32_bf16 v[106:109], v[164:167], v[180:183], v[106:109]
	v_mfma_f32_16x16x32_bf16 v[94:97], v[156:159], v[188:191], v[94:97]
	v_mfma_f32_16x16x32_bf16 v[90:93], v[164:167], v[188:191], v[90:93]
	v_mfma_f32_16x16x32_bf16 v[78:81], v[156:159], v[196:199], v[78:81]
	v_mfma_f32_16x16x32_bf16 v[74:77], v[164:167], v[196:199], v[74:77]
	s_barrier
	s_add_i32 s26, 0, 0x1c000
	s_add_i32 s27, s55, s36
	v_add_u32_e32 v150, s26, v152
	v_lshl_add_u64 v[146:147], v[146:147], 0, s[2:3]
	s_mov_b32 m0, s27
	ds_read_b128 v[200:203], v150
	ds_read_b128 v[204:207], v150 offset:1024
	ds_read_b128 v[208:211], v150 offset:2048
	ds_read_b128 v[212:215], v150 offset:3072
	global_load_lds_dwordx4 v[146:147], off
	v_lshl_add_u64 v[146:147], v[216:217], 0, s[2:3]
	s_add_i32 m0, s27, 0x2000
	s_nop 0
	global_load_lds_dwordx4 v[146:147], off
	s_barrier
	s_waitcnt lgkmcnt(0)
	s_waitcnt lgkmcnt(0)
	v_mfma_f32_16x16x32_bf16 v[118:121], v[200:203], v[168:171], v[118:121]
	v_mfma_f32_16x16x32_bf16 v[114:117], v[208:211], v[168:171], v[114:117]
	v_mfma_f32_16x16x32_bf16 v[102:105], v[200:203], v[176:179], v[102:105]
	v_mfma_f32_16x16x32_bf16 v[98:101], v[208:211], v[176:179], v[98:101]
	v_mfma_f32_16x16x32_bf16 v[86:89], v[200:203], v[184:187], v[86:89]
	v_mfma_f32_16x16x32_bf16 v[82:85], v[208:211], v[184:187], v[82:85]
	v_mfma_f32_16x16x32_bf16 v[70:73], v[200:203], v[192:195], v[70:73]
	v_mfma_f32_16x16x32_bf16 v[66:69], v[208:211], v[192:195], v[66:69]
	v_mfma_f32_16x16x32_bf16 v[118:121], v[204:207], v[172:175], v[118:121]
	v_mfma_f32_16x16x32_bf16 v[114:117], v[212:215], v[172:175], v[114:117]
	v_mfma_f32_16x16x32_bf16 v[102:105], v[204:207], v[180:183], v[102:105]
	v_mfma_f32_16x16x32_bf16 v[98:101], v[212:215], v[180:183], v[98:101]
	v_mfma_f32_16x16x32_bf16 v[86:89], v[204:207], v[188:191], v[86:89]
	v_mfma_f32_16x16x32_bf16 v[82:85], v[212:215], v[188:191], v[82:85]
	v_mfma_f32_16x16x32_bf16 v[70:73], v[204:207], v[196:199], v[70:73]
	v_mfma_f32_16x16x32_bf16 v[66:69], v[212:215], v[196:199], v[66:69]
	s_mov_b32 m0, s42
	v_lshl_add_u64 v[146:147], v[218:219], 0, s[2:3]
	s_barrier
	ds_read_b128 v[168:171], v148 offset:49152
	ds_read_b128 v[172:175], v148 offset:50176
	ds_read_b128 v[176:179], v148 offset:51200
	ds_read_b128 v[180:183], v148 offset:52224
	ds_read_b128 v[184:187], v148 offset:53248
	ds_read_b128 v[188:191], v148 offset:54272
	ds_read_b128 v[192:195], v148 offset:55296
	ds_read_b128 v[196:199], v148 offset:56320
	global_load_lds_dwordx4 v[146:147], off
	v_lshl_add_u64 v[146:147], v[220:221], 0, s[2:3]
	s_mov_b32 m0, s43
	s_nop 0
	global_load_lds_dwordx4 v[146:147], off
	s_barrier
	s_waitcnt lgkmcnt(0)
	s_waitcnt lgkmcnt(0)
	v_mfma_f32_16x16x32_bf16 v[62:65], v[142:145], v[168:171], v[62:65]
	v_mfma_f32_16x16x32_bf16 v[58:61], v[160:163], v[168:171], v[58:61]
	v_mfma_f32_16x16x32_bf16 v[46:49], v[142:145], v[176:179], v[46:49]
	v_mfma_f32_16x16x32_bf16 v[42:45], v[160:163], v[176:179], v[42:45]
	v_mfma_f32_16x16x32_bf16 v[30:33], v[142:145], v[184:187], v[30:33]
	v_mfma_f32_16x16x32_bf16 v[26:29], v[160:163], v[184:187], v[26:29]
	v_mfma_f32_16x16x32_bf16 v[14:17], v[142:145], v[192:195], v[14:17]
	v_mfma_f32_16x16x32_bf16 v[10:13], v[160:163], v[192:195], v[10:13]
	v_mfma_f32_16x16x32_bf16 v[62:65], v[156:159], v[172:175], v[62:65]
	v_mfma_f32_16x16x32_bf16 v[58:61], v[164:167], v[172:175], v[58:61]
	v_mfma_f32_16x16x32_bf16 v[46:49], v[156:159], v[180:183], v[46:49]
	v_mfma_f32_16x16x32_bf16 v[42:45], v[164:167], v[180:183], v[42:45]
	v_mfma_f32_16x16x32_bf16 v[30:33], v[156:159], v[188:191], v[30:33]
	v_mfma_f32_16x16x32_bf16 v[26:29], v[164:167], v[188:191], v[26:29]
	v_mfma_f32_16x16x32_bf16 v[14:17], v[156:159], v[196:199], v[14:17]
	v_mfma_f32_16x16x32_bf16 v[10:13], v[164:167], v[196:199], v[10:13]
	s_barrier
	s_add_u32 s24, s24, 0x40080
	s_addc_u32 s25, s25, 0
	s_add_i32 s26, s26, s36
	v_lshl_add_u64 v[142:143], s[24:25], 0, v[130:131]
	s_mov_b32 m0, s26
	s_nop 0
	global_load_lds_dwordx4 v[142:143], off
	v_lshl_add_u64 v[142:143], s[24:25], 0, v[132:133]
	s_add_i32 m0, s26, 0x2000
	s_nop 0
	global_load_lds_dwordx4 v[142:143], off
	s_waitcnt vmcnt(6)
	s_barrier
	v_mfma_f32_16x16x32_bf16 v[54:57], v[200:203], v[168:171], v[54:57]
	v_mfma_f32_16x16x32_bf16 v[50:53], v[208:211], v[168:171], v[50:53]
	v_mfma_f32_16x16x32_bf16 v[38:41], v[200:203], v[176:179], v[38:41]
	v_mfma_f32_16x16x32_bf16 v[34:37], v[208:211], v[176:179], v[34:37]
	v_mfma_f32_16x16x32_bf16 v[22:25], v[200:203], v[184:187], v[22:25]
	v_mfma_f32_16x16x32_bf16 v[18:21], v[208:211], v[184:187], v[18:21]
	v_mfma_f32_16x16x32_bf16 v[6:9], v[200:203], v[192:195], v[6:9]
	v_mfma_f32_16x16x32_bf16 v[2:5], v[208:211], v[192:195], v[2:5]
	v_mfma_f32_16x16x32_bf16 v[54:57], v[204:207], v[172:175], v[54:57]
	v_mfma_f32_16x16x32_bf16 v[50:53], v[212:215], v[172:175], v[50:53]
	v_mfma_f32_16x16x32_bf16 v[38:41], v[204:207], v[180:183], v[38:41]
	v_mfma_f32_16x16x32_bf16 v[34:37], v[212:215], v[180:183], v[34:37]
	v_mfma_f32_16x16x32_bf16 v[22:25], v[204:207], v[188:191], v[22:25]
	v_mfma_f32_16x16x32_bf16 v[18:21], v[212:215], v[188:191], v[18:21]
	v_mfma_f32_16x16x32_bf16 v[6:9], v[204:207], v[196:199], v[6:9]
	v_mfma_f32_16x16x32_bf16 v[2:5], v[212:215], v[196:199], v[2:5]
	s_add_i32 s54, s54, 2
	s_add_u32 s22, s22, 0x100
	s_addc_u32 s23, s23, 0
	s_add_u32 s52, s52, 0x100
	s_addc_u32 s53, s53, 0
	s_cmp_gt_u32 s54, 13
	s_barrier
	s_cbranch_scc0 .LBB0_3255
	v_lshl_or_b32 v142, s49, 8, v151
	v_lshl_add_u32 v144, s20, 8, v155
	v_ashrrev_i32_e32 v143, 31, v142
	v_mov_b64_e32 v[146:147], s[6:7]
	v_ashrrev_i32_e32 v145, 31, v144
	v_mad_i64_i32 v[156:157], s[22:23], v144, s47, v[146:147]
	v_lshlrev_b64 v[142:143], 1, v[142:143]
	v_lshl_add_u64 v[156:157], v[156:157], 0, v[142:143]
	v_lshlrev_b64 v[160:161], 12, v[144:145]
	v_add_co_u32_e32 v158, vcc, 0x2ec42000, v156
	v_lshl_add_u64 v[160:161], s[8:9], 0, v[160:161]
	s_nop 0
	v_addc_co_u32_e32 v159, vcc, 0, v157, vcc
	v_lshl_add_u64 v[160:161], v[160:161], 0, v[142:143]
	v_mov_b32_e32 v228, v158
	v_mov_b32_e32 v229, v159
	v_mov_b32_e32 v232, v160
	v_mov_b32_e32 v233, v161
	v_mov_b32_e32 v237, 0x1000
	global_load_dwordx2 v[168:169], v[228:229], off
	global_load_dwordx2 v[170:171], v[232:233], off
	global_load_dwordx2 v[172:173], v[228:229], off offset:32
	global_load_dwordx2 v[174:175], v[232:233], off offset:32
	global_load_dwordx2 v[176:177], v[228:229], off offset:256
	global_load_dwordx2 v[178:179], v[232:233], off offset:256
	global_load_dwordx2 v[180:181], v[228:229], off offset:288
	global_load_dwordx2 v[182:183], v[232:233], off offset:288
	v_mov_b32_e32 v236, 16
	v_mad_i64_i32 v[230:231], s[22:23], v236, s47, v[228:229]
	v_mad_i64_i32 v[234:235], s[22:23], v236, v237, v[232:233]
	global_load_dwordx2 v[184:185], v[230:231], off
	global_load_dwordx2 v[186:187], v[234:235], off
	global_load_dwordx2 v[188:189], v[230:231], off offset:32
	global_load_dwordx2 v[190:191], v[234:235], off offset:32
	global_load_dwordx2 v[192:193], v[230:231], off offset:256
	global_load_dwordx2 v[194:195], v[234:235], off offset:256
	global_load_dwordx2 v[196:197], v[230:231], off offset:288
	global_load_dwordx2 v[198:199], v[234:235], off offset:288
	v_mov_b32_e32 v236, 32
	v_mad_i64_i32 v[230:231], s[22:23], v236, s47, v[228:229]
	v_mad_i64_i32 v[234:235], s[22:23], v236, v237, v[232:233]
	global_load_dwordx2 v[200:201], v[230:231], off
	global_load_dwordx2 v[202:203], v[234:235], off
	global_load_dwordx2 v[204:205], v[230:231], off offset:32
	global_load_dwordx2 v[206:207], v[234:235], off offset:32
	global_load_dwordx2 v[208:209], v[230:231], off offset:256
	global_load_dwordx2 v[210:211], v[234:235], off offset:256
	global_load_dwordx2 v[212:213], v[230:231], off offset:288
	global_load_dwordx2 v[214:215], v[234:235], off offset:288
	s_waitcnt vmcnt(0)
	v_mov_b32_e32 v158, v168
	v_mov_b32_e32 v159, v169
	v_lshl_add_u64 v[156:157], v[156:157], 0, s[10:11]
	v_mov_b32_e32 v162, v170
	v_mov_b32_e32 v163, v171
	s_mov_b32 s49, s12
	s_mov_b32 s20, s14
	s_mov_b64 s[24:25], s[18:19]
	s_nop 0
	v_lshlrev_b32_e32 v164, 16, v158
	v_and_b32_e32 v165, 0xffff0000, v158
	v_lshlrev_b32_e32 v158, 16, v159
	v_and_b32_e32 v159, 0xffff0000, v159
	v_lshlrev_b32_e32 v166, 16, v162
	v_and_b32_e32 v167, 0xffff0000, v162
	v_lshlrev_b32_e32 v162, 16, v163
	v_and_b32_e32 v163, 0xffff0000, v163
	v_pk_fma_f32 v[128:129], v[128:129], v[158:159], v[162:163]
	v_pk_fma_f32 v[126:127], v[126:127], v[164:165], v[166:167]
	s_nop 0
	v_cvt_pk_bf16_f32 v126, v126, v127
	v_cvt_pk_bf16_f32 v127, v128, v129
	v_mov_b32_e32 v128, v172
	v_mov_b32_e32 v129, v173
	v_mov_b32_e32 v158, v174
	v_mov_b32_e32 v159, v175
	s_nop 0
	v_lshlrev_b32_e32 v162, 16, v158
	global_store_dwordx2 v[160:161], v[126:127], off
	v_lshlrev_b32_e32 v126, 16, v128
	v_and_b32_e32 v127, 0xffff0000, v128
	v_lshlrev_b32_e32 v128, 16, v129
	v_and_b32_e32 v129, 0xffff0000, v129
	v_and_b32_e32 v163, 0xffff0000, v158
	v_lshlrev_b32_e32 v158, 16, v159
	v_and_b32_e32 v159, 0xffff0000, v159
	v_pk_fma_f32 v[124:125], v[124:125], v[128:129], v[158:159]
	v_pk_fma_f32 v[122:123], v[122:123], v[126:127], v[162:163]
	s_nop 0
	v_cvt_pk_bf16_f32 v122, v122, v123
	v_cvt_pk_bf16_f32 v123, v124, v125
	v_mov_b32_e32 v124, v176
	v_mov_b32_e32 v125, v177
	v_mov_b32_e32 v126, v178
	v_mov_b32_e32 v127, v179
	s_nop 0
	v_lshlrev_b32_e32 v128, 16, v126
	global_store_dwordx2 v[160:161], v[122:123], off offset:32
	v_lshlrev_b32_e32 v122, 16, v124
	v_and_b32_e32 v123, 0xffff0000, v124
	v_lshlrev_b32_e32 v124, 16, v125
	v_and_b32_e32 v125, 0xffff0000, v125
	v_and_b32_e32 v129, 0xffff0000, v126
	v_lshlrev_b32_e32 v126, 16, v127
	v_and_b32_e32 v127, 0xffff0000, v127
	v_pk_fma_f32 v[120:121], v[120:121], v[124:125], v[126:127]
	v_pk_fma_f32 v[118:119], v[118:119], v[122:123], v[128:129]
	v_or_b32_e32 v124, 16, v144
	v_cvt_pk_bf16_f32 v118, v118, v119
	v_cvt_pk_bf16_f32 v119, v120, v121
	v_mov_b32_e32 v120, v180
	v_mov_b32_e32 v121, v181
	v_mov_b32_e32 v122, v182
	v_mov_b32_e32 v123, v183
	v_ashrrev_i32_e32 v125, 31, v124
	v_mad_i64_i32 v[126:127], s[22:23], v124, s47, v[146:147]
	global_store_dwordx2 v[160:161], v[118:119], off offset:256
	v_lshl_add_u64 v[126:127], v[126:127], 0, v[142:143]
	v_add_co_u32_e32 v128, vcc, s48, v126
	s_nop 0
	v_lshlrev_b32_e32 v118, 16, v120
	v_and_b32_e32 v119, 0xffff0000, v120
	v_lshlrev_b32_e32 v156, 16, v122
	v_and_b32_e32 v157, 0xffff0000, v122
	v_pk_fma_f32 v[114:115], v[114:115], v[118:119], v[156:157]
	v_lshlrev_b64 v[118:119], 12, v[124:125]
	v_lshlrev_b32_e32 v120, 16, v121
	v_and_b32_e32 v121, 0xffff0000, v121
	v_lshlrev_b32_e32 v122, 16, v123
	v_and_b32_e32 v123, 0xffff0000, v123
	v_lshl_add_u64 v[118:119], s[8:9], 0, v[118:119]
	v_addc_co_u32_e32 v129, vcc, 0, v127, vcc
	v_pk_fma_f32 v[116:117], v[116:117], v[120:121], v[122:123]
	v_lshl_add_u64 v[118:119], v[118:119], 0, v[142:143]
	v_cvt_pk_bf16_f32 v114, v114, v115
	v_cvt_pk_bf16_f32 v115, v116, v117
	v_mov_b32_e32 v116, v184
	v_mov_b32_e32 v117, v185
	v_mov_b32_e32 v120, v186
	v_mov_b32_e32 v121, v187
	v_lshl_add_u64 v[122:123], v[126:127], 0, s[10:11]
	global_store_dwordx2 v[160:161], v[114:115], off offset:288
	s_nop 0
	v_lshlrev_b32_e32 v114, 16, v116
	v_and_b32_e32 v115, 0xffff0000, v116
	v_lshlrev_b32_e32 v116, 16, v117
	v_and_b32_e32 v117, 0xffff0000, v117
	v_lshlrev_b32_e32 v124, 16, v120
	v_and_b32_e32 v125, 0xffff0000, v120
	v_lshlrev_b32_e32 v120, 16, v121
	v_and_b32_e32 v121, 0xffff0000, v121
	v_pk_fma_f32 v[112:113], v[112:113], v[116:117], v[120:121]
	v_pk_fma_f32 v[110:111], v[110:111], v[114:115], v[124:125]
	s_nop 0
	v_cvt_pk_bf16_f32 v110, v110, v111
	v_cvt_pk_bf16_f32 v111, v112, v113
	v_mov_b32_e32 v112, v188
	v_mov_b32_e32 v113, v189
	v_mov_b32_e32 v114, v190
	v_mov_b32_e32 v115, v191
	s_nop 0
	v_lshlrev_b32_e32 v116, 16, v114
	global_store_dwordx2 v[118:119], v[110:111], off
	v_lshlrev_b32_e32 v110, 16, v112
	v_and_b32_e32 v111, 0xffff0000, v112
	v_lshlrev_b32_e32 v112, 16, v113
	v_and_b32_e32 v113, 0xffff0000, v113
	v_and_b32_e32 v117, 0xffff0000, v114
	v_lshlrev_b32_e32 v114, 16, v115
	v_and_b32_e32 v115, 0xffff0000, v115
	v_pk_fma_f32 v[108:109], v[108:109], v[112:113], v[114:115]
	v_pk_fma_f32 v[106:107], v[106:107], v[110:111], v[116:117]
	s_nop 0
	v_cvt_pk_bf16_f32 v106, v106, v107
	v_cvt_pk_bf16_f32 v107, v108, v109
	v_mov_b32_e32 v108, v192
	v_mov_b32_e32 v109, v193
	v_mov_b32_e32 v110, v194
	v_mov_b32_e32 v111, v195
	s_nop 0
	v_lshlrev_b32_e32 v112, 16, v110
	global_store_dwordx2 v[118:119], v[106:107], off offset:32
	v_lshlrev_b32_e32 v106, 16, v108
	v_and_b32_e32 v107, 0xffff0000, v108
	v_lshlrev_b32_e32 v108, 16, v109
	v_and_b32_e32 v109, 0xffff0000, v109
	v_and_b32_e32 v113, 0xffff0000, v110
	v_lshlrev_b32_e32 v110, 16, v111
	v_and_b32_e32 v111, 0xffff0000, v111
	v_pk_fma_f32 v[104:105], v[104:105], v[108:109], v[110:111]
	v_pk_fma_f32 v[102:103], v[102:103], v[106:107], v[112:113]
	v_or_b32_e32 v108, 32, v144
	v_cvt_pk_bf16_f32 v102, v102, v103
	v_cvt_pk_bf16_f32 v103, v104, v105
	v_mov_b32_e32 v104, v196
	v_mov_b32_e32 v105, v197
	v_mov_b32_e32 v106, v198
	v_mov_b32_e32 v107, v199
	v_ashrrev_i32_e32 v109, 31, v108
	v_mad_i64_i32 v[110:111], s[22:23], v108, s47, v[146:147]
	global_store_dwordx2 v[118:119], v[102:103], off offset:256
	v_lshl_add_u64 v[110:111], v[110:111], 0, v[142:143]
	v_add_co_u32_e32 v112, vcc, s48, v110
	s_nop 0
	v_lshlrev_b32_e32 v102, 16, v104
	v_and_b32_e32 v103, 0xffff0000, v104
	v_lshlrev_b32_e32 v114, 16, v106
	v_and_b32_e32 v115, 0xffff0000, v106
	v_pk_fma_f32 v[98:99], v[98:99], v[102:103], v[114:115]
	v_lshlrev_b64 v[102:103], 12, v[108:109]
	v_lshlrev_b32_e32 v104, 16, v105
	v_and_b32_e32 v105, 0xffff0000, v105
	v_lshlrev_b32_e32 v106, 16, v107
	v_and_b32_e32 v107, 0xffff0000, v107
	v_lshl_add_u64 v[102:103], s[8:9], 0, v[102:103]
	v_addc_co_u32_e32 v113, vcc, 0, v111, vcc
	v_pk_fma_f32 v[100:101], v[100:101], v[104:105], v[106:107]
	v_lshl_add_u64 v[102:103], v[102:103], 0, v[142:143]
	v_cvt_pk_bf16_f32 v98, v98, v99
	v_cvt_pk_bf16_f32 v99, v100, v101
	v_mov_b32_e32 v100, v200
	v_mov_b32_e32 v101, v201
	v_mov_b32_e32 v104, v202
	v_mov_b32_e32 v105, v203
	v_lshl_add_u64 v[106:107], v[110:111], 0, s[10:11]
	global_store_dwordx2 v[118:119], v[98:99], off offset:288
	s_nop 0
	v_lshlrev_b32_e32 v98, 16, v100
	v_and_b32_e32 v99, 0xffff0000, v100
	v_lshlrev_b32_e32 v100, 16, v101
	v_and_b32_e32 v101, 0xffff0000, v101
	v_lshlrev_b32_e32 v108, 16, v104
	v_and_b32_e32 v109, 0xffff0000, v104
	v_lshlrev_b32_e32 v104, 16, v105
	v_and_b32_e32 v105, 0xffff0000, v105
	v_pk_fma_f32 v[96:97], v[96:97], v[100:101], v[104:105]
	v_pk_fma_f32 v[94:95], v[94:95], v[98:99], v[108:109]
	s_nop 0
	v_cvt_pk_bf16_f32 v94, v94, v95
	v_cvt_pk_bf16_f32 v95, v96, v97
	v_mov_b32_e32 v96, v204
	v_mov_b32_e32 v97, v205
	v_mov_b32_e32 v98, v206
	v_mov_b32_e32 v99, v207
	s_nop 0
	v_lshlrev_b32_e32 v100, 16, v98
	global_store_dwordx2 v[102:103], v[94:95], off
	v_lshlrev_b32_e32 v94, 16, v96
	v_and_b32_e32 v95, 0xffff0000, v96
	v_lshlrev_b32_e32 v96, 16, v97
	v_and_b32_e32 v97, 0xffff0000, v97
	v_and_b32_e32 v101, 0xffff0000, v98
	v_lshlrev_b32_e32 v98, 16, v99
	v_and_b32_e32 v99, 0xffff0000, v99
	v_pk_fma_f32 v[92:93], v[92:93], v[96:97], v[98:99]
	v_pk_fma_f32 v[90:91], v[90:91], v[94:95], v[100:101]
	s_nop 0
	v_cvt_pk_bf16_f32 v90, v90, v91
	v_cvt_pk_bf16_f32 v91, v92, v93
	v_mov_b32_e32 v92, v208
	v_mov_b32_e32 v93, v209
	v_mov_b32_e32 v94, v210
	v_mov_b32_e32 v95, v211
	s_nop 0
	v_lshlrev_b32_e32 v96, 16, v94
	global_store_dwordx2 v[102:103], v[90:91], off offset:32
	v_lshlrev_b32_e32 v90, 16, v92
	v_and_b32_e32 v91, 0xffff0000, v92
	v_lshlrev_b32_e32 v92, 16, v93
	v_and_b32_e32 v93, 0xffff0000, v93
	v_and_b32_e32 v97, 0xffff0000, v94
	v_lshlrev_b32_e32 v94, 16, v95
	v_and_b32_e32 v95, 0xffff0000, v95
	v_pk_fma_f32 v[88:89], v[88:89], v[92:93], v[94:95]
	v_pk_fma_f32 v[86:87], v[86:87], v[90:91], v[96:97]
	v_or_b32_e32 v92, 48, v144
	v_cvt_pk_bf16_f32 v86, v86, v87
	v_cvt_pk_bf16_f32 v87, v88, v89
	v_mov_b32_e32 v88, v212
	v_mov_b32_e32 v89, v213
	v_mov_b32_e32 v90, v214
	v_mov_b32_e32 v91, v215
	v_ashrrev_i32_e32 v93, 31, v92
	v_mad_i64_i32 v[94:95], s[22:23], v92, s47, v[146:147]
	global_store_dwordx2 v[102:103], v[86:87], off offset:256
	v_lshl_add_u64 v[94:95], v[94:95], 0, v[142:143]
	v_add_co_u32_e32 v96, vcc, s48, v94
	s_nop 0
	v_lshlrev_b32_e32 v86, 16, v88
	v_and_b32_e32 v87, 0xffff0000, v88
	v_lshlrev_b32_e32 v98, 16, v90
	v_and_b32_e32 v99, 0xffff0000, v90
	v_pk_fma_f32 v[82:83], v[82:83], v[86:87], v[98:99]
	v_lshlrev_b64 v[86:87], 12, v[92:93]
	v_lshlrev_b32_e32 v88, 16, v89
	v_and_b32_e32 v89, 0xffff0000, v89
	v_lshlrev_b32_e32 v90, 16, v91
	v_and_b32_e32 v91, 0xffff0000, v91
	v_lshl_add_u64 v[86:87], s[8:9], 0, v[86:87]
	v_addc_co_u32_e32 v97, vcc, 0, v95, vcc
	v_pk_fma_f32 v[84:85], v[84:85], v[88:89], v[90:91]
	v_lshl_add_u64 v[86:87], v[86:87], 0, v[142:143]
	v_cvt_pk_bf16_f32 v82, v82, v83
	v_cvt_pk_bf16_f32 v83, v84, v85
	v_mov_b32_e32 v237, 0x1000
	v_mov_b32_e32 v236, 48
	v_mad_i64_i32 v[230:231], s[22:23], v236, s47, v[228:229]
	v_mad_i64_i32 v[234:235], s[22:23], v236, v237, v[232:233]
	global_load_dwordx2 v[168:169], v[230:231], off
	global_load_dwordx2 v[170:171], v[234:235], off
	global_load_dwordx2 v[172:173], v[230:231], off offset:32
	global_load_dwordx2 v[174:175], v[234:235], off offset:32
	global_load_dwordx2 v[176:177], v[230:231], off offset:256
	global_load_dwordx2 v[178:179], v[234:235], off offset:256
	global_load_dwordx2 v[180:181], v[230:231], off offset:288
	global_load_dwordx2 v[182:183], v[234:235], off offset:288
	v_mov_b32_e32 v236, 128
	v_mad_i64_i32 v[230:231], s[22:23], v236, s47, v[228:229]
	v_mad_i64_i32 v[234:235], s[22:23], v236, v237, v[232:233]
	global_load_dwordx2 v[184:185], v[230:231], off
	global_load_dwordx2 v[186:187], v[234:235], off
	global_load_dwordx2 v[188:189], v[230:231], off offset:32
	global_load_dwordx2 v[190:191], v[234:235], off offset:32
	global_load_dwordx2 v[192:193], v[230:231], off offset:256
	global_load_dwordx2 v[194:195], v[234:235], off offset:256
	global_load_dwordx2 v[196:197], v[230:231], off offset:288
	global_load_dwordx2 v[198:199], v[234:235], off offset:288
	v_mov_b32_e32 v236, 144
	v_mad_i64_i32 v[230:231], s[22:23], v236, s47, v[228:229]
	v_mad_i64_i32 v[234:235], s[22:23], v236, v237, v[232:233]
	global_load_dwordx2 v[200:201], v[230:231], off
	global_load_dwordx2 v[202:203], v[234:235], off
	global_load_dwordx2 v[204:205], v[230:231], off offset:32
	global_load_dwordx2 v[206:207], v[234:235], off offset:32
	global_load_dwordx2 v[208:209], v[230:231], off offset:256
	global_load_dwordx2 v[210:211], v[234:235], off offset:256
	global_load_dwordx2 v[212:213], v[230:231], off offset:288
	global_load_dwordx2 v[214:215], v[234:235], off offset:288
	s_waitcnt vmcnt(0)
	v_mov_b32_e32 v84, v168
	v_mov_b32_e32 v85, v169
	v_mov_b32_e32 v88, v170
	v_mov_b32_e32 v89, v171
	v_lshl_add_u64 v[90:91], v[94:95], 0, s[10:11]
	global_store_dwordx2 v[102:103], v[82:83], off offset:288
	s_nop 0
	v_lshlrev_b32_e32 v82, 16, v84
	v_and_b32_e32 v83, 0xffff0000, v84
	v_lshlrev_b32_e32 v84, 16, v85
	v_and_b32_e32 v85, 0xffff0000, v85
	v_lshlrev_b32_e32 v92, 16, v88
	v_and_b32_e32 v93, 0xffff0000, v88
	v_lshlrev_b32_e32 v88, 16, v89
	v_and_b32_e32 v89, 0xffff0000, v89
	v_pk_fma_f32 v[80:81], v[80:81], v[84:85], v[88:89]
	v_pk_fma_f32 v[78:79], v[78:79], v[82:83], v[92:93]
	s_nop 0
	v_cvt_pk_bf16_f32 v78, v78, v79
	v_cvt_pk_bf16_f32 v79, v80, v81
	v_mov_b32_e32 v80, v172
	v_mov_b32_e32 v81, v173
	v_mov_b32_e32 v82, v174
	v_mov_b32_e32 v83, v175
	s_nop 0
	v_lshlrev_b32_e32 v84, 16, v82
	global_store_dwordx2 v[86:87], v[78:79], off
	v_lshlrev_b32_e32 v78, 16, v80
	v_and_b32_e32 v79, 0xffff0000, v80
	v_lshlrev_b32_e32 v80, 16, v81
	v_and_b32_e32 v81, 0xffff0000, v81
	v_and_b32_e32 v85, 0xffff0000, v82
	v_lshlrev_b32_e32 v82, 16, v83
	v_and_b32_e32 v83, 0xffff0000, v83
	v_pk_fma_f32 v[76:77], v[76:77], v[80:81], v[82:83]
	v_pk_fma_f32 v[74:75], v[74:75], v[78:79], v[84:85]
	s_nop 0
	v_cvt_pk_bf16_f32 v74, v74, v75
	v_cvt_pk_bf16_f32 v75, v76, v77
	v_mov_b32_e32 v76, v176
	v_mov_b32_e32 v77, v177
	v_mov_b32_e32 v78, v178
	v_mov_b32_e32 v79, v179
	s_nop 0
	v_lshlrev_b32_e32 v80, 16, v78
	global_store_dwordx2 v[86:87], v[74:75], off offset:32
	v_lshlrev_b32_e32 v74, 16, v76
	v_and_b32_e32 v75, 0xffff0000, v76
	v_lshlrev_b32_e32 v76, 16, v77
	v_and_b32_e32 v77, 0xffff0000, v77
	v_and_b32_e32 v81, 0xffff0000, v78
	v_lshlrev_b32_e32 v78, 16, v79
	v_and_b32_e32 v79, 0xffff0000, v79
	v_pk_fma_f32 v[72:73], v[72:73], v[76:77], v[78:79]
	v_pk_fma_f32 v[70:71], v[70:71], v[74:75], v[80:81]
	v_add_u32_e32 v76, 0x80, v144
	v_cvt_pk_bf16_f32 v70, v70, v71
	v_cvt_pk_bf16_f32 v71, v72, v73
	v_mov_b32_e32 v72, v180
	v_mov_b32_e32 v73, v181
	v_mov_b32_e32 v74, v182
	v_mov_b32_e32 v75, v183
	v_ashrrev_i32_e32 v77, 31, v76
	v_mad_i64_i32 v[78:79], s[22:23], v76, s47, v[146:147]
	global_store_dwordx2 v[86:87], v[70:71], off offset:256
	v_lshl_add_u64 v[78:79], v[78:79], 0, v[142:143]
	v_add_co_u32_e32 v80, vcc, s48, v78
	s_nop 0
	v_lshlrev_b32_e32 v70, 16, v72
	v_and_b32_e32 v71, 0xffff0000, v72
	v_lshlrev_b32_e32 v82, 16, v74
	v_and_b32_e32 v83, 0xffff0000, v74
	v_pk_fma_f32 v[66:67], v[66:67], v[70:71], v[82:83]
	v_lshlrev_b64 v[70:71], 12, v[76:77]
	v_lshlrev_b32_e32 v72, 16, v73
	v_and_b32_e32 v73, 0xffff0000, v73
	v_lshlrev_b32_e32 v74, 16, v75
	v_and_b32_e32 v75, 0xffff0000, v75
	v_lshl_add_u64 v[70:71], s[8:9], 0, v[70:71]
	v_addc_co_u32_e32 v81, vcc, 0, v79, vcc
	v_pk_fma_f32 v[68:69], v[68:69], v[72:73], v[74:75]
	v_lshl_add_u64 v[70:71], v[70:71], 0, v[142:143]
	v_cvt_pk_bf16_f32 v66, v66, v67
	v_cvt_pk_bf16_f32 v67, v68, v69
	v_mov_b32_e32 v68, v184
	v_mov_b32_e32 v69, v185
	v_mov_b32_e32 v72, v186
	v_mov_b32_e32 v73, v187
	v_lshl_add_u64 v[74:75], v[78:79], 0, s[10:11]
	global_store_dwordx2 v[86:87], v[66:67], off offset:288
	s_nop 0
	v_lshlrev_b32_e32 v66, 16, v68
	v_and_b32_e32 v67, 0xffff0000, v68
	v_lshlrev_b32_e32 v68, 16, v69
	v_and_b32_e32 v69, 0xffff0000, v69
	v_lshlrev_b32_e32 v76, 16, v72
	v_and_b32_e32 v77, 0xffff0000, v72
	v_lshlrev_b32_e32 v72, 16, v73
	v_and_b32_e32 v73, 0xffff0000, v73
	v_pk_fma_f32 v[64:65], v[64:65], v[68:69], v[72:73]
	v_pk_fma_f32 v[62:63], v[62:63], v[66:67], v[76:77]
	s_nop 0
	v_cvt_pk_bf16_f32 v62, v62, v63
	v_cvt_pk_bf16_f32 v63, v64, v65
	v_mov_b32_e32 v64, v188
	v_mov_b32_e32 v65, v189
	v_mov_b32_e32 v66, v190
	v_mov_b32_e32 v67, v191
	s_nop 0
	v_lshlrev_b32_e32 v68, 16, v66
	global_store_dwordx2 v[70:71], v[62:63], off
	v_lshlrev_b32_e32 v62, 16, v64
	v_and_b32_e32 v63, 0xffff0000, v64
	v_lshlrev_b32_e32 v64, 16, v65
	v_and_b32_e32 v65, 0xffff0000, v65
	v_and_b32_e32 v69, 0xffff0000, v66
	v_lshlrev_b32_e32 v66, 16, v67
	v_and_b32_e32 v67, 0xffff0000, v67
	v_pk_fma_f32 v[60:61], v[60:61], v[64:65], v[66:67]
	v_pk_fma_f32 v[58:59], v[58:59], v[62:63], v[68:69]
	s_nop 0
	v_cvt_pk_bf16_f32 v58, v58, v59
	v_cvt_pk_bf16_f32 v59, v60, v61
	v_mov_b32_e32 v60, v192
	v_mov_b32_e32 v61, v193
	v_mov_b32_e32 v62, v194
	v_mov_b32_e32 v63, v195
	s_nop 0
	v_lshlrev_b32_e32 v64, 16, v62
	global_store_dwordx2 v[70:71], v[58:59], off offset:32
	v_lshlrev_b32_e32 v58, 16, v60
	v_and_b32_e32 v59, 0xffff0000, v60
	v_lshlrev_b32_e32 v60, 16, v61
	v_and_b32_e32 v61, 0xffff0000, v61
	v_and_b32_e32 v65, 0xffff0000, v62
	v_lshlrev_b32_e32 v62, 16, v63
	v_and_b32_e32 v63, 0xffff0000, v63
	v_pk_fma_f32 v[56:57], v[56:57], v[60:61], v[62:63]
	v_pk_fma_f32 v[54:55], v[54:55], v[58:59], v[64:65]
	v_add_u32_e32 v60, 0x90, v144
	v_cvt_pk_bf16_f32 v54, v54, v55
	v_cvt_pk_bf16_f32 v55, v56, v57
	v_mov_b32_e32 v56, v196
	v_mov_b32_e32 v57, v197
	v_mov_b32_e32 v58, v198
	v_mov_b32_e32 v59, v199
	v_ashrrev_i32_e32 v61, 31, v60
	v_mad_i64_i32 v[62:63], s[22:23], v60, s47, v[146:147]
	global_store_dwordx2 v[70:71], v[54:55], off offset:256
	v_lshl_add_u64 v[62:63], v[62:63], 0, v[142:143]
	v_add_co_u32_e32 v64, vcc, s48, v62
	s_nop 0
	v_lshlrev_b32_e32 v54, 16, v56
	v_and_b32_e32 v55, 0xffff0000, v56
	v_lshlrev_b32_e32 v66, 16, v58
	v_and_b32_e32 v67, 0xffff0000, v58
	v_pk_fma_f32 v[50:51], v[50:51], v[54:55], v[66:67]
	v_lshlrev_b64 v[54:55], 12, v[60:61]
	v_lshlrev_b32_e32 v56, 16, v57
	v_and_b32_e32 v57, 0xffff0000, v57
	v_lshlrev_b32_e32 v58, 16, v59
	v_and_b32_e32 v59, 0xffff0000, v59
	v_lshl_add_u64 v[54:55], s[8:9], 0, v[54:55]
	v_addc_co_u32_e32 v65, vcc, 0, v63, vcc
	v_pk_fma_f32 v[52:53], v[52:53], v[56:57], v[58:59]
	v_lshl_add_u64 v[54:55], v[54:55], 0, v[142:143]
	v_cvt_pk_bf16_f32 v50, v50, v51
	v_cvt_pk_bf16_f32 v51, v52, v53
	v_mov_b32_e32 v52, v200
	v_mov_b32_e32 v53, v201
	v_mov_b32_e32 v56, v202
	v_mov_b32_e32 v57, v203
	v_lshl_add_u64 v[58:59], v[62:63], 0, s[10:11]
	global_store_dwordx2 v[70:71], v[50:51], off offset:288
	s_nop 0
	v_lshlrev_b32_e32 v50, 16, v52
	v_and_b32_e32 v51, 0xffff0000, v52
	v_lshlrev_b32_e32 v52, 16, v53
	v_and_b32_e32 v53, 0xffff0000, v53
	v_lshlrev_b32_e32 v60, 16, v56
	v_and_b32_e32 v61, 0xffff0000, v56
	v_lshlrev_b32_e32 v56, 16, v57
	v_and_b32_e32 v57, 0xffff0000, v57
	v_pk_fma_f32 v[48:49], v[48:49], v[52:53], v[56:57]
	v_pk_fma_f32 v[46:47], v[46:47], v[50:51], v[60:61]
	s_nop 0
	v_cvt_pk_bf16_f32 v46, v46, v47
	v_cvt_pk_bf16_f32 v47, v48, v49
	v_mov_b32_e32 v48, v204
	v_mov_b32_e32 v49, v205
	v_mov_b32_e32 v50, v206
	v_mov_b32_e32 v51, v207
	s_nop 0
	v_lshlrev_b32_e32 v52, 16, v50
	global_store_dwordx2 v[54:55], v[46:47], off
	v_lshlrev_b32_e32 v46, 16, v48
	v_and_b32_e32 v47, 0xffff0000, v48
	v_lshlrev_b32_e32 v48, 16, v49
	v_and_b32_e32 v49, 0xffff0000, v49
	v_and_b32_e32 v53, 0xffff0000, v50
	v_lshlrev_b32_e32 v50, 16, v51
	v_and_b32_e32 v51, 0xffff0000, v51
	v_pk_fma_f32 v[44:45], v[44:45], v[48:49], v[50:51]
	v_pk_fma_f32 v[42:43], v[42:43], v[46:47], v[52:53]
	s_nop 0
	v_cvt_pk_bf16_f32 v42, v42, v43
	v_cvt_pk_bf16_f32 v43, v44, v45
	v_mov_b32_e32 v44, v208
	v_mov_b32_e32 v45, v209
	v_mov_b32_e32 v46, v210
	v_mov_b32_e32 v47, v211
	s_nop 0
	v_lshlrev_b32_e32 v48, 16, v46
	global_store_dwordx2 v[54:55], v[42:43], off offset:32
	v_lshlrev_b32_e32 v42, 16, v44
	v_and_b32_e32 v43, 0xffff0000, v44
	v_lshlrev_b32_e32 v44, 16, v45
	v_and_b32_e32 v45, 0xffff0000, v45
	v_and_b32_e32 v49, 0xffff0000, v46
	v_lshlrev_b32_e32 v46, 16, v47
	v_and_b32_e32 v47, 0xffff0000, v47
	v_pk_fma_f32 v[40:41], v[40:41], v[44:45], v[46:47]
	v_pk_fma_f32 v[38:39], v[38:39], v[42:43], v[48:49]
	v_add_u32_e32 v44, 0xa0, v144
	v_cvt_pk_bf16_f32 v38, v38, v39
	v_cvt_pk_bf16_f32 v39, v40, v41
	v_mov_b32_e32 v40, v212
	v_mov_b32_e32 v41, v213
	v_mov_b32_e32 v42, v214
	v_mov_b32_e32 v43, v215
	v_ashrrev_i32_e32 v45, 31, v44
	v_mad_i64_i32 v[46:47], s[22:23], v44, s47, v[146:147]
	global_store_dwordx2 v[54:55], v[38:39], off offset:256
	v_lshl_add_u64 v[46:47], v[46:47], 0, v[142:143]
	v_add_co_u32_e32 v48, vcc, s48, v46
	s_nop 0
	v_lshlrev_b32_e32 v38, 16, v40
	v_and_b32_e32 v39, 0xffff0000, v40
	v_lshlrev_b32_e32 v50, 16, v42
	v_and_b32_e32 v51, 0xffff0000, v42
	v_pk_fma_f32 v[34:35], v[34:35], v[38:39], v[50:51]
	v_lshlrev_b64 v[38:39], 12, v[44:45]
	v_lshlrev_b32_e32 v40, 16, v41
	v_and_b32_e32 v41, 0xffff0000, v41
	v_lshlrev_b32_e32 v42, 16, v43
	v_and_b32_e32 v43, 0xffff0000, v43
	v_lshl_add_u64 v[38:39], s[8:9], 0, v[38:39]
	v_addc_co_u32_e32 v49, vcc, 0, v47, vcc
	v_pk_fma_f32 v[36:37], v[36:37], v[40:41], v[42:43]
	v_lshl_add_u64 v[38:39], v[38:39], 0, v[142:143]
	v_cvt_pk_bf16_f32 v34, v34, v35
	v_cvt_pk_bf16_f32 v35, v36, v37
	v_mov_b32_e32 v237, 0x1000
	v_mov_b32_e32 v236, 160
	v_mad_i64_i32 v[230:231], s[22:23], v236, s47, v[228:229]
	v_mad_i64_i32 v[234:235], s[22:23], v236, v237, v[232:233]
	global_load_dwordx2 v[168:169], v[230:231], off
	global_load_dwordx2 v[170:171], v[234:235], off
	global_load_dwordx2 v[172:173], v[230:231], off offset:32
	global_load_dwordx2 v[174:175], v[234:235], off offset:32
	global_load_dwordx2 v[176:177], v[230:231], off offset:256
	global_load_dwordx2 v[178:179], v[234:235], off offset:256
	global_load_dwordx2 v[180:181], v[230:231], off offset:288
	global_load_dwordx2 v[182:183], v[234:235], off offset:288
	v_mov_b32_e32 v236, 176
	v_mad_i64_i32 v[230:231], s[22:23], v236, s47, v[228:229]
	v_mad_i64_i32 v[234:235], s[22:23], v236, v237, v[232:233]
	global_load_dwordx2 v[184:185], v[230:231], off
	global_load_dwordx2 v[186:187], v[234:235], off
	global_load_dwordx2 v[188:189], v[230:231], off offset:32
	global_load_dwordx2 v[190:191], v[234:235], off offset:32
	global_load_dwordx2 v[192:193], v[230:231], off offset:256
	global_load_dwordx2 v[194:195], v[234:235], off offset:256
	global_load_dwordx2 v[196:197], v[230:231], off offset:288
	global_load_dwordx2 v[198:199], v[234:235], off offset:288
	s_waitcnt vmcnt(0)
	v_mov_b32_e32 v36, v168
	v_mov_b32_e32 v37, v169
	v_mov_b32_e32 v40, v170
	v_mov_b32_e32 v41, v171
	v_lshl_add_u64 v[42:43], v[46:47], 0, s[10:11]
	global_store_dwordx2 v[54:55], v[34:35], off offset:288
	s_nop 0
	v_lshlrev_b32_e32 v34, 16, v36
	v_and_b32_e32 v35, 0xffff0000, v36
	v_lshlrev_b32_e32 v36, 16, v37
	v_and_b32_e32 v37, 0xffff0000, v37
	v_lshlrev_b32_e32 v44, 16, v40
	v_and_b32_e32 v45, 0xffff0000, v40
	v_lshlrev_b32_e32 v40, 16, v41
	v_and_b32_e32 v41, 0xffff0000, v41
	v_pk_fma_f32 v[32:33], v[32:33], v[36:37], v[40:41]
	v_pk_fma_f32 v[30:31], v[30:31], v[34:35], v[44:45]
	s_nop 0
	v_cvt_pk_bf16_f32 v30, v30, v31
	v_cvt_pk_bf16_f32 v31, v32, v33
	v_mov_b32_e32 v32, v172
	v_mov_b32_e32 v33, v173
	v_mov_b32_e32 v34, v174
	v_mov_b32_e32 v35, v175
	s_nop 0
	v_lshlrev_b32_e32 v36, 16, v34
	global_store_dwordx2 v[38:39], v[30:31], off
	v_lshlrev_b32_e32 v30, 16, v32
	v_and_b32_e32 v31, 0xffff0000, v32
	v_lshlrev_b32_e32 v32, 16, v33
	v_and_b32_e32 v33, 0xffff0000, v33
	v_and_b32_e32 v37, 0xffff0000, v34
	v_lshlrev_b32_e32 v34, 16, v35
	v_and_b32_e32 v35, 0xffff0000, v35
	v_pk_fma_f32 v[28:29], v[28:29], v[32:33], v[34:35]
	v_pk_fma_f32 v[26:27], v[26:27], v[30:31], v[36:37]
	s_nop 0
	v_cvt_pk_bf16_f32 v26, v26, v27
	v_cvt_pk_bf16_f32 v27, v28, v29
	v_mov_b32_e32 v28, v176
	v_mov_b32_e32 v29, v177
	v_mov_b32_e32 v30, v178
	v_mov_b32_e32 v31, v179
	s_nop 0
	v_lshlrev_b32_e32 v32, 16, v30
	global_store_dwordx2 v[38:39], v[26:27], off offset:32
	v_lshlrev_b32_e32 v26, 16, v28
	v_and_b32_e32 v27, 0xffff0000, v28
	v_lshlrev_b32_e32 v28, 16, v29
	v_and_b32_e32 v29, 0xffff0000, v29
	v_and_b32_e32 v33, 0xffff0000, v30
	v_lshlrev_b32_e32 v30, 16, v31
	v_and_b32_e32 v31, 0xffff0000, v31
	v_pk_fma_f32 v[24:25], v[24:25], v[28:29], v[30:31]
	v_pk_fma_f32 v[22:23], v[22:23], v[26:27], v[32:33]
	v_add_u32_e32 v28, 0xb0, v144
	v_cvt_pk_bf16_f32 v22, v22, v23
	v_cvt_pk_bf16_f32 v23, v24, v25
	v_mov_b32_e32 v24, v180
	v_mov_b32_e32 v25, v181
	v_mov_b32_e32 v26, v182
	v_mov_b32_e32 v27, v183
	v_ashrrev_i32_e32 v29, 31, v28
	v_mad_i64_i32 v[30:31], s[22:23], v28, s47, v[146:147]
	global_store_dwordx2 v[38:39], v[22:23], off offset:256
	v_lshl_add_u64 v[30:31], v[30:31], 0, v[142:143]
	v_add_co_u32_e32 v32, vcc, s48, v30
	s_mov_b64 s[22:23], s[16:17]
	s_nop 0
	v_addc_co_u32_e32 v33, vcc, 0, v31, vcc
	s_and_b64 vcc, exec, s[0:1]
	s_nop 0
	v_lshlrev_b32_e32 v22, 16, v24
	v_and_b32_e32 v23, 0xffff0000, v24
	v_lshlrev_b32_e32 v34, 16, v26
	v_and_b32_e32 v35, 0xffff0000, v26
	v_pk_fma_f32 v[18:19], v[18:19], v[22:23], v[34:35]
	v_lshlrev_b64 v[22:23], 12, v[28:29]
	v_lshlrev_b32_e32 v24, 16, v25
	v_and_b32_e32 v25, 0xffff0000, v25
	v_lshlrev_b32_e32 v26, 16, v27
	v_and_b32_e32 v27, 0xffff0000, v27
	v_lshl_add_u64 v[22:23], s[8:9], 0, v[22:23]
	v_pk_fma_f32 v[20:21], v[20:21], v[24:25], v[26:27]
	v_lshl_add_u64 v[22:23], v[22:23], 0, v[142:143]
	v_cvt_pk_bf16_f32 v18, v18, v19
	v_cvt_pk_bf16_f32 v19, v20, v21
	v_mov_b32_e32 v20, v184
	v_mov_b32_e32 v21, v185
	v_mov_b32_e32 v24, v186
	v_mov_b32_e32 v25, v187
	v_lshl_add_u64 v[26:27], v[30:31], 0, s[10:11]
	global_store_dwordx2 v[38:39], v[18:19], off offset:288
	s_nop 0
	v_lshlrev_b32_e32 v18, 16, v20
	v_and_b32_e32 v19, 0xffff0000, v20
	v_lshlrev_b32_e32 v20, 16, v21
	v_and_b32_e32 v21, 0xffff0000, v21
	v_lshlrev_b32_e32 v28, 16, v24
	v_and_b32_e32 v29, 0xffff0000, v24
	v_lshlrev_b32_e32 v24, 16, v25
	v_and_b32_e32 v25, 0xffff0000, v25
	v_pk_fma_f32 v[16:17], v[16:17], v[20:21], v[24:25]
	v_pk_fma_f32 v[14:15], v[14:15], v[18:19], v[28:29]
	s_nop 0
	v_cvt_pk_bf16_f32 v14, v14, v15
	v_cvt_pk_bf16_f32 v15, v16, v17
	v_mov_b32_e32 v16, v188
	v_mov_b32_e32 v17, v189
	v_mov_b32_e32 v18, v190
	v_mov_b32_e32 v19, v191
	s_nop 0
	v_lshlrev_b32_e32 v20, 16, v18
	global_store_dwordx2 v[22:23], v[14:15], off
	v_lshlrev_b32_e32 v14, 16, v16
	v_and_b32_e32 v15, 0xffff0000, v16
	v_lshlrev_b32_e32 v16, 16, v17
	v_and_b32_e32 v17, 0xffff0000, v17
	v_and_b32_e32 v21, 0xffff0000, v18
	v_lshlrev_b32_e32 v18, 16, v19
	v_and_b32_e32 v19, 0xffff0000, v19
	v_pk_fma_f32 v[12:13], v[12:13], v[16:17], v[18:19]
	v_pk_fma_f32 v[10:11], v[10:11], v[14:15], v[20:21]
	s_nop 0
	v_cvt_pk_bf16_f32 v10, v10, v11
	v_cvt_pk_bf16_f32 v11, v12, v13
	v_mov_b32_e32 v12, v192
	v_mov_b32_e32 v13, v193
	v_mov_b32_e32 v14, v194
	v_mov_b32_e32 v15, v195
	s_nop 0
	v_lshlrev_b32_e32 v16, 16, v14
	global_store_dwordx2 v[22:23], v[10:11], off offset:32
	v_lshlrev_b32_e32 v10, 16, v12
	v_and_b32_e32 v11, 0xffff0000, v12
	v_lshlrev_b32_e32 v12, 16, v13
	v_and_b32_e32 v13, 0xffff0000, v13
	v_and_b32_e32 v17, 0xffff0000, v14
	v_lshlrev_b32_e32 v14, 16, v15
	v_and_b32_e32 v15, 0xffff0000, v15
	v_pk_fma_f32 v[8:9], v[8:9], v[12:13], v[14:15]
	v_pk_fma_f32 v[6:7], v[6:7], v[10:11], v[16:17]
	s_nop 0
	v_cvt_pk_bf16_f32 v6, v6, v7
	v_cvt_pk_bf16_f32 v7, v8, v9
	v_mov_b32_e32 v8, v196
	v_mov_b32_e32 v9, v197
	v_mov_b32_e32 v10, v198
	v_mov_b32_e32 v11, v199
	s_nop 0
	v_lshlrev_b32_e32 v12, 16, v10
	global_store_dwordx2 v[22:23], v[6:7], off offset:256
	v_lshlrev_b32_e32 v6, 16, v8
	v_and_b32_e32 v7, 0xffff0000, v8
	v_and_b32_e32 v13, 0xffff0000, v10
	v_lshlrev_b32_e32 v8, 16, v9
	v_and_b32_e32 v9, 0xffff0000, v9
	v_lshlrev_b32_e32 v10, 16, v11
	v_and_b32_e32 v11, 0xffff0000, v11
	v_pk_fma_f32 v[2:3], v[2:3], v[6:7], v[12:13]
	v_pk_fma_f32 v[4:5], v[4:5], v[8:9], v[10:11]
	v_cvt_pk_bf16_f32 v2, v2, v3
	s_nop 0
	v_cvt_pk_bf16_f32 v3, v4, v5
	global_store_dwordx2 v[22:23], v[2:3], off offset:288
	s_cbranch_vccz .LBB0_3252
	s_waitcnt vmcnt(0)
	s_cmpk_gt_u32 s28, 0xff
	s_cbranch_scc1 .LBB0_3259
	s_barrier

.LBB0_3261:
	s_cmp_gt_i32 s55, 19
	s_cselect_b64 s[0:1], -1, 0
	s_and_b64 s[2:3], s[4:5], s[0:1]
	s_andn2_b64 vcc, exec, s[2:3]
	s_cbranch_vccnz .LBB0_3311
	s_waitcnt vmcnt(0)
	s_barrier
	s_setprio 0
	s_mov_b64 s[2:3], exec
	v_readlane_b32 s4, v250, 5
	v_readlane_b32 s5, v250, 6
	s_and_b64 s[4:5], s[2:3], s[4:5]
	s_mov_b64 exec, s[4:5]
	s_cbranch_execz .LBB0_3310
	s_add_i32 s4, 0, 0x27ff0
	v_mov_b32_e32 v1, s4
	s_waitcnt vmcnt(0) expcnt(0) lgkmcnt(0)
	ds_read_b32 v3, v1
	s_add_i32 s4, 0, 0x27ff4
	v_mov_b32_e32 v1, s4
	ds_read_b32 v1, v1
	s_waitcnt lgkmcnt(1)
	v_cmp_ne_u32_e32 vcc, 0, v3
	s_cbranch_vccnz .LBB0_3278
	v_readlane_b32 s4, v250, 2
	v_readlane_b32 s5, v250, 3
	s_load_dwordx2 s[8:9], s[4:5], 0x4
	s_add_u32 s4, s52, 0x1000
	s_addc_u32 s5, s53, 0
	s_add_u32 s6, s52, 0x1100
	s_addc_u32 s7, s53, 0
	v_readlane_b32 s10, v250, 1
	s_waitcnt lgkmcnt(0)
	s_mul_i32 s18, s8, s10
	s_add_u32 s8, s52, 0x1200
	s_mul_i32 s18, s18, s9
	s_addc_u32 s9, s53, 0
	s_add_u32 s10, s52, 0x1300
	s_addc_u32 s11, s53, 0
	s_mov_b32 s19, 1
	v_mov_b32_e32 v17, 0
	s_branch .LBB0_3266

.LBB0_3311:
	s_cmp_lt_i32 s54, 20
	s_cselect_b64 s[2:3], -1, 0
	s_and_b64 s[0:1], s[2:3], s[0:1]
	s_andn2_b64 vcc, exec, s[0:1]
	s_cbranch_vccnz .LBB0_3325
	v_mov_b32_e32 v1, v0
	s_waitcnt vmcnt(11)
	v_mov_b32_e32 v2, v248
	v_readlane_b32 s33, v250, 0
	v_readlane_b32 s0, v250, 39
	v_readlane_b32 s40, v250, 1
	s_mov_b64 s[4:5], s[52:53]
	s_mov_b64 s[0:1], s[90:91]
	s_cmpk_gt_i32 s33, 0x1ff
	v_readfirstlane_b32 s41, v0
	s_barrier
	s_cbranch_scc1 .LBB0_3324
	s_add_u32 s42, s4, 0x2ab40000
	s_addc_u32 s43, s5, 0
	v_lshlrev_b32_e32 v1, 4, v0
	s_add_u32 s44, s4, 0x16140000
	s_waitcnt vmcnt(9)
	v_or_b32_e32 v10, 0x2000, v1
	s_addc_u32 s45, s5, 0
	v_lshrrev_b32_e32 v2, 7, v10
	v_bfe_u32 v13, v0, 2, 4
	s_movk_i32 s0, 0x70
	s_ashr_i32 s47, s33, 31
	v_and_or_b32 v2, v2, s0, v13
	s_lshr_b32 s0, s47, 29
	s_add_i32 s0, s33, s0
	s_ashr_i32 s7, s0, 3
	s_and_b32 s0, s0, -8
	s_sub_i32 s0, s33, s0
	s_lshr_b32 s8, s0, 31
	s_or_b32 s8, s8, 64
	s_mul_i32 s0, s8, s0
	s_add_i32 s0, s0, s7
	s_ashr_i32 s7, s0, 31
	s_lshr_b32 s7, s7, 26
	s_add_i32 s7, s0, s7
	s_ashr_i32 s8, s7, 6
	s_lshl_b32 s10, s8, 3
	s_sub_i32 s8, 64, s10
	s_min_u32 s11, s8, 8
	s_andn2_b32 s7, s7, 63
	v_and_b32_e32 v3, 32, v0
	s_sub_i32 s7, s0, s7
	v_cvt_f32_ubyte0_e32 v4, s11
	v_bitop3_b32 v11, v1, v3, 48 bitop3:0x6c
	v_and_b32_e32 v12, 64, v0
	v_cvt_f32_i32_e32 v3, s7
	v_rcp_iflag_f32_e32 v5, v4
	v_or_b32_e32 v1, v11, v12
	v_lshl_or_b32 v130, v2, 12, v1
	v_lshrrev_b32_e32 v2, 3, v0
	v_and_or_b32 v2, v2, 48, v13
	v_lshl_or_b32 v132, v2, 12, v1
	v_mul_f32_e32 v1, v3, v5
	v_trunc_f32_e32 v1, v1
	v_fma_f32 v2, -v1, v4, v3
	v_cvt_i32_f32_e32 v1, v1
	s_lshr_b32 s6, s41, 6
	s_ashr_i32 s0, s7, 30
	s_lshr_b32 s1, s41, 8
	s_lshl_b32 s46, s6, 10
	s_or_b32 s0, s0, 1
	v_cmp_ge_f32_e64 s[8:9], |v2|, v4
	s_and_b64 s[8:9], s[8:9], exec
	s_cselect_b32 s0, s0, 0
	v_readfirstlane_b32 s8, v1
	s_add_i32 s0, s8, s0
	s_mul_i32 s8, s0, s11
	s_sub_i32 s7, s7, s8
	s_sext_i32_i8 s7, s7
	s_add_i32 s30, s10, s7
	s_ashr_i32 s31, s30, 31
	s_lshl_b64 s[8:9], s[30:31], 20
	s_add_u32 s34, s42, s8
	s_addc_u32 s35, s43, s9
	s_bfe_i64 s[8:9], s[0:1], 0x80000
	s_lshl_b64 s[8:9], s[8:9], 20
	s_add_u32 s36, s44, s8
	s_addc_u32 s37, s45, s9
	s_add_i32 s31, s46, 0
	s_add_i32 m0, s31, 0x10000
	s_add_i32 s48, s31, 0x2000
	global_load_lds_dwordx4 v132, s[36:37]
	s_add_i32 m0, s31, 0x12000
	s_add_u32 s8, s36, 0x80000
	global_load_lds_dwordx4 v130, s[36:37]
	s_mov_b32 m0, s31
	s_addc_u32 s9, s37, 0
	global_load_lds_dwordx4 v132, s[34:35]
	s_mov_b32 m0, s48
	v_mov_b32_e32 v135, 0
	global_load_lds_dwordx4 v130, s[34:35]
	s_add_i32 m0, s31, 0x14000
	v_mov_b32_e32 v133, v135
	global_load_lds_dwordx4 v132, s[8:9]
	s_add_i32 m0, s31, 0x16000
	v_mov_b32_e32 v131, v135
	global_load_lds_dwordx4 v130, s[8:9]
	s_add_u32 s8, s34, 0x80000
	s_addc_u32 s9, s35, 0
	s_add_i32 s49, s31, 0x4000
	s_mov_b32 m0, s49
	s_add_i32 s50, s31, 0x6000
	global_load_lds_dwordx4 v132, s[8:9]
	s_mov_b32 m0, s50
	s_mov_b32 s51, 0
	global_load_lds_dwordx4 v130, s[8:9]
	v_lshl_add_u64 v[8:9], s[36:37], 0, v[132:133]
	v_lshl_add_u64 v[6:7], s[36:37], 0, v[130:131]
	v_lshl_add_u64 v[4:5], s[34:35], 0, v[132:133]
	s_setprio 1
	s_cmp_lg_u32 s1, 1
	v_lshl_add_u64 v[2:3], s[34:35], 0, v[130:131]
	s_cbranch_scc1 .LBB0_3315
	s_barrier
	s_setprio 0

.LBB0_3319:
	ds_read_b128 v[144:147], v152
	ds_read_b128 v[158:161], v152 offset:1024
	ds_read_b128 v[162:165], v152 offset:2048
	ds_read_b128 v[166:169], v152 offset:3072
	s_add_u32 s36, s34, 0xfff80080
	s_addc_u32 s37, s35, -1
	s_cmp_eq_u32 s69, 28
	s_cselect_b32 s39, s25, s37
	s_cselect_b32 s38, s65, s36
	s_cselect_b32 s37, s23, s68
	s_cselect_b32 s36, s66, s67
	v_lshl_add_u64 v[148:149], s[34:35], 0, v[136:137]
	s_add_i32 m0, s31, 0xc000
	ds_read_b128 v[170:173], v153
	ds_read_b128 v[174:177], v153 offset:1024
	ds_read_b128 v[178:181], v153 offset:2048
	ds_read_b128 v[182:185], v153 offset:3072
	ds_read_b128 v[186:189], v153 offset:4096
	ds_read_b128 v[190:193], v153 offset:5120
	ds_read_b128 v[194:197], v153 offset:6144
	ds_read_b128 v[198:201], v153 offset:7168
	global_load_lds_dwordx4 v[148:149], off
	v_lshl_add_u64 v[148:149], s[34:35], 0, v[138:139]
	s_add_i32 m0, s31, 0xe000
	s_nop 0
	global_load_lds_dwordx4 v[148:149], off
	s_waitcnt lgkmcnt(8)
	s_barrier
	s_waitcnt lgkmcnt(0)
	s_waitcnt lgkmcnt(0)
	v_mfma_f32_16x16x32_bf16 v[126:129], v[144:147], v[170:173], v[126:129]
	v_mfma_f32_16x16x32_bf16 v[122:125], v[162:165], v[170:173], v[122:125]
	v_mfma_f32_16x16x32_bf16 v[110:113], v[144:147], v[178:181], v[110:113]
	v_mfma_f32_16x16x32_bf16 v[106:109], v[162:165], v[178:181], v[106:109]
	v_mfma_f32_16x16x32_bf16 v[94:97], v[144:147], v[186:189], v[94:97]
	v_mfma_f32_16x16x32_bf16 v[90:93], v[162:165], v[186:189], v[90:93]
	v_mfma_f32_16x16x32_bf16 v[78:81], v[144:147], v[194:197], v[78:81]
	v_mfma_f32_16x16x32_bf16 v[74:77], v[162:165], v[194:197], v[74:77]
	v_mfma_f32_16x16x32_bf16 v[126:129], v[158:161], v[174:177], v[126:129]
	v_mfma_f32_16x16x32_bf16 v[122:125], v[166:169], v[174:177], v[122:125]
	v_mfma_f32_16x16x32_bf16 v[110:113], v[158:161], v[182:185], v[110:113]
	v_mfma_f32_16x16x32_bf16 v[106:109], v[166:169], v[182:185], v[106:109]
	v_mfma_f32_16x16x32_bf16 v[94:97], v[158:161], v[190:193], v[94:97]
	v_mfma_f32_16x16x32_bf16 v[90:93], v[166:169], v[190:193], v[90:93]
	v_mfma_f32_16x16x32_bf16 v[78:81], v[158:161], v[198:201], v[78:81]
	v_mfma_f32_16x16x32_bf16 v[74:77], v[166:169], v[198:201], v[74:77]
	s_barrier
	s_add_i32 s70, s55, s46
	v_lshl_add_u64 v[148:149], s[36:37], 0, v[132:133]
	s_mov_b32 m0, s70
	ds_read_b128 v[202:205], v154
	ds_read_b128 v[206:209], v154 offset:1024
	ds_read_b128 v[210:213], v154 offset:2048
	ds_read_b128 v[214:217], v154 offset:3072
	global_load_lds_dwordx4 v[148:149], off
	v_lshl_add_u64 v[218:219], s[36:37], 0, v[130:131]
	s_add_i32 m0, s70, 0x2000
	s_nop 0
	global_load_lds_dwordx4 v[218:219], off
	s_barrier
	s_waitcnt lgkmcnt(0)
	s_waitcnt lgkmcnt(0)
	v_mfma_f32_16x16x32_bf16 v[118:121], v[202:205], v[170:173], v[118:121]
	v_mfma_f32_16x16x32_bf16 v[114:117], v[210:213], v[170:173], v[114:117]
	v_mfma_f32_16x16x32_bf16 v[102:105], v[202:205], v[178:181], v[102:105]
	v_mfma_f32_16x16x32_bf16 v[98:101], v[210:213], v[178:181], v[98:101]
	v_mfma_f32_16x16x32_bf16 v[86:89], v[202:205], v[186:189], v[86:89]
	v_mfma_f32_16x16x32_bf16 v[82:85], v[210:213], v[186:189], v[82:85]
	v_mfma_f32_16x16x32_bf16 v[70:73], v[202:205], v[194:197], v[70:73]
	v_mfma_f32_16x16x32_bf16 v[66:69], v[210:213], v[194:197], v[66:69]
	v_mfma_f32_16x16x32_bf16 v[118:121], v[206:209], v[174:177], v[118:121]
	v_mfma_f32_16x16x32_bf16 v[114:117], v[214:217], v[174:177], v[114:117]
	v_mfma_f32_16x16x32_bf16 v[102:105], v[206:209], v[182:185], v[102:105]
	v_mfma_f32_16x16x32_bf16 v[98:101], v[214:217], v[182:185], v[98:101]
	v_mfma_f32_16x16x32_bf16 v[86:89], v[206:209], v[190:193], v[86:89]
	v_mfma_f32_16x16x32_bf16 v[82:85], v[214:217], v[190:193], v[82:85]
	v_mfma_f32_16x16x32_bf16 v[70:73], v[206:209], v[198:201], v[70:73]
	v_mfma_f32_16x16x32_bf16 v[66:69], v[214:217], v[198:201], v[66:69]
	s_mov_b32 m0, s31
	v_lshl_add_u64 v[220:221], s[38:39], 0, v[132:133]
	s_barrier
	ds_read_b128 v[170:173], v153 offset:16384
	ds_read_b128 v[174:177], v153 offset:17408
	ds_read_b128 v[178:181], v153 offset:18432
	ds_read_b128 v[182:185], v153 offset:19456
	ds_read_b128 v[186:189], v153 offset:20480
	ds_read_b128 v[190:193], v153 offset:21504
	ds_read_b128 v[194:197], v153 offset:22528
	ds_read_b128 v[198:201], v153 offset:23552
	global_load_lds_dwordx4 v[220:221], off
	v_lshl_add_u64 v[222:223], s[38:39], 0, v[130:131]
	s_mov_b32 m0, s48
	s_nop 0
	global_load_lds_dwordx4 v[222:223], off
	s_barrier
	s_waitcnt lgkmcnt(0)
	s_waitcnt lgkmcnt(0)
	v_mfma_f32_16x16x32_bf16 v[62:65], v[144:147], v[170:173], v[62:65]
	v_mfma_f32_16x16x32_bf16 v[58:61], v[162:165], v[170:173], v[58:61]
	v_mfma_f32_16x16x32_bf16 v[46:49], v[144:147], v[178:181], v[46:49]
	v_mfma_f32_16x16x32_bf16 v[42:45], v[162:165], v[178:181], v[42:45]
	v_mfma_f32_16x16x32_bf16 v[30:33], v[144:147], v[186:189], v[30:33]
	v_mfma_f32_16x16x32_bf16 v[26:29], v[162:165], v[186:189], v[26:29]
	v_mfma_f32_16x16x32_bf16 v[22:25], v[144:147], v[194:197], v[22:25]
	v_mfma_f32_16x16x32_bf16 v[14:17], v[162:165], v[194:197], v[14:17]
	v_mfma_f32_16x16x32_bf16 v[62:65], v[158:161], v[174:177], v[62:65]
	v_mfma_f32_16x16x32_bf16 v[58:61], v[166:169], v[174:177], v[58:61]
	v_mfma_f32_16x16x32_bf16 v[46:49], v[158:161], v[182:185], v[46:49]
	v_mfma_f32_16x16x32_bf16 v[42:45], v[166:169], v[182:185], v[42:45]
	v_mfma_f32_16x16x32_bf16 v[30:33], v[158:161], v[190:193], v[30:33]
	v_mfma_f32_16x16x32_bf16 v[26:29], v[166:169], v[190:193], v[26:29]
	v_mfma_f32_16x16x32_bf16 v[22:25], v[158:161], v[198:201], v[22:25]
	v_mfma_f32_16x16x32_bf16 v[14:17], v[166:169], v[198:201], v[14:17]
	s_barrier
	s_add_u32 s70, s36, 0x80000
	s_addc_u32 s71, s37, 0
	s_add_i32 s72, s56, s46
	v_lshl_add_u64 v[144:145], s[70:71], 0, v[132:133]
	s_mov_b32 m0, s72
	s_nop 0
	global_load_lds_dwordx4 v[144:145], off
	v_lshl_add_u64 v[144:145], s[70:71], 0, v[130:131]
	s_add_i32 m0, s72, 0x2000
	s_nop 0
	global_load_lds_dwordx4 v[144:145], off
	s_waitcnt vmcnt(6)
	s_barrier
	v_mfma_f32_16x16x32_bf16 v[54:57], v[202:205], v[170:173], v[54:57]
	v_mfma_f32_16x16x32_bf16 v[50:53], v[210:213], v[170:173], v[50:53]
	v_mfma_f32_16x16x32_bf16 v[38:41], v[202:205], v[178:181], v[38:41]
	v_mfma_f32_16x16x32_bf16 v[34:37], v[210:213], v[178:181], v[34:37]
	v_mfma_f32_16x16x32_bf16 v[18:21], v[202:205], v[186:189], v[18:21]
	v_mfma_f32_16x16x32_bf16 v[10:13], v[210:213], v[186:189], v[10:13]
	v_mfma_f32_16x16x32_bf16 v[6:9], v[202:205], v[194:197], v[6:9]
	v_mfma_f32_16x16x32_bf16 v[2:5], v[210:213], v[194:197], v[2:5]
	v_mfma_f32_16x16x32_bf16 v[54:57], v[206:209], v[174:177], v[54:57]
	v_mfma_f32_16x16x32_bf16 v[50:53], v[214:217], v[174:177], v[50:53]
	v_mfma_f32_16x16x32_bf16 v[38:41], v[206:209], v[182:185], v[38:41]
	v_mfma_f32_16x16x32_bf16 v[34:37], v[214:217], v[182:185], v[34:37]
	v_mfma_f32_16x16x32_bf16 v[18:21], v[206:209], v[190:193], v[18:21]
	v_mfma_f32_16x16x32_bf16 v[10:13], v[214:217], v[190:193], v[10:13]
	v_mfma_f32_16x16x32_bf16 v[6:9], v[206:209], v[198:201], v[6:9]
	v_mfma_f32_16x16x32_bf16 v[2:5], v[214:217], v[198:201], v[2:5]
	s_add_i32 s70, 0, 0x18000
	v_add_u32_e32 v134, s70, v150
	s_barrier
	ds_read_b128 v[144:147], v134
	ds_read_b128 v[158:161], v134 offset:1024
	ds_read_b128 v[162:165], v134 offset:2048
	ds_read_b128 v[166:169], v134 offset:3072
	s_add_u32 s38, s38, 0x80000
	s_addc_u32 s39, s39, 0
	s_mov_b32 m0, s49
	v_lshl_add_u64 v[202:203], s[38:39], 0, v[132:133]
	ds_read_b128 v[170:173], v153 offset:32768
	ds_read_b128 v[174:177], v153 offset:33792
	ds_read_b128 v[178:181], v153 offset:34816
	ds_read_b128 v[182:185], v153 offset:35840
	ds_read_b128 v[186:189], v153 offset:36864
	ds_read_b128 v[190:193], v153 offset:37888
	ds_read_b128 v[194:197], v153 offset:38912
	ds_read_b128 v[198:201], v153 offset:39936
	global_load_lds_dwordx4 v[202:203], off
	v_lshl_add_u64 v[202:203], s[38:39], 0, v[130:131]
	s_mov_b32 m0, s50
	s_nop 0
	global_load_lds_dwordx4 v[202:203], off
	s_waitcnt lgkmcnt(8)
	s_barrier
	s_waitcnt lgkmcnt(0)
	s_waitcnt lgkmcnt(0)
	v_mfma_f32_16x16x32_bf16 v[126:129], v[144:147], v[170:173], v[126:129]
	v_mfma_f32_16x16x32_bf16 v[122:125], v[162:165], v[170:173], v[122:125]
	v_mfma_f32_16x16x32_bf16 v[110:113], v[144:147], v[178:181], v[110:113]
	v_mfma_f32_16x16x32_bf16 v[106:109], v[162:165], v[178:181], v[106:109]
	v_mfma_f32_16x16x32_bf16 v[94:97], v[144:147], v[186:189], v[94:97]
	v_mfma_f32_16x16x32_bf16 v[90:93], v[162:165], v[186:189], v[90:93]
	v_mfma_f32_16x16x32_bf16 v[78:81], v[144:147], v[194:197], v[78:81]
	v_mfma_f32_16x16x32_bf16 v[74:77], v[162:165], v[194:197], v[74:77]
	v_mfma_f32_16x16x32_bf16 v[126:129], v[158:161], v[174:177], v[126:129]
	v_mfma_f32_16x16x32_bf16 v[122:125], v[166:169], v[174:177], v[122:125]
	v_mfma_f32_16x16x32_bf16 v[110:113], v[158:161], v[182:185], v[110:113]
	v_mfma_f32_16x16x32_bf16 v[106:109], v[166:169], v[182:185], v[106:109]
	v_mfma_f32_16x16x32_bf16 v[94:97], v[158:161], v[190:193], v[94:97]
	v_mfma_f32_16x16x32_bf16 v[90:93], v[166:169], v[190:193], v[90:93]
	v_mfma_f32_16x16x32_bf16 v[78:81], v[158:161], v[198:201], v[78:81]
	v_mfma_f32_16x16x32_bf16 v[74:77], v[166:169], v[198:201], v[74:77]
	s_barrier
	s_add_i32 s38, 0, 0x1c000
	s_add_i32 s39, s70, s46
	v_add_u32_e32 v134, s38, v150
	v_lshl_add_u64 v[148:149], v[148:149], 0, s[6:7]
	s_mov_b32 m0, s39
	ds_read_b128 v[202:205], v134
	ds_read_b128 v[206:209], v134 offset:1024
	ds_read_b128 v[210:213], v134 offset:2048
	ds_read_b128 v[214:217], v134 offset:3072
	global_load_lds_dwordx4 v[148:149], off
	v_lshl_add_u64 v[148:149], v[218:219], 0, s[6:7]
	s_add_i32 m0, s39, 0x2000
	s_nop 0
	global_load_lds_dwordx4 v[148:149], off
	s_barrier
	s_waitcnt lgkmcnt(0)
	s_waitcnt lgkmcnt(0)
	v_mfma_f32_16x16x32_bf16 v[118:121], v[202:205], v[170:173], v[118:121]
	v_mfma_f32_16x16x32_bf16 v[114:117], v[210:213], v[170:173], v[114:117]
	v_mfma_f32_16x16x32_bf16 v[102:105], v[202:205], v[178:181], v[102:105]
	v_mfma_f32_16x16x32_bf16 v[98:101], v[210:213], v[178:181], v[98:101]
	v_mfma_f32_16x16x32_bf16 v[86:89], v[202:205], v[186:189], v[86:89]
	v_mfma_f32_16x16x32_bf16 v[82:85], v[210:213], v[186:189], v[82:85]
	v_mfma_f32_16x16x32_bf16 v[70:73], v[202:205], v[194:197], v[70:73]
	v_mfma_f32_16x16x32_bf16 v[66:69], v[210:213], v[194:197], v[66:69]
	v_mfma_f32_16x16x32_bf16 v[118:121], v[206:209], v[174:177], v[118:121]
	v_mfma_f32_16x16x32_bf16 v[114:117], v[214:217], v[174:177], v[114:117]
	v_mfma_f32_16x16x32_bf16 v[102:105], v[206:209], v[182:185], v[102:105]
	v_mfma_f32_16x16x32_bf16 v[98:101], v[214:217], v[182:185], v[98:101]
	v_mfma_f32_16x16x32_bf16 v[86:89], v[206:209], v[190:193], v[86:89]
	v_mfma_f32_16x16x32_bf16 v[82:85], v[214:217], v[190:193], v[82:85]
	v_mfma_f32_16x16x32_bf16 v[70:73], v[206:209], v[198:201], v[70:73]
	v_mfma_f32_16x16x32_bf16 v[66:69], v[214:217], v[198:201], v[66:69]
	s_mov_b32 m0, s52
	v_lshl_add_u64 v[148:149], v[220:221], 0, s[6:7]
	s_barrier
	ds_read_b128 v[170:173], v153 offset:49152
	ds_read_b128 v[174:177], v153 offset:50176
	ds_read_b128 v[178:181], v153 offset:51200
	ds_read_b128 v[182:185], v153 offset:52224
	ds_read_b128 v[186:189], v153 offset:53248
	ds_read_b128 v[190:193], v153 offset:54272
	ds_read_b128 v[194:197], v153 offset:55296
	ds_read_b128 v[198:201], v153 offset:56320
	global_load_lds_dwordx4 v[148:149], off
	v_lshl_add_u64 v[148:149], v[222:223], 0, s[6:7]
	s_mov_b32 m0, s53
	s_nop 0
	global_load_lds_dwordx4 v[148:149], off
	s_barrier
	s_waitcnt lgkmcnt(0)
	s_waitcnt lgkmcnt(0)
	v_mfma_f32_16x16x32_bf16 v[62:65], v[144:147], v[170:173], v[62:65]
	v_mfma_f32_16x16x32_bf16 v[58:61], v[162:165], v[170:173], v[58:61]
	v_mfma_f32_16x16x32_bf16 v[46:49], v[144:147], v[178:181], v[46:49]
	v_mfma_f32_16x16x32_bf16 v[42:45], v[162:165], v[178:181], v[42:45]
	v_mfma_f32_16x16x32_bf16 v[30:33], v[144:147], v[186:189], v[30:33]
	v_mfma_f32_16x16x32_bf16 v[26:29], v[162:165], v[186:189], v[26:29]
	v_mfma_f32_16x16x32_bf16 v[22:25], v[144:147], v[194:197], v[22:25]
	v_mfma_f32_16x16x32_bf16 v[14:17], v[162:165], v[194:197], v[14:17]
	v_mfma_f32_16x16x32_bf16 v[62:65], v[158:161], v[174:177], v[62:65]
	v_mfma_f32_16x16x32_bf16 v[58:61], v[166:169], v[174:177], v[58:61]
	v_mfma_f32_16x16x32_bf16 v[46:49], v[158:161], v[182:185], v[46:49]
	v_mfma_f32_16x16x32_bf16 v[42:45], v[166:169], v[182:185], v[42:45]
	v_mfma_f32_16x16x32_bf16 v[30:33], v[158:161], v[190:193], v[30:33]
	v_mfma_f32_16x16x32_bf16 v[26:29], v[166:169], v[190:193], v[26:29]
	v_mfma_f32_16x16x32_bf16 v[22:25], v[158:161], v[198:201], v[22:25]
	v_mfma_f32_16x16x32_bf16 v[14:17], v[166:169], v[198:201], v[14:17]
	s_barrier
	s_add_u32 s36, s36, 0x80080
	s_addc_u32 s37, s37, 0
	s_add_i32 s38, s38, s46
	v_lshl_add_u64 v[144:145], s[36:37], 0, v[132:133]
	s_mov_b32 m0, s38
	s_nop 0
	global_load_lds_dwordx4 v[144:145], off
	v_lshl_add_u64 v[144:145], s[36:37], 0, v[130:131]
	s_add_i32 m0, s38, 0x2000
	s_nop 0
	global_load_lds_dwordx4 v[144:145], off
	s_waitcnt vmcnt(6)
	s_barrier
	v_mfma_f32_16x16x32_bf16 v[54:57], v[202:205], v[170:173], v[54:57]
	v_mfma_f32_16x16x32_bf16 v[50:53], v[210:213], v[170:173], v[50:53]
	v_mfma_f32_16x16x32_bf16 v[38:41], v[202:205], v[178:181], v[38:41]
	v_mfma_f32_16x16x32_bf16 v[34:37], v[210:213], v[178:181], v[34:37]
	v_mfma_f32_16x16x32_bf16 v[18:21], v[202:205], v[186:189], v[18:21]
	v_mfma_f32_16x16x32_bf16 v[10:13], v[210:213], v[186:189], v[10:13]
	v_mfma_f32_16x16x32_bf16 v[6:9], v[202:205], v[194:197], v[6:9]
	v_mfma_f32_16x16x32_bf16 v[2:5], v[210:213], v[194:197], v[2:5]
	v_mfma_f32_16x16x32_bf16 v[54:57], v[206:209], v[174:177], v[54:57]
	v_mfma_f32_16x16x32_bf16 v[50:53], v[214:217], v[174:177], v[50:53]
	v_mfma_f32_16x16x32_bf16 v[38:41], v[206:209], v[182:185], v[38:41]
	v_mfma_f32_16x16x32_bf16 v[34:37], v[214:217], v[182:185], v[34:37]
	v_mfma_f32_16x16x32_bf16 v[18:21], v[206:209], v[190:193], v[18:21]
	v_mfma_f32_16x16x32_bf16 v[10:13], v[214:217], v[190:193], v[10:13]
	v_mfma_f32_16x16x32_bf16 v[6:9], v[206:209], v[198:201], v[6:9]
	v_mfma_f32_16x16x32_bf16 v[2:5], v[214:217], v[198:201], v[2:5]
	s_add_i32 s69, s69, 2
	s_add_u32 s34, s34, 0x100
	s_addc_u32 s35, s35, 0
	s_add_u32 s67, s67, 0x100
	s_addc_u32 s68, s68, 0
	s_cmp_gt_u32 s69, 29
	s_barrier
	s_cbranch_scc0 .LBB0_3319
	v_lshl_add_u32 v146, s30, 8, v1
	v_lshl_or_b32 v144, s64, 8, v151
	v_ashrrev_i32_e32 v147, 31, v146
	s_movk_i32 s23, 0x3fff
	v_ashrrev_i32_e32 v145, 31, v144
	v_lshlrev_b64 v[148:149], 13, v[146:147]
	v_cmp_lt_i32_e32 vcc, s23, v146
	v_lshl_add_u64 v[158:159], s[8:9], 0, v[148:149]
	v_lshlrev_b64 v[144:145], 2, v[144:145]
	v_cndmask_b32_e32 v134, v155, v156, vcc
	v_lshl_add_u64 v[174:175], v[158:159], 0, v[144:145]
	v_lshl_add_u64 v[158:159], s[4:5], 0, v[134:135]
	v_lshl_add_u64 v[166:167], v[158:159], 0, v[144:145]
	v_add_co_u32_e32 v162, vcc, s57, v166
	s_nop 1
	v_addc_co_u32_e32 v163, vcc, 0, v167, vcc
	v_lshl_add_u64 v[170:171], s[10:11], 0, v[148:149]
	v_lshl_add_u64 v[180:181], v[170:171], 0, v[144:145]
	v_lshl_add_u64 v[178:179], v[166:167], 0, s[12:13]
	global_load_dwordx4 v[144:147], v[162:163], off
	global_load_dwordx4 v[158:161], v[178:179], off offset:64
	global_load_dwordx4 v[164:167], v[178:179], off offset:512
	global_load_dwordx4 v[168:171], v[178:179], off offset:576
	global_load_dwordx4 v[182:185], v[174:175], off
	global_load_dwordx4 v[186:189], v[174:175], off offset:64
	global_load_dwordx4 v[190:193], v[174:175], off offset:512
	global_load_dwordx4 v[194:197], v[174:175], off offset:576
	v_add_co_u32_e32 v172, vcc, 0x20000, v174
	s_nop 1
	v_addc_co_u32_e32 v173, vcc, 0, v175, vcc
	global_load_dwordx4 v[198:201], v[172:173], off
	global_load_dwordx4 v[202:205], v[172:173], off offset:64
	global_load_dwordx4 v[206:209], v[172:173], off offset:512
	global_load_dwordx4 v[210:213], v[172:173], off offset:576
	v_add_co_u32_e32 v214, vcc, 0x20000, v180
	s_nop 1
	v_addc_co_u32_e32 v215, vcc, 0, v181, vcc
	s_waitcnt vmcnt(0)
	v_pk_fma_f32 v[128:129], v[128:129], v[146:147], v[184:185]
	v_pk_fma_f32 v[126:127], v[126:127], v[144:145], v[182:183]
	global_store_dwordx4 v[180:181], v[126:129], off
	v_pk_fma_f32 v[124:125], v[124:125], v[160:161], v[188:189]
	v_pk_fma_f32 v[122:123], v[122:123], v[158:159], v[186:187]
	global_store_dwordx4 v[180:181], v[122:125], off offset:64
	v_pk_fma_f32 v[120:121], v[120:121], v[166:167], v[192:193]
	v_pk_fma_f32 v[118:119], v[118:119], v[164:165], v[190:191]
	global_store_dwordx4 v[180:181], v[118:121], off offset:512
	v_pk_fma_f32 v[116:117], v[116:117], v[170:171], v[196:197]
	v_pk_fma_f32 v[114:115], v[114:115], v[168:169], v[194:195]
	global_store_dwordx4 v[180:181], v[114:117], off offset:576
	v_pk_fma_f32 v[112:113], v[112:113], v[146:147], v[200:201]
	v_pk_fma_f32 v[110:111], v[110:111], v[144:145], v[198:199]
	global_store_dwordx4 v[214:215], v[110:113], off
	v_pk_fma_f32 v[108:109], v[108:109], v[160:161], v[204:205]
	v_pk_fma_f32 v[106:107], v[106:107], v[158:159], v[202:203]
	global_store_dwordx4 v[214:215], v[106:109], off offset:64
	v_pk_fma_f32 v[104:105], v[104:105], v[166:167], v[208:209]
	v_pk_fma_f32 v[102:103], v[102:103], v[164:165], v[206:207]
	global_store_dwordx4 v[214:215], v[102:105], off offset:512
	v_pk_fma_f32 v[100:101], v[100:101], v[170:171], v[212:213]
	v_pk_fma_f32 v[98:99], v[98:99], v[168:169], v[210:211]
	global_store_dwordx4 v[214:215], v[98:101], off offset:576
	v_add_co_u32_e32 v148, vcc, 0x40000, v174
	s_nop 1
	v_addc_co_u32_e32 v149, vcc, 0, v175, vcc
	global_load_dwordx4 v[182:185], v[148:149], off
	global_load_dwordx4 v[186:189], v[148:149], off offset:64
	global_load_dwordx4 v[190:193], v[148:149], off offset:512
	global_load_dwordx4 v[194:197], v[148:149], off offset:576
	v_add_co_u32_e32 v172, vcc, 0x60000, v174
	s_nop 1
	v_addc_co_u32_e32 v173, vcc, 0, v175, vcc
	global_load_dwordx4 v[198:201], v[172:173], off
	global_load_dwordx4 v[202:205], v[172:173], off offset:64
	global_load_dwordx4 v[206:209], v[172:173], off offset:512
	global_load_dwordx4 v[210:213], v[172:173], off offset:576
	v_add_co_u32_e32 v176, vcc, 0x40000, v180
	s_nop 1
	v_addc_co_u32_e32 v177, vcc, 0, v181, vcc
	v_add_co_u32_e32 v214, vcc, 0x60000, v180
	s_nop 1
	v_addc_co_u32_e32 v215, vcc, 0, v181, vcc
	s_waitcnt vmcnt(0)
	v_pk_fma_f32 v[96:97], v[96:97], v[146:147], v[184:185]
	v_pk_fma_f32 v[94:95], v[94:95], v[144:145], v[182:183]
	global_store_dwordx4 v[176:177], v[94:97], off
	v_pk_fma_f32 v[92:93], v[92:93], v[160:161], v[188:189]
	v_pk_fma_f32 v[90:91], v[90:91], v[158:159], v[186:187]
	global_store_dwordx4 v[176:177], v[90:93], off offset:64
	v_pk_fma_f32 v[88:89], v[88:89], v[166:167], v[192:193]
	v_pk_fma_f32 v[86:87], v[86:87], v[164:165], v[190:191]
	global_store_dwordx4 v[176:177], v[86:89], off offset:512
	v_pk_fma_f32 v[84:85], v[84:85], v[170:171], v[196:197]
	v_pk_fma_f32 v[82:83], v[82:83], v[168:169], v[194:195]
	global_store_dwordx4 v[176:177], v[82:85], off offset:576
	v_pk_fma_f32 v[80:81], v[80:81], v[146:147], v[200:201]
	v_pk_fma_f32 v[78:79], v[78:79], v[144:145], v[198:199]
	global_store_dwordx4 v[214:215], v[78:81], off
	v_pk_fma_f32 v[76:77], v[76:77], v[160:161], v[204:205]
	v_pk_fma_f32 v[74:75], v[74:75], v[158:159], v[202:203]
	global_store_dwordx4 v[214:215], v[74:77], off offset:64
	v_pk_fma_f32 v[72:73], v[72:73], v[166:167], v[208:209]
	v_pk_fma_f32 v[70:71], v[70:71], v[164:165], v[206:207]
	global_store_dwordx4 v[214:215], v[70:73], off offset:512
	v_pk_fma_f32 v[68:69], v[68:69], v[170:171], v[212:213]
	v_pk_fma_f32 v[66:67], v[66:67], v[168:169], v[210:211]
	global_store_dwordx4 v[214:215], v[66:69], off offset:576
	v_add_co_u32_e32 v148, vcc, 0x100000, v174
	s_nop 1
	v_addc_co_u32_e32 v149, vcc, 0, v175, vcc
	global_load_dwordx4 v[182:185], v[148:149], off
	global_load_dwordx4 v[186:189], v[148:149], off offset:64
	global_load_dwordx4 v[190:193], v[148:149], off offset:512
	global_load_dwordx4 v[194:197], v[148:149], off offset:576
	v_add_co_u32_e32 v172, vcc, 0x120000, v174
	s_nop 1
	v_addc_co_u32_e32 v173, vcc, 0, v175, vcc
	global_load_dwordx4 v[198:201], v[172:173], off
	global_load_dwordx4 v[202:205], v[172:173], off offset:64
	global_load_dwordx4 v[206:209], v[172:173], off offset:512
	global_load_dwordx4 v[210:213], v[172:173], off offset:576
	v_add_co_u32_e32 v176, vcc, 0x100000, v180
	s_nop 1
	v_addc_co_u32_e32 v177, vcc, 0, v181, vcc
	v_add_co_u32_e32 v214, vcc, 0x120000, v180
	s_nop 1
	v_addc_co_u32_e32 v215, vcc, 0, v181, vcc
	s_waitcnt vmcnt(0)
	v_pk_fma_f32 v[64:65], v[64:65], v[146:147], v[184:185]
	v_pk_fma_f32 v[62:63], v[62:63], v[144:145], v[182:183]
	global_store_dwordx4 v[176:177], v[62:65], off
	v_pk_fma_f32 v[60:61], v[60:61], v[160:161], v[188:189]
	v_pk_fma_f32 v[58:59], v[58:59], v[158:159], v[186:187]
	global_store_dwordx4 v[176:177], v[58:61], off offset:64
	v_pk_fma_f32 v[56:57], v[56:57], v[166:167], v[192:193]
	v_pk_fma_f32 v[54:55], v[54:55], v[164:165], v[190:191]
	global_store_dwordx4 v[176:177], v[54:57], off offset:512
	v_pk_fma_f32 v[52:53], v[52:53], v[170:171], v[196:197]
	v_pk_fma_f32 v[50:51], v[50:51], v[168:169], v[194:195]
	global_store_dwordx4 v[176:177], v[50:53], off offset:576
	v_pk_fma_f32 v[48:49], v[48:49], v[146:147], v[200:201]
	v_pk_fma_f32 v[46:47], v[46:47], v[144:145], v[198:199]
	global_store_dwordx4 v[214:215], v[46:49], off
	v_pk_fma_f32 v[44:45], v[44:45], v[160:161], v[204:205]
	v_pk_fma_f32 v[42:43], v[42:43], v[158:159], v[202:203]
	global_store_dwordx4 v[214:215], v[42:45], off offset:64
	v_pk_fma_f32 v[40:41], v[40:41], v[166:167], v[208:209]
	v_pk_fma_f32 v[38:39], v[38:39], v[164:165], v[206:207]
	global_store_dwordx4 v[214:215], v[38:41], off offset:512
	v_pk_fma_f32 v[36:37], v[36:37], v[170:171], v[212:213]
	v_pk_fma_f32 v[34:35], v[34:35], v[168:169], v[210:211]
	global_store_dwordx4 v[214:215], v[34:37], off offset:576
	v_add_co_u32_e32 v148, vcc, 0x140000, v174
	s_nop 1
	v_addc_co_u32_e32 v149, vcc, 0, v175, vcc
	global_load_dwordx4 v[182:185], v[148:149], off
	global_load_dwordx4 v[186:189], v[148:149], off offset:64
	global_load_dwordx4 v[190:193], v[148:149], off offset:512
	global_load_dwordx4 v[194:197], v[148:149], off offset:576
	v_add_co_u32_e32 v172, vcc, 0x160000, v174
	s_nop 1
	v_addc_co_u32_e32 v173, vcc, 0, v175, vcc
	global_load_dwordx4 v[198:201], v[172:173], off
	global_load_dwordx4 v[202:205], v[172:173], off offset:64
	global_load_dwordx4 v[206:209], v[172:173], off offset:512
	global_load_dwordx4 v[210:213], v[172:173], off offset:576
	v_add_co_u32_e32 v176, vcc, 0x140000, v180
	s_nop 1
	v_addc_co_u32_e32 v177, vcc, 0, v181, vcc
	v_add_co_u32_e32 v214, vcc, 0x160000, v180
	s_nop 1
	v_addc_co_u32_e32 v215, vcc, 0, v181, vcc
	s_waitcnt vmcnt(0)
	v_pk_fma_f32 v[32:33], v[32:33], v[146:147], v[184:185]
	v_pk_fma_f32 v[30:31], v[30:31], v[144:145], v[182:183]
	global_store_dwordx4 v[176:177], v[30:33], off
	v_pk_fma_f32 v[28:29], v[28:29], v[160:161], v[188:189]
	v_pk_fma_f32 v[26:27], v[26:27], v[158:159], v[186:187]
	global_store_dwordx4 v[176:177], v[26:29], off offset:64
	v_pk_fma_f32 v[20:21], v[20:21], v[166:167], v[192:193]
	v_pk_fma_f32 v[18:19], v[18:19], v[164:165], v[190:191]
	global_store_dwordx4 v[176:177], v[18:21], off offset:512
	v_pk_fma_f32 v[12:13], v[12:13], v[170:171], v[196:197]
	v_pk_fma_f32 v[10:11], v[10:11], v[168:169], v[194:195]
	global_store_dwordx4 v[176:177], v[10:13], off offset:576
	v_pk_fma_f32 v[24:25], v[24:25], v[146:147], v[200:201]
	v_pk_fma_f32 v[22:23], v[22:23], v[144:145], v[198:199]
	global_store_dwordx4 v[214:215], v[22:25], off
	v_pk_fma_f32 v[16:17], v[16:17], v[160:161], v[204:205]
	v_pk_fma_f32 v[14:15], v[14:15], v[158:159], v[202:203]
	global_store_dwordx4 v[214:215], v[14:17], off offset:64
	v_pk_fma_f32 v[8:9], v[8:9], v[166:167], v[208:209]
	v_pk_fma_f32 v[6:7], v[6:7], v[164:165], v[206:207]
	global_store_dwordx4 v[214:215], v[6:9], off offset:512
	v_pk_fma_f32 v[4:5], v[4:5], v[170:171], v[212:213]
	v_pk_fma_f32 v[2:3], v[2:3], v[168:169], v[210:211]
	global_store_dwordx4 v[214:215], v[2:5], off offset:576
	s_mov_b32 s64, s22
	s_mov_b32 s30, s24
	s_mov_b64 s[36:37], s[28:29]
	s_mov_b64 s[34:35], s[26:27]
	s_and_b64 vcc, exec, s[0:1]
	s_cbranch_vccz .LBB0_3316
	s_waitcnt vmcnt(0)
	v_readlane_b32 s52, v250, 40
	s_cmpk_gt_u32 s41, 0xff
	v_readlane_b32 s53, v250, 41
	v_readlane_b32 s54, v250, 42
	v_readlane_b32 s55, v250, 43
	s_cbranch_scc1 .LBB0_3323
	s_barrier

.LBB0_3325:
	s_cmp_gt_i32 s55, 20
	s_cselect_b64 s[0:1], -1, 0
	s_and_b64 s[2:3], s[2:3], s[0:1]
	s_andn2_b64 vcc, exec, s[2:3]
	s_cbranch_vccnz .LBB0_3375
	s_waitcnt vmcnt(0)
	s_barrier
	s_setprio 0
	s_mov_b64 s[2:3], exec
	v_readlane_b32 s4, v250, 5
	v_readlane_b32 s5, v250, 6
	s_and_b64 s[4:5], s[2:3], s[4:5]
	s_mov_b64 exec, s[4:5]
	s_cbranch_execz .LBB0_3374
	s_add_i32 s4, 0, 0x27ff0
	v_mov_b32_e32 v1, s4
	s_waitcnt vmcnt(0) expcnt(0) lgkmcnt(0)
	ds_read_b32 v3, v1
	s_add_i32 s4, 0, 0x27ff4
	v_mov_b32_e32 v1, s4
	ds_read_b32 v1, v1
	s_waitcnt lgkmcnt(1)
	v_cmp_ne_u32_e32 vcc, 0, v3
	s_cbranch_vccnz .LBB0_3342
	v_readlane_b32 s4, v250, 2
	v_readlane_b32 s5, v250, 3
	s_load_dwordx2 s[8:9], s[4:5], 0x4
	s_add_u32 s4, s52, 0x1000
	s_addc_u32 s5, s53, 0
	s_add_u32 s6, s52, 0x1100
	s_addc_u32 s7, s53, 0
	v_readlane_b32 s10, v250, 1
	s_waitcnt lgkmcnt(0)
	s_mul_i32 s18, s8, s10
	s_add_u32 s8, s52, 0x1200
	s_mul_i32 s18, s18, s9
	s_addc_u32 s9, s53, 0
	s_add_u32 s10, s52, 0x1300
	s_addc_u32 s11, s53, 0
	s_mov_b32 s19, 1
	v_mov_b32_e32 v17, 0
	s_branch .LBB0_3330

.LBB0_3401:
	s_cmp_gt_i32 s55, 21
	s_cselect_b64 s[0:1], -1, 0
	s_and_b64 s[2:3], s[36:37], s[0:1]
	s_andn2_b64 vcc, exec, s[2:3]
	s_cbranch_vccnz .LBB0_3451
	s_waitcnt vmcnt(0)
	s_barrier
	s_setprio 0
	s_mov_b64 s[2:3], exec
	v_readlane_b32 s4, v250, 5
	v_readlane_b32 s5, v250, 6
	s_and_b64 s[4:5], s[2:3], s[4:5]
	s_mov_b64 exec, s[4:5]
	s_cbranch_execz .LBB0_3450
	s_add_i32 s4, 0, 0x27ff0
	v_mov_b32_e32 v1, s4
	s_waitcnt vmcnt(0) expcnt(0) lgkmcnt(0)
	ds_read_b32 v3, v1
	s_add_i32 s4, 0, 0x27ff4
	v_mov_b32_e32 v1, s4
	ds_read_b32 v1, v1
	s_waitcnt lgkmcnt(1)
	v_cmp_ne_u32_e32 vcc, 0, v3
	s_cbranch_vccnz .LBB0_3418
	v_readlane_b32 s4, v250, 2
	v_readlane_b32 s5, v250, 3
	s_load_dwordx2 s[8:9], s[4:5], 0x4
	s_add_u32 s4, s52, 0x1000
	s_addc_u32 s5, s53, 0
	s_add_u32 s6, s52, 0x1100
	s_addc_u32 s7, s53, 0
	v_readlane_b32 s10, v250, 1
	s_waitcnt lgkmcnt(0)
	s_mul_i32 s18, s8, s10
	s_add_u32 s8, s52, 0x1200
	s_mul_i32 s18, s18, s9
	s_addc_u32 s9, s53, 0
	s_add_u32 s10, s52, 0x1300
	s_addc_u32 s11, s53, 0
	s_mov_b32 s19, 1
	v_mov_b32_e32 v17, 0
	s_branch .LBB0_3406

.LBB0_3819:
	s_cmp_gt_i32 s55, 22
	s_cselect_b64 s[0:1], -1, 0
	s_and_b64 s[2:3], s[56:57], s[0:1]
	s_andn2_b64 vcc, exec, s[2:3]
	s_cbranch_vccnz .LBB0_3869
	s_waitcnt vmcnt(0)
	s_barrier
	s_setprio 0
	s_mov_b64 s[2:3], exec
	v_readlane_b32 s4, v250, 5
	v_readlane_b32 s5, v250, 6
	s_and_b64 s[4:5], s[2:3], s[4:5]
	s_mov_b64 exec, s[4:5]
	s_cbranch_execz .LBB0_3868
	s_add_i32 s4, 0, 0x27ff0
	v_mov_b32_e32 v1, s4
	s_waitcnt vmcnt(0) expcnt(0) lgkmcnt(0)
	ds_read_b32 v3, v1
	s_add_i32 s4, 0, 0x27ff4
	v_mov_b32_e32 v1, s4
	ds_read_b32 v1, v1
	s_waitcnt lgkmcnt(1)
	v_cmp_ne_u32_e32 vcc, 0, v3
	s_cbranch_vccnz .LBB0_3836
	v_readlane_b32 s4, v250, 2
	v_readlane_b32 s5, v250, 3
	s_load_dwordx2 s[8:9], s[4:5], 0x4
	s_add_u32 s4, s52, 0x1000
	s_addc_u32 s5, s53, 0
	s_add_u32 s6, s52, 0x1100
	s_addc_u32 s7, s53, 0
	v_readlane_b32 s10, v250, 1
	s_waitcnt lgkmcnt(0)
	s_mul_i32 s18, s8, s10
	s_add_u32 s8, s52, 0x1200
	s_mul_i32 s18, s18, s9
	s_addc_u32 s9, s53, 0
	s_add_u32 s10, s52, 0x1300
	s_addc_u32 s11, s53, 0
	s_mov_b32 s19, 1
	v_mov_b32_e32 v17, 0
	s_branch .LBB0_3824

.LBB0_3869:
	s_cmp_lt_i32 s54, 23
	s_cselect_b64 s[6:7], -1, 0
	s_and_b64 s[0:1], s[6:7], s[0:1]
	s_andn2_b64 vcc, exec, s[0:1]
	s_cbranch_vccnz .LBB0_3887
	v_mov_b32_e32 v1, v248
	s_waitcnt vmcnt(5)
	v_mov_b32_e32 v2, v0
	v_readlane_b32 s33, v250, 1
	v_readlane_b32 s36, v250, 0
	v_readlane_b32 s0, v250, 39
	s_mov_b64 s[2:3], s[90:91]
	s_mov_b64 s[0:1], s[52:53]
	s_cmpk_gt_i32 s36, 0x3ff
	v_readfirstlane_b32 s37, v0
	s_barrier
	s_cbranch_scc1 .LBB0_3886
	s_add_u32 s8, s0, 0x2ec40000
	s_addc_u32 s9, s1, 0
	s_add_u32 s38, s0, 0x16940000
	s_addc_u32 s39, s1, 0
	s_add_u32 s10, s0, 0x1674000
	s_addc_u32 s11, s1, 0
	s_ashr_i32 s41, s36, 31
	s_lshr_b32 s5, s41, 29
	s_add_i32 s5, s36, s5
	s_lshr_b32 s4, s37, 6
	s_ashr_i32 s12, s5, 3
	s_and_b32 s5, s5, -8
	s_lshr_b32 s3, s37, 8
	s_lshl_b32 s40, s4, 10
	s_sub_i32 s5, s36, s5
	s_cmp_lt_i32 s5, 0
	s_movk_i32 s42, 0x81
	s_cselect_b32 s13, s42, 0x80
	s_mul_i32 s5, s13, s5
	s_add_i32 s5, s5, s12
	s_ashr_i32 s12, s5, 31
	s_lshr_b32 s12, s12, 26
	s_add_i32 s12, s5, s12
	s_ashr_i32 s13, s12, 6
	s_lshl_b32 s14, s13, 3
	s_sub_i32 s13, 0x80, s14
	s_min_u32 s15, s13, 8
	s_andn2_b32 s12, s12, 63
	s_sub_i32 s5, s5, s12
	v_cvt_f32_ubyte0_e32 v5, s15
	v_cvt_f32_i32_e32 v4, s5
	s_waitcnt vmcnt(4)
	v_rcp_iflag_f32_e32 v6, v5
	v_bfe_u32 v2, v0, 2, 4
	v_lshrrev_b32_e32 v3, 3, v0
	v_and_or_b32 v1, v3, 48, v2
	v_or_b32_e32 v3, 64, v3
	s_movk_i32 s2, 0x70
	v_and_or_b32 v150, v3, s2, v2
	v_mul_f32_e32 v2, v4, v6
	v_trunc_f32_e32 v2, v2
	v_fma_f32 v3, -v2, v5, v4
	v_cvt_i32_f32_e32 v2, v2
	s_ashr_i32 s2, s5, 30
	s_or_b32 s2, s2, 1
	v_cmp_ge_f32_e64 s[12:13], |v3|, v5
	s_and_b64 s[12:13], s[12:13], exec
	s_cselect_b32 s2, s2, 0
	v_readfirstlane_b32 s12, v2
	s_add_i32 s2, s12, s2
	s_mul_i32 s12, s2, s15
	s_sub_i32 s5, s5, s12
	s_sext_i32_i8 s5, s5
	s_add_i32 s58, s14, s5
	s_lshr_b32 s5, s58, 29
	s_add_i32 s5, s58, s5
	s_ashr_i32 s12, s5, 3
	s_lshl_b32 s13, s12, 11
	s_lshl_b32 s14, s58, 8
	s_mul_i32 s5, s12, 0x900
	s_sub_i32 s13, s14, s13
	s_add_i32 s5, s13, s5
	v_or_b32_e32 v2, s5, v1
	v_or_b32_e32 v4, s5, v150
	s_bitset1_b32 s5, 7
	v_ashrrev_i32_e32 v3, 31, v2
	v_or_b32_e32 v6, s5, v1
	v_or_b32_e32 v8, s5, v150
	v_lshl_add_u64 v[2:3], v[2:3], 2, s[10:11]
	v_ashrrev_i32_e32 v5, 31, v4
	v_ashrrev_i32_e32 v7, 31, v6
	v_ashrrev_i32_e32 v9, 31, v8
	v_lshl_add_u64 v[4:5], v[4:5], 2, s[10:11]
	v_lshl_add_u64 v[6:7], v[6:7], 2, s[10:11]
	v_lshl_add_u64 v[8:9], v[8:9], 2, s[10:11]
	global_load_dword v10, v[2:3], off
	global_load_dword v11, v[4:5], off
	global_load_dword v12, v[6:7], off
	global_load_dword v13, v[8:9], off
	s_bfe_i64 s[14:15], s[2:3], 0x80000
	s_ashr_i32 s13, s12, 31
	s_lshl_b64 s[14:15], s[14:15], 20
	s_lshl_b64 s[12:13], s[12:13], 23
	s_add_u32 s5, s38, s12
	v_lshlrev_b32_e32 v2, 4, v0
	v_and_b32_e32 v3, 32, v0
	s_addc_u32 s12, s39, s13
	v_bitop3_b32 v2, v2, v3, 48 bitop3:0x6c
	s_add_u32 s28, s5, s14
	v_and_or_b32 v151, v0, 64, v2
	s_addc_u32 s29, s12, s15
	s_add_i32 s43, s40, 0
	v_lshl_or_b32 v132, v1, 12, v151
	s_add_i32 m0, s43, 0x10000
	v_lshl_or_b32 v130, v150, 12, v151
	global_load_lds_dwordx4 v132, s[28:29]
	s_add_i32 m0, s43, 0x12000
	s_add_i32 s44, s43, 0x2000
	global_load_lds_dwordx4 v130, s[28:29]
	s_mov_b32 m0, s43
	s_add_u32 s12, s28, 0x80000
	s_addc_u32 s13, s29, 0
	s_add_i32 s45, s43, 0x4000
	s_add_i32 s46, s43, 0x6000
	v_mov_b32_e32 v135, 0
	v_mov_b32_e32 v133, v135
	v_mov_b32_e32 v131, v135
	s_mov_b32 s47, 0
	v_lshl_add_u64 v[4:5], s[28:29], 0, v[132:133]
	v_lshl_add_u64 v[2:3], s[28:29], 0, v[130:131]
	v_mov_b32_e32 v141, v135
	s_waitcnt vmcnt(0)
	v_lshl_or_b32 v134, v10, 12, v151
	v_lshl_or_b32 v140, v11, 12, v151
	global_load_lds_dwordx4 v134, s[8:9]
	s_mov_b32 m0, s44
	v_lshl_or_b32 v142, v12, 12, v151
	global_load_lds_dwordx4 v140, s[8:9]
	s_add_i32 m0, s43, 0x14000
	v_lshl_or_b32 v144, v13, 12, v151
	global_load_lds_dwordx4 v132, s[12:13]
	s_add_i32 m0, s43, 0x16000
	s_setprio 1
	s_cmp_lg_u32 s3, 1
	global_load_lds_dwordx4 v130, s[12:13]
	s_mov_b32 m0, s45
	s_nop 0
	global_load_lds_dwordx4 v142, s[8:9]
	s_mov_b32 m0, s46
	s_nop 0
	global_load_lds_dwordx4 v144, s[8:9]
	s_cbranch_scc1 .LBB0_3873
	s_barrier
	s_setprio 0

.LBB0_3881:
	s_add_u32 s28, s4, 0x100
	s_addc_u32 s29, s5, 0
	s_add_u32 s34, s27, s4
	ds_read_b128 v[162:165], v155
	ds_read_b128 v[166:169], v155 offset:1024
	ds_read_b128 v[170:173], v155 offset:2048
	ds_read_b128 v[174:177], v155 offset:3072
	s_addc_u32 s35, s60, s5
	s_cmpk_eq_i32 s4, 0xf00
	s_cselect_b64 vcc, -1, 0
	s_and_b64 s[30:31], vcc, exec
	s_cselect_b32 s63, 0, s28
	s_cselect_b32 s62, 0, s29
	s_cselect_b32 s30, s2, s34
	s_cselect_b32 s31, s3, s35
	s_add_u32 s34, s8, s63
	v_cndmask_b32_e32 v134, v141, v158, vcc
	v_cndmask_b32_e32 v226, v140, v159, vcc
	v_cndmask_b32_e32 v143, v142, v160, vcc
	v_cndmask_b32_e32 v145, v144, v161, vcc
	s_addc_u32 s35, s9, s62
	v_lshl_add_u64 v[210:211], v[146:147], 0, s[4:5]
	s_add_i32 m0, s43, 0xc000
	ds_read_b128 v[178:181], v156
	ds_read_b128 v[182:185], v156 offset:1024
	ds_read_b128 v[186:189], v156 offset:2048
	ds_read_b128 v[190:193], v156 offset:3072
	ds_read_b128 v[194:197], v156 offset:4096
	ds_read_b128 v[198:201], v156 offset:5120
	ds_read_b128 v[202:205], v156 offset:6144
	ds_read_b128 v[206:209], v156 offset:7168
	global_load_lds_dwordx4 v[210:211], off
	v_lshl_add_u64 v[210:211], v[148:149], 0, s[4:5]
	s_add_i32 m0, s43, 0xe000
	s_nop 0
	global_load_lds_dwordx4 v[210:211], off
	s_waitcnt lgkmcnt(8)
	s_barrier
	s_waitcnt lgkmcnt(0)
	s_waitcnt lgkmcnt(0)
	v_mfma_f32_16x16x32_bf16 v[126:129], v[162:165], v[178:181], v[126:129]
	v_mfma_f32_16x16x32_bf16 v[122:125], v[170:173], v[178:181], v[122:125]
	v_mfma_f32_16x16x32_bf16 v[110:113], v[162:165], v[186:189], v[110:113]
	v_mfma_f32_16x16x32_bf16 v[106:109], v[170:173], v[186:189], v[106:109]
	v_mfma_f32_16x16x32_bf16 v[94:97], v[162:165], v[194:197], v[94:97]
	v_mfma_f32_16x16x32_bf16 v[90:93], v[170:173], v[194:197], v[90:93]
	v_mfma_f32_16x16x32_bf16 v[78:81], v[162:165], v[202:205], v[78:81]
	v_mfma_f32_16x16x32_bf16 v[74:77], v[170:173], v[202:205], v[74:77]
	v_mfma_f32_16x16x32_bf16 v[126:129], v[166:169], v[182:185], v[126:129]
	v_mfma_f32_16x16x32_bf16 v[122:125], v[174:177], v[182:185], v[122:125]
	v_mfma_f32_16x16x32_bf16 v[110:113], v[166:169], v[190:193], v[110:113]
	v_mfma_f32_16x16x32_bf16 v[106:109], v[174:177], v[190:193], v[106:109]
	v_mfma_f32_16x16x32_bf16 v[94:97], v[166:169], v[198:201], v[94:97]
	v_mfma_f32_16x16x32_bf16 v[90:93], v[174:177], v[198:201], v[90:93]
	v_mfma_f32_16x16x32_bf16 v[78:81], v[166:169], v[206:209], v[78:81]
	v_mfma_f32_16x16x32_bf16 v[74:77], v[174:177], v[206:209], v[74:77]
	s_barrier
	s_add_i32 s4, s51, s40
	v_lshl_add_u64 v[228:229], s[30:31], 0, v[132:133]
	s_mov_b32 m0, s4
	ds_read_b128 v[210:213], v157
	ds_read_b128 v[214:217], v157 offset:1024
	ds_read_b128 v[218:221], v157 offset:2048
	ds_read_b128 v[222:225], v157 offset:3072
	global_load_lds_dwordx4 v[228:229], off
	v_lshl_add_u64 v[230:231], s[30:31], 0, v[130:131]
	s_add_i32 m0, s4, 0x2000
	s_nop 0
	global_load_lds_dwordx4 v[230:231], off
	s_barrier
	s_waitcnt lgkmcnt(0)
	s_waitcnt lgkmcnt(0)
	v_mfma_f32_16x16x32_bf16 v[118:121], v[210:213], v[178:181], v[118:121]
	v_mfma_f32_16x16x32_bf16 v[114:117], v[218:221], v[178:181], v[114:117]
	v_mfma_f32_16x16x32_bf16 v[102:105], v[210:213], v[186:189], v[102:105]
	v_mfma_f32_16x16x32_bf16 v[98:101], v[218:221], v[186:189], v[98:101]
	v_mfma_f32_16x16x32_bf16 v[86:89], v[210:213], v[194:197], v[86:89]
	v_mfma_f32_16x16x32_bf16 v[82:85], v[218:221], v[194:197], v[82:85]
	v_mfma_f32_16x16x32_bf16 v[70:73], v[210:213], v[202:205], v[70:73]
	v_mfma_f32_16x16x32_bf16 v[66:69], v[218:221], v[202:205], v[66:69]
	v_mfma_f32_16x16x32_bf16 v[118:121], v[214:217], v[182:185], v[118:121]
	v_mfma_f32_16x16x32_bf16 v[114:117], v[222:225], v[182:185], v[114:117]
	v_mfma_f32_16x16x32_bf16 v[102:105], v[214:217], v[190:193], v[102:105]
	v_mfma_f32_16x16x32_bf16 v[98:101], v[222:225], v[190:193], v[98:101]
	v_mfma_f32_16x16x32_bf16 v[86:89], v[214:217], v[198:201], v[86:89]
	v_mfma_f32_16x16x32_bf16 v[82:85], v[222:225], v[198:201], v[82:85]
	v_mfma_f32_16x16x32_bf16 v[70:73], v[214:217], v[206:209], v[70:73]
	v_mfma_f32_16x16x32_bf16 v[66:69], v[222:225], v[206:209], v[66:69]
	s_mov_b32 m0, s43
	s_barrier
	ds_read_b128 v[178:181], v156 offset:16384
	ds_read_b128 v[182:185], v156 offset:17408
	ds_read_b128 v[186:189], v156 offset:18432
	ds_read_b128 v[190:193], v156 offset:19456
	ds_read_b128 v[194:197], v156 offset:20480
	ds_read_b128 v[198:201], v156 offset:21504
	ds_read_b128 v[202:205], v156 offset:22528
	ds_read_b128 v[206:209], v156 offset:23552
	global_load_lds_dwordx4 v134, s[34:35]
	s_mov_b32 m0, s44
	v_mov_b32_e32 v227, v135
	global_load_lds_dwordx4 v226, s[34:35]
	s_barrier
	s_waitcnt lgkmcnt(0)
	v_lshl_add_u64 v[232:233], s[34:35], 0, v[134:135]
	v_lshl_add_u64 v[226:227], s[34:35], 0, v[226:227]
	s_waitcnt lgkmcnt(0)
	v_mfma_f32_16x16x32_bf16 v[62:65], v[162:165], v[178:181], v[62:65]
	v_mfma_f32_16x16x32_bf16 v[58:61], v[170:173], v[178:181], v[58:61]
	v_mfma_f32_16x16x32_bf16 v[46:49], v[162:165], v[186:189], v[46:49]
	v_mfma_f32_16x16x32_bf16 v[42:45], v[170:173], v[186:189], v[42:45]
	v_mfma_f32_16x16x32_bf16 v[30:33], v[162:165], v[194:197], v[30:33]
	v_mfma_f32_16x16x32_bf16 v[26:29], v[170:173], v[194:197], v[26:29]
	v_mfma_f32_16x16x32_bf16 v[14:17], v[162:165], v[202:205], v[14:17]
	v_mfma_f32_16x16x32_bf16 v[10:13], v[170:173], v[202:205], v[10:13]
	v_mfma_f32_16x16x32_bf16 v[62:65], v[166:169], v[182:185], v[62:65]
	v_mfma_f32_16x16x32_bf16 v[58:61], v[174:177], v[182:185], v[58:61]
	v_mfma_f32_16x16x32_bf16 v[46:49], v[166:169], v[190:193], v[46:49]
	v_mfma_f32_16x16x32_bf16 v[42:45], v[174:177], v[190:193], v[42:45]
	v_mfma_f32_16x16x32_bf16 v[30:33], v[166:169], v[198:201], v[30:33]
	v_mfma_f32_16x16x32_bf16 v[26:29], v[174:177], v[198:201], v[26:29]
	v_mfma_f32_16x16x32_bf16 v[14:17], v[166:169], v[206:209], v[14:17]
	v_mfma_f32_16x16x32_bf16 v[10:13], v[174:177], v[206:209], v[10:13]
	s_barrier
	s_add_u32 s4, s30, 0x80000
	s_addc_u32 s5, s31, 0
	s_add_i32 s62, s52, s40
	v_lshl_add_u64 v[162:163], s[4:5], 0, v[132:133]
	s_mov_b32 m0, s62
	s_nop 0
	global_load_lds_dwordx4 v[162:163], off
	v_lshl_add_u64 v[162:163], s[4:5], 0, v[130:131]
	s_add_i32 m0, s62, 0x2000
	s_nop 0
	global_load_lds_dwordx4 v[162:163], off
	s_waitcnt vmcnt(6)
	s_barrier
	v_mfma_f32_16x16x32_bf16 v[54:57], v[210:213], v[178:181], v[54:57]
	v_mfma_f32_16x16x32_bf16 v[50:53], v[218:221], v[178:181], v[50:53]
	v_mfma_f32_16x16x32_bf16 v[38:41], v[210:213], v[186:189], v[38:41]
	v_mfma_f32_16x16x32_bf16 v[34:37], v[218:221], v[186:189], v[34:37]
	v_mfma_f32_16x16x32_bf16 v[22:25], v[210:213], v[194:197], v[22:25]
	v_mfma_f32_16x16x32_bf16 v[18:21], v[218:221], v[194:197], v[18:21]
	v_mfma_f32_16x16x32_bf16 v[6:9], v[210:213], v[202:205], v[6:9]
	v_mfma_f32_16x16x32_bf16 v[2:5], v[218:221], v[202:205], v[2:5]
	v_mfma_f32_16x16x32_bf16 v[54:57], v[214:217], v[182:185], v[54:57]
	v_mfma_f32_16x16x32_bf16 v[50:53], v[222:225], v[182:185], v[50:53]
	v_mfma_f32_16x16x32_bf16 v[38:41], v[214:217], v[190:193], v[38:41]
	v_mfma_f32_16x16x32_bf16 v[34:37], v[222:225], v[190:193], v[34:37]
	v_mfma_f32_16x16x32_bf16 v[22:25], v[214:217], v[198:201], v[22:25]
	v_mfma_f32_16x16x32_bf16 v[18:21], v[222:225], v[198:201], v[18:21]
	v_mfma_f32_16x16x32_bf16 v[6:9], v[214:217], v[206:209], v[6:9]
	v_mfma_f32_16x16x32_bf16 v[2:5], v[222:225], v[206:209], v[2:5]
	s_add_i32 s4, 0, 0x18000
	v_add_u32_e32 v134, s4, v153
	s_barrier
	ds_read_b128 v[162:165], v134
	ds_read_b128 v[166:169], v134 offset:1024
	ds_read_b128 v[170:173], v134 offset:2048
	ds_read_b128 v[174:177], v134 offset:3072
	s_mov_b32 m0, s45
	ds_read_b128 v[178:181], v156 offset:32768
	ds_read_b128 v[182:185], v156 offset:33792
	ds_read_b128 v[186:189], v156 offset:34816
	ds_read_b128 v[190:193], v156 offset:35840
	ds_read_b128 v[194:197], v156 offset:36864
	ds_read_b128 v[198:201], v156 offset:37888
	ds_read_b128 v[202:205], v156 offset:38912
	ds_read_b128 v[206:209], v156 offset:39936
	global_load_lds_dwordx4 v143, s[34:35]
	s_mov_b32 m0, s46
	s_nop 0
	global_load_lds_dwordx4 v145, s[34:35]
	s_waitcnt lgkmcnt(8)
	s_barrier
	s_waitcnt lgkmcnt(0)
	s_waitcnt lgkmcnt(0)
	v_mfma_f32_16x16x32_bf16 v[126:129], v[162:165], v[178:181], v[126:129]
	v_mfma_f32_16x16x32_bf16 v[122:125], v[170:173], v[178:181], v[122:125]
	v_mfma_f32_16x16x32_bf16 v[110:113], v[162:165], v[186:189], v[110:113]
	v_mfma_f32_16x16x32_bf16 v[106:109], v[170:173], v[186:189], v[106:109]
	v_mfma_f32_16x16x32_bf16 v[94:97], v[162:165], v[194:197], v[94:97]
	v_mfma_f32_16x16x32_bf16 v[90:93], v[170:173], v[194:197], v[90:93]
	v_mfma_f32_16x16x32_bf16 v[78:81], v[162:165], v[202:205], v[78:81]
	v_mfma_f32_16x16x32_bf16 v[74:77], v[170:173], v[202:205], v[74:77]
	v_mfma_f32_16x16x32_bf16 v[126:129], v[166:169], v[182:185], v[126:129]
	v_mfma_f32_16x16x32_bf16 v[122:125], v[174:177], v[182:185], v[122:125]
	v_mfma_f32_16x16x32_bf16 v[110:113], v[166:169], v[190:193], v[110:113]
	v_mfma_f32_16x16x32_bf16 v[106:109], v[174:177], v[190:193], v[106:109]
	v_mfma_f32_16x16x32_bf16 v[94:97], v[166:169], v[198:201], v[94:97]
	v_mfma_f32_16x16x32_bf16 v[90:93], v[174:177], v[198:201], v[90:93]
	v_mfma_f32_16x16x32_bf16 v[78:81], v[166:169], v[206:209], v[78:81]
	v_mfma_f32_16x16x32_bf16 v[74:77], v[174:177], v[206:209], v[74:77]
	s_barrier
	s_add_i32 s34, 0, 0x1c000
	s_add_i32 s4, s4, s40
	v_add_u32_e32 v134, s34, v153
	v_lshl_add_u64 v[228:229], v[228:229], 0, s[14:15]
	s_mov_b32 m0, s4
	ds_read_b128 v[210:213], v134
	ds_read_b128 v[214:217], v134 offset:1024
	ds_read_b128 v[218:221], v134 offset:2048
	ds_read_b128 v[222:225], v134 offset:3072
	global_load_lds_dwordx4 v[228:229], off
	v_lshl_add_u64 v[228:229], v[230:231], 0, s[14:15]
	s_add_i32 m0, s4, 0x2000
	s_nop 0
	global_load_lds_dwordx4 v[228:229], off
	s_barrier
	s_waitcnt lgkmcnt(0)
	s_waitcnt lgkmcnt(0)
	v_mfma_f32_16x16x32_bf16 v[118:121], v[210:213], v[178:181], v[118:121]
	v_mfma_f32_16x16x32_bf16 v[114:117], v[218:221], v[178:181], v[114:117]
	v_mfma_f32_16x16x32_bf16 v[102:105], v[210:213], v[186:189], v[102:105]
	v_mfma_f32_16x16x32_bf16 v[98:101], v[218:221], v[186:189], v[98:101]
	v_mfma_f32_16x16x32_bf16 v[86:89], v[210:213], v[194:197], v[86:89]
	v_mfma_f32_16x16x32_bf16 v[82:85], v[218:221], v[194:197], v[82:85]
	v_mfma_f32_16x16x32_bf16 v[70:73], v[210:213], v[202:205], v[70:73]
	v_mfma_f32_16x16x32_bf16 v[66:69], v[218:221], v[202:205], v[66:69]
	v_mfma_f32_16x16x32_bf16 v[118:121], v[214:217], v[182:185], v[118:121]
	v_mfma_f32_16x16x32_bf16 v[114:117], v[222:225], v[182:185], v[114:117]
	v_mfma_f32_16x16x32_bf16 v[102:105], v[214:217], v[190:193], v[102:105]
	v_mfma_f32_16x16x32_bf16 v[98:101], v[222:225], v[190:193], v[98:101]
	v_mfma_f32_16x16x32_bf16 v[86:89], v[214:217], v[198:201], v[86:89]
	v_mfma_f32_16x16x32_bf16 v[82:85], v[222:225], v[198:201], v[82:85]
	v_mfma_f32_16x16x32_bf16 v[70:73], v[214:217], v[206:209], v[70:73]
	v_mfma_f32_16x16x32_bf16 v[66:69], v[222:225], v[206:209], v[66:69]
	s_mov_b32 m0, s48
	v_lshl_add_u64 v[228:229], v[232:233], 0, s[14:15]
	s_barrier
	ds_read_b128 v[178:181], v156 offset:49152
	ds_read_b128 v[182:185], v156 offset:50176
	ds_read_b128 v[186:189], v156 offset:51200
	ds_read_b128 v[190:193], v156 offset:52224
	ds_read_b128 v[194:197], v156 offset:53248
	ds_read_b128 v[198:201], v156 offset:54272
	ds_read_b128 v[202:205], v156 offset:55296
	ds_read_b128 v[206:209], v156 offset:56320
	global_load_lds_dwordx4 v[228:229], off
	v_lshl_add_u64 v[226:227], v[226:227], 0, s[14:15]
	s_mov_b32 m0, s49
	s_nop 0
	global_load_lds_dwordx4 v[226:227], off
	s_barrier
	s_waitcnt lgkmcnt(0)
	s_waitcnt lgkmcnt(0)
	v_mfma_f32_16x16x32_bf16 v[62:65], v[162:165], v[178:181], v[62:65]
	v_mfma_f32_16x16x32_bf16 v[58:61], v[170:173], v[178:181], v[58:61]
	v_mfma_f32_16x16x32_bf16 v[46:49], v[162:165], v[186:189], v[46:49]
	v_mfma_f32_16x16x32_bf16 v[42:45], v[170:173], v[186:189], v[42:45]
	v_mfma_f32_16x16x32_bf16 v[30:33], v[162:165], v[194:197], v[30:33]
	v_mfma_f32_16x16x32_bf16 v[26:29], v[170:173], v[194:197], v[26:29]
	v_mfma_f32_16x16x32_bf16 v[14:17], v[162:165], v[202:205], v[14:17]
	v_mfma_f32_16x16x32_bf16 v[10:13], v[170:173], v[202:205], v[10:13]
	v_mfma_f32_16x16x32_bf16 v[62:65], v[166:169], v[182:185], v[62:65]
	v_mfma_f32_16x16x32_bf16 v[58:61], v[174:177], v[182:185], v[58:61]
	v_mfma_f32_16x16x32_bf16 v[46:49], v[166:169], v[190:193], v[46:49]
	v_mfma_f32_16x16x32_bf16 v[42:45], v[174:177], v[190:193], v[42:45]
	v_mfma_f32_16x16x32_bf16 v[30:33], v[166:169], v[198:201], v[30:33]
	v_mfma_f32_16x16x32_bf16 v[26:29], v[174:177], v[198:201], v[26:29]
	v_mfma_f32_16x16x32_bf16 v[14:17], v[166:169], v[206:209], v[14:17]
	v_mfma_f32_16x16x32_bf16 v[10:13], v[174:177], v[206:209], v[10:13]
	s_barrier
	s_add_u32 s4, s30, 0x80080
	s_addc_u32 s5, s31, 0
	s_add_i32 s30, s34, s40
	v_lshl_add_u64 v[162:163], s[4:5], 0, v[132:133]
	s_mov_b32 m0, s30
	s_nop 0
	global_load_lds_dwordx4 v[162:163], off
	v_lshl_add_u64 v[162:163], s[4:5], 0, v[130:131]
	s_add_i32 m0, s30, 0x2000
	s_nop 0
	global_load_lds_dwordx4 v[162:163], off
	s_waitcnt vmcnt(6)
	s_barrier
	v_mfma_f32_16x16x32_bf16 v[54:57], v[210:213], v[178:181], v[54:57]
	v_mfma_f32_16x16x32_bf16 v[50:53], v[218:221], v[178:181], v[50:53]
	v_mfma_f32_16x16x32_bf16 v[38:41], v[210:213], v[186:189], v[38:41]
	v_mfma_f32_16x16x32_bf16 v[34:37], v[218:221], v[186:189], v[34:37]
	v_mfma_f32_16x16x32_bf16 v[22:25], v[210:213], v[194:197], v[22:25]
	v_mfma_f32_16x16x32_bf16 v[18:21], v[218:221], v[194:197], v[18:21]
	v_mfma_f32_16x16x32_bf16 v[6:9], v[210:213], v[202:205], v[6:9]
	v_mfma_f32_16x16x32_bf16 v[2:5], v[218:221], v[202:205], v[2:5]
	v_mfma_f32_16x16x32_bf16 v[54:57], v[214:217], v[182:185], v[54:57]
	v_mfma_f32_16x16x32_bf16 v[50:53], v[222:225], v[182:185], v[50:53]
	v_mfma_f32_16x16x32_bf16 v[38:41], v[214:217], v[190:193], v[38:41]
	v_mfma_f32_16x16x32_bf16 v[34:37], v[222:225], v[190:193], v[34:37]
	v_mfma_f32_16x16x32_bf16 v[22:25], v[214:217], v[198:201], v[22:25]
	v_mfma_f32_16x16x32_bf16 v[18:21], v[222:225], v[198:201], v[18:21]
	v_mfma_f32_16x16x32_bf16 v[6:9], v[214:217], v[206:209], v[6:9]
	v_mfma_f32_16x16x32_bf16 v[2:5], v[222:225], v[206:209], v[2:5]
	s_add_i32 s61, s61, 2
	s_cmp_gt_u32 s61, 29
	s_mov_b64 s[4:5], s[28:29]
	s_barrier
	s_cbranch_scc0 .LBB0_3881
	s_ashr_i32 s4, s58, 31
	s_lshr_b32 s4, s4, 29
	s_add_i32 s4, s58, s4
	s_ashr_i32 s4, s4, 3
	s_mul_i32 s5, s4, 0x900
	s_lshl_b32 s4, s4, 11
	s_lshl_b32 s27, s58, 8
	v_mul_f32_e32 v134, 0xbfb8aa3b, v126
	s_sub_i32 s4, s27, s4
	v_exp_f32_e32 v134, v134
	s_add_i32 s4, s4, s5
	v_add_u32_e32 v144, s4, v152
	v_lshl_or_b32 v140, s59, 7, v154
	v_ashrrev_i32_e32 v145, 31, v144
	v_ashrrev_i32_e32 v141, 31, v140
	v_lshlrev_b64 v[142:143], 11, v[144:145]
	v_add_f32_e32 v134, 1.0, v134
	v_lshl_add_u64 v[146:147], s[12:13], 0, v[142:143]
	v_lshlrev_b64 v[142:143], 1, v[140:141]
	v_rcp_f32_e32 v134, v134
	v_mul_f32_e32 v140, 0xbfb8aa3b, v127
	v_exp_f32_e32 v145, v140
	v_lshl_add_u64 v[140:141], v[146:147], 0, v[142:143]
	v_mul_f32_e32 v126, v126, v134
	v_mul_f32_e32 v122, v122, v126
	v_add_f32_e32 v126, 1.0, v145
	v_mul_f32_e32 v134, 0xbfb8aa3b, v128
	v_rcp_f32_e32 v126, v126
	v_exp_f32_e32 v134, v134
	v_mul_f32_e32 v145, 0xbfb8aa3b, v129
	v_exp_f32_e32 v145, v145
	v_mul_f32_e32 v126, v127, v126
	v_add_f32_e32 v127, 1.0, v134
	v_rcp_f32_e32 v127, v127
	v_add_f32_e32 v134, 1.0, v145
	v_rcp_f32_e32 v134, v134
	v_mul_f32_e32 v123, v123, v126
	v_mul_f32_e32 v126, v128, v127
	v_mul_f32_e32 v127, 0xbfb8aa3b, v118
	v_exp_f32_e32 v127, v127
	v_mul_f32_e32 v124, v124, v126
	v_mul_f32_e32 v126, v129, v134
	v_mul_f32_e32 v125, v125, v126
	v_cvt_pk_bf16_f32 v122, v122, v123
	v_cvt_pk_bf16_f32 v123, v124, v125
	v_add_f32_e32 v124, 1.0, v127
	v_rcp_f32_e32 v124, v124
	v_mul_f32_e32 v125, 0xbfb8aa3b, v119
	v_exp_f32_e32 v125, v125
	global_store_dwordx2 v[140:141], v[122:123], off
	v_mul_f32_e32 v118, v118, v124
	v_mul_f32_e32 v114, v114, v118
	v_add_f32_e32 v118, 1.0, v125
	v_mul_f32_e32 v122, 0xbfb8aa3b, v120
	v_rcp_f32_e32 v118, v118
	v_exp_f32_e32 v122, v122
	v_mul_f32_e32 v123, 0xbfb8aa3b, v121
	v_exp_f32_e32 v123, v123
	v_mul_f32_e32 v118, v119, v118
	v_add_f32_e32 v119, 1.0, v122
	v_rcp_f32_e32 v119, v119
	v_add_f32_e32 v122, 1.0, v123
	v_rcp_f32_e32 v122, v122
	v_mul_f32_e32 v115, v115, v118
	v_mul_f32_e32 v118, v120, v119
	v_mul_f32_e32 v116, v116, v118
	v_mul_f32_e32 v118, v121, v122
	v_mul_f32_e32 v117, v117, v118
	v_cvt_pk_bf16_f32 v114, v114, v115
	v_cvt_pk_bf16_f32 v115, v116, v117
	global_store_dwordx2 v[140:141], v[114:115], off offset:128
	v_mul_f32_e32 v115, 0xbfb8aa3b, v110
	v_exp_f32_e32 v116, v115
	v_mul_f32_e32 v117, 0xbfb8aa3b, v111
	v_exp_f32_e32 v117, v117
	v_or_b32_e32 v114, 16, v144
	v_add_f32_e32 v116, 1.0, v116
	v_rcp_f32_e32 v116, v116
	v_ashrrev_i32_e32 v115, 31, v114
	v_lshlrev_b64 v[114:115], 11, v[114:115]
	v_lshl_add_u64 v[114:115], s[12:13], 0, v[114:115]
	v_mul_f32_e32 v110, v110, v116
	v_mul_f32_e32 v106, v106, v110
	v_add_f32_e32 v110, 1.0, v117
	v_mul_f32_e32 v116, 0xbfb8aa3b, v112
	v_rcp_f32_e32 v110, v110
	v_exp_f32_e32 v116, v116
	v_mul_f32_e32 v117, 0xbfb8aa3b, v113
	v_exp_f32_e32 v117, v117
	v_mul_f32_e32 v110, v111, v110
	v_add_f32_e32 v111, 1.0, v116
	v_rcp_f32_e32 v111, v111
	v_add_f32_e32 v116, 1.0, v117
	v_rcp_f32_e32 v116, v116
	v_mul_f32_e32 v107, v107, v110
	v_mul_f32_e32 v110, v112, v111
	v_mul_f32_e32 v111, 0xbfb8aa3b, v102
	v_exp_f32_e32 v111, v111
	v_mul_f32_e32 v108, v108, v110
	v_mul_f32_e32 v110, v113, v116
	v_mul_f32_e32 v109, v109, v110
	v_cvt_pk_bf16_f32 v106, v106, v107
	v_cvt_pk_bf16_f32 v107, v108, v109
	v_add_f32_e32 v108, 1.0, v111
	v_rcp_f32_e32 v108, v108
	v_mul_f32_e32 v109, 0xbfb8aa3b, v103
	v_exp_f32_e32 v109, v109
	v_lshl_add_u64 v[114:115], v[114:115], 0, v[142:143]
	v_mul_f32_e32 v102, v102, v108
	global_store_dwordx2 v[114:115], v[106:107], off
	v_mul_f32_e32 v98, v98, v102
	v_add_f32_e32 v102, 1.0, v109
	v_mul_f32_e32 v106, 0xbfb8aa3b, v104
	v_rcp_f32_e32 v102, v102
	v_exp_f32_e32 v106, v106
	v_mul_f32_e32 v107, 0xbfb8aa3b, v105
	v_exp_f32_e32 v107, v107
	v_mul_f32_e32 v102, v103, v102
	v_add_f32_e32 v103, 1.0, v106
	v_rcp_f32_e32 v103, v103
	v_add_f32_e32 v106, 1.0, v107
	v_rcp_f32_e32 v106, v106
	v_mul_f32_e32 v99, v99, v102
	v_mul_f32_e32 v102, v104, v103
	v_mul_f32_e32 v100, v100, v102
	v_mul_f32_e32 v102, v105, v106
	v_mul_f32_e32 v101, v101, v102
	v_cvt_pk_bf16_f32 v98, v98, v99
	v_cvt_pk_bf16_f32 v99, v100, v101
	global_store_dwordx2 v[114:115], v[98:99], off offset:128
	v_mul_f32_e32 v99, 0xbfb8aa3b, v94
	v_exp_f32_e32 v100, v99
	v_mul_f32_e32 v101, 0xbfb8aa3b, v95
	v_exp_f32_e32 v101, v101
	v_or_b32_e32 v98, 32, v144
	v_add_f32_e32 v100, 1.0, v100
	v_rcp_f32_e32 v100, v100
	v_ashrrev_i32_e32 v99, 31, v98
	v_lshlrev_b64 v[98:99], 11, v[98:99]
	v_lshl_add_u64 v[98:99], s[12:13], 0, v[98:99]
	v_mul_f32_e32 v94, v94, v100
	v_mul_f32_e32 v90, v90, v94
	v_add_f32_e32 v94, 1.0, v101
	v_mul_f32_e32 v100, 0xbfb8aa3b, v96
	v_rcp_f32_e32 v94, v94
	v_exp_f32_e32 v100, v100
	v_mul_f32_e32 v101, 0xbfb8aa3b, v97
	v_exp_f32_e32 v101, v101
	v_mul_f32_e32 v94, v95, v94
	v_add_f32_e32 v95, 1.0, v100
	v_rcp_f32_e32 v95, v95
	v_add_f32_e32 v100, 1.0, v101
	v_rcp_f32_e32 v100, v100
	v_mul_f32_e32 v91, v91, v94
	v_mul_f32_e32 v94, v96, v95
	v_mul_f32_e32 v95, 0xbfb8aa3b, v86
	v_exp_f32_e32 v95, v95
	v_mul_f32_e32 v92, v92, v94
	v_mul_f32_e32 v94, v97, v100
	v_mul_f32_e32 v93, v93, v94
	v_cvt_pk_bf16_f32 v90, v90, v91
	v_cvt_pk_bf16_f32 v91, v92, v93
	v_add_f32_e32 v92, 1.0, v95
	v_rcp_f32_e32 v92, v92
	v_mul_f32_e32 v93, 0xbfb8aa3b, v87
	v_exp_f32_e32 v93, v93
	v_lshl_add_u64 v[98:99], v[98:99], 0, v[142:143]
	v_mul_f32_e32 v86, v86, v92
	global_store_dwordx2 v[98:99], v[90:91], off
	v_mul_f32_e32 v82, v82, v86
	v_add_f32_e32 v86, 1.0, v93
	v_mul_f32_e32 v90, 0xbfb8aa3b, v88
	v_rcp_f32_e32 v86, v86
	v_exp_f32_e32 v90, v90
	v_mul_f32_e32 v91, 0xbfb8aa3b, v89
	v_exp_f32_e32 v91, v91
	v_mul_f32_e32 v86, v87, v86
	v_add_f32_e32 v87, 1.0, v90
	v_rcp_f32_e32 v87, v87
	v_add_f32_e32 v90, 1.0, v91
	v_rcp_f32_e32 v90, v90
	v_mul_f32_e32 v83, v83, v86
	v_mul_f32_e32 v86, v88, v87
	v_mul_f32_e32 v84, v84, v86
	v_mul_f32_e32 v86, v89, v90
	v_mul_f32_e32 v85, v85, v86
	v_cvt_pk_bf16_f32 v82, v82, v83
	v_cvt_pk_bf16_f32 v83, v84, v85
	global_store_dwordx2 v[98:99], v[82:83], off offset:128
	v_mul_f32_e32 v83, 0xbfb8aa3b, v78
	v_exp_f32_e32 v84, v83
	v_mul_f32_e32 v85, 0xbfb8aa3b, v79
	v_exp_f32_e32 v85, v85
	v_or_b32_e32 v82, 48, v144
	v_add_f32_e32 v84, 1.0, v84
	v_rcp_f32_e32 v84, v84
	v_ashrrev_i32_e32 v83, 31, v82
	v_lshlrev_b64 v[82:83], 11, v[82:83]
	v_lshl_add_u64 v[82:83], s[12:13], 0, v[82:83]
	v_mul_f32_e32 v78, v78, v84
	v_mul_f32_e32 v74, v74, v78
	v_add_f32_e32 v78, 1.0, v85
	v_mul_f32_e32 v84, 0xbfb8aa3b, v80
	v_rcp_f32_e32 v78, v78
	v_exp_f32_e32 v84, v84
	v_mul_f32_e32 v85, 0xbfb8aa3b, v81
	v_exp_f32_e32 v85, v85
	v_mul_f32_e32 v78, v79, v78
	v_add_f32_e32 v79, 1.0, v84
	v_rcp_f32_e32 v79, v79
	v_add_f32_e32 v84, 1.0, v85
	v_rcp_f32_e32 v84, v84
	v_mul_f32_e32 v75, v75, v78
	v_mul_f32_e32 v78, v80, v79
	v_mul_f32_e32 v79, 0xbfb8aa3b, v70
	v_exp_f32_e32 v79, v79
	v_mul_f32_e32 v76, v76, v78
	v_mul_f32_e32 v78, v81, v84
	v_mul_f32_e32 v77, v77, v78
	v_cvt_pk_bf16_f32 v74, v74, v75
	v_cvt_pk_bf16_f32 v75, v76, v77
	v_add_f32_e32 v76, 1.0, v79
	v_rcp_f32_e32 v76, v76
	v_mul_f32_e32 v77, 0xbfb8aa3b, v71
	v_exp_f32_e32 v77, v77
	v_lshl_add_u64 v[82:83], v[82:83], 0, v[142:143]
	v_mul_f32_e32 v70, v70, v76
	global_store_dwordx2 v[82:83], v[74:75], off
	v_mul_f32_e32 v66, v66, v70
	v_add_f32_e32 v70, 1.0, v77
	v_mul_f32_e32 v74, 0xbfb8aa3b, v72
	v_rcp_f32_e32 v70, v70
	v_exp_f32_e32 v74, v74
	v_mul_f32_e32 v75, 0xbfb8aa3b, v73
	v_exp_f32_e32 v75, v75
	v_mul_f32_e32 v70, v71, v70
	v_add_f32_e32 v71, 1.0, v74
	v_rcp_f32_e32 v71, v71
	v_add_f32_e32 v74, 1.0, v75
	v_rcp_f32_e32 v74, v74
	v_mul_f32_e32 v67, v67, v70
	v_mul_f32_e32 v70, v72, v71
	v_mul_f32_e32 v68, v68, v70
	v_mul_f32_e32 v70, v73, v74
	v_mul_f32_e32 v69, v69, v70
	v_mul_f32_e32 v70, 0xbfb8aa3b, v62
	v_exp_f32_e32 v70, v70
	v_cvt_pk_bf16_f32 v66, v66, v67
	v_cvt_pk_bf16_f32 v67, v68, v69
	global_store_dwordx2 v[82:83], v[66:67], off offset:128
	v_add_f32_e32 v66, 1.0, v70
	v_rcp_f32_e32 v68, v66
	v_mul_f32_e32 v66, 0xbfb8aa3b, v63
	v_exp_f32_e32 v69, v66
	v_lshl_add_u64 v[66:67], v[140:141], 0, s[18:19]
	v_mul_f32_e32 v62, v62, v68
	v_mul_f32_e32 v58, v58, v62
	v_add_f32_e32 v62, 1.0, v69
	v_mul_f32_e32 v68, 0xbfb8aa3b, v64
	v_rcp_f32_e32 v62, v62
	v_exp_f32_e32 v68, v68
	v_mul_f32_e32 v69, 0xbfb8aa3b, v65
	v_exp_f32_e32 v69, v69
	v_mul_f32_e32 v62, v63, v62
	v_add_f32_e32 v63, 1.0, v68
	v_rcp_f32_e32 v63, v63
	v_add_f32_e32 v68, 1.0, v69
	v_rcp_f32_e32 v68, v68
	v_mul_f32_e32 v59, v59, v62
	v_mul_f32_e32 v62, v64, v63
	v_mul_f32_e32 v60, v60, v62
	v_mul_f32_e32 v62, v65, v68
	v_mul_f32_e32 v61, v61, v62
	v_cvt_pk_bf16_f32 v58, v58, v59
	v_cvt_pk_bf16_f32 v59, v60, v61
	v_mul_f32_e32 v60, 0xbfb8aa3b, v54
	v_exp_f32_e32 v62, v60
	v_mul_f32_e32 v63, 0xbfb8aa3b, v55
	v_exp_f32_e32 v63, v63
	v_add_co_u32_e32 v60, vcc, s53, v140
	v_add_f32_e32 v62, 1.0, v62
	v_rcp_f32_e32 v62, v62
	v_addc_co_u32_e32 v61, vcc, 0, v141, vcc
	global_store_dwordx2 v[60:61], v[58:59], off
	v_mul_f32_e32 v54, v54, v62
	v_mul_f32_e32 v50, v50, v54
	v_add_f32_e32 v54, 1.0, v63
	v_mul_f32_e32 v58, 0xbfb8aa3b, v56
	v_rcp_f32_e32 v54, v54
	v_exp_f32_e32 v58, v58
	v_mul_f32_e32 v59, 0xbfb8aa3b, v57
	v_exp_f32_e32 v59, v59
	v_mul_f32_e32 v54, v55, v54
	v_add_f32_e32 v55, 1.0, v58
	v_rcp_f32_e32 v55, v55
	v_add_f32_e32 v58, 1.0, v59
	v_rcp_f32_e32 v58, v58
	v_mul_f32_e32 v51, v51, v54
	v_mul_f32_e32 v54, v56, v55
	v_mul_f32_e32 v52, v52, v54
	v_mul_f32_e32 v54, v57, v58
	v_mul_f32_e32 v53, v53, v54
	v_mul_f32_e32 v54, 0xbfb8aa3b, v46
	v_exp_f32_e32 v54, v54
	v_cvt_pk_bf16_f32 v50, v50, v51
	v_cvt_pk_bf16_f32 v51, v52, v53
	global_store_dwordx2 v[66:67], v[50:51], off offset:128
	v_add_f32_e32 v50, 1.0, v54
	v_rcp_f32_e32 v52, v50
	v_mul_f32_e32 v50, 0xbfb8aa3b, v47
	v_exp_f32_e32 v53, v50
	v_lshl_add_u64 v[50:51], v[140:141], 0, s[20:21]
	v_mul_f32_e32 v46, v46, v52
	v_mul_f32_e32 v42, v42, v46
	v_add_f32_e32 v46, 1.0, v53
	v_mul_f32_e32 v52, 0xbfb8aa3b, v48
	v_rcp_f32_e32 v46, v46
	v_exp_f32_e32 v52, v52
	v_mul_f32_e32 v53, 0xbfb8aa3b, v49
	v_exp_f32_e32 v53, v53
	v_mul_f32_e32 v46, v47, v46
	v_add_f32_e32 v47, 1.0, v52
	v_rcp_f32_e32 v47, v47
	v_add_f32_e32 v52, 1.0, v53
	v_rcp_f32_e32 v52, v52
	v_mul_f32_e32 v43, v43, v46
	v_mul_f32_e32 v46, v48, v47
	v_mul_f32_e32 v44, v44, v46
	v_mul_f32_e32 v46, v49, v52
	v_mul_f32_e32 v45, v45, v46
	v_cvt_pk_bf16_f32 v42, v42, v43
	v_cvt_pk_bf16_f32 v43, v44, v45
	v_mul_f32_e32 v44, 0xbfb8aa3b, v38
	v_exp_f32_e32 v46, v44
	v_mul_f32_e32 v47, 0xbfb8aa3b, v39
	v_exp_f32_e32 v47, v47
	v_add_co_u32_e32 v44, vcc, s54, v140
	v_add_f32_e32 v46, 1.0, v46
	v_rcp_f32_e32 v46, v46
	v_addc_co_u32_e32 v45, vcc, 0, v141, vcc
	global_store_dwordx2 v[44:45], v[42:43], off
	v_mul_f32_e32 v38, v38, v46
	v_mul_f32_e32 v34, v34, v38
	v_add_f32_e32 v38, 1.0, v47
	v_mul_f32_e32 v42, 0xbfb8aa3b, v40
	v_rcp_f32_e32 v38, v38
	v_exp_f32_e32 v42, v42
	v_mul_f32_e32 v43, 0xbfb8aa3b, v41
	v_exp_f32_e32 v43, v43
	v_mul_f32_e32 v38, v39, v38
	v_add_f32_e32 v39, 1.0, v42
	v_rcp_f32_e32 v39, v39
	v_add_f32_e32 v42, 1.0, v43
	v_rcp_f32_e32 v42, v42
	v_mul_f32_e32 v35, v35, v38
	v_mul_f32_e32 v38, v40, v39
	v_mul_f32_e32 v36, v36, v38
	v_mul_f32_e32 v38, v41, v42
	v_mul_f32_e32 v37, v37, v38
	v_mul_f32_e32 v38, 0xbfb8aa3b, v30
	v_exp_f32_e32 v38, v38
	v_cvt_pk_bf16_f32 v34, v34, v35
	v_cvt_pk_bf16_f32 v35, v36, v37
	global_store_dwordx2 v[50:51], v[34:35], off offset:128
	v_add_f32_e32 v34, 1.0, v38
	v_rcp_f32_e32 v36, v34
	v_mul_f32_e32 v34, 0xbfb8aa3b, v31
	v_exp_f32_e32 v37, v34
	v_lshl_add_u64 v[34:35], v[140:141], 0, s[22:23]
	v_mul_f32_e32 v30, v30, v36
	v_mul_f32_e32 v26, v26, v30
	v_add_f32_e32 v30, 1.0, v37
	v_mul_f32_e32 v36, 0xbfb8aa3b, v32
	v_rcp_f32_e32 v30, v30
	v_exp_f32_e32 v36, v36
	v_mul_f32_e32 v37, 0xbfb8aa3b, v33
	v_exp_f32_e32 v37, v37
	v_mul_f32_e32 v30, v31, v30
	v_add_f32_e32 v31, 1.0, v36
	v_rcp_f32_e32 v31, v31
	v_add_f32_e32 v36, 1.0, v37
	v_rcp_f32_e32 v36, v36
	v_mul_f32_e32 v27, v27, v30
	v_mul_f32_e32 v30, v32, v31
	v_mul_f32_e32 v28, v28, v30
	v_mul_f32_e32 v30, v33, v36
	v_mul_f32_e32 v29, v29, v30
	v_cvt_pk_bf16_f32 v26, v26, v27
	v_cvt_pk_bf16_f32 v27, v28, v29
	v_mul_f32_e32 v28, 0xbfb8aa3b, v22
	v_exp_f32_e32 v30, v28
	v_mul_f32_e32 v31, 0xbfb8aa3b, v23
	v_exp_f32_e32 v31, v31
	v_add_co_u32_e32 v28, vcc, s55, v140
	v_add_f32_e32 v30, 1.0, v30
	v_rcp_f32_e32 v30, v30
	v_addc_co_u32_e32 v29, vcc, 0, v141, vcc
	global_store_dwordx2 v[28:29], v[26:27], off
	v_mul_f32_e32 v22, v22, v30
	v_mul_f32_e32 v18, v18, v22
	v_add_f32_e32 v22, 1.0, v31
	v_mul_f32_e32 v26, 0xbfb8aa3b, v24
	v_rcp_f32_e32 v22, v22
	v_exp_f32_e32 v26, v26
	v_mul_f32_e32 v27, 0xbfb8aa3b, v25
	v_exp_f32_e32 v27, v27
	v_mul_f32_e32 v22, v23, v22
	v_add_f32_e32 v23, 1.0, v26
	v_rcp_f32_e32 v23, v23
	v_add_f32_e32 v26, 1.0, v27
	v_rcp_f32_e32 v26, v26
	v_mul_f32_e32 v19, v19, v22
	v_mul_f32_e32 v22, v24, v23
	v_mul_f32_e32 v20, v20, v22
	v_mul_f32_e32 v22, v25, v26
	v_mul_f32_e32 v21, v21, v22
	v_mul_f32_e32 v22, 0xbfb8aa3b, v14
	v_exp_f32_e32 v22, v22
	v_cvt_pk_bf16_f32 v18, v18, v19
	v_cvt_pk_bf16_f32 v19, v20, v21
	global_store_dwordx2 v[34:35], v[18:19], off offset:128
	v_add_f32_e32 v18, 1.0, v22
	v_rcp_f32_e32 v20, v18
	v_mul_f32_e32 v18, 0xbfb8aa3b, v15
	v_exp_f32_e32 v21, v18
	v_lshl_add_u64 v[18:19], v[140:141], 0, s[24:25]
	v_mul_f32_e32 v14, v14, v20
	v_mul_f32_e32 v10, v10, v14
	v_add_f32_e32 v14, 1.0, v21
	v_mul_f32_e32 v20, 0xbfb8aa3b, v16
	v_rcp_f32_e32 v14, v14
	v_exp_f32_e32 v20, v20
	v_mul_f32_e32 v21, 0xbfb8aa3b, v17
	v_exp_f32_e32 v21, v21
	v_mul_f32_e32 v14, v15, v14
	v_add_f32_e32 v15, 1.0, v20
	v_rcp_f32_e32 v15, v15
	v_add_f32_e32 v20, 1.0, v21
	v_rcp_f32_e32 v20, v20
	v_mul_f32_e32 v11, v11, v14
	v_mul_f32_e32 v14, v16, v15
	v_mul_f32_e32 v12, v12, v14
	v_mul_f32_e32 v14, v17, v20
	v_mul_f32_e32 v13, v13, v14
	v_cvt_pk_bf16_f32 v10, v10, v11
	v_cvt_pk_bf16_f32 v11, v12, v13
	v_mul_f32_e32 v12, 0xbfb8aa3b, v6
	v_exp_f32_e32 v14, v12
	v_mul_f32_e32 v15, 0xbfb8aa3b, v7
	v_exp_f32_e32 v15, v15
	v_add_co_u32_e32 v12, vcc, s56, v140
	v_add_f32_e32 v14, 1.0, v14
	v_rcp_f32_e32 v14, v14
	v_addc_co_u32_e32 v13, vcc, 0, v141, vcc
	global_store_dwordx2 v[12:13], v[10:11], off
	v_mul_f32_e32 v6, v6, v14
	v_mul_f32_e32 v2, v2, v6
	v_add_f32_e32 v6, 1.0, v15
	v_mul_f32_e32 v10, 0xbfb8aa3b, v8
	v_rcp_f32_e32 v6, v6
	v_exp_f32_e32 v10, v10
	v_mul_f32_e32 v11, 0xbfb8aa3b, v9
	v_exp_f32_e32 v11, v11
	v_mul_f32_e32 v6, v7, v6
	v_add_f32_e32 v7, 1.0, v10
	v_rcp_f32_e32 v7, v7
	v_add_f32_e32 v10, 1.0, v11
	v_rcp_f32_e32 v10, v10
	v_mul_f32_e32 v3, v3, v6
	v_mul_f32_e32 v6, v8, v7
	v_mul_f32_e32 v4, v4, v6
	v_mul_f32_e32 v6, v9, v10
	s_and_b64 vcc, exec, s[0:1]
	v_mov_b32_e32 v141, v158
	v_mov_b32_e32 v140, v159
	v_mov_b32_e32 v142, v160
	v_mov_b32_e32 v144, v161
	s_mov_b32 s59, s26
	s_mov_b32 s58, s57
	s_mov_b64 s[28:29], s[2:3]
	v_mul_f32_e32 v5, v5, v6
	v_cvt_pk_bf16_f32 v2, v2, v3
	v_cvt_pk_bf16_f32 v3, v4, v5
	global_store_dwordx2 v[18:19], v[2:3], off offset:128
	s_cbranch_vccz .LBB0_3874
	s_waitcnt vmcnt(0)
	v_readlane_b32 s52, v250, 40
	s_cmpk_gt_u32 s37, 0xff
	v_readlane_b32 s53, v250, 41
	v_readlane_b32 s54, v250, 42
	v_readlane_b32 s55, v250, 43
	s_cbranch_scc1 .LBB0_3885
	s_barrier

.LBB0_3887:
	s_cmp_gt_i32 s55, 23
	s_cselect_b64 s[0:1], -1, 0
	s_and_b64 s[2:3], s[6:7], s[0:1]
	s_andn2_b64 vcc, exec, s[2:3]
	s_cbranch_vccnz .LBB0_3937
	s_waitcnt vmcnt(0)
	s_barrier
	s_setprio 0
	s_mov_b64 s[2:3], exec
	v_readlane_b32 s4, v250, 5
	v_readlane_b32 s5, v250, 6
	s_and_b64 s[4:5], s[2:3], s[4:5]
	s_mov_b64 exec, s[4:5]
	s_cbranch_execz .LBB0_3936
	s_add_i32 s4, 0, 0x27ff0
	v_mov_b32_e32 v1, s4
	s_waitcnt vmcnt(0) expcnt(0) lgkmcnt(0)
	ds_read_b32 v3, v1
	s_add_i32 s4, 0, 0x27ff4
	v_mov_b32_e32 v1, s4
	ds_read_b32 v1, v1
	s_waitcnt lgkmcnt(1)
	v_cmp_ne_u32_e32 vcc, 0, v3
	s_cbranch_vccnz .LBB0_3904
	v_readlane_b32 s4, v250, 2
	v_readlane_b32 s5, v250, 3
	s_load_dwordx2 s[8:9], s[4:5], 0x4
	s_add_u32 s4, s52, 0x1000
	s_addc_u32 s5, s53, 0
	s_add_u32 s6, s52, 0x1100
	s_addc_u32 s7, s53, 0
	v_readlane_b32 s10, v250, 1
	s_waitcnt lgkmcnt(0)
	s_mul_i32 s18, s8, s10
	s_add_u32 s8, s52, 0x1200
	s_mul_i32 s18, s18, s9
	s_addc_u32 s9, s53, 0
	s_add_u32 s10, s52, 0x1300
	s_addc_u32 s11, s53, 0
	s_mov_b32 s19, 1
	v_mov_b32_e32 v17, 0
	s_branch .LBB0_3892

.LBB0_3937:
	s_cmp_lt_i32 s54, 24
	s_cselect_b64 s[6:7], -1, 0
	s_and_b64 s[0:1], s[6:7], s[0:1]
	s_andn2_b64 vcc, exec, s[0:1]
	s_cbranch_vccnz .LBB0_3955
	v_mov_b32_e32 v1, v0
	s_waitcnt vmcnt(5)
	v_mov_b32_e32 v2, v248
	v_readlane_b32 s28, v250, 0
	v_readlane_b32 s0, v250, 39
	v_readlane_b32 s29, v250, 1
	s_mov_b64 s[2:3], s[90:91]
	s_mov_b64 s[0:1], s[52:53]
	s_cmpk_gt_i32 s28, 0x3ff
	v_readfirstlane_b32 s30, v0
	s_barrier
	s_cbranch_scc1 .LBB0_3954
	v_lshlrev_b32_e32 v1, 4, v0
	v_or_b32_e32 v10, 0x2000, v1
	v_and_b32_e32 v4, 32, v0
	v_lshrrev_b32_e32 v2, 7, v10
	v_bfe_u32 v13, v0, 2, 4
	s_movk_i32 s2, 0x70
	v_bitop3_b32 v11, v1, v4, 48 bitop3:0x6c
	v_and_b32_e32 v12, 64, v0
	s_add_u32 s31, s0, 0x32d40000
	v_and_or_b32 v3, v2, s2, v13
	v_or_b32_e32 v1, v11, v12
	s_addc_u32 s33, s1, 0
	v_lshl_or_b32 v130, v3, 11, v1
	v_lshrrev_b32_e32 v3, 5, v0
	v_lshrrev_b32_e32 v5, 1, v0
	s_add_u32 s34, s0, 0x1e940000
	v_and_b32_e32 v3, 4, v3
	v_bfe_u32 v4, v0, 2, 2
	v_and_b32_e32 v14, 24, v5
	s_addc_u32 s35, s1, 0
	v_or3_b32 v3, v3, v4, v14
	s_movk_i32 s2, 0x60
	s_ashr_i32 s37, s28, 31
	v_and_or_b32 v2, v2, s2, v3
	s_lshr_b32 s2, s37, 29
	s_add_i32 s2, s28, s2
	s_lshr_b32 s4, s30, 6
	s_ashr_i32 s5, s2, 3
	s_and_b32 s2, s2, -8
	s_lshr_b32 s3, s30, 8
	s_lshl_b32 s36, s4, 10
	s_sub_i32 s2, s28, s2
	s_cmp_lt_i32 s2, 0
	s_movk_i32 s38, 0x81
	s_cselect_b32 s8, s38, 0x80
	s_mul_i32 s2, s8, s2
	s_add_i32 s2, s2, s5
	s_ashr_i32 s5, s2, 31
	s_lshr_b32 s5, s5, 26
	s_add_i32 s5, s2, s5
	s_ashr_i32 s8, s5, 6
	s_lshl_b32 s10, s8, 3
	v_lshl_or_b32 v132, v2, 11, v1
	v_lshrrev_b32_e32 v2, 3, v0
	s_sub_i32 s8, 0x80, s10
	v_and_or_b32 v4, v2, 48, v13
	s_min_u32 s11, s8, 8
	s_andn2_b32 s5, s5, 63
	v_lshl_or_b32 v134, v4, 11, v1
	s_sub_i32 s5, s2, s5
	v_cvt_f32_ubyte0_e32 v4, s11
	v_and_or_b32 v2, v2, 32, v3
	v_cvt_f32_i32_e32 v3, s5
	v_rcp_iflag_f32_e32 v5, v4
	v_lshl_or_b32 v136, v2, 11, v1
	s_ashr_i32 s2, s5, 30
	s_or_b32 s2, s2, 1
	v_mul_f32_e32 v1, v3, v5
	v_trunc_f32_e32 v1, v1
	v_fma_f32 v2, -v1, v4, v3
	v_cvt_i32_f32_e32 v1, v1
	v_cmp_ge_f32_e64 s[8:9], |v2|, v4
	s_and_b64 s[8:9], s[8:9], exec
	s_cselect_b32 s2, s2, 0
	v_readfirstlane_b32 s8, v1
	s_add_i32 s2, s8, s2
	s_mul_i32 s8, s2, s11
	s_sub_i32 s5, s5, s8
	s_sext_i32_i8 s5, s5
	s_add_i32 s54, s10, s5
	s_lshr_b32 s5, s54, 29
	s_add_i32 s5, s54, s5
	s_ashr_i32 s8, s5, 3
	s_lshl_b32 s9, s54, 8
	s_lshl_b32 s10, s8, 11
	s_mul_i32 s5, s8, 0x900
	s_sub_i32 s9, s9, s10
	s_add_i32 s10, s9, s5
	s_ashr_i32 s11, s10, 31
	s_lshl_b64 s[10:11], s[10:11], 11
	s_add_u32 s22, s31, s10
	s_addc_u32 s23, s33, s11
	s_ashr_i32 s9, s8, 31
	s_bfe_i64 s[10:11], s[2:3], 0x80000
	s_lshl_b64 s[10:11], s[10:11], 19
	s_lshl_b64 s[8:9], s[8:9], 22
	s_add_u32 s5, s34, s8
	s_addc_u32 s8, s35, s9
	s_add_u32 s24, s5, s10
	s_addc_u32 s25, s8, s11
	s_add_i32 s39, s36, 0
	s_add_i32 m0, s39, 0x10000
	s_add_i32 s40, s39, 0x2000
	global_load_lds_dwordx4 v136, s[24:25]
	s_add_i32 m0, s39, 0x12000
	s_add_u32 s8, s24, 0x40000
	global_load_lds_dwordx4 v132, s[24:25]
	s_mov_b32 m0, s39
	s_addc_u32 s9, s25, 0
	global_load_lds_dwordx4 v134, s[22:23]
	s_mov_b32 m0, s40
	v_mov_b32_e32 v137, 0
	global_load_lds_dwordx4 v130, s[22:23]
	s_add_i32 m0, s39, 0x14000
	v_mov_b32_e32 v133, v137
	global_load_lds_dwordx4 v136, s[8:9]
	s_add_i32 m0, s39, 0x16000
	v_mov_b32_e32 v135, v137
	global_load_lds_dwordx4 v132, s[8:9]
	s_add_u32 s8, s22, 0x40000
	s_addc_u32 s9, s23, 0
	s_add_i32 s41, s39, 0x4000
	s_mov_b32 m0, s41
	s_add_i32 s42, s39, 0x6000
	global_load_lds_dwordx4 v134, s[8:9]
	s_mov_b32 m0, s42
	v_mov_b32_e32 v131, v137
	global_load_lds_dwordx4 v130, s[8:9]
	s_mov_b32 s43, 0
	s_waitcnt vmcnt(0)
	v_lshl_add_u64 v[8:9], s[24:25], 0, v[136:137]
	v_lshl_add_u64 v[6:7], s[24:25], 0, v[132:133]
	v_lshl_add_u64 v[4:5], s[22:23], 0, v[134:135]
	s_setprio 1
	s_cmp_lg_u32 s3, 1
	v_lshl_add_u64 v[2:3], s[22:23], 0, v[130:131]
	s_cbranch_scc1 .LBB0_3941
	s_barrier
	s_setprio 0

.LBB0_3949:
	ds_read_b128 v[154:157], v150
	ds_read_b128 v[158:161], v150 offset:1024
	ds_read_b128 v[162:165], v150 offset:2048
	ds_read_b128 v[166:169], v150 offset:3072
	s_add_u32 s24, s22, 0xfffc0080
	s_addc_u32 s25, s23, -1
	s_cmp_eq_u32 s57, 12
	s_cselect_b32 s27, s3, s25
	s_cselect_b32 s26, s2, s24
	s_cselect_b32 s25, s5, s56
	s_cselect_b32 s24, s4, s21
	v_lshl_add_u64 v[146:147], s[22:23], 0, v[138:139]
	s_add_i32 m0, s39, 0xc000
	ds_read_b128 v[170:173], v151
	ds_read_b128 v[174:177], v151 offset:1024
	ds_read_b128 v[178:181], v151 offset:2048
	ds_read_b128 v[182:185], v151 offset:3072
	ds_read_b128 v[186:189], v151 offset:4096
	ds_read_b128 v[190:193], v151 offset:5120
	ds_read_b128 v[194:197], v151 offset:6144
	ds_read_b128 v[198:201], v151 offset:7168
	global_load_lds_dwordx4 v[146:147], off
	v_lshl_add_u64 v[146:147], s[22:23], 0, v[140:141]
	s_add_i32 m0, s39, 0xe000
	s_nop 0
	global_load_lds_dwordx4 v[146:147], off
	s_waitcnt lgkmcnt(8)
	s_barrier
	s_waitcnt lgkmcnt(0)
	s_waitcnt lgkmcnt(0)
	v_mfma_f32_16x16x32_bf16 v[126:129], v[154:157], v[170:173], v[126:129]
	v_mfma_f32_16x16x32_bf16 v[122:125], v[162:165], v[170:173], v[122:125]
	v_mfma_f32_16x16x32_bf16 v[114:117], v[154:157], v[178:181], v[114:117]
	v_mfma_f32_16x16x32_bf16 v[106:109], v[162:165], v[178:181], v[106:109]
	v_mfma_f32_16x16x32_bf16 v[98:101], v[154:157], v[186:189], v[98:101]
	v_mfma_f32_16x16x32_bf16 v[90:93], v[162:165], v[186:189], v[90:93]
	v_mfma_f32_16x16x32_bf16 v[82:85], v[154:157], v[194:197], v[82:85]
	v_mfma_f32_16x16x32_bf16 v[74:77], v[162:165], v[194:197], v[74:77]
	v_mfma_f32_16x16x32_bf16 v[126:129], v[158:161], v[174:177], v[126:129]
	v_mfma_f32_16x16x32_bf16 v[122:125], v[166:169], v[174:177], v[122:125]
	v_mfma_f32_16x16x32_bf16 v[114:117], v[158:161], v[182:185], v[114:117]
	v_mfma_f32_16x16x32_bf16 v[106:109], v[166:169], v[182:185], v[106:109]
	v_mfma_f32_16x16x32_bf16 v[98:101], v[158:161], v[190:193], v[98:101]
	v_mfma_f32_16x16x32_bf16 v[90:93], v[166:169], v[190:193], v[90:93]
	v_mfma_f32_16x16x32_bf16 v[82:85], v[158:161], v[198:201], v[82:85]
	v_mfma_f32_16x16x32_bf16 v[74:77], v[166:169], v[198:201], v[74:77]
	s_barrier
	s_add_i32 s58, s47, s36
	v_lshl_add_u64 v[146:147], s[24:25], 0, v[136:137]
	s_mov_b32 m0, s58
	ds_read_b128 v[202:205], v152
	ds_read_b128 v[206:209], v152 offset:1024
	ds_read_b128 v[210:213], v152 offset:2048
	ds_read_b128 v[214:217], v152 offset:3072
	global_load_lds_dwordx4 v[146:147], off
	v_lshl_add_u64 v[218:219], s[24:25], 0, v[132:133]
	s_add_i32 m0, s58, 0x2000
	s_nop 0
	global_load_lds_dwordx4 v[218:219], off
	s_barrier
	s_waitcnt lgkmcnt(0)
	s_waitcnt lgkmcnt(0)
	v_mfma_f32_16x16x32_bf16 v[118:121], v[202:205], v[170:173], v[118:121]
	v_mfma_f32_16x16x32_bf16 v[110:113], v[210:213], v[170:173], v[110:113]
	v_mfma_f32_16x16x32_bf16 v[102:105], v[202:205], v[178:181], v[102:105]
	v_mfma_f32_16x16x32_bf16 v[94:97], v[210:213], v[178:181], v[94:97]
	v_mfma_f32_16x16x32_bf16 v[86:89], v[202:205], v[186:189], v[86:89]
	v_mfma_f32_16x16x32_bf16 v[78:81], v[210:213], v[186:189], v[78:81]
	v_mfma_f32_16x16x32_bf16 v[70:73], v[202:205], v[194:197], v[70:73]
	v_mfma_f32_16x16x32_bf16 v[66:69], v[210:213], v[194:197], v[66:69]
	v_mfma_f32_16x16x32_bf16 v[118:121], v[206:209], v[174:177], v[118:121]
	v_mfma_f32_16x16x32_bf16 v[110:113], v[214:217], v[174:177], v[110:113]
	v_mfma_f32_16x16x32_bf16 v[102:105], v[206:209], v[182:185], v[102:105]
	v_mfma_f32_16x16x32_bf16 v[94:97], v[214:217], v[182:185], v[94:97]
	v_mfma_f32_16x16x32_bf16 v[86:89], v[206:209], v[190:193], v[86:89]
	v_mfma_f32_16x16x32_bf16 v[78:81], v[214:217], v[190:193], v[78:81]
	v_mfma_f32_16x16x32_bf16 v[70:73], v[206:209], v[198:201], v[70:73]
	v_mfma_f32_16x16x32_bf16 v[66:69], v[214:217], v[198:201], v[66:69]
	s_mov_b32 m0, s39
	v_lshl_add_u64 v[220:221], s[26:27], 0, v[134:135]
	s_barrier
	ds_read_b128 v[170:173], v151 offset:16384
	ds_read_b128 v[174:177], v151 offset:17408
	ds_read_b128 v[178:181], v151 offset:18432
	ds_read_b128 v[182:185], v151 offset:19456
	ds_read_b128 v[186:189], v151 offset:20480
	ds_read_b128 v[190:193], v151 offset:21504
	ds_read_b128 v[194:197], v151 offset:22528
	ds_read_b128 v[198:201], v151 offset:23552
	global_load_lds_dwordx4 v[220:221], off
	v_lshl_add_u64 v[222:223], s[26:27], 0, v[130:131]
	s_mov_b32 m0, s40
	s_nop 0
	global_load_lds_dwordx4 v[222:223], off
	s_barrier
	s_waitcnt lgkmcnt(0)
	s_waitcnt lgkmcnt(0)
	v_mfma_f32_16x16x32_bf16 v[62:65], v[154:157], v[170:173], v[62:65]
	v_mfma_f32_16x16x32_bf16 v[58:61], v[162:165], v[170:173], v[58:61]
	v_mfma_f32_16x16x32_bf16 v[54:57], v[154:157], v[178:181], v[54:57]
	v_mfma_f32_16x16x32_bf16 v[46:49], v[162:165], v[178:181], v[46:49]
	v_mfma_f32_16x16x32_bf16 v[38:41], v[154:157], v[186:189], v[38:41]
	v_mfma_f32_16x16x32_bf16 v[30:33], v[162:165], v[186:189], v[30:33]
	v_mfma_f32_16x16x32_bf16 v[22:25], v[154:157], v[194:197], v[22:25]
	v_mfma_f32_16x16x32_bf16 v[14:17], v[162:165], v[194:197], v[14:17]
	v_mfma_f32_16x16x32_bf16 v[62:65], v[158:161], v[174:177], v[62:65]
	v_mfma_f32_16x16x32_bf16 v[58:61], v[166:169], v[174:177], v[58:61]
	v_mfma_f32_16x16x32_bf16 v[54:57], v[158:161], v[182:185], v[54:57]
	v_mfma_f32_16x16x32_bf16 v[46:49], v[166:169], v[182:185], v[46:49]
	v_mfma_f32_16x16x32_bf16 v[38:41], v[158:161], v[190:193], v[38:41]
	v_mfma_f32_16x16x32_bf16 v[30:33], v[166:169], v[190:193], v[30:33]
	v_mfma_f32_16x16x32_bf16 v[22:25], v[158:161], v[198:201], v[22:25]
	v_mfma_f32_16x16x32_bf16 v[14:17], v[166:169], v[198:201], v[14:17]
	s_barrier
	s_add_u32 s58, s24, 0x40000
	s_addc_u32 s59, s25, 0
	s_add_i32 s60, s48, s36
	v_lshl_add_u64 v[154:155], s[58:59], 0, v[136:137]
	s_mov_b32 m0, s60
	s_nop 0
	global_load_lds_dwordx4 v[154:155], off
	v_lshl_add_u64 v[154:155], s[58:59], 0, v[132:133]
	s_add_i32 m0, s60, 0x2000
	s_nop 0
	global_load_lds_dwordx4 v[154:155], off
	s_waitcnt vmcnt(6)
	s_barrier
	v_mfma_f32_16x16x32_bf16 v[50:53], v[202:205], v[170:173], v[50:53]
	v_mfma_f32_16x16x32_bf16 v[42:45], v[210:213], v[170:173], v[42:45]
	v_mfma_f32_16x16x32_bf16 v[34:37], v[202:205], v[178:181], v[34:37]
	v_mfma_f32_16x16x32_bf16 v[26:29], v[210:213], v[178:181], v[26:29]
	v_mfma_f32_16x16x32_bf16 v[18:21], v[202:205], v[186:189], v[18:21]
	v_mfma_f32_16x16x32_bf16 v[10:13], v[210:213], v[186:189], v[10:13]
	v_mfma_f32_16x16x32_bf16 v[6:9], v[202:205], v[194:197], v[6:9]
	v_mfma_f32_16x16x32_bf16 v[2:5], v[210:213], v[194:197], v[2:5]
	v_mfma_f32_16x16x32_bf16 v[50:53], v[206:209], v[174:177], v[50:53]
	v_mfma_f32_16x16x32_bf16 v[42:45], v[214:217], v[174:177], v[42:45]
	v_mfma_f32_16x16x32_bf16 v[34:37], v[206:209], v[182:185], v[34:37]
	v_mfma_f32_16x16x32_bf16 v[26:29], v[214:217], v[182:185], v[26:29]
	v_mfma_f32_16x16x32_bf16 v[18:21], v[206:209], v[190:193], v[18:21]
	v_mfma_f32_16x16x32_bf16 v[10:13], v[214:217], v[190:193], v[10:13]
	v_mfma_f32_16x16x32_bf16 v[6:9], v[206:209], v[198:201], v[6:9]
	v_mfma_f32_16x16x32_bf16 v[2:5], v[214:217], v[198:201], v[2:5]
	s_add_i32 s58, 0, 0x18000
	v_add_u32_e32 v153, s58, v148
	s_barrier
	ds_read_b128 v[154:157], v153
	ds_read_b128 v[158:161], v153 offset:1024
	ds_read_b128 v[162:165], v153 offset:2048
	ds_read_b128 v[166:169], v153 offset:3072
	s_add_u32 s26, s26, 0x40000
	s_addc_u32 s27, s27, 0
	s_mov_b32 m0, s41
	v_lshl_add_u64 v[202:203], s[26:27], 0, v[134:135]
	ds_read_b128 v[170:173], v151 offset:32768
	ds_read_b128 v[174:177], v151 offset:33792
	ds_read_b128 v[178:181], v151 offset:34816
	ds_read_b128 v[182:185], v151 offset:35840
	ds_read_b128 v[186:189], v151 offset:36864
	ds_read_b128 v[190:193], v151 offset:37888
	ds_read_b128 v[194:197], v151 offset:38912
	ds_read_b128 v[198:201], v151 offset:39936
	global_load_lds_dwordx4 v[202:203], off
	v_lshl_add_u64 v[202:203], s[26:27], 0, v[130:131]
	s_mov_b32 m0, s42
	s_nop 0
	global_load_lds_dwordx4 v[202:203], off
	s_waitcnt lgkmcnt(8)
	s_barrier
	s_waitcnt lgkmcnt(0)
	s_waitcnt lgkmcnt(0)
	v_mfma_f32_16x16x32_bf16 v[126:129], v[154:157], v[170:173], v[126:129]
	v_mfma_f32_16x16x32_bf16 v[122:125], v[162:165], v[170:173], v[122:125]
	v_mfma_f32_16x16x32_bf16 v[114:117], v[154:157], v[178:181], v[114:117]
	v_mfma_f32_16x16x32_bf16 v[106:109], v[162:165], v[178:181], v[106:109]
	v_mfma_f32_16x16x32_bf16 v[98:101], v[154:157], v[186:189], v[98:101]
	v_mfma_f32_16x16x32_bf16 v[90:93], v[162:165], v[186:189], v[90:93]
	v_mfma_f32_16x16x32_bf16 v[82:85], v[154:157], v[194:197], v[82:85]
	v_mfma_f32_16x16x32_bf16 v[74:77], v[162:165], v[194:197], v[74:77]
	v_mfma_f32_16x16x32_bf16 v[126:129], v[158:161], v[174:177], v[126:129]
	v_mfma_f32_16x16x32_bf16 v[122:125], v[166:169], v[174:177], v[122:125]
	v_mfma_f32_16x16x32_bf16 v[114:117], v[158:161], v[182:185], v[114:117]
	v_mfma_f32_16x16x32_bf16 v[106:109], v[166:169], v[182:185], v[106:109]
	v_mfma_f32_16x16x32_bf16 v[98:101], v[158:161], v[190:193], v[98:101]
	v_mfma_f32_16x16x32_bf16 v[90:93], v[166:169], v[190:193], v[90:93]
	v_mfma_f32_16x16x32_bf16 v[82:85], v[158:161], v[198:201], v[82:85]
	v_mfma_f32_16x16x32_bf16 v[74:77], v[166:169], v[198:201], v[74:77]
	s_barrier
	s_add_i32 s26, 0, 0x1c000
	s_add_i32 s27, s58, s36
	v_add_u32_e32 v153, s26, v148
	v_lshl_add_u64 v[146:147], v[146:147], 0, s[10:11]
	s_mov_b32 m0, s27
	ds_read_b128 v[202:205], v153
	ds_read_b128 v[206:209], v153 offset:1024
	ds_read_b128 v[210:213], v153 offset:2048
	ds_read_b128 v[214:217], v153 offset:3072
	global_load_lds_dwordx4 v[146:147], off
	v_lshl_add_u64 v[146:147], v[218:219], 0, s[10:11]
	s_add_i32 m0, s27, 0x2000
	s_nop 0
	global_load_lds_dwordx4 v[146:147], off
	s_barrier
	s_waitcnt lgkmcnt(0)
	s_waitcnt lgkmcnt(0)
	v_mfma_f32_16x16x32_bf16 v[118:121], v[202:205], v[170:173], v[118:121]
	v_mfma_f32_16x16x32_bf16 v[110:113], v[210:213], v[170:173], v[110:113]
	v_mfma_f32_16x16x32_bf16 v[102:105], v[202:205], v[178:181], v[102:105]
	v_mfma_f32_16x16x32_bf16 v[94:97], v[210:213], v[178:181], v[94:97]
	v_mfma_f32_16x16x32_bf16 v[86:89], v[202:205], v[186:189], v[86:89]
	v_mfma_f32_16x16x32_bf16 v[78:81], v[210:213], v[186:189], v[78:81]
	v_mfma_f32_16x16x32_bf16 v[70:73], v[202:205], v[194:197], v[70:73]
	v_mfma_f32_16x16x32_bf16 v[66:69], v[210:213], v[194:197], v[66:69]
	v_mfma_f32_16x16x32_bf16 v[118:121], v[206:209], v[174:177], v[118:121]
	v_mfma_f32_16x16x32_bf16 v[110:113], v[214:217], v[174:177], v[110:113]
	v_mfma_f32_16x16x32_bf16 v[102:105], v[206:209], v[182:185], v[102:105]
	v_mfma_f32_16x16x32_bf16 v[94:97], v[214:217], v[182:185], v[94:97]
	v_mfma_f32_16x16x32_bf16 v[86:89], v[206:209], v[190:193], v[86:89]
	v_mfma_f32_16x16x32_bf16 v[78:81], v[214:217], v[190:193], v[78:81]
	v_mfma_f32_16x16x32_bf16 v[70:73], v[206:209], v[198:201], v[70:73]
	v_mfma_f32_16x16x32_bf16 v[66:69], v[214:217], v[198:201], v[66:69]
	s_mov_b32 m0, s44
	v_lshl_add_u64 v[146:147], v[220:221], 0, s[10:11]
	s_barrier
	ds_read_b128 v[170:173], v151 offset:49152
	ds_read_b128 v[174:177], v151 offset:50176
	ds_read_b128 v[178:181], v151 offset:51200
	ds_read_b128 v[182:185], v151 offset:52224
	ds_read_b128 v[186:189], v151 offset:53248
	ds_read_b128 v[190:193], v151 offset:54272
	ds_read_b128 v[194:197], v151 offset:55296
	ds_read_b128 v[198:201], v151 offset:56320
	global_load_lds_dwordx4 v[146:147], off
	v_lshl_add_u64 v[146:147], v[222:223], 0, s[10:11]
	s_mov_b32 m0, s45
	s_nop 0
	global_load_lds_dwordx4 v[146:147], off
	s_barrier
	s_waitcnt lgkmcnt(0)
	s_waitcnt lgkmcnt(0)
	v_mfma_f32_16x16x32_bf16 v[62:65], v[154:157], v[170:173], v[62:65]
	v_mfma_f32_16x16x32_bf16 v[58:61], v[162:165], v[170:173], v[58:61]
	v_mfma_f32_16x16x32_bf16 v[54:57], v[154:157], v[178:181], v[54:57]
	v_mfma_f32_16x16x32_bf16 v[46:49], v[162:165], v[178:181], v[46:49]
	v_mfma_f32_16x16x32_bf16 v[38:41], v[154:157], v[186:189], v[38:41]
	v_mfma_f32_16x16x32_bf16 v[30:33], v[162:165], v[186:189], v[30:33]
	v_mfma_f32_16x16x32_bf16 v[22:25], v[154:157], v[194:197], v[22:25]
	v_mfma_f32_16x16x32_bf16 v[14:17], v[162:165], v[194:197], v[14:17]
	v_mfma_f32_16x16x32_bf16 v[62:65], v[158:161], v[174:177], v[62:65]
	v_mfma_f32_16x16x32_bf16 v[58:61], v[166:169], v[174:177], v[58:61]
	v_mfma_f32_16x16x32_bf16 v[54:57], v[158:161], v[182:185], v[54:57]
	v_mfma_f32_16x16x32_bf16 v[46:49], v[166:169], v[182:185], v[46:49]
	v_mfma_f32_16x16x32_bf16 v[38:41], v[158:161], v[190:193], v[38:41]
	v_mfma_f32_16x16x32_bf16 v[30:33], v[166:169], v[190:193], v[30:33]
	v_mfma_f32_16x16x32_bf16 v[22:25], v[158:161], v[198:201], v[22:25]
	v_mfma_f32_16x16x32_bf16 v[14:17], v[166:169], v[198:201], v[14:17]
	s_barrier
	s_add_u32 s24, s24, 0x40080
	s_addc_u32 s25, s25, 0
	s_add_i32 s26, s26, s36
	v_lshl_add_u64 v[146:147], s[24:25], 0, v[136:137]
	s_mov_b32 m0, s26
	s_nop 0
	global_load_lds_dwordx4 v[146:147], off
	v_lshl_add_u64 v[146:147], s[24:25], 0, v[132:133]
	s_add_i32 m0, s26, 0x2000
	s_nop 0
	global_load_lds_dwordx4 v[146:147], off
	s_waitcnt vmcnt(6)
	s_barrier
	v_mfma_f32_16x16x32_bf16 v[50:53], v[202:205], v[170:173], v[50:53]
	v_mfma_f32_16x16x32_bf16 v[42:45], v[210:213], v[170:173], v[42:45]
	v_mfma_f32_16x16x32_bf16 v[34:37], v[202:205], v[178:181], v[34:37]
	v_mfma_f32_16x16x32_bf16 v[26:29], v[210:213], v[178:181], v[26:29]
	v_mfma_f32_16x16x32_bf16 v[18:21], v[202:205], v[186:189], v[18:21]
	v_mfma_f32_16x16x32_bf16 v[10:13], v[210:213], v[186:189], v[10:13]
	v_mfma_f32_16x16x32_bf16 v[6:9], v[202:205], v[194:197], v[6:9]
	v_mfma_f32_16x16x32_bf16 v[2:5], v[210:213], v[194:197], v[2:5]
	v_mfma_f32_16x16x32_bf16 v[50:53], v[206:209], v[174:177], v[50:53]
	v_mfma_f32_16x16x32_bf16 v[42:45], v[214:217], v[174:177], v[42:45]
	v_mfma_f32_16x16x32_bf16 v[34:37], v[206:209], v[182:185], v[34:37]
	v_mfma_f32_16x16x32_bf16 v[26:29], v[214:217], v[182:185], v[26:29]
	v_mfma_f32_16x16x32_bf16 v[18:21], v[206:209], v[190:193], v[18:21]
	v_mfma_f32_16x16x32_bf16 v[10:13], v[214:217], v[190:193], v[10:13]
	v_mfma_f32_16x16x32_bf16 v[6:9], v[206:209], v[198:201], v[6:9]
	v_mfma_f32_16x16x32_bf16 v[2:5], v[214:217], v[198:201], v[2:5]
	s_add_i32 s57, s57, 2
	s_add_u32 s22, s22, 0x100
	s_addc_u32 s23, s23, 0
	s_add_u32 s21, s21, 0x100
	s_addc_u32 s56, s56, 0
	s_cmp_gt_u32 s57, 13
	s_barrier
	s_cbranch_scc0 .LBB0_3949
	s_ashr_i32 s21, s54, 31
	s_lshr_b32 s21, s21, 29
	s_add_i32 s21, s54, s21
	s_ashr_i32 s21, s21, 3
	s_mul_i32 s22, s21, 0x900
	s_lshl_b32 s21, s21, 11
	s_lshl_b32 s23, s54, 8
	s_sub_i32 s21, s23, s21
	s_add_i32 s21, s21, s22
	v_add_u32_e32 v154, s21, v1
	v_lshl_or_b32 v146, s55, 8, v149
	v_ashrrev_i32_e32 v155, 31, v154
	v_ashrrev_i32_e32 v147, 31, v146
	v_lshlrev_b64 v[156:157], 12, v[154:155]
	v_lshl_add_u64 v[156:157], s[8:9], 0, v[156:157]
	v_lshlrev_b64 v[158:159], 1, v[146:147]
	v_lshl_add_u64 v[146:147], v[156:157], 0, v[158:159]
	v_cvt_pk_bf16_f32 v126, v126, v127
	v_cvt_pk_bf16_f32 v127, v128, v129
	v_cvt_pk_bf16_f32 v128, v122, v123
	v_cvt_pk_bf16_f32 v129, v124, v125
	global_store_dwordx4 v[146:147], v[126:129], off
	v_cvt_pk_bf16_f32 v118, v118, v119
	v_cvt_pk_bf16_f32 v119, v120, v121
	v_cvt_pk_bf16_f32 v120, v110, v111
	v_or_b32_e32 v110, 16, v154
	v_ashrrev_i32_e32 v111, 31, v110
	v_lshlrev_b64 v[110:111], 12, v[110:111]
	v_lshl_add_u64 v[110:111], s[8:9], 0, v[110:111]
	v_cvt_pk_bf16_f32 v121, v112, v113
	global_store_dwordx4 v[146:147], v[118:121], off offset:256
	s_mov_b32 s55, s20
	s_mov_b32 s54, s53
	v_lshl_add_u64 v[118:119], v[110:111], 0, v[158:159]
	v_cvt_pk_bf16_f32 v110, v114, v115
	v_cvt_pk_bf16_f32 v111, v116, v117
	v_cvt_pk_bf16_f32 v112, v106, v107
	v_cvt_pk_bf16_f32 v113, v108, v109
	global_store_dwordx4 v[118:119], v[110:113], off
	v_cvt_pk_bf16_f32 v102, v102, v103
	v_cvt_pk_bf16_f32 v103, v104, v105
	v_cvt_pk_bf16_f32 v104, v94, v95
	v_or_b32_e32 v94, 32, v154
	v_ashrrev_i32_e32 v95, 31, v94
	v_lshlrev_b64 v[94:95], 12, v[94:95]
	v_lshl_add_u64 v[94:95], s[8:9], 0, v[94:95]
	v_cvt_pk_bf16_f32 v105, v96, v97
	global_store_dwordx4 v[118:119], v[102:105], off offset:256
	s_mov_b64 s[24:25], s[4:5]
	s_mov_b64 s[22:23], s[2:3]
	v_lshl_add_u64 v[102:103], v[94:95], 0, v[158:159]
	v_cvt_pk_bf16_f32 v94, v98, v99
	v_cvt_pk_bf16_f32 v95, v100, v101
	v_cvt_pk_bf16_f32 v96, v90, v91
	v_cvt_pk_bf16_f32 v97, v92, v93
	global_store_dwordx4 v[102:103], v[94:97], off
	v_cvt_pk_bf16_f32 v86, v86, v87
	v_cvt_pk_bf16_f32 v87, v88, v89
	v_cvt_pk_bf16_f32 v88, v78, v79
	v_or_b32_e32 v78, 48, v154
	v_ashrrev_i32_e32 v79, 31, v78
	v_lshlrev_b64 v[78:79], 12, v[78:79]
	v_lshl_add_u64 v[78:79], s[8:9], 0, v[78:79]
	v_cvt_pk_bf16_f32 v89, v80, v81
	global_store_dwordx4 v[102:103], v[86:89], off offset:256
	s_nop 1
	v_lshl_add_u64 v[86:87], v[78:79], 0, v[158:159]
	v_cvt_pk_bf16_f32 v78, v82, v83
	v_cvt_pk_bf16_f32 v79, v84, v85
	v_cvt_pk_bf16_f32 v80, v74, v75
	v_cvt_pk_bf16_f32 v81, v76, v77
	global_store_dwordx4 v[86:87], v[78:81], off
	v_cvt_pk_bf16_f32 v70, v70, v71
	v_cvt_pk_bf16_f32 v71, v72, v73
	v_cvt_pk_bf16_f32 v72, v66, v67
	v_cvt_pk_bf16_f32 v73, v68, v69
	global_store_dwordx4 v[86:87], v[70:73], off offset:256
	v_cvt_pk_bf16_f32 v62, v62, v63
	v_cvt_pk_bf16_f32 v63, v64, v65
	v_cvt_pk_bf16_f32 v64, v58, v59
	v_add_co_u32_e32 v58, vcc, s49, v146
	v_lshl_add_u64 v[66:67], v[146:147], 0, s[12:13]
	s_nop 0
	v_addc_co_u32_e32 v59, vcc, 0, v147, vcc
	v_cvt_pk_bf16_f32 v65, v60, v61
	global_store_dwordx4 v[58:59], v[62:65], off
	v_cvt_pk_bf16_f32 v50, v50, v51
	v_cvt_pk_bf16_f32 v51, v52, v53
	v_cvt_pk_bf16_f32 v52, v42, v43
	v_cvt_pk_bf16_f32 v53, v44, v45
	global_store_dwordx4 v[66:67], v[50:53], off offset:256
	v_cvt_pk_bf16_f32 v42, v54, v55
	v_cvt_pk_bf16_f32 v43, v56, v57
	v_cvt_pk_bf16_f32 v44, v46, v47
	v_add_co_u32_e32 v46, vcc, s50, v146
	s_nop 0
	v_lshl_add_u64 v[50:51], v[146:147], 0, s[14:15]
	v_addc_co_u32_e32 v47, vcc, 0, v147, vcc
	v_cvt_pk_bf16_f32 v45, v48, v49
	global_store_dwordx4 v[46:47], v[42:45], off
	v_cvt_pk_bf16_f32 v34, v34, v35
	v_cvt_pk_bf16_f32 v35, v36, v37
	v_cvt_pk_bf16_f32 v36, v26, v27
	v_cvt_pk_bf16_f32 v37, v28, v29
	global_store_dwordx4 v[50:51], v[34:37], off offset:256
	v_cvt_pk_bf16_f32 v26, v38, v39
	v_cvt_pk_bf16_f32 v27, v40, v41
	v_cvt_pk_bf16_f32 v28, v30, v31
	v_add_co_u32_e32 v30, vcc, s51, v146
	s_nop 0
	v_lshl_add_u64 v[34:35], v[146:147], 0, s[16:17]
	v_addc_co_u32_e32 v31, vcc, 0, v147, vcc
	v_cvt_pk_bf16_f32 v29, v32, v33
	global_store_dwordx4 v[30:31], v[26:29], off
	v_cvt_pk_bf16_f32 v18, v18, v19
	v_cvt_pk_bf16_f32 v19, v20, v21
	v_cvt_pk_bf16_f32 v20, v10, v11
	v_cvt_pk_bf16_f32 v21, v12, v13
	global_store_dwordx4 v[34:35], v[18:21], off offset:256
	v_cvt_pk_bf16_f32 v10, v22, v23
	v_cvt_pk_bf16_f32 v11, v24, v25
	v_cvt_pk_bf16_f32 v12, v14, v15
	v_add_co_u32_e32 v14, vcc, s52, v146
	s_nop 0
	v_lshl_add_u64 v[18:19], v[146:147], 0, s[18:19]
	v_addc_co_u32_e32 v15, vcc, 0, v147, vcc
	s_and_b64 vcc, exec, s[0:1]
	v_cvt_pk_bf16_f32 v13, v16, v17
	global_store_dwordx4 v[14:15], v[10:13], off
	v_cvt_pk_bf16_f32 v6, v6, v7
	v_cvt_pk_bf16_f32 v7, v8, v9
	v_cvt_pk_bf16_f32 v8, v2, v3
	v_cvt_pk_bf16_f32 v9, v4, v5
	global_store_dwordx4 v[18:19], v[6:9], off offset:256
	s_cbranch_vccz .LBB0_3942
	s_waitcnt vmcnt(0)
	s_cmpk_gt_u32 s30, 0xff
	s_cbranch_scc1 .LBB0_3953
	s_barrier

.LBB0_3955:
	s_cmp_gt_i32 s55, 24
	s_cselect_b64 s[0:1], -1, 0
	s_and_b64 s[2:3], s[6:7], s[0:1]
	s_andn2_b64 vcc, exec, s[2:3]
	s_cbranch_vccnz .LBB0_4005
	s_waitcnt vmcnt(0)
	s_barrier
	s_setprio 0
	s_mov_b64 s[2:3], exec
	v_readlane_b32 s4, v250, 5
	v_readlane_b32 s5, v250, 6
	s_and_b64 s[4:5], s[2:3], s[4:5]
	s_mov_b64 exec, s[4:5]
	s_cbranch_execz .LBB0_4004
	s_add_i32 s4, 0, 0x27ff0
	v_mov_b32_e32 v1, s4
	s_waitcnt vmcnt(0) expcnt(0) lgkmcnt(0)
	ds_read_b32 v3, v1
	s_add_i32 s4, 0, 0x27ff4
	v_mov_b32_e32 v1, s4
	ds_read_b32 v1, v1
	s_waitcnt lgkmcnt(1)
	v_cmp_ne_u32_e32 vcc, 0, v3
	s_cbranch_vccnz .LBB0_3972
	v_readlane_b32 s4, v250, 2
	v_readlane_b32 s5, v250, 3
	s_load_dwordx2 s[8:9], s[4:5], 0x4
	s_add_u32 s4, s52, 0x1000
	s_addc_u32 s5, s53, 0
	s_add_u32 s6, s52, 0x1100
	s_addc_u32 s7, s53, 0
	v_readlane_b32 s10, v250, 1
	s_waitcnt lgkmcnt(0)
	s_mul_i32 s18, s8, s10
	s_add_u32 s8, s52, 0x1200
	s_mul_i32 s18, s18, s9
	s_addc_u32 s9, s53, 0
	s_add_u32 s10, s52, 0x1300
	s_addc_u32 s11, s53, 0
	s_mov_b32 s19, 1
	v_mov_b32_e32 v17, 0
	s_branch .LBB0_3960
